# v34: v29 + fp8 pack sequences: dead destination v_mov before the two half-writing v_cvt_pk_fp8_f32 replaced by s_nop 0 (tied copies folded into the convert source); attention P packing and fp8 GEMM ep
# speedup vs baseline: 1.0053x; 1.0033x over previous
.LBB0_40:
	v_mov_b32_e32 v146, v52
	v_mov_b32_e32 v147, v48
	v_pk_mul_f32 v[146:147], v[146:147], s[18:19] op_sel_hi:[1,0]
	s_nop 0
	v_cvt_pk_fp8_f32 v130, v146, v147
	v_mov_b32_e32 v146, v60
	v_mov_b32_e32 v147, v56
	v_pk_mul_f32 v[146:147], v[146:147], s[18:19] op_sel_hi:[1,0]
	s_nop 0
	v_cvt_pk_fp8_f32 v130, v146, v147 op_sel:[0,0,1]
	v_mov_b32_e32 v146, v53
	v_mov_b32_e32 v147, v49
	v_pk_mul_f32 v[146:147], v[146:147], s[18:19] op_sel_hi:[1,0]
	s_nop 0
	v_cvt_pk_fp8_f32 v148, v146, v147
	v_mov_b32_e32 v146, v61
	v_mov_b32_e32 v147, v57
	v_pk_mul_f32 v[146:147], v[146:147], s[18:19] op_sel_hi:[1,0]
	s_nop 0
	v_cvt_pk_fp8_f32 v148, v146, v147 op_sel:[0,0,1]
	v_mov_b32_e32 v146, v54
	v_mov_b32_e32 v147, v50
	v_pk_mul_f32 v[146:147], v[146:147], s[18:19] op_sel_hi:[1,0]
	s_nop 0
	v_cvt_pk_fp8_f32 v149, v146, v147
	v_mov_b32_e32 v146, v62
	v_mov_b32_e32 v147, v58
	v_pk_mul_f32 v[146:147], v[146:147], s[18:19] op_sel_hi:[1,0]
	s_nop 0
	v_cvt_pk_fp8_f32 v149, v146, v147 op_sel:[0,0,1]
	v_mov_b32_e32 v146, v55
	v_mov_b32_e32 v147, v51
	v_pk_mul_f32 v[146:147], v[146:147], s[18:19] op_sel_hi:[1,0]
	s_nop 0
	v_cvt_pk_fp8_f32 v150, v146, v147
	v_mov_b32_e32 v146, v63
	v_mov_b32_e32 v147, v59
	v_pk_mul_f32 v[146:147], v[146:147], s[18:19] op_sel_hi:[1,0]
	s_nop 0
	v_cvt_pk_fp8_f32 v150, v146, v147 op_sel:[0,0,1]
	v_mov_b32_e32 v146, v76
	v_mov_b32_e32 v147, v72
	v_pk_mul_f32 v[146:147], v[146:147], s[18:19] op_sel_hi:[1,0]
	s_lshl_b32 s34, s45, 7
	v_cvt_pk_fp8_f32 v151, v146, v147
	v_mov_b32_e32 v146, v84
	v_mov_b32_e32 v147, v80
	v_pk_mul_f32 v[146:147], v[146:147], s[18:19] op_sel_hi:[1,0]
	s_ashr_i32 s35, s34, 31
	v_cvt_pk_fp8_f32 v151, v146, v147 op_sel:[0,0,1]
	v_mov_b32_e32 v146, v77
	v_mov_b32_e32 v147, v73
	v_pk_mul_f32 v[146:147], v[146:147], s[18:19] op_sel_hi:[1,0]
	s_add_i32 s44, s55, s19
	v_cvt_pk_fp8_f32 v152, v146, v147
	v_mov_b32_e32 v146, v85
	v_mov_b32_e32 v147, v81
	v_pk_mul_f32 v[146:147], v[146:147], s[18:19] op_sel_hi:[1,0]
	s_nop 0
	v_cvt_pk_fp8_f32 v152, v146, v147 op_sel:[0,0,1]
	v_mov_b32_e32 v146, v78
	v_mov_b32_e32 v147, v74
	v_pk_mul_f32 v[146:147], v[146:147], s[18:19] op_sel_hi:[1,0]
	s_nop 0
	v_cvt_pk_fp8_f32 v153, v146, v147
	v_mov_b32_e32 v146, v86
	v_mov_b32_e32 v147, v82
	v_pk_mul_f32 v[146:147], v[146:147], s[18:19] op_sel_hi:[1,0]
	s_nop 0
	v_cvt_pk_fp8_f32 v153, v146, v147 op_sel:[0,0,1]
	v_mov_b32_e32 v146, v79
	v_mov_b32_e32 v147, v75
	v_pk_mul_f32 v[146:147], v[146:147], s[18:19] op_sel_hi:[1,0]
	s_nop 0
	v_cvt_pk_fp8_f32 v154, v146, v147
	v_mov_b32_e32 v146, v87
	v_mov_b32_e32 v147, v83
	v_pk_mul_f32 v[146:147], v[146:147], s[18:19] op_sel_hi:[1,0]
	s_nop 0
	v_cvt_pk_fp8_f32 v154, v146, v147 op_sel:[0,0,1]
	v_mov_b32_e32 v146, v100
	v_mov_b32_e32 v147, v96
	ds_write2_b32 v136, v130, v148 offset1:33
	ds_write2_b32 v136, v149, v150 offset0:66 offset1:99
	ds_write2_b32 v138, v151, v152 offset0:128 offset1:161
	ds_write2_b32 v138, v153, v154 offset0:194 offset1:227
	v_pk_mul_f32 v[146:147], v[146:147], s[18:19] op_sel_hi:[1,0]
	s_nop 0
	v_cvt_pk_fp8_f32 v130, v146, v147
	v_mov_b32_e32 v146, v108
	v_mov_b32_e32 v147, v104
	v_pk_mul_f32 v[146:147], v[146:147], s[18:19] op_sel_hi:[1,0]
	s_nop 0
	v_cvt_pk_fp8_f32 v130, v146, v147 op_sel:[0,0,1]
	v_mov_b32_e32 v146, v101
	v_mov_b32_e32 v147, v97
	v_pk_mul_f32 v[146:147], v[146:147], s[18:19] op_sel_hi:[1,0]
	s_nop 0
	v_cvt_pk_fp8_f32 v138, v146, v147
	v_mov_b32_e32 v146, v109
	v_mov_b32_e32 v147, v105
	v_pk_mul_f32 v[146:147], v[146:147], s[18:19] op_sel_hi:[1,0]
	s_nop 0
	v_cvt_pk_fp8_f32 v138, v146, v147 op_sel:[0,0,1]
	v_mov_b32_e32 v146, v102
	v_mov_b32_e32 v147, v98
	v_pk_mul_f32 v[146:147], v[146:147], s[18:19] op_sel_hi:[1,0]
	s_nop 0
	v_cvt_pk_fp8_f32 v148, v146, v147
	v_mov_b32_e32 v146, v110
	v_mov_b32_e32 v147, v106
	v_pk_mul_f32 v[146:147], v[146:147], s[18:19] op_sel_hi:[1,0]
	s_nop 0
	v_cvt_pk_fp8_f32 v148, v146, v147 op_sel:[0,0,1]
	v_mov_b32_e32 v146, v103
	v_mov_b32_e32 v147, v99
	v_pk_mul_f32 v[146:147], v[146:147], s[18:19] op_sel_hi:[1,0]
	s_nop 0
	v_cvt_pk_fp8_f32 v149, v146, v147
	v_mov_b32_e32 v146, v111
	v_mov_b32_e32 v147, v107
	v_pk_mul_f32 v[146:147], v[146:147], s[18:19] op_sel_hi:[1,0]
	s_nop 0
	v_cvt_pk_fp8_f32 v149, v146, v147 op_sel:[0,0,1]
	v_mov_b32_e32 v146, v116
	v_mov_b32_e32 v147, v112
	v_pk_mul_f32 v[146:147], v[146:147], s[18:19] op_sel_hi:[1,0]
	s_nop 0
	v_cvt_pk_fp8_f32 v150, v146, v147
	v_mov_b32_e32 v146, v124
	v_mov_b32_e32 v147, v120
	v_pk_mul_f32 v[146:147], v[146:147], s[18:19] op_sel_hi:[1,0]
	s_nop 0
	v_cvt_pk_fp8_f32 v150, v146, v147 op_sel:[0,0,1]
	v_mov_b32_e32 v146, v117
	v_mov_b32_e32 v147, v113
	v_pk_mul_f32 v[146:147], v[146:147], s[18:19] op_sel_hi:[1,0]
	s_nop 0
	v_cvt_pk_fp8_f32 v151, v146, v147
	v_mov_b32_e32 v146, v125
	v_mov_b32_e32 v147, v121
	v_pk_mul_f32 v[146:147], v[146:147], s[18:19] op_sel_hi:[1,0]
	s_nop 0
	v_cvt_pk_fp8_f32 v151, v146, v147 op_sel:[0,0,1]
	v_mov_b32_e32 v146, v118
	v_mov_b32_e32 v147, v114
	v_pk_mul_f32 v[146:147], v[146:147], s[18:19] op_sel_hi:[1,0]
	s_nop 0
	v_cvt_pk_fp8_f32 v152, v146, v147
	v_mov_b32_e32 v146, v126
	v_mov_b32_e32 v147, v122
	v_pk_mul_f32 v[146:147], v[146:147], s[18:19] op_sel_hi:[1,0]
	s_nop 0
	v_cvt_pk_fp8_f32 v152, v146, v147 op_sel:[0,0,1]
	v_mov_b32_e32 v146, v119
	v_mov_b32_e32 v147, v115
	v_pk_mul_f32 v[146:147], v[146:147], s[18:19] op_sel_hi:[1,0]
	s_nop 0
	v_cvt_pk_fp8_f32 v153, v146, v147
	v_mov_b32_e32 v146, v127
	v_mov_b32_e32 v147, v123
	v_pk_mul_f32 v[146:147], v[146:147], s[18:19] op_sel_hi:[1,0]
	s_nop 0
	v_cvt_pk_fp8_f32 v153, v146, v147 op_sel:[0,0,1]
	ds_write2_b32 v137, v130, v138 offset1:33
	ds_write2_b32 v137, v148, v149 offset0:66 offset1:99
	ds_write2_b32 v139, v150, v151 offset0:128 offset1:161
	ds_write2_b32 v139, v152, v153 offset0:194 offset1:227
	v_lshl_add_u32 v138, s46, 6, v134
	s_waitcnt lgkmcnt(0)
	s_barrier
	ds_read2_b32 v[146:147], v135 offset1:1
	ds_read2_b32 v[148:149], v135 offset0:2 offset1:3
	v_ashrrev_i32_e32 v139, 31, v138
	v_lshlrev_b64 v[138:139], 11, v[138:139]
	v_lshl_add_u64 v[138:139], s[20:21], 0, v[138:139]
	v_lshl_add_u64 v[138:139], v[138:139], 0, s[34:35]
	v_lshl_add_u64 v[150:151], v[138:139], 0, v[132:133]
	ds_read2_b32 v[138:139], v140 offset1:1
	ds_read2_b32 v[140:141], v141 offset1:1
	s_waitcnt lgkmcnt(2)
	global_store_dwordx4 v[150:151], v[146:149], off nt
	s_lshl_b32 s34, s49, 7
	s_ashr_i32 s35, s34, 31
	v_lshl_add_u32 v146, s50, 6, v134
	v_ashrrev_i32_e32 v147, 31, v146
	v_lshlrev_b64 v[146:147], 11, v[146:147]
	v_lshl_add_u64 v[146:147], s[24:25], 0, v[146:147]
	v_lshl_add_u64 v[146:147], v[146:147], 0, s[34:35]
	v_lshl_add_u64 v[146:147], v[146:147], 0, v[132:133]
	s_waitcnt lgkmcnt(0)
	global_store_dwordx4 v[146:147], v[138:141], off nt
	v_lshl_add_u32 v146, s52, 6, v134
	ds_read2_b32 v[138:139], v142 offset1:1
	ds_read2_b32 v[140:141], v143 offset1:1
	v_ashrrev_i32_e32 v147, 31, v146
	v_lshlrev_b64 v[142:143], 11, v[146:147]
	s_lshl_b32 s34, s51, 7
	v_lshl_add_u64 v[142:143], s[28:29], 0, v[142:143]
	s_ashr_i32 s35, s34, 31
	v_lshl_add_u64 v[142:143], v[142:143], 0, s[34:35]
	v_lshl_add_u64 v[146:147], v[142:143], 0, v[132:133]
	ds_read2_b32 v[142:143], v144 offset1:1
	ds_read2_b32 v[144:145], v145 offset1:1
	s_waitcnt lgkmcnt(2)
	global_store_dwordx4 v[146:147], v[138:141], off nt
	s_lshl_b32 s34, s53, 7
	s_ashr_i32 s35, s34, 31
	v_lshl_add_u32 v138, s54, 6, v134
	v_ashrrev_i32_e32 v139, 31, v138
	v_lshlrev_b64 v[138:139], 11, v[138:139]
	v_lshl_add_u64 v[138:139], s[30:31], 0, v[138:139]
	v_lshl_add_u64 v[138:139], v[138:139], 0, s[34:35]
	s_cmpk_gt_i32 s44, 0x7ff
	v_lshl_add_u64 v[138:139], v[138:139], 0, v[132:133]
	s_cselect_b64 s[34:35], -1, 0
	s_waitcnt lgkmcnt(0)
	global_store_dwordx4 v[138:139], v[142:145], off nt
	s_barrier

.LBB0_60:
	s_waitcnt vmcnt(15)
	v_mov_b32_e32 v138, v0
	s_waitcnt vmcnt(14)
	v_mov_b32_e32 v139, v4
	v_pk_mul_f32 v[138:139], v[138:139], s[18:19] op_sel_hi:[1,0]
	s_nop 0
	v_cvt_pk_fp8_f32 v130, v138, v139
	s_waitcnt vmcnt(13)
	v_mov_b32_e32 v138, v8
	s_waitcnt vmcnt(12)
	v_mov_b32_e32 v139, v12
	v_pk_mul_f32 v[138:139], v[138:139], s[18:19] op_sel_hi:[1,0]
	s_nop 0
	v_cvt_pk_fp8_f32 v130, v138, v139 op_sel:[0,0,1]
	v_mov_b32_e32 v138, v1
	v_mov_b32_e32 v139, v5
	v_pk_mul_f32 v[138:139], v[138:139], s[18:19] op_sel_hi:[1,0]
	s_nop 0
	v_cvt_pk_fp8_f32 v137, v138, v139
	v_mov_b32_e32 v138, v9
	v_mov_b32_e32 v139, v13
	v_pk_mul_f32 v[138:139], v[138:139], s[18:19] op_sel_hi:[1,0]
	s_nop 0
	v_cvt_pk_fp8_f32 v137, v138, v139 op_sel:[0,0,1]
	v_mov_b32_e32 v138, v2
	v_mov_b32_e32 v139, v6
	v_pk_mul_f32 v[138:139], v[138:139], s[18:19] op_sel_hi:[1,0]
	s_nop 0
	v_cvt_pk_fp8_f32 v140, v138, v139
	v_mov_b32_e32 v138, v10
	v_mov_b32_e32 v139, v14
	v_pk_mul_f32 v[138:139], v[138:139], s[18:19] op_sel_hi:[1,0]
	s_nop 0
	v_cvt_pk_fp8_f32 v140, v138, v139 op_sel:[0,0,1]
	v_mov_b32_e32 v138, v3
	v_mov_b32_e32 v139, v7
	v_pk_mul_f32 v[138:139], v[138:139], s[18:19] op_sel_hi:[1,0]
	v_mov_b32_e32 v144, v131
	v_cvt_pk_fp8_f32 v141, v138, v139
	v_mov_b32_e32 v138, v11
	v_mov_b32_e32 v139, v15
	v_pk_mul_f32 v[138:139], v[138:139], s[18:19] op_sel_hi:[1,0]
	v_mov_b32_e32 v145, v131
	v_cvt_pk_fp8_f32 v141, v138, v139 op_sel:[0,0,1]
	s_waitcnt vmcnt(11)
	v_mov_b32_e32 v138, v16
	s_waitcnt vmcnt(10)
	v_mov_b32_e32 v139, v20
	ds_write2_b32 v136, v130, v137 offset1:33
	ds_write2_b32 v136, v140, v141 offset0:66 offset1:99
	v_pk_mul_f32 v[138:139], v[138:139], s[18:19] op_sel_hi:[1,0]
	s_nop 0
	v_cvt_pk_fp8_f32 v130, v138, v139
	s_waitcnt vmcnt(9)
	v_mov_b32_e32 v138, v24
	s_waitcnt vmcnt(8)
	v_mov_b32_e32 v139, v28
	v_pk_mul_f32 v[138:139], v[138:139], s[18:19] op_sel_hi:[1,0]
	s_nop 0
	v_cvt_pk_fp8_f32 v130, v138, v139 op_sel:[0,0,1]
	v_mov_b32_e32 v138, v17
	v_mov_b32_e32 v139, v21
	v_pk_mul_f32 v[138:139], v[138:139], s[18:19] op_sel_hi:[1,0]
	v_mov_b32_e32 v140, v18
	v_cvt_pk_fp8_f32 v137, v138, v139
	v_mov_b32_e32 v138, v25
	v_mov_b32_e32 v139, v29
	v_pk_mul_f32 v[138:139], v[138:139], s[18:19] op_sel_hi:[1,0]
	v_mov_b32_e32 v141, v22
	v_cvt_pk_fp8_f32 v137, v138, v139 op_sel:[0,0,1]
	v_pk_mul_f32 v[140:141], v[140:141], s[18:19] op_sel_hi:[1,0]
	s_nop 0
	v_cvt_pk_fp8_f32 v139, v140, v141
	v_mov_b32_e32 v140, v26
	v_mov_b32_e32 v141, v30
	v_pk_mul_f32 v[140:141], v[140:141], s[18:19] op_sel_hi:[1,0]
	v_add_u32_e32 v138, 0x4000, v136
	v_cvt_pk_fp8_f32 v139, v140, v141 op_sel:[0,0,1]
	v_mov_b32_e32 v140, v19
	v_mov_b32_e32 v141, v23
	v_pk_mul_f32 v[140:141], v[140:141], s[18:19] op_sel_hi:[1,0]
	s_lshl_b32 s36, s1, 7
	v_cvt_pk_fp8_f32 v142, v140, v141
	v_mov_b32_e32 v140, v27
	v_mov_b32_e32 v141, v31
	v_pk_mul_f32 v[140:141], v[140:141], s[18:19] op_sel_hi:[1,0]
	s_ashr_i32 s37, s36, 31
	v_cvt_pk_fp8_f32 v142, v140, v141 op_sel:[0,0,1]
	s_waitcnt vmcnt(7)
	v_mov_b32_e32 v140, v32
	s_waitcnt vmcnt(6)
	v_mov_b32_e32 v141, v36
	v_pk_mul_f32 v[140:141], v[140:141], s[18:19] op_sel_hi:[1,0]
	ds_write2_b32 v138, v130, v137 offset0:128 offset1:161
	ds_write2_b32 v138, v139, v142 offset0:194 offset1:227
	v_cvt_pk_fp8_f32 v143, v140, v141
	s_waitcnt vmcnt(5)
	v_mov_b32_e32 v140, v40
	s_waitcnt vmcnt(4)
	v_mov_b32_e32 v141, v44
	v_pk_mul_f32 v[140:141], v[140:141], s[18:19] op_sel_hi:[1,0]
	s_nop 0
	v_cvt_pk_fp8_f32 v143, v140, v141 op_sel:[0,0,1]
	v_mov_b32_e32 v140, v33
	v_mov_b32_e32 v141, v37
	v_pk_mul_f32 v[140:141], v[140:141], s[18:19] op_sel_hi:[1,0]
	s_nop 0
	v_cvt_pk_fp8_f32 v144, v140, v141
	v_mov_b32_e32 v140, v41
	v_mov_b32_e32 v141, v45
	v_pk_mul_f32 v[140:141], v[140:141], s[18:19] op_sel_hi:[1,0]
	s_nop 0
	v_cvt_pk_fp8_f32 v144, v140, v141 op_sel:[0,0,1]
	v_mov_b32_e32 v140, v34
	v_mov_b32_e32 v141, v38
	v_pk_mul_f32 v[140:141], v[140:141], s[18:19] op_sel_hi:[1,0]
	v_add_u32_e32 v137, 0x8400, v136
	v_cvt_pk_fp8_f32 v130, v140, v141
	v_mov_b32_e32 v140, v42
	v_mov_b32_e32 v141, v46
	v_pk_mul_f32 v[140:141], v[140:141], s[18:19] op_sel_hi:[1,0]
	ds_write2_b32 v137, v143, v144 offset1:33
	v_cvt_pk_fp8_f32 v130, v140, v141 op_sel:[0,0,1]
	v_mov_b32_e32 v140, v35
	v_mov_b32_e32 v141, v39
	v_pk_mul_f32 v[140:141], v[140:141], s[18:19] op_sel_hi:[1,0]
	s_nop 0
	v_cvt_pk_fp8_f32 v139, v140, v141
	v_mov_b32_e32 v140, v43
	v_mov_b32_e32 v141, v47
	v_pk_mul_f32 v[140:141], v[140:141], s[18:19] op_sel_hi:[1,0]
	s_nop 0
	v_cvt_pk_fp8_f32 v139, v140, v141 op_sel:[0,0,1]
	s_waitcnt vmcnt(3)
	v_mov_b32_e32 v140, v64
	s_waitcnt vmcnt(2)
	v_mov_b32_e32 v141, v68
	v_pk_mul_f32 v[140:141], v[140:141], s[18:19] op_sel_hi:[1,0]
	ds_write2_b32 v137, v130, v139 offset0:66 offset1:99
	v_cvt_pk_fp8_f32 v142, v140, v141
	s_waitcnt vmcnt(1)
	v_mov_b32_e32 v140, v88
	s_waitcnt vmcnt(0)
	v_mov_b32_e32 v141, v92
	v_pk_mul_f32 v[140:141], v[140:141], s[18:19] op_sel_hi:[1,0]
	v_add_u32_e32 v139, 0xc400, v136
	v_cvt_pk_fp8_f32 v142, v140, v141 op_sel:[0,0,1]
	v_mov_b32_e32 v140, v65
	v_mov_b32_e32 v141, v69
	v_pk_mul_f32 v[140:141], v[140:141], s[18:19] op_sel_hi:[1,0]
	s_andn2_b64 vcc, exec, s[34:35]
	v_cvt_pk_fp8_f32 v143, v140, v141
	v_mov_b32_e32 v140, v89
	v_mov_b32_e32 v141, v93
	v_pk_mul_f32 v[140:141], v[140:141], s[18:19] op_sel_hi:[1,0]
	s_mov_b64 s[34:35], -1
	v_cvt_pk_fp8_f32 v143, v140, v141 op_sel:[0,0,1]
	v_mov_b32_e32 v140, v66
	v_mov_b32_e32 v141, v70
	v_pk_mul_f32 v[140:141], v[140:141], s[18:19] op_sel_hi:[1,0]
	s_nop 0
	v_cvt_pk_fp8_f32 v144, v140, v141
	v_mov_b32_e32 v140, v90
	v_mov_b32_e32 v141, v94
	v_pk_mul_f32 v[140:141], v[140:141], s[18:19] op_sel_hi:[1,0]
	s_nop 0
	v_cvt_pk_fp8_f32 v144, v140, v141 op_sel:[0,0,1]
	v_mov_b32_e32 v140, v67
	v_mov_b32_e32 v141, v71
	v_pk_mul_f32 v[140:141], v[140:141], s[18:19] op_sel_hi:[1,0]
	s_nop 0
	v_cvt_pk_fp8_f32 v145, v140, v141
	v_mov_b32_e32 v140, v91
	v_mov_b32_e32 v141, v95
	v_pk_mul_f32 v[140:141], v[140:141], s[18:19] op_sel_hi:[1,0]
	s_nop 0
	v_cvt_pk_fp8_f32 v145, v140, v141 op_sel:[0,0,1]
	v_lshl_add_u32 v140, s0, 6, v134
	ds_write2_b32 v139, v142, v143 offset0:128 offset1:161
	ds_write2_b32 v139, v144, v145 offset0:194 offset1:227
	s_waitcnt lgkmcnt(0)
	s_barrier
	ds_read2_b32 v[142:143], v135 offset1:1
	ds_read2_b32 v[144:145], v135 offset0:2 offset1:3
	v_ashrrev_i32_e32 v141, 31, v140
	v_lshlrev_b64 v[140:141], 11, v[140:141]
	v_lshl_add_u64 v[140:141], s[14:15], 0, v[140:141]
	v_lshl_add_u64 v[140:141], v[140:141], 0, s[36:37]
	v_lshl_add_u64 v[150:151], v[140:141], 0, v[132:133]
	v_add_u32_e32 v140, 0x4200, v135
	v_add_u32_e32 v141, 0x4208, v135
	ds_read2_b32 v[146:147], v140 offset1:1
	ds_read2_b32 v[148:149], v141 offset1:1
	s_waitcnt lgkmcnt(2)
	global_store_dwordx4 v[150:151], v[142:145], off nt
	s_lshl_b32 s36, s33, 7
	s_ashr_i32 s37, s36, 31
	v_lshl_add_u32 v142, s40, 6, v134
	v_ashrrev_i32_e32 v143, 31, v142
	v_lshlrev_b64 v[142:143], 11, v[142:143]
	v_lshl_add_u64 v[142:143], s[12:13], 0, v[142:143]
	v_lshl_add_u64 v[142:143], v[142:143], 0, s[36:37]
	v_lshl_add_u64 v[142:143], v[142:143], 0, v[132:133]
	s_waitcnt lgkmcnt(0)
	global_store_dwordx4 v[142:143], v[146:149], off nt
	v_add_u32_e32 v142, 0x8400, v135
	v_lshl_add_u32 v144, s41, 6, v134
	v_add_u32_e32 v143, 0x8408, v135
	ds_read2_b32 v[146:147], v142 offset1:1
	ds_read2_b32 v[148:149], v143 offset1:1
	v_ashrrev_i32_e32 v145, 31, v144
	v_lshlrev_b64 v[144:145], 11, v[144:145]
	s_lshl_b32 s36, s42, 7
	v_lshl_add_u64 v[144:145], s[22:23], 0, v[144:145]
	s_ashr_i32 s37, s36, 31
	v_lshl_add_u64 v[144:145], v[144:145], 0, s[36:37]
	v_lshl_add_u64 v[154:155], v[144:145], 0, v[132:133]
	v_add_u32_e32 v144, 0xc600, v135
	v_add_u32_e32 v145, 0xc608, v135
	ds_read2_b32 v[150:151], v144 offset1:1
	ds_read2_b32 v[152:153], v145 offset1:1
	s_waitcnt lgkmcnt(2)
	global_store_dwordx4 v[154:155], v[146:149], off nt
	s_lshl_b32 s36, s47, 7
	s_ashr_i32 s37, s36, 31
	v_lshl_add_u32 v146, s48, 6, v134
	v_ashrrev_i32_e32 v147, 31, v146
	v_lshlrev_b64 v[146:147], 11, v[146:147]
	v_lshl_add_u64 v[146:147], s[26:27], 0, v[146:147]
	v_lshl_add_u64 v[146:147], v[146:147], 0, s[36:37]
	v_lshl_add_u64 v[146:147], v[146:147], 0, v[132:133]
	s_waitcnt lgkmcnt(0)
	global_store_dwordx4 v[146:147], v[150:153], off nt
	s_barrier
	s_cbranch_vccnz .LBB0_41
	s_add_i32 s36, s43, s44
	s_cmpk_gt_i32 s36, 0x7ff
	s_cbranch_scc1 .LBB0_40
	s_cmpk_gt_i32 s36, 0x5ff
	s_cbranch_scc0 .LBB0_64
	s_add_i32 s0, s36, 0xfffffa00
	s_lshr_b32 s1, s0, 5
	s_and_b32 s0, s36, 31
	s_mov_b64 s[12:13], s[10:11]
	s_mov_b64 s[22:23], 0x800
	s_mov_b64 s[14:15], s[4:5]
	s_cbranch_execz .LBB0_65
	s_branch .LBB0_66

.LBB0_143:
	v_mul_f32_e32 v66, v61, v61
	v_mul_f32_e32 v67, v57, v57
	v_fmac_f32_e32 v66, v60, v60
	v_fmac_f32_e32 v67, v56, v56
	v_fmac_f32_e32 v66, v62, v62
	v_fmac_f32_e32 v67, v58, v58
	s_ashr_i32 s4, s4, 12
	v_fmac_f32_e32 v66, v63, v63
	v_fmac_f32_e32 v67, v59, v59
	v_mov_b32_e32 v82, v53
	v_mov_b32_e32 v83, v49
	v_add_f32_e32 v88, v66, v67
	v_mov_b32_e32 v66, v52
	v_mov_b32_e32 v67, v48
	v_pk_mul_f32 v[82:83], v[82:83], v[82:83]
	s_mul_hi_i32 s5, s4, 0xc000
	s_mul_i32 s4, s4, 0xc000
	v_mov_b32_e32 v84, v54
	v_mov_b32_e32 v85, v50
	v_pk_fma_f32 v[66:67], v[66:67], v[66:67], v[82:83]
	s_add_u32 s28, s1, s4
	v_mov_b32_e32 v86, v55
	v_mov_b32_e32 v87, v51
	v_pk_fma_f32 v[66:67], v[84:85], v[84:85], v[66:67]
	s_addc_u32 s29, s45, s5
	v_pk_fma_f32 v[66:67], v[86:87], v[86:87], v[66:67]
	v_mov_b32_e32 v82, v45
	v_mov_b32_e32 v83, v41
	s_add_u32 s30, s28, 0x2000
	v_lshlrev_b64 v[86:87], 2, v[80:81]
	v_pk_mul_f32 v[94:95], v[82:83], v[82:83]
	s_addc_u32 s31, s29, 0
	v_lshl_add_u64 v[82:83], s[10:11], 0, v[86:87]
	v_add_f32_e32 v66, v88, v66
	global_load_dwordx4 v[82:85], v[82:83], off
	v_lshl_add_u64 v[88:89], s[30:31], 0, v[86:87]
	v_lshl_add_u64 v[90:91], s[28:29], 0, v[86:87]
	global_load_dwordx4 v[86:89], v[88:89], off
	s_nop 0
	global_load_dwordx4 v[90:93], v[90:91], off
	v_add_f32_e32 v100, v66, v67
	v_mov_b32_e32 v66, v44
	v_mov_b32_e32 v67, v40
	v_mov_b32_e32 v96, v46
	v_mov_b32_e32 v97, v42
	v_pk_fma_f32 v[66:67], v[66:67], v[66:67], v[94:95]
	v_mov_b32_e32 v98, v47
	v_mov_b32_e32 v99, v43
	v_pk_fma_f32 v[66:67], v[96:97], v[96:97], v[66:67]
	v_mov_b32_e32 v94, v37
	v_pk_fma_f32 v[66:67], v[98:99], v[98:99], v[66:67]
	v_mov_b32_e32 v95, v33
	v_add_f32_e32 v66, v100, v66
	v_add_f32_e32 v100, v66, v67
	v_mov_b32_e32 v66, v36
	v_mov_b32_e32 v67, v32
	v_pk_mul_f32 v[94:95], v[94:95], v[94:95]
	v_mov_b32_e32 v96, v38
	v_mov_b32_e32 v97, v34
	v_pk_fma_f32 v[66:67], v[66:67], v[66:67], v[94:95]
	v_mov_b32_e32 v98, v39
	v_mov_b32_e32 v99, v35
	v_pk_fma_f32 v[66:67], v[96:97], v[96:97], v[66:67]
	s_nop 0
	v_pk_fma_f32 v[66:67], v[98:99], v[98:99], v[66:67]
	s_nop 0
	v_add_f32_e32 v66, v100, v66
	v_add_f32_e32 v66, v66, v67
	s_nop 1
	v_add_f32_dpp v66, v66, v66 quad_perm:[1,0,3,2] row_mask:0xf bank_mask:0xf bound_ctrl:1
	s_nop 1
	v_add_f32_dpp v66, v66, v66 quad_perm:[2,3,0,1] row_mask:0xf bank_mask:0xf bound_ctrl:1
	s_nop 1
	v_add_f32_dpp v66, v66, v66 row_half_mirror row_mask:0xf bank_mask:0xf bound_ctrl:1
	s_nop 1
	v_add_f32_dpp v66, v66, v66 row_mirror row_mask:0xf bank_mask:0xf bound_ctrl:1
	s_nop 0
	v_readlane_b32 s23, v66, 16
	v_readlane_b32 s26, v66, 48
	v_readlane_b32 s4, v66, 0
	v_readlane_b32 s5, v66, 32
	v_mov_b32_e32 v66, s23
	v_mov_b32_e32 v67, s26
	v_pk_add_f32 v[66:67], s[4:5], v[66:67]
	s_nop 0
	v_add_f32_e32 v66, v66, v67
	v_fmamk_f32 v66, v66, 0x3a000000, v197
	v_mul_f32_e32 v67, 0x4f800000, v66
	v_cmp_gt_f32_e32 vcc, s15, v66
	s_nop 1
	v_cndmask_b32_e32 v66, v66, v67, vcc
	v_sqrt_f32_e32 v67, v66
	s_nop 0
	v_add_u32_e32 v94, -1, v67
	v_fma_f32 v95, -v94, v67, v66
	v_cmp_ge_f32_e64 s[4:5], 0, v95
	v_add_u32_e32 v95, 1, v67
	s_nop 0
	v_cndmask_b32_e64 v94, v67, v94, s[4:5]
	v_fma_f32 v67, -v95, v67, v66
	v_cmp_lt_f32_e64 s[4:5], 0, v67
	s_nop 1
	v_cndmask_b32_e64 v67, v94, v95, s[4:5]
	v_mul_f32_e32 v94, 0x37800000, v67
	v_cndmask_b32_e32 v67, v67, v94, vcc
	v_cmp_class_f32_e32 vcc, v66, v198
	s_nop 1
	v_cndmask_b32_e32 v66, v67, v66, vcc
	v_div_scale_f32 v67, s[4:5], v66, v66, 1.0
	v_rcp_f32_e32 v94, v67
	s_add_u32 s4, s48, s6
	s_addc_u32 s5, s49, s7
	s_add_u32 s26, s50, s6
	v_fma_f32 v95, -v67, v94, 1.0
	v_fmac_f32_e32 v94, v95, v94
	v_div_scale_f32 v95, vcc, 1.0, v66, 1.0
	v_mul_f32_e32 v96, v95, v94
	v_fma_f32 v97, -v67, v96, v95
	v_fmac_f32_e32 v96, v97, v94
	v_fma_f32 v67, -v67, v96, v95
	v_div_fmas_f32 v67, v67, v94, v96
	v_div_fixup_f32 v66, v67, v66, 1.0
	v_cvt_pk_bf16_f32 v96, v60, v61
	v_pk_mul_f32 v[60:61], v[60:61], v[66:67] op_sel_hi:[1,0]
	v_cvt_pk_bf16_f32 v97, v62, v63
	v_pk_mul_f32 v[62:63], v[62:63], v[66:67] op_sel_hi:[1,0]
	s_waitcnt vmcnt(2)
	v_pk_mul_f32 v[60:61], v[82:83], v[60:61]
	s_waitcnt vmcnt(1)
	v_pk_add_f32 v[82:83], v[86:87], 1.0 op_sel_hi:[1,0]
	s_nop 0
	s_waitcnt vmcnt(0)
	v_pk_fma_f32 v[166:167], v[82:83], v[60:61], v[90:91]
	v_pk_mul_f32 v[60:61], v[84:85], v[62:63]
	v_cvt_pk_fp8_f32 v67, v166, v167
	v_pk_add_f32 v[62:63], v[88:89], 1.0 op_sel_hi:[1,0]
	s_addc_u32 s27, s51, s7
	v_pk_fma_f32 v[164:165], v[62:63], v[60:61], v[92:93]
	v_lshl_add_u64 v[94:95], v[80:81], 1, s[4:5]
	v_cvt_pk_fp8_f32 v67, v164, v165 op_sel:[0,0,1]
	v_lshl_add_u64 v[60:61], s[26:27], 0, v[80:81]
	v_lshlrev_b64 v[80:81], 2, v[78:79]
	global_store_dwordx2 v[94:95], v[96:97], off
	global_store_dword v[60:61], v67, off
	v_lshl_add_u64 v[60:61], s[10:11], 0, v[80:81]
	global_load_dwordx4 v[60:63], v[60:61], off
	v_lshl_add_u64 v[82:83], s[30:31], 0, v[80:81]
	v_lshl_add_u64 v[84:85], s[28:29], 0, v[80:81]
	global_load_dwordx4 v[80:83], v[82:83], off
	s_nop 0
	global_load_dwordx4 v[84:87], v[84:85], off
	v_mov_b32_e32 v67, 0
	v_pk_mul_f32 v[98:99], v[56:57], v[66:67] op_sel_hi:[1,0]
	v_pk_mul_f32 v[96:97], v[58:59], v[66:67] op_sel_hi:[1,0]
	v_lshlrev_b64 v[88:89], 2, v[76:77]
	v_lshl_add_u64 v[94:95], v[78:79], 1, s[4:5]
	v_cvt_pk_bf16_f32 v56, v56, v57
	v_cvt_pk_bf16_f32 v57, v58, v59
	v_lshl_add_u64 v[90:91], s[10:11], 0, v[88:89]
	v_lshl_add_u64 v[78:79], s[26:27], 0, v[78:79]
	v_lshl_add_u64 v[92:93], s[28:29], 0, v[88:89]
	v_lshl_add_u64 v[88:89], s[30:31], 0, v[88:89]
	v_cmp_gt_i32_e32 vcc, 8, v160
	s_waitcnt vmcnt(2)
	v_pk_mul_f32 v[60:61], v[98:99], v[60:61]
	s_waitcnt vmcnt(1)
	v_pk_add_f32 v[80:81], v[80:81], 1.0 op_sel_hi:[1,0]
	s_waitcnt vmcnt(0)
	v_pk_fma_f32 v[170:171], v[60:61], v[80:81], v[84:85]
	v_pk_mul_f32 v[60:61], v[96:97], v[62:63]
	v_cvt_pk_fp8_f32 v67, v170, v171
	v_pk_add_f32 v[62:63], v[82:83], 1.0 op_sel_hi:[1,0]
	v_lshlrev_b64 v[82:83], 2, v[74:75]
	v_pk_fma_f32 v[168:169], v[60:61], v[62:63], v[86:87]
	v_lshl_add_u64 v[84:85], s[10:11], 0, v[82:83]
	v_cvt_pk_fp8_f32 v67, v168, v169 op_sel:[0,0,1]
	global_store_dwordx2 v[94:95], v[56:57], off
	global_store_dword v[78:79], v67, off
	global_load_dwordx4 v[56:59], v[90:91], off
	s_nop 0
	global_load_dwordx4 v[60:63], v[88:89], off
	global_load_dwordx4 v[78:81], v[92:93], off
	v_mov_b32_e32 v67, 0
	v_pk_mul_f32 v[92:93], v[52:53], v[66:67] op_sel_hi:[1,0]
	v_pk_mul_f32 v[90:91], v[54:55], v[66:67] op_sel_hi:[1,0]
	v_lshl_add_u64 v[88:89], v[76:77], 1, s[4:5]
	v_cvt_pk_bf16_f32 v52, v52, v53
	v_cvt_pk_bf16_f32 v53, v54, v55
	v_lshl_add_u64 v[76:77], s[26:27], 0, v[76:77]
	v_lshl_add_u64 v[86:87], s[28:29], 0, v[82:83]
	v_lshl_add_u64 v[82:83], s[30:31], 0, v[82:83]
	s_waitcnt vmcnt(2)
	v_pk_mul_f32 v[56:57], v[92:93], v[56:57]
	s_waitcnt vmcnt(1)
	v_pk_add_f32 v[60:61], v[60:61], 1.0 op_sel_hi:[1,0]
	s_waitcnt vmcnt(0)
	v_pk_fma_f32 v[174:175], v[56:57], v[60:61], v[78:79]
	v_pk_mul_f32 v[56:57], v[90:91], v[58:59]
	v_cvt_pk_fp8_f32 v67, v174, v175
	v_pk_add_f32 v[58:59], v[62:63], 1.0 op_sel_hi:[1,0]
	s_nop 0
	v_pk_fma_f32 v[172:173], v[56:57], v[58:59], v[80:81]
	s_nop 0
	v_cvt_pk_fp8_f32 v67, v172, v173 op_sel:[0,0,1]
	global_store_dwordx2 v[88:89], v[52:53], off
	global_store_dword v[76:77], v67, off
	global_load_dwordx4 v[52:55], v[84:85], off
	s_nop 0
	global_load_dwordx4 v[56:59], v[82:83], off
	global_load_dwordx4 v[60:63], v[86:87], off
	v_mov_b32_e32 v67, 0
	v_pk_mul_f32 v[86:87], v[48:49], v[66:67] op_sel_hi:[1,0]
	v_pk_mul_f32 v[84:85], v[50:51], v[66:67] op_sel_hi:[1,0]
	v_lshlrev_b64 v[76:77], 2, v[72:73]
	v_lshl_add_u64 v[82:83], v[74:75], 1, s[4:5]
	v_cvt_pk_bf16_f32 v48, v48, v49
	v_cvt_pk_bf16_f32 v49, v50, v51
	v_lshl_add_u64 v[78:79], s[10:11], 0, v[76:77]
	v_lshl_add_u64 v[74:75], s[26:27], 0, v[74:75]
	v_lshl_add_u64 v[80:81], s[28:29], 0, v[76:77]
	v_lshl_add_u64 v[76:77], s[30:31], 0, v[76:77]
	s_waitcnt vmcnt(2)
	v_pk_mul_f32 v[52:53], v[86:87], v[52:53]
	s_waitcnt vmcnt(1)
	v_pk_add_f32 v[56:57], v[56:57], 1.0 op_sel_hi:[1,0]
	s_waitcnt vmcnt(0)
	v_pk_fma_f32 v[178:179], v[52:53], v[56:57], v[60:61]
	v_pk_mul_f32 v[52:53], v[84:85], v[54:55]
	v_cvt_pk_fp8_f32 v67, v178, v179
	v_pk_add_f32 v[54:55], v[58:59], 1.0 op_sel_hi:[1,0]
	v_lshlrev_b64 v[60:61], 2, v[70:71]
	v_pk_fma_f32 v[176:177], v[52:53], v[54:55], v[62:63]
	v_lshl_add_u64 v[62:63], s[10:11], 0, v[60:61]
	v_cvt_pk_fp8_f32 v67, v176, v177 op_sel:[0,0,1]
	global_store_dwordx2 v[82:83], v[48:49], off
	global_store_dword v[74:75], v67, off
	global_load_dwordx4 v[48:51], v[78:79], off
	s_nop 0
	global_load_dwordx4 v[52:55], v[76:77], off
	global_load_dwordx4 v[56:59], v[80:81], off
	v_mov_b32_e32 v67, 0
	v_pk_mul_f32 v[80:81], v[44:45], v[66:67] op_sel_hi:[1,0]
	v_pk_mul_f32 v[78:79], v[46:47], v[66:67] op_sel_hi:[1,0]
	v_lshl_add_u64 v[76:77], v[72:73], 1, s[4:5]
	v_cvt_pk_bf16_f32 v44, v44, v45
	v_cvt_pk_bf16_f32 v45, v46, v47
	v_lshl_add_u64 v[72:73], s[26:27], 0, v[72:73]
	v_lshl_add_u64 v[74:75], s[28:29], 0, v[60:61]
	v_lshl_add_u64 v[60:61], s[30:31], 0, v[60:61]
	s_waitcnt vmcnt(2)
	v_pk_mul_f32 v[48:49], v[80:81], v[48:49]
	s_waitcnt vmcnt(1)
	v_pk_add_f32 v[52:53], v[52:53], 1.0 op_sel_hi:[1,0]
	s_waitcnt vmcnt(0)
	v_pk_fma_f32 v[182:183], v[48:49], v[52:53], v[56:57]
	v_pk_mul_f32 v[48:49], v[78:79], v[50:51]
	v_cvt_pk_fp8_f32 v67, v182, v183
	v_pk_add_f32 v[50:51], v[54:55], 1.0 op_sel_hi:[1,0]
	v_lshlrev_b64 v[56:57], 2, v[68:69]
	v_pk_fma_f32 v[180:181], v[48:49], v[50:51], v[58:59]
	v_lshl_add_u64 v[58:59], s[10:11], 0, v[56:57]
	v_cvt_pk_fp8_f32 v67, v180, v181 op_sel:[0,0,1]
	global_store_dwordx2 v[76:77], v[44:45], off
	global_store_dword v[72:73], v67, off
	global_load_dwordx4 v[44:47], v[62:63], off
	s_nop 0
	global_load_dwordx4 v[48:51], v[60:61], off
	global_load_dwordx4 v[52:55], v[74:75], off
	v_mov_b32_e32 v67, 0
	v_pk_mul_f32 v[74:75], v[40:41], v[66:67] op_sel_hi:[1,0]
	v_pk_mul_f32 v[72:73], v[42:43], v[66:67] op_sel_hi:[1,0]
	v_lshl_add_u64 v[62:63], v[70:71], 1, s[4:5]
	v_cvt_pk_bf16_f32 v40, v40, v41
	v_cvt_pk_bf16_f32 v41, v42, v43
	v_lshl_add_u64 v[70:71], s[26:27], 0, v[70:71]
	v_lshl_add_u64 v[60:61], s[28:29], 0, v[56:57]
	v_lshl_add_u64 v[56:57], s[30:31], 0, v[56:57]
	s_waitcnt vmcnt(2)
	v_pk_mul_f32 v[44:45], v[74:75], v[44:45]
	s_waitcnt vmcnt(1)
	v_pk_add_f32 v[48:49], v[48:49], 1.0 op_sel_hi:[1,0]
	s_waitcnt vmcnt(0)
	v_pk_fma_f32 v[186:187], v[44:45], v[48:49], v[52:53]
	v_pk_mul_f32 v[44:45], v[72:73], v[46:47]
	v_cvt_pk_fp8_f32 v67, v186, v187
	v_pk_add_f32 v[46:47], v[50:51], 1.0 op_sel_hi:[1,0]
	v_lshlrev_b64 v[52:53], 2, v[64:65]
	v_pk_fma_f32 v[184:185], v[44:45], v[46:47], v[54:55]
	v_lshl_add_u64 v[54:55], s[10:11], 0, v[52:53]
	v_cvt_pk_fp8_f32 v67, v184, v185 op_sel:[0,0,1]
	global_store_dwordx2 v[62:63], v[40:41], off
	global_store_dword v[70:71], v67, off
	global_load_dwordx4 v[40:43], v[58:59], off
	s_nop 0
	global_load_dwordx4 v[44:47], v[56:57], off
	global_load_dwordx4 v[48:51], v[60:61], off
	v_mov_b32_e32 v67, 0
	v_lshl_add_u64 v[58:59], v[68:69], 1, s[4:5]
	v_lshl_add_u64 v[60:61], s[26:27], 0, v[68:69]
	v_pk_mul_f32 v[68:69], v[36:37], v[66:67] op_sel_hi:[1,0]
	v_pk_mul_f32 v[62:63], v[38:39], v[66:67] op_sel_hi:[1,0]
	v_cvt_pk_bf16_f32 v36, v36, v37
	v_cvt_pk_bf16_f32 v37, v38, v39
	v_lshl_add_u64 v[56:57], s[28:29], 0, v[52:53]
	v_lshl_add_u64 v[52:53], s[30:31], 0, v[52:53]
	s_waitcnt vmcnt(2)
	v_pk_mul_f32 v[40:41], v[68:69], v[40:41]
	s_waitcnt vmcnt(1)
	v_pk_add_f32 v[44:45], v[44:45], 1.0 op_sel_hi:[1,0]
	s_waitcnt vmcnt(0)
	v_pk_fma_f32 v[190:191], v[40:41], v[44:45], v[48:49]
	v_pk_mul_f32 v[40:41], v[62:63], v[42:43]
	v_cvt_pk_fp8_f32 v67, v190, v191
	v_pk_add_f32 v[42:43], v[46:47], 1.0 op_sel_hi:[1,0]
	s_nop 0
	v_pk_fma_f32 v[188:189], v[40:41], v[42:43], v[50:51]
	v_lshlrev_b32_e32 v50, 4, v160
	v_cvt_pk_fp8_f32 v67, v188, v189 op_sel:[0,0,1]
	global_store_dwordx2 v[58:59], v[36:37], off
	global_store_dword v[60:61], v67, off
	global_load_dwordx4 v[36:39], v[54:55], off
	s_nop 0
	global_load_dwordx4 v[40:43], v[52:53], off
	global_load_dwordx4 v[44:47], v[56:57], off
	v_pk_mul_f32 v[62:63], v[32:33], v[66:67] op_sel_hi:[1,0]
	v_pk_mul_f32 v[60:61], v[34:35], v[66:67] op_sel_hi:[1,0]
	v_mov_b32_e32 v49, v50
	v_lshl_add_u64 v[56:57], v[64:65], 1, s[4:5]
	v_cvt_pk_bf16_f32 v32, v32, v33
	v_cvt_pk_bf16_f32 v33, v34, v35
	v_lshl_add_u64 v[58:59], s[26:27], 0, v[64:65]
	v_add_u32_e32 v51, 0x2000, v50
	v_add_u32_e32 v52, 0x4000, v50
	v_add_u32_e32 v53, 0x6000, v50
	v_add_u32_e32 v54, 0x8000, v50
	v_add_u32_e32 v55, 0xa000, v50
	v_add_u32_e32 v246, 0xc000, v50
	v_add_u32_e32 v247, 0xe000, v50
	s_waitcnt vmcnt(2)
	v_pk_mul_f32 v[36:37], v[62:63], v[36:37]
	s_waitcnt vmcnt(1)
	v_pk_add_f32 v[40:41], v[40:41], 1.0 op_sel_hi:[1,0]
	s_waitcnt vmcnt(0)
	v_pk_fma_f32 v[194:195], v[36:37], v[40:41], v[44:45]
	v_pk_mul_f32 v[36:37], v[60:61], v[38:39]
	v_cvt_pk_fp8_f32 v48, v194, v195
	v_pk_add_f32 v[38:39], v[42:43], 1.0 op_sel_hi:[1,0]
	s_nop 0
	v_pk_fma_f32 v[192:193], v[36:37], v[38:39], v[46:47]
	s_nop 0
	v_cvt_pk_fp8_f32 v48, v192, v193 op_sel:[0,0,1]
	global_store_dwordx2 v[56:57], v[32:33], off
	global_store_dword v[58:59], v48, off
	s_nop 0
	v_add_u32_e32 v48, 0, v49
	ds_read_b128 v[32:35], v48
	ds_read_b128 v[36:39], v48 offset:1024
	ds_read_b128 v[40:43], v48 offset:2048
	ds_read_b128 v[44:47], v48 offset:3072
	ds_read_b128 v[56:59], v48 offset:4096
	ds_read_b128 v[60:63], v48 offset:5120
	ds_read_b128 v[64:67], v48 offset:6144
	ds_read_b128 v[68:71], v48 offset:7168
	s_waitcnt lgkmcnt(7)
	v_mul_f32_e32 v33, v167, v33
	v_add_u32_e32 v72, 0, v51
	ds_read_b128 v[48:51], v72
	ds_read_b128 v[94:97], v72 offset:1024
	ds_read_b128 v[98:101], v72 offset:2048
	ds_read_b128 v[102:105], v72 offset:3072
	ds_read_b128 v[106:109], v72 offset:4096
	ds_read_b128 v[110:113], v72 offset:5120
	ds_read_b128 v[114:117], v72 offset:6144
	ds_read_b128 v[118:121], v72 offset:7168
	s_waitcnt lgkmcnt(14)
	v_mul_f32_e32 v37, v171, v37
	v_fmac_f32_e32 v33, v166, v32
	v_add_u32_e32 v52, 0, v52
	s_waitcnt lgkmcnt(13)
	v_mul_f32_e32 v41, v175, v41
	v_fmac_f32_e32 v37, v170, v36
	v_fmac_f32_e32 v33, v164, v34
	s_waitcnt lgkmcnt(7)
	v_mul_f32_e32 v32, v167, v49
	ds_read_b128 v[214:217], v52
	ds_read_b128 v[218:221], v52 offset:1024
	ds_read_b128 v[222:225], v52 offset:2048
	ds_read_b128 v[226:229], v52 offset:3072
	ds_read_b128 v[230:233], v52 offset:4096
	ds_read_b128 v[234:237], v52 offset:5120
	ds_read_b128 v[238:241], v52 offset:6144
	ds_read_b128 v[242:245], v52 offset:7168
	v_mul_f32_e32 v45, v179, v45
	v_fmac_f32_e32 v41, v174, v40
	v_fmac_f32_e32 v37, v168, v38
	s_waitcnt lgkmcnt(14)
	v_mul_f32_e32 v34, v171, v95
	v_fmac_f32_e32 v33, v165, v35
	v_fmac_f32_e32 v32, v166, v48
	v_mul_f32_e32 v248, v183, v57
	v_mul_f32_e32 v209, v191, v65
	v_mul_f32_e32 v206, v195, v69
	v_fmac_f32_e32 v45, v178, v44
	v_fmac_f32_e32 v41, v172, v42
	s_waitcnt lgkmcnt(13)
	v_mul_f32_e32 v250, v175, v99
	v_fmac_f32_e32 v37, v169, v39
	v_fmac_f32_e32 v34, v170, v94
	v_add_f32_e32 v33, 0, v33
	v_fmac_f32_e32 v32, v164, v50
	s_waitcnt lgkmcnt(7)
	v_mul_f32_e32 v215, v167, v215
	v_mul_f32_e32 v249, v187, v61
	v_add_u32_e32 v52, 0, v53
	v_fmac_f32_e32 v248, v182, v56
	v_fmac_f32_e32 v209, v190, v64
	v_fmac_f32_e32 v206, v194, v68
	v_fmac_f32_e32 v45, v176, v46
	v_mul_f32_e32 v251, v179, v103
	v_fmac_f32_e32 v41, v173, v43
	v_fmac_f32_e32 v250, v174, v98
	v_fmac_f32_e32 v34, v168, v96
	s_waitcnt lgkmcnt(6)
	v_mul_f32_e32 v219, v171, v219
	v_add_f32_e32 v33, v33, v37
	v_fmac_f32_e32 v32, v165, v51
	v_fmac_f32_e32 v215, v166, v214
	v_fmac_f32_e32 v249, v186, v60
	ds_read_b128 v[128:131], v52
	ds_read_b128 v[132:135], v52 offset:1024
	ds_read_b128 v[136:139], v52 offset:2048
	ds_read_b128 v[140:143], v52 offset:3072
	ds_read_b128 v[144:147], v52 offset:4096
	ds_read_b128 v[148:151], v52 offset:5120
	ds_read_b128 v[152:155], v52 offset:6144
	ds_read_b128 v[156:159], v52 offset:7168
	v_fmac_f32_e32 v248, v180, v58
	v_fmac_f32_e32 v209, v188, v66
	v_fmac_f32_e32 v206, v192, v70
	v_mul_f32_e32 v212, v183, v107
	v_mul_f32_e32 v210, v187, v111
	v_mul_f32_e32 v207, v191, v115
	v_mul_f32_e32 v205, v195, v119
	v_add_u32_e32 v36, 0, v54
	v_fmac_f32_e32 v45, v177, v47
	v_fmac_f32_e32 v251, v178, v102
	v_fmac_f32_e32 v250, v172, v100
	s_waitcnt lgkmcnt(13)
	v_mul_f32_e32 v223, v175, v223
	v_fmac_f32_e32 v34, v169, v97
	v_fmac_f32_e32 v219, v170, v218
	v_add_f32_e32 v33, v33, v41
	v_add_f32_e32 v32, 0, v32
	v_fmac_f32_e32 v215, v164, v216
	s_waitcnt lgkmcnt(7)
	v_mul_f32_e32 v216, v167, v129
	v_fmac_f32_e32 v249, v184, v62
	v_fmac_f32_e32 v248, v181, v59
	v_fmac_f32_e32 v209, v189, v67
	v_fmac_f32_e32 v206, v193, v71
	v_fmac_f32_e32 v212, v182, v106
	v_fmac_f32_e32 v210, v186, v110
	v_fmac_f32_e32 v207, v190, v114
	v_fmac_f32_e32 v205, v194, v118
	ds_read_b128 v[64:67], v36
	ds_read_b128 v[68:71], v36 offset:1024
	ds_read_b128 v[72:75], v36 offset:2048
	ds_read_b128 v[76:79], v36 offset:3072
	ds_read_b128 v[80:83], v36 offset:4096
	ds_read_b128 v[84:87], v36 offset:5120
	ds_read_b128 v[88:91], v36 offset:6144
	ds_read_b128 v[92:95], v36 offset:7168
	v_fmac_f32_e32 v251, v176, v104
	v_mul_f32_e32 v227, v179, v227
	v_fmac_f32_e32 v250, v173, v101
	v_fmac_f32_e32 v223, v174, v222
	v_fmac_f32_e32 v219, v168, v220
	s_waitcnt lgkmcnt(14)
	v_mul_f32_e32 v218, v171, v133
	v_add_f32_e32 v129, v33, v45
	v_add_f32_e32 v133, v32, v34
	v_fmac_f32_e32 v215, v165, v217
	v_fmac_f32_e32 v216, v166, v128
	v_fmac_f32_e32 v249, v185, v63
	v_fmac_f32_e32 v212, v180, v108
	v_fmac_f32_e32 v210, v184, v112
	v_fmac_f32_e32 v207, v188, v116
	v_fmac_f32_e32 v205, v192, v120
	v_mul_f32_e32 v213, v183, v231
	v_add_u32_e32 v35, 0, v55
	v_fmac_f32_e32 v251, v177, v105
	v_fmac_f32_e32 v227, v178, v226
	v_fmac_f32_e32 v223, v172, v224
	s_waitcnt lgkmcnt(13)
	v_mul_f32_e32 v220, v175, v137
	v_fmac_f32_e32 v219, v169, v221
	v_fmac_f32_e32 v218, v170, v132
	v_add_f32_e32 v128, v129, v248
	v_add_f32_e32 v129, v133, v250
	v_add_f32_e32 v132, 0, v215
	v_fmac_f32_e32 v216, v164, v130
	s_waitcnt lgkmcnt(7)
	v_mul_f32_e32 v65, v167, v65
	v_mul_f32_e32 v211, v187, v235
	v_fmac_f32_e32 v212, v181, v109
	v_fmac_f32_e32 v210, v185, v113
	v_fmac_f32_e32 v207, v189, v117
	v_fmac_f32_e32 v205, v193, v121
	v_fmac_f32_e32 v213, v182, v230
	ds_read_b128 v[96:99], v35
	ds_read_b128 v[100:103], v35 offset:1024
	ds_read_b128 v[104:107], v35 offset:2048
	ds_read_b128 v[108:111], v35 offset:3072
	ds_read_b128 v[112:115], v35 offset:4096
	ds_read_b128 v[116:119], v35 offset:5120
	ds_read_b128 v[120:123], v35 offset:6144
	ds_read_b128 v[124:127], v35 offset:7168
	v_fmac_f32_e32 v227, v176, v228
	v_mul_f32_e32 v222, v179, v141
	v_add_u32_e32 v60, 0, v246
	v_fmac_f32_e32 v223, v173, v225
	v_fmac_f32_e32 v220, v174, v136
	v_fmac_f32_e32 v218, v168, v134
	s_waitcnt lgkmcnt(14)
	v_mul_f32_e32 v69, v171, v69
	s_waitcnt lgkmcnt(13)
	v_mul_f32_e32 v73, v175, v73
	s_waitcnt lgkmcnt(12)
	v_mul_f32_e32 v77, v179, v77
	v_add_f32_e32 v215, v128, v249
	v_add_f32_e32 v217, v129, v251
	v_add_f32_e32 v219, v132, v219
	v_fmac_f32_e32 v216, v165, v131
	v_fmac_f32_e32 v65, v166, v64
	v_mul_f32_e32 v208, v191, v239
	v_fmac_f32_e32 v211, v186, v234
	v_fmac_f32_e32 v213, v180, v232
	v_mul_f32_e32 v214, v183, v145
	v_fmac_f32_e32 v227, v177, v229
	v_fmac_f32_e32 v222, v178, v140
	ds_read_b128 v[32:35], v60
	ds_read_b128 v[36:39], v60 offset:1024
	ds_read_b128 v[40:43], v60 offset:2048
	ds_read_b128 v[44:47], v60 offset:3072
	ds_read_b128 v[48:51], v60 offset:4096
	ds_read_b128 v[52:55], v60 offset:5120
	ds_read_b128 v[56:59], v60 offset:6144
	ds_read_b128 v[60:63], v60 offset:7168
	v_fmac_f32_e32 v220, v172, v138
	v_fmac_f32_e32 v218, v169, v135
	v_fmac_f32_e32 v69, v170, v68
	v_fmac_f32_e32 v73, v174, v72
	v_fmac_f32_e32 v77, v178, v76
	v_add_f32_e32 v64, v215, v209
	v_add_f32_e32 v68, v217, v212
	v_add_f32_e32 v72, v219, v223
	v_add_f32_e32 v76, 0, v216
	v_fmac_f32_e32 v65, v164, v66
	s_waitcnt lgkmcnt(14)
	v_mul_f32_e32 v66, v167, v97
	v_mul_f32_e32 v203, v195, v243
	v_fmac_f32_e32 v208, v190, v238
	v_fmac_f32_e32 v211, v184, v236
	v_mul_f32_e32 v204, v187, v149
	v_mul_f32_e32 v163, v191, v153
	v_mul_f32_e32 v161, v195, v157
	v_fmac_f32_e32 v213, v181, v233
	v_fmac_f32_e32 v214, v182, v144
	v_fmac_f32_e32 v222, v176, v142
	v_fmac_f32_e32 v220, v173, v139
	v_fmac_f32_e32 v69, v168, v70
	v_mul_f32_e32 v70, v171, v101
	v_add_f32_e32 v64, v64, v206
	v_add_f32_e32 v68, v68, v210
	v_add_f32_e32 v72, v72, v227
	v_add_f32_e32 v76, v76, v218
	v_fmac_f32_e32 v65, v165, v67
	v_fmac_f32_e32 v66, v166, v96
	v_fmac_f32_e32 v203, v194, v242
	v_fmac_f32_e32 v208, v188, v240
	v_fmac_f32_e32 v211, v185, v237
	v_fmac_f32_e32 v204, v186, v148
	v_fmac_f32_e32 v163, v190, v152
	v_fmac_f32_e32 v161, v194, v156
	v_fmac_f32_e32 v214, v180, v146
	v_mul_f32_e32 v81, v183, v81
	v_fmac_f32_e32 v222, v177, v143
	v_fmac_f32_e32 v73, v172, v74
	s_waitcnt lgkmcnt(13)
	v_mul_f32_e32 v74, v175, v105
	v_fmac_f32_e32 v69, v169, v71
	v_fmac_f32_e32 v70, v170, v100
	v_add_f32_dpp v64, v64, v64 quad_perm:[1,0,3,2] row_mask:0xf bank_mask:0xf bound_ctrl:1
	v_add_f32_e32 v67, v68, v207
	v_add_f32_e32 v68, v72, v213
	v_add_f32_e32 v71, v76, v220
	v_add_f32_e32 v65, 0, v65
	v_fmac_f32_e32 v66, v164, v98
	s_waitcnt lgkmcnt(7)
	v_mul_f32_e32 v33, v167, v33
	v_fmac_f32_e32 v203, v192, v244
	v_fmac_f32_e32 v208, v189, v241
	v_fmac_f32_e32 v204, v184, v150
	v_fmac_f32_e32 v163, v188, v154
	v_fmac_f32_e32 v161, v192, v158
	v_mul_f32_e32 v85, v187, v85
	v_add_u32_e32 v152, 0, v247
	v_fmac_f32_e32 v214, v181, v147
	v_fmac_f32_e32 v81, v182, v80
	v_fmac_f32_e32 v77, v176, v78
	v_mul_f32_e32 v78, v179, v109
	v_fmac_f32_e32 v73, v173, v75
	v_fmac_f32_e32 v74, v174, v104
	v_fmac_f32_e32 v70, v168, v102
	s_waitcnt lgkmcnt(6)
	v_mul_f32_e32 v37, v171, v37
	s_waitcnt lgkmcnt(5)
	v_mul_f32_e32 v41, v175, v41
	s_waitcnt lgkmcnt(4)
	v_mul_f32_e32 v45, v179, v45
	s_waitcnt lgkmcnt(3)
	v_mul_f32_e32 v49, v183, v49
	s_waitcnt lgkmcnt(2)
	v_mul_f32_e32 v53, v187, v53
	v_add_f32_dpp v64, v64, v64 quad_perm:[2,3,0,1] row_mask:0xf bank_mask:0xf bound_ctrl:1
	v_add_f32_e32 v67, v67, v205
	v_add_f32_e32 v68, v68, v211
	v_add_f32_e32 v71, v71, v222
	v_add_f32_e32 v65, v65, v69
	v_fmac_f32_e32 v66, v165, v99
	v_fmac_f32_e32 v33, v166, v32
	v_fmac_f32_e32 v203, v193, v245
	v_mul_f32_e32 v89, v191, v89
	v_fmac_f32_e32 v204, v185, v151
	v_fmac_f32_e32 v163, v189, v155
	v_fmac_f32_e32 v161, v193, v159
	v_fmac_f32_e32 v85, v186, v84
	ds_read_b128 v[128:131], v152
	ds_read_b128 v[132:135], v152 offset:1024
	ds_read_b128 v[136:139], v152 offset:2048
	ds_read_b128 v[140:143], v152 offset:3072
	ds_read_b128 v[144:147], v152 offset:4096
	ds_read_b128 v[148:151], v152 offset:5120
	ds_read_b128 v[156:159], v152 offset:6144
	ds_read_b128 v[152:155], v152 offset:7168
	v_fmac_f32_e32 v81, v180, v82
	v_mul_f32_e32 v80, v183, v113
	v_fmac_f32_e32 v77, v177, v79
	v_fmac_f32_e32 v78, v178, v108
	v_fmac_f32_e32 v74, v172, v106
	v_fmac_f32_e32 v70, v169, v103
	v_fmac_f32_e32 v37, v170, v36
	v_fmac_f32_e32 v41, v174, v40
	v_fmac_f32_e32 v45, v178, v44
	v_fmac_f32_e32 v49, v182, v48
	v_fmac_f32_e32 v53, v186, v52
	v_add_f32_dpp v32, v64, v64 row_half_mirror row_mask:0xf bank_mask:0xf bound_ctrl:1
	v_add_f32_dpp v36, v67, v67 quad_perm:[1,0,3,2] row_mask:0xf bank_mask:0xf bound_ctrl:1
	v_add_f32_e32 v40, v68, v208
	v_add_f32_e32 v44, v71, v214
	v_add_f32_e32 v48, v65, v73
	v_add_f32_e32 v52, 0, v66
	v_fmac_f32_e32 v33, v164, v34
	s_waitcnt lgkmcnt(7)
	v_mul_f32_e32 v34, v167, v129
	v_mul_f32_e32 v93, v195, v93
	v_fmac_f32_e32 v89, v190, v88
	v_fmac_f32_e32 v85, v184, v86
	v_mul_f32_e32 v82, v187, v117
	v_fmac_f32_e32 v81, v181, v83
	v_fmac_f32_e32 v80, v182, v112
	v_fmac_f32_e32 v78, v176, v110
	v_fmac_f32_e32 v74, v173, v107
	v_fmac_f32_e32 v37, v168, v38
	s_waitcnt lgkmcnt(6)
	v_mul_f32_e32 v38, v171, v133
	v_add_f32_dpp v32, v32, v32 row_mirror row_mask:0xf bank_mask:0xf bound_ctrl:1
	v_add_f32_dpp v36, v36, v36 quad_perm:[2,3,0,1] row_mask:0xf bank_mask:0xf bound_ctrl:1
	v_add_f32_e32 v40, v40, v203
	v_add_f32_e32 v44, v44, v204
	v_add_f32_e32 v48, v48, v77
	v_add_f32_e32 v52, v52, v70
	v_fmac_f32_e32 v33, v165, v35
	v_fmac_f32_e32 v34, v166, v128
	v_fmac_f32_e32 v93, v194, v92
	v_fmac_f32_e32 v89, v188, v90
	v_mul_f32_e32 v84, v191, v121
	v_fmac_f32_e32 v85, v185, v87
	v_fmac_f32_e32 v82, v186, v116
	v_fmac_f32_e32 v80, v180, v114
	v_fmac_f32_e32 v78, v177, v111
	v_fmac_f32_e32 v41, v172, v42
	s_waitcnt lgkmcnt(5)
	v_mul_f32_e32 v42, v175, v137
	v_fmac_f32_e32 v37, v169, v39
	v_fmac_f32_e32 v38, v170, v132
	v_readlane_b32 s26, v32, 0
	v_readlane_b32 s23, v32, 16
	v_readlane_b32 s27, v32, 32
	v_readlane_b32 s57, v32, 48
	v_add_f32_dpp v32, v36, v36 row_half_mirror row_mask:0xf bank_mask:0xf bound_ctrl:1
	v_add_f32_dpp v35, v40, v40 quad_perm:[1,0,3,2] row_mask:0xf bank_mask:0xf bound_ctrl:1
	v_add_f32_e32 v36, v44, v163
	v_add_f32_e32 v39, v48, v81
	v_add_f32_e32 v40, v52, v74
	v_add_f32_e32 v33, 0, v33
	v_fmac_f32_e32 v34, v164, v130
	v_fmac_f32_e32 v93, v192, v94
	v_mul_f32_e32 v86, v195, v125
	v_fmac_f32_e32 v89, v189, v91
	v_fmac_f32_e32 v84, v190, v120
	v_fmac_f32_e32 v82, v184, v118
	v_fmac_f32_e32 v80, v181, v115
	v_fmac_f32_e32 v45, v176, v46
	s_waitcnt lgkmcnt(4)
	v_mul_f32_e32 v46, v179, v141
	v_fmac_f32_e32 v41, v173, v43
	v_fmac_f32_e32 v42, v174, v136
	v_fmac_f32_e32 v38, v168, v134
	v_add_f32_dpp v32, v32, v32 row_mirror row_mask:0xf bank_mask:0xf bound_ctrl:1
	v_add_f32_dpp v35, v35, v35 quad_perm:[2,3,0,1] row_mask:0xf bank_mask:0xf bound_ctrl:1
	v_add_f32_e32 v36, v36, v161
	v_add_f32_e32 v39, v39, v85
	v_add_f32_e32 v40, v40, v78
	v_add_f32_e32 v33, v33, v37
	v_fmac_f32_e32 v34, v165, v131
	v_fmac_f32_e32 v93, v193, v95
	v_fmac_f32_e32 v86, v194, v124
	v_fmac_f32_e32 v84, v188, v122
	v_mul_f32_e32 v57, v191, v57
	v_fmac_f32_e32 v82, v185, v119
	v_fmac_f32_e32 v49, v180, v50
	s_waitcnt lgkmcnt(3)
	v_mul_f32_e32 v50, v183, v145
	v_fmac_f32_e32 v45, v177, v47
	v_fmac_f32_e32 v46, v178, v140
	v_fmac_f32_e32 v42, v172, v138
	v_fmac_f32_e32 v38, v169, v135
	v_readlane_b32 s28, v32, 0
	v_readlane_b32 s58, v32, 16
	v_readlane_b32 s29, v32, 32
	v_readlane_b32 s59, v32, 48
	v_add_f32_dpp v32, v35, v35 row_half_mirror row_mask:0xf bank_mask:0xf bound_ctrl:1
	v_add_f32_dpp v35, v36, v36 quad_perm:[1,0,3,2] row_mask:0xf bank_mask:0xf bound_ctrl:1
	v_add_f32_e32 v36, v39, v89
	v_add_f32_e32 v37, v40, v80
	v_add_f32_e32 v33, v33, v41
	v_add_f32_e32 v34, 0, v34
	v_fmac_f32_e32 v86, v192, v126
	v_mul_f32_e32 v61, v195, v61
	v_fmac_f32_e32 v84, v189, v123
	v_fmac_f32_e32 v57, v190, v56
	v_fmac_f32_e32 v53, v184, v54
	s_waitcnt lgkmcnt(2)
	v_mul_f32_e32 v54, v187, v149
	v_fmac_f32_e32 v49, v181, v51
	v_fmac_f32_e32 v50, v182, v144
	v_fmac_f32_e32 v46, v176, v142
	v_fmac_f32_e32 v42, v173, v139
	v_add_f32_dpp v32, v32, v32 row_mirror row_mask:0xf bank_mask:0xf bound_ctrl:1
	v_add_f32_dpp v35, v35, v35 quad_perm:[2,3,0,1] row_mask:0xf bank_mask:0xf bound_ctrl:1
	v_add_f32_e32 v36, v36, v93
	v_add_f32_e32 v37, v37, v82
	v_add_f32_e32 v33, v33, v45
	v_add_f32_e32 v34, v34, v38
	v_fmac_f32_e32 v86, v193, v127
	v_fmac_f32_e32 v61, v194, v60
	v_fmac_f32_e32 v57, v188, v58
	s_waitcnt lgkmcnt(1)
	v_mul_f32_e32 v56, v191, v157
	v_fmac_f32_e32 v53, v185, v55
	v_fmac_f32_e32 v54, v186, v148
	v_fmac_f32_e32 v50, v180, v146
	v_fmac_f32_e32 v46, v177, v143
	v_readlane_b32 s30, v32, 0
	v_readlane_b32 s60, v32, 16
	v_readlane_b32 s31, v32, 32
	v_readlane_b32 s61, v32, 48
	v_add_f32_dpp v32, v35, v35 row_half_mirror row_mask:0xf bank_mask:0xf bound_ctrl:1
	v_add_f32_dpp v35, v36, v36 quad_perm:[1,0,3,2] row_mask:0xf bank_mask:0xf bound_ctrl:1
	v_add_f32_e32 v36, v37, v84
	v_add_f32_e32 v33, v33, v49
	v_add_f32_e32 v34, v34, v42
	v_fmac_f32_e32 v61, v192, v62
	s_waitcnt lgkmcnt(0)
	v_mul_f32_e32 v58, v195, v153
	v_fmac_f32_e32 v57, v189, v59
	v_fmac_f32_e32 v56, v190, v156
	v_fmac_f32_e32 v54, v184, v150
	v_fmac_f32_e32 v50, v181, v147
	v_add_f32_dpp v32, v32, v32 row_mirror row_mask:0xf bank_mask:0xf bound_ctrl:1
	v_add_f32_dpp v35, v35, v35 quad_perm:[2,3,0,1] row_mask:0xf bank_mask:0xf bound_ctrl:1
	v_add_f32_e32 v36, v36, v86
	v_add_f32_e32 v33, v33, v53
	v_add_f32_e32 v34, v34, v46
	v_fmac_f32_e32 v61, v193, v63
	v_fmac_f32_e32 v58, v194, v152
	v_fmac_f32_e32 v56, v188, v158
	v_fmac_f32_e32 v54, v185, v151
	v_readlane_b32 s34, v32, 0
	v_readlane_b32 s62, v32, 16
	v_readlane_b32 s35, v32, 32
	v_readlane_b32 s63, v32, 48
	v_add_f32_dpp v32, v35, v35 row_half_mirror row_mask:0xf bank_mask:0xf bound_ctrl:1
	v_add_f32_dpp v35, v36, v36 quad_perm:[1,0,3,2] row_mask:0xf bank_mask:0xf bound_ctrl:1
	v_add_f32_e32 v33, v33, v57
	v_add_f32_e32 v34, v34, v50
	v_fmac_f32_e32 v58, v192, v154
	v_fmac_f32_e32 v56, v189, v159
	v_add_f32_dpp v32, v32, v32 row_mirror row_mask:0xf bank_mask:0xf bound_ctrl:1
	v_add_f32_dpp v35, v35, v35 quad_perm:[2,3,0,1] row_mask:0xf bank_mask:0xf bound_ctrl:1
	v_add_f32_e32 v33, v33, v61
	v_add_f32_e32 v34, v34, v54
	v_fmac_f32_e32 v58, v193, v155
	v_readlane_b32 s36, v32, 0
	v_readlane_b32 s64, v32, 16
	v_readlane_b32 s37, v32, 32
	v_readlane_b32 s65, v32, 48
	v_add_f32_dpp v32, v35, v35 row_half_mirror row_mask:0xf bank_mask:0xf bound_ctrl:1
	v_add_f32_dpp v33, v33, v33 quad_perm:[1,0,3,2] row_mask:0xf bank_mask:0xf bound_ctrl:1
	v_add_f32_e32 v34, v34, v56
	v_add_f32_dpp v32, v32, v32 row_mirror row_mask:0xf bank_mask:0xf bound_ctrl:1
	v_add_f32_dpp v33, v33, v33 quad_perm:[2,3,0,1] row_mask:0xf bank_mask:0xf bound_ctrl:1
	v_add_f32_e32 v34, v34, v58
	v_readlane_b32 s38, v32, 0
	v_readlane_b32 s66, v32, 16
	v_readlane_b32 s39, v32, 32
	v_readlane_b32 s67, v32, 48
	v_add_f32_dpp v32, v33, v33 row_half_mirror row_mask:0xf bank_mask:0xf bound_ctrl:1
	v_add_f32_dpp v33, v34, v34 quad_perm:[1,0,3,2] row_mask:0xf bank_mask:0xf bound_ctrl:1
	s_nop 0
	v_add_f32_dpp v32, v32, v32 row_mirror row_mask:0xf bank_mask:0xf bound_ctrl:1
	v_add_f32_dpp v33, v33, v33 quad_perm:[2,3,0,1] row_mask:0xf bank_mask:0xf bound_ctrl:1
	v_readlane_b32 s40, v32, 0
	v_readlane_b32 s68, v32, 16
	v_readlane_b32 s41, v32, 32
	v_readlane_b32 s69, v32, 48
	v_add_f32_dpp v32, v33, v33 row_half_mirror row_mask:0xf bank_mask:0xf bound_ctrl:1
	s_nop 1
	v_add_f32_dpp v32, v32, v32 row_mirror row_mask:0xf bank_mask:0xf bound_ctrl:1
	s_nop 0
	v_readlane_b32 s42, v32, 0
	v_readlane_b32 s70, v32, 16
	v_readlane_b32 s43, v32, 32
	v_readlane_b32 s71, v32, 48
	s_and_saveexec_b64 s[4:5], vcc
	s_cbranch_execz .LBB0_138
	v_ashrrev_i32_e32 v161, 31, v160
	v_lshlrev_b64 v[32:33], 2, v[160:161]
	v_lshl_add_u64 v[34:35], s[12:13], 0, v[32:33]
	global_load_dword v50, v[34:35], off
	v_mov_b32_e32 v34, s70
	v_mov_b32_e32 v35, s71
	v_mov_b32_e32 v36, s68
	v_mov_b32_e32 v37, s69
	v_mov_b32_e32 v40, s64
	v_mov_b32_e32 v41, s65
	v_mov_b32_e32 v46, s58
	v_mov_b32_e32 v47, s59
	v_mov_b32_e32 v48, s23
	v_mov_b32_e32 v49, s57
	v_mov_b32_e32 v38, s66
	v_mov_b32_e32 v39, s67
	v_mov_b32_e32 v44, s60
	v_mov_b32_e32 v45, s61
	v_pk_add_f32 v[34:35], s[42:43], v[34:35]
	v_pk_add_f32 v[36:37], s[40:41], v[36:37]
	v_pk_add_f32 v[40:41], s[36:37], v[40:41]
	v_pk_add_f32 v[46:47], s[28:29], v[46:47]
	v_pk_add_f32 v[48:49], s[26:27], v[48:49]
	v_mov_b32_e32 v42, s62
	v_mov_b32_e32 v43, s63
	v_pk_add_f32 v[38:39], s[38:39], v[38:39]
	v_pk_add_f32 v[44:45], s[30:31], v[44:45]
	v_add_f32_e32 v34, v34, v35
	v_add_f32_e32 v35, v36, v37
	v_add_f32_e32 v37, v40, v41
	v_add_f32_e32 v40, v46, v47
	v_add_f32_e32 v41, v48, v49
	v_cmp_eq_u32_e32 vcc, 1, v160
	v_pk_add_f32 v[42:43], s[34:35], v[42:43]
	v_add_f32_e32 v36, v38, v39
	v_add_f32_e32 v39, v44, v45
	v_cndmask_b32_e32 v40, v41, v40, vcc
	v_cmp_eq_u32_e32 vcc, 2, v160
	v_add_f32_e32 v38, v42, v43
	s_add_u32 s26, s46, s6
	v_cndmask_b32_e32 v39, v40, v39, vcc
	v_cmp_eq_u32_e32 vcc, 3, v160
	s_addc_u32 s27, s47, s7
	v_lshl_add_u64 v[32:33], s[26:27], 0, v[32:33]
	v_cndmask_b32_e32 v38, v39, v38, vcc
	v_cmp_eq_u32_e32 vcc, 4, v160
	s_nop 1
	v_cndmask_b32_e32 v37, v38, v37, vcc
	v_cmp_eq_u32_e32 vcc, 5, v160
	s_nop 1
	v_cndmask_b32_e32 v36, v37, v36, vcc
	v_cmp_eq_u32_e32 vcc, 6, v160
	s_nop 1
	v_cndmask_b32_e32 v35, v36, v35, vcc
	v_cmp_eq_u32_e32 vcc, 7, v160
	s_nop 1
	v_cndmask_b32_e32 v34, v35, v34, vcc
	s_waitcnt vmcnt(0)
	v_add_f32_e32 v34, v34, v50
	v_mul_f32_e64 v35, |v34|, s52
	v_exp_f32_e32 v48, v35
	v_min_f32_e32 v49, 0, v34
	v_add_f32_e32 v36, 1.0, v48
	v_add_f32_e32 v37, -1.0, v36
	v_frexp_mant_f32_e32 v38, v36
	v_cvt_f64_f32_e32 v[34:35], v36
	v_sub_f32_e32 v39, v37, v36
	v_frexp_exp_i32_f64_e32 v34, v[34:35]
	v_cmp_gt_f32_e32 vcc, s53, v38
	v_sub_f32_e32 v37, v48, v37
	v_add_f32_e32 v35, 1.0, v39
	v_subbrev_co_u32_e32 v34, vcc, 0, v34, vcc
	v_add_f32_e32 v35, v37, v35
	v_sub_u32_e32 v37, 0, v34
	v_ldexp_f32 v36, v36, v37
	v_add_f32_e32 v38, -1.0, v36
	v_add_f32_e32 v39, 1.0, v36
	v_ldexp_f32 v35, v35, v37
	v_add_f32_e32 v37, 1.0, v38
	v_add_f32_e32 v40, -1.0, v39
	v_sub_f32_e32 v37, v36, v37
	v_sub_f32_e32 v36, v36, v40
	v_add_f32_e32 v40, v35, v37
	v_add_f32_e32 v35, v35, v36
	v_add_f32_e32 v42, v39, v35
	v_rcp_f32_e32 v43, v42
	v_add_f32_e32 v37, v38, v40
	v_sub_f32_e32 v38, v37, v38
	v_sub_f32_e32 v36, v42, v39
	v_mul_f32_e32 v45, v37, v43
	v_sub_f32_e32 v44, v40, v38
	v_mul_f32_e32 v38, v42, v45
	v_sub_f32_e32 v35, v35, v36
	v_fma_f32 v40, v45, v42, -v38
	v_fmac_f32_e32 v40, v45, v35
	v_add_f32_e32 v36, v38, v40
	v_sub_f32_e32 v39, v37, v36
	v_mov_b32_e32 v41, v36
	v_pk_add_f32 v[36:37], v[36:37], v[38:39] neg_lo:[0,1] neg_hi:[0,1]
	v_cvt_f32_i32_e32 v34, v34
	v_pk_add_f32 v[36:37], v[36:37], v[40:41] neg_lo:[0,1] neg_hi:[0,1]
	v_cmp_neq_f32_e32 vcc, s55, v48
	v_add_f32_e32 v37, v44, v37
	v_add_f32_e32 v36, v36, v37
	v_add_f32_e32 v37, v39, v36
	v_mul_f32_e32 v41, v43, v37
	v_mul_f32_e32 v38, v42, v41
	v_sub_f32_e32 v39, v39, v37
	v_add_f32_e32 v46, v45, v41
	v_fma_f32 v40, v41, v42, -v38
	v_add_f32_e32 v44, v36, v39
	v_sub_f32_e32 v36, v46, v45
	v_fmac_f32_e32 v40, v41, v35
	v_sub_f32_e32 v35, v41, v36
	v_add_f32_e32 v36, v38, v40
	v_sub_f32_e32 v39, v37, v36
	v_mov_b32_e32 v41, v36
	v_pk_add_f32 v[36:37], v[36:37], v[38:39] neg_lo:[0,1] neg_hi:[0,1]
	s_nop 0
	v_pk_add_f32 v[36:37], v[36:37], v[40:41] neg_lo:[0,1] neg_hi:[0,1]
	s_nop 0
	v_add_f32_e32 v37, v44, v37
	v_add_f32_e32 v36, v36, v37
	v_add_f32_e32 v36, v39, v36
	v_mul_f32_e32 v36, v43, v36
	v_add_f32_e32 v35, v35, v36
	v_add_f32_e32 v36, v46, v35
	v_mul_f32_e32 v38, v36, v36
	v_sub_f32_e32 v39, v36, v46
	v_fmamk_f32 v40, v38, 0x3e9b6dac, v199
	v_sub_f32_e32 v39, v35, v39
	v_mul_f32_e32 v35, v36, v38
	v_fmaak_f32 v163, v38, v40, 0x3f2aaada
	v_ldexp_f32 v41, v39, 1
	v_pk_mul_f32 v[38:39], v[34:35], v[162:163]
	v_ldexp_f32 v37, v36, 1
	v_fma_f32 v36, v34, s54, -v38
	v_fmac_f32_e32 v36, 0xb102e308, v34
	v_pk_add_f32 v[34:35], v[38:39], v[36:37]
	v_mov_b32_e32 v40, v38
	v_sub_f32_e32 v44, v35, v37
	v_pk_add_f32 v[42:43], v[34:35], v[38:39] neg_lo:[0,1] neg_hi:[0,1]
	v_sub_f32_e32 v38, v39, v44
	v_add_f32_e32 v41, v41, v38
	v_pk_add_f32 v[38:39], v[34:35], v[40:41]
	v_mov_b32_e32 v37, v34
	v_mov_b32_e32 v43, v39
	v_pk_add_f32 v[46:47], v[36:37], v[42:43] neg_lo:[0,1] neg_hi:[0,1]
	v_pk_add_f32 v[36:37], v[36:37], v[42:43]
	v_mov_b32_e32 v44, v39
	v_pk_add_f32 v[42:43], v[36:37], v[34:35] op_sel:[1,0] op_sel_hi:[0,1] neg_lo:[0,1] neg_hi:[0,1]
	v_mov_b32_e32 v45, v37
	v_pk_add_f32 v[38:39], v[38:39], v[42:43] op_sel_hi:[1,0] neg_lo:[0,1] neg_hi:[0,1]
	v_pk_mov_b32 v[42:43], v[34:35], v[42:43] op_sel:[1,0]
	v_mov_b32_e32 v40, v41
	v_pk_add_f32 v[42:43], v[44:45], v[42:43] neg_lo:[0,1] neg_hi:[0,1]
	v_mov_b32_e32 v41, v34
	v_pk_add_f32 v[34:35], v[40:41], v[42:43] neg_lo:[0,1] neg_hi:[0,1]
	v_mov_b32_e32 v38, v46
	v_pk_add_f32 v[38:39], v[38:39], v[34:35]
	v_mov_b32_e32 v47, v37
	v_pk_add_f32 v[40:41], v[38:39], v[38:39] op_sel:[0,1] op_sel_hi:[1,0]
	s_nop 0
	v_pk_add_f32 v[36:37], v[36:37], v[40:41] op_sel:[1,0] op_sel_hi:[0,1]
	v_mov_b32_e32 v39, v36
	v_pk_add_f32 v[42:43], v[38:39], v[46:47] neg_lo:[0,1] neg_hi:[0,1]
	v_mov_b32_e32 v35, v40
	v_sub_f32_e32 v37, v38, v42
	v_pk_add_f32 v[34:35], v[34:35], v[42:43] neg_lo:[0,1] neg_hi:[0,1]
	v_sub_f32_e32 v37, v46, v37
	v_add_f32_e32 v34, v34, v37
	v_add_f32_e32 v34, v34, v35
	v_add_f32_e32 v34, v36, v34
	v_cndmask_b32_e32 v34, v200, v34, vcc
	v_cmp_ngt_f32_e32 vcc, -1.0, v48
	s_nop 1
	v_cndmask_b32_e32 v34, v201, v34, vcc
	v_cmp_neq_f32_e32 vcc, -1.0, v48
	s_nop 1
	v_cndmask_b32_e32 v34, v202, v34, vcc
	v_cmp_lt_f32_e64 vcc, |v48|, s56
	s_nop 1
	v_cndmask_b32_e32 v34, v34, v48, vcc
	v_sub_f32_e32 v34, v49, v34
	global_store_dword v[32:33], v34, off
	s_branch .LBB0_138

.Lpf_skip_g:
	v_cvt_pk_bf16_f32 v192, v130, v131
	s_nop 0
	v_lshlrev_b32_e32 v194, 16, v192
	v_and_b32_e32 v195, 0xffff0000, v192
	v_sub_f32_e32 v194, v130, v194
	v_sub_f32_e32 v195, v131, v195
	v_cvt_pk_bf16_f32 v193, v128, v129
	v_cvt_pk_bf16_f32 v194, v194, v195
	s_nop 0
	v_lshlrev_b32_e32 v195, 16, v193
	v_and_b32_e32 v196, 0xffff0000, v193
	v_sub_f32_e32 v195, v128, v195
	v_sub_f32_e32 v196, v129, v196
	v_cvt_pk_bf16_f32 v195, v195, v196
	v_xor_b32_e32 v196, s29, v248
	v_lshlrev_b32_e32 v196, 4, v196
	v_add3_u32 v196, s30, v196, v207
	ds_write_b64 v196, v[192:193]
	v_add_u32_e32 v192, 0x10000, v196
	ds_write_b64 v192, v[194:195]
	s_nop 0
	v_cvt_pk_fp8_f32 v192, v190, v191
	v_cvt_pk_fp8_f32 v192, v188, v189 op_sel:[0,0,1]
	v_lshl_add_u64 v[188:189], s[16:17], 0, v[222:223]
	global_store_dword v[188:189], v192, off
	s_nop 0
	v_cvt_pk_fp8_f32 v188, v182, v183
	v_cvt_pk_fp8_f32 v188, v180, v181 op_sel:[0,0,1]
	v_lshl_add_u64 v[180:181], s[16:17], 0, v[220:221]
	global_store_dword v[180:181], v188, off
	s_nop 0
	v_cvt_pk_fp8_f32 v180, v174, v175
	v_cvt_pk_fp8_f32 v180, v172, v173 op_sel:[0,0,1]
	v_lshl_add_u64 v[172:173], s[16:17], 0, v[218:219]
	global_store_dword v[172:173], v180, off
	s_nop 0
	v_cvt_pk_fp8_f32 v172, v166, v167
	v_cvt_pk_fp8_f32 v172, v164, v165 op_sel:[0,0,1]
	v_lshl_add_u64 v[164:165], s[16:17], 0, v[216:217]
	global_store_dword v[164:165], v172, off
	s_nop 0
	v_cvt_pk_fp8_f32 v164, v158, v159
	v_cvt_pk_fp8_f32 v164, v156, v157 op_sel:[0,0,1]
	v_lshl_add_u64 v[156:157], s[16:17], 0, v[214:215]
	global_store_dword v[156:157], v164, off
	s_nop 0
	v_cvt_pk_fp8_f32 v156, v150, v151
	v_cvt_pk_fp8_f32 v156, v148, v149 op_sel:[0,0,1]
	v_lshl_add_u64 v[148:149], s[16:17], 0, v[212:213]
	global_store_dword v[148:149], v156, off
	s_nop 0
	v_cvt_pk_fp8_f32 v148, v142, v143
	v_cvt_pk_fp8_f32 v148, v140, v141 op_sel:[0,0,1]
	v_lshl_add_u64 v[140:141], s[16:17], 0, v[210:211]
	global_store_dword v[140:141], v148, off
	s_nop 0
	v_cvt_pk_fp8_f32 v140, v134, v135
	s_nop 0
	v_cvt_pk_fp8_f32 v134, v186, v187
	v_cvt_pk_fp8_f32 v140, v132, v133 op_sel:[0,0,1]
	v_lshl_add_u64 v[132:133], s[16:17], 0, v[208:209]
	v_cvt_pk_fp8_f32 v134, v184, v185 op_sel:[0,0,1]
	global_store_dword v[132:133], v140, off
	v_lshl_add_u64 v[132:133], s[4:5], 0, v[222:223]
	global_store_dword v[132:133], v134, off
	s_nop 0
	v_cvt_pk_fp8_f32 v134, v178, v179
	v_lshl_add_u64 v[132:133], s[4:5], 0, v[220:221]
	v_cvt_pk_fp8_f32 v134, v176, v177 op_sel:[0,0,1]
	global_store_dword v[132:133], v134, off
	s_nop 0
	v_cvt_pk_fp8_f32 v134, v170, v171
	v_lshl_add_u64 v[132:133], s[4:5], 0, v[218:219]
	v_cvt_pk_fp8_f32 v134, v168, v169 op_sel:[0,0,1]
	global_store_dword v[132:133], v134, off
	s_nop 0
	v_cvt_pk_fp8_f32 v134, v162, v163
	v_lshl_add_u64 v[132:133], s[4:5], 0, v[216:217]
	v_cvt_pk_fp8_f32 v134, v160, v161 op_sel:[0,0,1]
	global_store_dword v[132:133], v134, off
	s_nop 0
	v_cvt_pk_fp8_f32 v134, v154, v155
	v_lshl_add_u64 v[132:133], s[4:5], 0, v[214:215]
	v_cvt_pk_fp8_f32 v134, v152, v153 op_sel:[0,0,1]
	global_store_dword v[132:133], v134, off
	s_nop 0
	v_cvt_pk_fp8_f32 v134, v146, v147
	v_lshl_add_u64 v[132:133], s[4:5], 0, v[212:213]
	v_cvt_pk_fp8_f32 v134, v144, v145 op_sel:[0,0,1]
	global_store_dword v[132:133], v134, off
	s_nop 0
	v_cvt_pk_fp8_f32 v134, v138, v139
	v_lshl_add_u64 v[132:133], s[4:5], 0, v[210:211]
	v_cvt_pk_fp8_f32 v134, v136, v137 op_sel:[0,0,1]
	global_store_dword v[132:133], v134, off
	s_nop 0
	v_cvt_pk_fp8_f32 v132, v130, v131
	v_cvt_pk_fp8_f32 v132, v128, v129 op_sel:[0,0,1]
	v_lshl_add_u64 v[128:129], s[4:5], 0, v[208:209]
	global_store_dword v[128:129], v132, off
	s_waitcnt lgkmcnt(0)
	s_barrier
	ds_read_b128 v[128:131], v227
	s_waitcnt lgkmcnt(0)
	v_mfma_f32_16x16x32_bf16 v[136:139], v[0:3], v[128:131], 0
	v_add_u32_e32 v132, 0x10000, v227
	ds_read_b128 v[132:135], v132
	v_mfma_f32_16x16x32_bf16 v[128:131], v[4:7], v[128:131], v[136:139]
	s_nop 4
	v_add_u32_e32 v136, 0x10000, v228
	ds_read_b128 v[136:139], v136
	s_waitcnt lgkmcnt(1)
	v_mfma_f32_16x16x32_bf16 v[128:131], v[0:3], v[132:135], v[128:131]
	ds_read_b128 v[132:135], v228
	s_waitcnt lgkmcnt(0)
	v_mfma_f32_16x16x32_bf16 v[128:131], v[8:11], v[132:135], v[128:131]
	v_mfma_f32_16x16x32_bf16 v[128:131], v[12:15], v[132:135], v[128:131]
	v_mfma_f32_16x16x32_bf16 v[128:131], v[8:11], v[136:139], v[128:131]
	ds_read_b128 v[132:135], v229
	ds_read_b128 v[136:139], v230
	s_waitcnt lgkmcnt(1)
	v_mfma_f32_16x16x32_bf16 v[128:131], v[16:19], v[132:135], v[128:131]
	v_mfma_f32_16x16x32_bf16 v[128:131], v[20:23], v[132:135], v[128:131]
	s_waitcnt lgkmcnt(0)
	v_mfma_f32_16x16x32_bf16 v[128:131], v[16:19], v[136:139], v[128:131]
	ds_read_b128 v[132:135], v231
	ds_read_b128 v[136:139], v232
	s_waitcnt lgkmcnt(1)
	v_mfma_f32_16x16x32_bf16 v[128:131], v[24:27], v[132:135], v[128:131]
	v_mfma_f32_16x16x32_bf16 v[128:131], v[28:31], v[132:135], v[128:131]
	s_waitcnt lgkmcnt(0)
	v_mfma_f32_16x16x32_bf16 v[128:131], v[24:27], v[136:139], v[128:131]
	ds_read_b128 v[132:135], v233
	ds_read_b128 v[136:139], v234
	s_waitcnt lgkmcnt(1)
	v_mfma_f32_16x16x32_bf16 v[128:131], v[32:35], v[132:135], v[128:131]
	v_mfma_f32_16x16x32_bf16 v[128:131], v[36:39], v[132:135], v[128:131]
	s_waitcnt lgkmcnt(0)
	v_mfma_f32_16x16x32_bf16 v[128:131], v[32:35], v[136:139], v[128:131]
	ds_read_b128 v[132:135], v235
	ds_read_b128 v[136:139], v236
	s_waitcnt lgkmcnt(1)
	v_mfma_f32_16x16x32_bf16 v[128:131], v[40:43], v[132:135], v[128:131]
	v_mfma_f32_16x16x32_bf16 v[128:131], v[44:47], v[132:135], v[128:131]
	s_waitcnt lgkmcnt(0)
	v_mfma_f32_16x16x32_bf16 v[128:131], v[40:43], v[136:139], v[128:131]
	ds_read_b128 v[132:135], v237
	ds_read_b128 v[136:139], v238
	s_waitcnt lgkmcnt(1)
	v_mfma_f32_16x16x32_bf16 v[128:131], v[48:51], v[132:135], v[128:131]
	v_mfma_f32_16x16x32_bf16 v[128:131], v[52:55], v[132:135], v[128:131]
	s_waitcnt lgkmcnt(0)
	v_mfma_f32_16x16x32_bf16 v[128:131], v[48:51], v[136:139], v[128:131]
	ds_read_b128 v[132:135], v239
	ds_read_b128 v[136:139], v240
	s_waitcnt lgkmcnt(1)
	v_mfma_f32_16x16x32_bf16 v[128:131], v[56:59], v[132:135], v[128:131]
	v_mfma_f32_16x16x32_bf16 v[128:131], v[60:63], v[132:135], v[128:131]
	s_waitcnt lgkmcnt(0)
	v_mfma_f32_16x16x32_bf16 v[128:131], v[56:59], v[136:139], v[128:131]
	s_nop 7
	ds_write_b128 v243, v[128:131]
	v_mov_b32_e32 v128, v225
	s_waitcnt lgkmcnt(0)
	s_barrier
	s_nop 0
	v_cmp_gt_i32_e32 vcc, s35, v128
	s_and_saveexec_b64 s[4:5], vcc
	s_cbranch_execz .LBB0_152
	v_lshlrev_b32_e32 v129, 2, v128
	v_and_b32_e32 v204, 28, v129
	global_load_dword v138, v204, s[10:11]
	v_ashrrev_i32_e32 v129, 3, v128
	s_add_i32 s13, 0, 0x22000
	v_ashrrev_i32_e32 v136, 4, v128
	v_lshlrev_b32_e32 v128, 6, v129
	v_and_b32_e32 v129, 1, v129
	v_add3_u32 v134, s13, v128, v204
	v_add_u32_e32 v137, s0, v129
	ds_read2st64_b32 v[128:129], v134 offset1:4
	ds_read2st64_b32 v[130:131], v134 offset0:8 offset1:12
	ds_read2st64_b32 v[132:133], v134 offset0:16 offset1:20
	ds_read2st64_b32 v[134:135], v134 offset0:24 offset1:28
	v_mul_lo_u32 v137, v137, s21
	s_waitcnt lgkmcnt(3)
	v_add_f32_e32 v128, 0, v128
	v_add_f32_e32 v128, v128, v129
	s_waitcnt lgkmcnt(2)
	v_add_f32_e32 v128, v128, v130
	v_add_f32_e32 v128, v128, v131
	s_waitcnt lgkmcnt(1)
	v_add_f32_e32 v128, v128, v132
	v_add_f32_e32 v128, v128, v133
	s_waitcnt lgkmcnt(0)
	v_add_f32_e32 v128, v128, v134
	v_add_f32_e32 v128, v128, v135
	v_add3_u32 v136, v136, s22, v137
	v_ashrrev_i32_e32 v137, 31, v136
	s_waitcnt vmcnt(0)
	v_add_f32_e32 v130, v128, v138
	v_mul_f32_e64 v128, |v130|, s36
	v_exp_f32_e32 v144, v128
	v_min_f32_e32 v145, 0, v130
	v_lshlrev_b64 v[128:129], 5, v[136:137]
	v_lshl_add_u64 v[128:129], s[14:15], 0, v[128:129]
	v_add_f32_e32 v132, 1.0, v144
	v_add_f32_e32 v133, -1.0, v132
	v_frexp_mant_f32_e32 v134, v132
	v_cvt_f64_f32_e32 v[130:131], v132
	v_sub_f32_e32 v135, v133, v132
	v_frexp_exp_i32_f64_e32 v130, v[130:131]
	v_cmp_gt_f32_e32 vcc, s37, v134
	v_sub_f32_e32 v133, v144, v133
	v_add_f32_e32 v131, 1.0, v135
	v_subbrev_co_u32_e32 v130, vcc, 0, v130, vcc
	v_add_f32_e32 v131, v133, v131
	v_sub_u32_e32 v133, 0, v130
	v_ldexp_f32 v132, v132, v133
	v_add_f32_e32 v134, -1.0, v132
	v_add_f32_e32 v135, 1.0, v132
	v_ldexp_f32 v131, v131, v133
	v_add_f32_e32 v133, 1.0, v134
	v_add_f32_e32 v136, -1.0, v135
	v_sub_f32_e32 v133, v132, v133
	v_sub_f32_e32 v132, v132, v136
	v_add_f32_e32 v136, v131, v133
	v_add_f32_e32 v131, v131, v132
	v_add_f32_e32 v138, v135, v131
	v_rcp_f32_e32 v139, v138
	v_add_f32_e32 v133, v134, v136
	v_sub_f32_e32 v134, v133, v134
	v_sub_f32_e32 v132, v138, v135
	v_mul_f32_e32 v141, v133, v139
	v_sub_f32_e32 v140, v136, v134
	v_mul_f32_e32 v134, v138, v141
	v_sub_f32_e32 v131, v131, v132
	v_fma_f32 v136, v141, v138, -v134
	v_fmac_f32_e32 v136, v141, v131
	v_add_f32_e32 v132, v134, v136
	v_sub_f32_e32 v135, v133, v132
	v_mov_b32_e32 v137, v132
	v_pk_add_f32 v[132:133], v[132:133], v[134:135] neg_lo:[0,1] neg_hi:[0,1]
	v_cvt_f32_i32_e32 v130, v130
	v_pk_add_f32 v[132:133], v[132:133], v[136:137] neg_lo:[0,1] neg_hi:[0,1]
	v_cmp_neq_f32_e32 vcc, s39, v144
	v_add_f32_e32 v133, v140, v133
	v_add_f32_e32 v132, v132, v133
	v_add_f32_e32 v133, v135, v132
	v_mul_f32_e32 v137, v139, v133
	v_mul_f32_e32 v134, v138, v137
	v_sub_f32_e32 v135, v135, v133
	v_add_f32_e32 v142, v141, v137
	v_fma_f32 v136, v137, v138, -v134
	v_add_f32_e32 v140, v132, v135
	v_sub_f32_e32 v132, v142, v141
	v_fmac_f32_e32 v136, v137, v131
	v_sub_f32_e32 v131, v137, v132
	v_add_f32_e32 v132, v134, v136
	v_sub_f32_e32 v135, v133, v132
	v_mov_b32_e32 v137, v132
	v_pk_add_f32 v[132:133], v[132:133], v[134:135] neg_lo:[0,1] neg_hi:[0,1]
	v_lshl_add_u64 v[128:129], v[128:129], 0, v[204:205]
	v_pk_add_f32 v[132:133], v[132:133], v[136:137] neg_lo:[0,1] neg_hi:[0,1]
	v_mov_b32_e32 v136, 0x3ecc95a3
	v_add_f32_e32 v133, v140, v133
	v_add_f32_e32 v132, v132, v133
	v_add_f32_e32 v132, v135, v132
	v_mul_f32_e32 v132, v139, v132
	v_add_f32_e32 v131, v131, v132
	v_add_f32_e32 v132, v142, v131
	v_mul_f32_e32 v134, v132, v132
	v_sub_f32_e32 v135, v132, v142
	v_fmamk_f32 v136, v134, 0x3e9b6dac, v136
	v_sub_f32_e32 v135, v131, v135
	v_mul_f32_e32 v131, v132, v134
	v_fmaak_f32 v207, v134, v136, 0x3f2aaada
	v_ldexp_f32 v137, v135, 1
	v_pk_mul_f32 v[134:135], v[130:131], v[206:207]
	v_ldexp_f32 v133, v132, 1
	v_fma_f32 v132, v130, s38, -v134
	v_fmac_f32_e32 v132, 0xb102e308, v130
	v_pk_add_f32 v[130:131], v[134:135], v[132:133]
	v_mov_b32_e32 v136, v134
	v_sub_f32_e32 v140, v131, v133
	v_pk_add_f32 v[138:139], v[130:131], v[134:135] neg_lo:[0,1] neg_hi:[0,1]
	v_sub_f32_e32 v134, v135, v140
	v_add_f32_e32 v137, v137, v134
	v_pk_add_f32 v[134:135], v[130:131], v[136:137]
	v_mov_b32_e32 v133, v130
	v_mov_b32_e32 v139, v135
	v_pk_add_f32 v[142:143], v[132:133], v[138:139] neg_lo:[0,1] neg_hi:[0,1]
	v_pk_add_f32 v[132:133], v[132:133], v[138:139]
	v_mov_b32_e32 v141, v130
	v_pk_add_f32 v[138:139], v[132:133], v[130:131] op_sel:[1,0] op_sel_hi:[0,1] neg_lo:[0,1] neg_hi:[0,1]
	v_mov_b32_e32 v140, v137
	v_mov_b32_e32 v136, v135
	v_mov_b32_e32 v137, v133
	v_pk_mov_b32 v[130:131], v[130:131], v[138:139] op_sel:[1,0]
	v_pk_add_f32 v[134:135], v[134:135], v[138:139] op_sel_hi:[1,0] neg_lo:[0,1] neg_hi:[0,1]
	v_pk_add_f32 v[130:131], v[136:137], v[130:131] neg_lo:[0,1] neg_hi:[0,1]
	v_mov_b32_e32 v134, v142
	v_pk_add_f32 v[130:131], v[140:141], v[130:131] neg_lo:[0,1] neg_hi:[0,1]
	v_mov_b32_e32 v143, v133
	v_pk_add_f32 v[134:135], v[134:135], v[130:131]
	s_nop 0
	v_pk_add_f32 v[136:137], v[134:135], v[134:135] op_sel:[0,1] op_sel_hi:[1,0]
	s_nop 0
	v_pk_add_f32 v[132:133], v[132:133], v[136:137] op_sel:[1,0] op_sel_hi:[0,1]
	v_mov_b32_e32 v135, v132
	v_mov_b32_e32 v131, v136
	v_pk_add_f32 v[136:137], v[134:135], v[142:143] neg_lo:[0,1] neg_hi:[0,1]
	s_nop 0
	v_sub_f32_e32 v133, v134, v136
	v_pk_add_f32 v[130:131], v[130:131], v[136:137] neg_lo:[0,1] neg_hi:[0,1]
	v_sub_f32_e32 v133, v142, v133
	v_add_f32_e32 v130, v130, v133
	v_add_f32_e32 v130, v130, v131
	v_add_f32_e32 v130, v132, v130
	v_mov_b32_e32 v131, 0x7f800000
	v_cndmask_b32_e32 v130, v131, v130, vcc
	v_cmp_ngt_f32_e32 vcc, -1.0, v144
	v_mov_b32_e32 v131, 0x7fc00000
	s_nop 0
	v_cndmask_b32_e32 v130, v131, v130, vcc
	v_cmp_neq_f32_e32 vcc, -1.0, v144
	v_mov_b32_e32 v131, 0xff800000
	s_nop 0
	v_cndmask_b32_e32 v130, v131, v130, vcc
	v_cmp_lt_f32_e64 vcc, |v144|, s40
	s_nop 1
	v_cndmask_b32_e32 v130, v130, v144, vcc
	v_sub_f32_e32 v130, v145, v130
	global_store_dword v[128:129], v130, off
	s_branch .LBB0_152

.Lpeel_exit_0:
	s_mul_hi_i32 s3, s24, 0x2aaaaaab
	s_lshr_b32 s5, s3, 31
	s_lshr_b32 s3, s3, 1
	s_add_i32 s3, s3, s5
	s_lshl_b32 s5, s24, 1
	s_and_b32 s5, s5, 6
	s_and_b32 s20, s12, -16
	s_lshl_b32 s3, s3, 3
	s_or_b32 s5, s5, s20
	s_add_i32 s24, s5, s3
	v_readlane_b32 s3, v252, 41
	v_mbcnt_lo_u32_b32 v0, -1, 0
	v_mbcnt_hi_u32_b32 v0, -1, v0
	s_ashr_i32 s25, s24, 31
	s_lshl_b64 s[20:21], s[24:25], 19
	v_and_or_b32 v51, v0, 15, s3
	s_lshl_b32 s3, s12, 8
	s_and_b32 s22, s3, 0xf00
	v_ashrrev_i32_e32 v50, 4, v0
	s_add_u32 s20, s87, s20
	v_readlane_b32 s3, v252, 59
	v_lshlrev_b32_e32 v0, 5, v50
	v_lshlrev_b32_e32 v50, 3, v50
	v_lshlrev_b32_e32 v132, 12, v51
	v_mov_b32_e32 v133, v1
	s_addc_u32 s21, s3, s21
	v_and_b32_e32 v130, -16, v50
	v_lshl_add_u64 v[50:51], s[20:21], 0, v[132:133]
	v_lshl_add_u64 v[50:51], v[50:51], 0, s[22:23]
	v_and_b32_e32 v0, 32, v0
	v_lshl_add_u64 v[50:51], v[50:51], 0, s[28:29]
	v_pk_mul_f32 v[52:53], v[126:127], s[68:69] op_sel_hi:[1,0]
	s_nop 0
	v_ashrrev_i32_e32 v131, 31, v130
	v_lshl_add_u64 v[50:51], v[50:51], 0, v[0:1]
	v_cvt_pk_fp8_f32 v126, v52, v53
	v_pk_mul_f32 v[52:53], v[122:123], s[68:69] op_sel_hi:[1,0]
	s_nop 0
	v_lshl_add_u64 v[134:135], v[50:51], 0, v[130:131]
	v_pk_mul_f32 v[50:51], v[128:129], s[68:69] op_sel_hi:[1,0]
	v_cvt_pk_fp8_f32 v127, v52, v53
	v_pk_mul_f32 v[52:53], v[118:119], s[68:69] op_sel_hi:[1,0]
	s_nop 0
	v_cvt_pk_fp8_f32 v128, v52, v53
	v_pk_mul_f32 v[52:53], v[114:115], s[68:69] op_sel_hi:[1,0]
	s_nop 0
	v_cvt_pk_fp8_f32 v129, v52, v53
	v_cvt_pk_fp8_f32 v126, v50, v51 op_sel:[0,0,1]
	v_pk_mul_f32 v[50:51], v[124:125], s[68:69] op_sel_hi:[1,0]
	v_pk_mul_f32 v[52:53], v[110:111], s[68:69] op_sel_hi:[1,0]
	v_cvt_pk_fp8_f32 v127, v50, v51 op_sel:[0,0,1]
	v_pk_mul_f32 v[50:51], v[120:121], s[68:69] op_sel_hi:[1,0]
	s_nop 0
	v_cvt_pk_fp8_f32 v128, v50, v51 op_sel:[0,0,1]
	v_pk_mul_f32 v[50:51], v[116:117], s[68:69] op_sel_hi:[1,0]
	v_cvt_pk_fp8_f32 v110, v52, v53
	v_pk_mul_f32 v[52:53], v[106:107], s[68:69] op_sel_hi:[1,0]
	s_nop 0
	v_cvt_pk_fp8_f32 v129, v50, v51 op_sel:[0,0,1]
	v_pk_mul_f32 v[50:51], v[112:113], s[68:69] op_sel_hi:[1,0]
	v_cvt_pk_fp8_f32 v111, v52, v53
	v_pk_mul_f32 v[52:53], v[102:103], s[68:69] op_sel_hi:[1,0]
	s_nop 0
	v_cvt_pk_fp8_f32 v112, v52, v53
	v_cvt_pk_fp8_f32 v110, v50, v51 op_sel:[0,0,1]
	v_pk_mul_f32 v[50:51], v[108:109], s[68:69] op_sel_hi:[1,0]
	v_pk_mul_f32 v[52:53], v[94:95], s[68:69] op_sel_hi:[1,0]
	v_cvt_pk_fp8_f32 v111, v50, v51 op_sel:[0,0,1]
	v_pk_mul_f32 v[50:51], v[104:105], s[68:69] op_sel_hi:[1,0]
	s_nop 0
	v_cvt_pk_fp8_f32 v112, v50, v51 op_sel:[0,0,1]
	v_pk_mul_f32 v[50:51], v[96:97], s[68:69] op_sel_hi:[1,0]
	v_pk_mul_f32 v[96:97], v[98:99], s[68:69] op_sel_hi:[1,0]
	v_pk_mul_f32 v[90:91], v[90:91], s[68:69] op_sel_hi:[1,0]
	v_cvt_pk_fp8_f32 v94, v96, v97
	s_nop 0
	v_cvt_pk_fp8_f32 v95, v90, v91
	v_pk_mul_f32 v[86:87], v[86:87], s[68:69] op_sel_hi:[1,0]
	s_nop 0
	v_mov_b32_e32 v113, v1
	v_cvt_pk_fp8_f32 v96, v86, v87
	v_pk_mul_f32 v[82:83], v[82:83], s[68:69] op_sel_hi:[1,0]
	s_nop 0
	v_cvt_pk_fp8_f32 v113, v52, v53
	v_pk_mul_f32 v[52:53], v[100:101], s[68:69] op_sel_hi:[1,0]
	v_cvt_pk_fp8_f32 v97, v82, v83
	v_cvt_pk_fp8_f32 v94, v52, v53 op_sel:[0,0,1]
	v_pk_mul_f32 v[52:53], v[92:93], s[68:69] op_sel_hi:[1,0]
	s_mov_b32 s5, 0x10000
	v_cvt_pk_fp8_f32 v95, v52, v53 op_sel:[0,0,1]
	v_pk_mul_f32 v[52:53], v[88:89], s[68:69] op_sel_hi:[1,0]
	v_pk_mul_f32 v[74:75], v[74:75], s[68:69] op_sel_hi:[1,0]
	v_cvt_pk_fp8_f32 v96, v52, v53 op_sel:[0,0,1]
	v_pk_mul_f32 v[52:53], v[84:85], s[68:69] op_sel_hi:[1,0]
	v_permlane32_swap_b32_e32 v94, v95
	v_cvt_pk_fp8_f32 v97, v52, v53 op_sel:[0,0,1]
	v_add_co_u32_e32 v52, vcc, s5, v134
	v_pk_mul_f32 v[70:71], v[70:71], s[68:69] op_sel_hi:[1,0]
	v_permlane32_swap_b32_e32 v96, v97
	v_addc_co_u32_e32 v53, vcc, 0, v135, vcc
	global_store_dwordx4 v[52:53], v[94:97], off
	v_pk_mul_f32 v[52:53], v[80:81], s[68:69] op_sel_hi:[1,0]
	v_pk_mul_f32 v[80:81], v[78:79], s[68:69] op_sel_hi:[1,0]
	s_nop 0
	v_cvt_pk_fp8_f32 v78, v80, v81
	s_nop 0
	v_cvt_pk_fp8_f32 v79, v74, v75
	s_nop 0
	v_cvt_pk_fp8_f32 v80, v70, v71
	v_pk_mul_f32 v[62:63], v[62:63], s[68:69] op_sel_hi:[1,0]
	s_nop 0
	v_cvt_pk_fp8_f32 v81, v62, v63
	v_cvt_pk_fp8_f32 v78, v52, v53 op_sel:[0,0,1]
	v_pk_mul_f32 v[52:53], v[76:77], s[68:69] op_sel_hi:[1,0]
	v_pk_mul_f32 v[18:19], v[18:19], s[68:69] op_sel_hi:[1,0]
	v_cvt_pk_fp8_f32 v79, v52, v53 op_sel:[0,0,1]
	v_pk_mul_f32 v[52:53], v[72:73], s[68:69] op_sel_hi:[1,0]
	v_pk_mul_f32 v[20:21], v[20:21], s[68:69] op_sel_hi:[1,0]
	v_cvt_pk_fp8_f32 v80, v52, v53 op_sel:[0,0,1]
	v_pk_mul_f32 v[52:53], v[64:65], s[68:69] op_sel_hi:[1,0]
	s_or_b32 s20, s24, 1
	v_cvt_pk_fp8_f32 v81, v52, v53 op_sel:[0,0,1]
	v_pk_mul_f32 v[52:53], v[66:67], s[68:69] op_sel_hi:[1,0]
	s_nop 0
	v_cvt_pk_fp8_f32 v67, v18, v19
	v_pk_mul_f32 v[18:19], v[48:49], s[68:69] op_sel_hi:[1,0]
	s_nop 0
	s_ashr_i32 s21, s20, 31
	v_cvt_pk_fp8_f32 v67, v20, v21 op_sel:[0,0,1]
	v_pk_mul_f32 v[20:21], v[46:47], s[68:69] op_sel_hi:[1,0]
	s_nop 0
	v_cvt_pk_fp8_f32 v46, v20, v21
	v_pk_mul_f32 v[20:21], v[42:43], s[68:69] op_sel_hi:[1,0]
	s_nop 0
	v_cvt_pk_fp8_f32 v47, v20, v21
	v_pk_mul_f32 v[20:21], v[34:35], s[68:69] op_sel_hi:[1,0]
	v_cvt_pk_fp8_f32 v46, v18, v19 op_sel:[0,0,1]
	v_cvt_pk_fp8_f32 v48, v20, v21
	v_pk_mul_f32 v[18:19], v[44:45], s[68:69] op_sel_hi:[1,0]
	v_pk_mul_f32 v[20:21], v[26:27], s[68:69] op_sel_hi:[1,0]
	v_cvt_pk_fp8_f32 v47, v18, v19 op_sel:[0,0,1]
	v_pk_mul_f32 v[18:19], v[36:37], s[68:69] op_sel_hi:[1,0]
	s_nop 0
	v_cvt_pk_fp8_f32 v48, v18, v19 op_sel:[0,0,1]
	v_pk_mul_f32 v[18:19], v[28:29], s[68:69] op_sel_hi:[1,0]
	v_pk_mul_f32 v[28:29], v[38:39], s[68:69] op_sel_hi:[1,0]
	s_nop 0
	v_cvt_pk_fp8_f32 v26, v28, v29
	v_pk_mul_f32 v[28:29], v[30:31], s[68:69] op_sel_hi:[1,0]
	v_pk_mul_f32 v[22:23], v[22:23], s[68:69] op_sel_hi:[1,0]
	v_cvt_pk_fp8_f32 v27, v28, v29
	s_nop 0
	s_lshl_b64 s[20:21], s[20:21], 19
	s_nop 0
	v_cvt_pk_fp8_f32 v28, v22, v23
	v_pk_mul_f32 v[22:23], v[164:165], s[68:69] op_sel_hi:[1,0]
	s_nop 0
	s_mov_b64 s[26:27], 0x10000
	s_add_u32 s20, s87, s20
	v_cvt_pk_fp8_f32 v49, v20, v21
	v_pk_mul_f32 v[20:21], v[40:41], s[68:69] op_sel_hi:[1,0]
	v_cvt_pk_fp8_f32 v29, v22, v23
	v_cvt_pk_fp8_f32 v113, v50, v51 op_sel:[0,0,1]
	v_lshl_add_u64 v[50:51], v[134:135], 0, s[26:27]
	v_permlane32_swap_b32_e32 v78, v79
	v_permlane32_swap_b32_e32 v80, v81
	s_addc_u32 s21, s3, s21
	v_cvt_pk_fp8_f32 v26, v20, v21 op_sel:[0,0,1]
	v_pk_mul_f32 v[20:21], v[32:33], s[68:69] op_sel_hi:[1,0]
	global_store_dwordx4 v[50:51], v[78:81], off offset:128
	v_lshl_add_u64 v[50:51], s[20:21], 0, v[132:133]
	v_cvt_pk_fp8_f32 v27, v20, v21 op_sel:[0,0,1]
	v_pk_mul_f32 v[20:21], v[24:25], s[68:69] op_sel_hi:[1,0]
	v_lshl_add_u64 v[50:51], v[50:51], 0, s[22:23]
	v_cvt_pk_fp8_f32 v28, v20, v21 op_sel:[0,0,1]
	v_pk_mul_f32 v[20:21], v[166:167], s[68:69] op_sel_hi:[1,0]
	v_lshl_add_u64 v[50:51], v[50:51], 0, s[28:29]
	v_cvt_pk_fp8_f32 v29, v20, v21 op_sel:[0,0,1]
	v_lshl_add_u64 v[50:51], v[50:51], 0, v[0:1]
	v_lshl_add_u64 v[62:63], v[50:51], 0, v[130:131]
	v_add_co_u32_e32 v20, vcc, s5, v62
	v_permlane32_swap_b32_e32 v26, v27
	v_permlane32_swap_b32_e32 v28, v29
	v_addc_co_u32_e32 v21, vcc, 0, v63, vcc
	global_store_dwordx4 v[20:21], v[26:29], off
	v_pk_mul_f32 v[20:21], v[14:15], s[68:69] op_sel_hi:[1,0]
	s_nop 0
	v_cvt_pk_fp8_f32 v14, v20, v21
	s_nop 0
	v_cvt_pk_fp8_f32 v64, v52, v53
	v_pk_mul_f32 v[52:53], v[58:59], s[68:69] op_sel_hi:[1,0]
	s_nop 0
	v_pk_mul_f32 v[16:17], v[16:17], s[68:69] op_sel_hi:[1,0]
	v_cvt_pk_fp8_f32 v65, v52, v53
	v_pk_mul_f32 v[52:53], v[54:55], s[68:69] op_sel_hi:[1,0]
	s_nop 0
	v_cvt_pk_fp8_f32 v14, v16, v17 op_sel:[0,0,1]
	v_pk_mul_f32 v[10:11], v[10:11], s[68:69] op_sel_hi:[1,0]
	s_nop 0
	v_pk_mul_f32 v[6:7], v[6:7], s[68:69] op_sel_hi:[1,0]
	s_nop 0
	v_pk_mul_f32 v[2:3], v[2:3], s[68:69] op_sel_hi:[1,0]
	s_nop 0
	v_cvt_pk_fp8_f32 v66, v52, v53
	v_cvt_pk_fp8_f32 v15, v10, v11
	v_cvt_pk_fp8_f32 v16, v6, v7
	v_cvt_pk_fp8_f32 v17, v2, v3
	v_pk_mul_f32 v[50:51], v[68:69], s[68:69] op_sel_hi:[1,0]
	v_pk_mul_f32 v[12:13], v[12:13], s[68:69] op_sel_hi:[1,0]
	v_cvt_pk_fp8_f32 v64, v50, v51 op_sel:[0,0,1]
	v_pk_mul_f32 v[50:51], v[60:61], s[68:69] op_sel_hi:[1,0]
	v_pk_mul_f32 v[8:9], v[8:9], s[68:69] op_sel_hi:[1,0]
	v_cvt_pk_fp8_f32 v65, v50, v51 op_sel:[0,0,1]
	v_pk_mul_f32 v[50:51], v[56:57], s[68:69] op_sel_hi:[1,0]
	v_pk_mul_f32 v[4:5], v[4:5], s[68:69] op_sel_hi:[1,0]
	v_cvt_pk_fp8_f32 v66, v50, v51 op_sel:[0,0,1]
	v_cvt_pk_fp8_f32 v49, v18, v19 op_sel:[0,0,1]
	v_cvt_pk_fp8_f32 v15, v12, v13 op_sel:[0,0,1]
	v_cvt_pk_fp8_f32 v16, v8, v9 op_sel:[0,0,1]
	v_cvt_pk_fp8_f32 v17, v4, v5 op_sel:[0,0,1]
	v_permlane32_swap_b32_e32 v126, v127
	v_permlane32_swap_b32_e32 v128, v129
	v_permlane32_swap_b32_e32 v110, v111
	v_permlane32_swap_b32_e32 v112, v113
	v_permlane32_swap_b32_e32 v64, v65
	v_permlane32_swap_b32_e32 v66, v67
	v_permlane32_swap_b32_e32 v46, v47
	v_permlane32_swap_b32_e32 v48, v49
	v_lshl_add_u64 v[18:19], v[62:63], 0, s[26:27]
	v_permlane32_swap_b32_e32 v14, v15
	v_permlane32_swap_b32_e32 v16, v17
	s_and_b64 vcc, exec, s[10:11]
	s_mov_b32 s12, s2
	s_mov_b32 s24, s4
	s_mov_b64 s[46:47], s[8:9]
	s_mov_b64 s[26:27], s[6:7]
	global_store_dwordx4 v[134:135], v[126:129], off
	global_store_dwordx4 v[134:135], v[110:113], off offset:128
	global_store_dwordx4 v[62:63], v[64:67], off
	global_store_dwordx4 v[62:63], v[46:49], off offset:128
	global_store_dwordx4 v[18:19], v[14:17], off offset:128
	s_cbranch_vccz .LBB0_241
	v_readlane_b32 s0, v252, 50
	s_waitcnt vmcnt(0)
	v_readlane_b32 s1, v252, 51
	s_andn2_b64 vcc, exec, s[0:1]
	s_cbranch_vccnz .LBB0_253
	s_barrier

.LBB0_284:
	s_mul_hi_i32 s3, s8, 0x2aaaaaab
	s_lshr_b32 s9, s3, 31
	s_lshr_b32 s3, s3, 1
	s_add_i32 s3, s3, s9
	s_and_b32 s16, s8, 3
	s_lshl_b32 s9, s3, 10
	s_lshl_b32 s3, s16, 8
	s_or_b32 s62, s9, s3
	s_cmp_lg_u32 s15, 2
	s_cselect_b64 s[30:31], -1, 0
	s_ashr_i32 s63, s62, 31
	s_lshl_b64 s[8:9], s[62:63], 1
	v_readlane_b32 s17, v252, 57
	s_add_u32 s8, s17, s8
	v_readlane_b32 s17, v252, 61
	v_mov_b64_e32 v[164:165], v[0:1]
	s_addc_u32 s9, s17, s9
	s_mov_b64 s[48:49], -1
	s_and_b64 vcc, exec, s[30:31]
	s_cbranch_vccz .LBB0_286
	s_nop 0
	s_nop 0
	v_cvt_pk_fp8_f32 v0, v176, v177
	v_cvt_pk_fp8_f32 v160, v166, v167
	v_mov_b32_e32 v2, v1
	v_mov_b32_e32 v3, v1
	v_cvt_pk_fp8_f32 v0, v178, v179 op_sel:[0,0,1]
	v_cvt_pk_fp8_f32 v160, v174, v175 op_sel:[0,0,1]
	v_mov_b32_e32 v161, v1
	v_mov_b32_e32 v162, v1
	v_mov_b32_e32 v163, v1
	s_mov_b64 s[48:49], 0

.LBB0_290:
	v_cndmask_b32_e64 v152, 0, 1, s[30:31]
	v_cmp_ne_u32_e64 s[8:9], 1, v152
	s_andn2_b64 vcc, exec, s[30:31]
	s_mov_b64 s[30:31], -1
	s_cbranch_vccnz .LBB0_292
	s_nop 0
	s_nop 0
	v_cvt_pk_fp8_f32 v168, v184, v185
	v_cvt_pk_fp8_f32 v169, v182, v183
	v_mov_b64_e32 v[154:155], v[2:3]
	v_mov_b64_e32 v[152:153], v[0:1]
	v_cvt_pk_fp8_f32 v168, v186, v187 op_sel:[0,0,1]
	v_cvt_pk_fp8_f32 v169, v180, v181 op_sel:[0,0,1]
	v_mov_b64_e32 v[156:157], v[160:161]
	v_mov_b64_e32 v[158:159], v[162:163]
	v_mov_b32_e32 v153, v168
	v_mov_b32_e32 v157, v169
	s_mov_b64 s[30:31], 0

.LBB0_296:
	s_and_b64 vcc, exec, s[8:9]
	s_mov_b64 s[30:31], -1
	s_cbranch_vccnz .LBB0_298
	s_nop 0
	s_nop 0
	v_cvt_pk_fp8_f32 v0, v188, v189
	v_cvt_pk_fp8_f32 v2, v162, v163
	v_mov_b64_e32 v[144:145], v[152:153]
	v_mov_b64_e32 v[148:149], v[156:157]
	v_cvt_pk_fp8_f32 v0, v190, v191 op_sel:[0,0,1]
	v_cvt_pk_fp8_f32 v2, v160, v161 op_sel:[0,0,1]
	v_mov_b64_e32 v[146:147], v[154:155]
	v_mov_b64_e32 v[150:151], v[158:159]
	v_mov_b32_e32 v146, v0
	v_mov_b32_e32 v150, v2
	v_or_b32_e32 v2, 32, v196
	s_cbranch_execz .LBB0_299
	s_branch .LBB0_300

.LBB0_302:
	s_and_b64 vcc, exec, s[8:9]
	s_mov_b64 s[30:31], -1
	s_cbranch_vccnz .LBB0_304
	s_nop 0
	s_nop 0
	v_cvt_pk_fp8_f32 v0, v156, v157
	v_cvt_pk_fp8_f32 v3, v152, v153
	v_mov_b64_e32 v[132:133], v[144:145]
	v_mov_b64_e32 v[136:137], v[148:149]
	v_cvt_pk_fp8_f32 v0, v158, v159 op_sel:[0,0,1]
	v_cvt_pk_fp8_f32 v3, v154, v155 op_sel:[0,0,1]
	v_mov_b64_e32 v[134:135], v[146:147]
	v_mov_b64_e32 v[138:139], v[150:151]
	v_mov_b32_e32 v135, v0
	v_mov_b32_e32 v139, v3
	v_or_b32_e32 v200, 48, v196
	s_cbranch_execz .LBB0_305
	s_branch .LBB0_306

.LBB0_313:
	s_and_b64 vcc, exec, s[8:9]
	s_mov_b64 s[30:31], -1
	s_cbranch_vccnz .LBB0_315
	s_nop 0
	s_nop 0
	v_cvt_pk_fp8_f32 v3, v150, v151
	v_cvt_pk_fp8_f32 v168, v146, v147
	v_mov_b64_e32 v[124:125], v[132:133]
	v_mov_b64_e32 v[128:129], v[136:137]
	v_cvt_pk_fp8_f32 v3, v148, v149 op_sel:[0,0,1]
	v_cvt_pk_fp8_f32 v168, v144, v145 op_sel:[0,0,1]
	v_mov_b64_e32 v[126:127], v[134:135]
	v_mov_b64_e32 v[130:131], v[138:139]
	v_mov_b32_e32 v124, v3
	v_mov_b32_e32 v128, v168
	s_cbranch_execz .LBB0_316
	s_branch .LBB0_317

.LBB0_319:
	s_and_b64 vcc, exec, s[8:9]
	s_mov_b64 s[30:31], -1
	s_cbranch_vccnz .LBB0_321
	s_nop 0
	s_nop 0
	v_cvt_pk_fp8_f32 v3, v138, v139
	v_cvt_pk_fp8_f32 v168, v134, v135
	v_mov_b64_e32 v[116:117], v[124:125]
	v_mov_b64_e32 v[120:121], v[128:129]
	v_cvt_pk_fp8_f32 v3, v136, v137 op_sel:[0,0,1]
	v_cvt_pk_fp8_f32 v168, v132, v133 op_sel:[0,0,1]
	v_mov_b64_e32 v[118:119], v[126:127]
	v_mov_b64_e32 v[122:123], v[130:131]
	v_mov_b32_e32 v117, v3
	v_mov_b32_e32 v121, v168
	s_cbranch_execz .LBB0_322
	s_branch .LBB0_323

.LBB0_325:
	s_and_b64 vcc, exec, s[8:9]
	s_mov_b64 s[30:31], -1
	s_cbranch_vccnz .LBB0_327
	s_nop 0
	s_nop 0
	v_cvt_pk_fp8_f32 v3, v130, v131
	v_cvt_pk_fp8_f32 v168, v126, v127
	v_mov_b64_e32 v[108:109], v[116:117]
	v_mov_b64_e32 v[112:113], v[120:121]
	v_cvt_pk_fp8_f32 v3, v128, v129 op_sel:[0,0,1]
	v_cvt_pk_fp8_f32 v168, v124, v125 op_sel:[0,0,1]
	v_mov_b64_e32 v[110:111], v[118:119]
	v_mov_b64_e32 v[114:115], v[122:123]
	v_mov_b32_e32 v110, v3
	v_mov_b32_e32 v114, v168
	s_cbranch_execz .LBB0_328
	s_branch .LBB0_329

.LBB0_331:
	s_and_b64 vcc, exec, s[8:9]
	s_mov_b64 s[30:31], -1
	s_cbranch_vccnz .LBB0_336
	s_nop 0
	s_nop 0
	v_cvt_pk_fp8_f32 v2, v122, v123
	v_cvt_pk_fp8_f32 v3, v118, v119
	v_mov_b64_e32 v[100:101], v[108:109]
	v_mov_b64_e32 v[104:105], v[112:113]
	v_cvt_pk_fp8_f32 v2, v120, v121 op_sel:[0,0,1]
	v_cvt_pk_fp8_f32 v3, v116, v117 op_sel:[0,0,1]
	v_mov_b64_e32 v[102:103], v[110:111]
	v_mov_b64_e32 v[106:107], v[114:115]
	v_mov_b32_e32 v103, v2
	v_mov_b32_e32 v107, v3
	s_cbranch_execz .LBB0_337

.LBB0_342:
	s_and_b64 vcc, exec, s[8:9]
	s_mov_b64 s[30:31], -1
	s_cbranch_vccnz .LBB0_344
	s_nop 0
	s_nop 0
	v_cvt_pk_fp8_f32 v2, v112, v113
	v_cvt_pk_fp8_f32 v3, v108, v109
	v_mov_b64_e32 v[76:77], v[100:101]
	v_mov_b64_e32 v[80:81], v[104:105]
	v_cvt_pk_fp8_f32 v2, v114, v115 op_sel:[0,0,1]
	v_cvt_pk_fp8_f32 v3, v110, v111 op_sel:[0,0,1]
	v_mov_b64_e32 v[78:79], v[102:103]
	v_mov_b64_e32 v[82:83], v[106:107]
	v_mov_b32_e32 v76, v2
	v_mov_b32_e32 v80, v3
	v_add_u32_e32 v2, 0x80, v196
	s_cbranch_execz .LBB0_345
	s_branch .LBB0_346

.LBB0_348:
	s_and_b64 vcc, exec, s[8:9]
	s_mov_b64 s[30:31], -1
	s_cbranch_vccnz .LBB0_350
	s_nop 0
	s_nop 0
	v_cvt_pk_fp8_f32 v3, v104, v105
	v_cvt_pk_fp8_f32 v140, v102, v103
	v_mov_b64_e32 v[60:61], v[76:77]
	v_mov_b64_e32 v[64:65], v[80:81]
	v_cvt_pk_fp8_f32 v3, v106, v107 op_sel:[0,0,1]
	v_cvt_pk_fp8_f32 v140, v100, v101 op_sel:[0,0,1]
	v_mov_b64_e32 v[62:63], v[78:79]
	v_mov_b64_e32 v[66:67], v[82:83]
	v_mov_b32_e32 v61, v3
	v_mov_b32_e32 v65, v140
	v_add_u32_e32 v140, 0x90, v196
	s_cbranch_execz .LBB0_351
	s_branch .LBB0_352

.LBB0_354:
	s_and_b64 vcc, exec, s[8:9]
	s_mov_b64 s[30:31], -1
	s_cbranch_vccnz .LBB0_356
	s_nop 0
	s_nop 0
	v_cvt_pk_fp8_f32 v3, v80, v81
	v_cvt_pk_fp8_f32 v141, v78, v79
	v_mov_b64_e32 v[44:45], v[60:61]
	v_mov_b64_e32 v[48:49], v[64:65]
	v_cvt_pk_fp8_f32 v3, v82, v83 op_sel:[0,0,1]
	v_cvt_pk_fp8_f32 v141, v76, v77 op_sel:[0,0,1]
	v_mov_b64_e32 v[46:47], v[62:63]
	v_mov_b64_e32 v[50:51], v[66:67]
	v_mov_b32_e32 v46, v3
	v_mov_b32_e32 v50, v141
	v_add_u32_e32 v142, 0xa0, v196
	s_cbranch_execz .LBB0_357
	s_branch .LBB0_358

.LBB0_360:
	s_and_b64 vcc, exec, s[8:9]
	s_mov_b64 s[30:31], -1
	s_cbranch_vccnz .LBB0_363
	s_nop 0
	s_nop 0
	v_cvt_pk_fp8_f32 v3, v64, v65
	v_cvt_pk_fp8_f32 v141, v62, v63
	v_mov_b64_e32 v[36:37], v[44:45]
	v_mov_b64_e32 v[40:41], v[48:49]
	v_cvt_pk_fp8_f32 v3, v66, v67 op_sel:[0,0,1]
	v_cvt_pk_fp8_f32 v141, v60, v61 op_sel:[0,0,1]
	v_mov_b64_e32 v[38:39], v[46:47]
	v_mov_b64_e32 v[42:43], v[50:51]
	v_mov_b32_e32 v39, v3
	v_mov_b32_e32 v43, v141
	v_add_u32_e32 v196, 0xb0, v196
	s_cbranch_execz .LBB0_364

.LBB0_373:
	s_and_b64 vcc, exec, s[8:9]
	s_mov_b64 s[30:31], -1
	s_cbranch_vccnz .LBB0_375
	s_nop 0
	s_nop 0
	v_cvt_pk_fp8_f32 v3, v50, v51
	v_cvt_pk_fp8_f32 v92, v46, v47
	v_mov_b64_e32 v[28:29], v[36:37]
	v_mov_b64_e32 v[32:33], v[40:41]
	v_cvt_pk_fp8_f32 v3, v48, v49 op_sel:[0,0,1]
	v_cvt_pk_fp8_f32 v92, v44, v45 op_sel:[0,0,1]
	v_mov_b64_e32 v[30:31], v[38:39]
	v_mov_b64_e32 v[34:35], v[42:43]
	v_mov_b32_e32 v28, v3
	v_mov_b32_e32 v32, v92
	s_cbranch_execz .LBB0_376
	s_branch .LBB0_377

.LBB0_379:
	s_and_b64 vcc, exec, s[8:9]
	s_mov_b64 s[30:31], -1
	s_cbranch_vccnz .LBB0_381
	s_nop 0
	s_nop 0
	v_cvt_pk_fp8_f32 v2, v42, v43
	v_cvt_pk_fp8_f32 v3, v38, v39
	v_mov_b64_e32 v[20:21], v[28:29]
	v_mov_b64_e32 v[24:25], v[32:33]
	v_cvt_pk_fp8_f32 v2, v40, v41 op_sel:[0,0,1]
	v_cvt_pk_fp8_f32 v3, v36, v37 op_sel:[0,0,1]
	v_mov_b64_e32 v[22:23], v[30:31]
	v_mov_b64_e32 v[26:27], v[34:35]
	v_mov_b32_e32 v21, v2
	v_mov_b32_e32 v25, v3
	s_cbranch_execz .LBB0_382
	s_branch .LBB0_383

.LBB0_385:
	s_and_b64 vcc, exec, s[8:9]
	s_mov_b64 s[30:31], -1
	s_cbranch_vccnz .LBB0_387
	s_nop 0
	s_nop 0
	v_cvt_pk_fp8_f32 v2, v34, v35
	v_cvt_pk_fp8_f32 v3, v30, v31
	v_mov_b64_e32 v[12:13], v[20:21]
	v_mov_b64_e32 v[16:17], v[24:25]
	v_cvt_pk_fp8_f32 v2, v32, v33 op_sel:[0,0,1]
	v_cvt_pk_fp8_f32 v3, v28, v29 op_sel:[0,0,1]
	v_mov_b64_e32 v[14:15], v[22:23]
	v_mov_b64_e32 v[18:19], v[26:27]
	v_mov_b32_e32 v14, v2
	v_mov_b32_e32 v18, v3
	s_cbranch_execz .LBB0_388
	s_branch .LBB0_389

.LBB0_391:
	s_and_b64 vcc, exec, s[8:9]
	s_mov_b64 s[6:7], -1
	s_cbranch_vccnz .LBB0_394
	s_nop 0
	s_nop 0
	v_cvt_pk_fp8_f32 v26, v24, v25
	v_cvt_pk_fp8_f32 v27, v20, v21
	v_mov_b64_e32 v[6:7], v[12:13]
	v_mov_b64_e32 v[2:3], v[16:17]
	v_cvt_pk_fp8_f32 v26, v22, v23 op_sel:[0,0,1]
	v_cvt_pk_fp8_f32 v27, v10, v11 op_sel:[0,0,1]
	v_mov_b64_e32 v[8:9], v[14:15]
	v_mov_b64_e32 v[4:5], v[18:19]
	v_mov_b32_e32 v9, v26
	v_mov_b32_e32 v5, v27
	s_cbranch_execz .LBB0_395

.LBB0_531:
	s_waitcnt vmcnt(31)
	v_mov_b32_e32 v130, v2
	s_waitcnt vmcnt(30)
	v_mov_b32_e32 v131, v6
	v_pk_mul_f32 v[130:131], v[130:131], s[72:73] op_sel_hi:[1,0]
	s_nop 0
	v_cvt_pk_fp8_f32 v0, v130, v131
	s_waitcnt vmcnt(29)
	v_mov_b32_e32 v130, v10
	s_waitcnt vmcnt(28)
	v_mov_b32_e32 v131, v14
	v_pk_mul_f32 v[130:131], v[130:131], s[72:73] op_sel_hi:[1,0]
	s_nop 0
	v_cvt_pk_fp8_f32 v0, v130, v131 op_sel:[0,0,1]
	v_mov_b32_e32 v130, v3
	v_mov_b32_e32 v131, v7
	v_pk_mul_f32 v[130:131], v[130:131], s[72:73] op_sel_hi:[1,0]
	s_nop 0
	v_cvt_pk_fp8_f32 v132, v130, v131
	v_mov_b32_e32 v130, v11
	v_mov_b32_e32 v131, v15
	v_pk_mul_f32 v[130:131], v[130:131], s[72:73] op_sel_hi:[1,0]
	s_nop 0
	v_cvt_pk_fp8_f32 v132, v130, v131 op_sel:[0,0,1]
	v_mov_b32_e32 v130, v4
	v_mov_b32_e32 v131, v8
	v_pk_mul_f32 v[130:131], v[130:131], s[72:73] op_sel_hi:[1,0]
	v_mov_b32_e32 v139, v1
	v_cvt_pk_fp8_f32 v133, v130, v131
	v_mov_b32_e32 v130, v12
	v_mov_b32_e32 v131, v16
	v_pk_mul_f32 v[130:131], v[130:131], s[72:73] op_sel_hi:[1,0]
	v_mov_b32_e32 v146, v1
	v_cvt_pk_fp8_f32 v133, v130, v131 op_sel:[0,0,1]
	v_mov_b32_e32 v130, v5
	v_mov_b32_e32 v131, v9
	v_pk_mul_f32 v[130:131], v[130:131], s[72:73] op_sel_hi:[1,0]
	v_add_u32_e32 v145, 0x4000, v143
	v_cvt_pk_fp8_f32 v138, v130, v131
	v_mov_b32_e32 v130, v13
	v_mov_b32_e32 v131, v17
	v_pk_mul_f32 v[130:131], v[130:131], s[72:73] op_sel_hi:[1,0]
	v_add_u32_e32 v144, 0x8400, v143
	v_cvt_pk_fp8_f32 v138, v130, v131 op_sel:[0,0,1]
	s_waitcnt vmcnt(27)
	v_mov_b32_e32 v130, v18
	s_waitcnt vmcnt(26)
	v_mov_b32_e32 v131, v22
	ds_write2_b32 v143, v0, v132 offset1:33
	ds_write2_b32 v143, v133, v138 offset0:66 offset1:99
	v_pk_mul_f32 v[130:131], v[130:131], s[72:73] op_sel_hi:[1,0]
	s_nop 0
	v_cvt_pk_fp8_f32 v0, v130, v131
	s_waitcnt vmcnt(25)
	v_mov_b32_e32 v130, v26
	s_waitcnt vmcnt(24)
	v_mov_b32_e32 v131, v30
	v_pk_mul_f32 v[130:131], v[130:131], s[72:73] op_sel_hi:[1,0]
	s_nop 0
	v_cvt_pk_fp8_f32 v0, v130, v131 op_sel:[0,0,1]
	v_mov_b32_e32 v130, v19
	v_mov_b32_e32 v131, v23
	v_pk_mul_f32 v[130:131], v[130:131], s[72:73] op_sel_hi:[1,0]
	s_nop 0
	v_cvt_pk_fp8_f32 v132, v130, v131
	v_mov_b32_e32 v130, v27
	v_mov_b32_e32 v131, v31
	v_pk_mul_f32 v[130:131], v[130:131], s[72:73] op_sel_hi:[1,0]
	s_nop 0
	v_cvt_pk_fp8_f32 v132, v130, v131 op_sel:[0,0,1]
	v_mov_b32_e32 v130, v20
	v_mov_b32_e32 v131, v24
	v_pk_mul_f32 v[130:131], v[130:131], s[72:73] op_sel_hi:[1,0]
	v_mov_b32_e32 v147, v1
	v_cvt_pk_fp8_f32 v133, v130, v131
	v_mov_b32_e32 v130, v28
	v_mov_b32_e32 v131, v32
	v_pk_mul_f32 v[130:131], v[130:131], s[72:73] op_sel_hi:[1,0]
	s_cmp_lt_i32 s40, 2
	v_cvt_pk_fp8_f32 v133, v130, v131 op_sel:[0,0,1]
	v_mov_b32_e32 v130, v21
	v_mov_b32_e32 v131, v25
	v_pk_mul_f32 v[130:131], v[130:131], s[72:73] op_sel_hi:[1,0]
	s_nop 0
	v_cvt_pk_fp8_f32 v138, v130, v131
	v_mov_b32_e32 v130, v29
	v_mov_b32_e32 v131, v33
	v_pk_mul_f32 v[130:131], v[130:131], s[72:73] op_sel_hi:[1,0]
	s_nop 0
	v_cvt_pk_fp8_f32 v138, v130, v131 op_sel:[0,0,1]
	s_waitcnt vmcnt(23)
	v_mov_b32_e32 v130, v50
	s_waitcnt vmcnt(22)
	v_mov_b32_e32 v131, v54
	v_pk_mul_f32 v[130:131], v[130:131], s[72:73] op_sel_hi:[1,0]
	ds_write2_b32 v145, v0, v132 offset0:128 offset1:161
	ds_write2_b32 v145, v133, v138 offset0:194 offset1:227
	v_cvt_pk_fp8_f32 v139, v130, v131
	s_waitcnt vmcnt(21)
	v_mov_b32_e32 v130, v58
	s_waitcnt vmcnt(20)
	v_mov_b32_e32 v131, v62
	v_pk_mul_f32 v[130:131], v[130:131], s[72:73] op_sel_hi:[1,0]
	s_nop 0
	v_cvt_pk_fp8_f32 v139, v130, v131 op_sel:[0,0,1]
	v_mov_b32_e32 v130, v51
	v_mov_b32_e32 v131, v55
	v_pk_mul_f32 v[130:131], v[130:131], s[72:73] op_sel_hi:[1,0]
	s_nop 0
	v_cvt_pk_fp8_f32 v146, v130, v131
	v_mov_b32_e32 v130, v59
	v_mov_b32_e32 v131, v63
	v_pk_mul_f32 v[130:131], v[130:131], s[72:73] op_sel_hi:[1,0]
	s_nop 0
	v_cvt_pk_fp8_f32 v146, v130, v131 op_sel:[0,0,1]
	v_mov_b32_e32 v130, v52
	v_mov_b32_e32 v131, v56
	v_pk_mul_f32 v[130:131], v[130:131], s[72:73] op_sel_hi:[1,0]
	s_nop 0
	v_cvt_pk_fp8_f32 v0, v130, v131
	v_mov_b32_e32 v130, v60
	v_mov_b32_e32 v131, v64
	v_pk_mul_f32 v[130:131], v[130:131], s[72:73] op_sel_hi:[1,0]
	ds_write2_b32 v144, v139, v146 offset1:33
	v_cvt_pk_fp8_f32 v0, v130, v131 op_sel:[0,0,1]
	v_mov_b32_e32 v130, v53
	v_mov_b32_e32 v131, v57
	v_pk_mul_f32 v[130:131], v[130:131], s[72:73] op_sel_hi:[1,0]
	s_nop 0
	v_cvt_pk_fp8_f32 v132, v130, v131
	v_mov_b32_e32 v130, v61
	v_mov_b32_e32 v131, v65
	v_pk_mul_f32 v[130:131], v[130:131], s[72:73] op_sel_hi:[1,0]
	v_add_u32_e32 v146, 0xc400, v143
	v_cvt_pk_fp8_f32 v132, v130, v131 op_sel:[0,0,1]
	s_waitcnt vmcnt(19)
	v_mov_b32_e32 v130, v82
	s_waitcnt vmcnt(18)
	v_mov_b32_e32 v131, v86
	v_pk_mul_f32 v[130:131], v[130:131], s[72:73] op_sel_hi:[1,0]
	ds_write2_b32 v144, v0, v132 offset0:66 offset1:99
	v_cvt_pk_fp8_f32 v133, v130, v131
	s_waitcnt vmcnt(17)
	v_mov_b32_e32 v130, v106
	s_waitcnt vmcnt(16)
	v_mov_b32_e32 v131, v110
	v_pk_mul_f32 v[130:131], v[130:131], s[72:73] op_sel_hi:[1,0]
	v_lshl_add_u32 v0, s21, 6, v140
	v_cvt_pk_fp8_f32 v133, v130, v131 op_sel:[0,0,1]
	v_mov_b32_e32 v130, v83
	v_mov_b32_e32 v131, v87
	v_pk_mul_f32 v[130:131], v[130:131], s[72:73] op_sel_hi:[1,0]
	s_nop 0
	v_cvt_pk_fp8_f32 v138, v130, v131
	v_mov_b32_e32 v130, v107
	v_mov_b32_e32 v131, v111
	v_pk_mul_f32 v[130:131], v[130:131], s[72:73] op_sel_hi:[1,0]
	s_nop 0
	v_cvt_pk_fp8_f32 v138, v130, v131 op_sel:[0,0,1]
	v_mov_b32_e32 v130, v84
	v_mov_b32_e32 v131, v88
	v_pk_mul_f32 v[130:131], v[130:131], s[72:73] op_sel_hi:[1,0]
	s_nop 0
	v_cvt_pk_fp8_f32 v139, v130, v131
	v_mov_b32_e32 v130, v108
	v_mov_b32_e32 v131, v112
	v_pk_mul_f32 v[130:131], v[130:131], s[72:73] op_sel_hi:[1,0]
	s_nop 0
	v_cvt_pk_fp8_f32 v139, v130, v131 op_sel:[0,0,1]
	v_mov_b32_e32 v130, v85
	v_mov_b32_e32 v131, v89
	v_pk_mul_f32 v[130:131], v[130:131], s[72:73] op_sel_hi:[1,0]
	s_nop 0
	v_cvt_pk_fp8_f32 v147, v130, v131
	v_mov_b32_e32 v130, v109
	v_mov_b32_e32 v131, v113
	v_pk_mul_f32 v[130:131], v[130:131], s[72:73] op_sel_hi:[1,0]
	s_nop 0
	v_cvt_pk_fp8_f32 v147, v130, v131 op_sel:[0,0,1]
	ds_write2_b32 v146, v133, v138 offset0:128 offset1:161
	ds_write2_b32 v146, v139, v147 offset0:194 offset1:227
	s_waitcnt lgkmcnt(0)
	s_barrier
	ds_read2_b32 v[130:131], v142 offset1:1
	ds_read2_b32 v[132:133], v142 offset0:2 offset1:3
	s_cbranch_scc1 .LBB0_537
	s_cmp_gt_i32 s40, 2
	s_cbranch_scc0 .LBB0_538
	s_cmp_eq_u32 s40, 3
	s_mov_b64 s[62:63], -1
	s_cbranch_scc0 .LBB0_535
	v_lshlrev_b32_e32 v138, 1, v0
	v_and_b32_e32 v139, 0x7f, v0
	s_movk_i32 s13, 0xff00
	v_and_or_b32 v138, v138, s13, v139
	s_mov_b64 s[62:63], 0

.Lcvw_c1:
	v_mov_b32_e32 v130, v38
	v_mov_b32_e32 v131, v34
	v_pk_mul_f32 v[130:131], v[130:131], s[72:73] op_sel_hi:[1,0]
	s_nop 0
	v_cvt_pk_fp8_f32 v0, v130, v131
	v_mov_b32_e32 v130, v46
	v_mov_b32_e32 v131, v42
	v_pk_mul_f32 v[130:131], v[130:131], s[72:73] op_sel_hi:[1,0]
	s_nop 0
	v_cvt_pk_fp8_f32 v0, v130, v131 op_sel:[0,0,1]
	v_mov_b32_e32 v130, v39
	v_mov_b32_e32 v131, v35
	v_pk_mul_f32 v[130:131], v[130:131], s[72:73] op_sel_hi:[1,0]
	s_nop 0
	v_cvt_pk_fp8_f32 v132, v130, v131
	v_mov_b32_e32 v130, v47
	v_mov_b32_e32 v131, v43
	v_pk_mul_f32 v[130:131], v[130:131], s[72:73] op_sel_hi:[1,0]
	s_nop 0
	v_cvt_pk_fp8_f32 v132, v130, v131 op_sel:[0,0,1]
	v_mov_b32_e32 v130, v40
	v_mov_b32_e32 v131, v36
	v_pk_mul_f32 v[130:131], v[130:131], s[72:73] op_sel_hi:[1,0]
	s_nop 0
	v_cvt_pk_fp8_f32 v133, v130, v131
	v_mov_b32_e32 v130, v48
	v_mov_b32_e32 v131, v44
	v_pk_mul_f32 v[130:131], v[130:131], s[72:73] op_sel_hi:[1,0]
	s_nop 0
	v_cvt_pk_fp8_f32 v133, v130, v131 op_sel:[0,0,1]
	v_mov_b32_e32 v130, v41
	v_mov_b32_e32 v131, v37
	v_pk_mul_f32 v[130:131], v[130:131], s[72:73] op_sel_hi:[1,0]
	s_nop 0
	v_cvt_pk_fp8_f32 v138, v130, v131
	v_mov_b32_e32 v130, v49
	v_mov_b32_e32 v131, v45
	v_pk_mul_f32 v[130:131], v[130:131], s[72:73] op_sel_hi:[1,0]
	s_nop 0
	v_cvt_pk_fp8_f32 v138, v130, v131 op_sel:[0,0,1]
	v_mov_b32_e32 v130, v70
	v_mov_b32_e32 v131, v66
	v_pk_mul_f32 v[130:131], v[130:131], s[72:73] op_sel_hi:[1,0]
	s_cmp_lt_i32 s60, 2
	v_cvt_pk_fp8_f32 v139, v130, v131
	v_mov_b32_e32 v130, v78
	v_mov_b32_e32 v131, v74
	v_pk_mul_f32 v[130:131], v[130:131], s[72:73] op_sel_hi:[1,0]
	s_nop 0
	v_cvt_pk_fp8_f32 v139, v130, v131 op_sel:[0,0,1]
	v_mov_b32_e32 v130, v71
	v_mov_b32_e32 v131, v67
	v_pk_mul_f32 v[130:131], v[130:131], s[72:73] op_sel_hi:[1,0]
	s_nop 0
	v_cvt_pk_fp8_f32 v153, v130, v131
	v_mov_b32_e32 v130, v79
	v_mov_b32_e32 v131, v75
	v_pk_mul_f32 v[130:131], v[130:131], s[72:73] op_sel_hi:[1,0]
	s_nop 0
	v_cvt_pk_fp8_f32 v153, v130, v131 op_sel:[0,0,1]
	v_mov_b32_e32 v130, v72
	v_mov_b32_e32 v131, v68
	v_pk_mul_f32 v[130:131], v[130:131], s[72:73] op_sel_hi:[1,0]
	s_nop 0
	v_cvt_pk_fp8_f32 v154, v130, v131
	v_mov_b32_e32 v130, v80
	v_mov_b32_e32 v131, v76
	v_pk_mul_f32 v[130:131], v[130:131], s[72:73] op_sel_hi:[1,0]
	s_nop 0
	v_cvt_pk_fp8_f32 v154, v130, v131 op_sel:[0,0,1]
	v_mov_b32_e32 v130, v73
	v_mov_b32_e32 v131, v69
	v_pk_mul_f32 v[130:131], v[130:131], s[72:73] op_sel_hi:[1,0]
	s_nop 0
	v_cvt_pk_fp8_f32 v155, v130, v131
	v_mov_b32_e32 v130, v81
	v_mov_b32_e32 v131, v77
	v_pk_mul_f32 v[130:131], v[130:131], s[72:73] op_sel_hi:[1,0]
	s_nop 0
	v_cvt_pk_fp8_f32 v155, v130, v131 op_sel:[0,0,1]
	v_mov_b32_e32 v130, v94
	v_mov_b32_e32 v131, v90
	ds_write2_b32 v143, v0, v132 offset1:33
	ds_write2_b32 v143, v133, v138 offset0:66 offset1:99
	ds_write2_b32 v145, v139, v153 offset0:128 offset1:161
	ds_write2_b32 v145, v154, v155 offset0:194 offset1:227
	v_pk_mul_f32 v[130:131], v[130:131], s[72:73] op_sel_hi:[1,0]
	s_nop 0
	v_cvt_pk_fp8_f32 v0, v130, v131
	v_mov_b32_e32 v130, v102
	v_mov_b32_e32 v131, v98
	v_pk_mul_f32 v[130:131], v[130:131], s[72:73] op_sel_hi:[1,0]
	s_nop 0
	v_cvt_pk_fp8_f32 v0, v130, v131 op_sel:[0,0,1]
	v_mov_b32_e32 v130, v95
	v_mov_b32_e32 v131, v91
	v_pk_mul_f32 v[130:131], v[130:131], s[72:73] op_sel_hi:[1,0]
	s_nop 0
	v_cvt_pk_fp8_f32 v132, v130, v131
	v_mov_b32_e32 v130, v103
	v_mov_b32_e32 v131, v99
	v_pk_mul_f32 v[130:131], v[130:131], s[72:73] op_sel_hi:[1,0]
	s_nop 0
	v_cvt_pk_fp8_f32 v132, v130, v131 op_sel:[0,0,1]
	v_mov_b32_e32 v130, v96
	v_mov_b32_e32 v131, v92
	v_pk_mul_f32 v[130:131], v[130:131], s[72:73] op_sel_hi:[1,0]
	s_nop 0
	v_cvt_pk_fp8_f32 v133, v130, v131
	v_mov_b32_e32 v130, v104
	v_mov_b32_e32 v131, v100
	v_pk_mul_f32 v[130:131], v[130:131], s[72:73] op_sel_hi:[1,0]
	s_nop 0
	v_cvt_pk_fp8_f32 v133, v130, v131 op_sel:[0,0,1]
	v_mov_b32_e32 v130, v97
	v_mov_b32_e32 v131, v93
	v_pk_mul_f32 v[130:131], v[130:131], s[72:73] op_sel_hi:[1,0]
	s_nop 0
	v_cvt_pk_fp8_f32 v138, v130, v131
	v_mov_b32_e32 v130, v105
	v_mov_b32_e32 v131, v101
	v_pk_mul_f32 v[130:131], v[130:131], s[72:73] op_sel_hi:[1,0]
	s_nop 0
	v_cvt_pk_fp8_f32 v138, v130, v131 op_sel:[0,0,1]
	v_mov_b32_e32 v130, v118
	v_mov_b32_e32 v131, v114
	v_pk_mul_f32 v[130:131], v[130:131], s[72:73] op_sel_hi:[1,0]
	s_nop 0
	v_cvt_pk_fp8_f32 v139, v130, v131
	v_mov_b32_e32 v130, v126
	v_mov_b32_e32 v131, v122
	v_pk_mul_f32 v[130:131], v[130:131], s[72:73] op_sel_hi:[1,0]
	s_nop 0
	v_cvt_pk_fp8_f32 v139, v130, v131 op_sel:[0,0,1]
	v_mov_b32_e32 v130, v119
	v_mov_b32_e32 v131, v115
	v_pk_mul_f32 v[130:131], v[130:131], s[72:73] op_sel_hi:[1,0]
	s_nop 0
	v_cvt_pk_fp8_f32 v145, v130, v131
	v_mov_b32_e32 v130, v127
	v_mov_b32_e32 v131, v123
	v_pk_mul_f32 v[130:131], v[130:131], s[72:73] op_sel_hi:[1,0]
	s_nop 0
	v_cvt_pk_fp8_f32 v145, v130, v131 op_sel:[0,0,1]
	v_mov_b32_e32 v130, v120
	v_mov_b32_e32 v131, v116
	v_pk_mul_f32 v[130:131], v[130:131], s[72:73] op_sel_hi:[1,0]
	s_nop 0
	v_cvt_pk_fp8_f32 v153, v130, v131
	v_mov_b32_e32 v130, v128
	v_mov_b32_e32 v131, v124
	v_pk_mul_f32 v[130:131], v[130:131], s[72:73] op_sel_hi:[1,0]
	s_nop 0
	v_cvt_pk_fp8_f32 v153, v130, v131 op_sel:[0,0,1]
	v_mov_b32_e32 v130, v121
	v_mov_b32_e32 v131, v117
	v_pk_mul_f32 v[130:131], v[130:131], s[72:73] op_sel_hi:[1,0]
	s_nop 0
	v_cvt_pk_fp8_f32 v154, v130, v131
	v_mov_b32_e32 v130, v129
	v_mov_b32_e32 v131, v125
	v_pk_mul_f32 v[130:131], v[130:131], s[72:73] op_sel_hi:[1,0]
	s_nop 0
	v_cvt_pk_fp8_f32 v154, v130, v131 op_sel:[0,0,1]
	ds_write2_b32 v144, v0, v132 offset1:33
	ds_write2_b32 v144, v133, v138 offset0:66 offset1:99
	ds_write2_b32 v146, v139, v145 offset0:128 offset1:161
	ds_write2_b32 v146, v153, v154 offset0:194 offset1:227
	s_waitcnt lgkmcnt(0)
	s_barrier
	ds_read2_b32 v[130:131], v142 offset1:1
	ds_read2_b32 v[132:133], v142 offset0:2 offset1:3
	v_lshl_add_u32 v0, s69, 6, v140
	s_cbranch_scc1 .LBB0_682
	s_cmp_gt_i32 s60, 2
	s_cbranch_scc0 .LBB0_683
	s_cmp_eq_u32 s60, 3
	s_mov_b64 s[46:47], -1
	s_cbranch_scc0 .LBB0_680
	v_lshlrev_b32_e32 v138, 1, v0
	v_and_b32_e32 v139, 0x7f, v0
	s_movk_i32 s9, 0xff00
	v_and_or_b32 v138, v138, s9, v139
	s_mov_b64 s[46:47], 0

.LBB0_838:
	s_nop 0
	s_nop 0
	s_nop 0
	s_nop 0
	s_nop 0
	s_nop 0
	s_nop 0
	s_nop 0
	v_cvt_pk_fp8_f32 v2, v13, v15
	v_cvt_pk_fp8_f32 v6, v10, v11
	v_cvt_pk_fp8_f32 v3, v146, v147
	v_cvt_pk_fp8_f32 v7, v130, v132
	v_cvt_pk_fp8_f32 v4, v150, v151
	v_cvt_pk_fp8_f32 v8, v136, v137
	v_cvt_pk_fp8_f32 v5, v154, v155
	v_cvt_pk_fp8_f32 v9, v140, v141
	v_lshl_add_u32 v156, s49, 14, v188
	v_add_u32_e32 v157, v156, v189
	v_add_u32_e32 v158, v156, v190
	ds_read_b128 v[210:213], v157
	ds_read_b128 v[214:217], v158
	v_cvt_pk_fp8_f32 v2, v131, v133 op_sel:[0,0,1]
	v_cvt_pk_fp8_f32 v6, v12, v14 op_sel:[0,0,1]
	v_cvt_pk_fp8_f32 v3, v148, v149 op_sel:[0,0,1]
	v_cvt_pk_fp8_f32 v7, v134, v135 op_sel:[0,0,1]
	v_cvt_pk_fp8_f32 v4, v152, v153 op_sel:[0,0,1]
	v_cvt_pk_fp8_f32 v8, v138, v139 op_sel:[0,0,1]
	v_cvt_pk_fp8_f32 v5, v144, v145 op_sel:[0,0,1]
	v_cvt_pk_fp8_f32 v9, v142, v143 op_sel:[0,0,1]
	v_fmamk_f32 v0, v104, 0x3e0293ee, v196
	v_exp_f32_e32 v104, v0
	v_fmamk_f32 v0, v120, 0x3e0293ee, v196
	v_exp_f32_e32 v120, v0
	v_fmamk_f32 v0, v105, 0x3e0293ee, v196
	s_waitcnt lgkmcnt(0)
	v_mfma_scale_f32_32x32x64_f8f6f4 v[66:81], v[210:217], v[2:9], v[66:81], v200, v200 op_sel_hi:[0,0,0]
	ds_read_b128 v[210:213], v157 offset:4096
	ds_read_b128 v[214:217], v158 offset:4096
	v_exp_f32_e32 v105, v0
	v_fmamk_f32 v0, v121, 0x3e0293ee, v196
	v_exp_f32_e32 v121, v0
	v_fmamk_f32 v0, v106, 0x3e0293ee, v196
	v_exp_f32_e32 v106, v0
	v_fmamk_f32 v0, v122, 0x3e0293ee, v196
	v_exp_f32_e32 v122, v0
	v_fmamk_f32 v0, v107, 0x3e0293ee, v196
	v_exp_f32_e32 v107, v0
	v_fmamk_f32 v0, v123, 0x3e0293ee, v196
	v_exp_f32_e32 v123, v0
	v_fmamk_f32 v0, v108, 0x3e0293ee, v196
	v_exp_f32_e32 v108, v0
	v_fmamk_f32 v0, v124, 0x3e0293ee, v196
	s_waitcnt lgkmcnt(0)
	v_mfma_scale_f32_32x32x64_f8f6f4 v[50:65], v[210:217], v[2:9], v[50:65], v200, v200 op_sel_hi:[0,0,0]
	ds_read_b128 v[210:213], v157 offset:8192
	ds_read_b128 v[214:217], v158 offset:8192
	v_exp_f32_e32 v124, v0
	v_fmamk_f32 v0, v109, 0x3e0293ee, v196
	v_exp_f32_e32 v109, v0
	v_fmamk_f32 v0, v125, 0x3e0293ee, v196
	v_exp_f32_e32 v125, v0
	v_fmamk_f32 v0, v110, 0x3e0293ee, v196
	v_exp_f32_e32 v110, v0
	v_fmamk_f32 v0, v126, 0x3e0293ee, v196
	v_exp_f32_e32 v126, v0
	v_fmamk_f32 v0, v111, 0x3e0293ee, v196
	v_exp_f32_e32 v111, v0
	v_fmamk_f32 v0, v127, 0x3e0293ee, v196
	v_exp_f32_e32 v127, v0
	s_mov_b32 s46, s40
	s_waitcnt lgkmcnt(0)
	v_mfma_scale_f32_32x32x64_f8f6f4 v[34:49], v[210:217], v[2:9], v[34:49], v200, v200 op_sel_hi:[0,0,0]
	ds_read_b128 v[216:219], v157 offset:12288
	ds_read_b128 v[220:223], v158 offset:12288
	s_mov_b32 s47, s40
	v_fmamk_f32 v0, v112, 0x3e0293ee, v196
	s_mov_b32 s41, s40
	s_mov_b32 s42, s40
	s_mov_b32 s43, s40
	s_mov_b32 s44, s40
	s_mov_b32 s45, s40
	v_exp_f32_e32 v112, v0
	v_fmamk_f32 v0, v128, 0x3e0293ee, v196
	v_exp_f32_e32 v128, v0
	v_fmamk_f32 v0, v113, 0x3e0293ee, v196
	v_fmac_f32_e32 v196, 0x3e0293ee, v129
	s_nop 0
	s_nop 0
	s_waitcnt lgkmcnt(0)
	v_mfma_scale_f32_32x32x64_f8f6f4 v[18:33], v[216:223], v[2:9], v[18:33], v200, v200 op_sel_hi:[0,0,0]
	v_mov_b64_e32 v[224:225], s[46:47]
	v_mov_b64_e32 v[222:223], s[44:45]
	v_mov_b64_e32 v[220:221], s[42:43]
	v_mov_b64_e32 v[218:219], s[40:41]
	s_nop 0
	s_nop 0
	s_nop 0
	s_nop 0
	s_nop 0
	s_nop 0
	v_exp_f32_e32 v113, v0
	v_cvt_pk_fp8_f32 v210, v98, v99
	v_exp_f32_e32 v129, v196
	v_cvt_pk_fp8_f32 v214, v114, v115
	v_cvt_pk_fp8_f32 v211, v102, v103
	v_cvt_pk_fp8_f32 v215, v118, v119
	v_cvt_pk_fp8_f32 v212, v106, v107
	v_cvt_pk_fp8_f32 v216, v122, v123
	v_cvt_pk_fp8_f32 v213, v110, v111
	v_cvt_pk_fp8_f32 v217, v126, v127
	v_add_u32_e32 v0, v156, v191
	v_mfma_scale_f32_32x32x64_f8f6f4 v[82:97], v[218:225], v[2:9], v[82:97], v200, v200 op_sel_hi:[0,0,0]
	v_add_u32_e32 v156, v156, v192
	ds_read_b128 v[2:5], v0
	ds_read_b128 v[6:9], v156
	v_cvt_pk_fp8_f32 v210, v100, v101 op_sel:[0,0,1]
	v_cvt_pk_fp8_f32 v214, v116, v117 op_sel:[0,0,1]
	v_cvt_pk_fp8_f32 v211, v104, v105 op_sel:[0,0,1]
	v_cvt_pk_fp8_f32 v215, v120, v121 op_sel:[0,0,1]
	v_cvt_pk_fp8_f32 v212, v108, v109 op_sel:[0,0,1]
	v_cvt_pk_fp8_f32 v216, v124, v125 op_sel:[0,0,1]
	v_cvt_pk_fp8_f32 v213, v112, v113 op_sel:[0,0,1]
	v_cvt_pk_fp8_f32 v217, v128, v129 op_sel:[0,0,1]
	s_waitcnt lgkmcnt(0)
	s_nop 0
	v_mfma_scale_f32_32x32x64_f8f6f4 v[66:81], v[2:9], v[210:217], v[66:81], v200, v200 op_sel_hi:[0,0,0]
	ds_read_b128 v[2:5], v0 offset:4096
	ds_read_b128 v[6:9], v156 offset:4096
	s_waitcnt lgkmcnt(0)
	v_mfma_scale_f32_32x32x64_f8f6f4 v[50:65], v[2:9], v[210:217], v[50:65], v200, v200 op_sel_hi:[0,0,0]
	ds_read_b128 v[2:5], v0 offset:8192
	ds_read_b128 v[6:9], v156 offset:8192
	s_waitcnt lgkmcnt(0)
	v_mfma_scale_f32_32x32x64_f8f6f4 v[34:49], v[2:9], v[210:217], v[34:49], v200, v200 op_sel_hi:[0,0,0]
	ds_read_b128 v[2:5], v0 offset:12288
	ds_read_b128 v[6:9], v156 offset:12288
	s_waitcnt lgkmcnt(0)
	v_mfma_scale_f32_32x32x64_f8f6f4 v[18:33], v[2:9], v[210:217], v[18:33], v200, v200 op_sel_hi:[0,0,0]
	v_mfma_scale_f32_32x32x64_f8f6f4 v[82:97], v[218:225], v[210:217], v[82:97], v200, v200 op_sel_hi:[0,0,0]

.LBB0_852:
	s_and_b64 vcc, exec, s[4:5]
	s_cbranch_vccz .LBB0_872
	s_waitcnt vmcnt(18)
	v_mov_b32_e32 v6, v198
	v_readlane_b32 s2, v252, 31
	v_readfirstlane_b32 s1, v6
	s_ashr_i32 s24, s1, 6
	s_lshl_b32 s1, s24, 5
	v_and_b32_e32 v14, 31, v6
	s_add_i32 s0, s1, s0
	v_or_b32_e32 v210, s0, v14
	v_readlane_b32 s3, v252, 32
	v_add_u32_e32 v2, s2, v210
	v_ashrrev_i32_e32 v3, 31, v2
	v_readlane_b32 s2, v254, 55
	v_lshlrev_b64 v[192:193], 11, v[2:3]
	v_readlane_b32 s3, v254, 56
	v_and_b32_e32 v0, 32, v6
	v_bfe_u32 v209, v6, 5, 1
	v_lshl_add_u64 v[2:3], s[2:3], 0, v[192:193]
	v_lshl_add_u64 v[2:3], v[2:3], 0, v[0:1]
	global_load_dwordx4 v[180:183], v[2:3], off offset:16
	global_load_dwordx4 v[176:179], v[2:3], off
	global_load_dwordx4 v[188:191], v[2:3], off offset:80
	global_load_dwordx4 v[184:187], v[2:3], off offset:64
	v_lshlrev_b32_e32 v0, 4, v6
	v_ashrrev_i32_e32 v17, 3, v6
	s_waitcnt vmcnt(16)
	v_bitop3_b32 v34, v0, s57, v6 bitop3:0x48
	s_cmp_eq_u32 s53, 0
	v_bfe_u32 v15, v6, 1, 3
	s_cbranch_scc1 .LBB0_874
	v_cmp_gt_i32_e32 vcc, 32, v17
	s_and_saveexec_b64 s[4:5], vcc
	v_readlane_b32 s42, v252, 57
	v_readlane_b32 s43, v252, 58
	s_cbranch_execz .LBB0_858
	v_cmp_gt_i32_e32 vcc, 16, v17
	v_mov_b32_e32 v2, 0
	v_mov_b32_e32 v3, 0
	v_mov_b32_e32 v4, 0
	v_mov_b32_e32 v5, 0
	s_and_saveexec_b64 s[6:7], vcc
	s_cbranch_execz .LBB0_857
	v_readlane_b32 s2, v253, 37
	v_and_b32_e32 v0, 0x70, v0
	v_lshlrev_b32_e32 v0, 2, v0
	v_add_u32_e32 v2, s2, v17
	v_ashrrev_i32_e32 v3, 31, v2
	v_readlane_b32 s2, v253, 14
	v_lshlrev_b64 v[2:3], 13, v[2:3]
	v_readlane_b32 s3, v253, 15
	s_nop 1
	v_lshl_add_u64 v[2:3], s[2:3], 0, v[2:3]
	v_lshl_add_u64 v[12:13], v[2:3], 0, v[0:1]
	s_mov_b64 s[2:3], 0x1000
	v_lshl_add_u64 v[40:41], v[12:13], 0, s[2:3]
	global_load_dwordx4 v[8:11], v[12:13], off offset:48
	global_load_dwordx4 v[18:21], v[12:13], off offset:32
	global_load_dwordx4 v[22:25], v[12:13], off offset:16
	global_load_dwordx4 v[2:5], v[12:13], off
	v_add_co_u32_e32 v12, vcc, 0x1000, v12
	s_mov_b32 s2, 0x3d800000
	s_nop 0
	v_addc_co_u32_e32 v13, vcc, 0, v13, vcc
	global_load_dwordx4 v[26:29], v[12:13], off
	global_load_dwordx4 v[30:33], v[40:41], off offset:48
	global_load_dwordx4 v[36:39], v[40:41], off offset:32
	s_nop 0
	global_load_dwordx4 v[40:43], v[40:41], off offset:16
	s_waitcnt vmcnt(3)
	v_pk_add_f32 v[2:3], v[2:3], v[26:27]
	s_nop 0
	v_pk_mul_f32 v[12:13], v[2:3], s[2:3] op_sel_hi:[1,0]
	s_nop 0
	v_cvt_pk_fp8_f32 v2, v12, v13
	s_waitcnt vmcnt(0)
	v_pk_add_f32 v[12:13], v[22:23], v[40:41]
	s_nop 0
	v_pk_mul_f32 v[12:13], v[12:13], s[2:3] op_sel_hi:[1,0]
	v_pk_add_f32 v[4:5], v[4:5], v[28:29]
	v_cvt_pk_fp8_f32 v3, v12, v13
	v_pk_mul_f32 v[4:5], v[4:5], s[2:3] op_sel_hi:[1,0]
	v_pk_add_f32 v[12:13], v[18:19], v[36:37]
	v_cvt_pk_fp8_f32 v2, v4, v5 op_sel:[0,0,1]
	v_pk_add_f32 v[4:5], v[24:25], v[42:43]
	v_pk_add_f32 v[8:9], v[8:9], v[30:31]
	v_pk_mul_f32 v[4:5], v[4:5], s[2:3] op_sel_hi:[1,0]
	v_pk_mul_f32 v[12:13], v[12:13], s[2:3] op_sel_hi:[1,0]
	v_cvt_pk_fp8_f32 v3, v4, v5 op_sel:[0,0,1]
	v_pk_add_f32 v[4:5], v[20:21], v[38:39]
	v_pk_mul_f32 v[8:9], v[8:9], s[2:3] op_sel_hi:[1,0]
	v_pk_mul_f32 v[18:19], v[4:5], s[2:3] op_sel_hi:[1,0]
	s_nop 0
	s_nop 0
	v_cvt_pk_fp8_f32 v4, v12, v13
	v_cvt_pk_fp8_f32 v5, v8, v9
	v_pk_add_f32 v[10:11], v[10:11], v[32:33]
	v_cvt_pk_fp8_f32 v4, v18, v19 op_sel:[0,0,1]
	v_pk_mul_f32 v[10:11], v[10:11], s[2:3] op_sel_hi:[1,0]
	s_nop 0
	v_cvt_pk_fp8_f32 v5, v10, v11 op_sel:[0,0,1]

.LBB0_871:
	s_nop 3
	v_rcp_f32_e32 v8, v82
	v_readlane_b32 s2, v254, 37
	v_readlane_b32 s3, v254, 38
	v_lshlrev_b32_e32 v0, 4, v17
	s_nop 0
	v_lshl_add_u64 v[2:3], s[2:3], 0, v[178:179]
	v_lshl_add_u64 v[6:7], v[2:3], 0, v[0:1]
	v_mul_f32_e32 v0, v66, v8
	v_mul_f32_e32 v3, v67, v8
	s_nop 0
	v_cvt_pk_fp8_f32 v2, v0, v3
	v_mul_f32_e32 v0, v70, v8
	v_mul_f32_e32 v3, v71, v8
	v_cvt_pk_fp8_f32 v4, v0, v3
	v_mul_f32_e32 v5, v68, v8
	v_mul_f32_e32 v9, v69, v8
	v_mul_f32_e32 v0, v72, v8
	v_mul_f32_e32 v3, v73, v8
	v_cvt_pk_fp8_f32 v2, v5, v9 op_sel:[0,0,1]
	v_cvt_pk_fp8_f32 v4, v0, v3 op_sel:[0,0,1]
	v_mul_f32_e32 v0, v74, v8
	v_mul_f32_e32 v5, v75, v8
	s_nop 0
	v_cvt_pk_fp8_f32 v3, v0, v5
	v_mul_f32_e32 v0, v78, v8
	v_mul_f32_e32 v11, v79, v8
	s_nop 0
	v_cvt_pk_fp8_f32 v5, v0, v11
	v_mul_f32_e32 v9, v76, v8
	v_mul_f32_e32 v10, v77, v8
	v_cvt_pk_fp8_f32 v3, v9, v10 op_sel:[0,0,1]
	v_mul_f32_e32 v0, v80, v8
	v_mul_f32_e32 v9, v81, v8
	v_cvt_pk_fp8_f32 v5, v0, v9 op_sel:[0,0,1]
	v_permlane32_swap_b32_e32 v2, v3
	v_mul_f32_e32 v0, v50, v8
	v_permlane32_swap_b32_e32 v4, v5
	global_store_dwordx4 v[6:7], v[2:5], off
	v_mul_f32_e32 v9, v53, v8
	v_mul_f32_e32 v11, v63, v8
	v_mul_f32_e32 v3, v51, v8
	s_nop 0
	v_cvt_pk_fp8_f32 v2, v0, v3
	v_mul_f32_e32 v0, v54, v8
	v_mul_f32_e32 v3, v55, v8
	s_nop 0
	v_cvt_pk_fp8_f32 v4, v0, v3
	v_mul_f32_e32 v5, v52, v8
	v_mul_f32_e32 v0, v56, v8
	v_mul_f32_e32 v3, v57, v8
	v_cvt_pk_fp8_f32 v2, v5, v9 op_sel:[0,0,1]
	v_cvt_pk_fp8_f32 v4, v0, v3 op_sel:[0,0,1]
	v_mul_f32_e32 v0, v58, v8
	v_mul_f32_e32 v5, v59, v8
	s_nop 0
	v_cvt_pk_fp8_f32 v3, v0, v5
	v_mul_f32_e32 v0, v62, v8
	s_nop 0
	v_cvt_pk_fp8_f32 v5, v0, v11
	v_mul_f32_e32 v9, v60, v8
	v_mul_f32_e32 v10, v61, v8
	v_cvt_pk_fp8_f32 v3, v9, v10 op_sel:[0,0,1]
	v_mul_f32_e32 v0, v64, v8
	v_mul_f32_e32 v9, v65, v8
	v_cvt_pk_fp8_f32 v5, v0, v9 op_sel:[0,0,1]
	v_permlane32_swap_b32_e32 v2, v3
	v_mul_f32_e32 v0, v34, v8
	v_permlane32_swap_b32_e32 v4, v5
	global_store_dwordx4 v[6:7], v[2:5], off offset:32
	v_mul_f32_e32 v9, v37, v8
	v_mul_f32_e32 v11, v47, v8
	v_mul_f32_e32 v3, v35, v8
	s_nop 0
	v_cvt_pk_fp8_f32 v2, v0, v3
	v_mul_f32_e32 v0, v38, v8
	v_mul_f32_e32 v3, v39, v8
	s_nop 0
	v_cvt_pk_fp8_f32 v4, v0, v3
	v_mul_f32_e32 v5, v36, v8
	v_mul_f32_e32 v0, v40, v8
	v_mul_f32_e32 v3, v41, v8
	v_cvt_pk_fp8_f32 v2, v5, v9 op_sel:[0,0,1]
	v_cvt_pk_fp8_f32 v4, v0, v3 op_sel:[0,0,1]
	v_mul_f32_e32 v0, v42, v8
	v_mul_f32_e32 v5, v43, v8
	s_nop 0
	v_cvt_pk_fp8_f32 v3, v0, v5
	v_mul_f32_e32 v0, v46, v8
	s_nop 0
	v_cvt_pk_fp8_f32 v5, v0, v11
	v_mul_f32_e32 v9, v44, v8
	v_mul_f32_e32 v10, v45, v8
	v_cvt_pk_fp8_f32 v3, v9, v10 op_sel:[0,0,1]
	v_mul_f32_e32 v0, v48, v8
	v_mul_f32_e32 v9, v49, v8
	v_cvt_pk_fp8_f32 v5, v0, v9 op_sel:[0,0,1]
	v_permlane32_swap_b32_e32 v2, v3
	v_mul_f32_e32 v0, v18, v8
	v_permlane32_swap_b32_e32 v4, v5
	global_store_dwordx4 v[6:7], v[2:5], off offset:64
	v_mul_f32_e32 v9, v21, v8
	v_mul_f32_e32 v11, v31, v8
	v_mul_f32_e32 v3, v19, v8
	s_nop 0
	v_cvt_pk_fp8_f32 v2, v0, v3
	v_mul_f32_e32 v0, v22, v8
	v_mul_f32_e32 v3, v23, v8
	s_nop 0
	v_cvt_pk_fp8_f32 v4, v0, v3
	v_mul_f32_e32 v5, v20, v8
	v_mul_f32_e32 v0, v24, v8
	v_mul_f32_e32 v3, v25, v8
	v_cvt_pk_fp8_f32 v2, v5, v9 op_sel:[0,0,1]
	v_cvt_pk_fp8_f32 v4, v0, v3 op_sel:[0,0,1]
	v_mul_f32_e32 v0, v26, v8
	v_mul_f32_e32 v5, v27, v8
	s_nop 0
	v_cvt_pk_fp8_f32 v3, v0, v5
	v_mul_f32_e32 v0, v30, v8
	s_nop 0
	v_cvt_pk_fp8_f32 v5, v0, v11
	v_mul_f32_e32 v9, v28, v8
	v_mul_f32_e32 v10, v29, v8
	v_mul_f32_e32 v0, v32, v8
	v_mul_f32_e32 v8, v33, v8
	v_cvt_pk_fp8_f32 v3, v9, v10 op_sel:[0,0,1]
	v_cvt_pk_fp8_f32 v5, v0, v8 op_sel:[0,0,1]
	s_nop 0
	v_permlane32_swap_b32_e32 v2, v3
	v_permlane32_swap_b32_e32 v4, v5
	global_store_dwordx4 v[6:7], v[2:5], off offset:96
	s_waitcnt vmcnt(0) lgkmcnt(0)
	s_barrier

.LBB0_888:
	s_nop 0
	s_nop 0
	s_nop 0
	s_nop 0
	s_nop 0
	s_nop 0
	s_nop 0
	s_nop 0
	v_cvt_pk_fp8_f32 v2, v13, v15
	v_cvt_pk_fp8_f32 v6, v10, v11
	v_cvt_pk_fp8_f32 v3, v22, v24
	v_cvt_pk_fp8_f32 v7, v17, v19
	v_cvt_pk_fp8_f32 v4, v30, v144
	v_cvt_pk_fp8_f32 v8, v25, v27
	v_cvt_pk_fp8_f32 v5, v150, v152
	v_cvt_pk_fp8_f32 v9, v145, v147
	v_lshl_add_u32 v155, s33, 14, v213
	v_add_u32_e32 v164, v155, v214
	v_add_u32_e32 v166, v155, v215
	ds_read_b128 v[156:159], v164
	ds_read_b128 v[160:163], v166
	v_cvt_pk_fp8_f32 v2, v18, v20 op_sel:[0,0,1]
	v_cvt_pk_fp8_f32 v6, v12, v14 op_sel:[0,0,1]
	v_cvt_pk_fp8_f32 v3, v26, v28 op_sel:[0,0,1]
	v_cvt_pk_fp8_f32 v7, v21, v23 op_sel:[0,0,1]
	v_cvt_pk_fp8_f32 v4, v146, v148 op_sel:[0,0,1]
	v_cvt_pk_fp8_f32 v8, v29, v31 op_sel:[0,0,1]
	v_cvt_pk_fp8_f32 v5, v153, v154 op_sel:[0,0,1]
	v_cvt_pk_fp8_f32 v9, v149, v151 op_sel:[0,0,1]
	v_fmamk_f32 v0, v118, 0x3e0293ee, v220
	v_exp_f32_e32 v118, v0
	v_fmamk_f32 v0, v134, 0x3e0293ee, v220
	v_exp_f32_e32 v134, v0
	v_fmamk_f32 v0, v119, 0x3e0293ee, v220
	s_waitcnt lgkmcnt(0)
	v_mfma_scale_f32_32x32x64_f8f6f4 v[80:95], v[156:163], v[2:9], v[80:95], v200, v200 op_sel_hi:[0,0,0]
	ds_read_b128 v[156:159], v164 offset:4096
	ds_read_b128 v[160:163], v166 offset:4096
	v_exp_f32_e32 v119, v0
	v_fmamk_f32 v0, v135, 0x3e0293ee, v220
	v_exp_f32_e32 v135, v0
	v_fmamk_f32 v0, v120, 0x3e0293ee, v220
	v_exp_f32_e32 v120, v0
	v_fmamk_f32 v0, v136, 0x3e0293ee, v220
	v_exp_f32_e32 v136, v0
	v_fmamk_f32 v0, v121, 0x3e0293ee, v220
	v_exp_f32_e32 v121, v0
	v_fmamk_f32 v0, v137, 0x3e0293ee, v220
	v_exp_f32_e32 v137, v0
	v_fmamk_f32 v0, v122, 0x3e0293ee, v220
	v_exp_f32_e32 v122, v0
	v_fmamk_f32 v0, v138, 0x3e0293ee, v220
	s_waitcnt lgkmcnt(0)
	v_mfma_scale_f32_32x32x64_f8f6f4 v[64:79], v[156:163], v[2:9], v[64:79], v200, v200 op_sel_hi:[0,0,0]
	ds_read_b128 v[156:159], v164 offset:8192
	ds_read_b128 v[160:163], v166 offset:8192
	v_exp_f32_e32 v138, v0
	v_fmamk_f32 v0, v123, 0x3e0293ee, v220
	v_exp_f32_e32 v123, v0
	v_fmamk_f32 v0, v139, 0x3e0293ee, v220
	v_exp_f32_e32 v139, v0
	v_fmamk_f32 v0, v124, 0x3e0293ee, v220
	v_exp_f32_e32 v124, v0
	v_fmamk_f32 v0, v140, 0x3e0293ee, v220
	v_exp_f32_e32 v140, v0
	v_fmamk_f32 v0, v125, 0x3e0293ee, v220
	v_exp_f32_e32 v125, v0
	v_fmamk_f32 v0, v141, 0x3e0293ee, v220
	v_exp_f32_e32 v141, v0
	s_mov_b32 s46, s40
	s_waitcnt lgkmcnt(0)
	v_mfma_scale_f32_32x32x64_f8f6f4 v[48:63], v[156:163], v[2:9], v[48:63], v200, v200 op_sel_hi:[0,0,0]
	ds_read_b128 v[162:165], v164 offset:12288
	ds_read_b128 v[166:169], v166 offset:12288
	s_mov_b32 s47, s40
	v_fmamk_f32 v0, v126, 0x3e0293ee, v220
	s_mov_b32 s41, s40
	s_mov_b32 s42, s40
	s_mov_b32 s43, s40
	s_mov_b32 s44, s40
	s_mov_b32 s45, s40
	v_exp_f32_e32 v126, v0
	v_fmamk_f32 v0, v142, 0x3e0293ee, v220
	v_exp_f32_e32 v142, v0
	v_fmamk_f32 v0, v127, 0x3e0293ee, v220
	v_fmac_f32_e32 v220, 0x3e0293ee, v143
	s_nop 0
	s_nop 0
	s_waitcnt lgkmcnt(0)
	v_mfma_scale_f32_32x32x64_f8f6f4 v[32:47], v[162:169], v[2:9], v[32:47], v200, v200 op_sel_hi:[0,0,0]
	v_mov_b64_e32 v[170:171], s[46:47]
	v_mov_b64_e32 v[168:169], s[44:45]
	v_mov_b64_e32 v[166:167], s[42:43]
	v_mov_b64_e32 v[164:165], s[40:41]
	s_nop 0
	s_nop 0
	s_nop 0
	s_nop 0
	s_nop 0
	s_nop 0
	v_exp_f32_e32 v127, v0
	v_cvt_pk_fp8_f32 v156, v112, v113
	v_exp_f32_e32 v143, v220
	v_cvt_pk_fp8_f32 v160, v128, v129
	v_cvt_pk_fp8_f32 v157, v116, v117
	v_cvt_pk_fp8_f32 v161, v132, v133
	v_cvt_pk_fp8_f32 v158, v120, v121
	v_cvt_pk_fp8_f32 v162, v136, v137
	v_cvt_pk_fp8_f32 v159, v124, v125
	v_cvt_pk_fp8_f32 v163, v140, v141
	v_add_u32_e32 v0, v155, v216
	v_mfma_scale_f32_32x32x64_f8f6f4 v[96:111], v[164:171], v[2:9], v[96:111], v200, v200 op_sel_hi:[0,0,0]
	v_add_u32_e32 v155, v155, v217
	ds_read_b128 v[2:5], v0
	ds_read_b128 v[6:9], v155
	v_cvt_pk_fp8_f32 v156, v114, v115 op_sel:[0,0,1]
	v_cvt_pk_fp8_f32 v160, v130, v131 op_sel:[0,0,1]
	v_cvt_pk_fp8_f32 v157, v118, v119 op_sel:[0,0,1]
	v_cvt_pk_fp8_f32 v161, v134, v135 op_sel:[0,0,1]
	v_cvt_pk_fp8_f32 v158, v122, v123 op_sel:[0,0,1]
	v_cvt_pk_fp8_f32 v162, v138, v139 op_sel:[0,0,1]
	v_cvt_pk_fp8_f32 v159, v126, v127 op_sel:[0,0,1]
	v_cvt_pk_fp8_f32 v163, v142, v143 op_sel:[0,0,1]
	s_waitcnt lgkmcnt(0)
	s_nop 0
	v_mfma_scale_f32_32x32x64_f8f6f4 v[80:95], v[2:9], v[156:163], v[80:95], v200, v200 op_sel_hi:[0,0,0]
	ds_read_b128 v[2:5], v0 offset:4096
	ds_read_b128 v[6:9], v155 offset:4096
	s_waitcnt lgkmcnt(0)
	v_mfma_scale_f32_32x32x64_f8f6f4 v[64:79], v[2:9], v[156:163], v[64:79], v200, v200 op_sel_hi:[0,0,0]
	ds_read_b128 v[2:5], v0 offset:8192
	ds_read_b128 v[6:9], v155 offset:8192
	s_waitcnt lgkmcnt(0)
	v_mfma_scale_f32_32x32x64_f8f6f4 v[48:63], v[2:9], v[156:163], v[48:63], v200, v200 op_sel_hi:[0,0,0]
	ds_read_b128 v[2:5], v0 offset:12288
	ds_read_b128 v[6:9], v155 offset:12288
	s_waitcnt lgkmcnt(0)
	v_mfma_scale_f32_32x32x64_f8f6f4 v[32:47], v[2:9], v[156:163], v[32:47], v200, v200 op_sel_hi:[0,0,0]
	v_mfma_scale_f32_32x32x64_f8f6f4 v[96:111], v[164:171], v[156:163], v[96:111], v200, v200 op_sel_hi:[0,0,0]

.LBB0_912:
	s_nop 3
	v_rcp_f32_e32 v8, v96
	v_readlane_b32 s0, v254, 57
	v_readlane_b32 s1, v254, 58
	v_lshlrev_b32_e32 v0, 4, v209
	s_nop 0
	v_lshl_add_u64 v[2:3], s[0:1], 0, v[192:193]
	v_lshl_add_u64 v[6:7], v[2:3], 0, v[0:1]
	v_mul_f32_e32 v0, v80, v8
	v_mul_f32_e32 v3, v81, v8
	s_nop 0
	v_cvt_pk_fp8_f32 v2, v0, v3
	v_mul_f32_e32 v0, v84, v8
	v_mul_f32_e32 v3, v85, v8
	v_cvt_pk_fp8_f32 v4, v0, v3
	v_mul_f32_e32 v5, v82, v8
	v_mul_f32_e32 v9, v83, v8
	v_mul_f32_e32 v0, v86, v8
	v_mul_f32_e32 v3, v87, v8
	v_cvt_pk_fp8_f32 v2, v5, v9 op_sel:[0,0,1]
	v_cvt_pk_fp8_f32 v4, v0, v3 op_sel:[0,0,1]
	v_mul_f32_e32 v0, v88, v8
	v_mul_f32_e32 v5, v89, v8
	s_nop 0
	v_cvt_pk_fp8_f32 v3, v0, v5
	v_mul_f32_e32 v0, v92, v8
	v_mul_f32_e32 v11, v93, v8
	s_nop 0
	v_cvt_pk_fp8_f32 v5, v0, v11
	v_mul_f32_e32 v9, v90, v8
	v_mul_f32_e32 v10, v91, v8
	v_cvt_pk_fp8_f32 v3, v9, v10 op_sel:[0,0,1]
	v_mul_f32_e32 v0, v94, v8
	v_mul_f32_e32 v9, v95, v8
	v_cvt_pk_fp8_f32 v5, v0, v9 op_sel:[0,0,1]
	v_permlane32_swap_b32_e32 v2, v3
	v_mul_f32_e32 v0, v64, v8
	v_permlane32_swap_b32_e32 v4, v5
	global_store_dwordx4 v[6:7], v[2:5], off
	v_mul_f32_e32 v9, v67, v8
	v_mul_f32_e32 v11, v77, v8
	v_mul_f32_e32 v3, v65, v8
	s_nop 0
	v_cvt_pk_fp8_f32 v2, v0, v3
	v_mul_f32_e32 v0, v68, v8
	v_mul_f32_e32 v3, v69, v8
	s_nop 0
	v_cvt_pk_fp8_f32 v4, v0, v3
	v_mul_f32_e32 v5, v66, v8
	v_mul_f32_e32 v0, v70, v8
	v_mul_f32_e32 v3, v71, v8
	v_cvt_pk_fp8_f32 v2, v5, v9 op_sel:[0,0,1]
	v_cvt_pk_fp8_f32 v4, v0, v3 op_sel:[0,0,1]
	v_mul_f32_e32 v0, v72, v8
	v_mul_f32_e32 v5, v73, v8
	s_nop 0
	v_cvt_pk_fp8_f32 v3, v0, v5
	v_mul_f32_e32 v0, v76, v8
	s_nop 0
	v_cvt_pk_fp8_f32 v5, v0, v11
	v_mul_f32_e32 v9, v74, v8
	v_mul_f32_e32 v10, v75, v8
	v_cvt_pk_fp8_f32 v3, v9, v10 op_sel:[0,0,1]
	v_mul_f32_e32 v0, v78, v8
	v_mul_f32_e32 v9, v79, v8
	v_cvt_pk_fp8_f32 v5, v0, v9 op_sel:[0,0,1]
	v_permlane32_swap_b32_e32 v2, v3
	v_mul_f32_e32 v0, v48, v8
	v_permlane32_swap_b32_e32 v4, v5
	global_store_dwordx4 v[6:7], v[2:5], off offset:32
	v_mul_f32_e32 v9, v51, v8
	v_mul_f32_e32 v11, v61, v8
	v_mul_f32_e32 v3, v49, v8
	s_nop 0
	v_cvt_pk_fp8_f32 v2, v0, v3
	v_mul_f32_e32 v0, v52, v8
	v_mul_f32_e32 v3, v53, v8
	s_nop 0
	v_cvt_pk_fp8_f32 v4, v0, v3
	v_mul_f32_e32 v5, v50, v8
	v_mul_f32_e32 v0, v54, v8
	v_mul_f32_e32 v3, v55, v8
	v_cvt_pk_fp8_f32 v2, v5, v9 op_sel:[0,0,1]
	v_cvt_pk_fp8_f32 v4, v0, v3 op_sel:[0,0,1]
	v_mul_f32_e32 v0, v56, v8
	v_mul_f32_e32 v5, v57, v8
	s_nop 0
	v_cvt_pk_fp8_f32 v3, v0, v5
	v_mul_f32_e32 v0, v60, v8
	s_nop 0
	v_cvt_pk_fp8_f32 v5, v0, v11
	v_mul_f32_e32 v9, v58, v8
	v_mul_f32_e32 v10, v59, v8
	v_cvt_pk_fp8_f32 v3, v9, v10 op_sel:[0,0,1]
	v_mul_f32_e32 v0, v62, v8
	v_mul_f32_e32 v9, v63, v8
	v_cvt_pk_fp8_f32 v5, v0, v9 op_sel:[0,0,1]
	v_permlane32_swap_b32_e32 v2, v3
	v_mul_f32_e32 v0, v32, v8
	v_permlane32_swap_b32_e32 v4, v5
	global_store_dwordx4 v[6:7], v[2:5], off offset:64
	v_mul_f32_e32 v9, v35, v8
	v_mul_f32_e32 v11, v45, v8
	v_mul_f32_e32 v3, v33, v8
	s_nop 0
	v_cvt_pk_fp8_f32 v2, v0, v3
	v_mul_f32_e32 v0, v36, v8
	v_mul_f32_e32 v3, v37, v8
	s_nop 0
	v_cvt_pk_fp8_f32 v4, v0, v3
	v_mul_f32_e32 v5, v34, v8
	v_mul_f32_e32 v0, v38, v8
	v_mul_f32_e32 v3, v39, v8
	v_cvt_pk_fp8_f32 v2, v5, v9 op_sel:[0,0,1]
	v_cvt_pk_fp8_f32 v4, v0, v3 op_sel:[0,0,1]
	v_mul_f32_e32 v0, v40, v8
	v_mul_f32_e32 v5, v41, v8
	s_nop 0
	v_cvt_pk_fp8_f32 v3, v0, v5
	v_mul_f32_e32 v0, v44, v8
	s_nop 0
	v_cvt_pk_fp8_f32 v5, v0, v11
	v_mul_f32_e32 v9, v42, v8
	v_mul_f32_e32 v10, v43, v8
	v_mul_f32_e32 v0, v46, v8
	v_mul_f32_e32 v8, v47, v8
	v_cvt_pk_fp8_f32 v3, v9, v10 op_sel:[0,0,1]
	v_cvt_pk_fp8_f32 v5, v0, v8 op_sel:[0,0,1]
	s_mov_b64 s[54:55], 0x100
	v_permlane32_swap_b32_e32 v2, v3
	v_permlane32_swap_b32_e32 v4, v5
	global_store_dwordx4 v[6:7], v[2:5], off offset:96
	s_waitcnt vmcnt(0) lgkmcnt(0)
	s_barrier
	s_and_b64 vcc, exec, s[50:51]
	s_cbranch_vccnz .LBB0_873

.LBB0_975:
	s_waitcnt vmcnt(31)
	v_mov_b32_e32 v134, v2
	s_waitcnt vmcnt(30)
	v_mov_b32_e32 v135, v6
	v_pk_mul_f32 v[134:135], v[134:135], s[88:89] op_sel_hi:[1,0]
	s_nop 0
	v_cvt_pk_fp8_f32 v136, v134, v135
	s_waitcnt vmcnt(29)
	v_mov_b32_e32 v134, v10
	s_waitcnt vmcnt(28)
	v_mov_b32_e32 v135, v18
	v_pk_mul_f32 v[134:135], v[134:135], s[88:89] op_sel_hi:[1,0]
	s_nop 0
	v_cvt_pk_fp8_f32 v136, v134, v135 op_sel:[0,0,1]
	v_mov_b32_e32 v134, v3
	v_mov_b32_e32 v135, v7
	v_pk_mul_f32 v[134:135], v[134:135], s[88:89] op_sel_hi:[1,0]
	s_nop 0
	v_cvt_pk_fp8_f32 v137, v134, v135
	v_mov_b32_e32 v134, v11
	v_mov_b32_e32 v135, v19
	v_pk_mul_f32 v[134:135], v[134:135], s[88:89] op_sel_hi:[1,0]
	s_nop 0
	v_cvt_pk_fp8_f32 v137, v134, v135 op_sel:[0,0,1]
	v_mov_b32_e32 v134, v4
	v_mov_b32_e32 v135, v8
	v_pk_mul_f32 v[134:135], v[134:135], s[88:89] op_sel_hi:[1,0]
	v_mov_b32_e32 v144, v1
	v_cvt_pk_fp8_f32 v138, v134, v135
	v_mov_b32_e32 v134, v12
	v_mov_b32_e32 v135, v20
	v_pk_mul_f32 v[134:135], v[134:135], s[88:89] op_sel_hi:[1,0]
	v_mov_b32_e32 v145, v1
	v_cvt_pk_fp8_f32 v138, v134, v135 op_sel:[0,0,1]
	v_mov_b32_e32 v134, v5
	v_mov_b32_e32 v135, v9
	v_pk_mul_f32 v[134:135], v[134:135], s[88:89] op_sel_hi:[1,0]
	v_add_u32_e32 v152, 0x4000, v143
	v_cvt_pk_fp8_f32 v139, v134, v135
	v_mov_b32_e32 v134, v13
	v_mov_b32_e32 v135, v21
	v_pk_mul_f32 v[134:135], v[134:135], s[88:89] op_sel_hi:[1,0]
	v_add_u32_e32 v151, 0x8400, v143
	v_cvt_pk_fp8_f32 v139, v134, v135 op_sel:[0,0,1]
	s_waitcnt vmcnt(27)
	v_mov_b32_e32 v134, v22
	s_waitcnt vmcnt(26)
	v_mov_b32_e32 v135, v26
	ds_write2_b32 v143, v136, v137 offset1:33
	ds_write2_b32 v143, v138, v139 offset0:66 offset1:99
	v_pk_mul_f32 v[134:135], v[134:135], s[88:89] op_sel_hi:[1,0]
	s_nop 0
	v_cvt_pk_fp8_f32 v136, v134, v135
	s_waitcnt vmcnt(25)
	v_mov_b32_e32 v134, v30
	s_waitcnt vmcnt(24)
	v_mov_b32_e32 v135, v34
	v_pk_mul_f32 v[134:135], v[134:135], s[88:89] op_sel_hi:[1,0]
	s_nop 0
	v_cvt_pk_fp8_f32 v136, v134, v135 op_sel:[0,0,1]
	v_mov_b32_e32 v134, v23
	v_mov_b32_e32 v135, v27
	v_pk_mul_f32 v[134:135], v[134:135], s[88:89] op_sel_hi:[1,0]
	s_nop 0
	v_cvt_pk_fp8_f32 v137, v134, v135
	v_mov_b32_e32 v134, v31
	v_mov_b32_e32 v135, v35
	v_pk_mul_f32 v[134:135], v[134:135], s[88:89] op_sel_hi:[1,0]
	s_nop 0
	v_cvt_pk_fp8_f32 v137, v134, v135 op_sel:[0,0,1]
	v_mov_b32_e32 v134, v24
	v_mov_b32_e32 v135, v28
	v_pk_mul_f32 v[134:135], v[134:135], s[88:89] op_sel_hi:[1,0]
	v_mov_b32_e32 v146, v1
	v_cvt_pk_fp8_f32 v138, v134, v135
	v_mov_b32_e32 v134, v32
	v_mov_b32_e32 v135, v36
	v_pk_mul_f32 v[134:135], v[134:135], s[88:89] op_sel_hi:[1,0]
	s_cmp_lt_i32 s41, 2
	v_cvt_pk_fp8_f32 v138, v134, v135 op_sel:[0,0,1]
	v_mov_b32_e32 v134, v25
	v_mov_b32_e32 v135, v29
	v_pk_mul_f32 v[134:135], v[134:135], s[88:89] op_sel_hi:[1,0]
	s_nop 0
	v_cvt_pk_fp8_f32 v139, v134, v135
	v_mov_b32_e32 v134, v33
	v_mov_b32_e32 v135, v37
	v_pk_mul_f32 v[134:135], v[134:135], s[88:89] op_sel_hi:[1,0]
	s_nop 0
	v_cvt_pk_fp8_f32 v139, v134, v135 op_sel:[0,0,1]
	s_waitcnt vmcnt(23)
	v_mov_b32_e32 v134, v54
	s_waitcnt vmcnt(22)
	v_mov_b32_e32 v135, v58
	v_pk_mul_f32 v[134:135], v[134:135], s[88:89] op_sel_hi:[1,0]
	ds_write2_b32 v152, v136, v137 offset0:128 offset1:161
	ds_write2_b32 v152, v138, v139 offset0:194 offset1:227
	v_cvt_pk_fp8_f32 v144, v134, v135
	s_waitcnt vmcnt(21)
	v_mov_b32_e32 v134, v62
	s_waitcnt vmcnt(20)
	v_mov_b32_e32 v135, v66
	v_pk_mul_f32 v[134:135], v[134:135], s[88:89] op_sel_hi:[1,0]
	s_nop 0
	v_cvt_pk_fp8_f32 v144, v134, v135 op_sel:[0,0,1]
	v_mov_b32_e32 v134, v55
	v_mov_b32_e32 v135, v59
	v_pk_mul_f32 v[134:135], v[134:135], s[88:89] op_sel_hi:[1,0]
	s_nop 0
	v_cvt_pk_fp8_f32 v145, v134, v135
	v_mov_b32_e32 v134, v63
	v_mov_b32_e32 v135, v67
	v_pk_mul_f32 v[134:135], v[134:135], s[88:89] op_sel_hi:[1,0]
	s_nop 0
	v_cvt_pk_fp8_f32 v145, v134, v135 op_sel:[0,0,1]
	v_mov_b32_e32 v134, v56
	v_mov_b32_e32 v135, v60
	v_pk_mul_f32 v[134:135], v[134:135], s[88:89] op_sel_hi:[1,0]
	s_nop 0
	v_cvt_pk_fp8_f32 v136, v134, v135
	v_mov_b32_e32 v134, v64
	v_mov_b32_e32 v135, v68
	v_pk_mul_f32 v[134:135], v[134:135], s[88:89] op_sel_hi:[1,0]
	ds_write2_b32 v151, v144, v145 offset1:33
	v_cvt_pk_fp8_f32 v136, v134, v135 op_sel:[0,0,1]
	v_mov_b32_e32 v134, v57
	v_mov_b32_e32 v135, v61
	v_pk_mul_f32 v[134:135], v[134:135], s[88:89] op_sel_hi:[1,0]
	s_nop 0
	v_cvt_pk_fp8_f32 v137, v134, v135
	v_mov_b32_e32 v134, v65
	v_mov_b32_e32 v135, v69
	v_pk_mul_f32 v[134:135], v[134:135], s[88:89] op_sel_hi:[1,0]
	v_add_u32_e32 v144, 0xc400, v143
	v_cvt_pk_fp8_f32 v137, v134, v135 op_sel:[0,0,1]
	s_waitcnt vmcnt(19)
	v_mov_b32_e32 v134, v102
	s_waitcnt vmcnt(18)
	v_mov_b32_e32 v135, v106
	v_pk_mul_f32 v[134:135], v[134:135], s[88:89] op_sel_hi:[1,0]
	ds_write2_b32 v151, v136, v137 offset0:66 offset1:99
	v_cvt_pk_fp8_f32 v138, v134, v135
	s_waitcnt vmcnt(17)
	v_mov_b32_e32 v134, v110
	s_waitcnt vmcnt(16)
	v_mov_b32_e32 v135, v114
	v_pk_mul_f32 v[134:135], v[134:135], s[88:89] op_sel_hi:[1,0]
	s_nop 0
	v_cvt_pk_fp8_f32 v138, v134, v135 op_sel:[0,0,1]
	v_mov_b32_e32 v134, v103
	v_mov_b32_e32 v135, v107
	v_pk_mul_f32 v[134:135], v[134:135], s[88:89] op_sel_hi:[1,0]
	s_nop 0
	v_cvt_pk_fp8_f32 v139, v134, v135
	v_mov_b32_e32 v134, v111
	v_mov_b32_e32 v135, v115
	v_pk_mul_f32 v[134:135], v[134:135], s[88:89] op_sel_hi:[1,0]
	s_nop 0
	v_cvt_pk_fp8_f32 v139, v134, v135 op_sel:[0,0,1]
	v_mov_b32_e32 v134, v104
	v_mov_b32_e32 v135, v108
	v_pk_mul_f32 v[134:135], v[134:135], s[88:89] op_sel_hi:[1,0]
	s_nop 0
	v_cvt_pk_fp8_f32 v145, v134, v135
	v_mov_b32_e32 v134, v112
	v_mov_b32_e32 v135, v116
	v_pk_mul_f32 v[134:135], v[134:135], s[88:89] op_sel_hi:[1,0]
	s_nop 0
	v_cvt_pk_fp8_f32 v145, v134, v135 op_sel:[0,0,1]
	v_mov_b32_e32 v134, v105
	v_mov_b32_e32 v135, v109
	v_pk_mul_f32 v[134:135], v[134:135], s[88:89] op_sel_hi:[1,0]
	s_nop 0
	v_cvt_pk_fp8_f32 v146, v134, v135
	v_mov_b32_e32 v134, v113
	v_mov_b32_e32 v135, v117
	v_pk_mul_f32 v[134:135], v[134:135], s[88:89] op_sel_hi:[1,0]
	s_nop 0
	v_cvt_pk_fp8_f32 v146, v134, v135 op_sel:[0,0,1]
	ds_write2_b32 v144, v138, v139 offset0:128 offset1:161
	ds_write2_b32 v144, v145, v146 offset0:194 offset1:227
	s_waitcnt lgkmcnt(0)
	s_barrier
	ds_read2_b32 v[134:135], v142 offset1:1
	ds_read2_b32 v[136:137], v142 offset0:2 offset1:3
	v_lshl_add_u32 v139, s1, 6, v140
	s_cbranch_scc1 .LBB0_981
	s_cmp_gt_i32 s41, 2
	s_cbranch_scc0 .LBB0_982
	s_cmp_eq_u32 s41, 3
	s_mov_b64 s[52:53], -1
	s_cbranch_scc0 .LBB0_979
	v_lshlrev_b32_e32 v138, 1, v139
	v_and_b32_e32 v145, 0x7f, v139
	s_movk_i32 s15, 0xff00
	v_and_or_b32 v138, v138, s15, v145
	s_mov_b64 s[52:53], 0

.Lcvw_c2:
	v_mov_b32_e32 v136, v42
	v_mov_b32_e32 v137, v38
	v_pk_mul_f32 v[136:137], v[136:137], s[88:89] op_sel_hi:[1,0]
	s_nop 0
	v_cvt_pk_fp8_f32 v138, v136, v137
	v_mov_b32_e32 v136, v43
	v_mov_b32_e32 v137, v39
	v_pk_mul_f32 v[136:137], v[136:137], s[88:89] op_sel_hi:[1,0]
	s_nop 0
	v_mov_b32_e32 v134, v50
	v_mov_b32_e32 v135, v46
	v_cvt_pk_fp8_f32 v139, v136, v137
	v_pk_mul_f32 v[134:135], v[134:135], s[88:89] op_sel_hi:[1,0]
	v_mov_b32_e32 v136, v44
	v_cvt_pk_fp8_f32 v138, v134, v135 op_sel:[0,0,1]
	v_mov_b32_e32 v134, v51
	v_mov_b32_e32 v135, v47
	v_pk_mul_f32 v[134:135], v[134:135], s[88:89] op_sel_hi:[1,0]
	v_mov_b32_e32 v137, v40
	v_cvt_pk_fp8_f32 v139, v134, v135 op_sel:[0,0,1]
	v_pk_mul_f32 v[136:137], v[136:137], s[88:89] op_sel_hi:[1,0]
	v_mov_b32_e32 v134, v52
	v_mov_b32_e32 v135, v48
	ds_write2_b32 v143, v138, v139 offset1:33
	s_nop 0
	v_cvt_pk_fp8_f32 v138, v136, v137
	v_mov_b32_e32 v136, v45
	v_mov_b32_e32 v137, v41
	v_pk_mul_f32 v[136:137], v[136:137], s[88:89] op_sel_hi:[1,0]
	s_nop 0
	v_cvt_pk_fp8_f32 v139, v136, v137
	v_pk_mul_f32 v[134:135], v[134:135], s[88:89] op_sel_hi:[1,0]
	v_mov_b32_e32 v136, v74
	v_cvt_pk_fp8_f32 v138, v134, v135 op_sel:[0,0,1]
	v_mov_b32_e32 v134, v53
	v_mov_b32_e32 v135, v49
	v_pk_mul_f32 v[134:135], v[134:135], s[88:89] op_sel_hi:[1,0]
	v_mov_b32_e32 v137, v70
	v_cvt_pk_fp8_f32 v139, v134, v135 op_sel:[0,0,1]
	v_pk_mul_f32 v[136:137], v[136:137], s[88:89] op_sel_hi:[1,0]
	v_mov_b32_e32 v134, v82
	v_mov_b32_e32 v135, v78
	ds_write2_b32 v143, v138, v139 offset0:66 offset1:99
	s_nop 0
	v_cvt_pk_fp8_f32 v138, v136, v137
	v_mov_b32_e32 v136, v75
	v_mov_b32_e32 v137, v71
	v_pk_mul_f32 v[136:137], v[136:137], s[88:89] op_sel_hi:[1,0]
	s_nop 0
	v_cvt_pk_fp8_f32 v139, v136, v137
	v_pk_mul_f32 v[134:135], v[134:135], s[88:89] op_sel_hi:[1,0]
	v_mov_b32_e32 v136, v76
	v_cvt_pk_fp8_f32 v138, v134, v135 op_sel:[0,0,1]
	v_mov_b32_e32 v134, v83
	v_mov_b32_e32 v135, v79
	v_pk_mul_f32 v[134:135], v[134:135], s[88:89] op_sel_hi:[1,0]
	v_mov_b32_e32 v137, v72
	v_cvt_pk_fp8_f32 v139, v134, v135 op_sel:[0,0,1]
	v_pk_mul_f32 v[136:137], v[136:137], s[88:89] op_sel_hi:[1,0]
	v_mov_b32_e32 v134, v84
	v_mov_b32_e32 v135, v80
	ds_write2_b32 v152, v138, v139 offset0:128 offset1:161
	s_nop 0
	v_cvt_pk_fp8_f32 v138, v136, v137
	v_mov_b32_e32 v136, v77
	v_mov_b32_e32 v137, v73
	v_pk_mul_f32 v[136:137], v[136:137], s[88:89] op_sel_hi:[1,0]
	s_nop 0
	v_cvt_pk_fp8_f32 v139, v136, v137
	v_pk_mul_f32 v[134:135], v[134:135], s[88:89] op_sel_hi:[1,0]
	v_mov_b32_e32 v136, v90
	v_cvt_pk_fp8_f32 v138, v134, v135 op_sel:[0,0,1]
	v_mov_b32_e32 v134, v85
	v_mov_b32_e32 v135, v81
	v_pk_mul_f32 v[134:135], v[134:135], s[88:89] op_sel_hi:[1,0]
	v_mov_b32_e32 v137, v86
	v_cvt_pk_fp8_f32 v139, v134, v135 op_sel:[0,0,1]
	v_pk_mul_f32 v[136:137], v[136:137], s[88:89] op_sel_hi:[1,0]
	v_mov_b32_e32 v134, v98
	v_mov_b32_e32 v135, v94
	ds_write2_b32 v152, v138, v139 offset0:194 offset1:227
	s_nop 0
	v_cvt_pk_fp8_f32 v138, v136, v137
	v_mov_b32_e32 v136, v91
	v_mov_b32_e32 v137, v87
	v_pk_mul_f32 v[136:137], v[136:137], s[88:89] op_sel_hi:[1,0]
	s_nop 0
	v_cvt_pk_fp8_f32 v139, v136, v137
	v_pk_mul_f32 v[134:135], v[134:135], s[88:89] op_sel_hi:[1,0]
	v_mov_b32_e32 v136, v92
	v_cvt_pk_fp8_f32 v138, v134, v135 op_sel:[0,0,1]
	v_mov_b32_e32 v134, v99
	v_mov_b32_e32 v135, v95
	v_pk_mul_f32 v[134:135], v[134:135], s[88:89] op_sel_hi:[1,0]
	v_mov_b32_e32 v137, v88
	v_cvt_pk_fp8_f32 v139, v134, v135 op_sel:[0,0,1]
	v_pk_mul_f32 v[136:137], v[136:137], s[88:89] op_sel_hi:[1,0]
	v_mov_b32_e32 v134, v100
	v_mov_b32_e32 v135, v96
	ds_write2_b32 v151, v138, v139 offset1:33
	s_nop 0
	v_cvt_pk_fp8_f32 v138, v136, v137
	v_mov_b32_e32 v136, v93
	v_mov_b32_e32 v137, v89
	v_pk_mul_f32 v[136:137], v[136:137], s[88:89] op_sel_hi:[1,0]
	s_nop 0
	v_cvt_pk_fp8_f32 v139, v136, v137
	v_pk_mul_f32 v[134:135], v[134:135], s[88:89] op_sel_hi:[1,0]
	v_mov_b32_e32 v136, v122
	v_cvt_pk_fp8_f32 v138, v134, v135 op_sel:[0,0,1]
	v_mov_b32_e32 v134, v101
	v_mov_b32_e32 v135, v97
	v_pk_mul_f32 v[134:135], v[134:135], s[88:89] op_sel_hi:[1,0]
	v_mov_b32_e32 v137, v118
	v_cvt_pk_fp8_f32 v139, v134, v135 op_sel:[0,0,1]
	v_pk_mul_f32 v[136:137], v[136:137], s[88:89] op_sel_hi:[1,0]
	v_mov_b32_e32 v134, v130
	v_mov_b32_e32 v135, v126
	ds_write2_b32 v151, v138, v139 offset0:66 offset1:99
	s_nop 0
	v_cvt_pk_fp8_f32 v138, v136, v137
	v_mov_b32_e32 v136, v123
	v_mov_b32_e32 v137, v119
	v_pk_mul_f32 v[136:137], v[136:137], s[88:89] op_sel_hi:[1,0]
	s_nop 0
	v_cvt_pk_fp8_f32 v139, v136, v137
	v_pk_mul_f32 v[134:135], v[134:135], s[88:89] op_sel_hi:[1,0]
	v_mov_b32_e32 v136, v124
	v_cvt_pk_fp8_f32 v138, v134, v135 op_sel:[0,0,1]
	v_mov_b32_e32 v134, v131
	v_mov_b32_e32 v135, v127
	v_pk_mul_f32 v[134:135], v[134:135], s[88:89] op_sel_hi:[1,0]
	v_mov_b32_e32 v137, v120
	v_cvt_pk_fp8_f32 v139, v134, v135 op_sel:[0,0,1]
	v_pk_mul_f32 v[136:137], v[136:137], s[88:89] op_sel_hi:[1,0]
	v_mov_b32_e32 v134, v132
	v_mov_b32_e32 v135, v128
	ds_write2_b32 v144, v138, v139 offset0:128 offset1:161
	s_nop 0
	v_cvt_pk_fp8_f32 v138, v136, v137
	v_mov_b32_e32 v136, v125
	v_mov_b32_e32 v137, v121
	v_pk_mul_f32 v[136:137], v[136:137], s[88:89] op_sel_hi:[1,0]
	s_nop 0
	v_cvt_pk_fp8_f32 v139, v136, v137
	v_pk_mul_f32 v[134:135], v[134:135], s[88:89] op_sel_hi:[1,0]
	s_cmp_lt_i32 s83, 2
	v_cvt_pk_fp8_f32 v138, v134, v135 op_sel:[0,0,1]
	v_mov_b32_e32 v134, v133
	v_mov_b32_e32 v135, v129
	v_pk_mul_f32 v[134:135], v[134:135], s[88:89] op_sel_hi:[1,0]
	s_nop 0
	v_cvt_pk_fp8_f32 v139, v134, v135 op_sel:[0,0,1]
	ds_write2_b32 v144, v138, v139 offset0:194 offset1:227
	s_waitcnt lgkmcnt(0)
	s_barrier
	ds_read2_b32 v[134:135], v142 offset1:1
	ds_read2_b32 v[136:137], v142 offset0:2 offset1:3
	v_lshl_add_u32 v139, s57, 6, v140
	s_cbranch_scc1 .LBB0_1099
	s_cmp_gt_i32 s83, 2
	s_cbranch_scc0 .LBB0_1100
	s_cmp_eq_u32 s83, 3
	s_mov_b64 s[62:63], -1
	s_cbranch_scc0 .LBB0_1097
	v_lshlrev_b32_e32 v138, 1, v139
	v_and_b32_e32 v144, 0x7f, v139
	s_movk_i32 s11, 0xff00
	v_and_or_b32 v138, v138, s11, v144
	s_mov_b64 s[62:63], 0

.LBB0_1294:
	s_waitcnt vmcnt(0)
	v_mov_b32_e32 v128, v0
	s_waitcnt vmcnt(14)
	v_mov_b32_e32 v129, v4
	v_pk_mul_f32 v[128:129], v[128:129], s[50:51] op_sel_hi:[1,0]
	s_nop 0
	v_cvt_pk_fp8_f32 v130, v128, v129
	s_waitcnt vmcnt(13)
	v_mov_b32_e32 v128, v8
	s_waitcnt vmcnt(12)
	v_mov_b32_e32 v129, v12
	v_pk_mul_f32 v[128:129], v[128:129], s[50:51] op_sel_hi:[1,0]
	s_nop 0
	v_cvt_pk_fp8_f32 v130, v128, v129 op_sel:[0,0,1]
	v_mov_b32_e32 v128, v1
	v_mov_b32_e32 v129, v5
	v_pk_mul_f32 v[128:129], v[128:129], s[50:51] op_sel_hi:[1,0]
	s_nop 0
	v_cvt_pk_fp8_f32 v131, v128, v129
	v_mov_b32_e32 v128, v9
	v_mov_b32_e32 v129, v13
	v_pk_mul_f32 v[128:129], v[128:129], s[50:51] op_sel_hi:[1,0]
	s_nop 0
	v_cvt_pk_fp8_f32 v131, v128, v129 op_sel:[0,0,1]
	v_mov_b32_e32 v128, v2
	v_mov_b32_e32 v129, v6
	v_pk_mul_f32 v[128:129], v[128:129], s[50:51] op_sel_hi:[1,0]
	v_mov_b32_e32 v141, v133
	v_cvt_pk_fp8_f32 v132, v128, v129
	v_mov_b32_e32 v128, v10
	v_mov_b32_e32 v129, v14
	v_pk_mul_f32 v[128:129], v[128:129], s[50:51] op_sel_hi:[1,0]
	v_mov_b32_e32 v152, v133
	v_cvt_pk_fp8_f32 v132, v128, v129 op_sel:[0,0,1]
	v_mov_b32_e32 v128, v3
	v_mov_b32_e32 v129, v7
	v_pk_mul_f32 v[128:129], v[128:129], s[50:51] op_sel_hi:[1,0]
	v_add_u32_e32 v151, 0x4000, v149
	v_cvt_pk_fp8_f32 v140, v128, v129
	v_mov_b32_e32 v128, v11
	v_mov_b32_e32 v129, v15
	v_pk_mul_f32 v[128:129], v[128:129], s[50:51] op_sel_hi:[1,0]
	v_add_u32_e32 v150, 0x8400, v149
	v_cvt_pk_fp8_f32 v140, v128, v129 op_sel:[0,0,1]
	s_waitcnt vmcnt(11)
	v_mov_b32_e32 v128, v16
	s_waitcnt vmcnt(10)
	v_mov_b32_e32 v129, v20
	ds_write2_b32 v149, v130, v131 offset1:33
	ds_write2_b32 v149, v132, v140 offset0:66 offset1:99
	v_pk_mul_f32 v[128:129], v[128:129], s[50:51] op_sel_hi:[1,0]
	s_nop 0
	v_cvt_pk_fp8_f32 v130, v128, v129
	s_waitcnt vmcnt(9)
	v_mov_b32_e32 v128, v24
	s_waitcnt vmcnt(8)
	v_mov_b32_e32 v129, v28
	v_pk_mul_f32 v[128:129], v[128:129], s[50:51] op_sel_hi:[1,0]
	s_nop 0
	v_cvt_pk_fp8_f32 v130, v128, v129 op_sel:[0,0,1]
	v_mov_b32_e32 v128, v17
	v_mov_b32_e32 v129, v21
	v_pk_mul_f32 v[128:129], v[128:129], s[50:51] op_sel_hi:[1,0]
	s_nop 0
	v_cvt_pk_fp8_f32 v131, v128, v129
	v_mov_b32_e32 v128, v25
	v_mov_b32_e32 v129, v29
	v_pk_mul_f32 v[128:129], v[128:129], s[50:51] op_sel_hi:[1,0]
	s_nop 0
	v_cvt_pk_fp8_f32 v131, v128, v129 op_sel:[0,0,1]
	v_mov_b32_e32 v128, v18
	v_mov_b32_e32 v129, v22
	v_pk_mul_f32 v[128:129], v[128:129], s[50:51] op_sel_hi:[1,0]
	v_mov_b32_e32 v153, v133
	v_cvt_pk_fp8_f32 v132, v128, v129
	v_mov_b32_e32 v128, v26
	v_mov_b32_e32 v129, v30
	v_pk_mul_f32 v[128:129], v[128:129], s[50:51] op_sel_hi:[1,0]
	s_cmp_lt_i32 s55, 2
	v_cvt_pk_fp8_f32 v132, v128, v129 op_sel:[0,0,1]
	v_mov_b32_e32 v128, v19
	v_mov_b32_e32 v129, v23
	v_pk_mul_f32 v[128:129], v[128:129], s[50:51] op_sel_hi:[1,0]
	s_nop 0
	v_cvt_pk_fp8_f32 v140, v128, v129
	v_mov_b32_e32 v128, v27
	v_mov_b32_e32 v129, v31
	v_pk_mul_f32 v[128:129], v[128:129], s[50:51] op_sel_hi:[1,0]
	s_nop 0
	v_cvt_pk_fp8_f32 v140, v128, v129 op_sel:[0,0,1]
	s_waitcnt vmcnt(7)
	v_mov_b32_e32 v128, v48
	s_waitcnt vmcnt(6)
	v_mov_b32_e32 v129, v52
	v_pk_mul_f32 v[128:129], v[128:129], s[50:51] op_sel_hi:[1,0]
	ds_write2_b32 v151, v130, v131 offset0:128 offset1:161
	ds_write2_b32 v151, v132, v140 offset0:194 offset1:227
	v_cvt_pk_fp8_f32 v141, v128, v129
	s_waitcnt vmcnt(5)
	v_mov_b32_e32 v128, v56
	s_waitcnt vmcnt(4)
	v_mov_b32_e32 v129, v60
	v_pk_mul_f32 v[128:129], v[128:129], s[50:51] op_sel_hi:[1,0]
	s_nop 0
	v_cvt_pk_fp8_f32 v141, v128, v129 op_sel:[0,0,1]
	v_mov_b32_e32 v128, v49
	v_mov_b32_e32 v129, v53
	v_pk_mul_f32 v[128:129], v[128:129], s[50:51] op_sel_hi:[1,0]
	s_nop 0
	v_cvt_pk_fp8_f32 v152, v128, v129
	v_mov_b32_e32 v128, v57
	v_mov_b32_e32 v129, v61
	v_pk_mul_f32 v[128:129], v[128:129], s[50:51] op_sel_hi:[1,0]
	s_nop 0
	v_cvt_pk_fp8_f32 v152, v128, v129 op_sel:[0,0,1]
	v_mov_b32_e32 v128, v50
	v_mov_b32_e32 v129, v54
	v_pk_mul_f32 v[128:129], v[128:129], s[50:51] op_sel_hi:[1,0]
	s_nop 0
	v_cvt_pk_fp8_f32 v130, v128, v129
	v_mov_b32_e32 v128, v58
	v_mov_b32_e32 v129, v62
	v_pk_mul_f32 v[128:129], v[128:129], s[50:51] op_sel_hi:[1,0]
	ds_write2_b32 v150, v141, v152 offset1:33
	v_cvt_pk_fp8_f32 v130, v128, v129 op_sel:[0,0,1]
	v_mov_b32_e32 v128, v51
	v_mov_b32_e32 v129, v55
	v_pk_mul_f32 v[128:129], v[128:129], s[50:51] op_sel_hi:[1,0]
	s_nop 0
	v_cvt_pk_fp8_f32 v131, v128, v129
	v_mov_b32_e32 v128, v59
	v_mov_b32_e32 v129, v63
	v_pk_mul_f32 v[128:129], v[128:129], s[50:51] op_sel_hi:[1,0]
	v_add_u32_e32 v152, 0xc400, v149
	v_cvt_pk_fp8_f32 v131, v128, v129 op_sel:[0,0,1]
	s_waitcnt vmcnt(3)
	v_mov_b32_e32 v128, v96
	s_waitcnt vmcnt(2)
	v_mov_b32_e32 v129, v100
	v_pk_mul_f32 v[128:129], v[128:129], s[50:51] op_sel_hi:[1,0]
	ds_write2_b32 v150, v130, v131 offset0:66 offset1:99
	v_cvt_pk_fp8_f32 v132, v128, v129
	s_waitcnt vmcnt(1)
	v_mov_b32_e32 v128, v104
	s_waitcnt vmcnt(0)
	v_mov_b32_e32 v129, v108
	v_pk_mul_f32 v[128:129], v[128:129], s[50:51] op_sel_hi:[1,0]
	s_nop 0
	v_cvt_pk_fp8_f32 v132, v128, v129 op_sel:[0,0,1]
	v_mov_b32_e32 v128, v97
	v_mov_b32_e32 v129, v101
	v_pk_mul_f32 v[128:129], v[128:129], s[50:51] op_sel_hi:[1,0]
	s_nop 0
	v_cvt_pk_fp8_f32 v140, v128, v129
	v_mov_b32_e32 v128, v105
	v_mov_b32_e32 v129, v109
	v_pk_mul_f32 v[128:129], v[128:129], s[50:51] op_sel_hi:[1,0]
	s_nop 0
	v_cvt_pk_fp8_f32 v140, v128, v129 op_sel:[0,0,1]
	v_mov_b32_e32 v128, v98
	v_mov_b32_e32 v129, v102
	v_pk_mul_f32 v[128:129], v[128:129], s[50:51] op_sel_hi:[1,0]
	s_nop 0
	v_cvt_pk_fp8_f32 v141, v128, v129
	v_mov_b32_e32 v128, v106
	v_mov_b32_e32 v129, v110
	v_pk_mul_f32 v[128:129], v[128:129], s[50:51] op_sel_hi:[1,0]
	s_nop 0
	v_cvt_pk_fp8_f32 v141, v128, v129 op_sel:[0,0,1]
	v_mov_b32_e32 v128, v99
	v_mov_b32_e32 v129, v103
	v_pk_mul_f32 v[128:129], v[128:129], s[50:51] op_sel_hi:[1,0]
	s_nop 0
	v_cvt_pk_fp8_f32 v153, v128, v129
	v_mov_b32_e32 v128, v107
	v_mov_b32_e32 v129, v111
	v_pk_mul_f32 v[128:129], v[128:129], s[50:51] op_sel_hi:[1,0]
	s_nop 0
	v_cvt_pk_fp8_f32 v153, v128, v129 op_sel:[0,0,1]
	ds_write2_b32 v152, v132, v140 offset0:128 offset1:161
	ds_write2_b32 v152, v141, v153 offset0:194 offset1:227
	s_waitcnt lgkmcnt(0)
	s_barrier
	ds_read2_b32 v[128:129], v148 offset1:1
	ds_read2_b32 v[130:131], v148 offset0:2 offset1:3
	v_lshl_add_u32 v132, s1, 6, v142
	s_cbranch_scc1 .LBB0_1300
	s_cmp_gt_i32 s55, 2
	s_cbranch_scc0 .LBB0_1301
	s_cmp_eq_u32 s55, 3
	s_mov_b64 s[38:39], -1
	s_cbranch_scc0 .LBB0_1298
	v_lshlrev_b32_e32 v140, 1, v132
	v_and_b32_e32 v141, 0x7f, v132
	s_movk_i32 s5, 0xff00
	v_and_or_b32 v140, v140, s5, v141
	s_mov_b64 s[38:39], 0

.LBB0_1414:
	v_mov_b32_e32 v128, v36
	v_mov_b32_e32 v129, v32
	v_pk_mul_f32 v[128:129], v[128:129], s[50:51] op_sel_hi:[1,0]
	s_nop 0
	v_cvt_pk_fp8_f32 v130, v128, v129
	v_mov_b32_e32 v128, v44
	v_mov_b32_e32 v129, v40
	v_pk_mul_f32 v[128:129], v[128:129], s[50:51] op_sel_hi:[1,0]
	s_nop 0
	v_cvt_pk_fp8_f32 v130, v128, v129 op_sel:[0,0,1]
	v_mov_b32_e32 v128, v37
	v_mov_b32_e32 v129, v33
	v_pk_mul_f32 v[128:129], v[128:129], s[50:51] op_sel_hi:[1,0]
	s_nop 0
	v_cvt_pk_fp8_f32 v131, v128, v129
	v_mov_b32_e32 v128, v45
	v_mov_b32_e32 v129, v41
	v_pk_mul_f32 v[128:129], v[128:129], s[50:51] op_sel_hi:[1,0]
	s_nop 0
	v_cvt_pk_fp8_f32 v131, v128, v129 op_sel:[0,0,1]
	v_mov_b32_e32 v128, v38
	v_mov_b32_e32 v129, v34
	v_pk_mul_f32 v[128:129], v[128:129], s[50:51] op_sel_hi:[1,0]
	s_nop 0
	v_cvt_pk_fp8_f32 v132, v128, v129
	v_mov_b32_e32 v128, v46
	v_mov_b32_e32 v129, v42
	v_pk_mul_f32 v[128:129], v[128:129], s[50:51] op_sel_hi:[1,0]
	s_nop 0
	v_cvt_pk_fp8_f32 v132, v128, v129 op_sel:[0,0,1]
	v_mov_b32_e32 v128, v39
	v_mov_b32_e32 v129, v35
	v_pk_mul_f32 v[128:129], v[128:129], s[50:51] op_sel_hi:[1,0]
	s_nop 0
	v_cvt_pk_fp8_f32 v140, v128, v129
	v_mov_b32_e32 v128, v47
	v_mov_b32_e32 v129, v43
	v_pk_mul_f32 v[128:129], v[128:129], s[50:51] op_sel_hi:[1,0]
	s_nop 0
	v_cvt_pk_fp8_f32 v140, v128, v129 op_sel:[0,0,1]
	v_mov_b32_e32 v128, v68
	v_mov_b32_e32 v129, v64
	v_pk_mul_f32 v[128:129], v[128:129], s[50:51] op_sel_hi:[1,0]
	s_cmp_lt_i32 s24, 2
	v_cvt_pk_fp8_f32 v141, v128, v129
	v_mov_b32_e32 v128, v76
	v_mov_b32_e32 v129, v72
	v_pk_mul_f32 v[128:129], v[128:129], s[50:51] op_sel_hi:[1,0]
	s_nop 0
	v_cvt_pk_fp8_f32 v141, v128, v129 op_sel:[0,0,1]
	v_mov_b32_e32 v128, v69
	v_mov_b32_e32 v129, v65
	v_pk_mul_f32 v[128:129], v[128:129], s[50:51] op_sel_hi:[1,0]
	s_nop 0
	v_cvt_pk_fp8_f32 v159, v128, v129
	v_mov_b32_e32 v128, v77
	v_mov_b32_e32 v129, v73
	v_pk_mul_f32 v[128:129], v[128:129], s[50:51] op_sel_hi:[1,0]
	s_nop 0
	v_cvt_pk_fp8_f32 v159, v128, v129 op_sel:[0,0,1]
	v_mov_b32_e32 v128, v70
	v_mov_b32_e32 v129, v66
	v_pk_mul_f32 v[128:129], v[128:129], s[50:51] op_sel_hi:[1,0]
	s_nop 0
	v_cvt_pk_fp8_f32 v160, v128, v129
	v_mov_b32_e32 v128, v78
	v_mov_b32_e32 v129, v74
	v_pk_mul_f32 v[128:129], v[128:129], s[50:51] op_sel_hi:[1,0]
	s_nop 0
	v_cvt_pk_fp8_f32 v160, v128, v129 op_sel:[0,0,1]
	v_mov_b32_e32 v128, v71
	v_mov_b32_e32 v129, v67
	v_pk_mul_f32 v[128:129], v[128:129], s[50:51] op_sel_hi:[1,0]
	s_nop 0
	v_cvt_pk_fp8_f32 v161, v128, v129
	v_mov_b32_e32 v128, v79
	v_mov_b32_e32 v129, v75
	v_pk_mul_f32 v[128:129], v[128:129], s[50:51] op_sel_hi:[1,0]
	s_nop 0
	v_cvt_pk_fp8_f32 v161, v128, v129 op_sel:[0,0,1]
	v_mov_b32_e32 v128, v84
	v_mov_b32_e32 v129, v80
	ds_write2_b32 v149, v130, v131 offset1:33
	ds_write2_b32 v149, v132, v140 offset0:66 offset1:99
	ds_write2_b32 v151, v141, v159 offset0:128 offset1:161
	ds_write2_b32 v151, v160, v161 offset0:194 offset1:227
	v_pk_mul_f32 v[128:129], v[128:129], s[50:51] op_sel_hi:[1,0]
	s_nop 0
	v_cvt_pk_fp8_f32 v130, v128, v129
	v_mov_b32_e32 v128, v92
	v_mov_b32_e32 v129, v88
	v_pk_mul_f32 v[128:129], v[128:129], s[50:51] op_sel_hi:[1,0]
	s_nop 0
	v_cvt_pk_fp8_f32 v130, v128, v129 op_sel:[0,0,1]
	v_mov_b32_e32 v128, v85
	v_mov_b32_e32 v129, v81
	v_pk_mul_f32 v[128:129], v[128:129], s[50:51] op_sel_hi:[1,0]
	s_nop 0
	v_cvt_pk_fp8_f32 v131, v128, v129
	v_mov_b32_e32 v128, v93
	v_mov_b32_e32 v129, v89
	v_pk_mul_f32 v[128:129], v[128:129], s[50:51] op_sel_hi:[1,0]
	s_nop 0
	v_cvt_pk_fp8_f32 v131, v128, v129 op_sel:[0,0,1]
	v_mov_b32_e32 v128, v86
	v_mov_b32_e32 v129, v82
	v_pk_mul_f32 v[128:129], v[128:129], s[50:51] op_sel_hi:[1,0]
	s_nop 0
	v_cvt_pk_fp8_f32 v132, v128, v129
	v_mov_b32_e32 v128, v94
	v_mov_b32_e32 v129, v90
	v_pk_mul_f32 v[128:129], v[128:129], s[50:51] op_sel_hi:[1,0]
	s_nop 0
	v_cvt_pk_fp8_f32 v132, v128, v129 op_sel:[0,0,1]
	v_mov_b32_e32 v128, v87
	v_mov_b32_e32 v129, v83
	v_pk_mul_f32 v[128:129], v[128:129], s[50:51] op_sel_hi:[1,0]
	s_nop 0
	v_cvt_pk_fp8_f32 v140, v128, v129
	v_mov_b32_e32 v128, v95
	v_mov_b32_e32 v129, v91
	v_pk_mul_f32 v[128:129], v[128:129], s[50:51] op_sel_hi:[1,0]
	s_nop 0
	v_cvt_pk_fp8_f32 v140, v128, v129 op_sel:[0,0,1]
	v_mov_b32_e32 v128, v116
	v_mov_b32_e32 v129, v112
	v_pk_mul_f32 v[128:129], v[128:129], s[50:51] op_sel_hi:[1,0]
	s_nop 0
	v_cvt_pk_fp8_f32 v141, v128, v129
	v_mov_b32_e32 v128, v124
	v_mov_b32_e32 v129, v120
	v_pk_mul_f32 v[128:129], v[128:129], s[50:51] op_sel_hi:[1,0]
	s_nop 0
	v_cvt_pk_fp8_f32 v141, v128, v129 op_sel:[0,0,1]
	v_mov_b32_e32 v128, v117
	v_mov_b32_e32 v129, v113
	v_pk_mul_f32 v[128:129], v[128:129], s[50:51] op_sel_hi:[1,0]
	s_nop 0
	v_cvt_pk_fp8_f32 v151, v128, v129
	v_mov_b32_e32 v128, v125
	v_mov_b32_e32 v129, v121
	v_pk_mul_f32 v[128:129], v[128:129], s[50:51] op_sel_hi:[1,0]
	s_nop 0
	v_cvt_pk_fp8_f32 v151, v128, v129 op_sel:[0,0,1]
	v_mov_b32_e32 v128, v118
	v_mov_b32_e32 v129, v114
	v_pk_mul_f32 v[128:129], v[128:129], s[50:51] op_sel_hi:[1,0]
	s_nop 0
	v_cvt_pk_fp8_f32 v159, v128, v129
	v_mov_b32_e32 v128, v126
	v_mov_b32_e32 v129, v122
	v_pk_mul_f32 v[128:129], v[128:129], s[50:51] op_sel_hi:[1,0]
	s_nop 0
	v_cvt_pk_fp8_f32 v159, v128, v129 op_sel:[0,0,1]
	v_mov_b32_e32 v128, v119
	v_mov_b32_e32 v129, v115
	v_pk_mul_f32 v[128:129], v[128:129], s[50:51] op_sel_hi:[1,0]
	s_nop 0
	v_cvt_pk_fp8_f32 v160, v128, v129
	v_mov_b32_e32 v128, v127
	v_mov_b32_e32 v129, v123
	v_pk_mul_f32 v[128:129], v[128:129], s[50:51] op_sel_hi:[1,0]
	s_nop 0
	v_cvt_pk_fp8_f32 v160, v128, v129 op_sel:[0,0,1]
	ds_write2_b32 v150, v130, v131 offset1:33
	ds_write2_b32 v150, v132, v140 offset0:66 offset1:99
	ds_write2_b32 v152, v141, v151 offset0:128 offset1:161
	ds_write2_b32 v152, v159, v160 offset0:194 offset1:227
	s_waitcnt lgkmcnt(0)
	s_barrier
	ds_read2_b32 v[128:129], v148 offset1:1
	ds_read2_b32 v[130:131], v148 offset0:2 offset1:3
	v_lshl_add_u32 v132, s9, 6, v142
	s_cbranch_scc1 .LBB0_1420
	s_cmp_gt_i32 s24, 2
	s_cbranch_scc0 .LBB0_1421
	s_cmp_eq_u32 s24, 3
	s_mov_b64 s[40:41], -1
	s_cbranch_scc0 .LBB0_1418
	v_lshlrev_b32_e32 v140, 1, v132
	v_and_b32_e32 v141, 0x7f, v132
	s_movk_i32 s40, 0xff00
	v_and_or_b32 v140, v140, s40, v141
	s_mov_b64 s[40:41], 0

.Lpeel_exit_2:
	s_ashr_i32 s2, s13, 4
	s_mul_hi_i32 s3, s2, 0xc000
	s_mul_i32 s2, s2, 0xc000
	s_add_u32 s7, s69, s2
	s_addc_u32 s20, s71, s3
	s_lshl_b32 s2, s15, 8
	s_ashr_i32 s3, s2, 31
	s_lshl_b64 s[24:25], s[2:3], 2
	s_add_u32 s7, s7, s24
	v_mbcnt_lo_u32_b32 v132, -1, 0
	v_mbcnt_hi_u32_b32 v132, -1, v132
	s_addc_u32 s15, s20, s25
	v_ashrrev_i32_e32 v136, 4, v132
	s_lshl_b32 s20, s23, 2
	s_add_u32 s24, s7, s20
	v_lshlrev_b32_e32 v128, 2, v136
	s_addc_u32 s25, s15, 0
	v_ashrrev_i32_e32 v129, 31, v128
	v_lshl_add_u64 v[130:131], v[128:129], 2, s[24:25]
	v_lshlrev_b32_e32 v128, 3, v136
	global_load_dwordx4 v[136:139], v[130:131], off
	global_load_dwordx4 v[152:155], v[130:131], off offset:64
	global_load_dwordx4 v[196:199], v[130:131], off offset:512
	global_load_dwordx4 v[200:203], v[130:131], off offset:576
	s_lshl_b32 s7, s13, 8
	s_add_i32 s24, s7, s16
	s_ashr_i32 s25, s24, 31
	s_lshl_b64 s[24:25], s[24:25], 11
	s_add_u32 s7, s61, s24
	s_addc_u32 s13, s65, s25
	s_add_u32 s2, s7, s2
	s_addc_u32 s3, s13, s3
	v_bfi_b32 v128, -16, v128, v132
	s_add_u32 s2, s2, s23
	v_ashrrev_i32_e32 v129, 31, v128
	s_addc_u32 s3, s3, 0
	v_lshlrev_b64 v[128:129], 11, v[128:129]
	v_lshl_add_u64 v[128:129], s[2:3], 0, v[128:129]
	v_and_b32_e32 v132, 16, v132
	v_lshl_add_u64 v[128:129], v[128:129], 0, v[132:133]
	s_mov_b32 s2, 0x10000
	s_mov_b32 s13, s36
	s_mov_b32 s15, s6
	s_mov_b64 s[34:35], s[58:59]
	s_waitcnt vmcnt(0)
	v_pk_mul_f32 v[140:141], v[138:139], s[54:55] op_sel_hi:[1,0]
	v_pk_mul_f32 v[138:139], v[136:137], s[54:55] op_sel_hi:[1,0]
	v_pk_mul_f32 v[136:137], v[152:153], s[54:55] op_sel_hi:[1,0]
	v_pk_mul_f32 v[152:153], v[124:125], v[138:139]
	s_nop 0
	v_cvt_pk_fp8_f32 v124, v152, v153
	v_pk_mul_f32 v[126:127], v[126:127], v[140:141]
	v_pk_mul_f32 v[112:113], v[112:113], v[136:137]
	v_pk_mul_f32 v[110:111], v[110:111], v[140:141]
	v_cvt_pk_fp8_f32 v124, v126, v127 op_sel:[0,0,1]
	s_nop 0
	v_cvt_pk_fp8_f32 v127, v112, v113
	v_pk_mul_f32 v[112:113], v[108:109], v[138:139]
	s_nop 0
	v_cvt_pk_fp8_f32 v108, v112, v113
	v_pk_mul_f32 v[96:97], v[96:97], v[136:137]
	v_pk_mul_f32 v[142:143], v[154:155], s[54:55] op_sel_hi:[1,0]
	v_pk_mul_f32 v[94:95], v[94:95], v[140:141]
	v_cvt_pk_fp8_f32 v108, v110, v111 op_sel:[0,0,1]
	s_nop 0
	v_cvt_pk_fp8_f32 v111, v96, v97
	v_pk_mul_f32 v[98:99], v[98:99], v[142:143]
	v_pk_mul_f32 v[80:81], v[80:81], v[136:137]
	v_pk_mul_f32 v[78:79], v[78:79], v[140:141]
	v_cvt_pk_fp8_f32 v111, v98, v99 op_sel:[0,0,1]
	v_pk_mul_f32 v[98:99], v[92:93], v[138:139]
	s_nop 0
	v_cvt_pk_fp8_f32 v92, v98, v99
	v_pk_mul_f32 v[120:121], v[120:121], v[136:137]
	s_nop 0
	v_pk_mul_f32 v[116:117], v[116:117], v[138:139]
	v_cvt_pk_fp8_f32 v92, v94, v95 op_sel:[0,0,1]
	s_nop 0
	v_cvt_pk_fp8_f32 v95, v80, v81
	v_pk_mul_f32 v[80:81], v[76:77], v[138:139]
	s_nop 0
	v_cvt_pk_fp8_f32 v76, v80, v81
	s_nop 0
	v_pk_mul_f32 v[104:105], v[104:105], v[136:137]
	s_nop 0
	v_pk_mul_f32 v[100:101], v[100:101], v[138:139]
	s_nop 0
	v_pk_mul_f32 v[88:89], v[88:89], v[136:137]
	s_nop 0
	v_pk_mul_f32 v[84:85], v[84:85], v[138:139]
	s_nop 0
	v_cvt_pk_fp8_f32 v76, v78, v79 op_sel:[0,0,1]
	v_pk_mul_f32 v[72:73], v[72:73], v[136:137]
	s_nop 0
	v_pk_mul_f32 v[68:69], v[68:69], v[138:139]
	s_nop 0
	v_pk_mul_f32 v[64:65], v[64:65], v[136:137]
	s_nop 0
	v_cvt_pk_fp8_f32 v125, v120, v121
	v_cvt_pk_fp8_f32 v126, v116, v117
	v_cvt_pk_fp8_f32 v109, v104, v105
	v_cvt_pk_fp8_f32 v110, v100, v101
	v_cvt_pk_fp8_f32 v93, v88, v89
	v_cvt_pk_fp8_f32 v94, v84, v85
	v_cvt_pk_fp8_f32 v77, v72, v73
	v_cvt_pk_fp8_f32 v78, v68, v69
	v_cvt_pk_fp8_f32 v79, v64, v65
	v_pk_mul_f32 v[122:123], v[122:123], v[142:143]
	v_pk_mul_f32 v[118:119], v[118:119], v[140:141]
	v_pk_mul_f32 v[114:115], v[114:115], v[142:143]
	v_pk_mul_f32 v[106:107], v[106:107], v[142:143]
	v_pk_mul_f32 v[102:103], v[102:103], v[140:141]
	v_pk_mul_f32 v[90:91], v[90:91], v[142:143]
	v_pk_mul_f32 v[86:87], v[86:87], v[140:141]
	v_pk_mul_f32 v[82:83], v[82:83], v[142:143]
	v_pk_mul_f32 v[74:75], v[74:75], v[142:143]
	v_pk_mul_f32 v[70:71], v[70:71], v[140:141]
	v_pk_mul_f32 v[66:67], v[66:67], v[142:143]
	v_cvt_pk_fp8_f32 v125, v122, v123 op_sel:[0,0,1]
	v_cvt_pk_fp8_f32 v126, v118, v119 op_sel:[0,0,1]
	v_cvt_pk_fp8_f32 v127, v114, v115 op_sel:[0,0,1]
	v_cvt_pk_fp8_f32 v109, v106, v107 op_sel:[0,0,1]
	v_cvt_pk_fp8_f32 v110, v102, v103 op_sel:[0,0,1]
	v_add_co_u32_e32 v96, vcc, s2, v128
	v_cvt_pk_fp8_f32 v93, v90, v91 op_sel:[0,0,1]
	v_cvt_pk_fp8_f32 v94, v86, v87 op_sel:[0,0,1]
	v_cvt_pk_fp8_f32 v95, v82, v83 op_sel:[0,0,1]
	v_cvt_pk_fp8_f32 v77, v74, v75 op_sel:[0,0,1]
	v_cvt_pk_fp8_f32 v78, v70, v71 op_sel:[0,0,1]
	v_cvt_pk_fp8_f32 v79, v66, v67 op_sel:[0,0,1]
	v_addc_co_u32_e32 v97, vcc, 0, v129, vcc
	s_mov_b32 s2, 0x40000
	v_add_co_u32_e32 v64, vcc, s2, v128
	s_mov_b32 s2, 0x50000
	s_nop 0
	v_addc_co_u32_e32 v65, vcc, 0, v129, vcc
	v_permlane32_swap_b32_e32 v124, v126
	v_permlane32_swap_b32_e32 v125, v127
	v_permlane32_swap_b32_e32 v108, v110
	v_permlane32_swap_b32_e32 v109, v111
	v_permlane32_swap_b32_e32 v92, v94
	v_permlane32_swap_b32_e32 v93, v95
	v_permlane32_swap_b32_e32 v76, v78
	v_permlane32_swap_b32_e32 v77, v79
	v_add_co_u32_e32 v66, vcc, s2, v128
	v_permlane16_swap_b32_e32 v124, v125
	v_permlane16_swap_b32_e32 v126, v127
	v_permlane16_swap_b32_e32 v108, v109
	v_permlane16_swap_b32_e32 v110, v111
	v_permlane16_swap_b32_e32 v92, v93
	v_permlane16_swap_b32_e32 v94, v95
	v_permlane16_swap_b32_e32 v76, v77
	v_permlane16_swap_b32_e32 v78, v79
	v_addc_co_u32_e32 v67, vcc, 0, v129, vcc
	global_store_dwordx4 v[128:129], v[124:127], off
	global_store_dwordx4 v[96:97], v[108:111], off
	global_store_dwordx4 v[64:65], v[92:95], off
	global_store_dwordx4 v[66:67], v[76:79], off
	s_and_b64 vcc, exec, s[4:5]
	s_mov_b64 s[2:3], s[48:49]
	v_pk_mul_f32 v[72:73], v[198:199], s[54:55] op_sel_hi:[1,0]
	v_pk_mul_f32 v[70:71], v[196:197], s[54:55] op_sel_hi:[1,0]
	v_pk_mul_f32 v[68:69], v[200:201], s[54:55] op_sel_hi:[1,0]
	v_pk_mul_f32 v[76:77], v[60:61], v[70:71]
	s_nop 0
	v_cvt_pk_fp8_f32 v60, v76, v77
	v_pk_mul_f32 v[62:63], v[62:63], v[72:73]
	v_pk_mul_f32 v[48:49], v[48:49], v[68:69]
	v_pk_mul_f32 v[46:47], v[46:47], v[72:73]
	v_cvt_pk_fp8_f32 v60, v62, v63 op_sel:[0,0,1]
	s_nop 0
	v_cvt_pk_fp8_f32 v63, v48, v49
	v_pk_mul_f32 v[48:49], v[44:45], v[70:71]
	s_nop 0
	v_cvt_pk_fp8_f32 v44, v48, v49
	v_pk_mul_f32 v[32:33], v[32:33], v[68:69]
	v_pk_mul_f32 v[30:31], v[30:31], v[72:73]
	v_pk_mul_f32 v[16:17], v[16:17], v[68:69]
	v_cvt_pk_fp8_f32 v44, v46, v47 op_sel:[0,0,1]
	s_nop 0
	v_cvt_pk_fp8_f32 v47, v32, v33
	v_pk_mul_f32 v[32:33], v[28:29], v[70:71]
	s_nop 0
	v_cvt_pk_fp8_f32 v28, v32, v33
	v_pk_mul_f32 v[56:57], v[56:57], v[68:69]
	s_nop 0
	v_pk_mul_f32 v[52:53], v[52:53], v[70:71]
	v_cvt_pk_fp8_f32 v28, v30, v31 op_sel:[0,0,1]
	s_nop 0
	v_cvt_pk_fp8_f32 v31, v16, v17
	v_pk_mul_f32 v[16:17], v[12:13], v[70:71]
	s_nop 0
	v_cvt_pk_fp8_f32 v12, v16, v17
	s_nop 0
	v_pk_mul_f32 v[24:25], v[24:25], v[68:69]
	s_nop 0
	v_pk_mul_f32 v[20:21], v[20:21], v[70:71]
	s_nop 0
	v_pk_mul_f32 v[14:15], v[14:15], v[72:73]
	v_cvt_pk_fp8_f32 v61, v56, v57
	v_cvt_pk_fp8_f32 v62, v52, v53
	v_pk_mul_f32 v[40:41], v[40:41], v[68:69]
	s_nop 0
	v_pk_mul_f32 v[36:37], v[36:37], v[70:71]
	s_nop 0
	v_cvt_pk_fp8_f32 v29, v24, v25
	v_cvt_pk_fp8_f32 v30, v20, v21
	v_cvt_pk_fp8_f32 v12, v14, v15 op_sel:[0,0,1]
	v_pk_mul_f32 v[8:9], v[8:9], v[68:69]
	s_nop 0
	v_pk_mul_f32 v[4:5], v[4:5], v[70:71]
	s_nop 0
	v_pk_mul_f32 v[0:1], v[0:1], v[68:69]
	s_nop 0
	v_cvt_pk_fp8_f32 v45, v40, v41
	v_cvt_pk_fp8_f32 v46, v36, v37
	v_cvt_pk_fp8_f32 v13, v8, v9
	v_cvt_pk_fp8_f32 v14, v4, v5
	v_cvt_pk_fp8_f32 v15, v0, v1
	v_pk_mul_f32 v[74:75], v[202:203], s[54:55] op_sel_hi:[1,0]
	v_pk_mul_f32 v[54:55], v[54:55], v[72:73]
	v_pk_mul_f32 v[58:59], v[58:59], v[74:75]
	v_pk_mul_f32 v[50:51], v[50:51], v[74:75]
	v_pk_mul_f32 v[26:27], v[26:27], v[74:75]
	v_pk_mul_f32 v[22:23], v[22:23], v[72:73]
	v_pk_mul_f32 v[18:19], v[18:19], v[74:75]
	v_cvt_pk_fp8_f32 v61, v58, v59 op_sel:[0,0,1]
	v_cvt_pk_fp8_f32 v62, v54, v55 op_sel:[0,0,1]
	v_cvt_pk_fp8_f32 v63, v50, v51 op_sel:[0,0,1]
	v_pk_mul_f32 v[42:43], v[42:43], v[74:75]
	v_pk_mul_f32 v[38:39], v[38:39], v[72:73]
	v_pk_mul_f32 v[34:35], v[34:35], v[74:75]
	v_cvt_pk_fp8_f32 v29, v26, v27 op_sel:[0,0,1]
	v_cvt_pk_fp8_f32 v30, v22, v23 op_sel:[0,0,1]
	v_cvt_pk_fp8_f32 v31, v18, v19 op_sel:[0,0,1]
	v_pk_mul_f32 v[10:11], v[10:11], v[74:75]
	v_pk_mul_f32 v[6:7], v[6:7], v[72:73]
	v_pk_mul_f32 v[2:3], v[2:3], v[74:75]
	v_cvt_pk_fp8_f32 v45, v42, v43 op_sel:[0,0,1]
	v_cvt_pk_fp8_f32 v46, v38, v39 op_sel:[0,0,1]
	v_cvt_pk_fp8_f32 v47, v34, v35 op_sel:[0,0,1]
	v_cvt_pk_fp8_f32 v13, v10, v11 op_sel:[0,0,1]
	v_cvt_pk_fp8_f32 v14, v6, v7 op_sel:[0,0,1]
	v_cvt_pk_fp8_f32 v15, v2, v3 op_sel:[0,0,1]
	v_permlane32_swap_b32_e32 v60, v62
	v_permlane32_swap_b32_e32 v61, v63
	v_permlane32_swap_b32_e32 v28, v30
	v_permlane32_swap_b32_e32 v29, v31
	v_permlane16_swap_b32_e32 v60, v61
	v_permlane16_swap_b32_e32 v62, v63
	v_permlane32_swap_b32_e32 v44, v46
	v_permlane32_swap_b32_e32 v45, v47
	v_permlane16_swap_b32_e32 v28, v29
	v_permlane16_swap_b32_e32 v30, v31
	v_permlane32_swap_b32_e32 v12, v14
	v_permlane32_swap_b32_e32 v13, v15
	v_permlane16_swap_b32_e32 v44, v45
	v_permlane16_swap_b32_e32 v46, v47
	global_store_dwordx4 v[128:129], v[60:63], off offset:128
	global_store_dwordx4 v[96:97], v[44:47], off offset:128
	v_permlane16_swap_b32_e32 v12, v13
	v_permlane16_swap_b32_e32 v14, v15
	global_store_dwordx4 v[64:65], v[28:31], off offset:128
	global_store_dwordx4 v[66:67], v[12:15], off offset:128
	s_cbranch_vccz .LBB0_1496
	v_readlane_b32 s0, v252, 18
	s_waitcnt vmcnt(0)
	v_readlane_b32 s1, v252, 19
	s_andn2_b64 vcc, exec, s[0:1]
	s_cbranch_vccnz .LBB0_1227
	s_barrier
	s_branch .LBB0_1227

.LBB0_1580:
	v_cvt_pk_f32_fp8_e32 v[62:63], v38
	v_cvt_pk_f32_fp8_sdwa v[38:39], v38 src0_sel:WORD_1
	v_lshlrev_b32_e32 v60, 16, v42
	v_and_b32_e32 v61, 0xffff0000, v42
	v_lshlrev_b32_e32 v42, 16, v43
	v_and_b32_e32 v43, 0xffff0000, v43
	v_pk_add_f32 v[74:75], v[38:39], v[42:43]
	v_cvt_pk_f32_fp8_e32 v[42:43], v56
	v_lshlrev_b32_e32 v38, 16, v34
	v_and_b32_e32 v39, 0xffff0000, v34
	v_cvt_pk_f32_fp8_sdwa v[56:57], v56 src0_sel:WORD_1
	v_pk_add_f32 v[72:73], v[42:43], v[38:39]
	v_cvt_pk_f32_fp8_e32 v[38:39], v55
	v_lshlrev_b32_e32 v34, 16, v35
	v_and_b32_e32 v35, 0xffff0000, v35
	v_pk_add_f32 v[70:71], v[56:57], v[34:35]
	v_lshlrev_b32_e32 v34, 16, v10
	v_and_b32_e32 v35, 0xffff0000, v10
	v_cvt_pk_f32_fp8_sdwa v[42:43], v55 src0_sel:WORD_1
	v_pk_add_f32 v[68:69], v[38:39], v[34:35]
	v_cvt_pk_f32_fp8_e32 v[38:39], v54
	v_lshlrev_b32_e32 v10, 16, v11
	v_and_b32_e32 v11, 0xffff0000, v11
	v_pk_add_f32 v[66:67], v[42:43], v[10:11]
	v_lshlrev_b32_e32 v10, 16, v8
	v_and_b32_e32 v11, 0xffff0000, v8
	v_cvt_pk_f32_fp8_sdwa v[34:35], v54 src0_sel:WORD_1
	v_pk_add_f32 v[64:65], v[38:39], v[10:11]
	v_cvt_pk_f32_fp8_e32 v[10:11], v51
	v_lshlrev_b32_e32 v8, 16, v9
	v_and_b32_e32 v9, 0xffff0000, v9
	v_pk_add_f32 v[34:35], v[34:35], v[8:9]
	v_lshlrev_b32_e32 v8, 16, v6
	v_and_b32_e32 v9, 0xffff0000, v6
	v_cvt_pk_f32_fp8_sdwa v[38:39], v51 src0_sel:WORD_1
	v_pk_add_f32 v[76:77], v[62:63], v[60:61]
	v_pk_add_f32 v[62:63], v[10:11], v[8:9]
	v_cvt_pk_f32_fp8_e32 v[8:9], v47
	v_lshlrev_b32_e32 v6, 16, v7
	v_and_b32_e32 v7, 0xffff0000, v7
	v_pk_add_f32 v[38:39], v[38:39], v[6:7]
	v_lshlrev_b32_e32 v6, 16, v4
	v_and_b32_e32 v7, 0xffff0000, v4
	v_cvt_pk_f32_fp8_sdwa v[10:11], v47 src0_sel:WORD_1
	v_pk_add_f32 v[60:61], v[8:9], v[6:7]
	v_cvt_pk_f32_fp8_e32 v[6:7], v46
	v_lshlrev_b32_e32 v4, 16, v5
	v_and_b32_e32 v5, 0xffff0000, v5
	v_pk_add_f32 v[42:43], v[10:11], v[4:5]
	v_lshlrev_b32_e32 v4, 16, v2
	v_and_b32_e32 v5, 0xffff0000, v2
	v_cvt_pk_f32_fp8_sdwa v[8:9], v46 src0_sel:WORD_1
	v_pk_add_f32 v[56:57], v[6:7], v[4:5]
	v_cvt_pk_f32_fp8_sdwa v[6:7], v50 src0_sel:WORD_1
	v_lshlrev_b32_e32 v2, 16, v3
	v_and_b32_e32 v3, 0xffff0000, v3
	v_pk_add_f32 v[46:47], v[8:9], v[2:3]
	v_lshlrev_b32_e32 v2, 16, v0
	v_and_b32_e32 v3, 0xffff0000, v0
	v_lshlrev_b32_e32 v0, 16, v1
	v_and_b32_e32 v1, 0xffff0000, v1
	v_cvt_pk_f32_fp8_e32 v[4:5], v50
	v_pk_add_f32 v[50:51], v[6:7], v[0:1]
	v_mul_f32_e32 v0, v77, v77
	v_mul_f32_e32 v1, v73, v73
	v_fmac_f32_e32 v0, v76, v76
	v_fmac_f32_e32 v1, v72, v72
	v_fmac_f32_e32 v0, v74, v74
	v_fmac_f32_e32 v1, v70, v70
	v_pk_add_f32 v[54:55], v[4:5], v[2:3]
	v_fmac_f32_e32 v0, v75, v75
	v_fmac_f32_e32 v1, v71, v71
	v_mov_b32_e32 v2, v69
	v_mov_b32_e32 v3, v65
	v_add_f32_e32 v8, v0, v1
	v_mov_b32_e32 v0, v68
	v_mov_b32_e32 v1, v64
	v_pk_mul_f32 v[2:3], v[2:3], v[2:3]
	v_mov_b32_e32 v4, v66
	v_mov_b32_e32 v5, v34
	v_pk_fma_f32 v[0:1], v[0:1], v[0:1], v[2:3]
	v_mov_b32_e32 v6, v67
	v_mov_b32_e32 v7, v35
	v_pk_fma_f32 v[0:1], v[4:5], v[4:5], v[0:1]
	v_mov_b32_e32 v2, v63
	v_pk_fma_f32 v[0:1], v[6:7], v[6:7], v[0:1]
	v_mov_b32_e32 v3, v61
	v_add_f32_e32 v0, v8, v0
	v_add_f32_e32 v8, v0, v1
	v_mov_b32_e32 v0, v62
	v_mov_b32_e32 v1, v60
	v_pk_mul_f32 v[2:3], v[2:3], v[2:3]
	v_mov_b32_e32 v4, v38
	v_mov_b32_e32 v5, v42
	v_pk_fma_f32 v[0:1], v[0:1], v[0:1], v[2:3]
	v_mov_b32_e32 v6, v39
	v_mov_b32_e32 v7, v43
	v_pk_fma_f32 v[0:1], v[4:5], v[4:5], v[0:1]
	v_mov_b32_e32 v2, v57
	v_pk_fma_f32 v[0:1], v[6:7], v[6:7], v[0:1]
	v_mov_b32_e32 v3, v55
	v_add_f32_e32 v0, v8, v0
	v_add_f32_e32 v8, v0, v1
	v_mov_b32_e32 v0, v56
	v_mov_b32_e32 v1, v54
	v_pk_mul_f32 v[2:3], v[2:3], v[2:3]
	v_mov_b32_e32 v4, v46
	v_mov_b32_e32 v5, v50
	v_pk_fma_f32 v[0:1], v[0:1], v[0:1], v[2:3]
	v_mov_b32_e32 v6, v47
	v_mov_b32_e32 v7, v51
	v_pk_fma_f32 v[0:1], v[4:5], v[4:5], v[0:1]
	s_ashr_i32 s0, s6, 12
	v_pk_fma_f32 v[0:1], v[6:7], v[6:7], v[0:1]
	s_nop 0
	v_add_f32_e32 v0, v8, v0
	v_add_f32_e32 v0, v0, v1
	s_nop 1
	v_add_f32_dpp v0, v0, v0 quad_perm:[1,0,3,2] row_mask:0xf bank_mask:0xf bound_ctrl:1
	s_nop 1
	v_add_f32_dpp v0, v0, v0 quad_perm:[2,3,0,1] row_mask:0xf bank_mask:0xf bound_ctrl:1
	s_nop 1
	v_add_f32_dpp v0, v0, v0 row_half_mirror row_mask:0xf bank_mask:0xf bound_ctrl:1
	s_nop 1
	v_add_f32_dpp v0, v0, v0 row_mirror row_mask:0xf bank_mask:0xf bound_ctrl:1
	s_nop 0
	v_readlane_b32 s1, v0, 16
	v_readlane_b32 s6, v0, 48
	v_readlane_b32 s4, v0, 0
	v_readlane_b32 s5, v0, 32
	v_mov_b32_e32 v0, s1
	v_mov_b32_e32 v1, s6
	v_pk_add_f32 v[0:1], s[4:5], v[0:1]
	s_mov_b32 s1, 0xf800000
	v_add_f32_e32 v0, v0, v1
	v_fmamk_f32 v0, v0, 0x3a000000, v81
	v_cmp_gt_f32_e32 vcc, s1, v0
	v_mul_f32_e32 v1, 0x4f800000, v0
	s_mul_hi_i32 s1, s0, 0xc000
	v_cndmask_b32_e32 v0, v0, v1, vcc
	v_sqrt_f32_e32 v1, v0
	s_mul_i32 s0, s0, 0xc000
	s_add_u32 s0, s2, s0
	s_addc_u32 s1, s3, s1
	v_add_u32_e32 v2, -1, v1
	v_fma_f32 v3, -v2, v1, v0
	v_cmp_ge_f32_e64 s[6:7], 0, v3
	v_add_u32_e32 v3, 1, v1
	s_nop 0
	v_cndmask_b32_e64 v2, v1, v2, s[6:7]
	v_fma_f32 v1, -v3, v1, v0
	v_cmp_lt_f32_e64 s[6:7], 0, v1
	s_nop 1
	v_cndmask_b32_e64 v1, v2, v3, s[6:7]
	v_mul_f32_e32 v2, 0x37800000, v1
	v_cndmask_b32_e32 v1, v1, v2, vcc
	v_cmp_class_f32_e32 vcc, v0, v82
	s_add_u32 s6, s0, 0xe000
	s_addc_u32 s7, s1, 0
	v_cndmask_b32_e32 v0, v1, v0, vcc
	v_div_scale_f32 v1, s[4:5], v0, v0, 1.0
	v_rcp_f32_e32 v2, v1
	s_add_u32 s8, s0, 0x10000
	s_addc_u32 s9, s1, 0
	v_fma_f32 v3, -v1, v2, 1.0
	v_fmac_f32_e32 v2, v3, v2
	v_div_scale_f32 v3, vcc, 1.0, v0, 1.0
	v_mul_f32_e32 v4, v3, v2
	v_fma_f32 v5, -v1, v4, v3
	v_fmac_f32_e32 v4, v5, v2
	v_fma_f32 v1, -v1, v4, v3
	v_div_fmas_f32 v1, v1, v2, v4
	v_lshlrev_b64 v[4:5], 2, v[14:15]
	v_div_fixup_f32 v58, v1, v0, 1.0
	v_lshl_add_u64 v[0:1], s[20:21], 0, v[4:5]
	global_load_dwordx4 v[8:11], v[0:1], off
	v_lshl_add_u64 v[0:1], s[8:9], 0, v[4:5]
	global_load_dwordx4 v[0:3], v[0:1], off
	v_lshl_add_u64 v[4:5], s[6:7], 0, v[4:5]
	global_load_dwordx4 v[4:7], v[4:5], off
	v_pk_mul_f32 v[74:75], v[74:75], v[58:59] op_sel_hi:[1,0]
	v_pk_mul_f32 v[76:77], v[76:77], v[58:59] op_sel_hi:[1,0]
	v_pk_mul_f32 v[66:67], v[66:67], v[58:59] op_sel_hi:[1,0]
	v_pk_mul_f32 v[68:69], v[68:69], v[58:59] op_sel_hi:[1,0]
	v_cmp_eq_u32_e32 vcc, 0, v80
	s_waitcnt vmcnt(2)
	v_pk_mul_f32 v[8:9], v[8:9], v[76:77]
	v_pk_mul_f32 v[10:11], v[10:11], v[74:75]
	s_waitcnt vmcnt(1)
	v_pk_add_f32 v[2:3], v[2:3], 1.0 op_sel_hi:[1,0]
	v_pk_add_f32 v[0:1], v[0:1], 1.0 op_sel_hi:[1,0]
	s_waitcnt vmcnt(0)
	v_pk_fma_f32 v[6:7], v[2:3], v[10:11], v[6:7]
	v_pk_fma_f32 v[10:11], v[0:1], v[8:9], v[4:5]
	s_nop 0
	v_cvt_pk_fp8_f32 v2, v10, v11
	v_lshl_add_u64 v[0:1], s[26:27], 0, v[14:15]
	v_lshlrev_b64 v[4:5], 2, v[12:13]
	v_lshl_add_u64 v[8:9], s[8:9], 0, v[4:5]
	v_cvt_pk_fp8_f32 v2, v6, v7 op_sel:[0,0,1]
	global_store_dword v[0:1], v2, off
	v_lshl_add_u64 v[0:1], s[20:21], 0, v[4:5]
	global_load_dwordx4 v[0:3], v[0:1], off
	v_lshl_add_u64 v[4:5], s[6:7], 0, v[4:5]
	global_load_dwordx4 v[74:77], v[8:9], off
	global_load_dwordx4 v[94:97], v[4:5], off
	v_pk_mul_f32 v[4:5], v[70:71], v[58:59] op_sel_hi:[1,0]
	v_pk_mul_f32 v[8:9], v[72:73], v[58:59] op_sel_hi:[1,0]
	v_lshlrev_b64 v[70:71], 2, v[32:33]
	s_waitcnt vmcnt(2)
	v_pk_mul_f32 v[0:1], v[0:1], v[8:9]
	v_pk_mul_f32 v[2:3], v[2:3], v[4:5]
	s_waitcnt vmcnt(1)
	v_pk_add_f32 v[4:5], v[76:77], 1.0 op_sel_hi:[1,0]
	v_pk_add_f32 v[8:9], v[74:75], 1.0 op_sel_hi:[1,0]
	s_waitcnt vmcnt(0)
	v_pk_fma_f32 v[4:5], v[4:5], v[2:3], v[96:97]
	v_pk_fma_f32 v[8:9], v[8:9], v[0:1], v[94:95]
	s_nop 0
	v_cvt_pk_fp8_f32 v2, v8, v9
	v_lshl_add_u64 v[0:1], s[26:27], 0, v[12:13]
	v_lshl_add_u64 v[12:13], s[8:9], 0, v[70:71]
	v_cvt_pk_fp8_f32 v2, v4, v5 op_sel:[0,0,1]
	global_store_dword v[0:1], v2, off
	v_lshl_add_u64 v[0:1], s[20:21], 0, v[70:71]
	global_load_dwordx4 v[0:3], v[0:1], off
	v_lshl_add_u64 v[70:71], s[6:7], 0, v[70:71]
	global_load_dwordx4 v[12:15], v[12:13], off
	s_waitcnt vmcnt(1)
	v_pk_mul_f32 v[0:1], v[68:69], v[0:1]
	global_load_dwordx4 v[70:73], v[70:71], off
	v_pk_mul_f32 v[2:3], v[66:67], v[2:3]
	s_waitcnt vmcnt(1)
	v_pk_add_f32 v[14:15], v[14:15], 1.0 op_sel_hi:[1,0]
	v_pk_add_f32 v[66:67], v[12:13], 1.0 op_sel_hi:[1,0]
	s_waitcnt vmcnt(0)
	v_pk_fma_f32 v[12:13], v[2:3], v[14:15], v[72:73]
	v_pk_fma_f32 v[14:15], v[0:1], v[66:67], v[70:71]
	s_nop 0
	v_cvt_pk_fp8_f32 v2, v14, v15
	v_lshl_add_u64 v[0:1], s[26:27], 0, v[32:33]
	v_lshlrev_b64 v[32:33], 2, v[36:37]
	v_lshl_add_u64 v[66:67], s[8:9], 0, v[32:33]
	v_cvt_pk_fp8_f32 v2, v12, v13 op_sel:[0,0,1]
	global_store_dword v[0:1], v2, off
	v_lshl_add_u64 v[0:1], s[20:21], 0, v[32:33]
	global_load_dwordx4 v[0:3], v[0:1], off
	v_lshl_add_u64 v[32:33], s[6:7], 0, v[32:33]
	global_load_dwordx4 v[66:69], v[66:67], off
	s_nop 0
	global_load_dwordx4 v[70:73], v[32:33], off
	v_pk_mul_f32 v[32:33], v[34:35], v[58:59] op_sel_hi:[1,0]
	v_pk_mul_f32 v[34:35], v[64:65], v[58:59] op_sel_hi:[1,0]
	s_waitcnt vmcnt(2)
	v_pk_mul_f32 v[2:3], v[32:33], v[2:3]
	v_pk_mul_f32 v[0:1], v[34:35], v[0:1]
	s_waitcnt vmcnt(1)
	v_pk_add_f32 v[32:33], v[68:69], 1.0 op_sel_hi:[1,0]
	v_pk_add_f32 v[34:35], v[66:67], 1.0 op_sel_hi:[1,0]
	s_waitcnt vmcnt(0)
	v_pk_fma_f32 v[32:33], v[2:3], v[32:33], v[72:73]
	v_pk_fma_f32 v[34:35], v[0:1], v[34:35], v[70:71]
	s_nop 0
	v_cvt_pk_fp8_f32 v2, v34, v35
	v_lshl_add_u64 v[0:1], s[26:27], 0, v[36:37]
	v_lshlrev_b64 v[36:37], 2, v[40:41]
	v_lshl_add_u64 v[64:65], s[8:9], 0, v[36:37]
	v_cvt_pk_fp8_f32 v2, v32, v33 op_sel:[0,0,1]
	global_store_dword v[0:1], v2, off
	v_lshl_add_u64 v[0:1], s[20:21], 0, v[36:37]
	global_load_dwordx4 v[0:3], v[0:1], off
	v_lshl_add_u64 v[36:37], s[6:7], 0, v[36:37]
	global_load_dwordx4 v[64:67], v[64:65], off
	s_nop 0
	global_load_dwordx4 v[68:71], v[36:37], off
	v_pk_mul_f32 v[36:37], v[38:39], v[58:59] op_sel_hi:[1,0]
	v_pk_mul_f32 v[38:39], v[62:63], v[58:59] op_sel_hi:[1,0]
	s_waitcnt vmcnt(2)
	v_pk_mul_f32 v[2:3], v[36:37], v[2:3]
	v_pk_mul_f32 v[0:1], v[38:39], v[0:1]
	s_waitcnt vmcnt(1)
	v_pk_add_f32 v[36:37], v[66:67], 1.0 op_sel_hi:[1,0]
	v_pk_add_f32 v[38:39], v[64:65], 1.0 op_sel_hi:[1,0]
	s_waitcnt vmcnt(0)
	v_pk_fma_f32 v[36:37], v[2:3], v[36:37], v[70:71]
	v_pk_fma_f32 v[38:39], v[0:1], v[38:39], v[68:69]
	s_nop 0
	v_cvt_pk_fp8_f32 v2, v38, v39
	v_lshl_add_u64 v[0:1], s[26:27], 0, v[40:41]
	v_lshlrev_b64 v[40:41], 2, v[44:45]
	v_lshl_add_u64 v[62:63], s[8:9], 0, v[40:41]
	v_cvt_pk_fp8_f32 v2, v36, v37 op_sel:[0,0,1]
	global_store_dword v[0:1], v2, off
	v_lshl_add_u64 v[0:1], s[20:21], 0, v[40:41]
	global_load_dwordx4 v[0:3], v[0:1], off
	v_lshl_add_u64 v[40:41], s[6:7], 0, v[40:41]
	global_load_dwordx4 v[62:65], v[62:63], off
	s_nop 0
	global_load_dwordx4 v[66:69], v[40:41], off
	v_pk_mul_f32 v[40:41], v[42:43], v[58:59] op_sel_hi:[1,0]
	v_pk_mul_f32 v[42:43], v[60:61], v[58:59] op_sel_hi:[1,0]
	s_waitcnt vmcnt(2)
	v_pk_mul_f32 v[2:3], v[40:41], v[2:3]
	v_pk_mul_f32 v[0:1], v[42:43], v[0:1]
	s_waitcnt vmcnt(1)
	v_pk_add_f32 v[40:41], v[64:65], 1.0 op_sel_hi:[1,0]
	v_pk_add_f32 v[42:43], v[62:63], 1.0 op_sel_hi:[1,0]
	s_waitcnt vmcnt(0)
	v_pk_fma_f32 v[40:41], v[2:3], v[40:41], v[68:69]
	v_pk_fma_f32 v[42:43], v[0:1], v[42:43], v[66:67]
	s_nop 0
	v_cvt_pk_fp8_f32 v2, v42, v43
	v_lshl_add_u64 v[0:1], s[26:27], 0, v[44:45]
	v_lshlrev_b64 v[44:45], 2, v[48:49]
	v_lshl_add_u64 v[60:61], s[8:9], 0, v[44:45]
	v_cvt_pk_fp8_f32 v2, v40, v41 op_sel:[0,0,1]
	global_store_dword v[0:1], v2, off
	v_lshl_add_u64 v[0:1], s[20:21], 0, v[44:45]
	global_load_dwordx4 v[0:3], v[0:1], off
	v_lshl_add_u64 v[44:45], s[6:7], 0, v[44:45]
	global_load_dwordx4 v[60:63], v[60:61], off
	s_nop 0
	global_load_dwordx4 v[64:67], v[44:45], off
	v_pk_mul_f32 v[44:45], v[46:47], v[58:59] op_sel_hi:[1,0]
	v_pk_mul_f32 v[46:47], v[56:57], v[58:59] op_sel_hi:[1,0]
	s_waitcnt vmcnt(2)
	v_pk_mul_f32 v[2:3], v[44:45], v[2:3]
	v_pk_mul_f32 v[0:1], v[46:47], v[0:1]
	s_waitcnt vmcnt(1)
	v_pk_add_f32 v[44:45], v[62:63], 1.0 op_sel_hi:[1,0]
	v_pk_add_f32 v[46:47], v[60:61], 1.0 op_sel_hi:[1,0]
	s_waitcnt vmcnt(0)
	v_pk_fma_f32 v[44:45], v[2:3], v[44:45], v[66:67]
	v_pk_fma_f32 v[46:47], v[0:1], v[46:47], v[64:65]
	s_nop 0
	v_cvt_pk_fp8_f32 v2, v46, v47
	v_lshl_add_u64 v[0:1], s[26:27], 0, v[48:49]
	v_lshlrev_b64 v[48:49], 2, v[52:53]
	v_lshl_add_u64 v[56:57], s[8:9], 0, v[48:49]
	v_cvt_pk_fp8_f32 v2, v44, v45 op_sel:[0,0,1]
	global_store_dword v[0:1], v2, off
	v_lshl_add_u64 v[0:1], s[20:21], 0, v[48:49]
	global_load_dwordx4 v[0:3], v[0:1], off
	v_lshl_add_u64 v[48:49], s[6:7], 0, v[48:49]
	global_load_dwordx4 v[60:63], v[56:57], off
	global_load_dwordx4 v[64:67], v[48:49], off
	v_pk_mul_f32 v[48:49], v[50:51], v[58:59] op_sel_hi:[1,0]
	v_pk_mul_f32 v[50:51], v[54:55], v[58:59] op_sel_hi:[1,0]
	s_waitcnt vmcnt(2)
	v_pk_mul_f32 v[2:3], v[48:49], v[2:3]
	v_pk_mul_f32 v[0:1], v[50:51], v[0:1]
	s_waitcnt vmcnt(1)
	v_pk_add_f32 v[48:49], v[62:63], 1.0 op_sel_hi:[1,0]
	v_pk_add_f32 v[50:51], v[60:61], 1.0 op_sel_hi:[1,0]
	s_waitcnt vmcnt(0)
	v_pk_fma_f32 v[48:49], v[2:3], v[48:49], v[66:67]
	v_pk_fma_f32 v[50:51], v[0:1], v[50:51], v[64:65]
	s_nop 0
	v_cvt_pk_fp8_f32 v2, v50, v51
	v_lshl_add_u64 v[0:1], s[26:27], 0, v[52:53]
	v_lshlrev_b32_e32 v52, 4, v80
	v_cvt_pk_fp8_f32 v2, v48, v49 op_sel:[0,0,1]
	global_store_dword v[0:1], v2, off
	v_mov_b32_e32 v0, v52
	s_nop 0
	v_add_u32_e32 v53, 0, v0
	ds_read_b128 v[0:3], v53
	s_waitcnt lgkmcnt(0)
	v_mul_f32_e32 v1, v11, v1
	v_fmac_f32_e32 v1, v10, v0
	v_fmac_f32_e32 v1, v6, v2
	v_fmac_f32_e32 v1, v7, v3
	v_add_f32_e32 v54, 0, v1
	ds_read_b128 v[0:3], v53 offset:1024
	s_waitcnt lgkmcnt(0)
	v_mul_f32_e32 v1, v9, v1
	v_fmac_f32_e32 v1, v8, v0
	v_fmac_f32_e32 v1, v4, v2
	v_fmac_f32_e32 v1, v5, v3
	v_add_f32_e32 v54, v54, v1
	ds_read_b128 v[0:3], v53 offset:2048
	s_waitcnt lgkmcnt(0)
	v_mul_f32_e32 v1, v15, v1
	v_fmac_f32_e32 v1, v14, v0
	v_fmac_f32_e32 v1, v12, v2
	v_fmac_f32_e32 v1, v13, v3
	v_add_f32_e32 v54, v54, v1
	ds_read_b128 v[0:3], v53 offset:3072
	s_waitcnt lgkmcnt(0)
	v_mul_f32_e32 v1, v35, v1
	v_fmac_f32_e32 v1, v34, v0
	v_fmac_f32_e32 v1, v32, v2
	v_fmac_f32_e32 v1, v33, v3
	v_add_f32_e32 v54, v54, v1
	ds_read_b128 v[0:3], v53 offset:4096
	s_waitcnt lgkmcnt(0)
	v_mul_f32_e32 v1, v39, v1
	v_fmac_f32_e32 v1, v38, v0
	v_fmac_f32_e32 v1, v36, v2
	v_fmac_f32_e32 v1, v37, v3
	v_add_f32_e32 v54, v54, v1
	ds_read_b128 v[0:3], v53 offset:5120
	s_waitcnt lgkmcnt(0)
	v_mul_f32_e32 v1, v43, v1
	v_fmac_f32_e32 v1, v42, v0
	v_fmac_f32_e32 v1, v40, v2
	v_fmac_f32_e32 v1, v41, v3
	v_add_f32_e32 v54, v54, v1
	ds_read_b128 v[0:3], v53 offset:6144
	s_waitcnt lgkmcnt(0)
	v_mul_f32_e32 v1, v47, v1
	v_fmac_f32_e32 v1, v46, v0
	v_fmac_f32_e32 v1, v44, v2
	v_fmac_f32_e32 v1, v45, v3
	v_add_f32_e32 v54, v54, v1
	ds_read_b128 v[0:3], v53 offset:7168
	s_waitcnt lgkmcnt(0)
	v_mul_f32_e32 v1, v51, v1
	v_fmac_f32_e32 v1, v50, v0
	v_fmac_f32_e32 v1, v48, v2
	v_fmac_f32_e32 v1, v49, v3
	v_add_f32_e32 v0, v54, v1
	s_nop 1
	v_add_f32_dpp v0, v0, v0 quad_perm:[1,0,3,2] row_mask:0xf bank_mask:0xf bound_ctrl:1
	s_nop 1
	v_add_f32_dpp v0, v0, v0 quad_perm:[2,3,0,1] row_mask:0xf bank_mask:0xf bound_ctrl:1
	s_nop 1
	v_add_f32_dpp v0, v0, v0 row_half_mirror row_mask:0xf bank_mask:0xf bound_ctrl:1
	s_nop 1
	v_add_f32_dpp v0, v0, v0 row_mirror row_mask:0xf bank_mask:0xf bound_ctrl:1
	s_nop 0
	v_readlane_b32 s6, v0, 0
	v_readlane_b32 s10, v0, 16
	v_readlane_b32 s7, v0, 32
	v_readlane_b32 s11, v0, 48
	v_add_u32_e32 v0, 0x2000, v52
	s_nop 0
	v_add_u32_e32 v53, 0, v0
	ds_read_b128 v[0:3], v53
	s_waitcnt lgkmcnt(0)
	v_mul_f32_e32 v1, v11, v1
	v_fmac_f32_e32 v1, v10, v0
	v_fmac_f32_e32 v1, v6, v2
	v_fmac_f32_e32 v1, v7, v3
	v_add_f32_e32 v54, 0, v1
	ds_read_b128 v[0:3], v53 offset:1024
	s_waitcnt lgkmcnt(0)
	v_mul_f32_e32 v1, v9, v1
	v_fmac_f32_e32 v1, v8, v0
	v_fmac_f32_e32 v1, v4, v2
	v_fmac_f32_e32 v1, v5, v3
	v_add_f32_e32 v54, v54, v1
	ds_read_b128 v[0:3], v53 offset:2048
	s_waitcnt lgkmcnt(0)
	v_mul_f32_e32 v1, v15, v1
	v_fmac_f32_e32 v1, v14, v0
	v_fmac_f32_e32 v1, v12, v2
	v_fmac_f32_e32 v1, v13, v3
	v_add_f32_e32 v54, v54, v1
	ds_read_b128 v[0:3], v53 offset:3072
	s_waitcnt lgkmcnt(0)
	v_mul_f32_e32 v1, v35, v1
	v_fmac_f32_e32 v1, v34, v0
	v_fmac_f32_e32 v1, v32, v2
	v_fmac_f32_e32 v1, v33, v3
	v_add_f32_e32 v54, v54, v1
	ds_read_b128 v[0:3], v53 offset:4096
	s_waitcnt lgkmcnt(0)
	v_mul_f32_e32 v1, v39, v1
	v_fmac_f32_e32 v1, v38, v0
	v_fmac_f32_e32 v1, v36, v2
	v_fmac_f32_e32 v1, v37, v3
	v_add_f32_e32 v54, v54, v1
	ds_read_b128 v[0:3], v53 offset:5120
	s_waitcnt lgkmcnt(0)
	v_mul_f32_e32 v1, v43, v1
	v_fmac_f32_e32 v1, v42, v0
	v_fmac_f32_e32 v1, v40, v2
	v_fmac_f32_e32 v1, v41, v3
	v_add_f32_e32 v54, v54, v1
	ds_read_b128 v[0:3], v53 offset:6144
	s_waitcnt lgkmcnt(0)
	v_mul_f32_e32 v1, v47, v1
	v_fmac_f32_e32 v1, v46, v0
	v_fmac_f32_e32 v1, v44, v2
	v_fmac_f32_e32 v1, v45, v3
	v_add_f32_e32 v54, v54, v1
	ds_read_b128 v[0:3], v53 offset:7168
	s_waitcnt lgkmcnt(0)
	v_mul_f32_e32 v1, v51, v1
	v_fmac_f32_e32 v1, v50, v0
	v_fmac_f32_e32 v1, v48, v2
	v_fmac_f32_e32 v1, v49, v3
	v_add_f32_e32 v0, v54, v1
	s_nop 1
	v_add_f32_dpp v0, v0, v0 quad_perm:[1,0,3,2] row_mask:0xf bank_mask:0xf bound_ctrl:1
	s_nop 1
	v_add_f32_dpp v0, v0, v0 quad_perm:[2,3,0,1] row_mask:0xf bank_mask:0xf bound_ctrl:1
	s_nop 1
	v_add_f32_dpp v0, v0, v0 row_half_mirror row_mask:0xf bank_mask:0xf bound_ctrl:1
	s_nop 1
	v_add_f32_dpp v0, v0, v0 row_mirror row_mask:0xf bank_mask:0xf bound_ctrl:1
	s_nop 0
	v_readlane_b32 s8, v0, 0
	v_readlane_b32 s25, v0, 16
	v_readlane_b32 s9, v0, 32
	v_readlane_b32 s31, v0, 48
	v_add_u32_e32 v0, 0x4000, v52
	s_nop 0
	v_add_u32_e32 v53, 0, v0
	ds_read_b128 v[0:3], v53
	s_waitcnt lgkmcnt(0)
	v_mul_f32_e32 v1, v11, v1
	v_fmac_f32_e32 v1, v10, v0
	v_fmac_f32_e32 v1, v6, v2
	v_fmac_f32_e32 v1, v7, v3
	v_add_f32_e32 v54, 0, v1
	ds_read_b128 v[0:3], v53 offset:1024
	s_waitcnt lgkmcnt(0)
	v_mul_f32_e32 v1, v9, v1
	v_fmac_f32_e32 v1, v8, v0
	v_fmac_f32_e32 v1, v4, v2
	v_fmac_f32_e32 v1, v5, v3
	v_add_f32_e32 v54, v54, v1
	ds_read_b128 v[0:3], v53 offset:2048
	s_waitcnt lgkmcnt(0)
	v_mul_f32_e32 v1, v15, v1
	v_fmac_f32_e32 v1, v14, v0
	v_fmac_f32_e32 v1, v12, v2
	v_fmac_f32_e32 v1, v13, v3
	v_add_f32_e32 v54, v54, v1
	ds_read_b128 v[0:3], v53 offset:3072
	s_waitcnt lgkmcnt(0)
	v_mul_f32_e32 v1, v35, v1
	v_fmac_f32_e32 v1, v34, v0
	v_fmac_f32_e32 v1, v32, v2
	v_fmac_f32_e32 v1, v33, v3
	v_add_f32_e32 v54, v54, v1
	ds_read_b128 v[0:3], v53 offset:4096
	s_waitcnt lgkmcnt(0)
	v_mul_f32_e32 v1, v39, v1
	v_fmac_f32_e32 v1, v38, v0
	v_fmac_f32_e32 v1, v36, v2
	v_fmac_f32_e32 v1, v37, v3
	v_add_f32_e32 v54, v54, v1
	ds_read_b128 v[0:3], v53 offset:5120
	s_waitcnt lgkmcnt(0)
	v_mul_f32_e32 v1, v43, v1
	v_fmac_f32_e32 v1, v42, v0
	v_fmac_f32_e32 v1, v40, v2
	v_fmac_f32_e32 v1, v41, v3
	v_add_f32_e32 v54, v54, v1
	ds_read_b128 v[0:3], v53 offset:6144
	s_waitcnt lgkmcnt(0)
	v_mul_f32_e32 v1, v47, v1
	v_fmac_f32_e32 v1, v46, v0
	v_fmac_f32_e32 v1, v44, v2
	v_fmac_f32_e32 v1, v45, v3
	v_add_f32_e32 v54, v54, v1
	ds_read_b128 v[0:3], v53 offset:7168
	s_waitcnt lgkmcnt(0)
	v_mul_f32_e32 v1, v51, v1
	v_fmac_f32_e32 v1, v50, v0
	v_fmac_f32_e32 v1, v48, v2
	v_fmac_f32_e32 v1, v49, v3
	v_add_f32_e32 v0, v54, v1
	s_nop 1
	v_add_f32_dpp v0, v0, v0 quad_perm:[1,0,3,2] row_mask:0xf bank_mask:0xf bound_ctrl:1
	s_nop 1
	v_add_f32_dpp v0, v0, v0 quad_perm:[2,3,0,1] row_mask:0xf bank_mask:0xf bound_ctrl:1
	s_nop 1
	v_add_f32_dpp v0, v0, v0 row_half_mirror row_mask:0xf bank_mask:0xf bound_ctrl:1
	s_nop 1
	v_add_f32_dpp v0, v0, v0 row_mirror row_mask:0xf bank_mask:0xf bound_ctrl:1
	s_nop 0
	v_readlane_b32 s12, v0, 0
	v_readlane_b32 s14, v0, 16
	v_readlane_b32 s13, v0, 32
	v_readlane_b32 s15, v0, 48
	v_add_u32_e32 v0, 0x6000, v52
	s_nop 0
	v_add_u32_e32 v53, 0, v0
	ds_read_b128 v[0:3], v53
	s_waitcnt lgkmcnt(0)
	v_mul_f32_e32 v1, v11, v1
	v_fmac_f32_e32 v1, v10, v0
	v_fmac_f32_e32 v1, v6, v2
	v_fmac_f32_e32 v1, v7, v3
	v_add_f32_e32 v54, 0, v1
	ds_read_b128 v[0:3], v53 offset:1024
	s_waitcnt lgkmcnt(0)
	v_mul_f32_e32 v1, v9, v1
	v_fmac_f32_e32 v1, v8, v0
	v_fmac_f32_e32 v1, v4, v2
	v_fmac_f32_e32 v1, v5, v3
	v_add_f32_e32 v54, v54, v1
	ds_read_b128 v[0:3], v53 offset:2048
	s_waitcnt lgkmcnt(0)
	v_mul_f32_e32 v1, v15, v1
	v_fmac_f32_e32 v1, v14, v0
	v_fmac_f32_e32 v1, v12, v2
	v_fmac_f32_e32 v1, v13, v3
	v_add_f32_e32 v54, v54, v1
	ds_read_b128 v[0:3], v53 offset:3072
	s_waitcnt lgkmcnt(0)
	v_mul_f32_e32 v1, v35, v1
	v_fmac_f32_e32 v1, v34, v0
	v_fmac_f32_e32 v1, v32, v2
	v_fmac_f32_e32 v1, v33, v3
	v_add_f32_e32 v54, v54, v1
	ds_read_b128 v[0:3], v53 offset:4096
	s_waitcnt lgkmcnt(0)
	v_mul_f32_e32 v1, v39, v1
	v_fmac_f32_e32 v1, v38, v0
	v_fmac_f32_e32 v1, v36, v2
	v_fmac_f32_e32 v1, v37, v3
	v_add_f32_e32 v54, v54, v1
	ds_read_b128 v[0:3], v53 offset:5120
	s_waitcnt lgkmcnt(0)
	v_mul_f32_e32 v1, v43, v1
	v_fmac_f32_e32 v1, v42, v0
	v_fmac_f32_e32 v1, v40, v2
	v_fmac_f32_e32 v1, v41, v3
	v_add_f32_e32 v54, v54, v1
	ds_read_b128 v[0:3], v53 offset:6144
	s_waitcnt lgkmcnt(0)
	v_mul_f32_e32 v1, v47, v1
	v_fmac_f32_e32 v1, v46, v0
	v_fmac_f32_e32 v1, v44, v2
	v_fmac_f32_e32 v1, v45, v3
	v_add_f32_e32 v54, v54, v1
	ds_read_b128 v[0:3], v53 offset:7168
	s_waitcnt lgkmcnt(0)
	v_mul_f32_e32 v1, v51, v1
	v_fmac_f32_e32 v1, v50, v0
	v_fmac_f32_e32 v1, v48, v2
	v_fmac_f32_e32 v1, v49, v3
	v_add_f32_e32 v0, v54, v1
	s_nop 1
	v_add_f32_dpp v0, v0, v0 quad_perm:[1,0,3,2] row_mask:0xf bank_mask:0xf bound_ctrl:1
	s_nop 1
	v_add_f32_dpp v0, v0, v0 quad_perm:[2,3,0,1] row_mask:0xf bank_mask:0xf bound_ctrl:1
	s_nop 1
	v_add_f32_dpp v0, v0, v0 row_half_mirror row_mask:0xf bank_mask:0xf bound_ctrl:1
	s_nop 1
	v_add_f32_dpp v0, v0, v0 row_mirror row_mask:0xf bank_mask:0xf bound_ctrl:1
	s_nop 0
	v_readlane_b32 s53, v0, 0
	v_readlane_b32 s55, v0, 16
	v_readlane_b32 s54, v0, 32
	v_readlane_b32 s56, v0, 48
	v_add_u32_e32 v0, 0x8000, v52
	s_nop 0
	v_add_u32_e32 v53, 0, v0
	ds_read_b128 v[0:3], v53
	s_waitcnt lgkmcnt(0)
	v_mul_f32_e32 v1, v11, v1
	v_fmac_f32_e32 v1, v10, v0
	v_fmac_f32_e32 v1, v6, v2
	v_fmac_f32_e32 v1, v7, v3
	v_add_f32_e32 v54, 0, v1
	ds_read_b128 v[0:3], v53 offset:1024
	s_waitcnt lgkmcnt(0)
	v_mul_f32_e32 v1, v9, v1
	v_fmac_f32_e32 v1, v8, v0
	v_fmac_f32_e32 v1, v4, v2
	v_fmac_f32_e32 v1, v5, v3
	v_add_f32_e32 v54, v54, v1
	ds_read_b128 v[0:3], v53 offset:2048
	s_waitcnt lgkmcnt(0)
	v_mul_f32_e32 v1, v15, v1
	v_fmac_f32_e32 v1, v14, v0
	v_fmac_f32_e32 v1, v12, v2
	v_fmac_f32_e32 v1, v13, v3
	v_add_f32_e32 v54, v54, v1
	ds_read_b128 v[0:3], v53 offset:3072
	s_waitcnt lgkmcnt(0)
	v_mul_f32_e32 v1, v35, v1
	v_fmac_f32_e32 v1, v34, v0
	v_fmac_f32_e32 v1, v32, v2
	v_fmac_f32_e32 v1, v33, v3
	v_add_f32_e32 v54, v54, v1
	ds_read_b128 v[0:3], v53 offset:4096
	s_waitcnt lgkmcnt(0)
	v_mul_f32_e32 v1, v39, v1
	v_fmac_f32_e32 v1, v38, v0
	v_fmac_f32_e32 v1, v36, v2
	v_fmac_f32_e32 v1, v37, v3
	v_add_f32_e32 v54, v54, v1
	ds_read_b128 v[0:3], v53 offset:5120
	s_waitcnt lgkmcnt(0)
	v_mul_f32_e32 v1, v43, v1
	v_fmac_f32_e32 v1, v42, v0
	v_fmac_f32_e32 v1, v40, v2
	v_fmac_f32_e32 v1, v41, v3
	v_add_f32_e32 v54, v54, v1
	ds_read_b128 v[0:3], v53 offset:6144
	s_waitcnt lgkmcnt(0)
	v_mul_f32_e32 v1, v47, v1
	v_fmac_f32_e32 v1, v46, v0
	v_fmac_f32_e32 v1, v44, v2
	v_fmac_f32_e32 v1, v45, v3
	v_add_f32_e32 v54, v54, v1
	ds_read_b128 v[0:3], v53 offset:7168
	s_waitcnt lgkmcnt(0)
	v_mul_f32_e32 v1, v51, v1
	v_fmac_f32_e32 v1, v50, v0
	v_fmac_f32_e32 v1, v48, v2
	v_fmac_f32_e32 v1, v49, v3
	v_add_f32_e32 v0, v54, v1
	s_nop 1
	v_add_f32_dpp v0, v0, v0 quad_perm:[1,0,3,2] row_mask:0xf bank_mask:0xf bound_ctrl:1
	s_nop 1
	v_add_f32_dpp v0, v0, v0 quad_perm:[2,3,0,1] row_mask:0xf bank_mask:0xf bound_ctrl:1
	s_nop 1
	v_add_f32_dpp v0, v0, v0 row_half_mirror row_mask:0xf bank_mask:0xf bound_ctrl:1
	s_nop 1
	v_add_f32_dpp v0, v0, v0 row_mirror row_mask:0xf bank_mask:0xf bound_ctrl:1
	s_nop 0
	v_readlane_b32 s57, v0, 0
	v_readlane_b32 s59, v0, 16
	v_readlane_b32 s58, v0, 32
	v_readlane_b32 s60, v0, 48
	v_add_u32_e32 v0, 0xa000, v52
	s_nop 0
	v_add_u32_e32 v53, 0, v0
	ds_read_b128 v[0:3], v53
	s_waitcnt lgkmcnt(0)
	v_mul_f32_e32 v1, v11, v1
	v_fmac_f32_e32 v1, v10, v0
	v_fmac_f32_e32 v1, v6, v2
	v_fmac_f32_e32 v1, v7, v3
	v_add_f32_e32 v54, 0, v1
	ds_read_b128 v[0:3], v53 offset:1024
	s_waitcnt lgkmcnt(0)
	v_mul_f32_e32 v1, v9, v1
	v_fmac_f32_e32 v1, v8, v0
	v_fmac_f32_e32 v1, v4, v2
	v_fmac_f32_e32 v1, v5, v3
	v_add_f32_e32 v54, v54, v1
	ds_read_b128 v[0:3], v53 offset:2048
	s_waitcnt lgkmcnt(0)
	v_mul_f32_e32 v1, v15, v1
	v_fmac_f32_e32 v1, v14, v0
	v_fmac_f32_e32 v1, v12, v2
	v_fmac_f32_e32 v1, v13, v3
	v_add_f32_e32 v54, v54, v1
	ds_read_b128 v[0:3], v53 offset:3072
	s_waitcnt lgkmcnt(0)
	v_mul_f32_e32 v1, v35, v1
	v_fmac_f32_e32 v1, v34, v0
	v_fmac_f32_e32 v1, v32, v2
	v_fmac_f32_e32 v1, v33, v3
	v_add_f32_e32 v54, v54, v1
	ds_read_b128 v[0:3], v53 offset:4096
	s_waitcnt lgkmcnt(0)
	v_mul_f32_e32 v1, v39, v1
	v_fmac_f32_e32 v1, v38, v0
	v_fmac_f32_e32 v1, v36, v2
	v_fmac_f32_e32 v1, v37, v3
	v_add_f32_e32 v54, v54, v1
	ds_read_b128 v[0:3], v53 offset:5120
	s_waitcnt lgkmcnt(0)
	v_mul_f32_e32 v1, v43, v1
	v_fmac_f32_e32 v1, v42, v0
	v_fmac_f32_e32 v1, v40, v2
	v_fmac_f32_e32 v1, v41, v3
	v_add_f32_e32 v54, v54, v1
	ds_read_b128 v[0:3], v53 offset:6144
	s_waitcnt lgkmcnt(0)
	v_mul_f32_e32 v1, v47, v1
	v_fmac_f32_e32 v1, v46, v0
	v_fmac_f32_e32 v1, v44, v2
	v_fmac_f32_e32 v1, v45, v3
	v_add_f32_e32 v54, v54, v1
	ds_read_b128 v[0:3], v53 offset:7168
	s_waitcnt lgkmcnt(0)
	v_mul_f32_e32 v1, v51, v1
	v_fmac_f32_e32 v1, v50, v0
	v_fmac_f32_e32 v1, v48, v2
	v_fmac_f32_e32 v1, v49, v3
	v_add_f32_e32 v0, v54, v1
	s_nop 1
	v_add_f32_dpp v0, v0, v0 quad_perm:[1,0,3,2] row_mask:0xf bank_mask:0xf bound_ctrl:1
	s_nop 1
	v_add_f32_dpp v0, v0, v0 quad_perm:[2,3,0,1] row_mask:0xf bank_mask:0xf bound_ctrl:1
	s_nop 1
	v_add_f32_dpp v0, v0, v0 row_half_mirror row_mask:0xf bank_mask:0xf bound_ctrl:1
	s_nop 1
	v_add_f32_dpp v0, v0, v0 row_mirror row_mask:0xf bank_mask:0xf bound_ctrl:1
	s_nop 0
	v_readlane_b32 s0, v0, 0
	v_readlane_b32 s61, v0, 16
	v_readlane_b32 s1, v0, 32
	v_readlane_b32 s62, v0, 48
	v_add_u32_e32 v0, 0xc000, v52
	s_nop 0
	v_add_u32_e32 v53, 0, v0
	ds_read_b128 v[0:3], v53
	s_waitcnt lgkmcnt(0)
	v_mul_f32_e32 v1, v11, v1
	v_fmac_f32_e32 v1, v10, v0
	v_fmac_f32_e32 v1, v6, v2
	v_fmac_f32_e32 v1, v7, v3
	v_add_f32_e32 v54, 0, v1
	ds_read_b128 v[0:3], v53 offset:1024
	s_waitcnt lgkmcnt(0)
	v_mul_f32_e32 v1, v9, v1
	v_fmac_f32_e32 v1, v8, v0
	v_fmac_f32_e32 v1, v4, v2
	v_fmac_f32_e32 v1, v5, v3
	v_add_f32_e32 v54, v54, v1
	ds_read_b128 v[0:3], v53 offset:2048
	s_waitcnt lgkmcnt(0)
	v_mul_f32_e32 v1, v15, v1
	v_fmac_f32_e32 v1, v14, v0
	v_fmac_f32_e32 v1, v12, v2
	v_fmac_f32_e32 v1, v13, v3
	v_add_f32_e32 v54, v54, v1
	ds_read_b128 v[0:3], v53 offset:3072
	s_waitcnt lgkmcnt(0)
	v_mul_f32_e32 v1, v35, v1
	v_fmac_f32_e32 v1, v34, v0
	v_fmac_f32_e32 v1, v32, v2
	v_fmac_f32_e32 v1, v33, v3
	v_add_f32_e32 v54, v54, v1
	ds_read_b128 v[0:3], v53 offset:4096
	s_waitcnt lgkmcnt(0)
	v_mul_f32_e32 v1, v39, v1
	v_fmac_f32_e32 v1, v38, v0
	v_fmac_f32_e32 v1, v36, v2
	v_fmac_f32_e32 v1, v37, v3
	v_add_f32_e32 v54, v54, v1
	ds_read_b128 v[0:3], v53 offset:5120
	s_waitcnt lgkmcnt(0)
	v_mul_f32_e32 v1, v43, v1
	v_fmac_f32_e32 v1, v42, v0
	v_fmac_f32_e32 v1, v40, v2
	v_fmac_f32_e32 v1, v41, v3
	v_add_f32_e32 v54, v54, v1
	ds_read_b128 v[0:3], v53 offset:6144
	s_waitcnt lgkmcnt(0)
	v_mul_f32_e32 v1, v47, v1
	v_fmac_f32_e32 v1, v46, v0
	v_fmac_f32_e32 v1, v44, v2
	v_fmac_f32_e32 v1, v45, v3
	v_add_f32_e32 v54, v54, v1
	ds_read_b128 v[0:3], v53 offset:7168
	s_waitcnt lgkmcnt(0)
	v_mul_f32_e32 v1, v51, v1
	v_fmac_f32_e32 v1, v50, v0
	v_fmac_f32_e32 v1, v48, v2
	v_fmac_f32_e32 v1, v49, v3
	v_add_f32_e32 v0, v54, v1
	s_nop 1
	v_add_f32_dpp v0, v0, v0 quad_perm:[1,0,3,2] row_mask:0xf bank_mask:0xf bound_ctrl:1
	s_nop 1
	v_add_f32_dpp v0, v0, v0 quad_perm:[2,3,0,1] row_mask:0xf bank_mask:0xf bound_ctrl:1
	s_nop 1
	v_add_f32_dpp v0, v0, v0 row_half_mirror row_mask:0xf bank_mask:0xf bound_ctrl:1
	s_nop 1
	v_add_f32_dpp v0, v0, v0 row_mirror row_mask:0xf bank_mask:0xf bound_ctrl:1
	s_nop 0
	v_readlane_b32 s63, v0, 0
	v_readlane_b32 s65, v0, 16
	v_readlane_b32 s64, v0, 32
	v_readlane_b32 s66, v0, 48
	v_add_u32_e32 v0, 0xe000, v52
	s_nop 0
	v_add_u32_e32 v53, 0, v0
	ds_read_b128 v[0:3], v53
	s_waitcnt lgkmcnt(0)
	v_mul_f32_e32 v1, v11, v1
	v_fmac_f32_e32 v1, v10, v0
	v_fmac_f32_e32 v1, v6, v2
	v_fmac_f32_e32 v1, v7, v3
	v_add_f32_e32 v54, 0, v1
	ds_read_b128 v[0:3], v53 offset:1024
	s_waitcnt lgkmcnt(0)
	v_mul_f32_e32 v1, v9, v1
	v_fmac_f32_e32 v1, v8, v0
	v_fmac_f32_e32 v1, v4, v2
	v_fmac_f32_e32 v1, v5, v3
	v_add_f32_e32 v54, v54, v1
	ds_read_b128 v[0:3], v53 offset:2048
	s_waitcnt lgkmcnt(0)
	v_mul_f32_e32 v1, v15, v1
	v_fmac_f32_e32 v1, v14, v0
	v_fmac_f32_e32 v1, v12, v2
	v_fmac_f32_e32 v1, v13, v3
	v_add_f32_e32 v54, v54, v1
	ds_read_b128 v[0:3], v53 offset:3072
	s_waitcnt lgkmcnt(0)
	v_mul_f32_e32 v1, v35, v1
	v_fmac_f32_e32 v1, v34, v0
	v_fmac_f32_e32 v1, v32, v2
	v_fmac_f32_e32 v1, v33, v3
	v_add_f32_e32 v54, v54, v1
	ds_read_b128 v[0:3], v53 offset:4096
	s_waitcnt lgkmcnt(0)
	v_mul_f32_e32 v1, v39, v1
	v_fmac_f32_e32 v1, v38, v0
	v_fmac_f32_e32 v1, v36, v2
	v_fmac_f32_e32 v1, v37, v3
	v_add_f32_e32 v54, v54, v1
	ds_read_b128 v[0:3], v53 offset:5120
	s_waitcnt lgkmcnt(0)
	v_mul_f32_e32 v1, v43, v1
	v_fmac_f32_e32 v1, v42, v0
	v_fmac_f32_e32 v1, v40, v2
	v_fmac_f32_e32 v1, v41, v3
	v_add_f32_e32 v54, v54, v1
	ds_read_b128 v[0:3], v53 offset:6144
	s_waitcnt lgkmcnt(0)
	v_mul_f32_e32 v1, v47, v1
	v_fmac_f32_e32 v1, v46, v0
	v_fmac_f32_e32 v1, v44, v2
	v_fmac_f32_e32 v1, v45, v3
	v_add_f32_e32 v54, v54, v1
	ds_read_b128 v[0:3], v53 offset:7168
	s_waitcnt lgkmcnt(0)
	v_mul_f32_e32 v1, v51, v1
	v_fmac_f32_e32 v1, v50, v0
	v_fmac_f32_e32 v1, v48, v2
	v_fmac_f32_e32 v1, v49, v3
	v_add_f32_e32 v0, v54, v1
	s_nop 1
	v_add_f32_dpp v0, v0, v0 quad_perm:[1,0,3,2] row_mask:0xf bank_mask:0xf bound_ctrl:1
	s_nop 1
	v_add_f32_dpp v0, v0, v0 quad_perm:[2,3,0,1] row_mask:0xf bank_mask:0xf bound_ctrl:1
	s_nop 1
	v_add_f32_dpp v0, v0, v0 row_half_mirror row_mask:0xf bank_mask:0xf bound_ctrl:1
	s_nop 1
	v_add_f32_dpp v0, v0, v0 row_mirror row_mask:0xf bank_mask:0xf bound_ctrl:1
	s_nop 0
	v_readlane_b32 s67, v0, 0
	v_readlane_b32 s69, v0, 16
	v_readlane_b32 s68, v0, 32
	v_readlane_b32 s70, v0, 48
	v_add_u32_e32 v0, 0x10000, v52
	s_nop 0
	v_add_u32_e32 v53, 0, v0
	ds_read_b128 v[0:3], v53
	s_waitcnt lgkmcnt(0)
	v_mul_f32_e32 v1, v11, v1
	v_fmac_f32_e32 v1, v10, v0
	v_fmac_f32_e32 v1, v6, v2
	v_fmac_f32_e32 v1, v7, v3
	v_add_f32_e32 v54, 0, v1
	ds_read_b128 v[0:3], v53 offset:1024
	s_waitcnt lgkmcnt(0)
	v_mul_f32_e32 v1, v9, v1
	v_fmac_f32_e32 v1, v8, v0
	v_fmac_f32_e32 v1, v4, v2
	v_fmac_f32_e32 v1, v5, v3
	v_add_f32_e32 v54, v54, v1
	ds_read_b128 v[0:3], v53 offset:2048
	s_waitcnt lgkmcnt(0)
	v_mul_f32_e32 v1, v15, v1
	v_fmac_f32_e32 v1, v14, v0
	v_fmac_f32_e32 v1, v12, v2
	v_fmac_f32_e32 v1, v13, v3
	v_add_f32_e32 v54, v54, v1
	ds_read_b128 v[0:3], v53 offset:3072
	s_waitcnt lgkmcnt(0)
	v_mul_f32_e32 v1, v35, v1
	v_fmac_f32_e32 v1, v34, v0
	v_fmac_f32_e32 v1, v32, v2
	v_fmac_f32_e32 v1, v33, v3
	v_add_f32_e32 v54, v54, v1
	ds_read_b128 v[0:3], v53 offset:4096
	s_waitcnt lgkmcnt(0)
	v_mul_f32_e32 v1, v39, v1
	v_fmac_f32_e32 v1, v38, v0
	v_fmac_f32_e32 v1, v36, v2
	v_fmac_f32_e32 v1, v37, v3
	v_add_f32_e32 v54, v54, v1
	ds_read_b128 v[0:3], v53 offset:5120
	s_waitcnt lgkmcnt(0)
	v_mul_f32_e32 v1, v43, v1
	v_fmac_f32_e32 v1, v42, v0
	v_fmac_f32_e32 v1, v40, v2
	v_fmac_f32_e32 v1, v41, v3
	v_add_f32_e32 v54, v54, v1
	ds_read_b128 v[0:3], v53 offset:6144
	s_waitcnt lgkmcnt(0)
	v_mul_f32_e32 v1, v47, v1
	v_fmac_f32_e32 v1, v46, v0
	v_fmac_f32_e32 v1, v44, v2
	v_fmac_f32_e32 v1, v45, v3
	v_add_f32_e32 v54, v54, v1
	ds_read_b128 v[0:3], v53 offset:7168
	s_waitcnt lgkmcnt(0)
	v_mul_f32_e32 v1, v51, v1
	v_fmac_f32_e32 v1, v50, v0
	v_fmac_f32_e32 v1, v48, v2
	v_fmac_f32_e32 v1, v49, v3
	v_add_f32_e32 v0, v54, v1
	s_nop 1
	v_add_f32_dpp v0, v0, v0 quad_perm:[1,0,3,2] row_mask:0xf bank_mask:0xf bound_ctrl:1
	s_nop 1
	v_add_f32_dpp v0, v0, v0 quad_perm:[2,3,0,1] row_mask:0xf bank_mask:0xf bound_ctrl:1
	s_nop 1
	v_add_f32_dpp v0, v0, v0 row_half_mirror row_mask:0xf bank_mask:0xf bound_ctrl:1
	s_nop 1
	v_add_f32_dpp v0, v0, v0 row_mirror row_mask:0xf bank_mask:0xf bound_ctrl:1
	s_nop 0
	v_readlane_b32 s71, v0, 0
	v_readlane_b32 s73, v0, 16
	v_readlane_b32 s72, v0, 32
	v_readlane_b32 s74, v0, 48
	v_add_u32_e32 v0, 0x12000, v52
	s_nop 0
	v_add_u32_e32 v53, 0, v0
	ds_read_b128 v[0:3], v53
	s_waitcnt lgkmcnt(0)
	v_mul_f32_e32 v1, v11, v1
	v_fmac_f32_e32 v1, v10, v0
	v_fmac_f32_e32 v1, v6, v2
	v_fmac_f32_e32 v1, v7, v3
	v_add_f32_e32 v54, 0, v1
	ds_read_b128 v[0:3], v53 offset:1024
	s_waitcnt lgkmcnt(0)
	v_mul_f32_e32 v1, v9, v1
	v_fmac_f32_e32 v1, v8, v0
	v_fmac_f32_e32 v1, v4, v2
	v_fmac_f32_e32 v1, v5, v3
	v_add_f32_e32 v54, v54, v1
	ds_read_b128 v[0:3], v53 offset:2048
	s_waitcnt lgkmcnt(0)
	v_mul_f32_e32 v1, v15, v1
	v_fmac_f32_e32 v1, v14, v0
	v_fmac_f32_e32 v1, v12, v2
	v_fmac_f32_e32 v1, v13, v3
	v_add_f32_e32 v54, v54, v1
	ds_read_b128 v[0:3], v53 offset:3072
	s_waitcnt lgkmcnt(0)
	v_mul_f32_e32 v1, v35, v1
	v_fmac_f32_e32 v1, v34, v0
	v_fmac_f32_e32 v1, v32, v2
	v_fmac_f32_e32 v1, v33, v3
	v_add_f32_e32 v54, v54, v1
	ds_read_b128 v[0:3], v53 offset:4096
	s_waitcnt lgkmcnt(0)
	v_mul_f32_e32 v1, v39, v1
	v_fmac_f32_e32 v1, v38, v0
	v_fmac_f32_e32 v1, v36, v2
	v_fmac_f32_e32 v1, v37, v3
	v_add_f32_e32 v54, v54, v1
	ds_read_b128 v[0:3], v53 offset:5120
	s_waitcnt lgkmcnt(0)
	v_mul_f32_e32 v1, v43, v1
	v_fmac_f32_e32 v1, v42, v0
	v_fmac_f32_e32 v1, v40, v2
	v_fmac_f32_e32 v1, v41, v3
	v_add_f32_e32 v54, v54, v1
	ds_read_b128 v[0:3], v53 offset:6144
	s_waitcnt lgkmcnt(0)
	v_mul_f32_e32 v1, v47, v1
	v_fmac_f32_e32 v1, v46, v0
	v_fmac_f32_e32 v1, v44, v2
	v_fmac_f32_e32 v1, v45, v3
	v_add_f32_e32 v54, v54, v1
	ds_read_b128 v[0:3], v53 offset:7168
	s_waitcnt lgkmcnt(0)
	v_mul_f32_e32 v1, v51, v1
	v_fmac_f32_e32 v1, v50, v0
	v_fmac_f32_e32 v1, v48, v2
	v_fmac_f32_e32 v1, v49, v3
	v_add_f32_e32 v0, v54, v1
	s_nop 1
	v_add_f32_dpp v0, v0, v0 quad_perm:[1,0,3,2] row_mask:0xf bank_mask:0xf bound_ctrl:1
	s_nop 1
	v_add_f32_dpp v0, v0, v0 quad_perm:[2,3,0,1] row_mask:0xf bank_mask:0xf bound_ctrl:1
	s_nop 1
	v_add_f32_dpp v0, v0, v0 row_half_mirror row_mask:0xf bank_mask:0xf bound_ctrl:1
	s_nop 1
	v_add_f32_dpp v0, v0, v0 row_mirror row_mask:0xf bank_mask:0xf bound_ctrl:1
	s_nop 0
	v_readlane_b32 s77, v0, 0
	v_readlane_b32 s78, v0, 16
	v_readlane_b32 s75, v0, 32
	v_readlane_b32 s76, v0, 48
	v_add_u32_e32 v0, 0x14000, v52
	s_nop 0
	v_add_u32_e32 v53, 0, v0
	ds_read_b128 v[0:3], v53
	s_waitcnt lgkmcnt(0)
	v_mul_f32_e32 v1, v11, v1
	v_fmac_f32_e32 v1, v10, v0
	v_fmac_f32_e32 v1, v6, v2
	v_fmac_f32_e32 v1, v7, v3
	v_add_f32_e32 v54, 0, v1
	ds_read_b128 v[0:3], v53 offset:1024
	s_waitcnt lgkmcnt(0)
	v_mul_f32_e32 v1, v9, v1
	v_fmac_f32_e32 v1, v8, v0
	v_fmac_f32_e32 v1, v4, v2
	v_fmac_f32_e32 v1, v5, v3
	v_add_f32_e32 v54, v54, v1
	ds_read_b128 v[0:3], v53 offset:2048
	s_waitcnt lgkmcnt(0)
	v_mul_f32_e32 v1, v15, v1
	v_fmac_f32_e32 v1, v14, v0
	v_fmac_f32_e32 v1, v12, v2
	v_fmac_f32_e32 v1, v13, v3
	v_add_f32_e32 v54, v54, v1
	ds_read_b128 v[0:3], v53 offset:3072
	s_waitcnt lgkmcnt(0)
	v_mul_f32_e32 v1, v35, v1
	v_fmac_f32_e32 v1, v34, v0
	v_fmac_f32_e32 v1, v32, v2
	v_fmac_f32_e32 v1, v33, v3
	v_add_f32_e32 v54, v54, v1
	ds_read_b128 v[0:3], v53 offset:4096
	s_waitcnt lgkmcnt(0)
	v_mul_f32_e32 v1, v39, v1
	v_fmac_f32_e32 v1, v38, v0
	v_fmac_f32_e32 v1, v36, v2
	v_fmac_f32_e32 v1, v37, v3
	v_add_f32_e32 v54, v54, v1
	ds_read_b128 v[0:3], v53 offset:5120
	s_waitcnt lgkmcnt(0)
	v_mul_f32_e32 v1, v43, v1
	v_fmac_f32_e32 v1, v42, v0
	v_fmac_f32_e32 v1, v40, v2
	v_fmac_f32_e32 v1, v41, v3
	v_add_f32_e32 v54, v54, v1
	ds_read_b128 v[0:3], v53 offset:6144
	s_waitcnt lgkmcnt(0)
	v_mul_f32_e32 v1, v47, v1
	v_fmac_f32_e32 v1, v46, v0
	v_fmac_f32_e32 v1, v44, v2
	v_fmac_f32_e32 v1, v45, v3
	v_add_f32_e32 v54, v54, v1
	ds_read_b128 v[0:3], v53 offset:7168
	s_waitcnt lgkmcnt(0)
	v_mul_f32_e32 v1, v51, v1
	v_fmac_f32_e32 v1, v50, v0
	v_fmac_f32_e32 v1, v48, v2
	v_fmac_f32_e32 v1, v49, v3
	v_add_f32_e32 v0, v54, v1
	s_nop 1
	v_add_f32_dpp v0, v0, v0 quad_perm:[1,0,3,2] row_mask:0xf bank_mask:0xf bound_ctrl:1
	s_nop 1
	v_add_f32_dpp v0, v0, v0 quad_perm:[2,3,0,1] row_mask:0xf bank_mask:0xf bound_ctrl:1
	s_nop 1
	v_add_f32_dpp v0, v0, v0 row_half_mirror row_mask:0xf bank_mask:0xf bound_ctrl:1
	s_nop 1
	v_add_f32_dpp v0, v0, v0 row_mirror row_mask:0xf bank_mask:0xf bound_ctrl:1
	s_nop 0
	v_readlane_b32 s79, v0, 0
	v_readlane_b32 s81, v0, 16
	v_readlane_b32 s80, v0, 32
	v_readlane_b32 s82, v0, 48
	v_add_u32_e32 v0, 0x16000, v52
	s_nop 0
	v_add_u32_e32 v53, 0, v0
	ds_read_b128 v[0:3], v53
	s_waitcnt lgkmcnt(0)
	v_mul_f32_e32 v1, v11, v1
	v_fmac_f32_e32 v1, v10, v0
	v_fmac_f32_e32 v1, v6, v2
	v_fmac_f32_e32 v1, v7, v3
	v_add_f32_e32 v54, 0, v1
	ds_read_b128 v[0:3], v53 offset:1024
	s_waitcnt lgkmcnt(0)
	v_mul_f32_e32 v1, v9, v1
	v_fmac_f32_e32 v1, v8, v0
	v_fmac_f32_e32 v1, v4, v2
	v_fmac_f32_e32 v1, v5, v3
	v_add_f32_e32 v54, v54, v1
	ds_read_b128 v[0:3], v53 offset:2048
	s_waitcnt lgkmcnt(0)
	v_mul_f32_e32 v1, v15, v1
	v_fmac_f32_e32 v1, v14, v0
	v_fmac_f32_e32 v1, v12, v2
	v_fmac_f32_e32 v1, v13, v3
	v_add_f32_e32 v54, v54, v1
	ds_read_b128 v[0:3], v53 offset:3072
	s_waitcnt lgkmcnt(0)
	v_mul_f32_e32 v1, v35, v1
	v_fmac_f32_e32 v1, v34, v0
	v_fmac_f32_e32 v1, v32, v2
	v_fmac_f32_e32 v1, v33, v3
	v_add_f32_e32 v54, v54, v1
	ds_read_b128 v[0:3], v53 offset:4096
	s_waitcnt lgkmcnt(0)
	v_mul_f32_e32 v1, v39, v1
	v_fmac_f32_e32 v1, v38, v0
	v_fmac_f32_e32 v1, v36, v2
	v_fmac_f32_e32 v1, v37, v3
	v_add_f32_e32 v54, v54, v1
	ds_read_b128 v[0:3], v53 offset:5120
	s_waitcnt lgkmcnt(0)
	v_mul_f32_e32 v1, v43, v1
	v_fmac_f32_e32 v1, v42, v0
	v_fmac_f32_e32 v1, v40, v2
	v_fmac_f32_e32 v1, v41, v3
	v_add_f32_e32 v54, v54, v1
	ds_read_b128 v[0:3], v53 offset:6144
	s_waitcnt lgkmcnt(0)
	v_mul_f32_e32 v1, v47, v1
	v_fmac_f32_e32 v1, v46, v0
	v_fmac_f32_e32 v1, v44, v2
	v_fmac_f32_e32 v1, v45, v3
	v_add_f32_e32 v54, v54, v1
	ds_read_b128 v[0:3], v53 offset:7168
	s_waitcnt lgkmcnt(0)
	v_mul_f32_e32 v1, v51, v1
	v_fmac_f32_e32 v1, v50, v0
	v_fmac_f32_e32 v1, v48, v2
	v_fmac_f32_e32 v1, v49, v3
	v_add_f32_e32 v0, v54, v1
	s_nop 1
	v_add_f32_dpp v0, v0, v0 quad_perm:[1,0,3,2] row_mask:0xf bank_mask:0xf bound_ctrl:1
	s_nop 1
	v_add_f32_dpp v0, v0, v0 quad_perm:[2,3,0,1] row_mask:0xf bank_mask:0xf bound_ctrl:1
	s_nop 1
	v_add_f32_dpp v0, v0, v0 row_half_mirror row_mask:0xf bank_mask:0xf bound_ctrl:1
	s_nop 1
	v_add_f32_dpp v0, v0, v0 row_mirror row_mask:0xf bank_mask:0xf bound_ctrl:1
	s_nop 0
	v_readlane_b32 s83, v0, 0
	v_readlane_b32 s85, v0, 16
	v_readlane_b32 s84, v0, 32
	v_readlane_b32 s86, v0, 48
	v_add_u32_e32 v0, 0x18000, v52
	s_nop 0
	v_add_u32_e32 v53, 0, v0
	ds_read_b128 v[0:3], v53
	s_waitcnt lgkmcnt(0)
	v_mul_f32_e32 v1, v11, v1
	v_fmac_f32_e32 v1, v10, v0
	v_fmac_f32_e32 v1, v6, v2
	v_fmac_f32_e32 v1, v7, v3
	v_add_f32_e32 v54, 0, v1
	ds_read_b128 v[0:3], v53 offset:1024
	s_waitcnt lgkmcnt(0)
	v_mul_f32_e32 v1, v9, v1
	v_fmac_f32_e32 v1, v8, v0
	v_fmac_f32_e32 v1, v4, v2
	v_fmac_f32_e32 v1, v5, v3
	v_add_f32_e32 v54, v54, v1
	ds_read_b128 v[0:3], v53 offset:2048
	s_waitcnt lgkmcnt(0)
	v_mul_f32_e32 v1, v15, v1
	v_fmac_f32_e32 v1, v14, v0
	v_fmac_f32_e32 v1, v12, v2
	v_fmac_f32_e32 v1, v13, v3
	v_add_f32_e32 v54, v54, v1
	ds_read_b128 v[0:3], v53 offset:3072
	s_waitcnt lgkmcnt(0)
	v_mul_f32_e32 v1, v35, v1
	v_fmac_f32_e32 v1, v34, v0
	v_fmac_f32_e32 v1, v32, v2
	v_fmac_f32_e32 v1, v33, v3
	v_add_f32_e32 v54, v54, v1
	ds_read_b128 v[0:3], v53 offset:4096
	s_waitcnt lgkmcnt(0)
	v_mul_f32_e32 v1, v39, v1
	v_fmac_f32_e32 v1, v38, v0
	v_fmac_f32_e32 v1, v36, v2
	v_fmac_f32_e32 v1, v37, v3
	v_add_f32_e32 v54, v54, v1
	ds_read_b128 v[0:3], v53 offset:5120
	s_waitcnt lgkmcnt(0)
	v_mul_f32_e32 v1, v43, v1
	v_fmac_f32_e32 v1, v42, v0
	v_fmac_f32_e32 v1, v40, v2
	v_fmac_f32_e32 v1, v41, v3
	v_add_f32_e32 v54, v54, v1
	ds_read_b128 v[0:3], v53 offset:6144
	s_waitcnt lgkmcnt(0)
	v_mul_f32_e32 v1, v47, v1
	v_fmac_f32_e32 v1, v46, v0
	v_fmac_f32_e32 v1, v44, v2
	v_fmac_f32_e32 v1, v45, v3
	v_add_f32_e32 v54, v54, v1
	ds_read_b128 v[0:3], v53 offset:7168
	s_waitcnt lgkmcnt(0)
	v_mul_f32_e32 v1, v51, v1
	v_fmac_f32_e32 v1, v50, v0
	v_fmac_f32_e32 v1, v48, v2
	v_fmac_f32_e32 v1, v49, v3
	v_add_f32_e32 v0, v54, v1
	s_nop 1
	v_add_f32_dpp v0, v0, v0 quad_perm:[1,0,3,2] row_mask:0xf bank_mask:0xf bound_ctrl:1
	s_nop 1
	v_add_f32_dpp v0, v0, v0 quad_perm:[2,3,0,1] row_mask:0xf bank_mask:0xf bound_ctrl:1
	s_nop 1
	v_add_f32_dpp v0, v0, v0 row_half_mirror row_mask:0xf bank_mask:0xf bound_ctrl:1
	s_nop 1
	v_add_f32_dpp v0, v0, v0 row_mirror row_mask:0xf bank_mask:0xf bound_ctrl:1
	s_nop 0
	v_readlane_b32 s87, v0, 0
	v_readlane_b32 s89, v0, 16
	v_readlane_b32 s88, v0, 32
	v_readlane_b32 s90, v0, 48
	v_add_u32_e32 v0, 0x1a000, v52
	s_nop 0
	v_add_u32_e32 v53, 0, v0
	ds_read_b128 v[0:3], v53
	s_waitcnt lgkmcnt(0)
	v_mul_f32_e32 v1, v11, v1
	v_fmac_f32_e32 v1, v10, v0
	v_fmac_f32_e32 v1, v6, v2
	v_fmac_f32_e32 v1, v7, v3
	v_add_f32_e32 v54, 0, v1
	ds_read_b128 v[0:3], v53 offset:1024
	s_waitcnt lgkmcnt(0)
	v_mul_f32_e32 v1, v9, v1
	v_fmac_f32_e32 v1, v8, v0
	v_fmac_f32_e32 v1, v4, v2
	v_fmac_f32_e32 v1, v5, v3
	v_add_f32_e32 v54, v54, v1
	ds_read_b128 v[0:3], v53 offset:2048
	s_waitcnt lgkmcnt(0)
	v_mul_f32_e32 v1, v15, v1
	v_fmac_f32_e32 v1, v14, v0
	v_fmac_f32_e32 v1, v12, v2
	v_fmac_f32_e32 v1, v13, v3
	v_add_f32_e32 v54, v54, v1
	ds_read_b128 v[0:3], v53 offset:3072
	s_waitcnt lgkmcnt(0)
	v_mul_f32_e32 v1, v35, v1
	v_fmac_f32_e32 v1, v34, v0
	v_fmac_f32_e32 v1, v32, v2
	v_fmac_f32_e32 v1, v33, v3
	v_add_f32_e32 v54, v54, v1
	ds_read_b128 v[0:3], v53 offset:4096
	s_waitcnt lgkmcnt(0)
	v_mul_f32_e32 v1, v39, v1
	v_fmac_f32_e32 v1, v38, v0
	v_fmac_f32_e32 v1, v36, v2
	v_fmac_f32_e32 v1, v37, v3
	v_add_f32_e32 v54, v54, v1
	ds_read_b128 v[0:3], v53 offset:5120
	s_waitcnt lgkmcnt(0)
	v_mul_f32_e32 v1, v43, v1
	v_fmac_f32_e32 v1, v42, v0
	v_fmac_f32_e32 v1, v40, v2
	v_fmac_f32_e32 v1, v41, v3
	v_add_f32_e32 v54, v54, v1
	ds_read_b128 v[0:3], v53 offset:6144
	s_waitcnt lgkmcnt(0)
	v_mul_f32_e32 v1, v47, v1
	v_fmac_f32_e32 v1, v46, v0
	v_fmac_f32_e32 v1, v44, v2
	v_fmac_f32_e32 v1, v45, v3
	v_add_f32_e32 v54, v54, v1
	ds_read_b128 v[0:3], v53 offset:7168
	s_waitcnt lgkmcnt(0)
	v_mul_f32_e32 v1, v51, v1
	v_fmac_f32_e32 v1, v50, v0
	v_fmac_f32_e32 v1, v48, v2
	v_fmac_f32_e32 v1, v49, v3
	v_add_f32_e32 v0, v54, v1
	s_nop 1
	v_add_f32_dpp v0, v0, v0 quad_perm:[1,0,3,2] row_mask:0xf bank_mask:0xf bound_ctrl:1
	s_nop 1
	v_add_f32_dpp v0, v0, v0 quad_perm:[2,3,0,1] row_mask:0xf bank_mask:0xf bound_ctrl:1
	s_nop 1
	v_add_f32_dpp v0, v0, v0 row_half_mirror row_mask:0xf bank_mask:0xf bound_ctrl:1
	s_nop 1
	v_add_f32_dpp v0, v0, v0 row_mirror row_mask:0xf bank_mask:0xf bound_ctrl:1
	s_nop 0
	v_readlane_b32 s93, v0, 0
	v_readlane_b32 s94, v0, 16
	v_readlane_b32 s91, v0, 32
	v_readlane_b32 s92, v0, 48
	v_add_u32_e32 v0, 0x1c000, v52
	s_nop 0
	v_add_u32_e32 v53, 0, v0
	ds_read_b128 v[0:3], v53
	s_waitcnt lgkmcnt(0)
	v_mul_f32_e32 v1, v11, v1
	v_fmac_f32_e32 v1, v10, v0
	v_fmac_f32_e32 v1, v6, v2
	v_fmac_f32_e32 v1, v7, v3
	v_add_f32_e32 v54, 0, v1
	ds_read_b128 v[0:3], v53 offset:1024
	s_waitcnt lgkmcnt(0)
	v_mul_f32_e32 v1, v9, v1
	v_fmac_f32_e32 v1, v8, v0
	v_fmac_f32_e32 v1, v4, v2
	v_fmac_f32_e32 v1, v5, v3
	v_add_f32_e32 v54, v54, v1
	ds_read_b128 v[0:3], v53 offset:2048
	s_waitcnt lgkmcnt(0)
	v_mul_f32_e32 v1, v15, v1
	v_fmac_f32_e32 v1, v14, v0
	v_fmac_f32_e32 v1, v12, v2
	v_fmac_f32_e32 v1, v13, v3
	v_add_f32_e32 v54, v54, v1
	ds_read_b128 v[0:3], v53 offset:3072
	s_waitcnt lgkmcnt(0)
	v_mul_f32_e32 v1, v35, v1
	v_fmac_f32_e32 v1, v34, v0
	v_fmac_f32_e32 v1, v32, v2
	v_fmac_f32_e32 v1, v33, v3
	v_add_f32_e32 v54, v54, v1
	ds_read_b128 v[0:3], v53 offset:4096
	s_waitcnt lgkmcnt(0)
	v_mul_f32_e32 v1, v39, v1
	v_fmac_f32_e32 v1, v38, v0
	v_fmac_f32_e32 v1, v36, v2
	v_fmac_f32_e32 v1, v37, v3
	v_add_f32_e32 v54, v54, v1
	ds_read_b128 v[0:3], v53 offset:5120
	s_waitcnt lgkmcnt(0)
	v_mul_f32_e32 v1, v43, v1
	v_fmac_f32_e32 v1, v42, v0
	v_fmac_f32_e32 v1, v40, v2
	v_fmac_f32_e32 v1, v41, v3
	v_add_f32_e32 v54, v54, v1
	ds_read_b128 v[0:3], v53 offset:6144
	s_waitcnt lgkmcnt(0)
	v_mul_f32_e32 v1, v47, v1
	v_fmac_f32_e32 v1, v46, v0
	v_fmac_f32_e32 v1, v44, v2
	v_fmac_f32_e32 v1, v45, v3
	v_add_f32_e32 v54, v54, v1
	ds_read_b128 v[0:3], v53 offset:7168
	s_waitcnt lgkmcnt(0)
	v_mul_f32_e32 v1, v51, v1
	v_fmac_f32_e32 v1, v50, v0
	v_fmac_f32_e32 v1, v48, v2
	v_fmac_f32_e32 v1, v49, v3
	v_add_f32_e32 v0, v54, v1
	s_nop 1
	v_add_f32_dpp v0, v0, v0 quad_perm:[1,0,3,2] row_mask:0xf bank_mask:0xf bound_ctrl:1
	s_nop 1
	v_add_f32_dpp v0, v0, v0 quad_perm:[2,3,0,1] row_mask:0xf bank_mask:0xf bound_ctrl:1
	s_nop 1
	v_add_f32_dpp v0, v0, v0 row_half_mirror row_mask:0xf bank_mask:0xf bound_ctrl:1
	s_nop 1
	v_add_f32_dpp v0, v0, v0 row_mirror row_mask:0xf bank_mask:0xf bound_ctrl:1
	s_nop 0
	v_readlane_b32 s95, v0, 0
	v_readlane_b32 s97, v0, 16
	v_readlane_b32 s96, v0, 32
	v_readlane_b32 s4, v0, 48
	v_add_u32_e32 v0, 0x1e000, v52
	s_nop 0
	v_add_u32_e32 v52, 0, v0
	ds_read_b128 v[0:3], v52
	s_waitcnt lgkmcnt(0)
	v_mul_f32_e32 v1, v11, v1
	v_fmac_f32_e32 v1, v10, v0
	v_fmac_f32_e32 v1, v6, v2
	v_fmac_f32_e32 v1, v7, v3
	v_add_f32_e32 v6, 0, v1
	ds_read_b128 v[0:3], v52 offset:1024
	s_waitcnt lgkmcnt(0)
	v_mul_f32_e32 v1, v9, v1
	v_fmac_f32_e32 v1, v8, v0
	v_fmac_f32_e32 v1, v4, v2
	v_fmac_f32_e32 v1, v5, v3
	v_add_f32_e32 v4, v6, v1
	ds_read_b128 v[0:3], v52 offset:2048
	s_waitcnt lgkmcnt(0)
	v_mul_f32_e32 v1, v15, v1
	v_fmac_f32_e32 v1, v14, v0
	v_fmac_f32_e32 v1, v12, v2
	v_fmac_f32_e32 v1, v13, v3
	v_add_f32_e32 v4, v4, v1
	ds_read_b128 v[0:3], v52 offset:3072
	s_waitcnt lgkmcnt(0)
	v_mul_f32_e32 v1, v35, v1
	v_fmac_f32_e32 v1, v34, v0
	v_fmac_f32_e32 v1, v32, v2
	v_fmac_f32_e32 v1, v33, v3
	v_add_f32_e32 v4, v4, v1
	ds_read_b128 v[0:3], v52 offset:4096
	s_waitcnt lgkmcnt(0)
	v_mul_f32_e32 v1, v39, v1
	v_fmac_f32_e32 v1, v38, v0
	v_fmac_f32_e32 v1, v36, v2
	v_fmac_f32_e32 v1, v37, v3
	v_add_f32_e32 v4, v4, v1
	ds_read_b128 v[0:3], v52 offset:5120
	s_waitcnt lgkmcnt(0)
	v_mul_f32_e32 v1, v43, v1
	v_fmac_f32_e32 v1, v42, v0
	v_fmac_f32_e32 v1, v40, v2
	v_fmac_f32_e32 v1, v41, v3
	v_add_f32_e32 v4, v4, v1
	ds_read_b128 v[0:3], v52 offset:6144
	s_waitcnt lgkmcnt(0)
	v_mul_f32_e32 v1, v47, v1
	v_fmac_f32_e32 v1, v46, v0
	v_fmac_f32_e32 v1, v44, v2
	v_fmac_f32_e32 v1, v45, v3
	v_add_f32_e32 v4, v4, v1
	ds_read_b128 v[0:3], v52 offset:7168
	s_waitcnt lgkmcnt(0)
	v_mul_f32_e32 v1, v51, v1
	v_fmac_f32_e32 v1, v50, v0
	v_fmac_f32_e32 v1, v48, v2
	v_fmac_f32_e32 v1, v49, v3
	v_add_f32_e32 v0, v4, v1
	s_nop 1
	v_add_f32_dpp v0, v0, v0 quad_perm:[1,0,3,2] row_mask:0xf bank_mask:0xf bound_ctrl:1
	s_nop 1
	v_add_f32_dpp v0, v0, v0 quad_perm:[2,3,0,1] row_mask:0xf bank_mask:0xf bound_ctrl:1
	s_nop 1
	v_add_f32_dpp v0, v0, v0 row_half_mirror row_mask:0xf bank_mask:0xf bound_ctrl:1
	s_nop 1
	v_add_f32_dpp v0, v0, v0 row_mirror row_mask:0xf bank_mask:0xf bound_ctrl:1
	s_nop 0
	v_readlane_b32 s5, v0, 0
	v_readlane_b32 s40, v0, 16
	v_readlane_b32 s33, v0, 32
	v_readlane_b32 s16, v0, 48
	s_and_saveexec_b64 s[36:37], vcc
	s_cbranch_execz .LBB0_1575
	v_mov_b32_e32 v0, s25
	v_mov_b32_e32 v1, s31
	v_pk_add_f32 v[0:1], s[8:9], v[0:1]
	s_nop 0
	v_add_f32_e32 v33, v0, v1
	v_mov_b32_e32 v0, s10
	v_mov_b32_e32 v1, s11
	v_pk_add_f32 v[0:1], s[6:7], v[0:1]
	v_mul_f32_e32 v34, 0xbfb8aa3b, v33
	v_add_f32_e32 v0, v0, v1
	v_mul_f32_e32 v1, 0xbfb8aa3b, v0
	v_fma_f32 v2, v0, s19, -v1
	v_rndne_f32_e32 v3, v1
	v_fmac_f32_e32 v2, 0xb2a5705f, v0
	v_sub_f32_e32 v1, v1, v3
	v_add_f32_e32 v1, v1, v2
	v_exp_f32_e32 v1, v1
	v_cvt_i32_f32_e32 v2, v3
	v_cmp_nlt_f32_e32 vcc, s50, v0
	v_fma_f32 v35, v33, s19, -v34
	v_rndne_f32_e32 v36, v34
	v_ldexp_f32 v1, v1, v2
	v_cndmask_b32_e32 v1, 0, v1, vcc
	v_cmp_ngt_f32_e32 vcc, s51, v0
	v_fmac_f32_e32 v35, 0xb2a5705f, v33
	v_sub_f32_e32 v34, v34, v36
	v_cndmask_b32_e32 v0, v84, v1, vcc
	v_add_f32_e32 v0, 1.0, v0
	v_div_scale_f32 v1, s[6:7], v0, v0, 1.0
	v_rcp_f32_e32 v2, v1
	v_add_f32_e32 v34, v34, v35
	v_exp_f32_e32 v34, v34
	v_cvt_i32_f32_e32 v35, v36
	v_fma_f32 v3, -v1, v2, 1.0
	v_fmac_f32_e32 v2, v3, v2
	v_div_scale_f32 v3, vcc, 1.0, v0, 1.0
	v_mul_f32_e32 v4, v3, v2
	v_fma_f32 v5, -v1, v4, v3
	v_fmac_f32_e32 v4, v5, v2
	v_fma_f32 v1, -v1, v4, v3
	v_div_fmas_f32 v1, v1, v2, v4
	v_div_fixup_f32 v32, v1, v0, 1.0
	global_load_dwordx4 v[0:3], v83, s[22:23] offset:48
	global_load_dwordx4 v[4:7], v83, s[22:23] offset:32
	global_load_dwordx4 v[8:11], v83, s[22:23] offset:16
	global_load_dwordx4 v[12:15], v83, s[22:23]
	v_ldexp_f32 v34, v34, v35
	v_cmp_nlt_f32_e32 vcc, s50, v33
	s_waitcnt vmcnt(0)
	v_add_f32_e32 v12, v32, v12
	v_cndmask_b32_e32 v34, 0, v34, vcc
	v_cmp_ngt_f32_e32 vcc, s51, v33
	v_cmp_lt_f32_e64 s[8:9], s52, v12
	s_nop 0
	v_cndmask_b32_e32 v33, v84, v34, vcc
	v_add_f32_e32 v33, 1.0, v33
	v_div_scale_f32 v34, s[6:7], v33, v33, 1.0
	v_rcp_f32_e32 v35, v34
	s_nop 0
	v_fma_f32 v36, -v34, v35, 1.0
	v_fmac_f32_e32 v35, v36, v35
	v_div_scale_f32 v36, vcc, 1.0, v33, 1.0
	v_mul_f32_e32 v37, v36, v35
	v_fma_f32 v38, -v34, v37, v36
	v_fmac_f32_e32 v37, v38, v35
	v_fma_f32 v34, -v34, v37, v36
	v_div_fmas_f32 v34, v34, v35, v37
	v_div_fixup_f32 v33, v34, v33, 1.0
	v_add_f32_e32 v34, v33, v13
	v_max_f32_e32 v35, 0xf149f2ca, v12
	v_cmp_gt_f32_e32 vcc, v34, v35
	v_cmp_ngt_f32_e64 s[6:7], v34, v35
	v_mov_b32_e32 v37, v34
	v_mov_b32_e32 v12, v35
	s_cbranch_vccnz .LBB0_1585
	v_cmp_nlt_f32_e32 vcc, s52, v34
	v_mov_b32_e32 v12, 0xf149f2ca
	s_cbranch_vccnz .LBB0_1584
	v_mov_b32_e32 v12, v34

.Lpf_skip_0:
	v_lshlrev_b32_e32 v90, 16, v88
	v_and_b32_e32 v91, 0xffff0000, v88
	v_sub_f32_e32 v90, v86, v90
	v_sub_f32_e32 v91, v87, v91
	v_cvt_pk_bf16_f32 v89, v84, v85
	v_cvt_pk_bf16_f32 v90, v90, v91
	v_lshlrev_b32_e32 v128, 4, v128
	v_lshlrev_b32_e32 v91, 16, v89
	v_sub_f32_e32 v91, v84, v91
	v_and_b32_e32 v129, 0xffff0000, v89
	v_add3_u32 v128, s46, v128, v228
	v_sub_f32_e32 v129, v85, v129
	v_cvt_pk_bf16_f32 v91, v91, v129
	ds_write_b64 v128, v[88:89]
	v_add_u32_e32 v88, 0x10000, v128
	ds_write_b64 v88, v[90:91]
	s_nop 0
	v_cvt_pk_fp8_f32 v90, v154, v155
	s_nop 0
	v_cvt_pk_fp8_f32 v91, v174, v175
	v_lshl_add_u64 v[88:89], s[6:7], 0, v[78:79]
	v_cvt_pk_fp8_f32 v90, v152, v153 op_sel:[0,0,1]
	s_nop 0
	v_cvt_pk_fp8_f32 v91, v170, v171 op_sel:[0,0,1]
	v_cvt_pk_fp8_f32 v128, v186, v187
	global_store_dword v[88:89], v90, off
	v_lshl_add_u64 v[88:89], s[6:7], 0, v[76:77]
	s_nop 0
	global_store_dword v[88:89], v91, off
	v_cvt_pk_fp8_f32 v90, v158, v159
	s_nop 0
	v_cvt_pk_fp8_f32 v91, v178, v179
	v_cvt_pk_fp8_f32 v128, v184, v185 op_sel:[0,0,1]
	v_cvt_pk_fp8_f32 v90, v156, v157 op_sel:[0,0,1]
	v_lshl_add_u64 v[88:89], s[6:7], 0, v[74:75]
	v_cvt_pk_fp8_f32 v91, v176, v177 op_sel:[0,0,1]
	global_store_dword v[88:89], v128, off
	v_lshl_add_u64 v[88:89], s[6:7], 0, v[72:73]
	s_nop 0
	global_store_dword v[88:89], v90, off
	v_lshl_add_u64 v[88:89], s[6:7], 0, v[70:71]
	v_cvt_pk_fp8_f32 v128, v134, v135
	global_store_dword v[88:89], v91, off
	s_nop 0
	v_cvt_pk_fp8_f32 v88, v240, v241
	s_nop 0
	v_cvt_pk_fp8_f32 v89, v80, v81
	v_cvt_pk_fp8_f32 v128, v130, v131 op_sel:[0,0,1]
	v_cvt_pk_fp8_f32 v88, v238, v239 op_sel:[0,0,1]
	v_lshl_add_u64 v[80:81], s[6:7], 0, v[68:69]
	v_cvt_pk_fp8_f32 v89, v82, v83 op_sel:[0,0,1]
	global_store_dword v[80:81], v128, off
	v_lshl_add_u64 v[80:81], s[6:7], 0, v[66:67]
	global_store_dword v[80:81], v88, off
	v_lshl_add_u64 v[80:81], s[6:7], 0, v[64:65]
	global_store_dword v[80:81], v89, off
	s_nop 0
	s_nop 0
	v_cvt_pk_fp8_f32 v80, v146, v147
	v_cvt_pk_fp8_f32 v81, v164, v165
	s_add_i32 s6, s1, s18
	s_ashr_i32 s7, s6, 31
	s_lshl_b64 s[6:7], s[6:7], 11
	v_cvt_pk_fp8_f32 v80, v136, v137 op_sel:[0,0,1]
	v_cvt_pk_fp8_f32 v81, v162, v163 op_sel:[0,0,1]
	s_add_u32 s6, s41, s6
	s_addc_u32 s7, s42, s7
	v_lshl_add_u64 v[78:79], s[6:7], 0, v[78:79]
	v_lshl_add_u64 v[76:77], s[6:7], 0, v[76:77]
	s_nop 0
	global_store_dword v[78:79], v80, off
	global_store_dword v[76:77], v81, off
	s_nop 0
	s_nop 0
	v_cvt_pk_fp8_f32 v82, v182, v183
	v_cvt_pk_fp8_f32 v76, v150, v151
	v_cvt_pk_fp8_f32 v77, v172, v173
	v_lshl_add_u64 v[74:75], s[6:7], 0, v[74:75]
	v_cvt_pk_fp8_f32 v82, v180, v181 op_sel:[0,0,1]
	v_cvt_pk_fp8_f32 v76, v148, v149 op_sel:[0,0,1]
	v_cvt_pk_fp8_f32 v77, v168, v169 op_sel:[0,0,1]
	v_lshl_add_u64 v[72:73], s[6:7], 0, v[72:73]
	v_lshl_add_u64 v[70:71], s[6:7], 0, v[70:71]
	global_store_dword v[74:75], v82, off
	s_nop 0
	global_store_dword v[72:73], v76, off
	global_store_dword v[70:71], v77, off
	s_nop 0
	s_nop 0
	v_cvt_pk_fp8_f32 v74, v94, v95
	v_cvt_pk_fp8_f32 v70, v140, v141
	v_cvt_pk_fp8_f32 v71, v86, v87
	v_lshl_add_u64 v[68:69], s[6:7], 0, v[68:69]
	v_cvt_pk_fp8_f32 v74, v92, v93 op_sel:[0,0,1]
	v_cvt_pk_fp8_f32 v70, v138, v139 op_sel:[0,0,1]
	v_cvt_pk_fp8_f32 v71, v84, v85 op_sel:[0,0,1]
	v_lshl_add_u64 v[66:67], s[6:7], 0, v[66:67]
	v_lshl_add_u64 v[64:65], s[6:7], 0, v[64:65]
	global_store_dword v[68:69], v74, off
	global_store_dword v[66:67], v70, off
	global_store_dword v[64:65], v71, off
	s_waitcnt lgkmcnt(0)
	s_barrier
	ds_read_b128 v[64:67], v190
	ds_read_b128 v[68:71], v191
	s_waitcnt lgkmcnt(1)
	v_mfma_f32_16x16x32_bf16 v[72:75], v[0:3], v[64:67], 0
	v_mov_b32_e32 v128, v167
	v_mfma_f32_16x16x32_bf16 v[64:67], v[4:7], v[64:67], v[72:75]
	s_waitcnt lgkmcnt(0)
	v_mfma_f32_16x16x32_bf16 v[64:67], v[0:3], v[68:71], v[64:67]
	ds_read_b128 v[68:71], v192
	s_nop 2
	ds_read_b128 v[72:75], v193
	s_waitcnt lgkmcnt(1)
	v_mfma_f32_16x16x32_bf16 v[64:67], v[8:11], v[68:71], v[64:67]
	v_mfma_f32_16x16x32_bf16 v[64:67], v[12:15], v[68:71], v[64:67]
	s_waitcnt lgkmcnt(0)
	v_mfma_f32_16x16x32_bf16 v[64:67], v[8:11], v[72:75], v[64:67]
	ds_read_b128 v[68:71], v194
	ds_read_b128 v[72:75], v195
	s_waitcnt lgkmcnt(1)
	v_mfma_f32_16x16x32_bf16 v[64:67], v[16:19], v[68:71], v[64:67]
	v_mfma_f32_16x16x32_bf16 v[64:67], v[20:23], v[68:71], v[64:67]
	s_waitcnt lgkmcnt(0)
	v_mfma_f32_16x16x32_bf16 v[64:67], v[16:19], v[72:75], v[64:67]
	ds_read_b128 v[68:71], v196
	ds_read_b128 v[72:75], v197
	s_waitcnt lgkmcnt(1)
	v_mfma_f32_16x16x32_bf16 v[64:67], v[24:27], v[68:71], v[64:67]
	v_mfma_f32_16x16x32_bf16 v[64:67], v[28:31], v[68:71], v[64:67]
	s_waitcnt lgkmcnt(0)
	v_mfma_f32_16x16x32_bf16 v[64:67], v[24:27], v[72:75], v[64:67]
	ds_read_b128 v[68:71], v198
	ds_read_b128 v[72:75], v199
	s_waitcnt lgkmcnt(1)
	v_mfma_f32_16x16x32_bf16 v[64:67], v[32:35], v[68:71], v[64:67]
	v_mfma_f32_16x16x32_bf16 v[64:67], v[36:39], v[68:71], v[64:67]
	s_waitcnt lgkmcnt(0)
	v_mfma_f32_16x16x32_bf16 v[64:67], v[32:35], v[72:75], v[64:67]
	ds_read_b128 v[68:71], v200
	ds_read_b128 v[72:75], v201
	s_waitcnt lgkmcnt(1)
	v_mfma_f32_16x16x32_bf16 v[64:67], v[40:43], v[68:71], v[64:67]
	v_mfma_f32_16x16x32_bf16 v[64:67], v[44:47], v[68:71], v[64:67]
	s_waitcnt lgkmcnt(0)
	v_mfma_f32_16x16x32_bf16 v[64:67], v[40:43], v[72:75], v[64:67]
	ds_read_b128 v[68:71], v202
	ds_read_b128 v[72:75], v203
	s_waitcnt lgkmcnt(1)
	v_mfma_f32_16x16x32_bf16 v[64:67], v[48:51], v[68:71], v[64:67]
	v_mfma_f32_16x16x32_bf16 v[64:67], v[52:55], v[68:71], v[64:67]
	s_waitcnt lgkmcnt(0)
	v_mfma_f32_16x16x32_bf16 v[64:67], v[48:51], v[72:75], v[64:67]
	ds_read_b128 v[68:71], v204
	ds_read_b128 v[72:75], v205
	s_waitcnt lgkmcnt(1)
	v_mfma_f32_16x16x32_bf16 v[64:67], v[56:59], v[68:71], v[64:67]
	v_mfma_f32_16x16x32_bf16 v[64:67], v[60:63], v[68:71], v[64:67]
	s_waitcnt lgkmcnt(0)
	v_mfma_f32_16x16x32_bf16 v[64:67], v[56:59], v[72:75], v[64:67]
	s_nop 7
	ds_write_b128 v208, v[64:67]
	s_waitcnt lgkmcnt(0)
	s_barrier
	s_nop 0
	v_cmp_gt_i32_e32 vcc, s48, v128
	s_and_saveexec_b64 s[6:7], vcc
	s_cbranch_execz .LBB0_1743
	v_lshl_add_u32 v72, v128, 2, 0
	v_add_u32_e32 v70, 0x22000, v72
	ds_read2st64_b32 v[64:65], v70 offset1:4
	ds_read2st64_b32 v[66:67], v70 offset0:8 offset1:12
	ds_read2st64_b32 v[68:69], v70 offset0:16 offset1:20
	ds_read2st64_b32 v[70:71], v70 offset0:24 offset1:28
	s_waitcnt lgkmcnt(3)
	v_add_f32_e32 v64, 0, v64
	v_add_f32_e32 v64, v64, v65
	s_waitcnt lgkmcnt(2)
	v_add_f32_e32 v64, v64, v66
	v_add_f32_e32 v64, v64, v67
	s_waitcnt lgkmcnt(1)
	v_add_f32_e32 v64, v64, v68
	v_add_f32_e32 v64, v64, v69
	s_waitcnt lgkmcnt(0)
	v_add_f32_e32 v64, v64, v70
	v_add_f32_e32 v64, v64, v71
	v_add_u32_e32 v65, 0x21000, v72
	ds_write_b32 v65, v64
	v_mul_f32_e32 v142, 0xbfb8aa3b, v64
	v_fma_f32 v143, v64, s50, -v142
	v_rndne_f32_e32 v144, v142
	v_fmac_f32_e32 v143, 0xb2a5705f, v64
	v_sub_f32_e32 v142, v142, v144
	v_add_f32_e32 v142, v142, v143
	v_cvt_i32_f32_e32 v145, v144
	v_exp_f32_e32 v146, v142
	v_cmp_nlt_f32_e32 vcc, s51, v64
	v_ldexp_f32 v145, v146, v145
	s_nop 0
	v_cndmask_b32_e32 v145, 0, v145, vcc
	v_cmp_ngt_f32_e32 vcc, s52, v64
	s_nop 1
	v_cndmask_b32_e32 v145, v211, v145, vcc
	v_add_f32_e32 v145, 1.0, v145
	v_div_scale_f32 v146, s[98:99], v145, v145, 1.0
	v_rcp_f32_e32 v147, v146
	v_div_scale_f32 v148, vcc, 1.0, v145, 1.0
	v_fma_f32 v149, -v146, v147, 1.0
	v_fmac_f32_e32 v147, v149, v147
	v_mul_f32_e32 v149, v148, v147
	v_fma_f32 v150, -v146, v149, v148
	v_fmac_f32_e32 v149, v150, v147
	v_fma_f32 v146, -v146, v149, v148
	v_div_fmas_f32 v146, v146, v147, v149
	v_div_fixup_f32 v146, v146, v145, 1.0
	ds_write_b32 v65, v146 offset:1024

.LBB0_1936:
	v_mbcnt_lo_u32_b32 v0, -1, 0
	v_mbcnt_hi_u32_b32 v0, -1, v0
	s_lshl_b32 s34, s59, 8
	v_ashrrev_i32_e32 v1, 1, v0
	v_bfi_b32 v2, -16, v1, v0
	v_and_b32_e32 v178, 16, v0
	v_mov_b32_e32 v0, v172
	v_mov_b32_e32 v1, v160
	v_pk_mul_f32 v[4:5], v[0:1], s[20:21] op_sel_hi:[1,0]
	v_mov_b32_e32 v160, v173
	v_mul_f32_e32 v0, 0xbfb8aa3b, v4
	v_exp_f32_e32 v0, v0
	v_pk_mul_f32 v[6:7], v[160:161], s[20:21] op_sel_hi:[1,0]
	s_add_i32 s34, s34, s50
	s_lshl_b32 s23, s30, 7
	v_add_f32_e32 v0, 1.0, v0
	v_rcp_f32_e32 v3, v0
	v_mul_f32_e32 v0, 0xbfb8aa3b, v6
	v_exp_f32_e32 v8, v0
	s_ashr_i32 s8, s23, 31
	v_mul_f32_e32 v3, v4, v3
	v_mul_f32_e32 v3, v3, v5
	v_add_f32_e32 v4, 1.0, v8
	v_rcp_f32_e32 v10, v4
	v_mov_b32_e32 v4, v174
	v_mov_b32_e32 v5, v162
	v_pk_mul_f32 v[4:5], v[4:5], s[20:21] op_sel_hi:[1,0]
	v_mov_b32_e32 v162, v175
	v_mul_f32_e32 v8, 0xbfb8aa3b, v4
	v_exp_f32_e32 v11, v8
	v_mul_f32_e32 v6, v6, v10
	v_pk_mul_f32 v[8:9], v[162:163], s[20:21] op_sel_hi:[1,0]
	s_mul_i32 s30, s34, 0x600
	v_add_f32_e32 v10, 1.0, v11
	v_rcp_f32_e32 v10, v10
	v_mul_f32_e32 v12, 0xbfb8aa3b, v8
	v_exp_f32_e32 v12, v12
	s_mul_hi_i32 s35, s34, 0x600
	v_mul_f32_e32 v4, v4, v10
	v_mul_f32_e32 v10, v4, v5
	v_mov_b32_e32 v4, v168
	v_mov_b32_e32 v5, v152
	v_add_f32_e32 v11, 1.0, v12
	v_mul_f32_e32 v12, v6, v7
	v_pk_mul_f32 v[6:7], v[4:5], s[20:21] op_sel_hi:[1,0]
	v_rcp_f32_e32 v11, v11
	v_mul_f32_e32 v4, 0xbfb8aa3b, v6
	v_exp_f32_e32 v5, v4
	s_nop 0
	v_cvt_pk_fp8_f32 v4, v3, v12
	v_mul_f32_e32 v8, v8, v11
	v_add_f32_e32 v3, 1.0, v5
	v_rcp_f32_e32 v3, v3
	v_mov_b32_e32 v152, v169
	v_mul_f32_e32 v11, v8, v9
	v_pk_mul_f32 v[8:9], v[152:153], s[20:21] op_sel_hi:[1,0]
	v_mul_f32_e32 v3, v6, v3
	v_mul_f32_e32 v5, 0xbfb8aa3b, v8
	v_exp_f32_e32 v5, v5
	v_mul_f32_e32 v3, v3, v7
	v_mov_b32_e32 v6, v170
	v_mov_b32_e32 v7, v154
	v_pk_mul_f32 v[6:7], v[6:7], s[20:21] op_sel_hi:[1,0]
	v_cvt_pk_fp8_f32 v4, v10, v11 op_sel:[0,0,1]
	v_mul_f32_e32 v10, 0xbfb8aa3b, v6
	v_mov_b32_e32 v154, v171
	v_add_f32_e32 v5, 1.0, v5
	v_exp_f32_e32 v12, v10
	v_pk_mul_f32 v[10:11], v[154:155], s[20:21] op_sel_hi:[1,0]
	v_rcp_f32_e32 v5, v5
	v_mul_f32_e32 v13, 0xbfb8aa3b, v10
	v_exp_f32_e32 v13, v13
	s_add_u32 s36, s48, s30
	v_mul_f32_e32 v5, v8, v5
	v_add_f32_e32 v8, 1.0, v12
	v_rcp_f32_e32 v8, v8
	v_add_f32_e32 v12, 1.0, v13
	v_rcp_f32_e32 v12, v12
	v_mul_f32_e32 v9, v5, v9
	v_mul_f32_e32 v5, v6, v8
	v_mul_f32_e32 v13, v5, v7
	v_mul_f32_e32 v5, v10, v12
	v_mul_f32_e32 v10, v5, v11
	s_nop 0
	v_mov_b32_e32 v7, v148
	v_mov_b32_e32 v148, v165
	v_cvt_pk_fp8_f32 v5, v3, v9
	v_pk_mul_f32 v[8:9], v[148:149], s[20:21] op_sel_hi:[1,0]
	v_mov_b32_e32 v6, v164
	v_mul_f32_e32 v11, 0xbfb8aa3b, v8
	v_pk_mul_f32 v[6:7], v[6:7], s[20:21] op_sel_hi:[1,0]
	v_exp_f32_e32 v11, v11
	v_mul_f32_e32 v3, 0xbfb8aa3b, v6
	v_exp_f32_e32 v3, v3
	v_cvt_pk_fp8_f32 v5, v13, v10 op_sel:[0,0,1]
	v_add_f32_e32 v10, 1.0, v11
	v_rcp_f32_e32 v12, v10
	v_mov_b32_e32 v10, v166
	v_mov_b32_e32 v11, v150
	v_add_f32_e32 v3, 1.0, v3
	v_pk_mul_f32 v[10:11], v[10:11], s[20:21] op_sel_hi:[1,0]
	v_rcp_f32_e32 v3, v3
	v_mul_f32_e32 v13, 0xbfb8aa3b, v10
	v_exp_f32_e32 v13, v13
	v_mov_b32_e32 v150, v167
	v_mul_f32_e32 v3, v6, v3
	v_mul_f32_e32 v3, v3, v7
	v_add_f32_e32 v7, 1.0, v13
	v_mul_f32_e32 v6, v8, v12
	v_rcp_f32_e32 v7, v7
	v_pk_mul_f32 v[12:13], v[150:151], s[20:21] op_sel_hi:[1,0]
	v_mul_f32_e32 v14, v6, v9
	v_mul_f32_e32 v8, 0xbfb8aa3b, v12
	v_exp_f32_e32 v8, v8
	v_mul_f32_e32 v6, v10, v7
	v_mul_f32_e32 v10, v6, v11
	v_mov_b32_e32 v6, v156
	v_mov_b32_e32 v7, v144
	v_add_f32_e32 v11, 1.0, v8
	v_pk_mul_f32 v[8:9], v[6:7], s[20:21] op_sel_hi:[1,0]
	v_rcp_f32_e32 v11, v11
	v_mul_f32_e32 v6, 0xbfb8aa3b, v8
	v_exp_f32_e32 v7, v6
	s_nop 0
	v_cvt_pk_fp8_f32 v6, v3, v14
	v_mov_b32_e32 v144, v157
	v_add_f32_e32 v3, 1.0, v7
	v_rcp_f32_e32 v3, v3
	v_mul_f32_e32 v7, v12, v11
	v_mul_f32_e32 v7, v7, v13
	v_mov_b32_e32 v12, v158
	v_mov_b32_e32 v13, v146
	v_pk_mul_f32 v[12:13], v[12:13], s[20:21] op_sel_hi:[1,0]
	v_cvt_pk_fp8_f32 v6, v10, v7 op_sel:[0,0,1]
	v_mul_f32_e32 v3, v8, v3
	v_pk_mul_f32 v[10:11], v[144:145], s[20:21] op_sel_hi:[1,0]
	v_mul_f32_e32 v8, 0xbfb8aa3b, v12
	v_mul_f32_e32 v7, 0xbfb8aa3b, v10
	v_exp_f32_e32 v8, v8
	v_exp_f32_e32 v7, v7
	v_mov_b32_e32 v146, v159
	v_mul_f32_e32 v3, v3, v9
	v_add_f32_e32 v8, 1.0, v8
	v_add_f32_e32 v7, 1.0, v7
	v_rcp_f32_e32 v14, v8
	v_pk_mul_f32 v[8:9], v[146:147], s[20:21] op_sel_hi:[1,0]
	v_rcp_f32_e32 v7, v7
	v_mul_f32_e32 v15, 0xbfb8aa3b, v8
	v_exp_f32_e32 v15, v15
	s_addc_u32 s35, s49, s35
	v_mul_f32_e32 v7, v10, v7
	v_mul_f32_e32 v10, v7, v11
	v_add_f32_e32 v7, 1.0, v15
	v_mul_f32_e32 v11, v12, v14
	v_rcp_f32_e32 v12, v7
	s_nop 0
	v_cvt_pk_fp8_f32 v7, v3, v10
	v_mul_f32_e32 v3, v11, v13
	v_mul_f32_e32 v8, v8, v12
	v_mul_f32_e32 v8, v8, v9
	v_cvt_pk_fp8_f32 v7, v3, v8 op_sel:[0,0,1]
	v_mov_b32_e32 v8, v140
	v_mov_b32_e32 v9, v136
	v_pk_mul_f32 v[8:9], v[8:9], s[20:21] op_sel_hi:[1,0]
	v_mov_b32_e32 v136, v141
	v_mul_f32_e32 v3, 0xbfb8aa3b, v8
	v_exp_f32_e32 v3, v3
	s_add_u32 s36, s36, s23
	v_pk_mul_f32 v[12:13], v[136:137], s[20:21] op_sel_hi:[1,0]
	s_addc_u32 s35, s35, s8
	v_mul_f32_e32 v14, 0xbfb8aa3b, v12
	s_add_u32 s36, s36, s51
	v_add_f32_e32 v3, 1.0, v3
	v_exp_f32_e32 v14, v14
	s_addc_u32 s37, s35, 0
	v_rcp_f32_e32 v3, v3
	v_lshl_add_u64 v[0:1], s[36:37], 0, v[178:179]
	v_permlane32_swap_b32_e32 v4, v6
	v_permlane32_swap_b32_e32 v5, v7
	s_nop 1
	v_permlane16_swap_b32_e32 v4, v5
	v_permlane16_swap_b32_e32 v6, v7
	v_mad_i64_i32 v[10:11], s[36:37], v2, s56, v[0:1]
	global_store_dwordx4 v[10:11], v[4:7], off
	v_mul_f32_e32 v3, v8, v3
	v_mul_f32_e32 v3, v3, v9
	v_add_f32_e32 v4, 1.0, v14
	v_rcp_f32_e32 v8, v4
	v_mov_b32_e32 v4, v142
	v_mov_b32_e32 v5, v138
	v_pk_mul_f32 v[4:5], v[4:5], s[20:21] op_sel_hi:[1,0]
	v_mov_b32_e32 v138, v143
	v_mul_f32_e32 v6, 0xbfb8aa3b, v4
	v_exp_f32_e32 v9, v6
	v_pk_mul_f32 v[6:7], v[138:139], s[20:21] op_sel_hi:[1,0]
	v_mul_f32_e32 v8, v12, v8
	v_mul_f32_e32 v10, 0xbfb8aa3b, v6
	v_add_f32_e32 v9, 1.0, v9
	v_rcp_f32_e32 v9, v9
	v_exp_f32_e32 v10, v10
	v_mul_f32_e32 v11, v8, v13
	s_addk_i32 s34, 0x80
	v_mul_f32_e32 v4, v4, v9
	v_mul_f32_e32 v12, v4, v5
	v_mov_b32_e32 v4, v132
	v_mov_b32_e32 v5, v128
	v_pk_mul_f32 v[8:9], v[4:5], s[20:21] op_sel_hi:[1,0]
	v_add_f32_e32 v10, 1.0, v10
	v_mul_f32_e32 v4, 0xbfb8aa3b, v8
	v_exp_f32_e32 v5, v4
	v_rcp_f32_e32 v10, v10
	s_nop 0
	v_cvt_pk_fp8_f32 v4, v3, v11
	v_add_f32_e32 v3, 1.0, v5
	v_rcp_f32_e32 v3, v3
	v_mul_f32_e32 v6, v6, v10
	v_mov_b32_e32 v128, v133
	v_mul_f32_e32 v10, v6, v7
	v_pk_mul_f32 v[6:7], v[128:129], s[20:21] op_sel_hi:[1,0]
	v_mul_f32_e32 v3, v8, v3
	v_mul_f32_e32 v5, 0xbfb8aa3b, v6
	v_exp_f32_e32 v5, v5
	v_mul_f32_e32 v3, v3, v9
	v_mov_b32_e32 v8, v134
	v_mov_b32_e32 v9, v130
	v_pk_mul_f32 v[8:9], v[8:9], s[20:21] op_sel_hi:[1,0]
	v_cvt_pk_fp8_f32 v4, v12, v10 op_sel:[0,0,1]
	v_mul_f32_e32 v10, 0xbfb8aa3b, v8
	v_mov_b32_e32 v130, v135
	v_add_f32_e32 v5, 1.0, v5
	v_exp_f32_e32 v12, v10
	v_pk_mul_f32 v[10:11], v[130:131], s[20:21] op_sel_hi:[1,0]
	v_rcp_f32_e32 v5, v5
	v_mul_f32_e32 v13, 0xbfb8aa3b, v10
	v_exp_f32_e32 v13, v13
	s_add_i32 s30, s30, 0x30000
	v_mul_f32_e32 v5, v6, v5
	v_add_f32_e32 v6, 1.0, v12
	v_rcp_f32_e32 v6, v6
	v_add_f32_e32 v12, 1.0, v13
	v_rcp_f32_e32 v12, v12
	v_mul_f32_e32 v7, v5, v7
	v_mul_f32_e32 v5, v8, v6
	v_mul_f32_e32 v13, v5, v9
	v_mul_f32_e32 v5, v10, v12
	v_mul_f32_e32 v10, v5, v11
	s_nop 0
	v_cvt_pk_fp8_f32 v5, v3, v7
	v_mov_b32_e32 v7, v124
	v_mov_b32_e32 v124, v121
	v_pk_mul_f32 v[8:9], v[124:125], s[20:21] op_sel_hi:[1,0]
	v_mov_b32_e32 v6, v120
	v_mul_f32_e32 v11, 0xbfb8aa3b, v8
	v_pk_mul_f32 v[6:7], v[6:7], s[20:21] op_sel_hi:[1,0]
	v_exp_f32_e32 v11, v11
	v_mul_f32_e32 v3, 0xbfb8aa3b, v6
	v_exp_f32_e32 v3, v3
	v_cvt_pk_fp8_f32 v5, v13, v10 op_sel:[0,0,1]
	v_add_f32_e32 v10, 1.0, v11
	v_rcp_f32_e32 v12, v10
	v_mov_b32_e32 v10, v122
	v_mov_b32_e32 v11, v126
	v_add_f32_e32 v3, 1.0, v3
	v_pk_mul_f32 v[10:11], v[10:11], s[20:21] op_sel_hi:[1,0]
	v_rcp_f32_e32 v3, v3
	v_mul_f32_e32 v13, 0xbfb8aa3b, v10
	v_exp_f32_e32 v13, v13
	v_mov_b32_e32 v126, v123
	v_mul_f32_e32 v3, v6, v3
	v_mul_f32_e32 v3, v3, v7
	v_add_f32_e32 v7, 1.0, v13
	v_mul_f32_e32 v6, v8, v12
	v_rcp_f32_e32 v7, v7
	v_pk_mul_f32 v[12:13], v[126:127], s[20:21] op_sel_hi:[1,0]
	v_mul_f32_e32 v14, v6, v9
	v_mul_f32_e32 v8, 0xbfb8aa3b, v12
	v_exp_f32_e32 v8, v8
	v_mul_f32_e32 v6, v10, v7
	v_mul_f32_e32 v10, v6, v11
	v_mov_b32_e32 v6, v112
	v_mov_b32_e32 v7, v116
	v_add_f32_e32 v11, 1.0, v8
	v_pk_mul_f32 v[8:9], v[6:7], s[20:21] op_sel_hi:[1,0]
	v_rcp_f32_e32 v11, v11
	v_mul_f32_e32 v6, 0xbfb8aa3b, v8
	v_exp_f32_e32 v7, v6
	s_nop 0
	v_cvt_pk_fp8_f32 v6, v3, v14
	v_mov_b32_e32 v116, v113
	v_add_f32_e32 v3, 1.0, v7
	v_rcp_f32_e32 v3, v3
	v_mul_f32_e32 v7, v12, v11
	v_mul_f32_e32 v7, v7, v13
	v_mov_b32_e32 v12, v114
	v_mov_b32_e32 v13, v118
	v_pk_mul_f32 v[12:13], v[12:13], s[20:21] op_sel_hi:[1,0]
	v_cvt_pk_fp8_f32 v6, v10, v7 op_sel:[0,0,1]
	v_mul_f32_e32 v3, v8, v3
	v_pk_mul_f32 v[10:11], v[116:117], s[20:21] op_sel_hi:[1,0]
	v_mul_f32_e32 v8, 0xbfb8aa3b, v12
	v_mul_f32_e32 v7, 0xbfb8aa3b, v10
	v_exp_f32_e32 v8, v8
	v_exp_f32_e32 v7, v7
	v_mov_b32_e32 v118, v115
	v_mul_f32_e32 v3, v3, v9
	v_add_f32_e32 v8, 1.0, v8
	v_add_f32_e32 v7, 1.0, v7
	v_rcp_f32_e32 v14, v8
	v_pk_mul_f32 v[8:9], v[118:119], s[20:21] op_sel_hi:[1,0]
	v_rcp_f32_e32 v7, v7
	v_mul_f32_e32 v15, 0xbfb8aa3b, v8
	v_exp_f32_e32 v15, v15
	v_permlane32_swap_b32_e32 v4, v6
	v_mul_f32_e32 v7, v10, v7
	v_mul_f32_e32 v10, v7, v11
	v_add_f32_e32 v7, 1.0, v15
	v_mul_f32_e32 v11, v12, v14
	v_rcp_f32_e32 v12, v7
	s_nop 0
	v_cvt_pk_fp8_f32 v7, v3, v10
	v_mul_f32_e32 v3, v11, v13
	v_mul_f32_e32 v8, v8, v12
	v_mul_f32_e32 v8, v8, v9
	v_cvt_pk_fp8_f32 v7, v3, v8 op_sel:[0,0,1]
	v_add_u32_e32 v14, 32, v2
	v_mad_i64_i32 v[0:1], s[36:37], v14, s56, v[0:1]
	v_permlane32_swap_b32_e32 v5, v7
	s_nop 1
	v_permlane16_swap_b32_e32 v4, v5
	v_permlane16_swap_b32_e32 v6, v7
	global_store_dwordx4 v[0:1], v[4:7], off
	v_mov_b32_e32 v0, v108
	v_mov_b32_e32 v1, v104
	v_pk_mul_f32 v[4:5], v[0:1], s[20:21] op_sel_hi:[1,0]
	v_mov_b32_e32 v104, v109
	v_mul_f32_e32 v0, 0xbfb8aa3b, v4
	v_exp_f32_e32 v0, v0
	v_pk_mul_f32 v[6:7], v[104:105], s[20:21] op_sel_hi:[1,0]
	s_mul_hi_i32 s34, s34, 0x600
	s_add_u32 s30, s48, s30
	v_add_f32_e32 v0, 1.0, v0
	v_rcp_f32_e32 v3, v0
	v_mul_f32_e32 v0, 0xbfb8aa3b, v6
	v_exp_f32_e32 v8, v0
	s_addc_u32 s34, s49, s34
	v_mul_f32_e32 v3, v4, v3
	v_mul_f32_e32 v3, v3, v5
	v_add_f32_e32 v4, 1.0, v8
	v_rcp_f32_e32 v10, v4
	v_mov_b32_e32 v4, v110
	v_mov_b32_e32 v5, v106
	v_pk_mul_f32 v[4:5], v[4:5], s[20:21] op_sel_hi:[1,0]
	v_mov_b32_e32 v106, v111
	v_mul_f32_e32 v8, 0xbfb8aa3b, v4
	v_exp_f32_e32 v11, v8
	v_mul_f32_e32 v6, v6, v10
	v_pk_mul_f32 v[8:9], v[106:107], s[20:21] op_sel_hi:[1,0]
	s_add_u32 s23, s30, s23
	v_add_f32_e32 v10, 1.0, v11
	v_rcp_f32_e32 v10, v10
	v_mul_f32_e32 v12, 0xbfb8aa3b, v8
	v_exp_f32_e32 v12, v12
	s_addc_u32 s8, s34, s8
	v_mul_f32_e32 v4, v4, v10
	v_mul_f32_e32 v10, v4, v5
	v_mov_b32_e32 v4, v100
	v_mov_b32_e32 v5, v96
	v_add_f32_e32 v11, 1.0, v12
	v_mul_f32_e32 v12, v6, v7
	v_pk_mul_f32 v[6:7], v[4:5], s[20:21] op_sel_hi:[1,0]
	v_rcp_f32_e32 v11, v11
	v_mul_f32_e32 v4, 0xbfb8aa3b, v6
	v_exp_f32_e32 v5, v4
	s_nop 0
	v_cvt_pk_fp8_f32 v4, v3, v12
	v_mul_f32_e32 v8, v8, v11
	v_add_f32_e32 v3, 1.0, v5
	v_rcp_f32_e32 v3, v3
	v_mov_b32_e32 v96, v101
	v_mul_f32_e32 v11, v8, v9
	v_pk_mul_f32 v[8:9], v[96:97], s[20:21] op_sel_hi:[1,0]
	v_mul_f32_e32 v3, v6, v3
	v_mul_f32_e32 v5, 0xbfb8aa3b, v8
	v_exp_f32_e32 v5, v5
	v_mul_f32_e32 v3, v3, v7
	v_mov_b32_e32 v6, v102
	v_mov_b32_e32 v7, v98
	v_pk_mul_f32 v[6:7], v[6:7], s[20:21] op_sel_hi:[1,0]
	v_cvt_pk_fp8_f32 v4, v10, v11 op_sel:[0,0,1]
	v_mul_f32_e32 v10, 0xbfb8aa3b, v6
	v_mov_b32_e32 v98, v103
	v_add_f32_e32 v5, 1.0, v5
	v_exp_f32_e32 v12, v10
	v_pk_mul_f32 v[10:11], v[98:99], s[20:21] op_sel_hi:[1,0]
	v_rcp_f32_e32 v5, v5
	v_mul_f32_e32 v13, 0xbfb8aa3b, v10
	v_exp_f32_e32 v13, v13
	s_add_u32 s34, s23, s51
	v_mul_f32_e32 v5, v8, v5
	v_add_f32_e32 v8, 1.0, v12
	v_rcp_f32_e32 v8, v8
	v_add_f32_e32 v12, 1.0, v13
	v_rcp_f32_e32 v12, v12
	v_mul_f32_e32 v9, v5, v9
	v_mul_f32_e32 v5, v6, v8
	v_mul_f32_e32 v13, v5, v7
	v_mul_f32_e32 v5, v10, v12
	v_mul_f32_e32 v10, v5, v11
	s_nop 0
	v_mov_b32_e32 v7, v88
	v_mov_b32_e32 v88, v93
	v_cvt_pk_fp8_f32 v5, v3, v9
	v_pk_mul_f32 v[8:9], v[88:89], s[20:21] op_sel_hi:[1,0]
	v_mov_b32_e32 v6, v92
	v_mul_f32_e32 v11, 0xbfb8aa3b, v8
	v_pk_mul_f32 v[6:7], v[6:7], s[20:21] op_sel_hi:[1,0]
	v_exp_f32_e32 v11, v11
	v_mul_f32_e32 v3, 0xbfb8aa3b, v6
	v_exp_f32_e32 v3, v3
	v_cvt_pk_fp8_f32 v5, v13, v10 op_sel:[0,0,1]
	v_add_f32_e32 v10, 1.0, v11
	v_rcp_f32_e32 v12, v10
	v_mov_b32_e32 v10, v94
	v_mov_b32_e32 v11, v90
	v_add_f32_e32 v3, 1.0, v3
	v_pk_mul_f32 v[10:11], v[10:11], s[20:21] op_sel_hi:[1,0]
	v_rcp_f32_e32 v3, v3
	v_mul_f32_e32 v13, 0xbfb8aa3b, v10
	v_exp_f32_e32 v13, v13
	v_mov_b32_e32 v90, v95
	v_mul_f32_e32 v3, v6, v3
	v_mul_f32_e32 v3, v3, v7
	v_add_f32_e32 v7, 1.0, v13
	v_mul_f32_e32 v6, v8, v12
	v_rcp_f32_e32 v7, v7
	v_pk_mul_f32 v[12:13], v[90:91], s[20:21] op_sel_hi:[1,0]
	v_mul_f32_e32 v15, v6, v9
	v_mul_f32_e32 v8, 0xbfb8aa3b, v12
	v_exp_f32_e32 v8, v8
	v_mul_f32_e32 v6, v10, v7
	v_mul_f32_e32 v10, v6, v11
	v_mov_b32_e32 v6, v84
	v_mov_b32_e32 v7, v80
	v_add_f32_e32 v11, 1.0, v8
	v_pk_mul_f32 v[8:9], v[6:7], s[20:21] op_sel_hi:[1,0]
	v_rcp_f32_e32 v11, v11
	v_mul_f32_e32 v6, 0xbfb8aa3b, v8
	v_exp_f32_e32 v7, v6
	s_nop 0
	v_cvt_pk_fp8_f32 v6, v3, v15
	v_mov_b32_e32 v80, v85
	v_add_f32_e32 v3, 1.0, v7
	v_rcp_f32_e32 v3, v3
	v_mul_f32_e32 v7, v12, v11
	v_mul_f32_e32 v7, v7, v13
	v_mov_b32_e32 v12, v86
	v_mov_b32_e32 v13, v82
	v_pk_mul_f32 v[12:13], v[12:13], s[20:21] op_sel_hi:[1,0]
	v_cvt_pk_fp8_f32 v6, v10, v7 op_sel:[0,0,1]
	v_mul_f32_e32 v3, v8, v3
	v_pk_mul_f32 v[10:11], v[80:81], s[20:21] op_sel_hi:[1,0]
	v_mul_f32_e32 v8, 0xbfb8aa3b, v12
	v_mul_f32_e32 v7, 0xbfb8aa3b, v10
	v_exp_f32_e32 v8, v8
	v_exp_f32_e32 v7, v7
	v_mov_b32_e32 v82, v87
	v_mul_f32_e32 v3, v3, v9
	v_add_f32_e32 v8, 1.0, v8
	v_add_f32_e32 v7, 1.0, v7
	v_rcp_f32_e32 v15, v8
	v_pk_mul_f32 v[8:9], v[82:83], s[20:21] op_sel_hi:[1,0]
	v_rcp_f32_e32 v7, v7
	v_mul_f32_e32 v16, 0xbfb8aa3b, v8
	v_exp_f32_e32 v16, v16
	s_addc_u32 s35, s8, 0
	v_mul_f32_e32 v7, v10, v7
	v_mul_f32_e32 v10, v7, v11
	v_add_f32_e32 v7, 1.0, v16
	v_mul_f32_e32 v11, v12, v15
	v_rcp_f32_e32 v12, v7
	s_nop 0
	v_cvt_pk_fp8_f32 v7, v3, v10
	v_mul_f32_e32 v3, v11, v13
	v_mul_f32_e32 v8, v8, v12
	v_mul_f32_e32 v8, v8, v9
	v_cvt_pk_fp8_f32 v7, v3, v8 op_sel:[0,0,1]
	v_mov_b32_e32 v8, v76
	v_mov_b32_e32 v9, v72
	v_pk_mul_f32 v[8:9], v[8:9], s[20:21] op_sel_hi:[1,0]
	v_mov_b32_e32 v72, v77
	v_mul_f32_e32 v3, 0xbfb8aa3b, v8
	v_exp_f32_e32 v10, v3
	v_lshl_add_u64 v[0:1], s[34:35], 0, v[178:179]
	v_permlane32_swap_b32_e32 v4, v6
	v_add_f32_e32 v10, 1.0, v10
	v_rcp_f32_e32 v12, v10
	v_pk_mul_f32 v[10:11], v[72:73], s[20:21] op_sel_hi:[1,0]
	v_permlane32_swap_b32_e32 v5, v7
	v_mul_f32_e32 v13, 0xbfb8aa3b, v10
	v_exp_f32_e32 v13, v13
	v_permlane16_swap_b32_e32 v4, v5
	v_permlane16_swap_b32_e32 v6, v7
	v_mad_i64_i32 v[2:3], s[34:35], v2, s56, v[0:1]
	global_store_dwordx4 v[2:3], v[4:7], off
	v_mul_f32_e32 v2, v8, v12
	v_mul_f32_e32 v8, v2, v9
	v_add_f32_e32 v2, 1.0, v13
	v_rcp_f32_e32 v6, v2
	v_mov_b32_e32 v2, v78
	v_mov_b32_e32 v3, v74
	v_pk_mul_f32 v[2:3], v[2:3], s[20:21] op_sel_hi:[1,0]
	v_mov_b32_e32 v74, v79
	v_mul_f32_e32 v4, 0xbfb8aa3b, v2
	v_exp_f32_e32 v7, v4
	v_pk_mul_f32 v[4:5], v[74:75], s[20:21] op_sel_hi:[1,0]
	v_mul_f32_e32 v6, v10, v6
	v_mul_f32_e32 v9, 0xbfb8aa3b, v4
	v_add_f32_e32 v7, 1.0, v7
	v_rcp_f32_e32 v7, v7
	v_exp_f32_e32 v9, v9
	v_mul_f32_e32 v10, v6, v11
	v_mad_i64_i32 v[0:1], s[34:35], v14, s56, v[0:1]
	v_mul_f32_e32 v2, v2, v7
	v_mul_f32_e32 v11, v2, v3
	v_mov_b32_e32 v2, v68
	v_mov_b32_e32 v3, v64
	v_pk_mul_f32 v[6:7], v[2:3], s[20:21] op_sel_hi:[1,0]
	v_add_f32_e32 v9, 1.0, v9
	v_mul_f32_e32 v2, 0xbfb8aa3b, v6
	v_exp_f32_e32 v3, v2
	v_rcp_f32_e32 v9, v9
	v_mov_b32_e32 v64, v69
	s_nop 0
	v_add_f32_e32 v3, 1.0, v3
	v_mul_f32_e32 v4, v4, v9
	v_rcp_f32_e32 v3, v3
	v_mul_f32_e32 v9, v4, v5
	v_pk_mul_f32 v[4:5], v[64:65], s[20:21] op_sel_hi:[1,0]
	v_cvt_pk_fp8_f32 v2, v8, v10
	v_mul_f32_e32 v8, 0xbfb8aa3b, v4
	v_exp_f32_e32 v8, v8
	v_mul_f32_e32 v3, v6, v3
	v_mul_f32_e32 v10, v3, v7
	v_mov_b32_e32 v6, v70
	v_mov_b32_e32 v7, v66
	v_pk_mul_f32 v[6:7], v[6:7], s[20:21] op_sel_hi:[1,0]
	v_add_f32_e32 v3, 1.0, v8
	v_mul_f32_e32 v8, 0xbfb8aa3b, v6
	v_mov_b32_e32 v66, v71
	v_cvt_pk_fp8_f32 v2, v11, v9 op_sel:[0,0,1]
	v_exp_f32_e32 v11, v8
	v_pk_mul_f32 v[8:9], v[66:67], s[20:21] op_sel_hi:[1,0]
	v_rcp_f32_e32 v3, v3
	v_mul_f32_e32 v12, 0xbfb8aa3b, v8
	v_exp_f32_e32 v12, v12
	s_and_b64 vcc, exec, s[24:25]
	v_mul_f32_e32 v3, v4, v3
	v_add_f32_e32 v4, 1.0, v11
	v_rcp_f32_e32 v4, v4
	v_add_f32_e32 v11, 1.0, v12
	v_rcp_f32_e32 v11, v11
	v_mul_f32_e32 v5, v3, v5
	v_mul_f32_e32 v3, v6, v4
	v_mul_f32_e32 v12, v3, v7
	v_mul_f32_e32 v3, v8, v11
	v_mul_f32_e32 v8, v3, v9
	s_nop 0
	v_cvt_pk_fp8_f32 v3, v10, v5
	v_mov_b32_e32 v4, v60
	v_mov_b32_e32 v5, v56
	v_pk_mul_f32 v[4:5], v[4:5], s[20:21] op_sel_hi:[1,0]
	v_mov_b32_e32 v56, v61
	v_mul_f32_e32 v6, 0xbfb8aa3b, v4
	v_exp_f32_e32 v9, v6
	v_pk_mul_f32 v[6:7], v[56:57], s[20:21] op_sel_hi:[1,0]
	v_cvt_pk_fp8_f32 v3, v12, v8 op_sel:[0,0,1]
	v_mul_f32_e32 v10, 0xbfb8aa3b, v6
	v_exp_f32_e32 v10, v10
	v_add_f32_e32 v8, 1.0, v9
	v_rcp_f32_e32 v11, v8
	v_mov_b32_e32 v9, v58
	v_add_f32_e32 v8, 1.0, v10
	v_rcp_f32_e32 v10, v8
	v_mov_b32_e32 v8, v62
	v_pk_mul_f32 v[8:9], v[8:9], s[20:21] op_sel_hi:[1,0]
	v_mul_f32_e32 v4, v4, v11
	v_mul_f32_e32 v12, 0xbfb8aa3b, v8
	v_exp_f32_e32 v12, v12
	v_mul_f32_e32 v13, v4, v5
	v_mov_b32_e32 v58, v63
	v_mul_f32_e32 v4, v6, v10
	v_add_f32_e32 v5, 1.0, v12
	v_rcp_f32_e32 v5, v5
	v_pk_mul_f32 v[10:11], v[58:59], s[20:21] op_sel_hi:[1,0]
	v_mul_f32_e32 v12, v4, v7
	v_mul_f32_e32 v6, 0xbfb8aa3b, v10
	v_exp_f32_e32 v6, v6
	v_mul_f32_e32 v4, v8, v5
	v_mul_f32_e32 v8, v4, v9
	v_mov_b32_e32 v4, v52
	v_mov_b32_e32 v5, v48
	v_add_f32_e32 v9, 1.0, v6
	v_pk_mul_f32 v[6:7], v[4:5], s[20:21] op_sel_hi:[1,0]
	v_rcp_f32_e32 v9, v9
	v_mul_f32_e32 v4, 0xbfb8aa3b, v6
	v_exp_f32_e32 v5, v4
	s_nop 0
	v_cvt_pk_fp8_f32 v4, v13, v12
	v_mul_f32_e32 v9, v10, v9
	v_add_f32_e32 v5, 1.0, v5
	v_rcp_f32_e32 v5, v5
	v_mul_f32_e32 v9, v9, v11
	v_mov_b32_e32 v48, v53
	v_mov_b32_e32 v10, v54
	v_mov_b32_e32 v11, v50
	v_cvt_pk_fp8_f32 v4, v8, v9 op_sel:[0,0,1]
	v_pk_mul_f32 v[8:9], v[48:49], s[20:21] op_sel_hi:[1,0]
	v_pk_mul_f32 v[10:11], v[10:11], s[20:21] op_sel_hi:[1,0]
	v_mul_f32_e32 v5, v6, v5
	v_mul_f32_e32 v6, 0xbfb8aa3b, v8
	v_mul_f32_e32 v12, 0xbfb8aa3b, v10
	v_exp_f32_e32 v6, v6
	v_exp_f32_e32 v12, v12
	v_mul_f32_e32 v13, v5, v7
	v_mov_b32_e32 v50, v55
	v_add_f32_e32 v5, 1.0, v6
	v_add_f32_e32 v6, 1.0, v12
	v_rcp_f32_e32 v12, v6
	v_pk_mul_f32 v[6:7], v[50:51], s[20:21] op_sel_hi:[1,0]
	v_rcp_f32_e32 v5, v5
	v_mul_f32_e32 v15, 0xbfb8aa3b, v6
	v_exp_f32_e32 v15, v15
	v_permlane32_swap_b32_e32 v2, v4
	v_mul_f32_e32 v5, v8, v5
	v_mul_f32_e32 v8, v5, v9
	v_add_f32_e32 v5, 1.0, v15
	v_mul_f32_e32 v9, v10, v12
	v_rcp_f32_e32 v10, v5
	s_nop 0
	v_cvt_pk_fp8_f32 v5, v13, v8
	v_mul_f32_e32 v8, v9, v11
	v_mul_f32_e32 v6, v6, v10
	v_mul_f32_e32 v6, v6, v7
	v_cvt_pk_fp8_f32 v5, v8, v6 op_sel:[0,0,1]
	s_mov_b32 s59, s58
	s_mov_b32 s30, s22
	s_mov_b64 s[36:37], s[26:27]
	v_permlane32_swap_b32_e32 v3, v5
	s_nop 1
	v_permlane16_swap_b32_e32 v2, v3
	v_permlane16_swap_b32_e32 v4, v5
	global_store_dwordx4 v[0:1], v[2:5], off
	s_cbranch_vccnz .LBB0_1947

.LBB0_2081:
	s_waitcnt vmcnt(31)
	v_mov_b32_e32 v128, v0
	s_waitcnt vmcnt(30)
	v_mov_b32_e32 v129, v4
	v_pk_mul_f32 v[128:129], v[128:129], s[34:35] op_sel_hi:[1,0]
	s_nop 0
	v_cvt_pk_fp8_f32 v130, v128, v129
	s_waitcnt vmcnt(29)
	v_mov_b32_e32 v128, v8
	s_waitcnt vmcnt(28)
	v_mov_b32_e32 v129, v12
	v_pk_mul_f32 v[128:129], v[128:129], s[34:35] op_sel_hi:[1,0]
	s_nop 0
	v_cvt_pk_fp8_f32 v130, v128, v129 op_sel:[0,0,1]
	v_mov_b32_e32 v128, v1
	v_mov_b32_e32 v129, v5
	v_pk_mul_f32 v[128:129], v[128:129], s[34:35] op_sel_hi:[1,0]
	s_nop 0
	v_cvt_pk_fp8_f32 v131, v128, v129
	v_mov_b32_e32 v128, v9
	v_mov_b32_e32 v129, v13
	v_pk_mul_f32 v[128:129], v[128:129], s[34:35] op_sel_hi:[1,0]
	s_nop 0
	v_cvt_pk_fp8_f32 v131, v128, v129 op_sel:[0,0,1]
	v_mov_b32_e32 v128, v2
	v_mov_b32_e32 v129, v6
	v_pk_mul_f32 v[128:129], v[128:129], s[34:35] op_sel_hi:[1,0]
	v_mov_b32_e32 v139, v135
	v_cvt_pk_fp8_f32 v134, v128, v129
	v_mov_b32_e32 v128, v10
	v_mov_b32_e32 v129, v14
	v_pk_mul_f32 v[128:129], v[128:129], s[34:35] op_sel_hi:[1,0]
	v_mov_b32_e32 v146, v135
	v_cvt_pk_fp8_f32 v134, v128, v129 op_sel:[0,0,1]
	v_mov_b32_e32 v128, v3
	v_mov_b32_e32 v129, v7
	v_pk_mul_f32 v[128:129], v[128:129], s[34:35] op_sel_hi:[1,0]
	v_add_u32_e32 v145, 0x4000, v143
	v_cvt_pk_fp8_f32 v138, v128, v129
	v_mov_b32_e32 v128, v11
	v_mov_b32_e32 v129, v15
	v_pk_mul_f32 v[128:129], v[128:129], s[34:35] op_sel_hi:[1,0]
	v_add_u32_e32 v144, 0x8400, v143
	v_cvt_pk_fp8_f32 v138, v128, v129 op_sel:[0,0,1]
	s_waitcnt vmcnt(27)
	v_mov_b32_e32 v128, v16
	s_waitcnt vmcnt(26)
	v_mov_b32_e32 v129, v20
	ds_write2_b32 v143, v130, v131 offset1:33
	ds_write2_b32 v143, v134, v138 offset0:66 offset1:99
	v_pk_mul_f32 v[128:129], v[128:129], s[34:35] op_sel_hi:[1,0]
	s_nop 0
	v_cvt_pk_fp8_f32 v130, v128, v129
	s_waitcnt vmcnt(25)
	v_mov_b32_e32 v128, v24
	s_waitcnt vmcnt(24)
	v_mov_b32_e32 v129, v28
	v_pk_mul_f32 v[128:129], v[128:129], s[34:35] op_sel_hi:[1,0]
	s_nop 0
	v_cvt_pk_fp8_f32 v130, v128, v129 op_sel:[0,0,1]
	v_mov_b32_e32 v128, v17
	v_mov_b32_e32 v129, v21
	v_pk_mul_f32 v[128:129], v[128:129], s[34:35] op_sel_hi:[1,0]
	s_nop 0
	v_cvt_pk_fp8_f32 v131, v128, v129
	v_mov_b32_e32 v128, v25
	v_mov_b32_e32 v129, v29
	v_pk_mul_f32 v[128:129], v[128:129], s[34:35] op_sel_hi:[1,0]
	s_nop 0
	v_cvt_pk_fp8_f32 v131, v128, v129 op_sel:[0,0,1]
	v_mov_b32_e32 v128, v18
	v_mov_b32_e32 v129, v22
	v_pk_mul_f32 v[128:129], v[128:129], s[34:35] op_sel_hi:[1,0]
	v_mov_b32_e32 v147, v135
	v_cvt_pk_fp8_f32 v134, v128, v129
	v_mov_b32_e32 v128, v26
	v_mov_b32_e32 v129, v30
	v_pk_mul_f32 v[128:129], v[128:129], s[34:35] op_sel_hi:[1,0]
	s_cmp_lt_i32 s78, 2
	v_cvt_pk_fp8_f32 v134, v128, v129 op_sel:[0,0,1]
	v_mov_b32_e32 v128, v19
	v_mov_b32_e32 v129, v23
	v_pk_mul_f32 v[128:129], v[128:129], s[34:35] op_sel_hi:[1,0]
	s_nop 0
	v_cvt_pk_fp8_f32 v138, v128, v129
	v_mov_b32_e32 v128, v27
	v_mov_b32_e32 v129, v31
	v_pk_mul_f32 v[128:129], v[128:129], s[34:35] op_sel_hi:[1,0]
	s_nop 0
	v_cvt_pk_fp8_f32 v138, v128, v129 op_sel:[0,0,1]
	s_waitcnt vmcnt(23)
	v_mov_b32_e32 v128, v48
	s_waitcnt vmcnt(22)
	v_mov_b32_e32 v129, v52
	v_pk_mul_f32 v[128:129], v[128:129], s[34:35] op_sel_hi:[1,0]
	ds_write2_b32 v145, v130, v131 offset0:128 offset1:161
	ds_write2_b32 v145, v134, v138 offset0:194 offset1:227
	v_cvt_pk_fp8_f32 v139, v128, v129
	s_waitcnt vmcnt(21)
	v_mov_b32_e32 v128, v56
	s_waitcnt vmcnt(20)
	v_mov_b32_e32 v129, v60
	v_pk_mul_f32 v[128:129], v[128:129], s[34:35] op_sel_hi:[1,0]
	s_nop 0
	v_cvt_pk_fp8_f32 v139, v128, v129 op_sel:[0,0,1]
	v_mov_b32_e32 v128, v49
	v_mov_b32_e32 v129, v53
	v_pk_mul_f32 v[128:129], v[128:129], s[34:35] op_sel_hi:[1,0]
	s_nop 0
	v_cvt_pk_fp8_f32 v146, v128, v129
	v_mov_b32_e32 v128, v57
	v_mov_b32_e32 v129, v61
	v_pk_mul_f32 v[128:129], v[128:129], s[34:35] op_sel_hi:[1,0]
	s_nop 0
	v_cvt_pk_fp8_f32 v146, v128, v129 op_sel:[0,0,1]
	v_mov_b32_e32 v128, v50
	v_mov_b32_e32 v129, v54
	v_pk_mul_f32 v[128:129], v[128:129], s[34:35] op_sel_hi:[1,0]
	s_nop 0
	v_cvt_pk_fp8_f32 v130, v128, v129
	v_mov_b32_e32 v128, v58
	v_mov_b32_e32 v129, v62
	v_pk_mul_f32 v[128:129], v[128:129], s[34:35] op_sel_hi:[1,0]
	ds_write2_b32 v144, v139, v146 offset1:33
	v_cvt_pk_fp8_f32 v130, v128, v129 op_sel:[0,0,1]
	v_mov_b32_e32 v128, v51
	v_mov_b32_e32 v129, v55
	v_pk_mul_f32 v[128:129], v[128:129], s[34:35] op_sel_hi:[1,0]
	s_nop 0
	v_cvt_pk_fp8_f32 v131, v128, v129
	v_mov_b32_e32 v128, v59
	v_mov_b32_e32 v129, v63
	v_pk_mul_f32 v[128:129], v[128:129], s[34:35] op_sel_hi:[1,0]
	v_add_u32_e32 v146, 0xc400, v143
	v_cvt_pk_fp8_f32 v131, v128, v129 op_sel:[0,0,1]
	s_waitcnt vmcnt(19)
	v_mov_b32_e32 v128, v96
	s_waitcnt vmcnt(18)
	v_mov_b32_e32 v129, v100
	v_pk_mul_f32 v[128:129], v[128:129], s[34:35] op_sel_hi:[1,0]
	ds_write2_b32 v144, v130, v131 offset0:66 offset1:99
	v_cvt_pk_fp8_f32 v134, v128, v129
	s_waitcnt vmcnt(17)
	v_mov_b32_e32 v128, v104
	s_waitcnt vmcnt(16)
	v_mov_b32_e32 v129, v108
	v_pk_mul_f32 v[128:129], v[128:129], s[34:35] op_sel_hi:[1,0]
	s_nop 0
	v_cvt_pk_fp8_f32 v134, v128, v129 op_sel:[0,0,1]
	v_mov_b32_e32 v128, v97
	v_mov_b32_e32 v129, v101
	v_pk_mul_f32 v[128:129], v[128:129], s[34:35] op_sel_hi:[1,0]
	s_nop 0
	v_cvt_pk_fp8_f32 v138, v128, v129
	v_mov_b32_e32 v128, v105
	v_mov_b32_e32 v129, v109
	v_pk_mul_f32 v[128:129], v[128:129], s[34:35] op_sel_hi:[1,0]
	s_nop 0
	v_cvt_pk_fp8_f32 v138, v128, v129 op_sel:[0,0,1]
	v_mov_b32_e32 v128, v98
	v_mov_b32_e32 v129, v102
	v_pk_mul_f32 v[128:129], v[128:129], s[34:35] op_sel_hi:[1,0]
	s_nop 0
	v_cvt_pk_fp8_f32 v139, v128, v129
	v_mov_b32_e32 v128, v106
	v_mov_b32_e32 v129, v110
	v_pk_mul_f32 v[128:129], v[128:129], s[34:35] op_sel_hi:[1,0]
	s_nop 0
	v_cvt_pk_fp8_f32 v139, v128, v129 op_sel:[0,0,1]
	v_mov_b32_e32 v128, v99
	v_mov_b32_e32 v129, v103
	v_pk_mul_f32 v[128:129], v[128:129], s[34:35] op_sel_hi:[1,0]
	s_nop 0
	v_cvt_pk_fp8_f32 v147, v128, v129
	v_mov_b32_e32 v128, v107
	v_mov_b32_e32 v129, v111
	v_pk_mul_f32 v[128:129], v[128:129], s[34:35] op_sel_hi:[1,0]
	s_nop 0
	v_cvt_pk_fp8_f32 v147, v128, v129 op_sel:[0,0,1]
	ds_write2_b32 v146, v134, v138 offset0:128 offset1:161
	ds_write2_b32 v146, v139, v147 offset0:194 offset1:227
	s_waitcnt lgkmcnt(0)
	s_barrier
	ds_read2_b32 v[128:129], v142 offset1:1
	ds_read2_b32 v[130:131], v142 offset0:2 offset1:3
	v_lshl_add_u32 v134, s77, 6, v140
	s_cbranch_scc1 .LBB0_2087
	s_cmp_gt_i32 s78, 2
	s_cbranch_scc0 .LBB0_2088
	s_cmp_eq_u32 s78, 3
	s_mov_b64 s[68:69], -1
	s_cbranch_scc0 .LBB0_2085
	v_lshlrev_b32_e32 v138, 1, v134
	v_and_b32_e32 v139, 0x7f, v134
	s_movk_i32 s11, 0xff00
	v_and_or_b32 v138, v138, s11, v139
	s_mov_b64 s[68:69], 0

.Lcvw_c3:
	v_mov_b32_e32 v128, v36
	v_mov_b32_e32 v129, v32
	v_pk_mul_f32 v[128:129], v[128:129], s[34:35] op_sel_hi:[1,0]
	s_nop 0
	v_cvt_pk_fp8_f32 v130, v128, v129
	v_mov_b32_e32 v128, v44
	v_mov_b32_e32 v129, v40
	v_pk_mul_f32 v[128:129], v[128:129], s[34:35] op_sel_hi:[1,0]
	s_nop 0
	v_cvt_pk_fp8_f32 v130, v128, v129 op_sel:[0,0,1]
	v_mov_b32_e32 v128, v37
	v_mov_b32_e32 v129, v33
	v_pk_mul_f32 v[128:129], v[128:129], s[34:35] op_sel_hi:[1,0]
	s_nop 0
	v_cvt_pk_fp8_f32 v131, v128, v129
	v_mov_b32_e32 v128, v45
	v_mov_b32_e32 v129, v41
	v_pk_mul_f32 v[128:129], v[128:129], s[34:35] op_sel_hi:[1,0]
	s_nop 0
	v_cvt_pk_fp8_f32 v131, v128, v129 op_sel:[0,0,1]
	v_mov_b32_e32 v128, v38
	v_mov_b32_e32 v129, v34
	v_pk_mul_f32 v[128:129], v[128:129], s[34:35] op_sel_hi:[1,0]
	s_nop 0
	v_cvt_pk_fp8_f32 v134, v128, v129
	v_mov_b32_e32 v128, v46
	v_mov_b32_e32 v129, v42
	v_pk_mul_f32 v[128:129], v[128:129], s[34:35] op_sel_hi:[1,0]
	s_nop 0
	v_cvt_pk_fp8_f32 v134, v128, v129 op_sel:[0,0,1]
	v_mov_b32_e32 v128, v39
	v_mov_b32_e32 v129, v35
	v_pk_mul_f32 v[128:129], v[128:129], s[34:35] op_sel_hi:[1,0]
	s_nop 0
	v_cvt_pk_fp8_f32 v138, v128, v129
	v_mov_b32_e32 v128, v47
	v_mov_b32_e32 v129, v43
	v_pk_mul_f32 v[128:129], v[128:129], s[34:35] op_sel_hi:[1,0]
	s_nop 0
	v_cvt_pk_fp8_f32 v138, v128, v129 op_sel:[0,0,1]
	v_mov_b32_e32 v128, v68
	v_mov_b32_e32 v129, v64
	v_pk_mul_f32 v[128:129], v[128:129], s[34:35] op_sel_hi:[1,0]
	s_cmp_lt_i32 s26, 2
	v_cvt_pk_fp8_f32 v139, v128, v129
	v_mov_b32_e32 v128, v76
	v_mov_b32_e32 v129, v72
	v_pk_mul_f32 v[128:129], v[128:129], s[34:35] op_sel_hi:[1,0]
	s_nop 0
	v_cvt_pk_fp8_f32 v139, v128, v129 op_sel:[0,0,1]
	v_mov_b32_e32 v128, v69
	v_mov_b32_e32 v129, v65
	v_pk_mul_f32 v[128:129], v[128:129], s[34:35] op_sel_hi:[1,0]
	s_nop 0
	v_cvt_pk_fp8_f32 v153, v128, v129
	v_mov_b32_e32 v128, v77
	v_mov_b32_e32 v129, v73
	v_pk_mul_f32 v[128:129], v[128:129], s[34:35] op_sel_hi:[1,0]
	s_nop 0
	v_cvt_pk_fp8_f32 v153, v128, v129 op_sel:[0,0,1]
	v_mov_b32_e32 v128, v70
	v_mov_b32_e32 v129, v66
	v_pk_mul_f32 v[128:129], v[128:129], s[34:35] op_sel_hi:[1,0]
	s_nop 0
	v_cvt_pk_fp8_f32 v154, v128, v129
	v_mov_b32_e32 v128, v78
	v_mov_b32_e32 v129, v74
	v_pk_mul_f32 v[128:129], v[128:129], s[34:35] op_sel_hi:[1,0]
	s_nop 0
	v_cvt_pk_fp8_f32 v154, v128, v129 op_sel:[0,0,1]
	v_mov_b32_e32 v128, v71
	v_mov_b32_e32 v129, v67
	v_pk_mul_f32 v[128:129], v[128:129], s[34:35] op_sel_hi:[1,0]
	s_nop 0
	v_cvt_pk_fp8_f32 v155, v128, v129
	v_mov_b32_e32 v128, v79
	v_mov_b32_e32 v129, v75
	v_pk_mul_f32 v[128:129], v[128:129], s[34:35] op_sel_hi:[1,0]
	s_nop 0
	v_cvt_pk_fp8_f32 v155, v128, v129 op_sel:[0,0,1]
	v_mov_b32_e32 v128, v84
	v_mov_b32_e32 v129, v80
	ds_write2_b32 v143, v130, v131 offset1:33
	ds_write2_b32 v143, v134, v138 offset0:66 offset1:99
	ds_write2_b32 v145, v139, v153 offset0:128 offset1:161
	ds_write2_b32 v145, v154, v155 offset0:194 offset1:227
	v_pk_mul_f32 v[128:129], v[128:129], s[34:35] op_sel_hi:[1,0]
	s_nop 0
	v_cvt_pk_fp8_f32 v130, v128, v129
	v_mov_b32_e32 v128, v92
	v_mov_b32_e32 v129, v88
	v_pk_mul_f32 v[128:129], v[128:129], s[34:35] op_sel_hi:[1,0]
	s_nop 0
	v_cvt_pk_fp8_f32 v130, v128, v129 op_sel:[0,0,1]
	v_mov_b32_e32 v128, v85
	v_mov_b32_e32 v129, v81
	v_pk_mul_f32 v[128:129], v[128:129], s[34:35] op_sel_hi:[1,0]
	s_nop 0
	v_cvt_pk_fp8_f32 v131, v128, v129
	v_mov_b32_e32 v128, v93
	v_mov_b32_e32 v129, v89
	v_pk_mul_f32 v[128:129], v[128:129], s[34:35] op_sel_hi:[1,0]
	s_nop 0
	v_cvt_pk_fp8_f32 v131, v128, v129 op_sel:[0,0,1]
	v_mov_b32_e32 v128, v86
	v_mov_b32_e32 v129, v82
	v_pk_mul_f32 v[128:129], v[128:129], s[34:35] op_sel_hi:[1,0]
	s_nop 0
	v_cvt_pk_fp8_f32 v134, v128, v129
	v_mov_b32_e32 v128, v94
	v_mov_b32_e32 v129, v90
	v_pk_mul_f32 v[128:129], v[128:129], s[34:35] op_sel_hi:[1,0]
	s_nop 0
	v_cvt_pk_fp8_f32 v134, v128, v129 op_sel:[0,0,1]
	v_mov_b32_e32 v128, v87
	v_mov_b32_e32 v129, v83
	v_pk_mul_f32 v[128:129], v[128:129], s[34:35] op_sel_hi:[1,0]
	s_nop 0
	v_cvt_pk_fp8_f32 v138, v128, v129
	v_mov_b32_e32 v128, v95
	v_mov_b32_e32 v129, v91
	v_pk_mul_f32 v[128:129], v[128:129], s[34:35] op_sel_hi:[1,0]
	s_nop 0
	v_cvt_pk_fp8_f32 v138, v128, v129 op_sel:[0,0,1]
	v_mov_b32_e32 v128, v116
	v_mov_b32_e32 v129, v112
	v_pk_mul_f32 v[128:129], v[128:129], s[34:35] op_sel_hi:[1,0]
	s_nop 0
	v_cvt_pk_fp8_f32 v139, v128, v129
	v_mov_b32_e32 v128, v124
	v_mov_b32_e32 v129, v120
	v_pk_mul_f32 v[128:129], v[128:129], s[34:35] op_sel_hi:[1,0]
	s_nop 0
	v_cvt_pk_fp8_f32 v139, v128, v129 op_sel:[0,0,1]
	v_mov_b32_e32 v128, v117
	v_mov_b32_e32 v129, v113
	v_pk_mul_f32 v[128:129], v[128:129], s[34:35] op_sel_hi:[1,0]
	s_nop 0
	v_cvt_pk_fp8_f32 v145, v128, v129
	v_mov_b32_e32 v128, v125
	v_mov_b32_e32 v129, v121
	v_pk_mul_f32 v[128:129], v[128:129], s[34:35] op_sel_hi:[1,0]
	s_nop 0
	v_cvt_pk_fp8_f32 v145, v128, v129 op_sel:[0,0,1]
	v_mov_b32_e32 v128, v118
	v_mov_b32_e32 v129, v114
	v_pk_mul_f32 v[128:129], v[128:129], s[34:35] op_sel_hi:[1,0]
	s_nop 0
	v_cvt_pk_fp8_f32 v153, v128, v129
	v_mov_b32_e32 v128, v126
	v_mov_b32_e32 v129, v122
	v_pk_mul_f32 v[128:129], v[128:129], s[34:35] op_sel_hi:[1,0]
	s_nop 0
	v_cvt_pk_fp8_f32 v153, v128, v129 op_sel:[0,0,1]
	v_mov_b32_e32 v128, v119
	v_mov_b32_e32 v129, v115
	v_pk_mul_f32 v[128:129], v[128:129], s[34:35] op_sel_hi:[1,0]
	s_nop 0
	v_cvt_pk_fp8_f32 v154, v128, v129
	v_mov_b32_e32 v128, v127
	v_mov_b32_e32 v129, v123
	v_pk_mul_f32 v[128:129], v[128:129], s[34:35] op_sel_hi:[1,0]
	s_nop 0
	v_cvt_pk_fp8_f32 v154, v128, v129 op_sel:[0,0,1]
	ds_write2_b32 v144, v130, v131 offset1:33
	ds_write2_b32 v144, v134, v138 offset0:66 offset1:99
	ds_write2_b32 v146, v139, v145 offset0:128 offset1:161
	ds_write2_b32 v146, v153, v154 offset0:194 offset1:227
	s_waitcnt lgkmcnt(0)
	s_barrier
	ds_read2_b32 v[128:129], v142 offset1:1
	ds_read2_b32 v[130:131], v142 offset0:2 offset1:3
	v_lshl_add_u32 v134, s91, 6, v140
	s_cbranch_scc1 .LBB0_2231
	s_cmp_gt_i32 s26, 2
	s_cbranch_scc0 .LBB0_2232
	s_cmp_eq_u32 s26, 3
	s_mov_b64 s[58:59], -1
	s_cbranch_scc0 .LBB0_2229
	v_lshlrev_b32_e32 v138, 1, v134
	v_and_b32_e32 v139, 0x7f, v134
	s_movk_i32 s5, 0xff00
	v_and_or_b32 v138, v138, s5, v139
	s_mov_b64 s[58:59], 0

.Lpeel_exit_4:
	v_pk_mul_f32 v[140:141], v[124:125], s[8:9] op_sel_hi:[1,0]
	v_pk_mul_f32 v[120:121], v[120:121], s[8:9] op_sel_hi:[1,0]
	v_mov_b32_e32 v125, v129
	v_cvt_pk_fp8_f32 v125, v120, v121
	v_pk_mul_f32 v[120:121], v[126:127], s[8:9] op_sel_hi:[1,0]
	v_pk_mul_f32 v[116:117], v[116:117], s[8:9] op_sel_hi:[1,0]
	s_nop 0
	v_cvt_pk_fp8_f32 v126, v116, v117
	v_pk_mul_f32 v[112:113], v[112:113], s[8:9] op_sel_hi:[1,0]
	s_nop 0
	v_cvt_pk_fp8_f32 v127, v112, v113
	v_pk_mul_f32 v[112:113], v[118:119], s[8:9] op_sel_hi:[1,0]
	v_pk_mul_f32 v[104:105], v[104:105], s[8:9] op_sel_hi:[1,0]
	v_cvt_pk_fp8_f32 v126, v112, v113 op_sel:[0,0,1]
	v_pk_mul_f32 v[112:113], v[114:115], s[8:9] op_sel_hi:[1,0]
	v_pk_mul_f32 v[100:101], v[100:101], s[8:9] op_sel_hi:[1,0]
	v_cvt_pk_fp8_f32 v127, v112, v113 op_sel:[0,0,1]
	v_pk_mul_f32 v[112:113], v[108:109], s[8:9] op_sel_hi:[1,0]
	v_mov_b32_e32 v109, v129
	v_cvt_pk_fp8_f32 v109, v104, v105
	v_pk_mul_f32 v[104:105], v[110:111], s[8:9] op_sel_hi:[1,0]
	v_mov_b32_e32 v110, v129
	v_cvt_pk_fp8_f32 v110, v100, v101
	v_pk_mul_f32 v[100:101], v[92:93], s[8:9] op_sel_hi:[1,0]
	v_pk_mul_f32 v[88:89], v[88:89], s[8:9] op_sel_hi:[1,0]
	v_mov_b32_e32 v93, v129
	v_cvt_pk_fp8_f32 v93, v88, v89
	v_pk_mul_f32 v[88:89], v[94:95], s[8:9] op_sel_hi:[1,0]
	v_pk_mul_f32 v[84:85], v[84:85], s[8:9] op_sel_hi:[1,0]
	s_nop 0
	v_cvt_pk_fp8_f32 v94, v84, v85
	v_pk_mul_f32 v[80:81], v[80:81], s[8:9] op_sel_hi:[1,0]
	s_nop 0
	v_cvt_pk_fp8_f32 v95, v80, v81
	v_pk_mul_f32 v[80:81], v[86:87], s[8:9] op_sel_hi:[1,0]
	v_pk_mul_f32 v[72:73], v[72:73], s[8:9] op_sel_hi:[1,0]
	v_cvt_pk_fp8_f32 v94, v80, v81 op_sel:[0,0,1]
	v_pk_mul_f32 v[80:81], v[82:83], s[8:9] op_sel_hi:[1,0]
	v_pk_mul_f32 v[68:69], v[68:69], s[8:9] op_sel_hi:[1,0]
	v_cvt_pk_fp8_f32 v95, v80, v81 op_sel:[0,0,1]
	v_pk_mul_f32 v[80:81], v[76:77], s[8:9] op_sel_hi:[1,0]
	v_mov_b32_e32 v77, v129
	v_cvt_pk_fp8_f32 v77, v72, v73
	v_pk_mul_f32 v[72:73], v[78:79], s[8:9] op_sel_hi:[1,0]
	s_nop 0
	v_cvt_pk_fp8_f32 v78, v68, v69
	v_pk_mul_f32 v[64:65], v[64:65], s[8:9] op_sel_hi:[1,0]
	s_nop 0
	v_cvt_pk_fp8_f32 v79, v64, v65
	v_pk_mul_f32 v[64:65], v[70:71], s[8:9] op_sel_hi:[1,0]
	v_pk_mul_f32 v[56:57], v[56:57], s[8:9] op_sel_hi:[1,0]
	v_cvt_pk_fp8_f32 v78, v64, v65 op_sel:[0,0,1]
	v_pk_mul_f32 v[64:65], v[66:67], s[8:9] op_sel_hi:[1,0]
	v_pk_mul_f32 v[52:53], v[52:53], s[8:9] op_sel_hi:[1,0]
	v_cvt_pk_fp8_f32 v79, v64, v65 op_sel:[0,0,1]
	v_pk_mul_f32 v[64:65], v[60:61], s[8:9] op_sel_hi:[1,0]
	v_mov_b32_e32 v61, v129
	v_cvt_pk_fp8_f32 v61, v56, v57
	v_pk_mul_f32 v[56:57], v[62:63], s[8:9] op_sel_hi:[1,0]
	s_nop 0
	v_cvt_pk_fp8_f32 v62, v52, v53
	v_pk_mul_f32 v[48:49], v[48:49], s[8:9] op_sel_hi:[1,0]
	s_nop 0
	v_cvt_pk_fp8_f32 v63, v48, v49
	s_lshl_b32 s16, s50, 8
	v_pk_mul_f32 v[48:49], v[54:55], s[8:9] op_sel_hi:[1,0]
	s_add_i32 s16, s16, s34
	v_cvt_pk_fp8_f32 v62, v48, v49 op_sel:[0,0,1]
	v_pk_mul_f32 v[48:49], v[50:51], s[8:9] op_sel_hi:[1,0]
	s_lshl_b32 s18, s51, 8
	s_ashr_i32 s17, s16, 31
	v_cvt_pk_fp8_f32 v63, v48, v49 op_sel:[0,0,1]
	v_pk_mul_f32 v[48:49], v[44:45], s[8:9] op_sel_hi:[1,0]
	v_pk_mul_f32 v[40:41], v[40:41], s[8:9] op_sel_hi:[1,0]
	v_mov_b32_e32 v45, v129
	s_ashr_i32 s19, s18, 31
	s_lshl_b64 s[20:21], s[16:17], 11
	v_cvt_pk_fp8_f32 v45, v40, v41
	v_pk_mul_f32 v[40:41], v[46:47], s[8:9] op_sel_hi:[1,0]
	v_pk_mul_f32 v[36:37], v[36:37], s[8:9] op_sel_hi:[1,0]
	v_mov_b32_e32 v46, v129
	s_add_u32 s17, s31, s20
	v_cvt_pk_fp8_f32 v46, v36, v37
	v_pk_mul_f32 v[36:37], v[28:29], s[8:9] op_sel_hi:[1,0]
	v_pk_mul_f32 v[24:25], v[24:25], s[8:9] op_sel_hi:[1,0]
	v_mov_b32_e32 v29, v129
	s_addc_u32 s20, s33, s21
	v_cvt_pk_fp8_f32 v29, v24, v25
	v_pk_mul_f32 v[24:25], v[30:31], s[8:9] op_sel_hi:[1,0]
	v_pk_mul_f32 v[20:21], v[20:21], s[8:9] op_sel_hi:[1,0]
	s_nop 0
	s_add_u32 s17, s17, s18
	v_cvt_pk_fp8_f32 v30, v20, v21
	v_pk_mul_f32 v[16:17], v[16:17], s[8:9] op_sel_hi:[1,0]
	s_nop 0
	s_addc_u32 s21, s20, s19
	v_cvt_pk_fp8_f32 v31, v16, v17
	s_add_u32 s20, s17, s35
	s_addc_u32 s21, s21, 0
	s_addk_i32 s16, 0x80
	v_pk_mul_f32 v[16:17], v[22:23], s[8:9] op_sel_hi:[1,0]
	s_ashr_i32 s17, s16, 31
	v_cvt_pk_fp8_f32 v30, v16, v17 op_sel:[0,0,1]
	v_pk_mul_f32 v[16:17], v[18:19], s[8:9] op_sel_hi:[1,0]
	s_nop 0
	s_nop 0
	v_pk_mul_f32 v[96:97], v[96:97], s[8:9] op_sel_hi:[1,0]
	s_nop 0
	s_nop 0
	s_lshl_b64 s[16:17], s[16:17], 11
	s_nop 0
	s_nop 0
	s_nop 0
	v_cvt_pk_fp8_f32 v31, v16, v17 op_sel:[0,0,1]
	v_pk_mul_f32 v[16:17], v[12:13], s[8:9] op_sel_hi:[1,0]
	v_pk_mul_f32 v[8:9], v[8:9], s[8:9] op_sel_hi:[1,0]
	s_nop 0
	v_mbcnt_lo_u32_b32 v128, -1, 0
	v_mbcnt_hi_u32_b32 v128, -1, v128
	v_cvt_pk_fp8_f32 v124, v140, v141
	v_ashrrev_i32_e32 v130, 1, v128
	v_cvt_pk_fp8_f32 v108, v112, v113
	v_cvt_pk_fp8_f32 v111, v96, v97
	v_cvt_pk_fp8_f32 v92, v100, v101
	s_nop 0
	v_cvt_pk_fp8_f32 v60, v64, v65
	v_cvt_pk_fp8_f32 v44, v48, v49
	v_pk_mul_f32 v[32:33], v[32:33], s[8:9] op_sel_hi:[1,0]
	s_nop 0
	s_add_u32 s16, s31, s16
	v_cvt_pk_fp8_f32 v28, v36, v37
	s_nop 0
	v_cvt_pk_fp8_f32 v13, v8, v9
	v_pk_mul_f32 v[8:9], v[14:15], s[8:9] op_sel_hi:[1,0]
	v_pk_mul_f32 v[4:5], v[4:5], s[8:9] op_sel_hi:[1,0]
	s_nop 0
	v_bfi_b32 v130, -16, v130, v128
	v_cvt_pk_fp8_f32 v76, v80, v81
	v_cvt_pk_fp8_f32 v47, v32, v33
	s_addc_u32 s17, s33, s17
	v_cvt_pk_fp8_f32 v12, v16, v17
	v_cvt_pk_fp8_f32 v14, v4, v5
	v_pk_mul_f32 v[0:1], v[0:1], s[8:9] op_sel_hi:[1,0]
	s_nop 0
	v_ashrrev_i32_e32 v131, 31, v130
	v_pk_mul_f32 v[96:97], v[102:103], s[8:9] op_sel_hi:[1,0]
	s_add_u32 s16, s16, s18
	v_cvt_pk_fp8_f32 v15, v0, v1
	v_lshlrev_b64 v[130:131], 11, v[130:131]
	v_cvt_pk_fp8_f32 v110, v96, v97 op_sel:[0,0,1]
	v_pk_mul_f32 v[96:97], v[98:99], s[8:9] op_sel_hi:[1,0]
	v_pk_mul_f32 v[32:33], v[38:39], s[8:9] op_sel_hi:[1,0]
	s_addc_u32 s17, s17, s19
	v_and_b32_e32 v128, 16, v128
	v_cvt_pk_fp8_f32 v124, v120, v121 op_sel:[0,0,1]
	v_pk_mul_f32 v[120:121], v[122:123], s[8:9] op_sel_hi:[1,0]
	v_cvt_pk_fp8_f32 v108, v104, v105 op_sel:[0,0,1]
	v_pk_mul_f32 v[104:105], v[106:107], s[8:9] op_sel_hi:[1,0]
	v_cvt_pk_fp8_f32 v111, v96, v97 op_sel:[0,0,1]
	v_lshl_add_u64 v[96:97], s[20:21], 0, v[130:131]
	v_cvt_pk_fp8_f32 v92, v88, v89 op_sel:[0,0,1]
	v_pk_mul_f32 v[88:89], v[90:91], s[8:9] op_sel_hi:[1,0]
	v_cvt_pk_fp8_f32 v60, v56, v57 op_sel:[0,0,1]
	v_pk_mul_f32 v[56:57], v[58:59], s[8:9] op_sel_hi:[1,0]
	v_cvt_pk_fp8_f32 v44, v40, v41 op_sel:[0,0,1]
	v_pk_mul_f32 v[40:41], v[42:43], s[8:9] op_sel_hi:[1,0]
	v_cvt_pk_fp8_f32 v46, v32, v33 op_sel:[0,0,1]
	v_pk_mul_f32 v[32:33], v[34:35], s[8:9] op_sel_hi:[1,0]
	s_add_u32 s16, s16, s35
	v_cvt_pk_fp8_f32 v28, v24, v25 op_sel:[0,0,1]
	v_pk_mul_f32 v[24:25], v[26:27], s[8:9] op_sel_hi:[1,0]
	v_pk_mul_f32 v[0:1], v[6:7], s[8:9] op_sel_hi:[1,0]
	v_cvt_pk_fp8_f32 v125, v120, v121 op_sel:[0,0,1]
	v_cvt_pk_fp8_f32 v109, v104, v105 op_sel:[0,0,1]
	v_lshl_add_u64 v[96:97], v[96:97], 0, v[128:129]
	v_cvt_pk_fp8_f32 v93, v88, v89 op_sel:[0,0,1]
	v_cvt_pk_fp8_f32 v76, v72, v73 op_sel:[0,0,1]
	v_pk_mul_f32 v[72:73], v[74:75], s[8:9] op_sel_hi:[1,0]
	v_cvt_pk_fp8_f32 v61, v56, v57 op_sel:[0,0,1]
	v_cvt_pk_fp8_f32 v45, v40, v41 op_sel:[0,0,1]
	v_cvt_pk_fp8_f32 v47, v32, v33 op_sel:[0,0,1]
	s_addc_u32 s17, s17, 0
	v_cvt_pk_fp8_f32 v29, v24, v25 op_sel:[0,0,1]
	v_cvt_pk_fp8_f32 v12, v8, v9 op_sel:[0,0,1]
	v_pk_mul_f32 v[8:9], v[10:11], s[8:9] op_sel_hi:[1,0]
	v_cvt_pk_fp8_f32 v14, v0, v1 op_sel:[0,0,1]
	v_pk_mul_f32 v[0:1], v[2:3], s[8:9] op_sel_hi:[1,0]
	v_add_co_u32_e32 v98, vcc, s30, v96
	v_cvt_pk_fp8_f32 v77, v72, v73 op_sel:[0,0,1]
	v_lshl_add_u64 v[32:33], s[16:17], 0, v[130:131]
	v_cvt_pk_fp8_f32 v13, v8, v9 op_sel:[0,0,1]
	v_cvt_pk_fp8_f32 v15, v0, v1 op_sel:[0,0,1]
	v_addc_co_u32_e32 v99, vcc, 0, v97, vcc
	v_lshl_add_u64 v[32:33], v[32:33], 0, v[128:129]
	v_add_co_u32_e32 v34, vcc, s30, v32
	v_permlane32_swap_b32_e32 v124, v126
	v_permlane32_swap_b32_e32 v125, v127
	v_permlane32_swap_b32_e32 v108, v110
	v_permlane32_swap_b32_e32 v109, v111
	v_permlane32_swap_b32_e32 v92, v94
	v_permlane32_swap_b32_e32 v93, v95
	v_permlane32_swap_b32_e32 v60, v62
	v_permlane32_swap_b32_e32 v61, v63
	v_permlane32_swap_b32_e32 v44, v46
	v_permlane32_swap_b32_e32 v45, v47
	v_addc_co_u32_e32 v35, vcc, 0, v33, vcc
	v_permlane32_swap_b32_e32 v28, v30
	v_permlane32_swap_b32_e32 v29, v31
	v_permlane16_swap_b32_e32 v124, v125
	v_permlane16_swap_b32_e32 v126, v127
	v_permlane16_swap_b32_e32 v108, v109
	v_permlane16_swap_b32_e32 v110, v111
	v_permlane16_swap_b32_e32 v92, v93
	v_permlane16_swap_b32_e32 v94, v95
	v_permlane32_swap_b32_e32 v76, v78
	v_permlane32_swap_b32_e32 v77, v79
	v_permlane16_swap_b32_e32 v60, v61
	v_permlane16_swap_b32_e32 v62, v63
	v_permlane16_swap_b32_e32 v44, v45
	v_permlane16_swap_b32_e32 v46, v47
	v_permlane16_swap_b32_e32 v28, v29
	v_permlane16_swap_b32_e32 v30, v31
	v_permlane32_swap_b32_e32 v12, v14
	v_permlane32_swap_b32_e32 v13, v15
	s_and_b64 vcc, exec, s[10:11]
	s_mov_b32 s51, s49
	s_mov_b32 s50, s48
	s_mov_b64 s[18:19], s[12:13]
	s_mov_b64 s[16:17], s[14:15]
	global_store_dwordx4 v[96:97], v[124:127], off
	global_store_dwordx4 v[98:99], v[108:111], off
	v_permlane16_swap_b32_e32 v76, v77
	v_permlane16_swap_b32_e32 v78, v79
	global_store_dwordx4 v[96:97], v[92:95], off offset:128
	global_store_dwordx4 v[98:99], v[76:79], off offset:128
	global_store_dwordx4 v[32:33], v[60:63], off
	global_store_dwordx4 v[34:35], v[44:47], off
	v_permlane16_swap_b32_e32 v12, v13
	v_permlane16_swap_b32_e32 v14, v15
	global_store_dwordx4 v[32:33], v[28:31], off offset:128
	global_store_dwordx4 v[34:35], v[12:15], off offset:128
	s_cbranch_vccz .LBB0_2377
	s_waitcnt vmcnt(0)
	v_readlane_b32 s0, v252, 2
	s_cmpk_gt_u32 s0, 0xff
	s_cbranch_scc1 .LBB0_2386
	s_barrier

.LBB0_2720:
	s_waitcnt vmcnt(15)
	v_mov_b32_e32 v128, v0
	s_waitcnt vmcnt(14)
	v_mov_b32_e32 v129, v4
	v_pk_mul_f32 v[128:129], v[128:129], s[70:71] op_sel_hi:[1,0]
	s_nop 0
	v_cvt_pk_fp8_f32 v130, v128, v129
	s_waitcnt vmcnt(13)
	v_mov_b32_e32 v128, v8
	s_waitcnt vmcnt(12)
	v_mov_b32_e32 v129, v12
	v_pk_mul_f32 v[128:129], v[128:129], s[70:71] op_sel_hi:[1,0]
	s_nop 0
	v_cvt_pk_fp8_f32 v130, v128, v129 op_sel:[0,0,1]
	v_mov_b32_e32 v128, v1
	v_mov_b32_e32 v129, v5
	v_pk_mul_f32 v[128:129], v[128:129], s[70:71] op_sel_hi:[1,0]
	s_nop 0
	v_cvt_pk_fp8_f32 v131, v128, v129
	v_mov_b32_e32 v128, v9
	v_mov_b32_e32 v129, v13
	v_pk_mul_f32 v[128:129], v[128:129], s[70:71] op_sel_hi:[1,0]
	s_nop 0
	v_cvt_pk_fp8_f32 v131, v128, v129 op_sel:[0,0,1]
	v_mov_b32_e32 v128, v2
	v_mov_b32_e32 v129, v6
	v_pk_mul_f32 v[128:129], v[128:129], s[70:71] op_sel_hi:[1,0]
	v_readlane_b32 s6, v252, 31
	v_cvt_pk_fp8_f32 v134, v128, v129
	v_mov_b32_e32 v128, v10
	v_mov_b32_e32 v129, v14
	v_pk_mul_f32 v[128:129], v[128:129], s[70:71] op_sel_hi:[1,0]
	v_readlane_b32 s7, v252, 32
	v_cvt_pk_fp8_f32 v134, v128, v129 op_sel:[0,0,1]
	v_mov_b32_e32 v128, v3
	v_mov_b32_e32 v129, v7
	v_pk_mul_f32 v[128:129], v[128:129], s[70:71] op_sel_hi:[1,0]
	s_cmp_eq_u64 s[6:7], 0
	v_cvt_pk_fp8_f32 v138, v128, v129
	v_mov_b32_e32 v128, v11
	v_mov_b32_e32 v129, v15
	v_pk_mul_f32 v[128:129], v[128:129], s[70:71] op_sel_hi:[1,0]
	ds_write2_b32 v143, v130, v131 offset1:33
	v_cvt_pk_fp8_f32 v138, v128, v129 op_sel:[0,0,1]
	ds_write2_b32 v143, v134, v138 offset0:66 offset1:99
	s_cbranch_scc1 .LBB0_2722
	v_lshl_add_u32 v128, s50, 7, v133
	v_ashrrev_i32_e32 v129, 31, v128
	v_lshl_add_u64 v[128:129], v[128:129], 2, s[6:7]
	global_load_dwordx4 v[128:131], v[128:129], off
	s_waitcnt vmcnt(0)
	v_pk_mul_f32 v[18:19], v[18:19], v[128:129] op_sel_hi:[1,0]
	v_pk_mul_f32 v[16:17], v[16:17], v[128:129] op_sel_hi:[1,0]
	v_pk_mul_f32 v[22:23], v[22:23], v[128:129] op_sel:[0,1]
	v_pk_mul_f32 v[20:21], v[20:21], v[128:129] op_sel:[0,1]
	v_mov_b32_e32 v128, v131
	v_pk_mul_f32 v[26:27], v[26:27], v[130:131] op_sel_hi:[1,0]
	v_pk_mul_f32 v[24:25], v[24:25], v[130:131] op_sel_hi:[1,0]
	v_pk_mul_f32 v[30:31], v[30:31], v[128:129] op_sel_hi:[1,0]
	v_pk_mul_f32 v[28:29], v[28:29], v[128:129] op_sel_hi:[1,0]
.LBB0_2722:
	s_waitcnt vmcnt(11)
	v_mov_b32_e32 v128, v16
	s_waitcnt vmcnt(10)
	v_mov_b32_e32 v129, v20
	v_pk_mul_f32 v[128:129], v[128:129], s[70:71] op_sel_hi:[1,0]
	s_nop 0
	v_cvt_pk_fp8_f32 v130, v128, v129
	s_waitcnt vmcnt(9)
	v_mov_b32_e32 v128, v24
	s_waitcnt vmcnt(8)
	v_mov_b32_e32 v129, v28
	v_pk_mul_f32 v[128:129], v[128:129], s[70:71] op_sel_hi:[1,0]
	s_nop 0
	v_cvt_pk_fp8_f32 v130, v128, v129 op_sel:[0,0,1]
	v_mov_b32_e32 v128, v17
	v_mov_b32_e32 v129, v21
	v_pk_mul_f32 v[128:129], v[128:129], s[70:71] op_sel_hi:[1,0]
	s_nop 0
	v_cvt_pk_fp8_f32 v131, v128, v129
	v_mov_b32_e32 v128, v25
	v_mov_b32_e32 v129, v29
	v_pk_mul_f32 v[128:129], v[128:129], s[70:71] op_sel_hi:[1,0]
	s_nop 0
	v_cvt_pk_fp8_f32 v131, v128, v129 op_sel:[0,0,1]
	v_mov_b32_e32 v128, v18
	v_mov_b32_e32 v129, v22
	v_pk_mul_f32 v[128:129], v[128:129], s[70:71] op_sel_hi:[1,0]
	v_add_u32_e32 v144, 0x4000, v143
	v_cvt_pk_fp8_f32 v134, v128, v129
	v_mov_b32_e32 v128, v26
	v_mov_b32_e32 v129, v30
	v_pk_mul_f32 v[128:129], v[128:129], s[70:71] op_sel_hi:[1,0]
	s_cmp_eq_u64 s[62:63], 0
	v_cvt_pk_fp8_f32 v134, v128, v129 op_sel:[0,0,1]
	v_mov_b32_e32 v128, v19
	v_mov_b32_e32 v129, v23
	v_pk_mul_f32 v[128:129], v[128:129], s[70:71] op_sel_hi:[1,0]
	s_mov_b64 s[36:37], s[22:23]
	v_cvt_pk_fp8_f32 v138, v128, v129
	v_mov_b32_e32 v128, v27
	v_mov_b32_e32 v129, v31
	v_pk_mul_f32 v[128:129], v[128:129], s[70:71] op_sel_hi:[1,0]
	s_mov_b64 s[6:7], s[20:21]
	v_cvt_pk_fp8_f32 v138, v128, v129 op_sel:[0,0,1]
	ds_write2_b32 v144, v130, v131 offset0:128 offset1:161
	ds_write2_b32 v144, v134, v138 offset0:194 offset1:227
	s_cbranch_scc1 .LBB0_2724
	v_lshl_add_u32 v128, s46, 7, v133
	v_ashrrev_i32_e32 v129, 31, v128
	v_lshl_add_u64 v[128:129], v[128:129], 2, s[62:63]
	global_load_dwordx4 v[128:131], v[128:129], off
	s_waitcnt vmcnt(0)
	v_pk_mul_f32 v[50:51], v[50:51], v[128:129] op_sel_hi:[1,0]
	v_pk_mul_f32 v[48:49], v[48:49], v[128:129] op_sel_hi:[1,0]
	v_pk_mul_f32 v[54:55], v[54:55], v[128:129] op_sel:[0,1]
	v_pk_mul_f32 v[52:53], v[52:53], v[128:129] op_sel:[0,1]
	v_mov_b32_e32 v128, v131
	v_pk_mul_f32 v[58:59], v[58:59], v[130:131] op_sel_hi:[1,0]
	v_pk_mul_f32 v[56:57], v[56:57], v[130:131] op_sel_hi:[1,0]
	v_pk_mul_f32 v[62:63], v[62:63], v[128:129] op_sel_hi:[1,0]
	v_pk_mul_f32 v[60:61], v[60:61], v[128:129] op_sel_hi:[1,0]
.LBB0_2724:
	s_waitcnt vmcnt(7)
	v_mov_b32_e32 v128, v48
	s_waitcnt vmcnt(6)
	v_mov_b32_e32 v129, v52
	v_pk_mul_f32 v[128:129], v[128:129], s[70:71] op_sel_hi:[1,0]
	s_nop 0
	v_cvt_pk_fp8_f32 v130, v128, v129
	s_waitcnt vmcnt(5)
	v_mov_b32_e32 v128, v56
	s_waitcnt vmcnt(4)
	v_mov_b32_e32 v129, v60
	v_pk_mul_f32 v[128:129], v[128:129], s[70:71] op_sel_hi:[1,0]
	s_nop 0
	v_cvt_pk_fp8_f32 v130, v128, v129 op_sel:[0,0,1]
	v_mov_b32_e32 v128, v49
	v_mov_b32_e32 v129, v53
	v_pk_mul_f32 v[128:129], v[128:129], s[70:71] op_sel_hi:[1,0]
	s_nop 0
	v_cvt_pk_fp8_f32 v131, v128, v129
	v_mov_b32_e32 v128, v57
	v_mov_b32_e32 v129, v61
	v_pk_mul_f32 v[128:129], v[128:129], s[70:71] op_sel_hi:[1,0]
	s_nop 0
	v_cvt_pk_fp8_f32 v131, v128, v129 op_sel:[0,0,1]
	v_mov_b32_e32 v128, v50
	v_mov_b32_e32 v129, v54
	v_pk_mul_f32 v[128:129], v[128:129], s[70:71] op_sel_hi:[1,0]
	v_readlane_b32 s8, v254, 39
	v_cvt_pk_fp8_f32 v134, v128, v129
	v_mov_b32_e32 v128, v58
	v_mov_b32_e32 v129, v62
	v_pk_mul_f32 v[128:129], v[128:129], s[70:71] op_sel_hi:[1,0]
	v_readlane_b32 s12, v254, 43
	v_cvt_pk_fp8_f32 v134, v128, v129 op_sel:[0,0,1]
	v_mov_b32_e32 v128, v51
	v_mov_b32_e32 v129, v55
	v_pk_mul_f32 v[128:129], v[128:129], s[70:71] op_sel_hi:[1,0]
	v_readlane_b32 s13, v254, 44
	v_cvt_pk_fp8_f32 v138, v128, v129
	v_mov_b32_e32 v128, v59
	v_mov_b32_e32 v129, v63
	v_pk_mul_f32 v[128:129], v[128:129], s[70:71] op_sel_hi:[1,0]
	v_add_u32_e32 v145, 0x8400, v143
	v_cvt_pk_fp8_f32 v138, v128, v129 op_sel:[0,0,1]
	s_cmp_eq_u64 s[12:13], 0
	ds_write2_b32 v145, v130, v131 offset1:33
	v_readlane_b32 s9, v254, 40
	v_readlane_b32 s10, v254, 41
	v_readlane_b32 s11, v254, 42
	v_readlane_b32 s14, v254, 45
	v_readlane_b32 s15, v254, 46
	v_readlane_b32 s16, v254, 47
	v_readlane_b32 s17, v254, 48
	v_readlane_b32 s18, v254, 49
	v_readlane_b32 s19, v254, 50
	v_readlane_b32 s20, v254, 51
	v_readlane_b32 s21, v254, 52
	v_readlane_b32 s22, v254, 53
	v_readlane_b32 s23, v254, 54
	ds_write2_b32 v145, v134, v138 offset0:66 offset1:99
	s_cbranch_scc1 .LBB0_2726
	v_lshl_add_u32 v128, s40, 7, v133
	v_ashrrev_i32_e32 v129, 31, v128
	v_lshl_add_u64 v[128:129], v[128:129], 2, s[12:13]
	global_load_dwordx4 v[128:131], v[128:129], off
	s_waitcnt vmcnt(0)
	v_pk_mul_f32 v[98:99], v[98:99], v[128:129] op_sel_hi:[1,0]
	v_pk_mul_f32 v[96:97], v[96:97], v[128:129] op_sel_hi:[1,0]
	v_pk_mul_f32 v[102:103], v[102:103], v[128:129] op_sel:[0,1]
	v_pk_mul_f32 v[100:101], v[100:101], v[128:129] op_sel:[0,1]
	v_mov_b32_e32 v128, v131
	v_pk_mul_f32 v[106:107], v[106:107], v[130:131] op_sel_hi:[1,0]
	v_pk_mul_f32 v[104:105], v[104:105], v[130:131] op_sel_hi:[1,0]
	v_pk_mul_f32 v[110:111], v[110:111], v[128:129] op_sel_hi:[1,0]
	v_pk_mul_f32 v[108:109], v[108:109], v[128:129] op_sel_hi:[1,0]
.LBB0_2726:
	s_waitcnt vmcnt(3)
	v_mov_b32_e32 v128, v96
	s_waitcnt vmcnt(2)
	v_mov_b32_e32 v129, v100
	v_pk_mul_f32 v[128:129], v[128:129], s[70:71] op_sel_hi:[1,0]
	s_nop 0
	v_cvt_pk_fp8_f32 v130, v128, v129
	s_waitcnt vmcnt(1)
	v_mov_b32_e32 v128, v104
	s_waitcnt vmcnt(0)
	v_mov_b32_e32 v129, v108
	v_pk_mul_f32 v[128:129], v[128:129], s[70:71] op_sel_hi:[1,0]
	s_nop 0
	v_cvt_pk_fp8_f32 v130, v128, v129 op_sel:[0,0,1]
	v_mov_b32_e32 v128, v97
	v_mov_b32_e32 v129, v101
	v_pk_mul_f32 v[128:129], v[128:129], s[70:71] op_sel_hi:[1,0]
	s_nop 0
	v_cvt_pk_fp8_f32 v131, v128, v129
	v_mov_b32_e32 v128, v105
	v_mov_b32_e32 v129, v109
	v_pk_mul_f32 v[128:129], v[128:129], s[70:71] op_sel_hi:[1,0]
	s_nop 0
	v_cvt_pk_fp8_f32 v131, v128, v129 op_sel:[0,0,1]
	v_mov_b32_e32 v128, v98
	v_mov_b32_e32 v129, v102
	v_pk_mul_f32 v[128:129], v[128:129], s[70:71] op_sel_hi:[1,0]
	v_add_u32_e32 v146, 0xc400, v143
	v_cvt_pk_fp8_f32 v134, v128, v129
	v_mov_b32_e32 v128, v106
	v_mov_b32_e32 v129, v110
	v_pk_mul_f32 v[128:129], v[128:129], s[70:71] op_sel_hi:[1,0]
	s_mov_b64 s[20:21], s[6:7]
	v_cvt_pk_fp8_f32 v134, v128, v129 op_sel:[0,0,1]
	v_mov_b32_e32 v128, v99
	v_mov_b32_e32 v129, v103
	v_pk_mul_f32 v[128:129], v[128:129], s[70:71] op_sel_hi:[1,0]
	s_mov_b64 s[22:23], s[36:37]
	v_cvt_pk_fp8_f32 v138, v128, v129
	v_mov_b32_e32 v128, v107
	v_mov_b32_e32 v129, v111
	v_pk_mul_f32 v[128:129], v[128:129], s[70:71] op_sel_hi:[1,0]
	s_cmp_lt_i32 s49, 2
	v_cvt_pk_fp8_f32 v138, v128, v129 op_sel:[0,0,1]
	ds_write2_b32 v146, v130, v131 offset0:128 offset1:161
	ds_write2_b32 v146, v134, v138 offset0:194 offset1:227
	s_waitcnt lgkmcnt(0)
	s_barrier
	ds_read2_b32 v[128:129], v142 offset1:1
	ds_read2_b32 v[130:131], v142 offset0:2 offset1:3
	v_lshl_add_u32 v134, s67, 6, v140
	s_cbranch_scc1 .LBB0_2732
	s_cmp_gt_i32 s49, 2
	s_cbranch_scc0 .LBB0_2733
	s_cmp_eq_u32 s49, 3
	s_mov_b64 s[6:7], -1
	s_cbranch_scc0 .LBB0_2730
	v_lshlrev_b32_e32 v138, 1, v134
	v_and_b32_e32 v139, 0x7f, v134
	s_movk_i32 s0, 0xff00
	v_and_or_b32 v138, v138, s0, v139
	s_mov_b64 s[6:7], 0

.LBB0_2967:
	v_mov_b32_e32 v128, v32
	v_mov_b32_e32 v129, v36
	v_pk_mul_f32 v[128:129], v[128:129], s[70:71] op_sel_hi:[1,0]
	s_nop 0
	v_cvt_pk_fp8_f32 v130, v128, v129
	v_mov_b32_e32 v128, v40
	v_mov_b32_e32 v129, v44
	v_pk_mul_f32 v[128:129], v[128:129], s[70:71] op_sel_hi:[1,0]
	s_nop 0
	v_cvt_pk_fp8_f32 v130, v128, v129 op_sel:[0,0,1]
	v_mov_b32_e32 v128, v33
	v_mov_b32_e32 v129, v37
	v_pk_mul_f32 v[128:129], v[128:129], s[70:71] op_sel_hi:[1,0]
	s_nop 0
	v_cvt_pk_fp8_f32 v131, v128, v129
	v_mov_b32_e32 v128, v41
	v_mov_b32_e32 v129, v45
	v_pk_mul_f32 v[128:129], v[128:129], s[70:71] op_sel_hi:[1,0]
	s_nop 0
	v_cvt_pk_fp8_f32 v131, v128, v129 op_sel:[0,0,1]
	v_mov_b32_e32 v128, v34
	v_mov_b32_e32 v129, v38
	v_pk_mul_f32 v[128:129], v[128:129], s[70:71] op_sel_hi:[1,0]
	s_cmp_eq_u64 s[22:23], 0
	v_cvt_pk_fp8_f32 v134, v128, v129
	v_mov_b32_e32 v128, v42
	v_mov_b32_e32 v129, v46
	v_pk_mul_f32 v[128:129], v[128:129], s[70:71] op_sel_hi:[1,0]
	ds_write2_b32 v143, v130, v131 offset1:33
	v_cvt_pk_fp8_f32 v134, v128, v129 op_sel:[0,0,1]
	v_mov_b32_e32 v128, v35
	v_mov_b32_e32 v129, v39
	v_pk_mul_f32 v[128:129], v[128:129], s[70:71] op_sel_hi:[1,0]
	s_nop 0
	v_cvt_pk_fp8_f32 v138, v128, v129
	v_mov_b32_e32 v128, v43
	v_mov_b32_e32 v129, v47
	v_pk_mul_f32 v[128:129], v[128:129], s[70:71] op_sel_hi:[1,0]
	s_nop 0
	v_cvt_pk_fp8_f32 v138, v128, v129 op_sel:[0,0,1]
	ds_write2_b32 v143, v134, v138 offset0:66 offset1:99
	s_cbranch_scc1 .LBB0_2969
	v_lshl_add_u32 v128, s53, 7, v133
	v_ashrrev_i32_e32 v129, 31, v128
	v_lshl_add_u64 v[128:129], v[128:129], 2, s[22:23]
	global_load_dwordx4 v[128:131], v[128:129], off
	s_waitcnt vmcnt(0)
	v_pk_mul_f32 v[66:67], v[66:67], v[128:129] op_sel_hi:[1,0]
	v_pk_mul_f32 v[64:65], v[64:65], v[128:129] op_sel_hi:[1,0]
	v_pk_mul_f32 v[70:71], v[70:71], v[128:129] op_sel:[0,1]
	v_pk_mul_f32 v[68:69], v[68:69], v[128:129] op_sel:[0,1]
	v_mov_b32_e32 v128, v131
	v_pk_mul_f32 v[74:75], v[74:75], v[130:131] op_sel_hi:[1,0]
	v_pk_mul_f32 v[72:73], v[72:73], v[130:131] op_sel_hi:[1,0]
	v_pk_mul_f32 v[78:79], v[78:79], v[128:129] op_sel_hi:[1,0]
	v_pk_mul_f32 v[76:77], v[76:77], v[128:129] op_sel_hi:[1,0]
.LBB0_2969:
	v_mov_b32_e32 v128, v64
	v_mov_b32_e32 v129, v68
	v_pk_mul_f32 v[128:129], v[128:129], s[70:71] op_sel_hi:[1,0]
	s_nop 0
	v_cvt_pk_fp8_f32 v130, v128, v129
	v_mov_b32_e32 v128, v72
	v_mov_b32_e32 v129, v76
	v_pk_mul_f32 v[128:129], v[128:129], s[70:71] op_sel_hi:[1,0]
	s_nop 0
	v_cvt_pk_fp8_f32 v130, v128, v129 op_sel:[0,0,1]
	v_mov_b32_e32 v128, v65
	v_mov_b32_e32 v129, v69
	v_pk_mul_f32 v[128:129], v[128:129], s[70:71] op_sel_hi:[1,0]
	s_nop 0
	v_cvt_pk_fp8_f32 v131, v128, v129
	v_mov_b32_e32 v128, v73
	v_mov_b32_e32 v129, v77
	v_pk_mul_f32 v[128:129], v[128:129], s[70:71] op_sel_hi:[1,0]
	s_nop 0
	v_cvt_pk_fp8_f32 v131, v128, v129 op_sel:[0,0,1]
	v_mov_b32_e32 v128, v66
	v_mov_b32_e32 v129, v70
	v_pk_mul_f32 v[128:129], v[128:129], s[70:71] op_sel_hi:[1,0]
	s_cmp_eq_u64 s[20:21], 0
	v_cvt_pk_fp8_f32 v134, v128, v129
	v_mov_b32_e32 v128, v74
	v_mov_b32_e32 v129, v78
	v_pk_mul_f32 v[128:129], v[128:129], s[70:71] op_sel_hi:[1,0]
	ds_write2_b32 v144, v130, v131 offset0:128 offset1:161
	v_cvt_pk_fp8_f32 v134, v128, v129 op_sel:[0,0,1]
	v_mov_b32_e32 v128, v67
	v_mov_b32_e32 v129, v71
	v_pk_mul_f32 v[128:129], v[128:129], s[70:71] op_sel_hi:[1,0]
	s_nop 0
	v_cvt_pk_fp8_f32 v138, v128, v129
	v_mov_b32_e32 v128, v75
	v_mov_b32_e32 v129, v79
	v_pk_mul_f32 v[128:129], v[128:129], s[70:71] op_sel_hi:[1,0]
	s_nop 0
	v_cvt_pk_fp8_f32 v138, v128, v129 op_sel:[0,0,1]
	ds_write2_b32 v144, v134, v138 offset0:194 offset1:227
	s_cbranch_scc1 .LBB0_2971
	v_lshl_add_u32 v128, s52, 7, v133
	v_ashrrev_i32_e32 v129, 31, v128
	v_lshl_add_u64 v[128:129], v[128:129], 2, s[20:21]
	global_load_dwordx4 v[128:131], v[128:129], off
	s_waitcnt vmcnt(0)
	v_pk_mul_f32 v[82:83], v[82:83], v[128:129] op_sel_hi:[1,0]
	v_pk_mul_f32 v[80:81], v[80:81], v[128:129] op_sel_hi:[1,0]
	v_pk_mul_f32 v[86:87], v[86:87], v[128:129] op_sel:[0,1]
	v_pk_mul_f32 v[84:85], v[84:85], v[128:129] op_sel:[0,1]
	v_mov_b32_e32 v128, v131
	v_pk_mul_f32 v[90:91], v[90:91], v[130:131] op_sel_hi:[1,0]
	v_pk_mul_f32 v[88:89], v[88:89], v[130:131] op_sel_hi:[1,0]
	v_pk_mul_f32 v[94:95], v[94:95], v[128:129] op_sel_hi:[1,0]
	v_pk_mul_f32 v[92:93], v[92:93], v[128:129] op_sel_hi:[1,0]
.LBB0_2971:
	v_mov_b32_e32 v128, v80
	v_mov_b32_e32 v129, v84
	v_pk_mul_f32 v[128:129], v[128:129], s[70:71] op_sel_hi:[1,0]
	s_nop 0
	v_cvt_pk_fp8_f32 v130, v128, v129
	v_mov_b32_e32 v128, v88
	v_mov_b32_e32 v129, v92
	v_pk_mul_f32 v[128:129], v[128:129], s[70:71] op_sel_hi:[1,0]
	s_nop 0
	v_cvt_pk_fp8_f32 v130, v128, v129 op_sel:[0,0,1]
	v_mov_b32_e32 v128, v81
	v_mov_b32_e32 v129, v85
	v_pk_mul_f32 v[128:129], v[128:129], s[70:71] op_sel_hi:[1,0]
	s_nop 0
	v_cvt_pk_fp8_f32 v131, v128, v129
	v_mov_b32_e32 v128, v89
	v_mov_b32_e32 v129, v93
	v_pk_mul_f32 v[128:129], v[128:129], s[70:71] op_sel_hi:[1,0]
	s_nop 0
	v_cvt_pk_fp8_f32 v131, v128, v129 op_sel:[0,0,1]
	v_mov_b32_e32 v128, v82
	v_mov_b32_e32 v129, v86
	v_pk_mul_f32 v[128:129], v[128:129], s[70:71] op_sel_hi:[1,0]
	s_cmp_eq_u64 s[80:81], 0
	v_cvt_pk_fp8_f32 v134, v128, v129
	v_mov_b32_e32 v128, v90
	v_mov_b32_e32 v129, v94
	v_pk_mul_f32 v[128:129], v[128:129], s[70:71] op_sel_hi:[1,0]
	ds_write2_b32 v145, v130, v131 offset1:33
	v_cvt_pk_fp8_f32 v134, v128, v129 op_sel:[0,0,1]
	v_mov_b32_e32 v128, v83
	v_mov_b32_e32 v129, v87
	v_pk_mul_f32 v[128:129], v[128:129], s[70:71] op_sel_hi:[1,0]
	s_nop 0
	v_cvt_pk_fp8_f32 v138, v128, v129
	v_mov_b32_e32 v128, v91
	v_mov_b32_e32 v129, v95
	v_pk_mul_f32 v[128:129], v[128:129], s[70:71] op_sel_hi:[1,0]
	s_nop 0
	v_cvt_pk_fp8_f32 v138, v128, v129 op_sel:[0,0,1]
	ds_write2_b32 v145, v134, v138 offset0:66 offset1:99
	s_cbranch_scc1 .LBB0_2973
	v_lshl_add_u32 v128, s3, 7, v133
	v_ashrrev_i32_e32 v129, 31, v128
	v_lshl_add_u64 v[128:129], v[128:129], 2, s[80:81]
	global_load_dwordx4 v[128:131], v[128:129], off
	s_waitcnt vmcnt(0)
	v_pk_mul_f32 v[114:115], v[114:115], v[128:129] op_sel_hi:[1,0]
	v_pk_mul_f32 v[112:113], v[112:113], v[128:129] op_sel_hi:[1,0]
	v_pk_mul_f32 v[118:119], v[118:119], v[128:129] op_sel:[0,1]
	v_pk_mul_f32 v[116:117], v[116:117], v[128:129] op_sel:[0,1]
	v_mov_b32_e32 v128, v131
	v_pk_mul_f32 v[122:123], v[122:123], v[130:131] op_sel_hi:[1,0]
	v_pk_mul_f32 v[120:121], v[120:121], v[130:131] op_sel_hi:[1,0]
	v_pk_mul_f32 v[126:127], v[126:127], v[128:129] op_sel_hi:[1,0]
	v_pk_mul_f32 v[124:125], v[124:125], v[128:129] op_sel_hi:[1,0]
.LBB0_2973:
	v_mov_b32_e32 v128, v112
	v_mov_b32_e32 v129, v116
	v_pk_mul_f32 v[128:129], v[128:129], s[70:71] op_sel_hi:[1,0]
	s_nop 0
	v_cvt_pk_fp8_f32 v130, v128, v129
	v_mov_b32_e32 v128, v120
	v_mov_b32_e32 v129, v124
	v_pk_mul_f32 v[128:129], v[128:129], s[70:71] op_sel_hi:[1,0]
	s_nop 0
	v_cvt_pk_fp8_f32 v130, v128, v129 op_sel:[0,0,1]
	v_mov_b32_e32 v128, v113
	v_mov_b32_e32 v129, v117
	v_pk_mul_f32 v[128:129], v[128:129], s[70:71] op_sel_hi:[1,0]
	s_nop 0
	v_cvt_pk_fp8_f32 v131, v128, v129
	v_mov_b32_e32 v128, v121
	v_mov_b32_e32 v129, v125
	v_pk_mul_f32 v[128:129], v[128:129], s[70:71] op_sel_hi:[1,0]
	s_nop 0
	v_cvt_pk_fp8_f32 v131, v128, v129 op_sel:[0,0,1]
	v_mov_b32_e32 v128, v114
	v_mov_b32_e32 v129, v118
	v_pk_mul_f32 v[128:129], v[128:129], s[70:71] op_sel_hi:[1,0]
	s_cmp_lt_i32 s59, 2
	v_cvt_pk_fp8_f32 v134, v128, v129
	v_mov_b32_e32 v128, v122
	v_mov_b32_e32 v129, v126
	v_pk_mul_f32 v[128:129], v[128:129], s[70:71] op_sel_hi:[1,0]
	s_nop 0
	v_cvt_pk_fp8_f32 v134, v128, v129 op_sel:[0,0,1]
	v_mov_b32_e32 v128, v115
	v_mov_b32_e32 v129, v119
	v_pk_mul_f32 v[128:129], v[128:129], s[70:71] op_sel_hi:[1,0]
	s_nop 0
	v_cvt_pk_fp8_f32 v138, v128, v129
	v_mov_b32_e32 v128, v123
	v_mov_b32_e32 v129, v127
	v_pk_mul_f32 v[128:129], v[128:129], s[70:71] op_sel_hi:[1,0]
	s_nop 0
	v_cvt_pk_fp8_f32 v138, v128, v129 op_sel:[0,0,1]
	ds_write2_b32 v146, v130, v131 offset0:128 offset1:161
	ds_write2_b32 v146, v134, v138 offset0:194 offset1:227
	s_waitcnt lgkmcnt(0)
	s_barrier
	ds_read2_b32 v[128:129], v142 offset1:1
	ds_read2_b32 v[130:131], v142 offset0:2 offset1:3
	v_lshl_add_u32 v134, s61, 6, v140
	s_cbranch_scc1 .LBB0_2979
	s_cmp_gt_i32 s59, 2
	s_cbranch_scc0 .LBB0_2980
	s_cmp_eq_u32 s59, 3
	s_mov_b64 s[6:7], -1
	s_cbranch_scc0 .LBB0_2977
	v_lshlrev_b32_e32 v138, 1, v134
	v_and_b32_e32 v139, 0x7f, v134
	s_movk_i32 s1, 0xff00
	v_and_or_b32 v138, v138, s1, v139
	s_mov_b64 s[6:7], 0

.LBB0_3213:
	v_mbcnt_lo_u32_b32 v16, -1, 0
	v_mbcnt_hi_u32_b32 v16, -1, v16
	s_lshl_b32 s6, s26, 8
	v_ashrrev_i32_e32 v0, 4, v16
	s_add_i32 s26, s6, s55
	v_lshlrev_b32_e32 v12, 2, v0
	v_lshlrev_b32_e32 v0, 3, v0
	s_cmp_gt_i32 s68, 3
	v_bfi_b32 v8, -16, v0, v16
	s_cselect_b64 s[28:29], -1, 0
	v_ashrrev_i32_e32 v9, 31, v8
	v_and_b32_e32 v205, 15, v16
	v_ashrrev_i32_e32 v13, 31, v12
	v_lshlrev_b64 v[10:11], 6, v[8:9]
	v_cmp_gt_u32_e64 s[6:7], 16, v16
	s_and_b64 vcc, exec, s[28:29]
	s_cbranch_vccz .LBB0_3216
	s_mov_b64 s[30:31], 0
	s_and_b64 vcc, exec, s[10:11]
	s_mov_b64 s[34:35], 0
	s_cbranch_vccz .LBB0_3217
	s_and_b32 s8, s26, 0xfc0
	v_or_b32_e32 v2, s8, v205
	v_lshl_add_u64 v[0:1], v[12:13], 2, s[12:13]
	v_lshlrev_b32_e32 v64, 8, v2
	v_lshl_add_u64 v[0:1], v[0:1], 0, v[64:65]
	v_add_co_u32_e32 v2, vcc, 0x1000, v0
	global_load_dwordx4 v[18:21], v[0:1], off offset:128
	global_load_dwordx4 v[22:25], v[0:1], off
	v_addc_co_u32_e32 v3, vcc, 0, v1, vcc
	global_load_dwordx4 v[26:29], v[2:3], off offset:128
	s_waitcnt lgkmcnt(0)
	global_load_dwordx4 v[30:33], v[2:3], off
	v_add_co_u32_e32 v2, vcc, s48, v0
	v_pk_mul_f32 v[50:51], v[192:193], s[16:17] op_sel_hi:[1,0]
	s_nop 0
	v_addc_co_u32_e32 v3, vcc, 0, v1, vcc
	v_add_co_u32_e32 v0, vcc, 0x3000, v0
	global_load_dwordx4 v[34:37], v[2:3], off offset:128
	global_load_dwordx4 v[38:41], v[2:3], off
	v_addc_co_u32_e32 v1, vcc, 0, v1, vcc
	global_load_dwordx4 v[42:45], v[0:1], off offset:128
	global_load_dwordx4 v[46:49], v[0:1], off
	v_pk_mul_f32 v[54:55], v[188:189], s[16:17] op_sel_hi:[1,0]
	v_pk_mul_f32 v[14:15], v[194:195], s[16:17] op_sel_hi:[1,0]
	v_pk_mul_f32 v[52:53], v[190:191], s[16:17] op_sel_hi:[1,0]
	s_nop 0
	v_pk_mul_f32 v[56:57], v[178:179], s[16:17] op_sel_hi:[1,0]
	v_pk_mul_f32 v[58:59], v[176:177], s[16:17] op_sel_hi:[1,0]
	v_pk_mul_f32 v[60:61], v[174:175], s[16:17] op_sel_hi:[1,0]
	v_pk_mul_f32 v[62:63], v[172:173], s[16:17] op_sel_hi:[1,0]
	v_pk_mul_f32 v[66:67], v[162:163], s[16:17] op_sel_hi:[1,0]
	v_pk_mul_f32 v[206:207], v[160:161], s[16:17] op_sel_hi:[1,0]
	v_pk_mul_f32 v[208:209], v[158:159], s[16:17] op_sel_hi:[1,0]
	v_pk_mul_f32 v[210:211], v[156:157], s[16:17] op_sel_hi:[1,0]
	s_nop 0
	s_nop 0
	s_nop 0
	v_pk_mul_f32 v[214:215], v[144:145], s[16:17] op_sel_hi:[1,0]
	v_pk_mul_f32 v[216:217], v[142:143], s[16:17] op_sel_hi:[1,0]
	v_pk_mul_f32 v[218:219], v[140:141], s[16:17] op_sel_hi:[1,0]
	s_nop 0
	s_nop 0
	v_pk_mul_f32 v[212:213], v[146:147], s[16:17] op_sel_hi:[1,0]
	s_nop 0
	s_nop 0
	s_ashr_i32 s27, s26, 31
	s_lshl_b64 s[8:9], s[26:27], 6
	s_add_u32 s8, s66, s8
	s_addc_u32 s9, s67, s9
	s_mov_b64 s[34:35], -1
	s_waitcnt vmcnt(0)
	v_pk_mul_f32 v[222:223], v[54:55], v[18:19]
	v_pk_mul_f32 v[18:19], v[50:51], v[18:19]
	v_pk_mul_f32 v[220:221], v[52:53], v[20:21]
	v_pk_mul_f32 v[20:21], v[14:15], v[20:21]
	v_pk_fma_f32 v[18:19], v[54:55], v[22:23], v[18:19]
	v_pk_fma_f32 v[14:15], v[14:15], v[24:25], v[220:221] neg_lo:[0,0,1] neg_hi:[0,0,1]
	v_pk_fma_f32 v[50:51], v[50:51], v[22:23], v[222:223] neg_lo:[0,0,1] neg_hi:[0,0,1]
	v_pk_fma_f32 v[20:21], v[52:53], v[24:25], v[20:21]
	v_cvt_pk_fp8_f32 v1, v18, v19
	v_pk_mul_f32 v[18:19], v[60:61], v[28:29]
	v_pk_mul_f32 v[22:23], v[62:63], v[26:27]
	v_pk_mul_f32 v[24:25], v[56:57], v[28:29]
	v_pk_mul_f32 v[26:27], v[58:59], v[26:27]
	v_pk_fma_f32 v[18:19], v[56:57], v[32:33], v[18:19] neg_lo:[0,0,1] neg_hi:[0,0,1]
	v_pk_fma_f32 v[22:23], v[58:59], v[30:31], v[22:23] neg_lo:[0,0,1] neg_hi:[0,0,1]
	v_pk_fma_f32 v[24:25], v[60:61], v[32:33], v[24:25]
	v_pk_fma_f32 v[26:27], v[62:63], v[30:31], v[26:27]
	v_pk_mul_f32 v[28:29], v[208:209], v[36:37]
	v_pk_mul_f32 v[30:31], v[210:211], v[34:35]
	v_pk_mul_f32 v[32:33], v[66:67], v[36:37]
	v_pk_mul_f32 v[34:35], v[206:207], v[34:35]
	v_cvt_pk_fp8_f32 v0, v50, v51
	v_cvt_pk_fp8_f32 v2, v22, v23
	v_cvt_pk_fp8_f32 v3, v26, v27
	v_pk_fma_f32 v[22:23], v[66:67], v[40:41], v[28:29] neg_lo:[0,0,1] neg_hi:[0,0,1]
	v_pk_fma_f32 v[26:27], v[206:207], v[38:39], v[30:31] neg_lo:[0,0,1] neg_hi:[0,0,1]
	v_pk_fma_f32 v[28:29], v[208:209], v[40:41], v[32:33]
	v_pk_fma_f32 v[30:31], v[210:211], v[38:39], v[34:35]
	v_pk_mul_f32 v[32:33], v[216:217], v[44:45]
	v_pk_mul_f32 v[34:35], v[218:219], v[42:43]
	v_pk_mul_f32 v[36:37], v[214:215], v[42:43]
	v_cvt_pk_fp8_f32 v4, v26, v27
	v_cvt_pk_fp8_f32 v5, v30, v31
	v_pk_fma_f32 v[26:27], v[212:213], v[48:49], v[32:33] neg_lo:[0,0,1] neg_hi:[0,0,1]
	v_pk_fma_f32 v[30:31], v[214:215], v[46:47], v[34:35] neg_lo:[0,0,1] neg_hi:[0,0,1]
	v_pk_fma_f32 v[32:33], v[218:219], v[46:47], v[36:37]
	v_cvt_pk_fp8_f32 v6, v30, v31
	v_cvt_pk_fp8_f32 v7, v32, v33
	v_cvt_pk_fp8_f32 v0, v14, v15 op_sel:[0,0,1]
	v_pk_mul_f32 v[14:15], v[212:213], v[44:45]
	v_cvt_pk_fp8_f32 v1, v20, v21 op_sel:[0,0,1]
	v_pk_fma_f32 v[14:15], v[216:217], v[48:49], v[14:15]
	v_cvt_pk_fp8_f32 v2, v18, v19 op_sel:[0,0,1]
	v_cvt_pk_fp8_f32 v3, v24, v25 op_sel:[0,0,1]
	v_cvt_pk_fp8_f32 v4, v22, v23 op_sel:[0,0,1]
	v_cvt_pk_fp8_f32 v5, v28, v29 op_sel:[0,0,1]
	v_cvt_pk_fp8_f32 v6, v26, v27 op_sel:[0,0,1]
	v_cvt_pk_fp8_f32 v7, v14, v15 op_sel:[0,0,1]
	v_permlane32_swap_b32_e32 v0, v2
	v_permlane32_swap_b32_e32 v1, v3
	v_permlane32_swap_b32_e32 v4, v6
	v_permlane32_swap_b32_e32 v5, v7
	v_permlane16_swap_b32_e32 v0, v1
	v_permlane16_swap_b32_e32 v2, v3
	v_permlane16_swap_b32_e32 v4, v5
	v_permlane16_swap_b32_e32 v6, v7
	v_lshl_add_u64 v[14:15], s[8:9], 0, v[10:11]
	s_branch .LBB0_3217

.LBB0_3226:
	s_or_b64 exec, exec, s[34:35]
	s_waitcnt lgkmcnt(0)
	s_nop 0
	v_cvt_pk_fp8_f32 v138, v6, v7
	s_nop 0
	v_cvt_pk_fp8_f32 v6, v136, v137
	s_nop 0
	v_cvt_pk_fp8_f32 v136, v4, v5
	s_nop 0
	v_cvt_pk_fp8_f32 v3, v42, v43
	s_nop 0
	v_cvt_pk_fp8_f32 v136, v44, v45 op_sel:[0,0,1]
	s_nop 0
	s_nop 0
	s_nop 0
	v_cvt_pk_fp8_f32 v44, v32, v33
	v_cvt_pk_fp8_f32 v45, v34, v35
	v_cvt_pk_fp8_f32 v42, v0, v1
	v_cvt_pk_fp8_f32 v43, v18, v19
	s_ashr_i32 s27, s26, 31
	s_nop 0
	s_nop 0
	s_lshl_b64 s[30:31], s[26:27], 10
	v_cvt_pk_fp8_f32 v139, v62, v63
	s_nop 0
	v_cvt_pk_fp8_f32 v137, v48, v49
	s_nop 0
	s_nop 0
	s_nop 0
	s_nop 0
	s_nop 0
	s_add_u32 s27, s52, s30
	v_cvt_pk_fp8_f32 v7, v132, v133
	v_cvt_pk_fp8_f32 v4, v52, v53
	v_cvt_pk_fp8_f32 v5, v56, v57
	v_cvt_pk_fp8_f32 v2, v38, v39
	v_cvt_pk_fp8_f32 v0, v22, v23
	v_cvt_pk_fp8_f32 v1, v26, v27
	s_addc_u32 s30, s53, s31
	v_cvt_pk_fp8_f32 v44, v28, v29 op_sel:[0,0,1]
	v_cvt_pk_fp8_f32 v45, v30, v31 op_sel:[0,0,1]
	v_cvt_pk_fp8_f32 v42, v14, v15 op_sel:[0,0,1]
	v_cvt_pk_fp8_f32 v43, v16, v17 op_sel:[0,0,1]
	s_add_u32 s27, s27, s21
	s_addc_u32 s31, s30, s38
	v_cvt_pk_fp8_f32 v138, v58, v59 op_sel:[0,0,1]
	v_cvt_pk_fp8_f32 v139, v60, v61 op_sel:[0,0,1]
	v_cvt_pk_fp8_f32 v137, v46, v47 op_sel:[0,0,1]
	s_add_u32 s30, s27, s56
	v_cvt_pk_fp8_f32 v6, v66, v67 op_sel:[0,0,1]
	v_cvt_pk_fp8_f32 v7, v134, v135 op_sel:[0,0,1]
	v_cvt_pk_fp8_f32 v4, v50, v51 op_sel:[0,0,1]
	v_cvt_pk_fp8_f32 v5, v54, v55 op_sel:[0,0,1]
	v_cvt_pk_fp8_f32 v2, v36, v37 op_sel:[0,0,1]
	v_cvt_pk_fp8_f32 v3, v40, v41 op_sel:[0,0,1]
	v_cvt_pk_fp8_f32 v0, v20, v21 op_sel:[0,0,1]
	v_cvt_pk_fp8_f32 v1, v24, v25 op_sel:[0,0,1]
	s_addc_u32 s31, s31, 0
	v_permlane32_swap_b32_e32 v42, v44
	v_permlane32_swap_b32_e32 v43, v45
	v_lshl_add_u64 v[14:15], s[30:31], 0, v[8:9]
	s_nop 0
	v_permlane16_swap_b32_e32 v42, v43
	v_permlane16_swap_b32_e32 v44, v45
	v_lshl_add_u64 v[16:17], v[14:15], 0, v[64:65]
	v_permlane32_swap_b32_e32 v136, v138
	v_permlane32_swap_b32_e32 v137, v139
	global_store_dwordx4 v[16:17], v[42:45], off
	v_add_co_u32_e32 v16, vcc, s63, v16
	v_permlane16_swap_b32_e32 v136, v137
	v_permlane16_swap_b32_e32 v138, v139
	v_addc_co_u32_e32 v17, vcc, 0, v17, vcc
	v_permlane32_swap_b32_e32 v0, v2
	v_permlane32_swap_b32_e32 v1, v3
	v_permlane32_swap_b32_e32 v4, v6
	v_permlane32_swap_b32_e32 v5, v7
	global_store_dwordx4 v[16:17], v[136:139], off
	v_permlane16_swap_b32_e32 v0, v1
	v_permlane16_swap_b32_e32 v2, v3
	v_permlane16_swap_b32_e32 v4, v5
	v_permlane16_swap_b32_e32 v6, v7
	v_lshl_add_u64 v[14:15], v[14:15], 0, s[2:3]
	s_mov_b64 s[36:37], 0x8000
	s_cbranch_execnz .LBB0_3231

.LBB0_3228:
	s_mov_b64 s[28:29], 0
	s_and_b64 vcc, exec, s[10:11]
	s_mov_b64 s[30:31], 0
	s_cbranch_vccz .LBB0_3233
	s_and_b32 s27, s26, 0xfc0
	v_or_b32_e32 v2, s27, v205
	v_lshl_add_u64 v[0:1], v[12:13], 2, s[12:13]
	v_lshlrev_b32_e32 v2, 8, v2
	v_mov_b32_e32 v3, v65
	v_lshl_add_u64 v[0:1], v[0:1], 0, v[2:3]
	v_add_co_u32_e32 v2, vcc, 0x1000, v0
	global_load_dwordx4 v[12:15], v[0:1], off offset:128
	global_load_dwordx4 v[16:19], v[0:1], off
	v_addc_co_u32_e32 v3, vcc, 0, v1, vcc
	global_load_dwordx4 v[20:23], v[2:3], off offset:128
	global_load_dwordx4 v[24:27], v[2:3], off
	v_add_co_u32_e32 v2, vcc, s48, v0
	s_waitcnt lgkmcnt(0)
	v_pk_mul_f32 v[46:47], v[128:129], s[16:17] op_sel_hi:[1,0]
	v_addc_co_u32_e32 v3, vcc, 0, v1, vcc
	v_add_co_u32_e32 v0, vcc, 0x3000, v0
	global_load_dwordx4 v[28:31], v[2:3], off offset:128
	global_load_dwordx4 v[32:35], v[2:3], off
	v_addc_co_u32_e32 v1, vcc, 0, v1, vcc
	global_load_dwordx4 v[36:39], v[0:1], off offset:128
	global_load_dwordx4 v[40:43], v[0:1], off
	v_pk_mul_f32 v[50:51], v[124:125], s[16:17] op_sel_hi:[1,0]
	v_pk_mul_f32 v[58:59], v[108:109], s[16:17] op_sel_hi:[1,0]
	v_pk_mul_f32 v[54:55], v[112:113], s[16:17] op_sel_hi:[1,0]
	s_nop 0
	v_pk_mul_f32 v[44:45], v[130:131], s[16:17] op_sel_hi:[1,0]
	v_pk_mul_f32 v[48:49], v[126:127], s[16:17] op_sel_hi:[1,0]
	s_nop 0
	v_pk_mul_f32 v[52:53], v[114:115], s[16:17] op_sel_hi:[1,0]
	v_pk_mul_f32 v[56:57], v[110:111], s[16:17] op_sel_hi:[1,0]
	v_pk_mul_f32 v[62:63], v[96:97], s[16:17] op_sel_hi:[1,0]
	v_pk_mul_f32 v[132:133], v[92:93], s[16:17] op_sel_hi:[1,0]
	s_nop 0
	v_pk_mul_f32 v[60:61], v[98:99], s[16:17] op_sel_hi:[1,0]
	v_pk_mul_f32 v[66:67], v[94:95], s[16:17] op_sel_hi:[1,0]
	v_pk_mul_f32 v[136:137], v[80:81], s[16:17] op_sel_hi:[1,0]
	v_pk_mul_f32 v[140:141], v[76:77], s[16:17] op_sel_hi:[1,0]
	s_nop 0
	s_nop 0
	s_nop 0
	s_nop 0
	s_nop 0
	v_pk_mul_f32 v[134:135], v[82:83], s[16:17] op_sel_hi:[1,0]
	v_pk_mul_f32 v[138:139], v[78:79], s[16:17] op_sel_hi:[1,0]
	s_ashr_i32 s27, s26, 31
	s_lshl_b64 s[30:31], s[26:27], 6
	s_add_u32 s30, s66, s30
	s_addc_u32 s31, s67, s31
	s_waitcnt vmcnt(0)
	v_pk_mul_f32 v[144:145], v[50:51], v[12:13]
	v_pk_mul_f32 v[12:13], v[46:47], v[12:13]
	v_pk_fma_f32 v[46:47], v[46:47], v[16:17], v[144:145] neg_lo:[0,0,1] neg_hi:[0,0,1]
	v_pk_fma_f32 v[12:13], v[50:51], v[16:17], v[12:13]
	v_pk_mul_f32 v[16:17], v[58:59], v[20:21]
	v_pk_mul_f32 v[142:143], v[48:49], v[14:15]
	v_pk_fma_f32 v[16:17], v[54:55], v[24:25], v[16:17] neg_lo:[0,0,1] neg_hi:[0,0,1]
	v_pk_mul_f32 v[14:15], v[44:45], v[14:15]
	v_cvt_pk_fp8_f32 v2, v16, v17
	v_pk_mul_f32 v[20:21], v[54:55], v[20:21]
	v_pk_fma_f32 v[44:45], v[44:45], v[18:19], v[142:143] neg_lo:[0,0,1] neg_hi:[0,0,1]
	v_pk_fma_f32 v[14:15], v[48:49], v[18:19], v[14:15]
	v_cvt_pk_fp8_f32 v1, v12, v13
	v_pk_mul_f32 v[12:13], v[56:57], v[22:23]
	v_pk_mul_f32 v[18:19], v[52:53], v[22:23]
	v_pk_fma_f32 v[20:21], v[58:59], v[24:25], v[20:21]
	v_pk_mul_f32 v[24:25], v[132:133], v[28:29]
	v_pk_mul_f32 v[28:29], v[62:63], v[28:29]
	v_pk_fma_f32 v[12:13], v[52:53], v[26:27], v[12:13] neg_lo:[0,0,1] neg_hi:[0,0,1]
	v_pk_fma_f32 v[18:19], v[56:57], v[26:27], v[18:19]
	v_pk_mul_f32 v[22:23], v[66:67], v[30:31]
	v_pk_mul_f32 v[26:27], v[60:61], v[30:31]
	v_cvt_pk_fp8_f32 v3, v20, v21
	v_pk_fma_f32 v[20:21], v[62:63], v[32:33], v[24:25] neg_lo:[0,0,1] neg_hi:[0,0,1]
	v_pk_fma_f32 v[24:25], v[132:133], v[32:33], v[28:29]
	v_pk_mul_f32 v[28:29], v[140:141], v[36:37]
	v_pk_mul_f32 v[30:31], v[136:137], v[36:37]
	v_cvt_pk_fp8_f32 v5, v24, v25
	v_pk_fma_f32 v[24:25], v[136:137], v[40:41], v[28:29] neg_lo:[0,0,1] neg_hi:[0,0,1]
	v_cvt_pk_fp8_f32 v2, v12, v13 op_sel:[0,0,1]
	v_pk_fma_f32 v[12:13], v[140:141], v[40:41], v[30:31]
	v_cvt_pk_fp8_f32 v0, v46, v47
	v_cvt_pk_fp8_f32 v4, v20, v21
	v_cvt_pk_fp8_f32 v6, v24, v25
	v_cvt_pk_fp8_f32 v7, v12, v13
	v_pk_fma_f32 v[16:17], v[60:61], v[34:35], v[22:23] neg_lo:[0,0,1] neg_hi:[0,0,1]
	v_pk_fma_f32 v[22:23], v[66:67], v[34:35], v[26:27]
	v_pk_mul_f32 v[26:27], v[138:139], v[38:39]
	v_pk_mul_f32 v[12:13], v[134:135], v[38:39]
	v_pk_fma_f32 v[20:21], v[134:135], v[42:43], v[26:27] neg_lo:[0,0,1] neg_hi:[0,0,1]
	v_pk_fma_f32 v[12:13], v[138:139], v[42:43], v[12:13]
	v_cvt_pk_fp8_f32 v0, v44, v45 op_sel:[0,0,1]
	v_cvt_pk_fp8_f32 v1, v14, v15 op_sel:[0,0,1]
	v_cvt_pk_fp8_f32 v3, v18, v19 op_sel:[0,0,1]
	v_cvt_pk_fp8_f32 v4, v16, v17 op_sel:[0,0,1]
	v_cvt_pk_fp8_f32 v5, v22, v23 op_sel:[0,0,1]
	v_cvt_pk_fp8_f32 v6, v20, v21 op_sel:[0,0,1]
	v_cvt_pk_fp8_f32 v7, v12, v13 op_sel:[0,0,1]
	v_permlane32_swap_b32_e32 v0, v2
	v_permlane32_swap_b32_e32 v1, v3
	v_permlane32_swap_b32_e32 v4, v6
	v_permlane32_swap_b32_e32 v5, v7
	v_permlane16_swap_b32_e32 v0, v1
	v_permlane16_swap_b32_e32 v2, v3
	v_permlane16_swap_b32_e32 v4, v5
	v_permlane16_swap_b32_e32 v6, v7
	v_lshl_add_u64 v[14:15], s[30:31], 0, v[10:11]
	s_mov_b64 s[30:31], -1
	s_branch .LBB0_3233

.LBB0_3242:
	s_or_b64 exec, exec, s[28:29]
	s_waitcnt lgkmcnt(0)
	s_nop 0
	v_cvt_pk_fp8_f32 v70, v6, v7
	s_nop 0
	v_cvt_pk_fp8_f32 v7, v68, v69
	s_nop 0
	v_cvt_pk_fp8_f32 v68, v4, v5
	s_nop 0
	v_cvt_pk_fp8_f32 v3, v38, v39
	s_nop 0
	v_cvt_pk_fp8_f32 v68, v40, v41 op_sel:[0,0,1]
	s_nop 0
	s_nop 0
	s_nop 0
	v_cvt_pk_fp8_f32 v40, v28, v29
	v_cvt_pk_fp8_f32 v41, v30, v31
	v_cvt_pk_fp8_f32 v38, v0, v1
	v_cvt_pk_fp8_f32 v39, v14, v15
	s_ashr_i32 s27, s26, 31
	s_nop 0
	s_nop 0
	s_nop 0
	s_nop 0
	s_nop 0
	s_nop 0
	s_nop 0
	s_nop 0
	s_lshl_b64 s[6:7], s[26:27], 10
	v_cvt_pk_fp8_f32 v71, v58, v59
	v_cvt_pk_fp8_f32 v6, v62, v63
	v_cvt_pk_fp8_f32 v69, v44, v45
	v_cvt_pk_fp8_f32 v4, v48, v49
	v_cvt_pk_fp8_f32 v5, v52, v53
	v_cvt_pk_fp8_f32 v2, v34, v35
	v_cvt_pk_fp8_f32 v0, v18, v19
	v_cvt_pk_fp8_f32 v1, v22, v23
	s_add_u32 s6, s52, s6
	s_addc_u32 s7, s53, s7
	v_cvt_pk_fp8_f32 v40, v24, v25 op_sel:[0,0,1]
	v_cvt_pk_fp8_f32 v41, v26, v27 op_sel:[0,0,1]
	v_cvt_pk_fp8_f32 v38, v10, v11 op_sel:[0,0,1]
	v_cvt_pk_fp8_f32 v39, v12, v13 op_sel:[0,0,1]
	s_add_u32 s6, s6, s21
	s_addc_u32 s7, s7, s38
	v_cvt_pk_fp8_f32 v70, v54, v55 op_sel:[0,0,1]
	v_cvt_pk_fp8_f32 v71, v56, v57 op_sel:[0,0,1]
	v_cvt_pk_fp8_f32 v6, v60, v61 op_sel:[0,0,1]
	v_cvt_pk_fp8_f32 v7, v66, v67 op_sel:[0,0,1]
	v_cvt_pk_fp8_f32 v69, v42, v43 op_sel:[0,0,1]
	v_cvt_pk_fp8_f32 v4, v46, v47 op_sel:[0,0,1]
	v_cvt_pk_fp8_f32 v5, v50, v51 op_sel:[0,0,1]
	v_cvt_pk_fp8_f32 v2, v32, v33 op_sel:[0,0,1]
	v_cvt_pk_fp8_f32 v3, v36, v37 op_sel:[0,0,1]
	v_cvt_pk_fp8_f32 v0, v16, v17 op_sel:[0,0,1]
	v_cvt_pk_fp8_f32 v1, v20, v21 op_sel:[0,0,1]
	s_add_u32 s6, s6, s56
	s_addc_u32 s7, s7, 0
	v_permlane32_swap_b32_e32 v38, v40
	v_permlane32_swap_b32_e32 v39, v41
	v_lshl_add_u64 v[8:9], s[6:7], 0, v[8:9]
	s_nop 0
	v_permlane16_swap_b32_e32 v38, v39
	v_permlane16_swap_b32_e32 v40, v41
	v_lshl_add_u64 v[10:11], v[8:9], 0, v[64:65]
	v_permlane32_swap_b32_e32 v68, v70
	v_permlane32_swap_b32_e32 v69, v71
	global_store_dwordx4 v[10:11], v[38:41], off
	v_add_co_u32_e32 v10, vcc, s63, v10
	v_permlane32_swap_b32_e32 v0, v2
	v_permlane32_swap_b32_e32 v1, v3
	v_permlane32_swap_b32_e32 v4, v6
	v_permlane32_swap_b32_e32 v5, v7
	v_permlane16_swap_b32_e32 v68, v69
	v_permlane16_swap_b32_e32 v70, v71
	v_addc_co_u32_e32 v11, vcc, 0, v11, vcc
	v_permlane16_swap_b32_e32 v0, v1
	v_permlane16_swap_b32_e32 v2, v3
	v_permlane16_swap_b32_e32 v4, v5
	v_permlane16_swap_b32_e32 v6, v7
	v_lshl_add_u64 v[14:15], v[8:9], 0, s[2:3]
	s_mov_b64 s[30:31], -1
	s_mov_b64 s[34:35], 0x8000
	global_store_dwordx4 v[10:11], v[68:71], off

.LBB0_3577:
	s_waitcnt vmcnt(15)
	v_mov_b32_e32 v128, v0
	s_waitcnt vmcnt(14)
	v_mov_b32_e32 v129, v4
	v_pk_mul_f32 v[128:129], v[128:129], s[70:71] op_sel_hi:[1,0]
	s_nop 0
	v_cvt_pk_fp8_f32 v130, v128, v129
	s_waitcnt vmcnt(13)
	v_mov_b32_e32 v128, v8
	s_waitcnt vmcnt(12)
	v_mov_b32_e32 v129, v12
	v_pk_mul_f32 v[128:129], v[128:129], s[70:71] op_sel_hi:[1,0]
	s_nop 0
	v_cvt_pk_fp8_f32 v130, v128, v129 op_sel:[0,0,1]
	v_mov_b32_e32 v128, v1
	v_mov_b32_e32 v129, v5
	v_pk_mul_f32 v[128:129], v[128:129], s[70:71] op_sel_hi:[1,0]
	s_nop 0
	v_cvt_pk_fp8_f32 v131, v128, v129
	v_mov_b32_e32 v128, v9
	v_mov_b32_e32 v129, v13
	v_pk_mul_f32 v[128:129], v[128:129], s[70:71] op_sel_hi:[1,0]
	s_nop 0
	v_cvt_pk_fp8_f32 v131, v128, v129 op_sel:[0,0,1]
	v_mov_b32_e32 v128, v2
	v_mov_b32_e32 v129, v6
	v_pk_mul_f32 v[128:129], v[128:129], s[70:71] op_sel_hi:[1,0]
	s_cmp_eq_u64 s[54:55], 0
	v_cvt_pk_fp8_f32 v134, v128, v129
	v_mov_b32_e32 v128, v10
	v_mov_b32_e32 v129, v14
	v_pk_mul_f32 v[128:129], v[128:129], s[70:71] op_sel_hi:[1,0]
	ds_write2_b32 v143, v130, v131 offset1:33
	v_cvt_pk_fp8_f32 v134, v128, v129 op_sel:[0,0,1]
	v_mov_b32_e32 v128, v3
	v_mov_b32_e32 v129, v7
	v_pk_mul_f32 v[128:129], v[128:129], s[70:71] op_sel_hi:[1,0]
	s_nop 0
	v_cvt_pk_fp8_f32 v138, v128, v129
	v_mov_b32_e32 v128, v11
	v_mov_b32_e32 v129, v15
	v_pk_mul_f32 v[128:129], v[128:129], s[70:71] op_sel_hi:[1,0]
	s_nop 0
	v_cvt_pk_fp8_f32 v138, v128, v129 op_sel:[0,0,1]
	ds_write2_b32 v143, v134, v138 offset0:66 offset1:99
	s_cbranch_scc1 .LBB0_3579
	v_lshl_add_u32 v128, s46, 7, v133
	v_ashrrev_i32_e32 v129, 31, v128
	v_lshl_add_u64 v[128:129], v[128:129], 2, s[54:55]
	global_load_dwordx4 v[128:131], v[128:129], off
	s_waitcnt vmcnt(0)
	v_pk_mul_f32 v[18:19], v[18:19], v[128:129] op_sel_hi:[1,0]
	v_pk_mul_f32 v[16:17], v[16:17], v[128:129] op_sel_hi:[1,0]
	v_pk_mul_f32 v[22:23], v[22:23], v[128:129] op_sel:[0,1]
	v_pk_mul_f32 v[20:21], v[20:21], v[128:129] op_sel:[0,1]
	v_mov_b32_e32 v128, v131
	v_pk_mul_f32 v[26:27], v[26:27], v[130:131] op_sel_hi:[1,0]
	v_pk_mul_f32 v[24:25], v[24:25], v[130:131] op_sel_hi:[1,0]
	v_pk_mul_f32 v[30:31], v[30:31], v[128:129] op_sel_hi:[1,0]
	v_pk_mul_f32 v[28:29], v[28:29], v[128:129] op_sel_hi:[1,0]
.LBB0_3579:
	s_waitcnt vmcnt(11)
	v_mov_b32_e32 v128, v16
	s_waitcnt vmcnt(10)
	v_mov_b32_e32 v129, v20
	v_pk_mul_f32 v[128:129], v[128:129], s[70:71] op_sel_hi:[1,0]
	s_nop 0
	v_cvt_pk_fp8_f32 v130, v128, v129
	s_waitcnt vmcnt(9)
	v_mov_b32_e32 v128, v24
	s_waitcnt vmcnt(8)
	v_mov_b32_e32 v129, v28
	v_pk_mul_f32 v[128:129], v[128:129], s[70:71] op_sel_hi:[1,0]
	s_nop 0
	v_cvt_pk_fp8_f32 v130, v128, v129 op_sel:[0,0,1]
	v_mov_b32_e32 v128, v17
	v_mov_b32_e32 v129, v21
	v_pk_mul_f32 v[128:129], v[128:129], s[70:71] op_sel_hi:[1,0]
	s_nop 0
	v_cvt_pk_fp8_f32 v131, v128, v129
	v_mov_b32_e32 v128, v25
	v_mov_b32_e32 v129, v29
	v_pk_mul_f32 v[128:129], v[128:129], s[70:71] op_sel_hi:[1,0]
	s_nop 0
	v_cvt_pk_fp8_f32 v131, v128, v129 op_sel:[0,0,1]
	v_mov_b32_e32 v128, v18
	v_mov_b32_e32 v129, v22
	v_pk_mul_f32 v[128:129], v[128:129], s[70:71] op_sel_hi:[1,0]
	v_add_u32_e32 v144, 0x4000, v143
	v_cvt_pk_fp8_f32 v134, v128, v129
	v_mov_b32_e32 v128, v26
	v_mov_b32_e32 v129, v30
	v_pk_mul_f32 v[128:129], v[128:129], s[70:71] op_sel_hi:[1,0]
	s_cmp_eq_u64 s[62:63], 0
	v_cvt_pk_fp8_f32 v134, v128, v129 op_sel:[0,0,1]
	v_mov_b32_e32 v128, v19
	v_mov_b32_e32 v129, v23
	v_pk_mul_f32 v[128:129], v[128:129], s[70:71] op_sel_hi:[1,0]
	s_mov_b64 s[72:73], s[22:23]
	v_cvt_pk_fp8_f32 v138, v128, v129
	v_mov_b32_e32 v128, v27
	v_mov_b32_e32 v129, v31
	v_pk_mul_f32 v[128:129], v[128:129], s[70:71] op_sel_hi:[1,0]
	s_mov_b64 s[36:37], s[20:21]
	v_cvt_pk_fp8_f32 v138, v128, v129 op_sel:[0,0,1]
	ds_write2_b32 v144, v130, v131 offset0:128 offset1:161
	ds_write2_b32 v144, v134, v138 offset0:194 offset1:227
	s_cbranch_scc1 .LBB0_3581
	v_lshl_add_u32 v128, s44, 7, v133
	v_ashrrev_i32_e32 v129, 31, v128
	v_lshl_add_u64 v[128:129], v[128:129], 2, s[62:63]
	global_load_dwordx4 v[128:131], v[128:129], off
	s_waitcnt vmcnt(0)
	v_pk_mul_f32 v[50:51], v[50:51], v[128:129] op_sel_hi:[1,0]
	v_pk_mul_f32 v[48:49], v[48:49], v[128:129] op_sel_hi:[1,0]
	v_pk_mul_f32 v[54:55], v[54:55], v[128:129] op_sel:[0,1]
	v_pk_mul_f32 v[52:53], v[52:53], v[128:129] op_sel:[0,1]
	v_mov_b32_e32 v128, v131
	v_pk_mul_f32 v[58:59], v[58:59], v[130:131] op_sel_hi:[1,0]
	v_pk_mul_f32 v[56:57], v[56:57], v[130:131] op_sel_hi:[1,0]
	v_pk_mul_f32 v[62:63], v[62:63], v[128:129] op_sel_hi:[1,0]
	v_pk_mul_f32 v[60:61], v[60:61], v[128:129] op_sel_hi:[1,0]
.LBB0_3581:
	s_waitcnt vmcnt(7)
	v_mov_b32_e32 v128, v48
	s_waitcnt vmcnt(6)
	v_mov_b32_e32 v129, v52
	v_pk_mul_f32 v[128:129], v[128:129], s[70:71] op_sel_hi:[1,0]
	s_nop 0
	v_cvt_pk_fp8_f32 v130, v128, v129
	s_waitcnt vmcnt(5)
	v_mov_b32_e32 v128, v56
	s_waitcnt vmcnt(4)
	v_mov_b32_e32 v129, v60
	v_pk_mul_f32 v[128:129], v[128:129], s[70:71] op_sel_hi:[1,0]
	s_nop 0
	v_cvt_pk_fp8_f32 v130, v128, v129 op_sel:[0,0,1]
	v_mov_b32_e32 v128, v49
	v_mov_b32_e32 v129, v53
	v_pk_mul_f32 v[128:129], v[128:129], s[70:71] op_sel_hi:[1,0]
	s_nop 0
	v_cvt_pk_fp8_f32 v131, v128, v129
	v_mov_b32_e32 v128, v57
	v_mov_b32_e32 v129, v61
	v_pk_mul_f32 v[128:129], v[128:129], s[70:71] op_sel_hi:[1,0]
	s_nop 0
	v_cvt_pk_fp8_f32 v131, v128, v129 op_sel:[0,0,1]
	v_mov_b32_e32 v128, v50
	v_mov_b32_e32 v129, v54
	v_pk_mul_f32 v[128:129], v[128:129], s[70:71] op_sel_hi:[1,0]
	v_readlane_b32 s8, v254, 39
	v_cvt_pk_fp8_f32 v134, v128, v129
	v_mov_b32_e32 v128, v58
	v_mov_b32_e32 v129, v62
	v_pk_mul_f32 v[128:129], v[128:129], s[70:71] op_sel_hi:[1,0]
	v_readlane_b32 s12, v254, 43
	v_cvt_pk_fp8_f32 v134, v128, v129 op_sel:[0,0,1]
	v_mov_b32_e32 v128, v51
	v_mov_b32_e32 v129, v55
	v_pk_mul_f32 v[128:129], v[128:129], s[70:71] op_sel_hi:[1,0]
	v_readlane_b32 s13, v254, 44
	v_cvt_pk_fp8_f32 v138, v128, v129
	v_mov_b32_e32 v128, v59
	v_mov_b32_e32 v129, v63
	v_pk_mul_f32 v[128:129], v[128:129], s[70:71] op_sel_hi:[1,0]
	v_add_u32_e32 v145, 0x8400, v143
	v_cvt_pk_fp8_f32 v138, v128, v129 op_sel:[0,0,1]
	s_cmp_eq_u64 s[12:13], 0
	ds_write2_b32 v145, v130, v131 offset1:33
	v_readlane_b32 s9, v254, 40
	v_readlane_b32 s10, v254, 41
	v_readlane_b32 s11, v254, 42
	v_readlane_b32 s14, v254, 45
	v_readlane_b32 s15, v254, 46
	v_readlane_b32 s16, v254, 47
	v_readlane_b32 s17, v254, 48
	v_readlane_b32 s18, v254, 49
	v_readlane_b32 s19, v254, 50
	v_readlane_b32 s20, v254, 51
	v_readlane_b32 s21, v254, 52
	v_readlane_b32 s22, v254, 53
	v_readlane_b32 s23, v254, 54
	ds_write2_b32 v145, v134, v138 offset0:66 offset1:99
	s_cbranch_scc1 .LBB0_3583
	v_lshl_add_u32 v128, s48, 7, v133
	v_ashrrev_i32_e32 v129, 31, v128
	v_lshl_add_u64 v[128:129], v[128:129], 2, s[12:13]
	global_load_dwordx4 v[128:131], v[128:129], off
	s_waitcnt vmcnt(0)
	v_pk_mul_f32 v[98:99], v[98:99], v[128:129] op_sel_hi:[1,0]
	v_pk_mul_f32 v[96:97], v[96:97], v[128:129] op_sel_hi:[1,0]
	v_pk_mul_f32 v[102:103], v[102:103], v[128:129] op_sel:[0,1]
	v_pk_mul_f32 v[100:101], v[100:101], v[128:129] op_sel:[0,1]
	v_mov_b32_e32 v128, v131
	v_pk_mul_f32 v[106:107], v[106:107], v[130:131] op_sel_hi:[1,0]
	v_pk_mul_f32 v[104:105], v[104:105], v[130:131] op_sel_hi:[1,0]
	v_pk_mul_f32 v[110:111], v[110:111], v[128:129] op_sel_hi:[1,0]
	v_pk_mul_f32 v[108:109], v[108:109], v[128:129] op_sel_hi:[1,0]
.LBB0_3583:
	s_waitcnt vmcnt(3)
	v_mov_b32_e32 v128, v96
	s_waitcnt vmcnt(2)
	v_mov_b32_e32 v129, v100
	v_pk_mul_f32 v[128:129], v[128:129], s[70:71] op_sel_hi:[1,0]
	s_nop 0
	v_cvt_pk_fp8_f32 v130, v128, v129
	s_waitcnt vmcnt(1)
	v_mov_b32_e32 v128, v104
	s_waitcnt vmcnt(0)
	v_mov_b32_e32 v129, v108
	v_pk_mul_f32 v[128:129], v[128:129], s[70:71] op_sel_hi:[1,0]
	s_nop 0
	v_cvt_pk_fp8_f32 v130, v128, v129 op_sel:[0,0,1]
	v_mov_b32_e32 v128, v97
	v_mov_b32_e32 v129, v101
	v_pk_mul_f32 v[128:129], v[128:129], s[70:71] op_sel_hi:[1,0]
	s_nop 0
	v_cvt_pk_fp8_f32 v131, v128, v129
	v_mov_b32_e32 v128, v105
	v_mov_b32_e32 v129, v109
	v_pk_mul_f32 v[128:129], v[128:129], s[70:71] op_sel_hi:[1,0]
	s_nop 0
	v_cvt_pk_fp8_f32 v131, v128, v129 op_sel:[0,0,1]
	v_mov_b32_e32 v128, v98
	v_mov_b32_e32 v129, v102
	v_pk_mul_f32 v[128:129], v[128:129], s[70:71] op_sel_hi:[1,0]
	v_add_u32_e32 v148, 0xc400, v143
	v_cvt_pk_fp8_f32 v134, v128, v129
	v_mov_b32_e32 v128, v106
	v_mov_b32_e32 v129, v110
	v_pk_mul_f32 v[128:129], v[128:129], s[70:71] op_sel_hi:[1,0]
	s_mov_b64 s[20:21], s[36:37]
	v_cvt_pk_fp8_f32 v134, v128, v129 op_sel:[0,0,1]
	v_mov_b32_e32 v128, v99
	v_mov_b32_e32 v129, v103
	v_pk_mul_f32 v[128:129], v[128:129], s[70:71] op_sel_hi:[1,0]
	s_mov_b64 s[22:23], s[72:73]
	v_cvt_pk_fp8_f32 v138, v128, v129
	v_mov_b32_e32 v128, v107
	v_mov_b32_e32 v129, v111
	v_pk_mul_f32 v[128:129], v[128:129], s[70:71] op_sel_hi:[1,0]
	s_cmp_lt_i32 s71, 2
	v_cvt_pk_fp8_f32 v138, v128, v129 op_sel:[0,0,1]
	ds_write2_b32 v148, v130, v131 offset0:128 offset1:161
	ds_write2_b32 v148, v134, v138 offset0:194 offset1:227
	s_waitcnt lgkmcnt(0)
	s_barrier
	ds_read2_b32 v[128:129], v142 offset1:1
	ds_read2_b32 v[130:131], v142 offset0:2 offset1:3
	v_lshl_add_u32 v134, s67, 6, v140
	s_cbranch_scc1 .LBB0_3589
	s_cmp_gt_i32 s71, 2
	s_cbranch_scc0 .LBB0_3590
	s_cmp_eq_u32 s71, 3
	s_mov_b64 s[18:19], -1
	s_cbranch_scc0 .LBB0_3587
	v_lshlrev_b32_e32 v138, 1, v134
	v_and_b32_e32 v139, 0x7f, v134
	s_movk_i32 s0, 0xff00
	v_and_or_b32 v138, v138, s0, v139
	s_mov_b64 s[18:19], 0

.LBB0_3830:
	v_mov_b32_e32 v128, v112
	v_mov_b32_e32 v129, v116
	v_pk_mul_f32 v[128:129], v[128:129], s[70:71] op_sel_hi:[1,0]
	s_nop 0
	v_cvt_pk_fp8_f32 v130, v128, v129
	v_mov_b32_e32 v128, v120
	v_mov_b32_e32 v129, v124
	v_pk_mul_f32 v[128:129], v[128:129], s[70:71] op_sel_hi:[1,0]
	s_nop 0
	v_cvt_pk_fp8_f32 v130, v128, v129 op_sel:[0,0,1]
	v_mov_b32_e32 v128, v113
	v_mov_b32_e32 v129, v117
	v_pk_mul_f32 v[128:129], v[128:129], s[70:71] op_sel_hi:[1,0]
	s_nop 0
	v_cvt_pk_fp8_f32 v131, v128, v129
	v_mov_b32_e32 v128, v121
	v_mov_b32_e32 v129, v125
	v_pk_mul_f32 v[128:129], v[128:129], s[70:71] op_sel_hi:[1,0]
	s_nop 0
	v_cvt_pk_fp8_f32 v131, v128, v129 op_sel:[0,0,1]
	v_mov_b32_e32 v128, v114
	v_mov_b32_e32 v129, v118
	v_pk_mul_f32 v[128:129], v[128:129], s[70:71] op_sel_hi:[1,0]
	s_cmp_lt_i32 s59, 2
	v_cvt_pk_fp8_f32 v134, v128, v129
	v_mov_b32_e32 v128, v122
	v_mov_b32_e32 v129, v126
	v_pk_mul_f32 v[128:129], v[128:129], s[70:71] op_sel_hi:[1,0]
	s_nop 0
	v_cvt_pk_fp8_f32 v134, v128, v129 op_sel:[0,0,1]
	v_mov_b32_e32 v128, v115
	v_mov_b32_e32 v129, v119
	v_pk_mul_f32 v[128:129], v[128:129], s[70:71] op_sel_hi:[1,0]
	s_nop 0
	v_cvt_pk_fp8_f32 v138, v128, v129
	v_mov_b32_e32 v128, v123
	v_mov_b32_e32 v129, v127
	v_pk_mul_f32 v[128:129], v[128:129], s[70:71] op_sel_hi:[1,0]
	s_nop 0
	v_cvt_pk_fp8_f32 v138, v128, v129 op_sel:[0,0,1]
	ds_write2_b32 v148, v130, v131 offset0:128 offset1:161
	ds_write2_b32 v148, v134, v138 offset0:194 offset1:227
	s_waitcnt lgkmcnt(0)
	s_barrier
	ds_read2_b32 v[128:129], v142 offset1:1
	ds_read2_b32 v[130:131], v142 offset0:2 offset1:3
	v_lshl_add_u32 v134, s2, 6, v140
	s_cbranch_scc1 .LBB0_3836
	s_cmp_gt_i32 s59, 2
	s_cbranch_scc0 .LBB0_3837
	s_cmp_eq_u32 s59, 3
	s_mov_b64 s[18:19], -1
	s_cbranch_scc0 .LBB0_3834
	v_lshlrev_b32_e32 v138, 1, v134
	v_and_b32_e32 v139, 0x7f, v134
	s_movk_i32 s1, 0xff00
	v_and_or_b32 v138, v138, s1, v139
	s_mov_b64 s[18:19], 0

.LBB0_4001:
	v_lshl_add_u32 v184, v185, 2, s50
	ds_read_b32 v130, v184
	v_and_b32_e32 v178, -16, v129
	s_mov_b64 s[6:7], -1
	s_and_b64 vcc, exec, s[72:73]
	s_waitcnt lgkmcnt(0)
	v_mov_b32_e32 v131, v130
	s_cbranch_vccz .LBB0_4003
	v_pk_mul_f32 v[150:151], v[120:121], v[130:131]
	s_nop 0
	v_add_u32_e32 v132, s50, v178
	v_cvt_pk_fp8_f32 v128, v150, v151
	ds_read_b128 v[150:153], v132
	v_mov_b32_e32 v172, v130
	v_mov_b32_e32 v173, v130
	v_pk_mul_f32 v[174:175], v[122:123], v[172:173]
	s_nop 0
	v_cvt_pk_fp8_f32 v128, v174, v175 op_sel:[0,0,1]
	v_pk_mul_f32 v[174:175], v[124:125], v[130:131]
	s_nop 0
	v_cvt_pk_fp8_f32 v186, v174, v175
	s_waitcnt lgkmcnt(0)
	v_pk_mul_f32 v[174:175], v[116:117], v[150:151]
	v_pk_mul_f32 v[172:173], v[126:127], v[172:173]
	v_cvt_pk_fp8_f32 v132, v174, v175
	v_cvt_pk_fp8_f32 v186, v172, v173 op_sel:[0,0,1]
	v_pk_mul_f32 v[172:173], v[118:119], v[152:153]
	v_pk_mul_f32 v[152:153], v[114:115], v[152:153]
	v_cvt_pk_fp8_f32 v132, v172, v173 op_sel:[0,0,1]
	v_pk_mul_f32 v[150:151], v[112:113], v[150:151]
	s_mov_b64 s[6:7], 0
.LBB0_4003:
	s_andn2_b64 vcc, exec, s[6:7]
	s_cbranch_vccnz .LBB0_4005
	v_pk_mul_f32 v[124:125], v[124:125], v[130:131]
	v_pk_mul_f32 v[120:121], v[120:121], v[130:131]
	s_waitcnt vmcnt(0)
	v_pk_mul_f32 v[172:173], v[162:163], v[124:125]
	v_pk_mul_f32 v[186:187], v[166:167], v[124:125]
	v_pk_fma_f32 v[172:173], v[166:167], v[120:121], v[172:173] neg_lo:[0,0,1] neg_hi:[0,0,1]
	v_pk_fma_f32 v[186:187], v[162:163], v[120:121], v[186:187]
	v_mov_b32_e32 v150, v130
	v_mov_b32_e32 v151, v130
	v_cndmask_b32_e64 v121, v121, v173, s[4:5]
	v_cndmask_b32_e64 v120, v120, v172, s[4:5]
	v_cndmask_b32_e64 v125, v125, v187, s[4:5]
	v_cndmask_b32_e64 v124, v124, v186, s[4:5]
	s_nop 0
	s_nop 0
	v_pk_mul_f32 v[126:127], v[126:127], v[150:151]
	v_cvt_pk_fp8_f32 v128, v120, v121
	v_cvt_pk_fp8_f32 v186, v124, v125
	v_pk_mul_f32 v[122:123], v[122:123], v[150:151]
	v_pk_mul_f32 v[152:153], v[164:165], v[126:127]
	v_pk_mul_f32 v[174:175], v[168:169], v[126:127]
	v_pk_fma_f32 v[152:153], v[168:169], v[122:123], v[152:153] neg_lo:[0,0,1] neg_hi:[0,0,1]
	v_pk_fma_f32 v[174:175], v[164:165], v[122:123], v[174:175]
	v_cndmask_b32_e64 v123, v123, v153, s[4:5]
	v_cndmask_b32_e64 v122, v122, v152, s[4:5]
	v_cndmask_b32_e64 v120, v127, v175, s[4:5]
	v_cndmask_b32_e64 v121, v126, v174, s[4:5]
	v_pk_mul_f32 v[114:115], v[114:115], v[150:151]
	v_pk_mul_f32 v[112:113], v[112:113], v[130:131]
	v_cvt_pk_fp8_f32 v128, v122, v123 op_sel:[0,0,1]
	v_cvt_pk_fp8_f32 v186, v121, v120 op_sel:[0,0,1]
	v_pk_mul_f32 v[118:119], v[118:119], v[150:151]
	v_pk_mul_f32 v[116:117], v[116:117], v[130:131]
	s_xor_b64 s[6:7], s[4:5], -1
	v_pk_mul_f32 v[120:121], v[164:165], v[114:115]
	v_pk_mul_f32 v[122:123], v[162:163], v[112:113]
	v_pk_fma_f32 v[120:121], v[168:169], v[118:119], v[120:121] neg_lo:[0,0,1] neg_hi:[0,0,1]
	v_pk_fma_f32 v[122:123], v[166:167], v[116:117], v[122:123] neg_lo:[0,0,1] neg_hi:[0,0,1]
	v_pk_mul_f32 v[124:125], v[168:169], v[114:115]
	s_and_b64 vcc, s[6:7], s[30:31]
	v_pk_fma_f32 v[124:125], v[164:165], v[118:119], v[124:125]
	v_cndmask_b32_e32 v119, v119, v121, vcc
	v_cndmask_b32_e32 v121, v117, v123, vcc
	v_cndmask_b32_e32 v122, v116, v122, vcc
	s_nop 0
	v_cvt_pk_fp8_f32 v132, v122, v121
	v_cndmask_b32_e32 v118, v118, v120, vcc
	v_pk_mul_f32 v[126:127], v[166:167], v[112:113]
	v_cndmask_b32_e32 v153, v115, v125, vcc
	v_cvt_pk_fp8_f32 v132, v118, v119 op_sel:[0,0,1]
	v_pk_fma_f32 v[116:117], v[162:163], v[116:117], v[126:127]
	v_cndmask_b32_e32 v152, v114, v124, vcc
	v_cndmask_b32_e32 v151, v113, v117, vcc
	v_cndmask_b32_e32 v150, v112, v116, vcc
.LBB0_4005:
	ds_read_b32 v116, v184 offset:64
	v_cndmask_b32_e64 v112, 0, 1, s[72:73]
	v_cmp_ne_u32_e64 s[6:7], 1, v112
	s_andn2_b64 vcc, exec, s[72:73]
	s_mov_b64 s[34:35], -1
	s_waitcnt lgkmcnt(0)
	v_mov_b32_e32 v117, v116
	s_cbranch_vccnz .LBB0_4007
	v_pk_mul_f32 v[112:113], v[108:109], v[116:117]
	s_nop 0
	v_cvt_pk_fp8_f32 v118, v112, v113
	v_add_u32_e32 v112, s50, v178
	ds_read_b128 v[112:115], v112 offset:64
	v_mov_b32_e32 v120, v116
	v_mov_b32_e32 v121, v116
	v_pk_mul_f32 v[122:123], v[110:111], v[120:121]
	s_nop 0
	v_cvt_pk_fp8_f32 v118, v122, v123 op_sel:[0,0,1]
	v_pk_mul_f32 v[122:123], v[104:105], v[116:117]
	s_nop 0
	v_cvt_pk_fp8_f32 v131, v122, v123
	s_waitcnt lgkmcnt(0)
	v_pk_mul_f32 v[122:123], v[100:101], v[112:113]
	v_pk_mul_f32 v[120:121], v[106:107], v[120:121]
	v_cvt_pk_fp8_f32 v119, v122, v123
	v_cvt_pk_fp8_f32 v131, v120, v121 op_sel:[0,0,1]
	v_pk_mul_f32 v[120:121], v[102:103], v[114:115]
	v_pk_mul_f32 v[114:115], v[98:99], v[114:115]
	v_cvt_pk_fp8_f32 v119, v120, v121 op_sel:[0,0,1]
	v_pk_mul_f32 v[112:113], v[96:97], v[112:113]
	s_mov_b64 s[34:35], 0
.LBB0_4007:
	s_andn2_b64 vcc, exec, s[34:35]
	s_waitcnt vmcnt(0)
	v_mov_b32_e32 v169, v179
	s_cbranch_vccnz .LBB0_4009
	v_pk_mul_f32 v[104:105], v[104:105], v[116:117]
	v_pk_mul_f32 v[108:109], v[108:109], v[116:117]
	v_pk_mul_f32 v[120:121], v[158:159], v[104:105]
	v_mov_b32_e32 v112, v116
	v_pk_fma_f32 v[120:121], v[154:155], v[108:109], v[120:121]
	v_mov_b32_e32 v113, v116
	v_pk_mul_f32 v[114:115], v[154:155], v[104:105]
	v_cndmask_b32_e64 v105, v105, v121, s[4:5]
	v_cndmask_b32_e64 v104, v104, v120, s[4:5]
	s_nop 0
	v_pk_mul_f32 v[106:107], v[106:107], v[112:113]
	v_cvt_pk_fp8_f32 v131, v104, v105
	v_pk_mul_f32 v[110:111], v[110:111], v[112:113]
	v_pk_mul_f32 v[122:123], v[160:161], v[106:107]
	v_pk_mul_f32 v[118:119], v[156:157], v[106:107]
	v_pk_fma_f32 v[122:123], v[156:157], v[110:111], v[122:123]
	v_pk_fma_f32 v[118:119], v[160:161], v[110:111], v[118:119] neg_lo:[0,0,1] neg_hi:[0,0,1]
	v_pk_fma_f32 v[114:115], v[158:159], v[108:109], v[114:115] neg_lo:[0,0,1] neg_hi:[0,0,1]
	v_cndmask_b32_e64 v104, v107, v123, s[4:5]
	v_cndmask_b32_e64 v105, v106, v122, s[4:5]
	v_pk_mul_f32 v[96:97], v[96:97], v[116:117]
	v_cndmask_b32_e64 v110, v110, v118, s[4:5]
	v_cndmask_b32_e64 v109, v109, v115, s[4:5]
	v_cndmask_b32_e64 v108, v108, v114, s[4:5]
	s_nop 0
	v_cvt_pk_fp8_f32 v131, v105, v104 op_sel:[0,0,1]
	v_pk_mul_f32 v[100:101], v[100:101], v[116:117]
	s_xor_b64 s[34:35], s[4:5], -1
	v_pk_mul_f32 v[104:105], v[154:155], v[96:97]
	v_cvt_pk_fp8_f32 v118, v108, v109
	v_pk_fma_f32 v[104:105], v[158:159], v[100:101], v[104:105] neg_lo:[0,0,1] neg_hi:[0,0,1]
	s_and_b64 vcc, s[34:35], s[30:31]
	v_cndmask_b32_e64 v111, v111, v119, s[4:5]
	v_cndmask_b32_e32 v105, v101, v105, vcc
	v_cndmask_b32_e32 v104, v100, v104, vcc
	s_nop 0
	v_pk_mul_f32 v[98:99], v[98:99], v[112:113]
	v_cvt_pk_fp8_f32 v119, v104, v105
	v_pk_mul_f32 v[102:103], v[102:103], v[112:113]
	v_pk_mul_f32 v[106:107], v[156:157], v[98:99]
	v_cvt_pk_fp8_f32 v118, v110, v111 op_sel:[0,0,1]
	v_pk_fma_f32 v[106:107], v[160:161], v[102:103], v[106:107] neg_lo:[0,0,1] neg_hi:[0,0,1]
	v_pk_mul_f32 v[110:111], v[160:161], v[98:99]
	v_pk_mul_f32 v[108:109], v[158:159], v[96:97]
	v_pk_fma_f32 v[110:111], v[156:157], v[102:103], v[110:111]
	v_cndmask_b32_e32 v103, v103, v107, vcc
	v_cndmask_b32_e32 v102, v102, v106, vcc
	v_cvt_pk_fp8_f32 v119, v102, v103 op_sel:[0,0,1]
	v_pk_fma_f32 v[100:101], v[154:155], v[100:101], v[108:109]
	v_cndmask_b32_e32 v115, v99, v111, vcc
	v_cndmask_b32_e32 v114, v98, v110, vcc
	v_cndmask_b32_e32 v113, v97, v101, vcc
	v_cndmask_b32_e32 v112, v96, v100, vcc
.LBB0_4009:
	ds_read_b32 v98, v184 offset:128
	s_and_b64 vcc, exec, s[6:7]
	s_mov_b64 s[34:35], -1
	s_waitcnt lgkmcnt(0)
	v_mov_b32_e32 v99, v98
	s_cbranch_vccnz .LBB0_4011
	v_pk_mul_f32 v[100:101], v[92:93], v[98:99]
	s_nop 0
	v_add_u32_e32 v97, s50, v178
	v_cvt_pk_fp8_f32 v96, v100, v101
	ds_read_b128 v[102:105], v97 offset:128
	v_mov_b32_e32 v106, v98
	v_mov_b32_e32 v107, v98
	v_pk_mul_f32 v[100:101], v[94:95], v[106:107]
	s_nop 0
	v_cvt_pk_fp8_f32 v96, v100, v101 op_sel:[0,0,1]
	v_pk_mul_f32 v[100:101], v[88:89], v[98:99]
	s_waitcnt lgkmcnt(0)
	v_pk_mul_f32 v[108:109], v[84:85], v[102:103]
	v_cvt_pk_fp8_f32 v97, v100, v101
	s_nop 0
	v_cvt_pk_fp8_f32 v100, v108, v109
	v_pk_mul_f32 v[106:107], v[90:91], v[106:107]
	v_pk_mul_f32 v[102:103], v[80:81], v[102:103]
	v_cvt_pk_fp8_f32 v97, v106, v107 op_sel:[0,0,1]
	v_pk_mul_f32 v[106:107], v[86:87], v[104:105]
	v_pk_mul_f32 v[104:105], v[82:83], v[104:105]
	v_cvt_pk_fp8_f32 v100, v106, v107 op_sel:[0,0,1]
	s_mov_b64 s[34:35], 0
.LBB0_4011:
	s_andn2_b64 vcc, exec, s[34:35]
	s_cbranch_vccnz .LBB0_4013
	v_pk_mul_f32 v[88:89], v[88:89], v[98:99]
	v_pk_mul_f32 v[92:93], v[92:93], v[98:99]
	v_pk_mul_f32 v[96:97], v[142:143], v[88:89]
	v_pk_mul_f32 v[104:105], v[146:147], v[88:89]
	v_pk_fma_f32 v[96:97], v[146:147], v[92:93], v[96:97] neg_lo:[0,0,1] neg_hi:[0,0,1]
	v_pk_fma_f32 v[104:105], v[142:143], v[92:93], v[104:105]
	v_mov_b32_e32 v100, v98
	v_mov_b32_e32 v101, v98
	v_cndmask_b32_e64 v93, v93, v97, s[4:5]
	v_cndmask_b32_e64 v89, v89, v105, s[4:5]
	v_cndmask_b32_e64 v88, v88, v104, s[4:5]
	s_nop 0
	v_pk_mul_f32 v[90:91], v[90:91], v[100:101]
	v_cvt_pk_fp8_f32 v97, v88, v89
	v_pk_mul_f32 v[94:95], v[94:95], v[100:101]
	v_pk_mul_f32 v[106:107], v[148:149], v[90:91]
	v_pk_mul_f32 v[80:81], v[80:81], v[98:99]
	v_pk_fma_f32 v[106:107], v[144:145], v[94:95], v[106:107]
	v_cndmask_b32_e64 v92, v92, v96, s[4:5]
	v_cndmask_b32_e64 v88, v91, v107, s[4:5]
	v_cndmask_b32_e64 v89, v90, v106, s[4:5]
	s_nop 0
	v_cvt_pk_fp8_f32 v97, v89, v88 op_sel:[0,0,1]
	v_pk_mul_f32 v[84:85], v[84:85], v[98:99]
	s_xor_b64 s[34:35], s[4:5], -1
	v_pk_mul_f32 v[88:89], v[142:143], v[80:81]
	v_cvt_pk_fp8_f32 v96, v92, v93
	v_pk_fma_f32 v[88:89], v[146:147], v[84:85], v[88:89] neg_lo:[0,0,1] neg_hi:[0,0,1]
	s_and_b64 vcc, s[34:35], s[30:31]
	v_pk_mul_f32 v[102:103], v[144:145], v[90:91]
	v_pk_mul_f32 v[86:87], v[86:87], v[100:101]
	v_pk_mul_f32 v[82:83], v[82:83], v[100:101]
	v_cndmask_b32_e32 v89, v85, v89, vcc
	v_cndmask_b32_e32 v88, v84, v88, vcc
	s_nop 0
	v_pk_fma_f32 v[102:103], v[148:149], v[94:95], v[102:103] neg_lo:[0,0,1] neg_hi:[0,0,1]
	v_cvt_pk_fp8_f32 v100, v88, v89
	v_cndmask_b32_e64 v95, v95, v103, s[4:5]
	v_cndmask_b32_e64 v94, v94, v102, s[4:5]
	v_pk_mul_f32 v[90:91], v[144:145], v[82:83]
	v_cvt_pk_fp8_f32 v96, v94, v95 op_sel:[0,0,1]
	v_pk_fma_f32 v[90:91], v[148:149], v[86:87], v[90:91] neg_lo:[0,0,1] neg_hi:[0,0,1]
	v_pk_mul_f32 v[94:95], v[148:149], v[82:83]
	v_pk_mul_f32 v[92:93], v[146:147], v[80:81]
	v_pk_fma_f32 v[94:95], v[144:145], v[86:87], v[94:95]
	v_cndmask_b32_e32 v87, v87, v91, vcc
	v_cndmask_b32_e32 v86, v86, v90, vcc
	v_cvt_pk_fp8_f32 v100, v86, v87 op_sel:[0,0,1]
	v_pk_fma_f32 v[84:85], v[142:143], v[84:85], v[92:93]
	v_cndmask_b32_e32 v105, v83, v95, vcc
	v_cndmask_b32_e32 v104, v82, v94, vcc
	v_cndmask_b32_e32 v103, v81, v85, vcc
	v_cndmask_b32_e32 v102, v80, v84, vcc
.LBB0_4013:
	ds_read_b32 v80, v184 offset:192
	s_and_b64 vcc, exec, s[6:7]
	s_mov_b64 s[34:35], -1
	s_waitcnt lgkmcnt(0)
	v_mov_b32_e32 v81, v80
	v_pk_mul_f32 v[84:85], v[78:79], v[80:81] op_sel_hi:[1,0]
	v_pk_mul_f32 v[82:83], v[76:77], v[80:81] op_sel_hi:[1,0]
	s_cbranch_vccnz .LBB0_4015
	v_add_u32_e32 v76, s50, v178
	ds_read_b128 v[76:79], v76 offset:192
	v_pk_mul_f32 v[90:91], v[72:73], v[80:81]
	s_nop 0
	s_nop 0
	v_cvt_pk_fp8_f32 v99, v90, v91
	s_waitcnt lgkmcnt(0)
	v_pk_mul_f32 v[90:91], v[68:69], v[76:77]
	s_nop 0
	v_cvt_pk_fp8_f32 v86, v82, v83
	v_cvt_pk_fp8_f32 v87, v90, v91
	v_mov_b32_e32 v88, v80
	v_mov_b32_e32 v89, v80
	v_pk_mul_f32 v[88:89], v[74:75], v[88:89]
	v_cvt_pk_fp8_f32 v86, v84, v85 op_sel:[0,0,1]
	v_cvt_pk_fp8_f32 v99, v88, v89 op_sel:[0,0,1]
	v_pk_mul_f32 v[88:89], v[70:71], v[78:79]
	v_pk_mul_f32 v[78:79], v[66:67], v[78:79]
	v_cvt_pk_fp8_f32 v87, v88, v89 op_sel:[0,0,1]
	v_pk_mul_f32 v[76:77], v[64:65], v[76:77]
	s_mov_b64 s[34:35], 0
.LBB0_4015:
	s_andn2_b64 vcc, exec, s[34:35]
	s_cbranch_vccnz .LBB0_4017
	v_pk_mul_f32 v[72:73], v[72:73], v[80:81]
	v_mov_b32_e32 v76, v80
	v_pk_mul_f32 v[90:91], v[138:139], v[72:73]
	v_mov_b32_e32 v77, v80
	v_pk_fma_f32 v[90:91], v[134:135], v[82:83], v[90:91]
	v_pk_mul_f32 v[86:87], v[134:135], v[72:73]
	v_cndmask_b32_e64 v73, v73, v91, s[4:5]
	v_cndmask_b32_e64 v72, v72, v90, s[4:5]
	s_nop 0
	v_pk_mul_f32 v[74:75], v[74:75], v[76:77]
	v_cvt_pk_fp8_f32 v99, v72, v73
	v_pk_mul_f32 v[88:89], v[140:141], v[74:75]
	v_pk_fma_f32 v[86:87], v[138:139], v[82:83], v[86:87] neg_lo:[0,0,1] neg_hi:[0,0,1]
	v_pk_fma_f32 v[88:89], v[136:137], v[84:85], v[88:89]
	v_pk_mul_f32 v[64:65], v[64:65], v[80:81]
	v_cndmask_b32_e64 v72, v75, v89, s[4:5]
	v_cndmask_b32_e64 v73, v74, v88, s[4:5]
	v_cndmask_b32_e64 v83, v83, v87, s[4:5]
	v_cndmask_b32_e64 v82, v82, v86, s[4:5]
	s_nop 0
	v_cvt_pk_fp8_f32 v99, v73, v72 op_sel:[0,0,1]
	v_pk_mul_f32 v[68:69], v[68:69], v[80:81]
	s_xor_b64 s[34:35], s[4:5], -1
	v_pk_mul_f32 v[72:73], v[134:135], v[64:65]
	v_cvt_pk_fp8_f32 v86, v82, v83
	v_pk_fma_f32 v[72:73], v[138:139], v[68:69], v[72:73] neg_lo:[0,0,1] neg_hi:[0,0,1]
	s_and_b64 vcc, s[34:35], s[30:31]
	v_pk_mul_f32 v[78:79], v[136:137], v[74:75]
	v_cndmask_b32_e32 v73, v69, v73, vcc
	v_cndmask_b32_e32 v72, v68, v72, vcc
	s_nop 0
	v_pk_fma_f32 v[78:79], v[140:141], v[84:85], v[78:79] neg_lo:[0,0,1] neg_hi:[0,0,1]
	v_pk_mul_f32 v[66:67], v[66:67], v[76:77]
	v_cvt_pk_fp8_f32 v87, v72, v73
	v_cndmask_b32_e64 v79, v85, v79, s[4:5]
	v_cndmask_b32_e64 v78, v84, v78, s[4:5]
	v_pk_mul_f32 v[70:71], v[70:71], v[76:77]
	v_pk_mul_f32 v[74:75], v[136:137], v[66:67]
	v_cvt_pk_fp8_f32 v86, v78, v79 op_sel:[0,0,1]
	v_pk_fma_f32 v[74:75], v[140:141], v[70:71], v[74:75] neg_lo:[0,0,1] neg_hi:[0,0,1]
	v_pk_mul_f32 v[78:79], v[140:141], v[66:67]
	v_pk_mul_f32 v[76:77], v[138:139], v[64:65]
	v_pk_fma_f32 v[78:79], v[136:137], v[70:71], v[78:79]
	v_cndmask_b32_e32 v71, v71, v75, vcc
	v_cndmask_b32_e32 v70, v70, v74, vcc
	v_cvt_pk_fp8_f32 v87, v70, v71 op_sel:[0,0,1]
	v_pk_fma_f32 v[68:69], v[134:135], v[68:69], v[76:77]
	v_cndmask_b32_e32 v79, v67, v79, vcc
	v_cndmask_b32_e32 v78, v66, v78, vcc
	v_cndmask_b32_e32 v77, v65, v69, vcc
	v_cndmask_b32_e32 v76, v64, v68, vcc
.LBB0_4017:
	s_nop 0
	v_cvt_pk_fp8_f32 v66, v102, v103
	s_nop 0
	s_nop 0
	s_nop 0
	v_cvt_pk_fp8_f32 v135, v112, v113
	v_cvt_pk_fp8_f32 v67, v150, v151
	v_cvt_pk_fp8_f32 v103, v76, v77
	v_lshlrev_b32_e32 v64, 3, v133
	v_cvt_pk_fp8_f32 v66, v104, v105 op_sel:[0,0,1]
	v_cvt_pk_fp8_f32 v135, v114, v115 op_sel:[0,0,1]
	v_cvt_pk_fp8_f32 v67, v152, v153 op_sel:[0,0,1]
	v_and_b32_e32 v106, -16, v64
	v_cvt_pk_fp8_f32 v103, v78, v79 op_sel:[0,0,1]
	v_or_b32_e32 v64, v106, v185
	v_ashrrev_i32_e32 v65, 31, v64
	v_lshlrev_b32_e32 v68, 5, v133
	v_lshlrev_b64 v[110:111], 11, v[64:65]
	v_and_b32_e32 v170, 16, v129
	v_or_b32_e32 v65, s44, v185
	v_and_b32_e32 v108, 32, v68
	v_mov_b32_e32 v109, v171
	v_ashrrev_i32_e32 v107, 31, v106
	s_ashr_i32 s71, s70, 31
	s_and_b64 vcc, exec, s[6:7]
	s_mov_b64 s[34:35], -1
	s_cbranch_vccnz .LBB0_4019
	s_lshl_b64 s[34:35], s[70:71], 11
	v_readlane_b32 s27, v253, 61
	s_add_u32 s27, s27, s34
	v_readlane_b32 s34, v252, 59
	s_addc_u32 s34, s34, s35
	s_lshl_b32 s35, s2, 7
	s_ashr_i32 s36, s35, 31
	s_add_u32 s27, s27, s35
	s_addc_u32 s35, s34, s36
	s_add_u32 s34, s27, s44
	s_addc_u32 s35, s35, 0
	v_mov_b32_e32 v70, v118
	v_mov_b32_e32 v68, v128
	v_mov_b32_e32 v69, v186
	v_mov_b32_e32 v71, v131
	v_permlane32_swap_b32_e32 v68, v70
	s_nop 0
	v_permlane32_swap_b32_e32 v69, v71
	v_lshl_add_u64 v[76:77], s[34:35], 0, v[110:111]
	s_nop 0
	v_permlane16_swap_b32_e32 v68, v69
	v_permlane16_swap_b32_e32 v70, v71
	v_lshl_add_u64 v[76:77], v[76:77], 0, v[170:171]
	s_mov_b32 s27, 0x10000
	global_store_dwordx4 v[76:77], v[68:71], off
	v_mov_b32_e32 v74, v86
	v_mov_b32_e32 v72, v96
	v_add_co_u32_e32 v68, vcc, s27, v76
	s_and_b32 s27, s10, -16
	s_add_i32 s34, s2, s27
	v_mov_b32_e32 v73, v97
	v_mov_b32_e32 v75, v99
	s_ashr_i32 s35, s34, 31
	v_permlane32_swap_b32_e32 v72, v74
	v_permlane32_swap_b32_e32 v73, v75
	s_lshl_b64 s[34:35], s[34:35], 19
	s_nop 0
	v_permlane16_swap_b32_e32 v72, v73
	v_permlane16_swap_b32_e32 v74, v75
	v_addc_co_u32_e32 v69, vcc, 0, v77, vcc
	s_add_u32 s34, s97, s34
	v_readlane_b32 s27, v253, 52
	global_store_dwordx4 v[68:69], v[72:75], off
	s_addc_u32 s35, s27, s35
	s_and_b32 s48, s22, 0xf00
	v_lshlrev_b32_e32 v72, 12, v65
	v_mov_b32_e32 v73, v171
	v_lshl_add_u64 v[72:73], s[34:35], 0, v[72:73]
	v_lshl_add_u64 v[72:73], v[72:73], 0, s[48:49]
	v_lshl_add_u64 v[72:73], v[72:73], 0, s[28:29]
	v_mov_b32_e32 v68, v132
	v_mov_b32_e32 v69, v100
	v_mov_b32_e32 v70, v119
	v_mov_b32_e32 v71, v87
	v_lshl_add_u64 v[72:73], v[72:73], 0, v[108:109]
	v_permlane32_swap_b32_e32 v68, v69
	v_permlane32_swap_b32_e32 v70, v71
	v_lshl_add_u64 v[72:73], v[72:73], 0, v[106:107]
	global_store_dwordx4 v[72:73], v[68:71], off
	v_add_co_u32_e32 v72, vcc, 0x10000, v72
	s_nop 0
	v_mov_b32_e32 v69, v66
	v_mov_b32_e32 v68, v67
	v_mov_b32_e32 v70, v135
	v_mov_b32_e32 v71, v103
	v_permlane32_swap_b32_e32 v68, v69
	s_nop 0
	v_permlane32_swap_b32_e32 v70, v71
	v_addc_co_u32_e32 v73, vcc, 0, v73, vcc
	global_store_dwordx4 v[72:73], v[68:71], off
	s_mov_b64 s[34:35], 0

.LBB0_4024:
	ds_read_b32 v66, v184 offset:512
	s_and_b64 vcc, exec, s[6:7]
	s_mov_b64 s[34:35], -1
	s_waitcnt lgkmcnt(0)
	v_mov_b32_e32 v67, v66
	s_cbranch_vccnz .LBB0_4026
	v_pk_mul_f32 v[72:73], v[60:61], v[66:67]
	s_nop 0
	v_add_u32_e32 v86, s50, v178
	v_cvt_pk_fp8_f32 v64, v72, v73
	ds_read_b128 v[86:89], v86 offset:512
	v_mov_b32_e32 v114, v66
	v_mov_b32_e32 v115, v66
	v_pk_mul_f32 v[72:73], v[62:63], v[114:115]
	v_pk_mul_f32 v[116:117], v[56:57], v[66:67]
	v_cvt_pk_fp8_f32 v64, v72, v73 op_sel:[0,0,1]
	s_nop 0
	v_cvt_pk_fp8_f32 v73, v116, v117
	s_waitcnt lgkmcnt(0)
	v_pk_mul_f32 v[116:117], v[52:53], v[86:87]
	s_nop 0
	v_cvt_pk_fp8_f32 v72, v116, v117
	v_pk_mul_f32 v[114:115], v[58:59], v[114:115]
	v_pk_mul_f32 v[86:87], v[48:49], v[86:87]
	v_cvt_pk_fp8_f32 v73, v114, v115 op_sel:[0,0,1]
	v_pk_mul_f32 v[114:115], v[54:55], v[88:89]
	v_pk_mul_f32 v[88:89], v[50:51], v[88:89]
	v_cvt_pk_fp8_f32 v72, v114, v115 op_sel:[0,0,1]
	s_mov_b64 s[34:35], 0
.LBB0_4026:
	s_andn2_b64 vcc, exec, s[34:35]
	s_cbranch_vccnz .LBB0_4028
	v_mov_b32_e32 v86, v66
	v_mov_b32_e32 v87, v66
	v_pk_mul_f32 v[58:59], v[58:59], v[86:87]
	v_pk_mul_f32 v[56:57], v[56:57], v[66:67]
	v_pk_mul_f32 v[62:63], v[62:63], v[86:87]
	v_pk_mul_f32 v[60:61], v[60:61], v[66:67]
	s_waitcnt vmcnt(6)
	v_pk_mul_f32 v[72:73], v[100:101], v[58:59]
	v_pk_mul_f32 v[116:117], v[102:103], v[56:57]
	v_pk_fma_f32 v[72:73], v[104:105], v[62:63], v[72:73] neg_lo:[0,0,1] neg_hi:[0,0,1]
	v_pk_mul_f32 v[114:115], v[104:105], v[58:59]
	v_pk_fma_f32 v[116:117], v[98:99], v[60:61], v[116:117]
	v_pk_mul_f32 v[88:89], v[98:99], v[56:57]
	v_pk_fma_f32 v[114:115], v[100:101], v[62:63], v[114:115]
	v_cndmask_b32_e64 v63, v63, v73, s[4:5]
	v_cndmask_b32_e64 v57, v57, v117, s[4:5]
	v_cndmask_b32_e64 v56, v56, v116, s[4:5]
	s_nop 0
	v_cvt_pk_fp8_f32 v73, v56, v57
	v_pk_fma_f32 v[88:89], v[102:103], v[60:61], v[88:89] neg_lo:[0,0,1] neg_hi:[0,0,1]
	v_cndmask_b32_e64 v56, v59, v115, s[4:5]
	v_cndmask_b32_e64 v57, v58, v114, s[4:5]
	v_pk_mul_f32 v[50:51], v[50:51], v[86:87]
	v_pk_mul_f32 v[48:49], v[48:49], v[66:67]
	v_cndmask_b32_e64 v61, v61, v89, s[4:5]
	v_cndmask_b32_e64 v60, v60, v88, s[4:5]
	s_nop 0
	v_cvt_pk_fp8_f32 v73, v57, v56 op_sel:[0,0,1]
	v_pk_mul_f32 v[54:55], v[54:55], v[86:87]
	v_pk_mul_f32 v[52:53], v[52:53], v[66:67]
	s_xor_b64 s[34:35], s[4:5], -1
	v_pk_mul_f32 v[56:57], v[100:101], v[50:51]
	v_pk_mul_f32 v[58:59], v[98:99], v[48:49]
	v_cvt_pk_fp8_f32 v64, v60, v61
	v_pk_fma_f32 v[56:57], v[104:105], v[54:55], v[56:57] neg_lo:[0,0,1] neg_hi:[0,0,1]
	v_pk_fma_f32 v[58:59], v[102:103], v[52:53], v[58:59] neg_lo:[0,0,1] neg_hi:[0,0,1]
	v_pk_mul_f32 v[60:61], v[104:105], v[50:51]
	s_and_b64 vcc, s[34:35], s[30:31]
	v_cndmask_b32_e64 v62, v62, v72, s[4:5]
	v_pk_fma_f32 v[60:61], v[100:101], v[54:55], v[60:61]
	v_cndmask_b32_e32 v55, v55, v57, vcc
	v_cndmask_b32_e32 v57, v53, v59, vcc
	v_cndmask_b32_e32 v58, v52, v58, vcc
	s_nop 0
	v_cvt_pk_fp8_f32 v72, v58, v57
	v_cndmask_b32_e32 v54, v54, v56, vcc
	v_cvt_pk_fp8_f32 v64, v62, v63 op_sel:[0,0,1]
	v_pk_mul_f32 v[62:63], v[102:103], v[48:49]
	v_cvt_pk_fp8_f32 v72, v54, v55 op_sel:[0,0,1]
	v_pk_fma_f32 v[52:53], v[98:99], v[52:53], v[62:63]
	v_cndmask_b32_e32 v89, v51, v61, vcc
	v_cndmask_b32_e32 v88, v50, v60, vcc
	v_cndmask_b32_e32 v87, v49, v53, vcc
	v_cndmask_b32_e32 v86, v48, v52, vcc
.LBB0_4028:
	ds_read_b32 v52, v184 offset:576
	s_and_b64 vcc, exec, s[6:7]
	s_mov_b64 s[34:35], -1
	s_waitcnt lgkmcnt(0)
	v_mov_b32_e32 v53, v52
	s_cbranch_vccnz .LBB0_4030
	v_pk_mul_f32 v[48:49], v[44:45], v[52:53]
	s_nop 0
	v_cvt_pk_fp8_f32 v54, v48, v49
	v_add_u32_e32 v48, s50, v178
	ds_read_b128 v[48:51], v48 offset:576
	v_mov_b32_e32 v56, v52
	v_mov_b32_e32 v57, v52
	v_pk_mul_f32 v[58:59], v[46:47], v[56:57]
	s_nop 0
	v_cvt_pk_fp8_f32 v54, v58, v59 op_sel:[0,0,1]
	v_pk_mul_f32 v[58:59], v[40:41], v[52:53]
	s_nop 0
	v_cvt_pk_fp8_f32 v67, v58, v59
	s_waitcnt lgkmcnt(0)
	v_pk_mul_f32 v[58:59], v[36:37], v[48:49]
	v_pk_mul_f32 v[56:57], v[42:43], v[56:57]
	v_cvt_pk_fp8_f32 v55, v58, v59
	v_cvt_pk_fp8_f32 v67, v56, v57 op_sel:[0,0,1]
	v_pk_mul_f32 v[56:57], v[38:39], v[50:51]
	v_pk_mul_f32 v[50:51], v[34:35], v[50:51]
	v_cvt_pk_fp8_f32 v55, v56, v57 op_sel:[0,0,1]
	v_pk_mul_f32 v[48:49], v[32:33], v[48:49]
	s_mov_b64 s[34:35], 0
.LBB0_4030:
	s_andn2_b64 vcc, exec, s[34:35]
	s_cbranch_vccnz .LBB0_4032
	v_pk_mul_f32 v[40:41], v[40:41], v[52:53]
	v_pk_mul_f32 v[44:45], v[44:45], v[52:53]
	s_waitcnt vmcnt(5)
	v_pk_mul_f32 v[56:57], v[94:95], v[40:41]
	v_mov_b32_e32 v48, v52
	s_waitcnt vmcnt(4)
	v_pk_fma_f32 v[56:57], v[90:91], v[44:45], v[56:57]
	v_mov_b32_e32 v49, v52
	v_pk_mul_f32 v[50:51], v[90:91], v[40:41]
	v_cndmask_b32_e64 v41, v41, v57, s[4:5]
	v_cndmask_b32_e64 v40, v40, v56, s[4:5]
	s_nop 0
	v_pk_mul_f32 v[42:43], v[42:43], v[48:49]
	v_cvt_pk_fp8_f32 v67, v40, v41
	v_pk_mul_f32 v[46:47], v[46:47], v[48:49]
	v_pk_mul_f32 v[58:59], v[96:97], v[42:43]
	v_pk_mul_f32 v[54:55], v[92:93], v[42:43]
	v_pk_fma_f32 v[58:59], v[92:93], v[46:47], v[58:59]
	v_pk_fma_f32 v[54:55], v[96:97], v[46:47], v[54:55] neg_lo:[0,0,1] neg_hi:[0,0,1]
	v_pk_fma_f32 v[50:51], v[94:95], v[44:45], v[50:51] neg_lo:[0,0,1] neg_hi:[0,0,1]
	v_cndmask_b32_e64 v40, v43, v59, s[4:5]
	v_cndmask_b32_e64 v41, v42, v58, s[4:5]
	v_pk_mul_f32 v[32:33], v[32:33], v[52:53]
	v_cndmask_b32_e64 v46, v46, v54, s[4:5]
	v_cndmask_b32_e64 v45, v45, v51, s[4:5]
	v_cndmask_b32_e64 v44, v44, v50, s[4:5]
	s_nop 0
	v_cvt_pk_fp8_f32 v67, v41, v40 op_sel:[0,0,1]
	v_pk_mul_f32 v[36:37], v[36:37], v[52:53]
	s_xor_b64 s[34:35], s[4:5], -1
	v_pk_mul_f32 v[40:41], v[90:91], v[32:33]
	v_cvt_pk_fp8_f32 v54, v44, v45
	v_pk_fma_f32 v[40:41], v[94:95], v[36:37], v[40:41] neg_lo:[0,0,1] neg_hi:[0,0,1]
	s_and_b64 vcc, s[34:35], s[30:31]
	v_cndmask_b32_e64 v47, v47, v55, s[4:5]
	v_cndmask_b32_e32 v41, v37, v41, vcc
	v_cndmask_b32_e32 v40, v36, v40, vcc
	s_nop 0
	v_pk_mul_f32 v[34:35], v[34:35], v[48:49]
	v_cvt_pk_fp8_f32 v55, v40, v41
	v_pk_mul_f32 v[38:39], v[38:39], v[48:49]
	v_pk_mul_f32 v[42:43], v[92:93], v[34:35]
	v_cvt_pk_fp8_f32 v54, v46, v47 op_sel:[0,0,1]
	v_pk_fma_f32 v[42:43], v[96:97], v[38:39], v[42:43] neg_lo:[0,0,1] neg_hi:[0,0,1]
	v_pk_mul_f32 v[46:47], v[96:97], v[34:35]
	v_pk_mul_f32 v[44:45], v[94:95], v[32:33]
	v_pk_fma_f32 v[46:47], v[92:93], v[38:39], v[46:47]
	v_cndmask_b32_e32 v39, v39, v43, vcc
	v_cndmask_b32_e32 v38, v38, v42, vcc
	v_cvt_pk_fp8_f32 v55, v38, v39 op_sel:[0,0,1]
	v_pk_fma_f32 v[36:37], v[90:91], v[36:37], v[44:45]
	v_cndmask_b32_e32 v51, v35, v47, vcc
	v_cndmask_b32_e32 v50, v34, v46, vcc
	v_cndmask_b32_e32 v49, v33, v37, vcc
	v_cndmask_b32_e32 v48, v32, v36, vcc
.LBB0_4032:
	ds_read_b32 v34, v184 offset:640
	s_and_b64 vcc, exec, s[6:7]
	s_mov_b64 s[34:35], -1
	s_waitcnt lgkmcnt(0)
	v_mov_b32_e32 v35, v34
	s_cbranch_vccnz .LBB0_4034
	v_pk_mul_f32 v[36:37], v[28:29], v[34:35]
	s_nop 0
	v_add_u32_e32 v33, s50, v178
	v_cvt_pk_fp8_f32 v32, v36, v37
	ds_read_b128 v[38:41], v33 offset:640
	v_mov_b32_e32 v42, v34
	v_mov_b32_e32 v43, v34
	v_pk_mul_f32 v[36:37], v[30:31], v[42:43]
	s_nop 0
	v_cvt_pk_fp8_f32 v32, v36, v37 op_sel:[0,0,1]
	v_pk_mul_f32 v[36:37], v[24:25], v[34:35]
	s_waitcnt lgkmcnt(0)
	v_pk_mul_f32 v[44:45], v[20:21], v[38:39]
	v_cvt_pk_fp8_f32 v33, v36, v37
	s_nop 0
	v_cvt_pk_fp8_f32 v36, v44, v45
	v_pk_mul_f32 v[42:43], v[26:27], v[42:43]
	v_pk_mul_f32 v[38:39], v[16:17], v[38:39]
	v_cvt_pk_fp8_f32 v33, v42, v43 op_sel:[0,0,1]
	v_pk_mul_f32 v[42:43], v[22:23], v[40:41]
	v_pk_mul_f32 v[40:41], v[18:19], v[40:41]
	v_cvt_pk_fp8_f32 v36, v42, v43 op_sel:[0,0,1]
	s_mov_b64 s[34:35], 0
.LBB0_4034:
	s_andn2_b64 vcc, exec, s[34:35]
	s_cbranch_vccnz .LBB0_4036
	v_pk_mul_f32 v[24:25], v[24:25], v[34:35]
	v_pk_mul_f32 v[28:29], v[28:29], v[34:35]
	s_waitcnt vmcnt(2)
	v_pk_mul_f32 v[32:33], v[78:79], v[24:25]
	v_pk_mul_f32 v[40:41], v[82:83], v[24:25]
	v_pk_fma_f32 v[32:33], v[82:83], v[28:29], v[32:33] neg_lo:[0,0,1] neg_hi:[0,0,1]
	v_pk_fma_f32 v[40:41], v[78:79], v[28:29], v[40:41]
	v_mov_b32_e32 v36, v34
	v_mov_b32_e32 v37, v34
	v_cndmask_b32_e64 v29, v29, v33, s[4:5]
	v_cndmask_b32_e64 v25, v25, v41, s[4:5]
	v_cndmask_b32_e64 v24, v24, v40, s[4:5]
	s_nop 0
	v_pk_mul_f32 v[26:27], v[26:27], v[36:37]
	v_cvt_pk_fp8_f32 v33, v24, v25
	v_pk_mul_f32 v[30:31], v[30:31], v[36:37]
	v_pk_mul_f32 v[42:43], v[84:85], v[26:27]
	v_pk_mul_f32 v[16:17], v[16:17], v[34:35]
	v_pk_fma_f32 v[42:43], v[80:81], v[30:31], v[42:43]
	v_cndmask_b32_e64 v28, v28, v32, s[4:5]
	v_cndmask_b32_e64 v24, v27, v43, s[4:5]
	v_cndmask_b32_e64 v25, v26, v42, s[4:5]
	s_nop 0
	v_cvt_pk_fp8_f32 v33, v25, v24 op_sel:[0,0,1]
	v_pk_mul_f32 v[20:21], v[20:21], v[34:35]
	s_xor_b64 s[34:35], s[4:5], -1
	v_pk_mul_f32 v[24:25], v[78:79], v[16:17]
	v_cvt_pk_fp8_f32 v32, v28, v29
	v_pk_fma_f32 v[24:25], v[82:83], v[20:21], v[24:25] neg_lo:[0,0,1] neg_hi:[0,0,1]
	s_and_b64 vcc, s[34:35], s[30:31]
	v_pk_mul_f32 v[38:39], v[80:81], v[26:27]
	v_pk_mul_f32 v[22:23], v[22:23], v[36:37]
	v_pk_mul_f32 v[18:19], v[18:19], v[36:37]
	v_cndmask_b32_e32 v25, v21, v25, vcc
	v_cndmask_b32_e32 v24, v20, v24, vcc
	s_nop 0
	v_pk_fma_f32 v[38:39], v[84:85], v[30:31], v[38:39] neg_lo:[0,0,1] neg_hi:[0,0,1]
	v_cvt_pk_fp8_f32 v36, v24, v25
	v_cndmask_b32_e64 v31, v31, v39, s[4:5]
	v_cndmask_b32_e64 v30, v30, v38, s[4:5]
	v_pk_mul_f32 v[26:27], v[80:81], v[18:19]
	v_cvt_pk_fp8_f32 v32, v30, v31 op_sel:[0,0,1]
	v_pk_fma_f32 v[26:27], v[84:85], v[22:23], v[26:27] neg_lo:[0,0,1] neg_hi:[0,0,1]
	v_pk_mul_f32 v[30:31], v[84:85], v[18:19]
	v_pk_mul_f32 v[28:29], v[82:83], v[16:17]
	v_pk_fma_f32 v[30:31], v[80:81], v[22:23], v[30:31]
	v_cndmask_b32_e32 v23, v23, v27, vcc
	v_cndmask_b32_e32 v22, v22, v26, vcc
	v_cvt_pk_fp8_f32 v36, v22, v23 op_sel:[0,0,1]
	v_pk_fma_f32 v[20:21], v[78:79], v[20:21], v[28:29]
	v_cndmask_b32_e32 v41, v19, v31, vcc
	v_cndmask_b32_e32 v40, v18, v30, vcc
	v_cndmask_b32_e32 v39, v17, v21, vcc
	v_cndmask_b32_e32 v38, v16, v20, vcc
.LBB0_4036:
	ds_read_b32 v16, v184 offset:704
	s_and_b64 vcc, exec, s[6:7]
	s_mov_b64 s[34:35], -1
	s_waitcnt lgkmcnt(0)
	v_mov_b32_e32 v17, v16
	v_pk_mul_f32 v[20:21], v[14:15], v[16:17] op_sel_hi:[1,0]
	v_pk_mul_f32 v[18:19], v[12:13], v[16:17] op_sel_hi:[1,0]
	s_cbranch_vccnz .LBB0_4038
	v_add_u32_e32 v12, s50, v178
	ds_read_b128 v[12:15], v12 offset:704
	v_pk_mul_f32 v[26:27], v[8:9], v[16:17]
	s_nop 0
	s_nop 0
	v_cvt_pk_fp8_f32 v35, v26, v27
	s_waitcnt lgkmcnt(0)
	v_pk_mul_f32 v[26:27], v[4:5], v[12:13]
	s_nop 0
	v_cvt_pk_fp8_f32 v22, v18, v19
	v_cvt_pk_fp8_f32 v23, v26, v27
	v_mov_b32_e32 v24, v16
	v_mov_b32_e32 v25, v16
	v_pk_mul_f32 v[24:25], v[10:11], v[24:25]
	v_cvt_pk_fp8_f32 v22, v20, v21 op_sel:[0,0,1]
	v_cvt_pk_fp8_f32 v35, v24, v25 op_sel:[0,0,1]
	v_pk_mul_f32 v[24:25], v[6:7], v[14:15]
	v_pk_mul_f32 v[14:15], v[2:3], v[14:15]
	v_cvt_pk_fp8_f32 v23, v24, v25 op_sel:[0,0,1]
	v_pk_mul_f32 v[12:13], v[0:1], v[12:13]
	s_mov_b64 s[34:35], 0
.LBB0_4038:
	s_andn2_b64 vcc, exec, s[34:35]
	s_cbranch_vccnz .LBB0_4040
	v_pk_mul_f32 v[8:9], v[8:9], v[16:17]
	v_mov_b32_e32 v12, v16
	s_waitcnt vmcnt(1)
	v_pk_mul_f32 v[26:27], v[74:75], v[8:9]
	v_mov_b32_e32 v13, v16
	s_waitcnt vmcnt(0)
	v_pk_fma_f32 v[26:27], v[68:69], v[18:19], v[26:27]
	v_pk_mul_f32 v[22:23], v[68:69], v[8:9]
	v_cndmask_b32_e64 v9, v9, v27, s[4:5]
	v_cndmask_b32_e64 v8, v8, v26, s[4:5]
	s_nop 0
	v_pk_mul_f32 v[10:11], v[10:11], v[12:13]
	v_cvt_pk_fp8_f32 v35, v8, v9
	v_pk_mul_f32 v[24:25], v[76:77], v[10:11]
	v_pk_mul_f32 v[14:15], v[70:71], v[10:11]
	v_pk_fma_f32 v[24:25], v[70:71], v[20:21], v[24:25]
	v_pk_fma_f32 v[22:23], v[74:75], v[18:19], v[22:23] neg_lo:[0,0,1] neg_hi:[0,0,1]
	v_pk_fma_f32 v[14:15], v[76:77], v[20:21], v[14:15] neg_lo:[0,0,1] neg_hi:[0,0,1]
	v_cndmask_b32_e64 v8, v11, v25, s[4:5]
	v_cndmask_b32_e64 v9, v10, v24, s[4:5]
	v_pk_mul_f32 v[0:1], v[0:1], v[16:17]
	v_cndmask_b32_e64 v15, v21, v15, s[4:5]
	v_cndmask_b32_e64 v14, v20, v14, s[4:5]
	v_cndmask_b32_e64 v19, v19, v23, s[4:5]
	v_cndmask_b32_e64 v18, v18, v22, s[4:5]
	s_nop 0
	v_cvt_pk_fp8_f32 v35, v9, v8 op_sel:[0,0,1]
	v_pk_mul_f32 v[4:5], v[4:5], v[16:17]
	s_xor_b64 s[4:5], s[4:5], -1
	v_pk_mul_f32 v[8:9], v[68:69], v[0:1]
	v_cvt_pk_fp8_f32 v22, v18, v19
	v_pk_fma_f32 v[8:9], v[74:75], v[4:5], v[8:9] neg_lo:[0,0,1] neg_hi:[0,0,1]
	s_and_b64 vcc, s[4:5], s[30:31]
	v_cndmask_b32_e32 v9, v5, v9, vcc
	v_cndmask_b32_e32 v8, v4, v8, vcc
	s_nop 0
	v_pk_mul_f32 v[2:3], v[2:3], v[12:13]
	v_cvt_pk_fp8_f32 v23, v8, v9
	v_pk_mul_f32 v[6:7], v[6:7], v[12:13]
	v_pk_mul_f32 v[10:11], v[70:71], v[2:3]
	v_cvt_pk_fp8_f32 v22, v14, v15 op_sel:[0,0,1]
	v_pk_fma_f32 v[10:11], v[76:77], v[6:7], v[10:11] neg_lo:[0,0,1] neg_hi:[0,0,1]
	v_pk_mul_f32 v[14:15], v[76:77], v[2:3]
	v_pk_mul_f32 v[12:13], v[74:75], v[0:1]
	v_pk_fma_f32 v[14:15], v[70:71], v[6:7], v[14:15]
	v_cndmask_b32_e32 v7, v7, v11, vcc
	v_cndmask_b32_e32 v6, v6, v10, vcc
	v_cvt_pk_fp8_f32 v23, v6, v7 op_sel:[0,0,1]
	v_pk_fma_f32 v[4:5], v[68:69], v[4:5], v[12:13]
	v_cndmask_b32_e32 v15, v3, v15, vcc
	v_cndmask_b32_e32 v14, v2, v14, vcc
	v_cndmask_b32_e32 v13, v1, v5, vcc
	v_cndmask_b32_e32 v12, v0, v4, vcc
.LBB0_4040:
	s_nop 0
	v_cvt_pk_fp8_f32 v0, v38, v39
	s_waitcnt vmcnt(1)
	s_nop 0
	s_nop 0
	s_nop 0
	v_cvt_pk_fp8_f32 v75, v48, v49
	v_cvt_pk_fp8_f32 v1, v86, v87
	v_cvt_pk_fp8_f32 v39, v12, v13
	v_cvt_pk_fp8_f32 v0, v40, v41 op_sel:[0,0,1]
	v_cvt_pk_fp8_f32 v75, v50, v51 op_sel:[0,0,1]
	v_cvt_pk_fp8_f32 v1, v88, v89 op_sel:[0,0,1]
	v_cvt_pk_fp8_f32 v39, v14, v15 op_sel:[0,0,1]
	s_ashr_i32 s9, s8, 31
	s_and_b64 vcc, exec, s[6:7]
	s_mov_b64 s[4:5], -1
	v_readlane_b32 s27, v254, 39
	s_cbranch_vccnz .LBB0_4042
	s_lshl_b64 s[4:5], s[8:9], 11
	v_readlane_b32 s6, v253, 61
	s_add_u32 s4, s6, s4
	v_readlane_b32 s6, v252, 59
	s_addc_u32 s5, s6, s5
	s_lshl_b32 s6, s2, 7
	s_ashr_i32 s7, s6, 31
	s_add_u32 s4, s4, s6
	s_addc_u32 s5, s5, s7
	s_add_u32 s4, s4, s44
	s_addc_u32 s5, s5, 0
	v_mov_b32_e32 v2, v64
	v_mov_b32_e32 v4, v54
	v_mov_b32_e32 v5, v67
	v_mov_b32_e32 v3, v73
	v_permlane32_swap_b32_e32 v2, v4
	s_nop 0
	v_permlane32_swap_b32_e32 v3, v5
	v_lshl_add_u64 v[10:11], s[4:5], 0, v[110:111]
	s_nop 0
	v_permlane16_swap_b32_e32 v2, v3
	v_permlane16_swap_b32_e32 v4, v5
	v_lshl_add_u64 v[10:11], v[10:11], 0, v[170:171]
	s_mov_b32 s4, 0x10000
	global_store_dwordx4 v[10:11], v[2:5], off
	v_mov_b32_e32 v6, v32
	v_mov_b32_e32 v8, v22
	v_add_co_u32_e32 v2, vcc, s4, v10
	s_and_b32 s4, s10, -16
	s_add_i32 s4, s2, s4
	v_mov_b32_e32 v9, v35
	v_mov_b32_e32 v7, v33
	s_ashr_i32 s5, s4, 31
	v_permlane32_swap_b32_e32 v6, v8
	v_permlane32_swap_b32_e32 v7, v9
	s_lshl_b64 s[4:5], s[4:5], 19
	s_nop 0
	v_permlane16_swap_b32_e32 v6, v7
	v_permlane16_swap_b32_e32 v8, v9
	v_addc_co_u32_e32 v3, vcc, 0, v11, vcc
	s_add_u32 s4, s97, s4
	v_readlane_b32 s6, v253, 52
	global_store_dwordx4 v[2:3], v[6:9], off
	s_addc_u32 s5, s6, s5
	s_and_b32 s48, s22, 0xf00
	v_lshlrev_b32_e32 v6, 12, v65
	v_mov_b32_e32 v7, v171
	v_lshl_add_u64 v[6:7], s[4:5], 0, v[6:7]
	v_lshl_add_u64 v[6:7], v[6:7], 0, s[48:49]
	v_lshl_add_u64 v[6:7], v[6:7], 0, s[28:29]
	v_mov_b32_e32 v2, v72
	v_mov_b32_e32 v3, v36
	v_mov_b32_e32 v4, v55
	v_mov_b32_e32 v5, v23
	v_lshl_add_u64 v[6:7], v[6:7], 0, v[108:109]
	v_permlane32_swap_b32_e32 v2, v3
	v_permlane32_swap_b32_e32 v4, v5
	v_lshl_add_u64 v[6:7], v[6:7], 0, v[106:107]
	global_store_dwordx4 v[6:7], v[2:5], off offset:128
	v_add_co_u32_e32 v6, vcc, 0x10000, v6
	s_nop 0
	v_mov_b32_e32 v2, v1
	v_mov_b32_e32 v3, v0
	v_mov_b32_e32 v4, v75
	v_mov_b32_e32 v5, v39
	v_permlane32_swap_b32_e32 v2, v3
	s_nop 0
	v_permlane32_swap_b32_e32 v4, v5
	v_addc_co_u32_e32 v7, vcc, 0, v7, vcc
	s_mov_b64 s[4:5], 0
	global_store_dwordx4 v[6:7], v[2:5], off offset:128

.LBB0_4072:
	v_lshl_add_u32 v184, v185, 2, s50
	ds_read_b32 v130, v184
	v_and_b32_e32 v174, -16, v129
	s_mov_b64 s[6:7], -1
	s_and_b64 vcc, exec, s[72:73]
	s_waitcnt lgkmcnt(0)
	v_mov_b32_e32 v131, v130
	s_cbranch_vccz .LBB0_4074
	v_pk_mul_f32 v[150:151], v[120:121], v[130:131]
	s_nop 0
	v_add_u32_e32 v132, s50, v174
	v_cvt_pk_fp8_f32 v128, v150, v151
	ds_read_b128 v[150:153], v132
	v_mov_b32_e32 v176, v130
	v_mov_b32_e32 v177, v130
	v_pk_mul_f32 v[178:179], v[122:123], v[176:177]
	s_nop 0
	v_cvt_pk_fp8_f32 v128, v178, v179 op_sel:[0,0,1]
	v_pk_mul_f32 v[178:179], v[124:125], v[130:131]
	s_nop 0
	v_cvt_pk_fp8_f32 v186, v178, v179
	s_waitcnt lgkmcnt(0)
	v_pk_mul_f32 v[178:179], v[116:117], v[150:151]
	v_pk_mul_f32 v[176:177], v[126:127], v[176:177]
	v_cvt_pk_fp8_f32 v132, v178, v179
	v_cvt_pk_fp8_f32 v186, v176, v177 op_sel:[0,0,1]
	v_pk_mul_f32 v[176:177], v[118:119], v[152:153]
	v_pk_mul_f32 v[152:153], v[114:115], v[152:153]
	v_cvt_pk_fp8_f32 v132, v176, v177 op_sel:[0,0,1]
	v_pk_mul_f32 v[150:151], v[112:113], v[150:151]
	s_mov_b64 s[6:7], 0
.LBB0_4074:
	s_andn2_b64 vcc, exec, s[6:7]
	s_cbranch_vccnz .LBB0_4076
	v_pk_mul_f32 v[124:125], v[124:125], v[130:131]
	v_pk_mul_f32 v[120:121], v[120:121], v[130:131]
	s_waitcnt vmcnt(0)
	v_pk_mul_f32 v[176:177], v[162:163], v[124:125]
	v_pk_mul_f32 v[186:187], v[166:167], v[124:125]
	v_pk_fma_f32 v[176:177], v[166:167], v[120:121], v[176:177] neg_lo:[0,0,1] neg_hi:[0,0,1]
	v_pk_fma_f32 v[186:187], v[162:163], v[120:121], v[186:187]
	v_mov_b32_e32 v150, v130
	v_mov_b32_e32 v151, v130
	v_cndmask_b32_e64 v121, v121, v177, s[4:5]
	v_cndmask_b32_e64 v120, v120, v176, s[4:5]
	v_cndmask_b32_e64 v125, v125, v187, s[4:5]
	v_cndmask_b32_e64 v124, v124, v186, s[4:5]
	s_nop 0
	s_nop 0
	v_pk_mul_f32 v[126:127], v[126:127], v[150:151]
	v_cvt_pk_fp8_f32 v128, v120, v121
	v_cvt_pk_fp8_f32 v186, v124, v125
	v_pk_mul_f32 v[122:123], v[122:123], v[150:151]
	v_pk_mul_f32 v[152:153], v[164:165], v[126:127]
	v_pk_mul_f32 v[178:179], v[168:169], v[126:127]
	v_pk_fma_f32 v[152:153], v[168:169], v[122:123], v[152:153] neg_lo:[0,0,1] neg_hi:[0,0,1]
	v_pk_fma_f32 v[178:179], v[164:165], v[122:123], v[178:179]
	v_cndmask_b32_e64 v123, v123, v153, s[4:5]
	v_cndmask_b32_e64 v122, v122, v152, s[4:5]
	v_cndmask_b32_e64 v120, v127, v179, s[4:5]
	v_cndmask_b32_e64 v121, v126, v178, s[4:5]
	v_pk_mul_f32 v[114:115], v[114:115], v[150:151]
	v_pk_mul_f32 v[112:113], v[112:113], v[130:131]
	v_cvt_pk_fp8_f32 v128, v122, v123 op_sel:[0,0,1]
	v_cvt_pk_fp8_f32 v186, v121, v120 op_sel:[0,0,1]
	v_pk_mul_f32 v[118:119], v[118:119], v[150:151]
	v_pk_mul_f32 v[116:117], v[116:117], v[130:131]
	s_xor_b64 s[6:7], s[4:5], -1
	v_pk_mul_f32 v[120:121], v[164:165], v[114:115]
	v_pk_mul_f32 v[122:123], v[162:163], v[112:113]
	v_pk_fma_f32 v[120:121], v[168:169], v[118:119], v[120:121] neg_lo:[0,0,1] neg_hi:[0,0,1]
	v_pk_fma_f32 v[122:123], v[166:167], v[116:117], v[122:123] neg_lo:[0,0,1] neg_hi:[0,0,1]
	v_pk_mul_f32 v[124:125], v[168:169], v[114:115]
	s_and_b64 vcc, s[6:7], s[30:31]
	v_pk_fma_f32 v[124:125], v[164:165], v[118:119], v[124:125]
	v_cndmask_b32_e32 v119, v119, v121, vcc
	v_cndmask_b32_e32 v121, v117, v123, vcc
	v_cndmask_b32_e32 v122, v116, v122, vcc
	s_nop 0
	v_cvt_pk_fp8_f32 v132, v122, v121
	v_cndmask_b32_e32 v118, v118, v120, vcc
	v_pk_mul_f32 v[126:127], v[166:167], v[112:113]
	v_cndmask_b32_e32 v153, v115, v125, vcc
	v_cvt_pk_fp8_f32 v132, v118, v119 op_sel:[0,0,1]
	v_pk_fma_f32 v[116:117], v[162:163], v[116:117], v[126:127]
	v_cndmask_b32_e32 v152, v114, v124, vcc
	v_cndmask_b32_e32 v151, v113, v117, vcc
	v_cndmask_b32_e32 v150, v112, v116, vcc
.LBB0_4076:
	ds_read_b32 v116, v184 offset:64
	v_cndmask_b32_e64 v112, 0, 1, s[72:73]
	v_cmp_ne_u32_e64 s[6:7], 1, v112
	s_andn2_b64 vcc, exec, s[72:73]
	s_mov_b64 s[34:35], -1
	s_waitcnt lgkmcnt(0)
	v_mov_b32_e32 v117, v116
	s_cbranch_vccnz .LBB0_4078
	v_pk_mul_f32 v[112:113], v[108:109], v[116:117]
	s_nop 0
	v_cvt_pk_fp8_f32 v118, v112, v113
	v_add_u32_e32 v112, s50, v174
	ds_read_b128 v[112:115], v112 offset:64
	v_mov_b32_e32 v120, v116
	v_mov_b32_e32 v121, v116
	v_pk_mul_f32 v[122:123], v[110:111], v[120:121]
	s_nop 0
	v_cvt_pk_fp8_f32 v118, v122, v123 op_sel:[0,0,1]
	v_pk_mul_f32 v[122:123], v[104:105], v[116:117]
	s_nop 0
	v_cvt_pk_fp8_f32 v131, v122, v123
	s_waitcnt lgkmcnt(0)
	v_pk_mul_f32 v[122:123], v[100:101], v[112:113]
	v_pk_mul_f32 v[120:121], v[106:107], v[120:121]
	v_cvt_pk_fp8_f32 v119, v122, v123
	v_cvt_pk_fp8_f32 v131, v120, v121 op_sel:[0,0,1]
	v_pk_mul_f32 v[120:121], v[102:103], v[114:115]
	v_pk_mul_f32 v[114:115], v[98:99], v[114:115]
	v_cvt_pk_fp8_f32 v119, v120, v121 op_sel:[0,0,1]
	v_pk_mul_f32 v[112:113], v[96:97], v[112:113]
	s_mov_b64 s[34:35], 0
.LBB0_4078:
	s_andn2_b64 vcc, exec, s[34:35]
	s_waitcnt vmcnt(0)
	v_mov_b32_e32 v169, v175
	s_cbranch_vccnz .LBB0_4080
	v_pk_mul_f32 v[104:105], v[104:105], v[116:117]
	v_pk_mul_f32 v[108:109], v[108:109], v[116:117]
	v_pk_mul_f32 v[120:121], v[158:159], v[104:105]
	v_mov_b32_e32 v112, v116
	v_pk_fma_f32 v[120:121], v[154:155], v[108:109], v[120:121]
	v_mov_b32_e32 v113, v116
	v_pk_mul_f32 v[114:115], v[154:155], v[104:105]
	v_cndmask_b32_e64 v105, v105, v121, s[4:5]
	v_cndmask_b32_e64 v104, v104, v120, s[4:5]
	s_nop 0
	v_pk_mul_f32 v[106:107], v[106:107], v[112:113]
	v_cvt_pk_fp8_f32 v131, v104, v105
	v_pk_mul_f32 v[110:111], v[110:111], v[112:113]
	v_pk_mul_f32 v[122:123], v[160:161], v[106:107]
	v_pk_mul_f32 v[118:119], v[156:157], v[106:107]
	v_pk_fma_f32 v[122:123], v[156:157], v[110:111], v[122:123]
	v_pk_fma_f32 v[118:119], v[160:161], v[110:111], v[118:119] neg_lo:[0,0,1] neg_hi:[0,0,1]
	v_pk_fma_f32 v[114:115], v[158:159], v[108:109], v[114:115] neg_lo:[0,0,1] neg_hi:[0,0,1]
	v_cndmask_b32_e64 v104, v107, v123, s[4:5]
	v_cndmask_b32_e64 v105, v106, v122, s[4:5]
	v_pk_mul_f32 v[96:97], v[96:97], v[116:117]
	v_cndmask_b32_e64 v110, v110, v118, s[4:5]
	v_cndmask_b32_e64 v109, v109, v115, s[4:5]
	v_cndmask_b32_e64 v108, v108, v114, s[4:5]
	s_nop 0
	v_cvt_pk_fp8_f32 v131, v105, v104 op_sel:[0,0,1]
	v_pk_mul_f32 v[100:101], v[100:101], v[116:117]
	s_xor_b64 s[34:35], s[4:5], -1
	v_pk_mul_f32 v[104:105], v[154:155], v[96:97]
	v_cvt_pk_fp8_f32 v118, v108, v109
	v_pk_fma_f32 v[104:105], v[158:159], v[100:101], v[104:105] neg_lo:[0,0,1] neg_hi:[0,0,1]
	s_and_b64 vcc, s[34:35], s[30:31]
	v_cndmask_b32_e64 v111, v111, v119, s[4:5]
	v_cndmask_b32_e32 v105, v101, v105, vcc
	v_cndmask_b32_e32 v104, v100, v104, vcc
	s_nop 0
	v_pk_mul_f32 v[98:99], v[98:99], v[112:113]
	v_cvt_pk_fp8_f32 v119, v104, v105
	v_pk_mul_f32 v[102:103], v[102:103], v[112:113]
	v_pk_mul_f32 v[106:107], v[156:157], v[98:99]
	v_cvt_pk_fp8_f32 v118, v110, v111 op_sel:[0,0,1]
	v_pk_fma_f32 v[106:107], v[160:161], v[102:103], v[106:107] neg_lo:[0,0,1] neg_hi:[0,0,1]
	v_pk_mul_f32 v[110:111], v[160:161], v[98:99]
	v_pk_mul_f32 v[108:109], v[158:159], v[96:97]
	v_pk_fma_f32 v[110:111], v[156:157], v[102:103], v[110:111]
	v_cndmask_b32_e32 v103, v103, v107, vcc
	v_cndmask_b32_e32 v102, v102, v106, vcc
	v_cvt_pk_fp8_f32 v119, v102, v103 op_sel:[0,0,1]
	v_pk_fma_f32 v[100:101], v[154:155], v[100:101], v[108:109]
	v_cndmask_b32_e32 v115, v99, v111, vcc
	v_cndmask_b32_e32 v114, v98, v110, vcc
	v_cndmask_b32_e32 v113, v97, v101, vcc
	v_cndmask_b32_e32 v112, v96, v100, vcc
.LBB0_4080:
	ds_read_b32 v98, v184 offset:128
	s_and_b64 vcc, exec, s[6:7]
	s_mov_b64 s[34:35], -1
	s_waitcnt lgkmcnt(0)
	v_mov_b32_e32 v99, v98
	s_cbranch_vccnz .LBB0_4082
	v_pk_mul_f32 v[100:101], v[92:93], v[98:99]
	s_nop 0
	v_add_u32_e32 v97, s50, v174
	v_cvt_pk_fp8_f32 v96, v100, v101
	ds_read_b128 v[102:105], v97 offset:128
	v_mov_b32_e32 v106, v98
	v_mov_b32_e32 v107, v98
	v_pk_mul_f32 v[100:101], v[94:95], v[106:107]
	s_nop 0
	v_cvt_pk_fp8_f32 v96, v100, v101 op_sel:[0,0,1]
	v_pk_mul_f32 v[100:101], v[88:89], v[98:99]
	s_waitcnt lgkmcnt(0)
	v_pk_mul_f32 v[108:109], v[84:85], v[102:103]
	v_cvt_pk_fp8_f32 v97, v100, v101
	s_nop 0
	v_cvt_pk_fp8_f32 v100, v108, v109
	v_pk_mul_f32 v[106:107], v[90:91], v[106:107]
	v_pk_mul_f32 v[102:103], v[80:81], v[102:103]
	v_cvt_pk_fp8_f32 v97, v106, v107 op_sel:[0,0,1]
	v_pk_mul_f32 v[106:107], v[86:87], v[104:105]
	v_pk_mul_f32 v[104:105], v[82:83], v[104:105]
	v_cvt_pk_fp8_f32 v100, v106, v107 op_sel:[0,0,1]
	s_mov_b64 s[34:35], 0

.LBB0_4084:
	ds_read_b32 v80, v184 offset:192
	s_and_b64 vcc, exec, s[6:7]
	s_mov_b64 s[34:35], -1
	s_waitcnt lgkmcnt(0)
	v_mov_b32_e32 v81, v80
	v_pk_mul_f32 v[84:85], v[78:79], v[80:81] op_sel_hi:[1,0]
	v_pk_mul_f32 v[82:83], v[76:77], v[80:81] op_sel_hi:[1,0]
	s_cbranch_vccnz .LBB0_4086
	v_add_u32_e32 v76, s50, v174
	ds_read_b128 v[76:79], v76 offset:192
	v_pk_mul_f32 v[90:91], v[72:73], v[80:81]
	s_nop 0
	s_nop 0
	v_cvt_pk_fp8_f32 v99, v90, v91
	s_waitcnt lgkmcnt(0)
	v_pk_mul_f32 v[90:91], v[68:69], v[76:77]
	s_nop 0
	v_cvt_pk_fp8_f32 v86, v82, v83
	v_cvt_pk_fp8_f32 v87, v90, v91
	v_mov_b32_e32 v88, v80
	v_mov_b32_e32 v89, v80
	v_pk_mul_f32 v[88:89], v[74:75], v[88:89]
	v_cvt_pk_fp8_f32 v86, v84, v85 op_sel:[0,0,1]
	v_cvt_pk_fp8_f32 v99, v88, v89 op_sel:[0,0,1]
	v_pk_mul_f32 v[88:89], v[70:71], v[78:79]
	v_pk_mul_f32 v[78:79], v[66:67], v[78:79]
	v_cvt_pk_fp8_f32 v87, v88, v89 op_sel:[0,0,1]
	v_pk_mul_f32 v[76:77], v[64:65], v[76:77]
	s_mov_b64 s[34:35], 0

.LBB0_4088:
	s_nop 0
	v_cvt_pk_fp8_f32 v66, v102, v103
	s_nop 0
	s_nop 0
	s_nop 0
	v_cvt_pk_fp8_f32 v135, v112, v113
	v_cvt_pk_fp8_f32 v67, v150, v151
	v_cvt_pk_fp8_f32 v103, v76, v77
	v_lshlrev_b32_e32 v64, 3, v133
	v_cvt_pk_fp8_f32 v66, v104, v105 op_sel:[0,0,1]
	v_cvt_pk_fp8_f32 v135, v114, v115 op_sel:[0,0,1]
	v_cvt_pk_fp8_f32 v67, v152, v153 op_sel:[0,0,1]
	v_and_b32_e32 v106, -16, v64
	v_cvt_pk_fp8_f32 v103, v78, v79 op_sel:[0,0,1]
	v_or_b32_e32 v64, v106, v185
	v_ashrrev_i32_e32 v65, 31, v64
	v_lshlrev_b32_e32 v68, 5, v133
	v_lshlrev_b64 v[110:111], 11, v[64:65]
	v_and_b32_e32 v170, 16, v129
	v_or_b32_e32 v65, s44, v185
	v_and_b32_e32 v108, 32, v68
	v_mov_b32_e32 v109, v171
	v_ashrrev_i32_e32 v107, 31, v106
	s_ashr_i32 s71, s70, 31
	s_and_b64 vcc, exec, s[6:7]
	s_mov_b64 s[34:35], -1
	s_cbranch_vccnz .LBB0_4090
	s_lshl_b64 s[34:35], s[70:71], 11
	v_readlane_b32 s27, v253, 61
	s_add_u32 s27, s27, s34
	v_readlane_b32 s34, v252, 59
	s_addc_u32 s34, s34, s35
	s_lshl_b32 s35, s2, 7
	s_ashr_i32 s36, s35, 31
	s_add_u32 s27, s27, s35
	s_addc_u32 s35, s34, s36
	s_add_u32 s34, s27, s44
	s_addc_u32 s35, s35, 0
	v_mov_b32_e32 v68, v128
	v_mov_b32_e32 v70, v118
	v_mov_b32_e32 v69, v186
	v_mov_b32_e32 v71, v131
	v_permlane32_swap_b32_e32 v68, v70
	s_nop 0
	v_permlane32_swap_b32_e32 v69, v71
	v_lshl_add_u64 v[76:77], s[34:35], 0, v[110:111]
	s_nop 0
	v_permlane16_swap_b32_e32 v68, v69
	v_permlane16_swap_b32_e32 v70, v71
	v_lshl_add_u64 v[76:77], v[76:77], 0, v[170:171]
	s_mov_b32 s27, 0x10000
	global_store_dwordx4 v[76:77], v[68:71], off
	v_mov_b32_e32 v72, v96
	v_mov_b32_e32 v74, v86
	v_add_co_u32_e32 v68, vcc, s27, v76
	s_and_b32 s27, s10, -16
	s_add_i32 s34, s2, s27
	v_mov_b32_e32 v73, v97
	v_mov_b32_e32 v75, v99
	s_ashr_i32 s35, s34, 31
	v_permlane32_swap_b32_e32 v72, v74
	v_permlane32_swap_b32_e32 v73, v75
	s_lshl_b64 s[34:35], s[34:35], 19
	s_nop 0
	v_permlane16_swap_b32_e32 v72, v73
	v_permlane16_swap_b32_e32 v74, v75
	v_addc_co_u32_e32 v69, vcc, 0, v77, vcc
	s_add_u32 s34, s97, s34
	v_readlane_b32 s27, v253, 52
	global_store_dwordx4 v[68:69], v[72:75], off
	s_addc_u32 s35, s27, s35
	s_and_b32 s48, s22, 0xf00
	v_lshlrev_b32_e32 v72, 12, v65
	v_mov_b32_e32 v73, v171
	v_lshl_add_u64 v[72:73], s[34:35], 0, v[72:73]
	v_lshl_add_u64 v[72:73], v[72:73], 0, s[48:49]
	v_lshl_add_u64 v[72:73], v[72:73], 0, s[28:29]
	v_mov_b32_e32 v69, v100
	v_mov_b32_e32 v68, v132
	v_mov_b32_e32 v70, v119
	v_mov_b32_e32 v71, v87
	v_lshl_add_u64 v[72:73], v[72:73], 0, v[108:109]
	v_permlane32_swap_b32_e32 v68, v69
	v_permlane32_swap_b32_e32 v70, v71
	v_lshl_add_u64 v[72:73], v[72:73], 0, v[106:107]
	global_store_dwordx4 v[72:73], v[68:71], off
	v_add_co_u32_e32 v72, vcc, 0x10000, v72
	s_nop 0
	v_mov_b32_e32 v69, v66
	v_mov_b32_e32 v68, v67
	v_mov_b32_e32 v70, v135
	v_mov_b32_e32 v71, v103
	v_permlane32_swap_b32_e32 v68, v69
	s_nop 0
	v_permlane32_swap_b32_e32 v70, v71
	v_addc_co_u32_e32 v73, vcc, 0, v73, vcc
	global_store_dwordx4 v[72:73], v[68:71], off
	s_mov_b64 s[34:35], 0

.LBB0_4095:
	ds_read_b32 v66, v184 offset:512
	s_and_b64 vcc, exec, s[6:7]
	s_mov_b64 s[34:35], -1
	s_waitcnt lgkmcnt(0)
	v_mov_b32_e32 v67, v66
	s_cbranch_vccnz .LBB0_4097
	v_pk_mul_f32 v[72:73], v[60:61], v[66:67]
	s_nop 0
	v_add_u32_e32 v86, s50, v174
	v_cvt_pk_fp8_f32 v64, v72, v73
	ds_read_b128 v[86:89], v86 offset:512
	v_mov_b32_e32 v114, v66
	v_mov_b32_e32 v115, v66
	v_pk_mul_f32 v[72:73], v[62:63], v[114:115]
	v_pk_mul_f32 v[116:117], v[56:57], v[66:67]
	v_cvt_pk_fp8_f32 v64, v72, v73 op_sel:[0,0,1]
	s_nop 0
	v_cvt_pk_fp8_f32 v73, v116, v117
	s_waitcnt lgkmcnt(0)
	v_pk_mul_f32 v[116:117], v[52:53], v[86:87]
	s_nop 0
	v_cvt_pk_fp8_f32 v72, v116, v117
	v_pk_mul_f32 v[114:115], v[58:59], v[114:115]
	v_pk_mul_f32 v[86:87], v[48:49], v[86:87]
	v_cvt_pk_fp8_f32 v73, v114, v115 op_sel:[0,0,1]
	v_pk_mul_f32 v[114:115], v[54:55], v[88:89]
	v_pk_mul_f32 v[88:89], v[50:51], v[88:89]
	v_cvt_pk_fp8_f32 v72, v114, v115 op_sel:[0,0,1]
	s_mov_b64 s[34:35], 0

.LBB0_4099:
	ds_read_b32 v52, v184 offset:576
	s_and_b64 vcc, exec, s[6:7]
	s_mov_b64 s[34:35], -1
	s_waitcnt lgkmcnt(0)
	v_mov_b32_e32 v53, v52
	s_cbranch_vccnz .LBB0_4101
	v_pk_mul_f32 v[48:49], v[44:45], v[52:53]
	s_nop 0
	v_cvt_pk_fp8_f32 v54, v48, v49
	v_add_u32_e32 v48, s50, v174
	ds_read_b128 v[48:51], v48 offset:576
	v_mov_b32_e32 v56, v52
	v_mov_b32_e32 v57, v52
	v_pk_mul_f32 v[58:59], v[46:47], v[56:57]
	s_nop 0
	v_cvt_pk_fp8_f32 v54, v58, v59 op_sel:[0,0,1]
	v_pk_mul_f32 v[58:59], v[40:41], v[52:53]
	s_nop 0
	v_cvt_pk_fp8_f32 v67, v58, v59
	s_waitcnt lgkmcnt(0)
	v_pk_mul_f32 v[58:59], v[36:37], v[48:49]
	v_pk_mul_f32 v[56:57], v[42:43], v[56:57]
	v_cvt_pk_fp8_f32 v55, v58, v59
	v_cvt_pk_fp8_f32 v67, v56, v57 op_sel:[0,0,1]
	v_pk_mul_f32 v[56:57], v[38:39], v[50:51]
	v_pk_mul_f32 v[50:51], v[34:35], v[50:51]
	v_cvt_pk_fp8_f32 v55, v56, v57 op_sel:[0,0,1]
	v_pk_mul_f32 v[48:49], v[32:33], v[48:49]
	s_mov_b64 s[34:35], 0

.LBB0_4103:
	ds_read_b32 v34, v184 offset:640
	s_and_b64 vcc, exec, s[6:7]
	s_mov_b64 s[34:35], -1
	s_waitcnt lgkmcnt(0)
	v_mov_b32_e32 v35, v34
	s_cbranch_vccnz .LBB0_4105
	v_pk_mul_f32 v[36:37], v[28:29], v[34:35]
	s_nop 0
	v_add_u32_e32 v33, s50, v174
	v_cvt_pk_fp8_f32 v32, v36, v37
	ds_read_b128 v[38:41], v33 offset:640
	v_mov_b32_e32 v42, v34
	v_mov_b32_e32 v43, v34
	v_pk_mul_f32 v[36:37], v[30:31], v[42:43]
	s_nop 0
	v_cvt_pk_fp8_f32 v32, v36, v37 op_sel:[0,0,1]
	v_pk_mul_f32 v[36:37], v[24:25], v[34:35]
	s_waitcnt lgkmcnt(0)
	v_pk_mul_f32 v[44:45], v[20:21], v[38:39]
	v_cvt_pk_fp8_f32 v33, v36, v37
	s_nop 0
	v_cvt_pk_fp8_f32 v36, v44, v45
	v_pk_mul_f32 v[42:43], v[26:27], v[42:43]
	v_pk_mul_f32 v[38:39], v[16:17], v[38:39]
	v_cvt_pk_fp8_f32 v33, v42, v43 op_sel:[0,0,1]
	v_pk_mul_f32 v[42:43], v[22:23], v[40:41]
	v_pk_mul_f32 v[40:41], v[18:19], v[40:41]
	v_cvt_pk_fp8_f32 v36, v42, v43 op_sel:[0,0,1]
	s_mov_b64 s[34:35], 0

.LBB0_4107:
	ds_read_b32 v16, v184 offset:704
	s_and_b64 vcc, exec, s[6:7]
	s_mov_b64 s[34:35], -1
	s_waitcnt lgkmcnt(0)
	v_mov_b32_e32 v17, v16
	v_pk_mul_f32 v[20:21], v[14:15], v[16:17] op_sel_hi:[1,0]
	v_pk_mul_f32 v[18:19], v[12:13], v[16:17] op_sel_hi:[1,0]
	s_cbranch_vccnz .LBB0_4109
	v_add_u32_e32 v12, s50, v174
	ds_read_b128 v[12:15], v12 offset:704
	v_pk_mul_f32 v[26:27], v[8:9], v[16:17]
	s_nop 0
	s_nop 0
	v_cvt_pk_fp8_f32 v35, v26, v27
	s_waitcnt lgkmcnt(0)
	v_pk_mul_f32 v[26:27], v[4:5], v[12:13]
	s_nop 0
	v_cvt_pk_fp8_f32 v22, v18, v19
	v_cvt_pk_fp8_f32 v23, v26, v27
	v_mov_b32_e32 v24, v16
	v_mov_b32_e32 v25, v16
	v_pk_mul_f32 v[24:25], v[10:11], v[24:25]
	v_cvt_pk_fp8_f32 v22, v20, v21 op_sel:[0,0,1]
	v_cvt_pk_fp8_f32 v35, v24, v25 op_sel:[0,0,1]
	v_pk_mul_f32 v[24:25], v[6:7], v[14:15]
	v_pk_mul_f32 v[14:15], v[2:3], v[14:15]
	v_cvt_pk_fp8_f32 v23, v24, v25 op_sel:[0,0,1]
	v_pk_mul_f32 v[12:13], v[0:1], v[12:13]
	s_mov_b64 s[34:35], 0

.LBB0_4111:
	s_nop 0
	v_cvt_pk_fp8_f32 v0, v38, v39
	s_waitcnt vmcnt(1)
	s_nop 0
	s_nop 0
	s_nop 0
	v_cvt_pk_fp8_f32 v75, v48, v49
	v_cvt_pk_fp8_f32 v1, v86, v87
	v_cvt_pk_fp8_f32 v39, v12, v13
	v_cvt_pk_fp8_f32 v0, v40, v41 op_sel:[0,0,1]
	v_cvt_pk_fp8_f32 v75, v50, v51 op_sel:[0,0,1]
	v_cvt_pk_fp8_f32 v1, v88, v89 op_sel:[0,0,1]
	v_cvt_pk_fp8_f32 v39, v14, v15 op_sel:[0,0,1]
	s_ashr_i32 s9, s8, 31
	s_and_b64 vcc, exec, s[6:7]
	s_mov_b64 s[4:5], -1
	v_readlane_b32 s27, v254, 39
	s_cbranch_vccnz .LBB0_4113
	s_lshl_b64 s[4:5], s[8:9], 11
	v_readlane_b32 s6, v253, 61
	s_add_u32 s4, s6, s4
	v_readlane_b32 s6, v252, 59
	s_addc_u32 s5, s6, s5
	s_lshl_b32 s6, s2, 7
	s_ashr_i32 s7, s6, 31
	s_add_u32 s4, s4, s6
	s_addc_u32 s5, s5, s7
	s_add_u32 s4, s4, s44
	s_addc_u32 s5, s5, 0
	v_mov_b32_e32 v4, v54
	v_mov_b32_e32 v2, v64
	v_mov_b32_e32 v5, v67
	v_mov_b32_e32 v3, v73
	v_permlane32_swap_b32_e32 v2, v4
	s_nop 0
	v_permlane32_swap_b32_e32 v3, v5
	v_lshl_add_u64 v[10:11], s[4:5], 0, v[110:111]
	s_nop 0
	v_permlane16_swap_b32_e32 v2, v3
	v_permlane16_swap_b32_e32 v4, v5
	v_lshl_add_u64 v[10:11], v[10:11], 0, v[170:171]
	s_mov_b32 s4, 0x10000
	global_store_dwordx4 v[10:11], v[2:5], off
	v_mov_b32_e32 v8, v22
	v_mov_b32_e32 v6, v32
	v_add_co_u32_e32 v2, vcc, s4, v10
	s_and_b32 s4, s10, -16
	s_add_i32 s4, s2, s4
	v_mov_b32_e32 v9, v35
	v_mov_b32_e32 v7, v33
	s_ashr_i32 s5, s4, 31
	v_permlane32_swap_b32_e32 v6, v8
	v_permlane32_swap_b32_e32 v7, v9
	s_lshl_b64 s[4:5], s[4:5], 19
	s_nop 0
	v_permlane16_swap_b32_e32 v6, v7
	v_permlane16_swap_b32_e32 v8, v9
	v_addc_co_u32_e32 v3, vcc, 0, v11, vcc
	s_add_u32 s4, s97, s4
	v_readlane_b32 s6, v253, 52
	global_store_dwordx4 v[2:3], v[6:9], off
	s_addc_u32 s5, s6, s5
	s_and_b32 s48, s22, 0xf00
	v_lshlrev_b32_e32 v6, 12, v65
	v_mov_b32_e32 v7, v171
	v_lshl_add_u64 v[6:7], s[4:5], 0, v[6:7]
	v_lshl_add_u64 v[6:7], v[6:7], 0, s[48:49]
	v_lshl_add_u64 v[6:7], v[6:7], 0, s[28:29]
	v_mov_b32_e32 v2, v72
	v_mov_b32_e32 v3, v36
	v_mov_b32_e32 v5, v23
	v_mov_b32_e32 v4, v55
	v_lshl_add_u64 v[6:7], v[6:7], 0, v[108:109]
	v_permlane32_swap_b32_e32 v2, v3
	v_permlane32_swap_b32_e32 v4, v5
	v_lshl_add_u64 v[6:7], v[6:7], 0, v[106:107]
	global_store_dwordx4 v[6:7], v[2:5], off offset:128
	v_add_co_u32_e32 v6, vcc, 0x10000, v6
	s_nop 0
	v_mov_b32_e32 v2, v1
	v_mov_b32_e32 v3, v0
	v_mov_b32_e32 v5, v39
	v_mov_b32_e32 v4, v75
	v_permlane32_swap_b32_e32 v2, v3
	s_nop 0
	v_permlane32_swap_b32_e32 v4, v5
	v_addc_co_u32_e32 v7, vcc, 0, v7, vcc
	s_mov_b64 s[4:5], 0
	global_store_dwordx4 v[6:7], v[2:5], off offset:128

.LBB0_4221:
	s_waitcnt vmcnt(31)
	v_mov_b32_e32 v128, v0
	s_waitcnt vmcnt(30)
	v_mov_b32_e32 v129, v4
	v_pk_mul_f32 v[128:129], v[128:129], s[68:69] op_sel_hi:[1,0]
	s_nop 0
	v_cvt_pk_fp8_f32 v130, v128, v129
	s_waitcnt vmcnt(29)
	v_mov_b32_e32 v128, v8
	s_waitcnt vmcnt(28)
	v_mov_b32_e32 v129, v12
	v_pk_mul_f32 v[128:129], v[128:129], s[68:69] op_sel_hi:[1,0]
	s_nop 0
	v_cvt_pk_fp8_f32 v130, v128, v129 op_sel:[0,0,1]
	v_mov_b32_e32 v128, v1
	v_mov_b32_e32 v129, v5
	v_pk_mul_f32 v[128:129], v[128:129], s[68:69] op_sel_hi:[1,0]
	s_nop 0
	v_cvt_pk_fp8_f32 v131, v128, v129
	v_mov_b32_e32 v128, v9
	v_mov_b32_e32 v129, v13
	v_pk_mul_f32 v[128:129], v[128:129], s[68:69] op_sel_hi:[1,0]
	s_nop 0
	v_cvt_pk_fp8_f32 v131, v128, v129 op_sel:[0,0,1]
	v_mov_b32_e32 v128, v2
	v_mov_b32_e32 v129, v6
	v_pk_mul_f32 v[128:129], v[128:129], s[68:69] op_sel_hi:[1,0]
	v_mov_b32_e32 v144, v171
	v_cvt_pk_fp8_f32 v136, v128, v129
	v_mov_b32_e32 v128, v10
	v_mov_b32_e32 v129, v14
	v_pk_mul_f32 v[128:129], v[128:129], s[68:69] op_sel_hi:[1,0]
	v_mov_b32_e32 v145, v171
	v_cvt_pk_fp8_f32 v136, v128, v129 op_sel:[0,0,1]
	v_mov_b32_e32 v128, v3
	v_mov_b32_e32 v129, v7
	v_pk_mul_f32 v[128:129], v[128:129], s[68:69] op_sel_hi:[1,0]
	v_add_u32_e32 v143, 0x4000, v141
	v_cvt_pk_fp8_f32 v137, v128, v129
	v_mov_b32_e32 v128, v11
	v_mov_b32_e32 v129, v15
	v_pk_mul_f32 v[128:129], v[128:129], s[68:69] op_sel_hi:[1,0]
	v_add_u32_e32 v142, 0x8400, v141
	v_cvt_pk_fp8_f32 v137, v128, v129 op_sel:[0,0,1]
	s_waitcnt vmcnt(27)
	v_mov_b32_e32 v128, v16
	s_waitcnt vmcnt(26)
	v_mov_b32_e32 v129, v20
	ds_write2_b32 v141, v130, v131 offset1:33
	ds_write2_b32 v141, v136, v137 offset0:66 offset1:99
	v_pk_mul_f32 v[128:129], v[128:129], s[68:69] op_sel_hi:[1,0]
	s_nop 0
	v_cvt_pk_fp8_f32 v130, v128, v129
	s_waitcnt vmcnt(25)
	v_mov_b32_e32 v128, v24
	s_waitcnt vmcnt(24)
	v_mov_b32_e32 v129, v28
	v_pk_mul_f32 v[128:129], v[128:129], s[68:69] op_sel_hi:[1,0]
	s_nop 0
	v_cvt_pk_fp8_f32 v130, v128, v129 op_sel:[0,0,1]
	v_mov_b32_e32 v128, v17
	v_mov_b32_e32 v129, v21
	v_pk_mul_f32 v[128:129], v[128:129], s[68:69] op_sel_hi:[1,0]
	s_nop 0
	v_cvt_pk_fp8_f32 v131, v128, v129
	v_mov_b32_e32 v128, v25
	v_mov_b32_e32 v129, v29
	v_pk_mul_f32 v[128:129], v[128:129], s[68:69] op_sel_hi:[1,0]
	s_nop 0
	v_cvt_pk_fp8_f32 v131, v128, v129 op_sel:[0,0,1]
	v_mov_b32_e32 v128, v18
	v_mov_b32_e32 v129, v22
	v_pk_mul_f32 v[128:129], v[128:129], s[68:69] op_sel_hi:[1,0]
	v_mov_b32_e32 v146, v171
	v_cvt_pk_fp8_f32 v136, v128, v129
	v_mov_b32_e32 v128, v26
	v_mov_b32_e32 v129, v30
	v_pk_mul_f32 v[128:129], v[128:129], s[68:69] op_sel_hi:[1,0]
	s_cmp_lt_i32 s66, 2
	v_cvt_pk_fp8_f32 v136, v128, v129 op_sel:[0,0,1]
	v_mov_b32_e32 v128, v19
	v_mov_b32_e32 v129, v23
	v_pk_mul_f32 v[128:129], v[128:129], s[68:69] op_sel_hi:[1,0]
	s_nop 0
	v_cvt_pk_fp8_f32 v137, v128, v129
	v_mov_b32_e32 v128, v27
	v_mov_b32_e32 v129, v31
	v_pk_mul_f32 v[128:129], v[128:129], s[68:69] op_sel_hi:[1,0]
	s_nop 0
	v_cvt_pk_fp8_f32 v137, v128, v129 op_sel:[0,0,1]
	s_waitcnt vmcnt(23)
	v_mov_b32_e32 v128, v48
	s_waitcnt vmcnt(22)
	v_mov_b32_e32 v129, v52
	v_pk_mul_f32 v[128:129], v[128:129], s[68:69] op_sel_hi:[1,0]
	ds_write2_b32 v143, v130, v131 offset0:128 offset1:161
	ds_write2_b32 v143, v136, v137 offset0:194 offset1:227
	v_cvt_pk_fp8_f32 v144, v128, v129
	s_waitcnt vmcnt(21)
	v_mov_b32_e32 v128, v56
	s_waitcnt vmcnt(20)
	v_mov_b32_e32 v129, v60
	v_pk_mul_f32 v[128:129], v[128:129], s[68:69] op_sel_hi:[1,0]
	s_nop 0
	v_cvt_pk_fp8_f32 v144, v128, v129 op_sel:[0,0,1]
	v_mov_b32_e32 v128, v49
	v_mov_b32_e32 v129, v53
	v_pk_mul_f32 v[128:129], v[128:129], s[68:69] op_sel_hi:[1,0]
	s_nop 0
	v_cvt_pk_fp8_f32 v145, v128, v129
	v_mov_b32_e32 v128, v57
	v_mov_b32_e32 v129, v61
	v_pk_mul_f32 v[128:129], v[128:129], s[68:69] op_sel_hi:[1,0]
	s_nop 0
	v_cvt_pk_fp8_f32 v145, v128, v129 op_sel:[0,0,1]
	v_mov_b32_e32 v128, v50
	v_mov_b32_e32 v129, v54
	v_pk_mul_f32 v[128:129], v[128:129], s[68:69] op_sel_hi:[1,0]
	s_nop 0
	v_cvt_pk_fp8_f32 v130, v128, v129
	v_mov_b32_e32 v128, v58
	v_mov_b32_e32 v129, v62
	v_pk_mul_f32 v[128:129], v[128:129], s[68:69] op_sel_hi:[1,0]
	ds_write2_b32 v142, v144, v145 offset1:33
	v_cvt_pk_fp8_f32 v130, v128, v129 op_sel:[0,0,1]
	v_mov_b32_e32 v128, v51
	v_mov_b32_e32 v129, v55
	v_pk_mul_f32 v[128:129], v[128:129], s[68:69] op_sel_hi:[1,0]
	s_nop 0
	v_cvt_pk_fp8_f32 v131, v128, v129
	v_mov_b32_e32 v128, v59
	v_mov_b32_e32 v129, v63
	v_pk_mul_f32 v[128:129], v[128:129], s[68:69] op_sel_hi:[1,0]
	v_add_u32_e32 v144, 0xc400, v141
	v_cvt_pk_fp8_f32 v131, v128, v129 op_sel:[0,0,1]
	s_waitcnt vmcnt(19)
	v_mov_b32_e32 v128, v96
	s_waitcnt vmcnt(18)
	v_mov_b32_e32 v129, v100
	v_pk_mul_f32 v[128:129], v[128:129], s[68:69] op_sel_hi:[1,0]
	ds_write2_b32 v142, v130, v131 offset0:66 offset1:99
	v_cvt_pk_fp8_f32 v136, v128, v129
	s_waitcnt vmcnt(17)
	v_mov_b32_e32 v128, v104
	s_waitcnt vmcnt(16)
	v_mov_b32_e32 v129, v108
	v_pk_mul_f32 v[128:129], v[128:129], s[68:69] op_sel_hi:[1,0]
	s_nop 0
	v_cvt_pk_fp8_f32 v136, v128, v129 op_sel:[0,0,1]
	v_mov_b32_e32 v128, v97
	v_mov_b32_e32 v129, v101
	v_pk_mul_f32 v[128:129], v[128:129], s[68:69] op_sel_hi:[1,0]
	s_nop 0
	v_cvt_pk_fp8_f32 v137, v128, v129
	v_mov_b32_e32 v128, v105
	v_mov_b32_e32 v129, v109
	v_pk_mul_f32 v[128:129], v[128:129], s[68:69] op_sel_hi:[1,0]
	s_nop 0
	v_cvt_pk_fp8_f32 v137, v128, v129 op_sel:[0,0,1]
	v_mov_b32_e32 v128, v98
	v_mov_b32_e32 v129, v102
	v_pk_mul_f32 v[128:129], v[128:129], s[68:69] op_sel_hi:[1,0]
	s_nop 0
	v_cvt_pk_fp8_f32 v145, v128, v129
	v_mov_b32_e32 v128, v106
	v_mov_b32_e32 v129, v110
	v_pk_mul_f32 v[128:129], v[128:129], s[68:69] op_sel_hi:[1,0]
	s_nop 0
	v_cvt_pk_fp8_f32 v145, v128, v129 op_sel:[0,0,1]
	v_mov_b32_e32 v128, v99
	v_mov_b32_e32 v129, v103
	v_pk_mul_f32 v[128:129], v[128:129], s[68:69] op_sel_hi:[1,0]
	s_nop 0
	v_cvt_pk_fp8_f32 v146, v128, v129
	v_mov_b32_e32 v128, v107
	v_mov_b32_e32 v129, v111
	v_pk_mul_f32 v[128:129], v[128:129], s[68:69] op_sel_hi:[1,0]
	s_nop 0
	v_cvt_pk_fp8_f32 v146, v128, v129 op_sel:[0,0,1]
	ds_write2_b32 v144, v136, v137 offset0:128 offset1:161
	ds_write2_b32 v144, v145, v146 offset0:194 offset1:227
	s_waitcnt lgkmcnt(0)
	s_barrier
	ds_read2_b32 v[128:129], v140 offset1:1
	ds_read2_b32 v[130:131], v140 offset0:2 offset1:3
	v_lshl_add_u32 v136, s65, 6, v138
	s_cbranch_scc1 .LBB0_4227
	s_cmp_gt_i32 s66, 2
	s_cbranch_scc0 .LBB0_4228
	s_cmp_eq_u32 s66, 3
	s_mov_b64 s[34:35], -1
	s_cbranch_scc0 .LBB0_4225
	v_lshlrev_b32_e32 v137, 1, v136
	v_and_b32_e32 v145, 0x7f, v136
	s_movk_i32 s11, 0xff00
	v_and_or_b32 v137, v137, s11, v145
	s_mov_b64 s[34:35], 0

.Lcvw_c4:
	v_mov_b32_e32 v128, v36
	v_mov_b32_e32 v129, v32
	v_pk_mul_f32 v[128:129], v[128:129], s[68:69] op_sel_hi:[1,0]
	s_nop 0
	v_cvt_pk_fp8_f32 v130, v128, v129
	v_mov_b32_e32 v128, v44
	v_mov_b32_e32 v129, v40
	v_pk_mul_f32 v[128:129], v[128:129], s[68:69] op_sel_hi:[1,0]
	s_nop 0
	v_cvt_pk_fp8_f32 v130, v128, v129 op_sel:[0,0,1]
	v_mov_b32_e32 v128, v37
	v_mov_b32_e32 v129, v33
	v_pk_mul_f32 v[128:129], v[128:129], s[68:69] op_sel_hi:[1,0]
	s_nop 0
	v_cvt_pk_fp8_f32 v131, v128, v129
	v_mov_b32_e32 v128, v45
	v_mov_b32_e32 v129, v41
	v_pk_mul_f32 v[128:129], v[128:129], s[68:69] op_sel_hi:[1,0]
	s_nop 0
	v_cvt_pk_fp8_f32 v131, v128, v129 op_sel:[0,0,1]
	v_mov_b32_e32 v128, v38
	v_mov_b32_e32 v129, v34
	v_pk_mul_f32 v[128:129], v[128:129], s[68:69] op_sel_hi:[1,0]
	s_nop 0
	v_cvt_pk_fp8_f32 v136, v128, v129
	v_mov_b32_e32 v128, v46
	v_mov_b32_e32 v129, v42
	v_pk_mul_f32 v[128:129], v[128:129], s[68:69] op_sel_hi:[1,0]
	s_nop 0
	v_cvt_pk_fp8_f32 v136, v128, v129 op_sel:[0,0,1]
	v_mov_b32_e32 v128, v39
	v_mov_b32_e32 v129, v35
	v_pk_mul_f32 v[128:129], v[128:129], s[68:69] op_sel_hi:[1,0]
	s_nop 0
	v_cvt_pk_fp8_f32 v137, v128, v129
	v_mov_b32_e32 v128, v47
	v_mov_b32_e32 v129, v43
	v_pk_mul_f32 v[128:129], v[128:129], s[68:69] op_sel_hi:[1,0]
	s_nop 0
	v_cvt_pk_fp8_f32 v137, v128, v129 op_sel:[0,0,1]
	v_mov_b32_e32 v128, v68
	v_mov_b32_e32 v129, v64
	v_pk_mul_f32 v[128:129], v[128:129], s[68:69] op_sel_hi:[1,0]
	s_cmp_lt_i32 s17, 2
	v_cvt_pk_fp8_f32 v151, v128, v129
	v_mov_b32_e32 v128, v76
	v_mov_b32_e32 v129, v72
	v_pk_mul_f32 v[128:129], v[128:129], s[68:69] op_sel_hi:[1,0]
	s_nop 0
	v_cvt_pk_fp8_f32 v151, v128, v129 op_sel:[0,0,1]
	v_mov_b32_e32 v128, v69
	v_mov_b32_e32 v129, v65
	v_pk_mul_f32 v[128:129], v[128:129], s[68:69] op_sel_hi:[1,0]
	s_nop 0
	v_cvt_pk_fp8_f32 v152, v128, v129
	v_mov_b32_e32 v128, v77
	v_mov_b32_e32 v129, v73
	v_pk_mul_f32 v[128:129], v[128:129], s[68:69] op_sel_hi:[1,0]
	s_nop 0
	v_cvt_pk_fp8_f32 v152, v128, v129 op_sel:[0,0,1]
	v_mov_b32_e32 v128, v70
	v_mov_b32_e32 v129, v66
	v_pk_mul_f32 v[128:129], v[128:129], s[68:69] op_sel_hi:[1,0]
	s_nop 0
	v_cvt_pk_fp8_f32 v153, v128, v129
	v_mov_b32_e32 v128, v78
	v_mov_b32_e32 v129, v74
	v_pk_mul_f32 v[128:129], v[128:129], s[68:69] op_sel_hi:[1,0]
	s_nop 0
	v_cvt_pk_fp8_f32 v153, v128, v129 op_sel:[0,0,1]
	v_mov_b32_e32 v128, v71
	v_mov_b32_e32 v129, v67
	v_pk_mul_f32 v[128:129], v[128:129], s[68:69] op_sel_hi:[1,0]
	s_nop 0
	v_cvt_pk_fp8_f32 v154, v128, v129
	v_mov_b32_e32 v128, v79
	v_mov_b32_e32 v129, v75
	v_pk_mul_f32 v[128:129], v[128:129], s[68:69] op_sel_hi:[1,0]
	s_nop 0
	v_cvt_pk_fp8_f32 v154, v128, v129 op_sel:[0,0,1]
	v_mov_b32_e32 v128, v84
	v_mov_b32_e32 v129, v80
	ds_write2_b32 v141, v130, v131 offset1:33
	ds_write2_b32 v141, v136, v137 offset0:66 offset1:99
	ds_write2_b32 v143, v151, v152 offset0:128 offset1:161
	ds_write2_b32 v143, v153, v154 offset0:194 offset1:227
	v_pk_mul_f32 v[128:129], v[128:129], s[68:69] op_sel_hi:[1,0]
	s_nop 0
	v_cvt_pk_fp8_f32 v130, v128, v129
	v_mov_b32_e32 v128, v92
	v_mov_b32_e32 v129, v88
	v_pk_mul_f32 v[128:129], v[128:129], s[68:69] op_sel_hi:[1,0]
	s_nop 0
	v_cvt_pk_fp8_f32 v130, v128, v129 op_sel:[0,0,1]
	v_mov_b32_e32 v128, v85
	v_mov_b32_e32 v129, v81
	v_pk_mul_f32 v[128:129], v[128:129], s[68:69] op_sel_hi:[1,0]
	s_nop 0
	v_cvt_pk_fp8_f32 v131, v128, v129
	v_mov_b32_e32 v128, v93
	v_mov_b32_e32 v129, v89
	v_pk_mul_f32 v[128:129], v[128:129], s[68:69] op_sel_hi:[1,0]
	s_nop 0
	v_cvt_pk_fp8_f32 v131, v128, v129 op_sel:[0,0,1]
	v_mov_b32_e32 v128, v86
	v_mov_b32_e32 v129, v82
	v_pk_mul_f32 v[128:129], v[128:129], s[68:69] op_sel_hi:[1,0]
	s_nop 0
	v_cvt_pk_fp8_f32 v136, v128, v129
	v_mov_b32_e32 v128, v94
	v_mov_b32_e32 v129, v90
	v_pk_mul_f32 v[128:129], v[128:129], s[68:69] op_sel_hi:[1,0]
	s_nop 0
	v_cvt_pk_fp8_f32 v136, v128, v129 op_sel:[0,0,1]
	v_mov_b32_e32 v128, v87
	v_mov_b32_e32 v129, v83
	v_pk_mul_f32 v[128:129], v[128:129], s[68:69] op_sel_hi:[1,0]
	s_nop 0
	v_cvt_pk_fp8_f32 v137, v128, v129
	v_mov_b32_e32 v128, v95
	v_mov_b32_e32 v129, v91
	v_pk_mul_f32 v[128:129], v[128:129], s[68:69] op_sel_hi:[1,0]
	s_nop 0
	v_cvt_pk_fp8_f32 v137, v128, v129 op_sel:[0,0,1]
	v_mov_b32_e32 v128, v116
	v_mov_b32_e32 v129, v112
	v_pk_mul_f32 v[128:129], v[128:129], s[68:69] op_sel_hi:[1,0]
	s_nop 0
	v_cvt_pk_fp8_f32 v143, v128, v129
	v_mov_b32_e32 v128, v124
	v_mov_b32_e32 v129, v120
	v_pk_mul_f32 v[128:129], v[128:129], s[68:69] op_sel_hi:[1,0]
	s_nop 0
	v_cvt_pk_fp8_f32 v143, v128, v129 op_sel:[0,0,1]
	v_mov_b32_e32 v128, v117
	v_mov_b32_e32 v129, v113
	v_pk_mul_f32 v[128:129], v[128:129], s[68:69] op_sel_hi:[1,0]
	s_nop 0
	v_cvt_pk_fp8_f32 v151, v128, v129
	v_mov_b32_e32 v128, v125
	v_mov_b32_e32 v129, v121
	v_pk_mul_f32 v[128:129], v[128:129], s[68:69] op_sel_hi:[1,0]
	s_nop 0
	v_cvt_pk_fp8_f32 v151, v128, v129 op_sel:[0,0,1]
	v_mov_b32_e32 v128, v118
	v_mov_b32_e32 v129, v114
	v_pk_mul_f32 v[128:129], v[128:129], s[68:69] op_sel_hi:[1,0]
	s_nop 0
	v_cvt_pk_fp8_f32 v152, v128, v129
	v_mov_b32_e32 v128, v126
	v_mov_b32_e32 v129, v122
	v_pk_mul_f32 v[128:129], v[128:129], s[68:69] op_sel_hi:[1,0]
	s_nop 0
	v_cvt_pk_fp8_f32 v152, v128, v129 op_sel:[0,0,1]
	v_mov_b32_e32 v128, v119
	v_mov_b32_e32 v129, v115
	v_pk_mul_f32 v[128:129], v[128:129], s[68:69] op_sel_hi:[1,0]
	s_nop 0
	v_cvt_pk_fp8_f32 v153, v128, v129
	v_mov_b32_e32 v128, v127
	v_mov_b32_e32 v129, v123
	v_pk_mul_f32 v[128:129], v[128:129], s[68:69] op_sel_hi:[1,0]
	s_nop 0
	v_cvt_pk_fp8_f32 v153, v128, v129 op_sel:[0,0,1]
	ds_write2_b32 v142, v130, v131 offset1:33
	ds_write2_b32 v142, v136, v137 offset0:66 offset1:99
	ds_write2_b32 v144, v143, v151 offset0:128 offset1:161
	ds_write2_b32 v144, v152, v153 offset0:194 offset1:227
	s_waitcnt lgkmcnt(0)
	s_barrier
	ds_read2_b32 v[128:129], v140 offset1:1
	ds_read2_b32 v[130:131], v140 offset0:2 offset1:3
	v_lshl_add_u32 v136, s2, 6, v138
	s_cbranch_scc1 .LBB0_4371
	s_cmp_gt_i32 s17, 2
	s_cbranch_scc0 .LBB0_4372
	s_cmp_eq_u32 s17, 3
	s_mov_b64 s[34:35], -1
	s_cbranch_scc0 .LBB0_4369
	v_lshlrev_b32_e32 v137, 1, v136
	v_and_b32_e32 v142, 0x7f, v136
	s_movk_i32 s25, 0xff00
	v_and_or_b32 v137, v137, s25, v142
	s_mov_b64 s[34:35], 0

.LBB0_4516:
	s_nop 0
	s_nop 0
	s_nop 0
	s_nop 0
	s_nop 0
	s_nop 0
	s_nop 0
	s_nop 0
	v_cvt_pk_fp8_f32 v2, v13, v15
	v_cvt_pk_fp8_f32 v6, v10, v11
	v_cvt_pk_fp8_f32 v3, v144, v145
	v_cvt_pk_fp8_f32 v7, v128, v130
	v_cvt_pk_fp8_f32 v4, v148, v149
	v_cvt_pk_fp8_f32 v8, v134, v135
	v_cvt_pk_fp8_f32 v5, v152, v153
	v_cvt_pk_fp8_f32 v9, v138, v139
	v_lshl_add_u32 v154, s49, 14, v202
	v_add_u32_e32 v155, v154, v203
	v_add_u32_e32 v156, v154, v204
	ds_read_b128 v[210:213], v155
	ds_read_b128 v[214:217], v156
	v_cvt_pk_fp8_f32 v2, v129, v131 op_sel:[0,0,1]
	v_cvt_pk_fp8_f32 v6, v12, v14 op_sel:[0,0,1]
	v_cvt_pk_fp8_f32 v3, v146, v147 op_sel:[0,0,1]
	v_cvt_pk_fp8_f32 v7, v132, v133 op_sel:[0,0,1]
	v_cvt_pk_fp8_f32 v4, v150, v151 op_sel:[0,0,1]
	v_cvt_pk_fp8_f32 v8, v136, v137 op_sel:[0,0,1]
	v_cvt_pk_fp8_f32 v5, v142, v143 op_sel:[0,0,1]
	v_cvt_pk_fp8_f32 v9, v140, v141 op_sel:[0,0,1]
	v_fmamk_f32 v0, v102, 0x3dd53b94, v209
	v_exp_f32_e32 v102, v0
	v_fmamk_f32 v0, v118, 0x3dd53b94, v209
	v_exp_f32_e32 v118, v0
	v_fmamk_f32 v0, v103, 0x3dd53b94, v209
	s_waitcnt lgkmcnt(0)
	v_mfma_scale_f32_32x32x64_f8f6f4 v[64:79], v[210:217], v[2:9], v[64:79], v195, v195 op_sel_hi:[0,0,0]
	ds_read_b128 v[210:213], v155 offset:4096
	ds_read_b128 v[214:217], v156 offset:4096
	v_exp_f32_e32 v103, v0
	v_fmamk_f32 v0, v119, 0x3dd53b94, v209
	v_exp_f32_e32 v119, v0
	v_fmamk_f32 v0, v104, 0x3dd53b94, v209
	v_exp_f32_e32 v104, v0
	v_fmamk_f32 v0, v120, 0x3dd53b94, v209
	v_exp_f32_e32 v120, v0
	v_fmamk_f32 v0, v105, 0x3dd53b94, v209
	v_exp_f32_e32 v105, v0
	v_fmamk_f32 v0, v121, 0x3dd53b94, v209
	v_exp_f32_e32 v121, v0
	v_fmamk_f32 v0, v106, 0x3dd53b94, v209
	v_exp_f32_e32 v106, v0
	v_fmamk_f32 v0, v122, 0x3dd53b94, v209
	s_waitcnt lgkmcnt(0)
	v_mfma_scale_f32_32x32x64_f8f6f4 v[48:63], v[210:217], v[2:9], v[48:63], v195, v195 op_sel_hi:[0,0,0]
	ds_read_b128 v[210:213], v155 offset:8192
	ds_read_b128 v[214:217], v156 offset:8192
	v_exp_f32_e32 v122, v0
	v_fmamk_f32 v0, v107, 0x3dd53b94, v209
	v_exp_f32_e32 v107, v0
	v_fmamk_f32 v0, v123, 0x3dd53b94, v209
	v_exp_f32_e32 v123, v0
	v_fmamk_f32 v0, v108, 0x3dd53b94, v209
	v_exp_f32_e32 v108, v0
	v_fmamk_f32 v0, v124, 0x3dd53b94, v209
	v_exp_f32_e32 v124, v0
	v_fmamk_f32 v0, v109, 0x3dd53b94, v209
	v_exp_f32_e32 v109, v0
	v_fmamk_f32 v0, v125, 0x3dd53b94, v209
	v_exp_f32_e32 v125, v0
	s_mov_b32 s46, s40
	s_waitcnt lgkmcnt(0)
	v_mfma_scale_f32_32x32x64_f8f6f4 v[32:47], v[210:217], v[2:9], v[32:47], v195, v195 op_sel_hi:[0,0,0]
	ds_read_b128 v[216:219], v155 offset:12288
	ds_read_b128 v[220:223], v156 offset:12288
	s_mov_b32 s47, s40
	v_fmamk_f32 v0, v110, 0x3dd53b94, v209
	s_mov_b32 s41, s40
	s_mov_b32 s42, s40
	s_mov_b32 s43, s40
	s_mov_b32 s44, s40
	s_mov_b32 s45, s40
	v_exp_f32_e32 v110, v0
	v_fmamk_f32 v0, v126, 0x3dd53b94, v209
	v_exp_f32_e32 v126, v0
	v_fmamk_f32 v0, v111, 0x3dd53b94, v209
	v_fmac_f32_e32 v209, 0x3dd53b94, v127
	s_nop 0
	s_nop 0
	s_waitcnt lgkmcnt(0)
	v_mfma_scale_f32_32x32x64_f8f6f4 v[16:31], v[216:223], v[2:9], v[16:31], v195, v195 op_sel_hi:[0,0,0]
	v_mov_b64_e32 v[224:225], s[46:47]
	v_mov_b64_e32 v[222:223], s[44:45]
	v_mov_b64_e32 v[220:221], s[42:43]
	v_mov_b64_e32 v[218:219], s[40:41]
	s_nop 0
	s_nop 0
	s_nop 0
	s_nop 0
	s_nop 0
	s_nop 0
	v_exp_f32_e32 v111, v0
	v_cvt_pk_fp8_f32 v210, v96, v97
	v_exp_f32_e32 v127, v209
	v_cvt_pk_fp8_f32 v214, v112, v113
	v_cvt_pk_fp8_f32 v211, v100, v101
	v_cvt_pk_fp8_f32 v215, v116, v117
	v_cvt_pk_fp8_f32 v212, v104, v105
	v_cvt_pk_fp8_f32 v216, v120, v121
	v_cvt_pk_fp8_f32 v213, v108, v109
	v_cvt_pk_fp8_f32 v217, v124, v125
	v_add_u32_e32 v0, v154, v205
	v_mfma_scale_f32_32x32x64_f8f6f4 v[80:95], v[218:225], v[2:9], v[80:95], v195, v195 op_sel_hi:[0,0,0]
	v_add_u32_e32 v154, v154, v206
	ds_read_b128 v[2:5], v0
	ds_read_b128 v[6:9], v154
	v_cvt_pk_fp8_f32 v210, v98, v99 op_sel:[0,0,1]
	v_cvt_pk_fp8_f32 v214, v114, v115 op_sel:[0,0,1]
	v_cvt_pk_fp8_f32 v211, v102, v103 op_sel:[0,0,1]
	v_cvt_pk_fp8_f32 v215, v118, v119 op_sel:[0,0,1]
	v_cvt_pk_fp8_f32 v212, v106, v107 op_sel:[0,0,1]
	v_cvt_pk_fp8_f32 v216, v122, v123 op_sel:[0,0,1]
	v_cvt_pk_fp8_f32 v213, v110, v111 op_sel:[0,0,1]
	v_cvt_pk_fp8_f32 v217, v126, v127 op_sel:[0,0,1]
	s_waitcnt lgkmcnt(0)
	s_nop 0
	v_mfma_scale_f32_32x32x64_f8f6f4 v[64:79], v[2:9], v[210:217], v[64:79], v195, v195 op_sel_hi:[0,0,0]
	ds_read_b128 v[2:5], v0 offset:4096
	ds_read_b128 v[6:9], v154 offset:4096
	s_waitcnt lgkmcnt(0)
	v_mfma_scale_f32_32x32x64_f8f6f4 v[48:63], v[2:9], v[210:217], v[48:63], v195, v195 op_sel_hi:[0,0,0]
	ds_read_b128 v[2:5], v0 offset:8192
	ds_read_b128 v[6:9], v154 offset:8192
	s_waitcnt lgkmcnt(0)
	v_mfma_scale_f32_32x32x64_f8f6f4 v[32:47], v[2:9], v[210:217], v[32:47], v195, v195 op_sel_hi:[0,0,0]
	ds_read_b128 v[2:5], v0 offset:12288
	ds_read_b128 v[6:9], v154 offset:12288
	s_waitcnt lgkmcnt(0)
	v_mfma_scale_f32_32x32x64_f8f6f4 v[16:31], v[2:9], v[210:217], v[16:31], v195, v195 op_sel_hi:[0,0,0]
	v_mfma_scale_f32_32x32x64_f8f6f4 v[80:95], v[218:225], v[210:217], v[80:95], v195, v195 op_sel_hi:[0,0,0]

.LBB0_4533:
	s_nop 6
	v_rcp_f32_e32 v8, v80
	v_lshlrev_b64 v[2:3], 11, v[186:187]
	v_lshl_add_u64 v[2:3], s[82:83], 0, v[2:3]
	v_lshlrev_b32_e32 v0, 4, v197
	v_lshl_add_u64 v[6:7], v[2:3], 0, v[0:1]
	v_mul_f32_e32 v0, v64, v8
	v_mul_f32_e32 v3, v65, v8
	s_nop 0
	v_cvt_pk_fp8_f32 v2, v0, v3
	v_mul_f32_e32 v0, v68, v8
	v_mul_f32_e32 v3, v69, v8
	s_nop 0
	v_cvt_pk_fp8_f32 v4, v0, v3
	v_mul_f32_e32 v5, v66, v8
	v_mul_f32_e32 v9, v67, v8
	v_mul_f32_e32 v0, v70, v8
	v_mul_f32_e32 v3, v71, v8
	v_cvt_pk_fp8_f32 v2, v5, v9 op_sel:[0,0,1]
	v_cvt_pk_fp8_f32 v4, v0, v3 op_sel:[0,0,1]
	v_mul_f32_e32 v0, v72, v8
	v_mul_f32_e32 v5, v73, v8
	s_nop 0
	v_cvt_pk_fp8_f32 v3, v0, v5
	v_mul_f32_e32 v0, v76, v8
	v_mul_f32_e32 v11, v77, v8
	s_nop 0
	v_cvt_pk_fp8_f32 v5, v0, v11
	v_mul_f32_e32 v9, v74, v8
	v_mul_f32_e32 v10, v75, v8
	v_cvt_pk_fp8_f32 v3, v9, v10 op_sel:[0,0,1]
	v_mul_f32_e32 v0, v78, v8
	v_mul_f32_e32 v9, v79, v8
	v_cvt_pk_fp8_f32 v5, v0, v9 op_sel:[0,0,1]
	v_permlane32_swap_b32_e32 v2, v3
	v_mul_f32_e32 v0, v48, v8
	v_permlane32_swap_b32_e32 v4, v5
	global_store_dwordx4 v[6:7], v[2:5], off
	v_mul_f32_e32 v9, v51, v8
	v_mul_f32_e32 v11, v61, v8
	v_mul_f32_e32 v3, v49, v8
	s_nop 0
	v_cvt_pk_fp8_f32 v2, v0, v3
	v_mul_f32_e32 v0, v52, v8
	v_mul_f32_e32 v3, v53, v8
	s_nop 0
	v_cvt_pk_fp8_f32 v4, v0, v3
	v_mul_f32_e32 v5, v50, v8
	v_mul_f32_e32 v0, v54, v8
	v_mul_f32_e32 v3, v55, v8
	v_cvt_pk_fp8_f32 v2, v5, v9 op_sel:[0,0,1]
	v_cvt_pk_fp8_f32 v4, v0, v3 op_sel:[0,0,1]
	v_mul_f32_e32 v0, v56, v8
	v_mul_f32_e32 v5, v57, v8
	s_nop 0
	v_cvt_pk_fp8_f32 v3, v0, v5
	v_mul_f32_e32 v0, v60, v8
	s_nop 0
	v_cvt_pk_fp8_f32 v5, v0, v11
	v_mul_f32_e32 v9, v58, v8
	v_mul_f32_e32 v10, v59, v8
	v_cvt_pk_fp8_f32 v3, v9, v10 op_sel:[0,0,1]
	v_mul_f32_e32 v0, v62, v8
	v_mul_f32_e32 v9, v63, v8
	v_cvt_pk_fp8_f32 v5, v0, v9 op_sel:[0,0,1]
	v_permlane32_swap_b32_e32 v2, v3
	v_mul_f32_e32 v0, v32, v8
	v_permlane32_swap_b32_e32 v4, v5
	global_store_dwordx4 v[6:7], v[2:5], off offset:32
	v_mul_f32_e32 v9, v35, v8
	v_mul_f32_e32 v11, v45, v8
	v_mul_f32_e32 v3, v33, v8
	s_nop 0
	v_cvt_pk_fp8_f32 v2, v0, v3
	v_mul_f32_e32 v0, v36, v8
	v_mul_f32_e32 v3, v37, v8
	s_nop 0
	v_cvt_pk_fp8_f32 v4, v0, v3
	v_mul_f32_e32 v5, v34, v8
	v_mul_f32_e32 v0, v38, v8
	v_mul_f32_e32 v3, v39, v8
	v_cvt_pk_fp8_f32 v2, v5, v9 op_sel:[0,0,1]
	v_cvt_pk_fp8_f32 v4, v0, v3 op_sel:[0,0,1]
	v_mul_f32_e32 v0, v40, v8
	v_mul_f32_e32 v5, v41, v8
	s_nop 0
	v_cvt_pk_fp8_f32 v3, v0, v5
	v_mul_f32_e32 v0, v44, v8
	s_nop 0
	v_cvt_pk_fp8_f32 v5, v0, v11
	v_mul_f32_e32 v9, v42, v8
	v_mul_f32_e32 v10, v43, v8
	v_cvt_pk_fp8_f32 v3, v9, v10 op_sel:[0,0,1]
	v_mul_f32_e32 v0, v46, v8
	v_mul_f32_e32 v9, v47, v8
	v_cvt_pk_fp8_f32 v5, v0, v9 op_sel:[0,0,1]
	v_permlane32_swap_b32_e32 v2, v3
	v_mul_f32_e32 v0, v16, v8
	v_permlane32_swap_b32_e32 v4, v5
	global_store_dwordx4 v[6:7], v[2:5], off offset:64
	v_mul_f32_e32 v9, v19, v8
	v_mul_f32_e32 v11, v29, v8
	v_mul_f32_e32 v3, v17, v8
	s_nop 0
	v_cvt_pk_fp8_f32 v2, v0, v3
	v_mul_f32_e32 v0, v20, v8
	v_mul_f32_e32 v3, v21, v8
	s_nop 0
	v_cvt_pk_fp8_f32 v4, v0, v3
	v_mul_f32_e32 v5, v18, v8
	v_mul_f32_e32 v0, v22, v8
	v_mul_f32_e32 v3, v23, v8
	v_cvt_pk_fp8_f32 v2, v5, v9 op_sel:[0,0,1]
	v_cvt_pk_fp8_f32 v4, v0, v3 op_sel:[0,0,1]
	v_mul_f32_e32 v0, v24, v8
	v_mul_f32_e32 v5, v25, v8
	s_nop 0
	v_cvt_pk_fp8_f32 v3, v0, v5
	v_mul_f32_e32 v0, v28, v8
	s_nop 0
	v_cvt_pk_fp8_f32 v5, v0, v11
	v_mul_f32_e32 v9, v26, v8
	v_mul_f32_e32 v10, v27, v8
	v_mul_f32_e32 v0, v30, v8
	v_mul_f32_e32 v8, v31, v8
	v_cvt_pk_fp8_f32 v3, v9, v10 op_sel:[0,0,1]
	v_cvt_pk_fp8_f32 v5, v0, v8 op_sel:[0,0,1]
	s_and_b64 vcc, exec, s[52:53]
	v_permlane32_swap_b32_e32 v2, v3
	v_permlane32_swap_b32_e32 v4, v5
	global_store_dwordx4 v[6:7], v[2:5], off offset:96
	s_waitcnt vmcnt(0) lgkmcnt(0)
	s_barrier
	s_cbranch_vccz .LBB0_4535
	v_readlane_b32 s4, v254, 57
	v_readlane_b32 s5, v254, 58
	s_and_b64 s[4:5], s[4:5], s[78:79]
	s_cbranch_execz .LBB0_4536
	s_branch .LBB0_4537

.LBB0_4635:
	s_waitcnt vmcnt(31)
	v_mov_b32_e32 v130, v2
	s_waitcnt vmcnt(30)
	v_mov_b32_e32 v131, v6
	v_pk_mul_f32 v[130:131], v[130:131], s[64:65] op_sel_hi:[1,0]
	s_nop 0
	v_cvt_pk_fp8_f32 v132, v130, v131
	s_waitcnt vmcnt(29)
	v_mov_b32_e32 v130, v10
	s_waitcnt vmcnt(28)
	v_mov_b32_e32 v131, v14
	v_pk_mul_f32 v[130:131], v[130:131], s[64:65] op_sel_hi:[1,0]
	s_nop 0
	v_cvt_pk_fp8_f32 v132, v130, v131 op_sel:[0,0,1]
	v_mov_b32_e32 v130, v3
	v_mov_b32_e32 v131, v7
	v_pk_mul_f32 v[130:131], v[130:131], s[64:65] op_sel_hi:[1,0]
	s_nop 0
	v_cvt_pk_fp8_f32 v133, v130, v131
	v_mov_b32_e32 v130, v11
	v_mov_b32_e32 v131, v15
	v_pk_mul_f32 v[130:131], v[130:131], s[64:65] op_sel_hi:[1,0]
	s_nop 0
	v_cvt_pk_fp8_f32 v133, v130, v131 op_sel:[0,0,1]
	v_mov_b32_e32 v130, v4
	v_mov_b32_e32 v131, v8
	v_pk_mul_f32 v[130:131], v[130:131], s[64:65] op_sel_hi:[1,0]
	v_mov_b32_e32 v145, v1
	v_cvt_pk_fp8_f32 v136, v130, v131
	v_mov_b32_e32 v130, v12
	v_mov_b32_e32 v131, v16
	v_pk_mul_f32 v[130:131], v[130:131], s[64:65] op_sel_hi:[1,0]
	v_mov_b32_e32 v146, v1
	v_cvt_pk_fp8_f32 v136, v130, v131 op_sel:[0,0,1]
	v_mov_b32_e32 v130, v5
	v_mov_b32_e32 v131, v9
	v_pk_mul_f32 v[130:131], v[130:131], s[64:65] op_sel_hi:[1,0]
	v_add_u32_e32 v144, 0x4000, v142
	v_cvt_pk_fp8_f32 v137, v130, v131
	v_mov_b32_e32 v130, v13
	v_mov_b32_e32 v131, v17
	v_pk_mul_f32 v[130:131], v[130:131], s[64:65] op_sel_hi:[1,0]
	v_add_u32_e32 v143, 0x8400, v142
	v_cvt_pk_fp8_f32 v137, v130, v131 op_sel:[0,0,1]
	s_waitcnt vmcnt(27)
	v_mov_b32_e32 v130, v18
	s_waitcnt vmcnt(26)
	v_mov_b32_e32 v131, v22
	ds_write2_b32 v142, v132, v133 offset1:33
	ds_write2_b32 v142, v136, v137 offset0:66 offset1:99
	v_pk_mul_f32 v[130:131], v[130:131], s[64:65] op_sel_hi:[1,0]
	s_nop 0
	v_cvt_pk_fp8_f32 v132, v130, v131
	s_waitcnt vmcnt(25)
	v_mov_b32_e32 v130, v26
	s_waitcnt vmcnt(24)
	v_mov_b32_e32 v131, v30
	v_pk_mul_f32 v[130:131], v[130:131], s[64:65] op_sel_hi:[1,0]
	s_nop 0
	v_cvt_pk_fp8_f32 v132, v130, v131 op_sel:[0,0,1]
	v_mov_b32_e32 v130, v19
	v_mov_b32_e32 v131, v23
	v_pk_mul_f32 v[130:131], v[130:131], s[64:65] op_sel_hi:[1,0]
	s_nop 0
	v_cvt_pk_fp8_f32 v133, v130, v131
	v_mov_b32_e32 v130, v27
	v_mov_b32_e32 v131, v31
	v_pk_mul_f32 v[130:131], v[130:131], s[64:65] op_sel_hi:[1,0]
	s_nop 0
	v_cvt_pk_fp8_f32 v133, v130, v131 op_sel:[0,0,1]
	v_mov_b32_e32 v130, v20
	v_mov_b32_e32 v131, v24
	v_pk_mul_f32 v[130:131], v[130:131], s[64:65] op_sel_hi:[1,0]
	v_mov_b32_e32 v147, v1
	v_cvt_pk_fp8_f32 v136, v130, v131
	v_mov_b32_e32 v130, v28
	v_mov_b32_e32 v131, v32
	v_pk_mul_f32 v[130:131], v[130:131], s[64:65] op_sel_hi:[1,0]
	s_cmp_lt_i32 s66, 2
	v_cvt_pk_fp8_f32 v136, v130, v131 op_sel:[0,0,1]
	v_mov_b32_e32 v130, v21
	v_mov_b32_e32 v131, v25
	v_pk_mul_f32 v[130:131], v[130:131], s[64:65] op_sel_hi:[1,0]
	s_nop 0
	v_cvt_pk_fp8_f32 v137, v130, v131
	v_mov_b32_e32 v130, v29
	v_mov_b32_e32 v131, v33
	v_pk_mul_f32 v[130:131], v[130:131], s[64:65] op_sel_hi:[1,0]
	s_nop 0
	v_cvt_pk_fp8_f32 v137, v130, v131 op_sel:[0,0,1]
	s_waitcnt vmcnt(23)
	v_mov_b32_e32 v130, v50
	s_waitcnt vmcnt(22)
	v_mov_b32_e32 v131, v54
	v_pk_mul_f32 v[130:131], v[130:131], s[64:65] op_sel_hi:[1,0]
	ds_write2_b32 v144, v132, v133 offset0:128 offset1:161
	ds_write2_b32 v144, v136, v137 offset0:194 offset1:227
	v_cvt_pk_fp8_f32 v145, v130, v131
	s_waitcnt vmcnt(21)
	v_mov_b32_e32 v130, v74
	s_waitcnt vmcnt(20)
	v_mov_b32_e32 v131, v78
	v_pk_mul_f32 v[130:131], v[130:131], s[64:65] op_sel_hi:[1,0]
	s_nop 0
	v_cvt_pk_fp8_f32 v145, v130, v131 op_sel:[0,0,1]
	v_mov_b32_e32 v130, v51
	v_mov_b32_e32 v131, v55
	v_pk_mul_f32 v[130:131], v[130:131], s[64:65] op_sel_hi:[1,0]
	s_nop 0
	v_cvt_pk_fp8_f32 v146, v130, v131
	v_mov_b32_e32 v130, v75
	v_mov_b32_e32 v131, v79
	v_pk_mul_f32 v[130:131], v[130:131], s[64:65] op_sel_hi:[1,0]
	s_nop 0
	v_cvt_pk_fp8_f32 v146, v130, v131 op_sel:[0,0,1]
	v_mov_b32_e32 v130, v52
	v_mov_b32_e32 v131, v56
	v_pk_mul_f32 v[130:131], v[130:131], s[64:65] op_sel_hi:[1,0]
	s_nop 0
	v_cvt_pk_fp8_f32 v132, v130, v131
	v_mov_b32_e32 v130, v76
	v_mov_b32_e32 v131, v80
	v_pk_mul_f32 v[130:131], v[130:131], s[64:65] op_sel_hi:[1,0]
	ds_write2_b32 v143, v145, v146 offset1:33
	v_cvt_pk_fp8_f32 v132, v130, v131 op_sel:[0,0,1]
	v_mov_b32_e32 v130, v53
	v_mov_b32_e32 v131, v57
	v_pk_mul_f32 v[130:131], v[130:131], s[64:65] op_sel_hi:[1,0]
	s_nop 0
	v_cvt_pk_fp8_f32 v133, v130, v131
	v_mov_b32_e32 v130, v77
	v_mov_b32_e32 v131, v81
	v_pk_mul_f32 v[130:131], v[130:131], s[64:65] op_sel_hi:[1,0]
	v_add_u32_e32 v145, 0xc400, v142
	v_cvt_pk_fp8_f32 v133, v130, v131 op_sel:[0,0,1]
	s_waitcnt vmcnt(19)
	v_mov_b32_e32 v130, v98
	s_waitcnt vmcnt(18)
	v_mov_b32_e32 v131, v102
	v_pk_mul_f32 v[130:131], v[130:131], s[64:65] op_sel_hi:[1,0]
	ds_write2_b32 v143, v132, v133 offset0:66 offset1:99
	v_cvt_pk_fp8_f32 v136, v130, v131
	s_waitcnt vmcnt(17)
	v_mov_b32_e32 v130, v106
	s_waitcnt vmcnt(16)
	v_mov_b32_e32 v131, v110
	v_pk_mul_f32 v[130:131], v[130:131], s[64:65] op_sel_hi:[1,0]
	s_nop 0
	v_cvt_pk_fp8_f32 v136, v130, v131 op_sel:[0,0,1]
	v_mov_b32_e32 v130, v99
	v_mov_b32_e32 v131, v103
	v_pk_mul_f32 v[130:131], v[130:131], s[64:65] op_sel_hi:[1,0]
	s_nop 0
	v_cvt_pk_fp8_f32 v137, v130, v131
	v_mov_b32_e32 v130, v107
	v_mov_b32_e32 v131, v111
	v_pk_mul_f32 v[130:131], v[130:131], s[64:65] op_sel_hi:[1,0]
	s_nop 0
	v_cvt_pk_fp8_f32 v137, v130, v131 op_sel:[0,0,1]
	v_mov_b32_e32 v130, v100
	v_mov_b32_e32 v131, v104
	v_pk_mul_f32 v[130:131], v[130:131], s[64:65] op_sel_hi:[1,0]
	s_nop 0
	v_cvt_pk_fp8_f32 v146, v130, v131
	v_mov_b32_e32 v130, v108
	v_mov_b32_e32 v131, v112
	v_pk_mul_f32 v[130:131], v[130:131], s[64:65] op_sel_hi:[1,0]
	s_nop 0
	v_cvt_pk_fp8_f32 v146, v130, v131 op_sel:[0,0,1]
	v_mov_b32_e32 v130, v101
	v_mov_b32_e32 v131, v105
	v_pk_mul_f32 v[130:131], v[130:131], s[64:65] op_sel_hi:[1,0]
	s_nop 0
	v_cvt_pk_fp8_f32 v147, v130, v131
	v_mov_b32_e32 v130, v109
	v_mov_b32_e32 v131, v113
	v_pk_mul_f32 v[130:131], v[130:131], s[64:65] op_sel_hi:[1,0]
	s_nop 0
	v_cvt_pk_fp8_f32 v147, v130, v131 op_sel:[0,0,1]
	ds_write2_b32 v145, v136, v137 offset0:128 offset1:161
	ds_write2_b32 v145, v146, v147 offset0:194 offset1:227
	s_waitcnt lgkmcnt(0)
	s_barrier
	ds_read2_b32 v[130:131], v141 offset1:1
	ds_read2_b32 v[132:133], v141 offset0:2 offset1:3
	v_lshl_add_u32 v136, s67, 6, v139
	s_cbranch_scc1 .LBB0_4641
	s_cmp_gt_i32 s66, 2
	s_cbranch_scc0 .LBB0_4642
	s_cmp_eq_u32 s66, 3
	s_mov_b64 s[94:95], -1
	s_cbranch_scc0 .LBB0_4639
	v_lshlrev_b32_e32 v137, 1, v136
	v_and_b32_e32 v146, 0x7f, v136
	s_movk_i32 s19, 0xff00
	v_and_or_b32 v137, v137, s19, v146
	s_mov_b64 s[94:95], 0

.Lcvw_c5:
	v_mov_b32_e32 v130, v38
	v_mov_b32_e32 v131, v34
	v_pk_mul_f32 v[130:131], v[130:131], s[64:65] op_sel_hi:[1,0]
	s_nop 0
	v_cvt_pk_fp8_f32 v132, v130, v131
	v_mov_b32_e32 v130, v46
	v_mov_b32_e32 v131, v42
	v_pk_mul_f32 v[130:131], v[130:131], s[64:65] op_sel_hi:[1,0]
	s_nop 0
	v_cvt_pk_fp8_f32 v132, v130, v131 op_sel:[0,0,1]
	v_mov_b32_e32 v130, v39
	v_mov_b32_e32 v131, v35
	v_pk_mul_f32 v[130:131], v[130:131], s[64:65] op_sel_hi:[1,0]
	s_nop 0
	v_cvt_pk_fp8_f32 v133, v130, v131
	v_mov_b32_e32 v130, v47
	v_mov_b32_e32 v131, v43
	v_pk_mul_f32 v[130:131], v[130:131], s[64:65] op_sel_hi:[1,0]
	s_nop 0
	v_cvt_pk_fp8_f32 v133, v130, v131 op_sel:[0,0,1]
	v_mov_b32_e32 v130, v40
	v_mov_b32_e32 v131, v36
	v_pk_mul_f32 v[130:131], v[130:131], s[64:65] op_sel_hi:[1,0]
	s_nop 0
	v_cvt_pk_fp8_f32 v136, v130, v131
	v_mov_b32_e32 v130, v48
	v_mov_b32_e32 v131, v44
	v_pk_mul_f32 v[130:131], v[130:131], s[64:65] op_sel_hi:[1,0]
	s_nop 0
	v_cvt_pk_fp8_f32 v136, v130, v131 op_sel:[0,0,1]
	v_mov_b32_e32 v130, v41
	v_mov_b32_e32 v131, v37
	v_pk_mul_f32 v[130:131], v[130:131], s[64:65] op_sel_hi:[1,0]
	s_nop 0
	v_cvt_pk_fp8_f32 v137, v130, v131
	v_mov_b32_e32 v130, v49
	v_mov_b32_e32 v131, v45
	v_pk_mul_f32 v[130:131], v[130:131], s[64:65] op_sel_hi:[1,0]
	s_nop 0
	v_cvt_pk_fp8_f32 v137, v130, v131 op_sel:[0,0,1]
	v_mov_b32_e32 v130, v62
	v_mov_b32_e32 v131, v58
	v_pk_mul_f32 v[130:131], v[130:131], s[64:65] op_sel_hi:[1,0]
	s_cmp_lt_i32 s71, 2
	v_cvt_pk_fp8_f32 v152, v130, v131
	v_mov_b32_e32 v130, v70
	v_mov_b32_e32 v131, v66
	v_pk_mul_f32 v[130:131], v[130:131], s[64:65] op_sel_hi:[1,0]
	s_nop 0
	v_cvt_pk_fp8_f32 v152, v130, v131 op_sel:[0,0,1]
	v_mov_b32_e32 v130, v63
	v_mov_b32_e32 v131, v59
	v_pk_mul_f32 v[130:131], v[130:131], s[64:65] op_sel_hi:[1,0]
	s_nop 0
	v_cvt_pk_fp8_f32 v153, v130, v131
	v_mov_b32_e32 v130, v71
	v_mov_b32_e32 v131, v67
	v_pk_mul_f32 v[130:131], v[130:131], s[64:65] op_sel_hi:[1,0]
	s_nop 0
	v_cvt_pk_fp8_f32 v153, v130, v131 op_sel:[0,0,1]
	v_mov_b32_e32 v130, v64
	v_mov_b32_e32 v131, v60
	v_pk_mul_f32 v[130:131], v[130:131], s[64:65] op_sel_hi:[1,0]
	s_nop 0
	v_cvt_pk_fp8_f32 v154, v130, v131
	v_mov_b32_e32 v130, v72
	v_mov_b32_e32 v131, v68
	v_pk_mul_f32 v[130:131], v[130:131], s[64:65] op_sel_hi:[1,0]
	s_nop 0
	v_cvt_pk_fp8_f32 v154, v130, v131 op_sel:[0,0,1]
	v_mov_b32_e32 v130, v65
	v_mov_b32_e32 v131, v61
	v_pk_mul_f32 v[130:131], v[130:131], s[64:65] op_sel_hi:[1,0]
	s_nop 0
	v_cvt_pk_fp8_f32 v155, v130, v131
	v_mov_b32_e32 v130, v73
	v_mov_b32_e32 v131, v69
	v_pk_mul_f32 v[130:131], v[130:131], s[64:65] op_sel_hi:[1,0]
	s_nop 0
	v_cvt_pk_fp8_f32 v155, v130, v131 op_sel:[0,0,1]
	v_mov_b32_e32 v130, v86
	v_mov_b32_e32 v131, v82
	ds_write2_b32 v142, v132, v133 offset1:33
	ds_write2_b32 v142, v136, v137 offset0:66 offset1:99
	ds_write2_b32 v144, v152, v153 offset0:128 offset1:161
	ds_write2_b32 v144, v154, v155 offset0:194 offset1:227
	v_pk_mul_f32 v[130:131], v[130:131], s[64:65] op_sel_hi:[1,0]
	s_nop 0
	v_cvt_pk_fp8_f32 v132, v130, v131
	v_mov_b32_e32 v130, v94
	v_mov_b32_e32 v131, v90
	v_pk_mul_f32 v[130:131], v[130:131], s[64:65] op_sel_hi:[1,0]
	s_nop 0
	v_cvt_pk_fp8_f32 v132, v130, v131 op_sel:[0,0,1]
	v_mov_b32_e32 v130, v87
	v_mov_b32_e32 v131, v83
	v_pk_mul_f32 v[130:131], v[130:131], s[64:65] op_sel_hi:[1,0]
	s_nop 0
	v_cvt_pk_fp8_f32 v133, v130, v131
	v_mov_b32_e32 v130, v95
	v_mov_b32_e32 v131, v91
	v_pk_mul_f32 v[130:131], v[130:131], s[64:65] op_sel_hi:[1,0]
	s_nop 0
	v_cvt_pk_fp8_f32 v133, v130, v131 op_sel:[0,0,1]
	v_mov_b32_e32 v130, v88
	v_mov_b32_e32 v131, v84
	v_pk_mul_f32 v[130:131], v[130:131], s[64:65] op_sel_hi:[1,0]
	s_nop 0
	v_cvt_pk_fp8_f32 v136, v130, v131
	v_mov_b32_e32 v130, v96
	v_mov_b32_e32 v131, v92
	v_pk_mul_f32 v[130:131], v[130:131], s[64:65] op_sel_hi:[1,0]
	s_nop 0
	v_cvt_pk_fp8_f32 v136, v130, v131 op_sel:[0,0,1]
	v_mov_b32_e32 v130, v89
	v_mov_b32_e32 v131, v85
	v_pk_mul_f32 v[130:131], v[130:131], s[64:65] op_sel_hi:[1,0]
	s_nop 0
	v_cvt_pk_fp8_f32 v137, v130, v131
	v_mov_b32_e32 v130, v97
	v_mov_b32_e32 v131, v93
	v_pk_mul_f32 v[130:131], v[130:131], s[64:65] op_sel_hi:[1,0]
	s_nop 0
	v_cvt_pk_fp8_f32 v137, v130, v131 op_sel:[0,0,1]
	v_mov_b32_e32 v130, v118
	v_mov_b32_e32 v131, v114
	v_pk_mul_f32 v[130:131], v[130:131], s[64:65] op_sel_hi:[1,0]
	s_nop 0
	v_cvt_pk_fp8_f32 v144, v130, v131
	v_mov_b32_e32 v130, v126
	v_mov_b32_e32 v131, v122
	v_pk_mul_f32 v[130:131], v[130:131], s[64:65] op_sel_hi:[1,0]
	s_nop 0
	v_cvt_pk_fp8_f32 v144, v130, v131 op_sel:[0,0,1]
	v_mov_b32_e32 v130, v119
	v_mov_b32_e32 v131, v115
	v_pk_mul_f32 v[130:131], v[130:131], s[64:65] op_sel_hi:[1,0]
	s_nop 0
	v_cvt_pk_fp8_f32 v152, v130, v131
	v_mov_b32_e32 v130, v127
	v_mov_b32_e32 v131, v123
	v_pk_mul_f32 v[130:131], v[130:131], s[64:65] op_sel_hi:[1,0]
	s_nop 0
	v_cvt_pk_fp8_f32 v152, v130, v131 op_sel:[0,0,1]
	v_mov_b32_e32 v130, v120
	v_mov_b32_e32 v131, v116
	v_pk_mul_f32 v[130:131], v[130:131], s[64:65] op_sel_hi:[1,0]
	s_nop 0
	v_cvt_pk_fp8_f32 v153, v130, v131
	v_mov_b32_e32 v130, v128
	v_mov_b32_e32 v131, v124
	v_pk_mul_f32 v[130:131], v[130:131], s[64:65] op_sel_hi:[1,0]
	s_nop 0
	v_cvt_pk_fp8_f32 v153, v130, v131 op_sel:[0,0,1]
	v_mov_b32_e32 v130, v121
	v_mov_b32_e32 v131, v117
	v_pk_mul_f32 v[130:131], v[130:131], s[64:65] op_sel_hi:[1,0]
	s_nop 0
	v_cvt_pk_fp8_f32 v154, v130, v131
	v_mov_b32_e32 v130, v129
	v_mov_b32_e32 v131, v125
	v_pk_mul_f32 v[130:131], v[130:131], s[64:65] op_sel_hi:[1,0]
	s_nop 0
	v_cvt_pk_fp8_f32 v154, v130, v131 op_sel:[0,0,1]
	ds_write2_b32 v143, v132, v133 offset1:33
	ds_write2_b32 v143, v136, v137 offset0:66 offset1:99
	ds_write2_b32 v145, v144, v152 offset0:128 offset1:161
	ds_write2_b32 v145, v153, v154 offset0:194 offset1:227
	s_waitcnt lgkmcnt(0)
	s_barrier
	ds_read2_b32 v[130:131], v141 offset1:1
	ds_read2_b32 v[132:133], v141 offset0:2 offset1:3
	v_lshl_add_u32 v136, s49, 6, v139
	s_cbranch_scc1 .LBB0_4784
	s_cmp_gt_i32 s71, 2
	s_cbranch_scc0 .LBB0_4785
	s_cmp_eq_u32 s71, 3
	s_mov_b64 s[94:95], -1
	s_cbranch_scc0 .LBB0_4782
	v_lshlrev_b32_e32 v137, 1, v136
	v_and_b32_e32 v143, 0x7f, v136
	s_movk_i32 s13, 0xff00
	v_and_or_b32 v137, v137, s13, v143
	s_mov_b64 s[94:95], 0

.Lpeel_exit_7:
	s_ashr_i32 s11, s18, 4
	s_mul_hi_i32 s13, s11, 0xc000
	s_mul_i32 s11, s11, 0xc000
	s_add_u32 s11, s37, s11
	s_addc_u32 s13, s38, s13
	s_lshl_b32 s20, s49, 8
	s_ashr_i32 s21, s20, 31
	s_lshl_b64 s[22:23], s[20:21], 2
	s_add_u32 s11, s11, s22
	v_mbcnt_lo_u32_b32 v134, -1, 0
	v_mbcnt_hi_u32_b32 v134, -1, v134
	s_addc_u32 s13, s13, s23
	v_ashrrev_i32_e32 v135, 4, v134
	s_add_u32 s22, s11, s46
	v_lshlrev_b32_e32 v132, 2, v135
	s_addc_u32 s23, s13, 0
	v_ashrrev_i32_e32 v133, 31, v132
	v_lshl_add_u64 v[132:133], v[132:133], 2, s[22:23]
	global_load_dwordx4 v[146:149], v[132:133], off
	global_load_dwordx4 v[150:153], v[132:133], off offset:64
	global_load_dwordx4 v[196:199], v[132:133], off offset:512
	global_load_dwordx4 v[200:203], v[132:133], off offset:576
	s_nop 0
	s_lshl_b32 s11, s18, 8
	s_nop 0
	s_add_i32 s22, s11, s39
	s_ashr_i32 s23, s22, 31
	s_lshl_b64 s[22:23], s[22:23], 11
	s_add_u32 s11, s35, s22
	s_addc_u32 s13, s36, s23
	s_nop 0
	v_lshlrev_b32_e32 v135, 3, v135
	s_add_u32 s11, s11, s20
	s_nop 0
	s_nop 0
	s_nop 0
	s_nop 0
	v_and_b32_e32 v128, 16, v134
	v_bfi_b32 v134, -16, v135, v134
	s_addc_u32 s13, s13, s21
	s_nop 0
	s_nop 0
	s_nop 0
	s_nop 0
	s_nop 0
	v_ashrrev_i32_e32 v135, 31, v134
	s_add_u32 s20, s11, s40
	v_lshlrev_b64 v[134:135], 11, v[134:135]
	s_addc_u32 s21, s13, 0
	v_lshl_add_u64 v[134:135], s[20:21], 0, v[134:135]
	v_lshl_add_u64 v[134:135], v[134:135], 0, v[128:129]
	v_add_co_u32_e32 v136, vcc, s34, v134
	s_mov_b32 s18, s12
	s_nop 0
	v_addc_co_u32_e32 v137, vcc, 0, v135, vcc
	s_mov_b32 s49, s10
	s_mov_b64 s[22:23], s[16:17]
	s_mov_b64 s[20:21], s[14:15]
	s_waitcnt vmcnt(0)
	v_pk_mul_f32 v[146:147], v[146:147], s[8:9] op_sel_hi:[1,0]
	v_pk_mul_f32 v[150:151], v[150:151], s[8:9] op_sel_hi:[1,0]
	v_pk_mul_f32 v[84:85], v[84:85], v[146:147]
	v_pk_mul_f32 v[80:81], v[80:81], v[150:151]
	v_cvt_pk_fp8_f32 v164, v84, v85
	v_cvt_pk_fp8_f32 v165, v80, v81
	v_pk_mul_f32 v[148:149], v[148:149], s[8:9] op_sel_hi:[1,0]
	v_pk_mul_f32 v[152:153], v[152:153], s[8:9] op_sel_hi:[1,0]
	v_pk_mul_f32 v[80:81], v[86:87], v[148:149]
	v_pk_mul_f32 v[72:73], v[72:73], v[150:151]
	v_cvt_pk_fp8_f32 v164, v80, v81 op_sel:[0,0,1]
	v_pk_mul_f32 v[80:81], v[82:83], v[152:153]
	v_pk_mul_f32 v[92:93], v[92:93], v[146:147]
	v_cvt_pk_fp8_f32 v165, v80, v81 op_sel:[0,0,1]
	v_pk_mul_f32 v[80:81], v[76:77], v[146:147]
	s_nop 0
	s_nop 0
	v_cvt_pk_fp8_f32 v77, v72, v73
	v_pk_mul_f32 v[72:73], v[78:79], v[148:149]
	v_pk_mul_f32 v[68:69], v[68:69], v[146:147]
	s_nop 0
	v_pk_mul_f32 v[124:125], v[124:125], v[146:147]
	v_pk_mul_f32 v[120:121], v[120:121], v[150:151]
	v_pk_mul_f32 v[116:117], v[116:117], v[146:147]
	v_pk_mul_f32 v[112:113], v[112:113], v[150:151]
	v_cvt_pk_fp8_f32 v162, v92, v93
	v_pk_mul_f32 v[88:89], v[88:89], v[150:151]
	v_cvt_pk_fp8_f32 v76, v80, v81
	v_cvt_pk_fp8_f32 v78, v68, v69
	v_pk_mul_f32 v[64:65], v[64:65], v[150:151]
	s_nop 0
	v_pk_mul_f32 v[108:109], v[108:109], v[146:147]
	v_pk_mul_f32 v[104:105], v[104:105], v[150:151]
	v_pk_mul_f32 v[100:101], v[100:101], v[146:147]
	v_pk_mul_f32 v[96:97], v[96:97], v[150:151]
	v_cvt_pk_fp8_f32 v154, v124, v125
	v_cvt_pk_fp8_f32 v155, v120, v121
	v_cvt_pk_fp8_f32 v156, v116, v117
	v_cvt_pk_fp8_f32 v157, v112, v113
	v_cvt_pk_fp8_f32 v163, v88, v89
	v_cvt_pk_fp8_f32 v79, v64, v65
	v_cvt_pk_fp8_f32 v158, v108, v109
	v_cvt_pk_fp8_f32 v159, v104, v105
	v_cvt_pk_fp8_f32 v160, v100, v101
	v_cvt_pk_fp8_f32 v161, v96, v97
	v_pk_mul_f32 v[88:89], v[94:95], v[148:149]
	v_pk_mul_f32 v[64:65], v[70:71], v[148:149]
	v_pk_mul_f32 v[126:127], v[126:127], v[148:149]
	v_pk_mul_f32 v[122:123], v[122:123], v[152:153]
	v_pk_mul_f32 v[118:119], v[118:119], v[148:149]
	v_pk_mul_f32 v[114:115], v[114:115], v[152:153]
	v_cvt_pk_fp8_f32 v162, v88, v89 op_sel:[0,0,1]
	v_pk_mul_f32 v[88:89], v[90:91], v[152:153]
	v_cvt_pk_fp8_f32 v76, v72, v73 op_sel:[0,0,1]
	v_pk_mul_f32 v[72:73], v[74:75], v[152:153]
	v_cvt_pk_fp8_f32 v78, v64, v65 op_sel:[0,0,1]
	v_pk_mul_f32 v[64:65], v[66:67], v[152:153]
	v_pk_mul_f32 v[110:111], v[110:111], v[148:149]
	v_pk_mul_f32 v[106:107], v[106:107], v[152:153]
	v_pk_mul_f32 v[102:103], v[102:103], v[148:149]
	v_pk_mul_f32 v[98:99], v[98:99], v[152:153]
	v_cvt_pk_fp8_f32 v154, v126, v127 op_sel:[0,0,1]
	v_cvt_pk_fp8_f32 v155, v122, v123 op_sel:[0,0,1]
	v_cvt_pk_fp8_f32 v156, v118, v119 op_sel:[0,0,1]
	v_cvt_pk_fp8_f32 v157, v114, v115 op_sel:[0,0,1]
	v_cvt_pk_fp8_f32 v163, v88, v89 op_sel:[0,0,1]
	v_cvt_pk_fp8_f32 v77, v72, v73 op_sel:[0,0,1]
	v_cvt_pk_fp8_f32 v79, v64, v65 op_sel:[0,0,1]
	v_cvt_pk_fp8_f32 v158, v110, v111 op_sel:[0,0,1]
	v_cvt_pk_fp8_f32 v159, v106, v107 op_sel:[0,0,1]
	v_cvt_pk_fp8_f32 v160, v102, v103 op_sel:[0,0,1]
	v_cvt_pk_fp8_f32 v161, v98, v99 op_sel:[0,0,1]
	v_add_co_u32_e32 v80, vcc, s47, v134
	v_permlane32_swap_b32_e32 v154, v156
	s_nop 0
	v_addc_co_u32_e32 v81, vcc, 0, v135, vcc
	v_permlane32_swap_b32_e32 v155, v157
	v_permlane32_swap_b32_e32 v162, v164
	v_permlane32_swap_b32_e32 v163, v165
	v_permlane32_swap_b32_e32 v76, v78
	v_permlane32_swap_b32_e32 v77, v79
	v_add_co_u32_e32 v82, vcc, s48, v134
	v_permlane32_swap_b32_e32 v158, v160
	v_permlane32_swap_b32_e32 v159, v161
	v_permlane16_swap_b32_e32 v154, v155
	v_permlane16_swap_b32_e32 v156, v157
	v_permlane16_swap_b32_e32 v162, v163
	v_permlane16_swap_b32_e32 v164, v165
	v_permlane16_swap_b32_e32 v76, v77
	v_permlane16_swap_b32_e32 v78, v79
	v_addc_co_u32_e32 v83, vcc, 0, v135, vcc
	v_permlane16_swap_b32_e32 v158, v159
	v_permlane16_swap_b32_e32 v160, v161
	global_store_dwordx4 v[134:135], v[154:157], off
	global_store_dwordx4 v[136:137], v[158:161], off
	global_store_dwordx4 v[80:81], v[162:165], off
	global_store_dwordx4 v[82:83], v[76:79], off
	s_nop 0
	s_nop 0
	s_nop 0
	s_nop 0
	s_and_b64 vcc, exec, s[4:5]
	v_pk_mul_f32 v[64:65], v[196:197], s[8:9] op_sel_hi:[1,0]
	v_pk_mul_f32 v[68:69], v[200:201], s[8:9] op_sel_hi:[1,0]
	v_pk_mul_f32 v[70:71], v[202:203], s[8:9] op_sel_hi:[1,0]
	v_pk_mul_f32 v[48:49], v[48:49], v[68:69]
	v_pk_mul_f32 v[66:67], v[198:199], s[8:9] op_sel_hi:[1,0]
	v_cvt_pk_fp8_f32 v75, v48, v49
	v_pk_mul_f32 v[48:49], v[50:51], v[70:71]
	v_pk_mul_f32 v[40:41], v[40:41], v[68:69]
	v_pk_mul_f32 v[36:37], v[36:37], v[64:65]
	v_cvt_pk_fp8_f32 v75, v48, v49 op_sel:[0,0,1]
	v_pk_mul_f32 v[48:49], v[44:45], v[64:65]
	s_nop 0
	v_cvt_pk_fp8_f32 v45, v40, v41
	v_pk_mul_f32 v[40:41], v[46:47], v[66:67]
	s_nop 0
	v_cvt_pk_fp8_f32 v46, v36, v37
	v_pk_mul_f32 v[32:33], v[32:33], v[68:69]
	s_nop 0
	v_cvt_pk_fp8_f32 v47, v32, v33
	v_pk_mul_f32 v[32:33], v[38:39], v[66:67]
	v_pk_mul_f32 v[24:25], v[24:25], v[68:69]
	v_cvt_pk_fp8_f32 v46, v32, v33 op_sel:[0,0,1]
	v_pk_mul_f32 v[32:33], v[34:35], v[70:71]
	v_pk_mul_f32 v[20:21], v[20:21], v[64:65]
	v_cvt_pk_fp8_f32 v47, v32, v33 op_sel:[0,0,1]
	v_pk_mul_f32 v[32:33], v[28:29], v[64:65]
	s_nop 0
	v_cvt_pk_fp8_f32 v29, v24, v25
	v_pk_mul_f32 v[24:25], v[30:31], v[66:67]
	s_nop 0
	v_cvt_pk_fp8_f32 v30, v20, v21
	v_pk_mul_f32 v[16:17], v[16:17], v[68:69]
	s_nop 0
	v_cvt_pk_fp8_f32 v31, v16, v17
	v_pk_mul_f32 v[16:17], v[22:23], v[66:67]
	s_nop 0
	v_cvt_pk_fp8_f32 v30, v16, v17 op_sel:[0,0,1]
	v_pk_mul_f32 v[16:17], v[18:19], v[70:71]
	v_pk_mul_f32 v[8:9], v[8:9], v[68:69]
	v_cvt_pk_fp8_f32 v31, v16, v17 op_sel:[0,0,1]
	v_pk_mul_f32 v[16:17], v[12:13], v[64:65]
	s_nop 0
	v_pk_mul_f32 v[60:61], v[60:61], v[64:65]
	v_pk_mul_f32 v[56:57], v[56:57], v[68:69]
	v_pk_mul_f32 v[52:53], v[52:53], v[64:65]
	s_nop 0
	v_cvt_pk_fp8_f32 v28, v32, v33
	s_nop 0
	v_cvt_pk_fp8_f32 v13, v8, v9
	v_pk_mul_f32 v[8:9], v[14:15], v[66:67]
	v_pk_mul_f32 v[4:5], v[4:5], v[64:65]
	s_nop 0
	v_cvt_pk_fp8_f32 v72, v60, v61
	v_cvt_pk_fp8_f32 v73, v56, v57
	v_cvt_pk_fp8_f32 v74, v52, v53
	v_cvt_pk_fp8_f32 v44, v48, v49
	v_cvt_pk_fp8_f32 v12, v16, v17
	v_cvt_pk_fp8_f32 v14, v4, v5
	v_pk_mul_f32 v[0:1], v[0:1], v[68:69]
	s_nop 0
	v_cvt_pk_fp8_f32 v15, v0, v1
	v_pk_mul_f32 v[62:63], v[62:63], v[66:67]
	v_pk_mul_f32 v[58:59], v[58:59], v[70:71]
	v_pk_mul_f32 v[54:55], v[54:55], v[66:67]
	v_cvt_pk_fp8_f32 v28, v24, v25 op_sel:[0,0,1]
	v_pk_mul_f32 v[24:25], v[26:27], v[70:71]
	v_pk_mul_f32 v[0:1], v[6:7], v[66:67]
	v_cvt_pk_fp8_f32 v72, v62, v63 op_sel:[0,0,1]
	v_cvt_pk_fp8_f32 v73, v58, v59 op_sel:[0,0,1]
	v_cvt_pk_fp8_f32 v74, v54, v55 op_sel:[0,0,1]
	v_cvt_pk_fp8_f32 v44, v40, v41 op_sel:[0,0,1]
	v_pk_mul_f32 v[40:41], v[42:43], v[70:71]
	v_cvt_pk_fp8_f32 v29, v24, v25 op_sel:[0,0,1]
	v_cvt_pk_fp8_f32 v12, v8, v9 op_sel:[0,0,1]
	v_pk_mul_f32 v[8:9], v[10:11], v[70:71]
	v_cvt_pk_fp8_f32 v14, v0, v1 op_sel:[0,0,1]
	v_pk_mul_f32 v[0:1], v[2:3], v[70:71]
	v_cvt_pk_fp8_f32 v45, v40, v41 op_sel:[0,0,1]
	v_cvt_pk_fp8_f32 v13, v8, v9 op_sel:[0,0,1]
	v_cvt_pk_fp8_f32 v15, v0, v1 op_sel:[0,0,1]
	v_permlane32_swap_b32_e32 v72, v74
	v_permlane32_swap_b32_e32 v73, v75
	v_permlane32_swap_b32_e32 v28, v30
	v_permlane32_swap_b32_e32 v29, v31
	v_permlane16_swap_b32_e32 v72, v73
	v_permlane16_swap_b32_e32 v74, v75
	v_permlane32_swap_b32_e32 v44, v46
	v_permlane32_swap_b32_e32 v45, v47
	v_permlane16_swap_b32_e32 v28, v29
	v_permlane16_swap_b32_e32 v30, v31
	v_permlane32_swap_b32_e32 v12, v14
	v_permlane32_swap_b32_e32 v13, v15
	v_permlane16_swap_b32_e32 v44, v45
	v_permlane16_swap_b32_e32 v46, v47
	global_store_dwordx4 v[134:135], v[72:75], off offset:128
	global_store_dwordx4 v[136:137], v[44:47], off offset:128
	v_permlane16_swap_b32_e32 v12, v13
	v_permlane16_swap_b32_e32 v14, v15
	global_store_dwordx4 v[80:81], v[28:31], off offset:128
	global_store_dwordx4 v[82:83], v[12:15], off offset:128
	s_cbranch_vccz .LBB0_4925
	s_waitcnt vmcnt(0)
	v_readlane_b32 s0, v252, 2
	s_cmpk_gt_u32 s0, 0xff
	s_cbranch_scc1 .LBB0_4936
	s_barrier

.LBB0_5009:
	v_cvt_pk_f32_fp8_e32 v[62:63], v38
	v_cvt_pk_f32_fp8_sdwa v[38:39], v38 src0_sel:WORD_1
	v_lshlrev_b32_e32 v60, 16, v42
	v_and_b32_e32 v61, 0xffff0000, v42
	v_lshlrev_b32_e32 v42, 16, v43
	v_and_b32_e32 v43, 0xffff0000, v43
	v_pk_add_f32 v[74:75], v[38:39], v[42:43]
	v_cvt_pk_f32_fp8_e32 v[42:43], v56
	v_lshlrev_b32_e32 v38, 16, v34
	v_and_b32_e32 v39, 0xffff0000, v34
	v_cvt_pk_f32_fp8_sdwa v[56:57], v56 src0_sel:WORD_1
	v_pk_add_f32 v[72:73], v[42:43], v[38:39]
	v_cvt_pk_f32_fp8_e32 v[38:39], v55
	v_lshlrev_b32_e32 v34, 16, v35
	v_and_b32_e32 v35, 0xffff0000, v35
	v_pk_add_f32 v[70:71], v[56:57], v[34:35]
	v_lshlrev_b32_e32 v34, 16, v10
	v_and_b32_e32 v35, 0xffff0000, v10
	v_cvt_pk_f32_fp8_sdwa v[42:43], v55 src0_sel:WORD_1
	v_pk_add_f32 v[68:69], v[38:39], v[34:35]
	v_cvt_pk_f32_fp8_e32 v[38:39], v54
	v_lshlrev_b32_e32 v10, 16, v11
	v_and_b32_e32 v11, 0xffff0000, v11
	v_pk_add_f32 v[66:67], v[42:43], v[10:11]
	v_lshlrev_b32_e32 v10, 16, v8
	v_and_b32_e32 v11, 0xffff0000, v8
	v_cvt_pk_f32_fp8_sdwa v[34:35], v54 src0_sel:WORD_1
	v_pk_add_f32 v[64:65], v[38:39], v[10:11]
	v_cvt_pk_f32_fp8_e32 v[10:11], v51
	v_lshlrev_b32_e32 v8, 16, v9
	v_and_b32_e32 v9, 0xffff0000, v9
	v_pk_add_f32 v[34:35], v[34:35], v[8:9]
	v_lshlrev_b32_e32 v8, 16, v6
	v_and_b32_e32 v9, 0xffff0000, v6
	v_cvt_pk_f32_fp8_sdwa v[38:39], v51 src0_sel:WORD_1
	v_pk_add_f32 v[76:77], v[62:63], v[60:61]
	v_pk_add_f32 v[62:63], v[10:11], v[8:9]
	v_cvt_pk_f32_fp8_e32 v[8:9], v47
	v_lshlrev_b32_e32 v6, 16, v7
	v_and_b32_e32 v7, 0xffff0000, v7
	v_pk_add_f32 v[38:39], v[38:39], v[6:7]
	v_lshlrev_b32_e32 v6, 16, v4
	v_and_b32_e32 v7, 0xffff0000, v4
	v_cvt_pk_f32_fp8_sdwa v[10:11], v47 src0_sel:WORD_1
	v_pk_add_f32 v[60:61], v[8:9], v[6:7]
	v_cvt_pk_f32_fp8_e32 v[6:7], v46
	v_lshlrev_b32_e32 v4, 16, v5
	v_and_b32_e32 v5, 0xffff0000, v5
	v_pk_add_f32 v[42:43], v[10:11], v[4:5]
	v_lshlrev_b32_e32 v4, 16, v2
	v_and_b32_e32 v5, 0xffff0000, v2
	v_cvt_pk_f32_fp8_sdwa v[8:9], v46 src0_sel:WORD_1
	v_pk_add_f32 v[56:57], v[6:7], v[4:5]
	v_cvt_pk_f32_fp8_sdwa v[6:7], v50 src0_sel:WORD_1
	v_lshlrev_b32_e32 v2, 16, v3
	v_and_b32_e32 v3, 0xffff0000, v3
	v_pk_add_f32 v[46:47], v[8:9], v[2:3]
	v_lshlrev_b32_e32 v2, 16, v0
	v_and_b32_e32 v3, 0xffff0000, v0
	v_lshlrev_b32_e32 v0, 16, v1
	v_and_b32_e32 v1, 0xffff0000, v1
	v_cvt_pk_f32_fp8_e32 v[4:5], v50
	v_pk_add_f32 v[50:51], v[6:7], v[0:1]
	v_mul_f32_e32 v0, v77, v77
	v_mul_f32_e32 v1, v73, v73
	v_fmac_f32_e32 v0, v76, v76
	v_fmac_f32_e32 v1, v72, v72
	v_fmac_f32_e32 v0, v74, v74
	v_fmac_f32_e32 v1, v70, v70
	v_pk_add_f32 v[54:55], v[4:5], v[2:3]
	v_fmac_f32_e32 v0, v75, v75
	v_fmac_f32_e32 v1, v71, v71
	v_mov_b32_e32 v2, v69
	v_mov_b32_e32 v3, v65
	v_add_f32_e32 v8, v0, v1
	v_mov_b32_e32 v0, v68
	v_mov_b32_e32 v1, v64
	v_pk_mul_f32 v[2:3], v[2:3], v[2:3]
	v_mov_b32_e32 v4, v66
	v_mov_b32_e32 v5, v34
	v_pk_fma_f32 v[0:1], v[0:1], v[0:1], v[2:3]
	v_mov_b32_e32 v6, v67
	v_mov_b32_e32 v7, v35
	v_pk_fma_f32 v[0:1], v[4:5], v[4:5], v[0:1]
	v_mov_b32_e32 v2, v63
	v_pk_fma_f32 v[0:1], v[6:7], v[6:7], v[0:1]
	v_mov_b32_e32 v3, v61
	v_add_f32_e32 v0, v8, v0
	v_add_f32_e32 v8, v0, v1
	v_mov_b32_e32 v0, v62
	v_mov_b32_e32 v1, v60
	v_pk_mul_f32 v[2:3], v[2:3], v[2:3]
	v_mov_b32_e32 v4, v38
	v_mov_b32_e32 v5, v42
	v_pk_fma_f32 v[0:1], v[0:1], v[0:1], v[2:3]
	v_mov_b32_e32 v6, v39
	v_mov_b32_e32 v7, v43
	v_pk_fma_f32 v[0:1], v[4:5], v[4:5], v[0:1]
	v_mov_b32_e32 v2, v57
	v_pk_fma_f32 v[0:1], v[6:7], v[6:7], v[0:1]
	v_mov_b32_e32 v3, v55
	v_add_f32_e32 v0, v8, v0
	v_add_f32_e32 v8, v0, v1
	v_mov_b32_e32 v0, v56
	v_mov_b32_e32 v1, v54
	v_pk_mul_f32 v[2:3], v[2:3], v[2:3]
	v_mov_b32_e32 v4, v46
	v_mov_b32_e32 v5, v50
	v_pk_fma_f32 v[0:1], v[0:1], v[0:1], v[2:3]
	v_mov_b32_e32 v6, v47
	v_mov_b32_e32 v7, v51
	v_pk_fma_f32 v[0:1], v[4:5], v[4:5], v[0:1]
	s_ashr_i32 s0, s6, 12
	v_pk_fma_f32 v[0:1], v[6:7], v[6:7], v[0:1]
	s_add_i32 s0, s0, 4
	v_add_f32_e32 v0, v8, v0
	v_add_f32_e32 v0, v0, v1
	s_nop 1
	v_add_f32_dpp v0, v0, v0 quad_perm:[1,0,3,2] row_mask:0xf bank_mask:0xf bound_ctrl:1
	s_nop 1
	v_add_f32_dpp v0, v0, v0 quad_perm:[2,3,0,1] row_mask:0xf bank_mask:0xf bound_ctrl:1
	s_nop 1
	v_add_f32_dpp v0, v0, v0 row_half_mirror row_mask:0xf bank_mask:0xf bound_ctrl:1
	s_nop 1
	v_add_f32_dpp v0, v0, v0 row_mirror row_mask:0xf bank_mask:0xf bound_ctrl:1
	s_nop 0
	v_readlane_b32 s1, v0, 16
	v_readlane_b32 s6, v0, 48
	v_readlane_b32 s4, v0, 0
	v_readlane_b32 s5, v0, 32
	v_mov_b32_e32 v0, s1
	v_mov_b32_e32 v1, s6
	v_pk_add_f32 v[0:1], s[4:5], v[0:1]
	s_mov_b32 s1, 0xf800000
	v_add_f32_e32 v0, v0, v1
	v_fmamk_f32 v0, v0, 0x3a000000, v81
	v_cmp_gt_f32_e32 vcc, s1, v0
	v_mul_f32_e32 v1, 0x4f800000, v0
	s_mul_hi_i32 s1, s0, 0xc000
	v_cndmask_b32_e32 v0, v0, v1, vcc
	v_sqrt_f32_e32 v1, v0
	s_mul_i32 s0, s0, 0xc000
	s_add_u32 s0, s2, s0
	s_addc_u32 s1, s3, s1
	v_add_u32_e32 v2, -1, v1
	v_fma_f32 v3, -v2, v1, v0
	v_cmp_ge_f32_e64 s[6:7], 0, v3
	v_add_u32_e32 v3, 1, v1
	s_nop 0
	v_cndmask_b32_e64 v2, v1, v2, s[6:7]
	v_fma_f32 v1, -v3, v1, v0
	v_cmp_lt_f32_e64 s[6:7], 0, v1
	s_nop 1
	v_cndmask_b32_e64 v1, v2, v3, s[6:7]
	v_mul_f32_e32 v2, 0x37800000, v1
	v_cndmask_b32_e32 v1, v1, v2, vcc
	v_cmp_class_f32_e32 vcc, v0, v82
	s_add_u32 s6, s0, 0xe000
	s_addc_u32 s7, s1, 0
	v_cndmask_b32_e32 v0, v1, v0, vcc
	v_div_scale_f32 v1, s[4:5], v0, v0, 1.0
	v_rcp_f32_e32 v2, v1
	s_add_u32 s8, s0, 0x10000
	s_addc_u32 s9, s1, 0
	v_fma_f32 v3, -v1, v2, 1.0
	v_fmac_f32_e32 v2, v3, v2
	v_div_scale_f32 v3, vcc, 1.0, v0, 1.0
	v_mul_f32_e32 v4, v3, v2
	v_fma_f32 v5, -v1, v4, v3
	v_fmac_f32_e32 v4, v5, v2
	v_fma_f32 v1, -v1, v4, v3
	v_div_fmas_f32 v1, v1, v2, v4
	v_lshlrev_b64 v[4:5], 2, v[14:15]
	v_div_fixup_f32 v58, v1, v0, 1.0
	v_lshl_add_u64 v[0:1], s[20:21], 0, v[4:5]
	global_load_dwordx4 v[8:11], v[0:1], off
	v_lshl_add_u64 v[0:1], s[8:9], 0, v[4:5]
	global_load_dwordx4 v[0:3], v[0:1], off
	v_lshl_add_u64 v[4:5], s[6:7], 0, v[4:5]
	global_load_dwordx4 v[4:7], v[4:5], off
	v_pk_mul_f32 v[74:75], v[74:75], v[58:59] op_sel_hi:[1,0]
	v_pk_mul_f32 v[76:77], v[76:77], v[58:59] op_sel_hi:[1,0]
	v_pk_mul_f32 v[66:67], v[66:67], v[58:59] op_sel_hi:[1,0]
	v_pk_mul_f32 v[68:69], v[68:69], v[58:59] op_sel_hi:[1,0]
	v_cmp_eq_u32_e32 vcc, 0, v80
	s_waitcnt vmcnt(2)
	v_pk_mul_f32 v[8:9], v[8:9], v[76:77]
	v_pk_mul_f32 v[10:11], v[10:11], v[74:75]
	s_waitcnt vmcnt(1)
	v_pk_add_f32 v[2:3], v[2:3], 1.0 op_sel_hi:[1,0]
	v_pk_add_f32 v[0:1], v[0:1], 1.0 op_sel_hi:[1,0]
	s_waitcnt vmcnt(0)
	v_pk_fma_f32 v[6:7], v[2:3], v[10:11], v[6:7]
	v_pk_fma_f32 v[10:11], v[0:1], v[8:9], v[4:5]
	s_nop 0
	v_cvt_pk_fp8_f32 v2, v10, v11
	v_lshl_add_u64 v[0:1], s[26:27], 0, v[14:15]
	v_lshlrev_b64 v[4:5], 2, v[12:13]
	v_lshl_add_u64 v[8:9], s[8:9], 0, v[4:5]
	v_cvt_pk_fp8_f32 v2, v6, v7 op_sel:[0,0,1]
	global_store_dword v[0:1], v2, off
	v_lshl_add_u64 v[0:1], s[20:21], 0, v[4:5]
	global_load_dwordx4 v[0:3], v[0:1], off
	v_lshl_add_u64 v[4:5], s[6:7], 0, v[4:5]
	global_load_dwordx4 v[74:77], v[8:9], off
	global_load_dwordx4 v[94:97], v[4:5], off
	v_pk_mul_f32 v[4:5], v[70:71], v[58:59] op_sel_hi:[1,0]
	v_pk_mul_f32 v[8:9], v[72:73], v[58:59] op_sel_hi:[1,0]
	v_lshlrev_b64 v[70:71], 2, v[32:33]
	s_waitcnt vmcnt(2)
	v_pk_mul_f32 v[0:1], v[0:1], v[8:9]
	v_pk_mul_f32 v[2:3], v[2:3], v[4:5]
	s_waitcnt vmcnt(1)
	v_pk_add_f32 v[4:5], v[76:77], 1.0 op_sel_hi:[1,0]
	v_pk_add_f32 v[8:9], v[74:75], 1.0 op_sel_hi:[1,0]
	s_waitcnt vmcnt(0)
	v_pk_fma_f32 v[4:5], v[4:5], v[2:3], v[96:97]
	v_pk_fma_f32 v[8:9], v[8:9], v[0:1], v[94:95]
	s_nop 0
	v_cvt_pk_fp8_f32 v2, v8, v9
	v_lshl_add_u64 v[0:1], s[26:27], 0, v[12:13]
	v_lshl_add_u64 v[12:13], s[8:9], 0, v[70:71]
	v_cvt_pk_fp8_f32 v2, v4, v5 op_sel:[0,0,1]
	global_store_dword v[0:1], v2, off
	v_lshl_add_u64 v[0:1], s[20:21], 0, v[70:71]
	global_load_dwordx4 v[0:3], v[0:1], off
	v_lshl_add_u64 v[70:71], s[6:7], 0, v[70:71]
	global_load_dwordx4 v[12:15], v[12:13], off
	s_waitcnt vmcnt(1)
	v_pk_mul_f32 v[0:1], v[68:69], v[0:1]
	global_load_dwordx4 v[70:73], v[70:71], off
	v_pk_mul_f32 v[2:3], v[66:67], v[2:3]
	s_waitcnt vmcnt(1)
	v_pk_add_f32 v[14:15], v[14:15], 1.0 op_sel_hi:[1,0]
	v_pk_add_f32 v[66:67], v[12:13], 1.0 op_sel_hi:[1,0]
	s_waitcnt vmcnt(0)
	v_pk_fma_f32 v[12:13], v[2:3], v[14:15], v[72:73]
	v_pk_fma_f32 v[14:15], v[0:1], v[66:67], v[70:71]
	s_nop 0
	v_cvt_pk_fp8_f32 v2, v14, v15
	v_lshl_add_u64 v[0:1], s[26:27], 0, v[32:33]
	v_lshlrev_b64 v[32:33], 2, v[36:37]
	v_lshl_add_u64 v[66:67], s[8:9], 0, v[32:33]
	v_cvt_pk_fp8_f32 v2, v12, v13 op_sel:[0,0,1]
	global_store_dword v[0:1], v2, off
	v_lshl_add_u64 v[0:1], s[20:21], 0, v[32:33]
	global_load_dwordx4 v[0:3], v[0:1], off
	v_lshl_add_u64 v[32:33], s[6:7], 0, v[32:33]
	global_load_dwordx4 v[66:69], v[66:67], off
	s_nop 0
	global_load_dwordx4 v[70:73], v[32:33], off
	v_pk_mul_f32 v[32:33], v[34:35], v[58:59] op_sel_hi:[1,0]
	v_pk_mul_f32 v[34:35], v[64:65], v[58:59] op_sel_hi:[1,0]
	s_waitcnt vmcnt(2)
	v_pk_mul_f32 v[2:3], v[32:33], v[2:3]
	v_pk_mul_f32 v[0:1], v[34:35], v[0:1]
	s_waitcnt vmcnt(1)
	v_pk_add_f32 v[32:33], v[68:69], 1.0 op_sel_hi:[1,0]
	v_pk_add_f32 v[34:35], v[66:67], 1.0 op_sel_hi:[1,0]
	s_waitcnt vmcnt(0)
	v_pk_fma_f32 v[32:33], v[2:3], v[32:33], v[72:73]
	v_pk_fma_f32 v[34:35], v[0:1], v[34:35], v[70:71]
	s_nop 0
	v_cvt_pk_fp8_f32 v2, v34, v35
	v_lshl_add_u64 v[0:1], s[26:27], 0, v[36:37]
	v_lshlrev_b64 v[36:37], 2, v[40:41]
	v_lshl_add_u64 v[64:65], s[8:9], 0, v[36:37]
	v_cvt_pk_fp8_f32 v2, v32, v33 op_sel:[0,0,1]
	global_store_dword v[0:1], v2, off
	v_lshl_add_u64 v[0:1], s[20:21], 0, v[36:37]
	global_load_dwordx4 v[0:3], v[0:1], off
	v_lshl_add_u64 v[36:37], s[6:7], 0, v[36:37]
	global_load_dwordx4 v[64:67], v[64:65], off
	s_nop 0
	global_load_dwordx4 v[68:71], v[36:37], off
	v_pk_mul_f32 v[36:37], v[38:39], v[58:59] op_sel_hi:[1,0]
	v_pk_mul_f32 v[38:39], v[62:63], v[58:59] op_sel_hi:[1,0]
	s_waitcnt vmcnt(2)
	v_pk_mul_f32 v[2:3], v[36:37], v[2:3]
	v_pk_mul_f32 v[0:1], v[38:39], v[0:1]
	s_waitcnt vmcnt(1)
	v_pk_add_f32 v[36:37], v[66:67], 1.0 op_sel_hi:[1,0]
	v_pk_add_f32 v[38:39], v[64:65], 1.0 op_sel_hi:[1,0]
	s_waitcnt vmcnt(0)
	v_pk_fma_f32 v[36:37], v[2:3], v[36:37], v[70:71]
	v_pk_fma_f32 v[38:39], v[0:1], v[38:39], v[68:69]
	s_nop 0
	v_cvt_pk_fp8_f32 v2, v38, v39
	v_lshl_add_u64 v[0:1], s[26:27], 0, v[40:41]
	v_lshlrev_b64 v[40:41], 2, v[44:45]
	v_lshl_add_u64 v[62:63], s[8:9], 0, v[40:41]
	v_cvt_pk_fp8_f32 v2, v36, v37 op_sel:[0,0,1]
	global_store_dword v[0:1], v2, off
	v_lshl_add_u64 v[0:1], s[20:21], 0, v[40:41]
	global_load_dwordx4 v[0:3], v[0:1], off
	v_lshl_add_u64 v[40:41], s[6:7], 0, v[40:41]
	global_load_dwordx4 v[62:65], v[62:63], off
	s_nop 0
	global_load_dwordx4 v[66:69], v[40:41], off
	v_pk_mul_f32 v[40:41], v[42:43], v[58:59] op_sel_hi:[1,0]
	v_pk_mul_f32 v[42:43], v[60:61], v[58:59] op_sel_hi:[1,0]
	s_waitcnt vmcnt(2)
	v_pk_mul_f32 v[2:3], v[40:41], v[2:3]
	v_pk_mul_f32 v[0:1], v[42:43], v[0:1]
	s_waitcnt vmcnt(1)
	v_pk_add_f32 v[40:41], v[64:65], 1.0 op_sel_hi:[1,0]
	v_pk_add_f32 v[42:43], v[62:63], 1.0 op_sel_hi:[1,0]
	s_waitcnt vmcnt(0)
	v_pk_fma_f32 v[40:41], v[2:3], v[40:41], v[68:69]
	v_pk_fma_f32 v[42:43], v[0:1], v[42:43], v[66:67]
	s_nop 0
	v_cvt_pk_fp8_f32 v2, v42, v43
	v_lshl_add_u64 v[0:1], s[26:27], 0, v[44:45]
	v_lshlrev_b64 v[44:45], 2, v[48:49]
	v_lshl_add_u64 v[60:61], s[8:9], 0, v[44:45]
	v_cvt_pk_fp8_f32 v2, v40, v41 op_sel:[0,0,1]
	global_store_dword v[0:1], v2, off
	v_lshl_add_u64 v[0:1], s[20:21], 0, v[44:45]
	global_load_dwordx4 v[0:3], v[0:1], off
	v_lshl_add_u64 v[44:45], s[6:7], 0, v[44:45]
	global_load_dwordx4 v[60:63], v[60:61], off
	s_nop 0
	global_load_dwordx4 v[64:67], v[44:45], off
	v_pk_mul_f32 v[44:45], v[46:47], v[58:59] op_sel_hi:[1,0]
	v_pk_mul_f32 v[46:47], v[56:57], v[58:59] op_sel_hi:[1,0]
	s_waitcnt vmcnt(2)
	v_pk_mul_f32 v[2:3], v[44:45], v[2:3]
	v_pk_mul_f32 v[0:1], v[46:47], v[0:1]
	s_waitcnt vmcnt(1)
	v_pk_add_f32 v[44:45], v[62:63], 1.0 op_sel_hi:[1,0]
	v_pk_add_f32 v[46:47], v[60:61], 1.0 op_sel_hi:[1,0]
	s_waitcnt vmcnt(0)
	v_pk_fma_f32 v[44:45], v[2:3], v[44:45], v[66:67]
	v_pk_fma_f32 v[46:47], v[0:1], v[46:47], v[64:65]
	s_nop 0
	v_cvt_pk_fp8_f32 v2, v46, v47
	v_lshl_add_u64 v[0:1], s[26:27], 0, v[48:49]
	v_lshlrev_b64 v[48:49], 2, v[52:53]
	v_lshl_add_u64 v[56:57], s[8:9], 0, v[48:49]
	v_cvt_pk_fp8_f32 v2, v44, v45 op_sel:[0,0,1]
	global_store_dword v[0:1], v2, off
	v_lshl_add_u64 v[0:1], s[20:21], 0, v[48:49]
	global_load_dwordx4 v[0:3], v[0:1], off
	v_lshl_add_u64 v[48:49], s[6:7], 0, v[48:49]
	global_load_dwordx4 v[60:63], v[56:57], off
	global_load_dwordx4 v[64:67], v[48:49], off
	v_pk_mul_f32 v[48:49], v[50:51], v[58:59] op_sel_hi:[1,0]
	v_pk_mul_f32 v[50:51], v[54:55], v[58:59] op_sel_hi:[1,0]
	s_waitcnt vmcnt(2)
	v_pk_mul_f32 v[2:3], v[48:49], v[2:3]
	v_pk_mul_f32 v[0:1], v[50:51], v[0:1]
	s_waitcnt vmcnt(1)
	v_pk_add_f32 v[48:49], v[62:63], 1.0 op_sel_hi:[1,0]
	v_pk_add_f32 v[50:51], v[60:61], 1.0 op_sel_hi:[1,0]
	s_waitcnt vmcnt(0)
	v_pk_fma_f32 v[48:49], v[2:3], v[48:49], v[66:67]
	v_pk_fma_f32 v[50:51], v[0:1], v[50:51], v[64:65]
	s_nop 0
	v_cvt_pk_fp8_f32 v2, v50, v51
	v_lshl_add_u64 v[0:1], s[26:27], 0, v[52:53]
	v_lshlrev_b32_e32 v52, 4, v80
	v_cvt_pk_fp8_f32 v2, v48, v49 op_sel:[0,0,1]
	global_store_dword v[0:1], v2, off
	v_mov_b32_e32 v0, v52
	s_nop 0
	v_add_u32_e32 v53, 0, v0
	ds_read_b128 v[0:3], v53
	s_waitcnt lgkmcnt(0)
	v_mul_f32_e32 v1, v11, v1
	v_fmac_f32_e32 v1, v10, v0
	v_fmac_f32_e32 v1, v6, v2
	v_fmac_f32_e32 v1, v7, v3
	v_add_f32_e32 v54, 0, v1
	ds_read_b128 v[0:3], v53 offset:1024
	s_waitcnt lgkmcnt(0)
	v_mul_f32_e32 v1, v9, v1
	v_fmac_f32_e32 v1, v8, v0
	v_fmac_f32_e32 v1, v4, v2
	v_fmac_f32_e32 v1, v5, v3
	v_add_f32_e32 v54, v54, v1
	ds_read_b128 v[0:3], v53 offset:2048
	s_waitcnt lgkmcnt(0)
	v_mul_f32_e32 v1, v15, v1
	v_fmac_f32_e32 v1, v14, v0
	v_fmac_f32_e32 v1, v12, v2
	v_fmac_f32_e32 v1, v13, v3
	v_add_f32_e32 v54, v54, v1
	ds_read_b128 v[0:3], v53 offset:3072
	s_waitcnt lgkmcnt(0)
	v_mul_f32_e32 v1, v35, v1
	v_fmac_f32_e32 v1, v34, v0
	v_fmac_f32_e32 v1, v32, v2
	v_fmac_f32_e32 v1, v33, v3
	v_add_f32_e32 v54, v54, v1
	ds_read_b128 v[0:3], v53 offset:4096
	s_waitcnt lgkmcnt(0)
	v_mul_f32_e32 v1, v39, v1
	v_fmac_f32_e32 v1, v38, v0
	v_fmac_f32_e32 v1, v36, v2
	v_fmac_f32_e32 v1, v37, v3
	v_add_f32_e32 v54, v54, v1
	ds_read_b128 v[0:3], v53 offset:5120
	s_waitcnt lgkmcnt(0)
	v_mul_f32_e32 v1, v43, v1
	v_fmac_f32_e32 v1, v42, v0
	v_fmac_f32_e32 v1, v40, v2
	v_fmac_f32_e32 v1, v41, v3
	v_add_f32_e32 v54, v54, v1
	ds_read_b128 v[0:3], v53 offset:6144
	s_waitcnt lgkmcnt(0)
	v_mul_f32_e32 v1, v47, v1
	v_fmac_f32_e32 v1, v46, v0
	v_fmac_f32_e32 v1, v44, v2
	v_fmac_f32_e32 v1, v45, v3
	v_add_f32_e32 v54, v54, v1
	ds_read_b128 v[0:3], v53 offset:7168
	s_waitcnt lgkmcnt(0)
	v_mul_f32_e32 v1, v51, v1
	v_fmac_f32_e32 v1, v50, v0
	v_fmac_f32_e32 v1, v48, v2
	v_fmac_f32_e32 v1, v49, v3
	v_add_f32_e32 v0, v54, v1
	s_nop 1
	v_add_f32_dpp v0, v0, v0 quad_perm:[1,0,3,2] row_mask:0xf bank_mask:0xf bound_ctrl:1
	s_nop 1
	v_add_f32_dpp v0, v0, v0 quad_perm:[2,3,0,1] row_mask:0xf bank_mask:0xf bound_ctrl:1
	s_nop 1
	v_add_f32_dpp v0, v0, v0 row_half_mirror row_mask:0xf bank_mask:0xf bound_ctrl:1
	s_nop 1
	v_add_f32_dpp v0, v0, v0 row_mirror row_mask:0xf bank_mask:0xf bound_ctrl:1
	s_nop 0
	v_readlane_b32 s6, v0, 0
	v_readlane_b32 s10, v0, 16
	v_readlane_b32 s7, v0, 32
	v_readlane_b32 s11, v0, 48
	v_add_u32_e32 v0, 0x2000, v52
	s_nop 0
	v_add_u32_e32 v53, 0, v0
	ds_read_b128 v[0:3], v53
	s_waitcnt lgkmcnt(0)
	v_mul_f32_e32 v1, v11, v1
	v_fmac_f32_e32 v1, v10, v0
	v_fmac_f32_e32 v1, v6, v2
	v_fmac_f32_e32 v1, v7, v3
	v_add_f32_e32 v54, 0, v1
	ds_read_b128 v[0:3], v53 offset:1024
	s_waitcnt lgkmcnt(0)
	v_mul_f32_e32 v1, v9, v1
	v_fmac_f32_e32 v1, v8, v0
	v_fmac_f32_e32 v1, v4, v2
	v_fmac_f32_e32 v1, v5, v3
	v_add_f32_e32 v54, v54, v1
	ds_read_b128 v[0:3], v53 offset:2048
	s_waitcnt lgkmcnt(0)
	v_mul_f32_e32 v1, v15, v1
	v_fmac_f32_e32 v1, v14, v0
	v_fmac_f32_e32 v1, v12, v2
	v_fmac_f32_e32 v1, v13, v3
	v_add_f32_e32 v54, v54, v1
	ds_read_b128 v[0:3], v53 offset:3072
	s_waitcnt lgkmcnt(0)
	v_mul_f32_e32 v1, v35, v1
	v_fmac_f32_e32 v1, v34, v0
	v_fmac_f32_e32 v1, v32, v2
	v_fmac_f32_e32 v1, v33, v3
	v_add_f32_e32 v54, v54, v1
	ds_read_b128 v[0:3], v53 offset:4096
	s_waitcnt lgkmcnt(0)
	v_mul_f32_e32 v1, v39, v1
	v_fmac_f32_e32 v1, v38, v0
	v_fmac_f32_e32 v1, v36, v2
	v_fmac_f32_e32 v1, v37, v3
	v_add_f32_e32 v54, v54, v1
	ds_read_b128 v[0:3], v53 offset:5120
	s_waitcnt lgkmcnt(0)
	v_mul_f32_e32 v1, v43, v1
	v_fmac_f32_e32 v1, v42, v0
	v_fmac_f32_e32 v1, v40, v2
	v_fmac_f32_e32 v1, v41, v3
	v_add_f32_e32 v54, v54, v1
	ds_read_b128 v[0:3], v53 offset:6144
	s_waitcnt lgkmcnt(0)
	v_mul_f32_e32 v1, v47, v1
	v_fmac_f32_e32 v1, v46, v0
	v_fmac_f32_e32 v1, v44, v2
	v_fmac_f32_e32 v1, v45, v3
	v_add_f32_e32 v54, v54, v1
	ds_read_b128 v[0:3], v53 offset:7168
	s_waitcnt lgkmcnt(0)
	v_mul_f32_e32 v1, v51, v1
	v_fmac_f32_e32 v1, v50, v0
	v_fmac_f32_e32 v1, v48, v2
	v_fmac_f32_e32 v1, v49, v3
	v_add_f32_e32 v0, v54, v1
	s_nop 1
	v_add_f32_dpp v0, v0, v0 quad_perm:[1,0,3,2] row_mask:0xf bank_mask:0xf bound_ctrl:1
	s_nop 1
	v_add_f32_dpp v0, v0, v0 quad_perm:[2,3,0,1] row_mask:0xf bank_mask:0xf bound_ctrl:1
	s_nop 1
	v_add_f32_dpp v0, v0, v0 row_half_mirror row_mask:0xf bank_mask:0xf bound_ctrl:1
	s_nop 1
	v_add_f32_dpp v0, v0, v0 row_mirror row_mask:0xf bank_mask:0xf bound_ctrl:1
	s_nop 0
	v_readlane_b32 s8, v0, 0
	v_readlane_b32 s25, v0, 16
	v_readlane_b32 s9, v0, 32
	v_readlane_b32 s31, v0, 48
	v_add_u32_e32 v0, 0x4000, v52
	s_nop 0
	v_add_u32_e32 v53, 0, v0
	ds_read_b128 v[0:3], v53
	s_waitcnt lgkmcnt(0)
	v_mul_f32_e32 v1, v11, v1
	v_fmac_f32_e32 v1, v10, v0
	v_fmac_f32_e32 v1, v6, v2
	v_fmac_f32_e32 v1, v7, v3
	v_add_f32_e32 v54, 0, v1
	ds_read_b128 v[0:3], v53 offset:1024
	s_waitcnt lgkmcnt(0)
	v_mul_f32_e32 v1, v9, v1
	v_fmac_f32_e32 v1, v8, v0
	v_fmac_f32_e32 v1, v4, v2
	v_fmac_f32_e32 v1, v5, v3
	v_add_f32_e32 v54, v54, v1
	ds_read_b128 v[0:3], v53 offset:2048
	s_waitcnt lgkmcnt(0)
	v_mul_f32_e32 v1, v15, v1
	v_fmac_f32_e32 v1, v14, v0
	v_fmac_f32_e32 v1, v12, v2
	v_fmac_f32_e32 v1, v13, v3
	v_add_f32_e32 v54, v54, v1
	ds_read_b128 v[0:3], v53 offset:3072
	s_waitcnt lgkmcnt(0)
	v_mul_f32_e32 v1, v35, v1
	v_fmac_f32_e32 v1, v34, v0
	v_fmac_f32_e32 v1, v32, v2
	v_fmac_f32_e32 v1, v33, v3
	v_add_f32_e32 v54, v54, v1
	ds_read_b128 v[0:3], v53 offset:4096
	s_waitcnt lgkmcnt(0)
	v_mul_f32_e32 v1, v39, v1
	v_fmac_f32_e32 v1, v38, v0
	v_fmac_f32_e32 v1, v36, v2
	v_fmac_f32_e32 v1, v37, v3
	v_add_f32_e32 v54, v54, v1
	ds_read_b128 v[0:3], v53 offset:5120
	s_waitcnt lgkmcnt(0)
	v_mul_f32_e32 v1, v43, v1
	v_fmac_f32_e32 v1, v42, v0
	v_fmac_f32_e32 v1, v40, v2
	v_fmac_f32_e32 v1, v41, v3
	v_add_f32_e32 v54, v54, v1
	ds_read_b128 v[0:3], v53 offset:6144
	s_waitcnt lgkmcnt(0)
	v_mul_f32_e32 v1, v47, v1
	v_fmac_f32_e32 v1, v46, v0
	v_fmac_f32_e32 v1, v44, v2
	v_fmac_f32_e32 v1, v45, v3
	v_add_f32_e32 v54, v54, v1
	ds_read_b128 v[0:3], v53 offset:7168
	s_waitcnt lgkmcnt(0)
	v_mul_f32_e32 v1, v51, v1
	v_fmac_f32_e32 v1, v50, v0
	v_fmac_f32_e32 v1, v48, v2
	v_fmac_f32_e32 v1, v49, v3
	v_add_f32_e32 v0, v54, v1
	s_nop 1
	v_add_f32_dpp v0, v0, v0 quad_perm:[1,0,3,2] row_mask:0xf bank_mask:0xf bound_ctrl:1
	s_nop 1
	v_add_f32_dpp v0, v0, v0 quad_perm:[2,3,0,1] row_mask:0xf bank_mask:0xf bound_ctrl:1
	s_nop 1
	v_add_f32_dpp v0, v0, v0 row_half_mirror row_mask:0xf bank_mask:0xf bound_ctrl:1
	s_nop 1
	v_add_f32_dpp v0, v0, v0 row_mirror row_mask:0xf bank_mask:0xf bound_ctrl:1
	s_nop 0
	v_readlane_b32 s12, v0, 0
	v_readlane_b32 s14, v0, 16
	v_readlane_b32 s13, v0, 32
	v_readlane_b32 s15, v0, 48
	v_add_u32_e32 v0, 0x6000, v52
	s_nop 0
	v_add_u32_e32 v53, 0, v0
	ds_read_b128 v[0:3], v53
	s_waitcnt lgkmcnt(0)
	v_mul_f32_e32 v1, v11, v1
	v_fmac_f32_e32 v1, v10, v0
	v_fmac_f32_e32 v1, v6, v2
	v_fmac_f32_e32 v1, v7, v3
	v_add_f32_e32 v54, 0, v1
	ds_read_b128 v[0:3], v53 offset:1024
	s_waitcnt lgkmcnt(0)
	v_mul_f32_e32 v1, v9, v1
	v_fmac_f32_e32 v1, v8, v0
	v_fmac_f32_e32 v1, v4, v2
	v_fmac_f32_e32 v1, v5, v3
	v_add_f32_e32 v54, v54, v1
	ds_read_b128 v[0:3], v53 offset:2048
	s_waitcnt lgkmcnt(0)
	v_mul_f32_e32 v1, v15, v1
	v_fmac_f32_e32 v1, v14, v0
	v_fmac_f32_e32 v1, v12, v2
	v_fmac_f32_e32 v1, v13, v3
	v_add_f32_e32 v54, v54, v1
	ds_read_b128 v[0:3], v53 offset:3072
	s_waitcnt lgkmcnt(0)
	v_mul_f32_e32 v1, v35, v1
	v_fmac_f32_e32 v1, v34, v0
	v_fmac_f32_e32 v1, v32, v2
	v_fmac_f32_e32 v1, v33, v3
	v_add_f32_e32 v54, v54, v1
	ds_read_b128 v[0:3], v53 offset:4096
	s_waitcnt lgkmcnt(0)
	v_mul_f32_e32 v1, v39, v1
	v_fmac_f32_e32 v1, v38, v0
	v_fmac_f32_e32 v1, v36, v2
	v_fmac_f32_e32 v1, v37, v3
	v_add_f32_e32 v54, v54, v1
	ds_read_b128 v[0:3], v53 offset:5120
	s_waitcnt lgkmcnt(0)
	v_mul_f32_e32 v1, v43, v1
	v_fmac_f32_e32 v1, v42, v0
	v_fmac_f32_e32 v1, v40, v2
	v_fmac_f32_e32 v1, v41, v3
	v_add_f32_e32 v54, v54, v1
	ds_read_b128 v[0:3], v53 offset:6144
	s_waitcnt lgkmcnt(0)
	v_mul_f32_e32 v1, v47, v1
	v_fmac_f32_e32 v1, v46, v0
	v_fmac_f32_e32 v1, v44, v2
	v_fmac_f32_e32 v1, v45, v3
	v_add_f32_e32 v54, v54, v1
	ds_read_b128 v[0:3], v53 offset:7168
	s_waitcnt lgkmcnt(0)
	v_mul_f32_e32 v1, v51, v1
	v_fmac_f32_e32 v1, v50, v0
	v_fmac_f32_e32 v1, v48, v2
	v_fmac_f32_e32 v1, v49, v3
	v_add_f32_e32 v0, v54, v1
	s_nop 1
	v_add_f32_dpp v0, v0, v0 quad_perm:[1,0,3,2] row_mask:0xf bank_mask:0xf bound_ctrl:1
	s_nop 1
	v_add_f32_dpp v0, v0, v0 quad_perm:[2,3,0,1] row_mask:0xf bank_mask:0xf bound_ctrl:1
	s_nop 1
	v_add_f32_dpp v0, v0, v0 row_half_mirror row_mask:0xf bank_mask:0xf bound_ctrl:1
	s_nop 1
	v_add_f32_dpp v0, v0, v0 row_mirror row_mask:0xf bank_mask:0xf bound_ctrl:1
	s_nop 0
	v_readlane_b32 s53, v0, 0
	v_readlane_b32 s55, v0, 16
	v_readlane_b32 s54, v0, 32
	v_readlane_b32 s56, v0, 48
	v_add_u32_e32 v0, 0x8000, v52
	s_nop 0
	v_add_u32_e32 v53, 0, v0
	ds_read_b128 v[0:3], v53
	s_waitcnt lgkmcnt(0)
	v_mul_f32_e32 v1, v11, v1
	v_fmac_f32_e32 v1, v10, v0
	v_fmac_f32_e32 v1, v6, v2
	v_fmac_f32_e32 v1, v7, v3
	v_add_f32_e32 v54, 0, v1
	ds_read_b128 v[0:3], v53 offset:1024
	s_waitcnt lgkmcnt(0)
	v_mul_f32_e32 v1, v9, v1
	v_fmac_f32_e32 v1, v8, v0
	v_fmac_f32_e32 v1, v4, v2
	v_fmac_f32_e32 v1, v5, v3
	v_add_f32_e32 v54, v54, v1
	ds_read_b128 v[0:3], v53 offset:2048
	s_waitcnt lgkmcnt(0)
	v_mul_f32_e32 v1, v15, v1
	v_fmac_f32_e32 v1, v14, v0
	v_fmac_f32_e32 v1, v12, v2
	v_fmac_f32_e32 v1, v13, v3
	v_add_f32_e32 v54, v54, v1
	ds_read_b128 v[0:3], v53 offset:3072
	s_waitcnt lgkmcnt(0)
	v_mul_f32_e32 v1, v35, v1
	v_fmac_f32_e32 v1, v34, v0
	v_fmac_f32_e32 v1, v32, v2
	v_fmac_f32_e32 v1, v33, v3
	v_add_f32_e32 v54, v54, v1
	ds_read_b128 v[0:3], v53 offset:4096
	s_waitcnt lgkmcnt(0)
	v_mul_f32_e32 v1, v39, v1
	v_fmac_f32_e32 v1, v38, v0
	v_fmac_f32_e32 v1, v36, v2
	v_fmac_f32_e32 v1, v37, v3
	v_add_f32_e32 v54, v54, v1
	ds_read_b128 v[0:3], v53 offset:5120
	s_waitcnt lgkmcnt(0)
	v_mul_f32_e32 v1, v43, v1
	v_fmac_f32_e32 v1, v42, v0
	v_fmac_f32_e32 v1, v40, v2
	v_fmac_f32_e32 v1, v41, v3
	v_add_f32_e32 v54, v54, v1
	ds_read_b128 v[0:3], v53 offset:6144
	s_waitcnt lgkmcnt(0)
	v_mul_f32_e32 v1, v47, v1
	v_fmac_f32_e32 v1, v46, v0
	v_fmac_f32_e32 v1, v44, v2
	v_fmac_f32_e32 v1, v45, v3
	v_add_f32_e32 v54, v54, v1
	ds_read_b128 v[0:3], v53 offset:7168
	s_waitcnt lgkmcnt(0)
	v_mul_f32_e32 v1, v51, v1
	v_fmac_f32_e32 v1, v50, v0
	v_fmac_f32_e32 v1, v48, v2
	v_fmac_f32_e32 v1, v49, v3
	v_add_f32_e32 v0, v54, v1
	s_nop 1
	v_add_f32_dpp v0, v0, v0 quad_perm:[1,0,3,2] row_mask:0xf bank_mask:0xf bound_ctrl:1
	s_nop 1
	v_add_f32_dpp v0, v0, v0 quad_perm:[2,3,0,1] row_mask:0xf bank_mask:0xf bound_ctrl:1
	s_nop 1
	v_add_f32_dpp v0, v0, v0 row_half_mirror row_mask:0xf bank_mask:0xf bound_ctrl:1
	s_nop 1
	v_add_f32_dpp v0, v0, v0 row_mirror row_mask:0xf bank_mask:0xf bound_ctrl:1
	s_nop 0
	v_readlane_b32 s57, v0, 0
	v_readlane_b32 s59, v0, 16
	v_readlane_b32 s58, v0, 32
	v_readlane_b32 s60, v0, 48
	v_add_u32_e32 v0, 0xa000, v52
	s_nop 0
	v_add_u32_e32 v53, 0, v0
	ds_read_b128 v[0:3], v53
	s_waitcnt lgkmcnt(0)
	v_mul_f32_e32 v1, v11, v1
	v_fmac_f32_e32 v1, v10, v0
	v_fmac_f32_e32 v1, v6, v2
	v_fmac_f32_e32 v1, v7, v3
	v_add_f32_e32 v54, 0, v1
	ds_read_b128 v[0:3], v53 offset:1024
	s_waitcnt lgkmcnt(0)
	v_mul_f32_e32 v1, v9, v1
	v_fmac_f32_e32 v1, v8, v0
	v_fmac_f32_e32 v1, v4, v2
	v_fmac_f32_e32 v1, v5, v3
	v_add_f32_e32 v54, v54, v1
	ds_read_b128 v[0:3], v53 offset:2048
	s_waitcnt lgkmcnt(0)
	v_mul_f32_e32 v1, v15, v1
	v_fmac_f32_e32 v1, v14, v0
	v_fmac_f32_e32 v1, v12, v2
	v_fmac_f32_e32 v1, v13, v3
	v_add_f32_e32 v54, v54, v1
	ds_read_b128 v[0:3], v53 offset:3072
	s_waitcnt lgkmcnt(0)
	v_mul_f32_e32 v1, v35, v1
	v_fmac_f32_e32 v1, v34, v0
	v_fmac_f32_e32 v1, v32, v2
	v_fmac_f32_e32 v1, v33, v3
	v_add_f32_e32 v54, v54, v1
	ds_read_b128 v[0:3], v53 offset:4096
	s_waitcnt lgkmcnt(0)
	v_mul_f32_e32 v1, v39, v1
	v_fmac_f32_e32 v1, v38, v0
	v_fmac_f32_e32 v1, v36, v2
	v_fmac_f32_e32 v1, v37, v3
	v_add_f32_e32 v54, v54, v1
	ds_read_b128 v[0:3], v53 offset:5120
	s_waitcnt lgkmcnt(0)
	v_mul_f32_e32 v1, v43, v1
	v_fmac_f32_e32 v1, v42, v0
	v_fmac_f32_e32 v1, v40, v2
	v_fmac_f32_e32 v1, v41, v3
	v_add_f32_e32 v54, v54, v1
	ds_read_b128 v[0:3], v53 offset:6144
	s_waitcnt lgkmcnt(0)
	v_mul_f32_e32 v1, v47, v1
	v_fmac_f32_e32 v1, v46, v0
	v_fmac_f32_e32 v1, v44, v2
	v_fmac_f32_e32 v1, v45, v3
	v_add_f32_e32 v54, v54, v1
	ds_read_b128 v[0:3], v53 offset:7168
	s_waitcnt lgkmcnt(0)
	v_mul_f32_e32 v1, v51, v1
	v_fmac_f32_e32 v1, v50, v0
	v_fmac_f32_e32 v1, v48, v2
	v_fmac_f32_e32 v1, v49, v3
	v_add_f32_e32 v0, v54, v1
	s_nop 1
	v_add_f32_dpp v0, v0, v0 quad_perm:[1,0,3,2] row_mask:0xf bank_mask:0xf bound_ctrl:1
	s_nop 1
	v_add_f32_dpp v0, v0, v0 quad_perm:[2,3,0,1] row_mask:0xf bank_mask:0xf bound_ctrl:1
	s_nop 1
	v_add_f32_dpp v0, v0, v0 row_half_mirror row_mask:0xf bank_mask:0xf bound_ctrl:1
	s_nop 1
	v_add_f32_dpp v0, v0, v0 row_mirror row_mask:0xf bank_mask:0xf bound_ctrl:1
	s_nop 0
	v_readlane_b32 s0, v0, 0
	v_readlane_b32 s61, v0, 16
	v_readlane_b32 s1, v0, 32
	v_readlane_b32 s62, v0, 48
	v_add_u32_e32 v0, 0xc000, v52
	s_nop 0
	v_add_u32_e32 v53, 0, v0
	ds_read_b128 v[0:3], v53
	s_waitcnt lgkmcnt(0)
	v_mul_f32_e32 v1, v11, v1
	v_fmac_f32_e32 v1, v10, v0
	v_fmac_f32_e32 v1, v6, v2
	v_fmac_f32_e32 v1, v7, v3
	v_add_f32_e32 v54, 0, v1
	ds_read_b128 v[0:3], v53 offset:1024
	s_waitcnt lgkmcnt(0)
	v_mul_f32_e32 v1, v9, v1
	v_fmac_f32_e32 v1, v8, v0
	v_fmac_f32_e32 v1, v4, v2
	v_fmac_f32_e32 v1, v5, v3
	v_add_f32_e32 v54, v54, v1
	ds_read_b128 v[0:3], v53 offset:2048
	s_waitcnt lgkmcnt(0)
	v_mul_f32_e32 v1, v15, v1
	v_fmac_f32_e32 v1, v14, v0
	v_fmac_f32_e32 v1, v12, v2
	v_fmac_f32_e32 v1, v13, v3
	v_add_f32_e32 v54, v54, v1
	ds_read_b128 v[0:3], v53 offset:3072
	s_waitcnt lgkmcnt(0)
	v_mul_f32_e32 v1, v35, v1
	v_fmac_f32_e32 v1, v34, v0
	v_fmac_f32_e32 v1, v32, v2
	v_fmac_f32_e32 v1, v33, v3
	v_add_f32_e32 v54, v54, v1
	ds_read_b128 v[0:3], v53 offset:4096
	s_waitcnt lgkmcnt(0)
	v_mul_f32_e32 v1, v39, v1
	v_fmac_f32_e32 v1, v38, v0
	v_fmac_f32_e32 v1, v36, v2
	v_fmac_f32_e32 v1, v37, v3
	v_add_f32_e32 v54, v54, v1
	ds_read_b128 v[0:3], v53 offset:5120
	s_waitcnt lgkmcnt(0)
	v_mul_f32_e32 v1, v43, v1
	v_fmac_f32_e32 v1, v42, v0
	v_fmac_f32_e32 v1, v40, v2
	v_fmac_f32_e32 v1, v41, v3
	v_add_f32_e32 v54, v54, v1
	ds_read_b128 v[0:3], v53 offset:6144
	s_waitcnt lgkmcnt(0)
	v_mul_f32_e32 v1, v47, v1
	v_fmac_f32_e32 v1, v46, v0
	v_fmac_f32_e32 v1, v44, v2
	v_fmac_f32_e32 v1, v45, v3
	v_add_f32_e32 v54, v54, v1
	ds_read_b128 v[0:3], v53 offset:7168
	s_waitcnt lgkmcnt(0)
	v_mul_f32_e32 v1, v51, v1
	v_fmac_f32_e32 v1, v50, v0
	v_fmac_f32_e32 v1, v48, v2
	v_fmac_f32_e32 v1, v49, v3
	v_add_f32_e32 v0, v54, v1
	s_nop 1
	v_add_f32_dpp v0, v0, v0 quad_perm:[1,0,3,2] row_mask:0xf bank_mask:0xf bound_ctrl:1
	s_nop 1
	v_add_f32_dpp v0, v0, v0 quad_perm:[2,3,0,1] row_mask:0xf bank_mask:0xf bound_ctrl:1
	s_nop 1
	v_add_f32_dpp v0, v0, v0 row_half_mirror row_mask:0xf bank_mask:0xf bound_ctrl:1
	s_nop 1
	v_add_f32_dpp v0, v0, v0 row_mirror row_mask:0xf bank_mask:0xf bound_ctrl:1
	s_nop 0
	v_readlane_b32 s63, v0, 0
	v_readlane_b32 s65, v0, 16
	v_readlane_b32 s64, v0, 32
	v_readlane_b32 s66, v0, 48
	v_add_u32_e32 v0, 0xe000, v52
	s_nop 0
	v_add_u32_e32 v53, 0, v0
	ds_read_b128 v[0:3], v53
	s_waitcnt lgkmcnt(0)
	v_mul_f32_e32 v1, v11, v1
	v_fmac_f32_e32 v1, v10, v0
	v_fmac_f32_e32 v1, v6, v2
	v_fmac_f32_e32 v1, v7, v3
	v_add_f32_e32 v54, 0, v1
	ds_read_b128 v[0:3], v53 offset:1024
	s_waitcnt lgkmcnt(0)
	v_mul_f32_e32 v1, v9, v1
	v_fmac_f32_e32 v1, v8, v0
	v_fmac_f32_e32 v1, v4, v2
	v_fmac_f32_e32 v1, v5, v3
	v_add_f32_e32 v54, v54, v1
	ds_read_b128 v[0:3], v53 offset:2048
	s_waitcnt lgkmcnt(0)
	v_mul_f32_e32 v1, v15, v1
	v_fmac_f32_e32 v1, v14, v0
	v_fmac_f32_e32 v1, v12, v2
	v_fmac_f32_e32 v1, v13, v3
	v_add_f32_e32 v54, v54, v1
	ds_read_b128 v[0:3], v53 offset:3072
	s_waitcnt lgkmcnt(0)
	v_mul_f32_e32 v1, v35, v1
	v_fmac_f32_e32 v1, v34, v0
	v_fmac_f32_e32 v1, v32, v2
	v_fmac_f32_e32 v1, v33, v3
	v_add_f32_e32 v54, v54, v1
	ds_read_b128 v[0:3], v53 offset:4096
	s_waitcnt lgkmcnt(0)
	v_mul_f32_e32 v1, v39, v1
	v_fmac_f32_e32 v1, v38, v0
	v_fmac_f32_e32 v1, v36, v2
	v_fmac_f32_e32 v1, v37, v3
	v_add_f32_e32 v54, v54, v1
	ds_read_b128 v[0:3], v53 offset:5120
	s_waitcnt lgkmcnt(0)
	v_mul_f32_e32 v1, v43, v1
	v_fmac_f32_e32 v1, v42, v0
	v_fmac_f32_e32 v1, v40, v2
	v_fmac_f32_e32 v1, v41, v3
	v_add_f32_e32 v54, v54, v1
	ds_read_b128 v[0:3], v53 offset:6144
	s_waitcnt lgkmcnt(0)
	v_mul_f32_e32 v1, v47, v1
	v_fmac_f32_e32 v1, v46, v0
	v_fmac_f32_e32 v1, v44, v2
	v_fmac_f32_e32 v1, v45, v3
	v_add_f32_e32 v54, v54, v1
	ds_read_b128 v[0:3], v53 offset:7168
	s_waitcnt lgkmcnt(0)
	v_mul_f32_e32 v1, v51, v1
	v_fmac_f32_e32 v1, v50, v0
	v_fmac_f32_e32 v1, v48, v2
	v_fmac_f32_e32 v1, v49, v3
	v_add_f32_e32 v0, v54, v1
	s_nop 1
	v_add_f32_dpp v0, v0, v0 quad_perm:[1,0,3,2] row_mask:0xf bank_mask:0xf bound_ctrl:1
	s_nop 1
	v_add_f32_dpp v0, v0, v0 quad_perm:[2,3,0,1] row_mask:0xf bank_mask:0xf bound_ctrl:1
	s_nop 1
	v_add_f32_dpp v0, v0, v0 row_half_mirror row_mask:0xf bank_mask:0xf bound_ctrl:1
	s_nop 1
	v_add_f32_dpp v0, v0, v0 row_mirror row_mask:0xf bank_mask:0xf bound_ctrl:1
	s_nop 0
	v_readlane_b32 s67, v0, 0
	v_readlane_b32 s69, v0, 16
	v_readlane_b32 s68, v0, 32
	v_readlane_b32 s70, v0, 48
	v_add_u32_e32 v0, 0x10000, v52
	s_nop 0
	v_add_u32_e32 v53, 0, v0
	ds_read_b128 v[0:3], v53
	s_waitcnt lgkmcnt(0)
	v_mul_f32_e32 v1, v11, v1
	v_fmac_f32_e32 v1, v10, v0
	v_fmac_f32_e32 v1, v6, v2
	v_fmac_f32_e32 v1, v7, v3
	v_add_f32_e32 v54, 0, v1
	ds_read_b128 v[0:3], v53 offset:1024
	s_waitcnt lgkmcnt(0)
	v_mul_f32_e32 v1, v9, v1
	v_fmac_f32_e32 v1, v8, v0
	v_fmac_f32_e32 v1, v4, v2
	v_fmac_f32_e32 v1, v5, v3
	v_add_f32_e32 v54, v54, v1
	ds_read_b128 v[0:3], v53 offset:2048
	s_waitcnt lgkmcnt(0)
	v_mul_f32_e32 v1, v15, v1
	v_fmac_f32_e32 v1, v14, v0
	v_fmac_f32_e32 v1, v12, v2
	v_fmac_f32_e32 v1, v13, v3
	v_add_f32_e32 v54, v54, v1
	ds_read_b128 v[0:3], v53 offset:3072
	s_waitcnt lgkmcnt(0)
	v_mul_f32_e32 v1, v35, v1
	v_fmac_f32_e32 v1, v34, v0
	v_fmac_f32_e32 v1, v32, v2
	v_fmac_f32_e32 v1, v33, v3
	v_add_f32_e32 v54, v54, v1
	ds_read_b128 v[0:3], v53 offset:4096
	s_waitcnt lgkmcnt(0)
	v_mul_f32_e32 v1, v39, v1
	v_fmac_f32_e32 v1, v38, v0
	v_fmac_f32_e32 v1, v36, v2
	v_fmac_f32_e32 v1, v37, v3
	v_add_f32_e32 v54, v54, v1
	ds_read_b128 v[0:3], v53 offset:5120
	s_waitcnt lgkmcnt(0)
	v_mul_f32_e32 v1, v43, v1
	v_fmac_f32_e32 v1, v42, v0
	v_fmac_f32_e32 v1, v40, v2
	v_fmac_f32_e32 v1, v41, v3
	v_add_f32_e32 v54, v54, v1
	ds_read_b128 v[0:3], v53 offset:6144
	s_waitcnt lgkmcnt(0)
	v_mul_f32_e32 v1, v47, v1
	v_fmac_f32_e32 v1, v46, v0
	v_fmac_f32_e32 v1, v44, v2
	v_fmac_f32_e32 v1, v45, v3
	v_add_f32_e32 v54, v54, v1
	ds_read_b128 v[0:3], v53 offset:7168
	s_waitcnt lgkmcnt(0)
	v_mul_f32_e32 v1, v51, v1
	v_fmac_f32_e32 v1, v50, v0
	v_fmac_f32_e32 v1, v48, v2
	v_fmac_f32_e32 v1, v49, v3
	v_add_f32_e32 v0, v54, v1
	s_nop 1
	v_add_f32_dpp v0, v0, v0 quad_perm:[1,0,3,2] row_mask:0xf bank_mask:0xf bound_ctrl:1
	s_nop 1
	v_add_f32_dpp v0, v0, v0 quad_perm:[2,3,0,1] row_mask:0xf bank_mask:0xf bound_ctrl:1
	s_nop 1
	v_add_f32_dpp v0, v0, v0 row_half_mirror row_mask:0xf bank_mask:0xf bound_ctrl:1
	s_nop 1
	v_add_f32_dpp v0, v0, v0 row_mirror row_mask:0xf bank_mask:0xf bound_ctrl:1
	s_nop 0
	v_readlane_b32 s71, v0, 0
	v_readlane_b32 s73, v0, 16
	v_readlane_b32 s72, v0, 32
	v_readlane_b32 s74, v0, 48
	v_add_u32_e32 v0, 0x12000, v52
	s_nop 0
	v_add_u32_e32 v53, 0, v0
	ds_read_b128 v[0:3], v53
	s_waitcnt lgkmcnt(0)
	v_mul_f32_e32 v1, v11, v1
	v_fmac_f32_e32 v1, v10, v0
	v_fmac_f32_e32 v1, v6, v2
	v_fmac_f32_e32 v1, v7, v3
	v_add_f32_e32 v54, 0, v1
	ds_read_b128 v[0:3], v53 offset:1024
	s_waitcnt lgkmcnt(0)
	v_mul_f32_e32 v1, v9, v1
	v_fmac_f32_e32 v1, v8, v0
	v_fmac_f32_e32 v1, v4, v2
	v_fmac_f32_e32 v1, v5, v3
	v_add_f32_e32 v54, v54, v1
	ds_read_b128 v[0:3], v53 offset:2048
	s_waitcnt lgkmcnt(0)
	v_mul_f32_e32 v1, v15, v1
	v_fmac_f32_e32 v1, v14, v0
	v_fmac_f32_e32 v1, v12, v2
	v_fmac_f32_e32 v1, v13, v3
	v_add_f32_e32 v54, v54, v1
	ds_read_b128 v[0:3], v53 offset:3072
	s_waitcnt lgkmcnt(0)
	v_mul_f32_e32 v1, v35, v1
	v_fmac_f32_e32 v1, v34, v0
	v_fmac_f32_e32 v1, v32, v2
	v_fmac_f32_e32 v1, v33, v3
	v_add_f32_e32 v54, v54, v1
	ds_read_b128 v[0:3], v53 offset:4096
	s_waitcnt lgkmcnt(0)
	v_mul_f32_e32 v1, v39, v1
	v_fmac_f32_e32 v1, v38, v0
	v_fmac_f32_e32 v1, v36, v2
	v_fmac_f32_e32 v1, v37, v3
	v_add_f32_e32 v54, v54, v1
	ds_read_b128 v[0:3], v53 offset:5120
	s_waitcnt lgkmcnt(0)
	v_mul_f32_e32 v1, v43, v1
	v_fmac_f32_e32 v1, v42, v0
	v_fmac_f32_e32 v1, v40, v2
	v_fmac_f32_e32 v1, v41, v3
	v_add_f32_e32 v54, v54, v1
	ds_read_b128 v[0:3], v53 offset:6144
	s_waitcnt lgkmcnt(0)
	v_mul_f32_e32 v1, v47, v1
	v_fmac_f32_e32 v1, v46, v0
	v_fmac_f32_e32 v1, v44, v2
	v_fmac_f32_e32 v1, v45, v3
	v_add_f32_e32 v54, v54, v1
	ds_read_b128 v[0:3], v53 offset:7168
	s_waitcnt lgkmcnt(0)
	v_mul_f32_e32 v1, v51, v1
	v_fmac_f32_e32 v1, v50, v0
	v_fmac_f32_e32 v1, v48, v2
	v_fmac_f32_e32 v1, v49, v3
	v_add_f32_e32 v0, v54, v1
	s_nop 1
	v_add_f32_dpp v0, v0, v0 quad_perm:[1,0,3,2] row_mask:0xf bank_mask:0xf bound_ctrl:1
	s_nop 1
	v_add_f32_dpp v0, v0, v0 quad_perm:[2,3,0,1] row_mask:0xf bank_mask:0xf bound_ctrl:1
	s_nop 1
	v_add_f32_dpp v0, v0, v0 row_half_mirror row_mask:0xf bank_mask:0xf bound_ctrl:1
	s_nop 1
	v_add_f32_dpp v0, v0, v0 row_mirror row_mask:0xf bank_mask:0xf bound_ctrl:1
	s_nop 0
	v_readlane_b32 s77, v0, 0
	v_readlane_b32 s78, v0, 16
	v_readlane_b32 s75, v0, 32
	v_readlane_b32 s76, v0, 48
	v_add_u32_e32 v0, 0x14000, v52
	s_nop 0
	v_add_u32_e32 v53, 0, v0
	ds_read_b128 v[0:3], v53
	s_waitcnt lgkmcnt(0)
	v_mul_f32_e32 v1, v11, v1
	v_fmac_f32_e32 v1, v10, v0
	v_fmac_f32_e32 v1, v6, v2
	v_fmac_f32_e32 v1, v7, v3
	v_add_f32_e32 v54, 0, v1
	ds_read_b128 v[0:3], v53 offset:1024
	s_waitcnt lgkmcnt(0)
	v_mul_f32_e32 v1, v9, v1
	v_fmac_f32_e32 v1, v8, v0
	v_fmac_f32_e32 v1, v4, v2
	v_fmac_f32_e32 v1, v5, v3
	v_add_f32_e32 v54, v54, v1
	ds_read_b128 v[0:3], v53 offset:2048
	s_waitcnt lgkmcnt(0)
	v_mul_f32_e32 v1, v15, v1
	v_fmac_f32_e32 v1, v14, v0
	v_fmac_f32_e32 v1, v12, v2
	v_fmac_f32_e32 v1, v13, v3
	v_add_f32_e32 v54, v54, v1
	ds_read_b128 v[0:3], v53 offset:3072
	s_waitcnt lgkmcnt(0)
	v_mul_f32_e32 v1, v35, v1
	v_fmac_f32_e32 v1, v34, v0
	v_fmac_f32_e32 v1, v32, v2
	v_fmac_f32_e32 v1, v33, v3
	v_add_f32_e32 v54, v54, v1
	ds_read_b128 v[0:3], v53 offset:4096
	s_waitcnt lgkmcnt(0)
	v_mul_f32_e32 v1, v39, v1
	v_fmac_f32_e32 v1, v38, v0
	v_fmac_f32_e32 v1, v36, v2
	v_fmac_f32_e32 v1, v37, v3
	v_add_f32_e32 v54, v54, v1
	ds_read_b128 v[0:3], v53 offset:5120
	s_waitcnt lgkmcnt(0)
	v_mul_f32_e32 v1, v43, v1
	v_fmac_f32_e32 v1, v42, v0
	v_fmac_f32_e32 v1, v40, v2
	v_fmac_f32_e32 v1, v41, v3
	v_add_f32_e32 v54, v54, v1
	ds_read_b128 v[0:3], v53 offset:6144
	s_waitcnt lgkmcnt(0)
	v_mul_f32_e32 v1, v47, v1
	v_fmac_f32_e32 v1, v46, v0
	v_fmac_f32_e32 v1, v44, v2
	v_fmac_f32_e32 v1, v45, v3
	v_add_f32_e32 v54, v54, v1
	ds_read_b128 v[0:3], v53 offset:7168
	s_waitcnt lgkmcnt(0)
	v_mul_f32_e32 v1, v51, v1
	v_fmac_f32_e32 v1, v50, v0
	v_fmac_f32_e32 v1, v48, v2
	v_fmac_f32_e32 v1, v49, v3
	v_add_f32_e32 v0, v54, v1
	s_nop 1
	v_add_f32_dpp v0, v0, v0 quad_perm:[1,0,3,2] row_mask:0xf bank_mask:0xf bound_ctrl:1
	s_nop 1
	v_add_f32_dpp v0, v0, v0 quad_perm:[2,3,0,1] row_mask:0xf bank_mask:0xf bound_ctrl:1
	s_nop 1
	v_add_f32_dpp v0, v0, v0 row_half_mirror row_mask:0xf bank_mask:0xf bound_ctrl:1
	s_nop 1
	v_add_f32_dpp v0, v0, v0 row_mirror row_mask:0xf bank_mask:0xf bound_ctrl:1
	s_nop 0
	v_readlane_b32 s79, v0, 0
	v_readlane_b32 s81, v0, 16
	v_readlane_b32 s80, v0, 32
	v_readlane_b32 s82, v0, 48
	v_add_u32_e32 v0, 0x16000, v52
	s_nop 0
	v_add_u32_e32 v53, 0, v0
	ds_read_b128 v[0:3], v53
	s_waitcnt lgkmcnt(0)
	v_mul_f32_e32 v1, v11, v1
	v_fmac_f32_e32 v1, v10, v0
	v_fmac_f32_e32 v1, v6, v2
	v_fmac_f32_e32 v1, v7, v3
	v_add_f32_e32 v54, 0, v1
	ds_read_b128 v[0:3], v53 offset:1024
	s_waitcnt lgkmcnt(0)
	v_mul_f32_e32 v1, v9, v1
	v_fmac_f32_e32 v1, v8, v0
	v_fmac_f32_e32 v1, v4, v2
	v_fmac_f32_e32 v1, v5, v3
	v_add_f32_e32 v54, v54, v1
	ds_read_b128 v[0:3], v53 offset:2048
	s_waitcnt lgkmcnt(0)
	v_mul_f32_e32 v1, v15, v1
	v_fmac_f32_e32 v1, v14, v0
	v_fmac_f32_e32 v1, v12, v2
	v_fmac_f32_e32 v1, v13, v3
	v_add_f32_e32 v54, v54, v1
	ds_read_b128 v[0:3], v53 offset:3072
	s_waitcnt lgkmcnt(0)
	v_mul_f32_e32 v1, v35, v1
	v_fmac_f32_e32 v1, v34, v0
	v_fmac_f32_e32 v1, v32, v2
	v_fmac_f32_e32 v1, v33, v3
	v_add_f32_e32 v54, v54, v1
	ds_read_b128 v[0:3], v53 offset:4096
	s_waitcnt lgkmcnt(0)
	v_mul_f32_e32 v1, v39, v1
	v_fmac_f32_e32 v1, v38, v0
	v_fmac_f32_e32 v1, v36, v2
	v_fmac_f32_e32 v1, v37, v3
	v_add_f32_e32 v54, v54, v1
	ds_read_b128 v[0:3], v53 offset:5120
	s_waitcnt lgkmcnt(0)
	v_mul_f32_e32 v1, v43, v1
	v_fmac_f32_e32 v1, v42, v0
	v_fmac_f32_e32 v1, v40, v2
	v_fmac_f32_e32 v1, v41, v3
	v_add_f32_e32 v54, v54, v1
	ds_read_b128 v[0:3], v53 offset:6144
	s_waitcnt lgkmcnt(0)
	v_mul_f32_e32 v1, v47, v1
	v_fmac_f32_e32 v1, v46, v0
	v_fmac_f32_e32 v1, v44, v2
	v_fmac_f32_e32 v1, v45, v3
	v_add_f32_e32 v54, v54, v1
	ds_read_b128 v[0:3], v53 offset:7168
	s_waitcnt lgkmcnt(0)
	v_mul_f32_e32 v1, v51, v1
	v_fmac_f32_e32 v1, v50, v0
	v_fmac_f32_e32 v1, v48, v2
	v_fmac_f32_e32 v1, v49, v3
	v_add_f32_e32 v0, v54, v1
	s_nop 1
	v_add_f32_dpp v0, v0, v0 quad_perm:[1,0,3,2] row_mask:0xf bank_mask:0xf bound_ctrl:1
	s_nop 1
	v_add_f32_dpp v0, v0, v0 quad_perm:[2,3,0,1] row_mask:0xf bank_mask:0xf bound_ctrl:1
	s_nop 1
	v_add_f32_dpp v0, v0, v0 row_half_mirror row_mask:0xf bank_mask:0xf bound_ctrl:1
	s_nop 1
	v_add_f32_dpp v0, v0, v0 row_mirror row_mask:0xf bank_mask:0xf bound_ctrl:1
	s_nop 0
	v_readlane_b32 s83, v0, 0
	v_readlane_b32 s85, v0, 16
	v_readlane_b32 s84, v0, 32
	v_readlane_b32 s86, v0, 48
	v_add_u32_e32 v0, 0x18000, v52
	s_nop 0
	v_add_u32_e32 v53, 0, v0
	ds_read_b128 v[0:3], v53
	s_waitcnt lgkmcnt(0)
	v_mul_f32_e32 v1, v11, v1
	v_fmac_f32_e32 v1, v10, v0
	v_fmac_f32_e32 v1, v6, v2
	v_fmac_f32_e32 v1, v7, v3
	v_add_f32_e32 v54, 0, v1
	ds_read_b128 v[0:3], v53 offset:1024
	s_waitcnt lgkmcnt(0)
	v_mul_f32_e32 v1, v9, v1
	v_fmac_f32_e32 v1, v8, v0
	v_fmac_f32_e32 v1, v4, v2
	v_fmac_f32_e32 v1, v5, v3
	v_add_f32_e32 v54, v54, v1
	ds_read_b128 v[0:3], v53 offset:2048
	s_waitcnt lgkmcnt(0)
	v_mul_f32_e32 v1, v15, v1
	v_fmac_f32_e32 v1, v14, v0
	v_fmac_f32_e32 v1, v12, v2
	v_fmac_f32_e32 v1, v13, v3
	v_add_f32_e32 v54, v54, v1
	ds_read_b128 v[0:3], v53 offset:3072
	s_waitcnt lgkmcnt(0)
	v_mul_f32_e32 v1, v35, v1
	v_fmac_f32_e32 v1, v34, v0
	v_fmac_f32_e32 v1, v32, v2
	v_fmac_f32_e32 v1, v33, v3
	v_add_f32_e32 v54, v54, v1
	ds_read_b128 v[0:3], v53 offset:4096
	s_waitcnt lgkmcnt(0)
	v_mul_f32_e32 v1, v39, v1
	v_fmac_f32_e32 v1, v38, v0
	v_fmac_f32_e32 v1, v36, v2
	v_fmac_f32_e32 v1, v37, v3
	v_add_f32_e32 v54, v54, v1
	ds_read_b128 v[0:3], v53 offset:5120
	s_waitcnt lgkmcnt(0)
	v_mul_f32_e32 v1, v43, v1
	v_fmac_f32_e32 v1, v42, v0
	v_fmac_f32_e32 v1, v40, v2
	v_fmac_f32_e32 v1, v41, v3
	v_add_f32_e32 v54, v54, v1
	ds_read_b128 v[0:3], v53 offset:6144
	s_waitcnt lgkmcnt(0)
	v_mul_f32_e32 v1, v47, v1
	v_fmac_f32_e32 v1, v46, v0
	v_fmac_f32_e32 v1, v44, v2
	v_fmac_f32_e32 v1, v45, v3
	v_add_f32_e32 v54, v54, v1
	ds_read_b128 v[0:3], v53 offset:7168
	s_waitcnt lgkmcnt(0)
	v_mul_f32_e32 v1, v51, v1
	v_fmac_f32_e32 v1, v50, v0
	v_fmac_f32_e32 v1, v48, v2
	v_fmac_f32_e32 v1, v49, v3
	v_add_f32_e32 v0, v54, v1
	s_nop 1
	v_add_f32_dpp v0, v0, v0 quad_perm:[1,0,3,2] row_mask:0xf bank_mask:0xf bound_ctrl:1
	s_nop 1
	v_add_f32_dpp v0, v0, v0 quad_perm:[2,3,0,1] row_mask:0xf bank_mask:0xf bound_ctrl:1
	s_nop 1
	v_add_f32_dpp v0, v0, v0 row_half_mirror row_mask:0xf bank_mask:0xf bound_ctrl:1
	s_nop 1
	v_add_f32_dpp v0, v0, v0 row_mirror row_mask:0xf bank_mask:0xf bound_ctrl:1
	s_nop 0
	v_readlane_b32 s87, v0, 0
	v_readlane_b32 s89, v0, 16
	v_readlane_b32 s88, v0, 32
	v_readlane_b32 s90, v0, 48
	v_add_u32_e32 v0, 0x1a000, v52
	s_nop 0
	v_add_u32_e32 v53, 0, v0
	ds_read_b128 v[0:3], v53
	s_waitcnt lgkmcnt(0)
	v_mul_f32_e32 v1, v11, v1
	v_fmac_f32_e32 v1, v10, v0
	v_fmac_f32_e32 v1, v6, v2
	v_fmac_f32_e32 v1, v7, v3
	v_add_f32_e32 v54, 0, v1
	ds_read_b128 v[0:3], v53 offset:1024
	s_waitcnt lgkmcnt(0)
	v_mul_f32_e32 v1, v9, v1
	v_fmac_f32_e32 v1, v8, v0
	v_fmac_f32_e32 v1, v4, v2
	v_fmac_f32_e32 v1, v5, v3
	v_add_f32_e32 v54, v54, v1
	ds_read_b128 v[0:3], v53 offset:2048
	s_waitcnt lgkmcnt(0)
	v_mul_f32_e32 v1, v15, v1
	v_fmac_f32_e32 v1, v14, v0
	v_fmac_f32_e32 v1, v12, v2
	v_fmac_f32_e32 v1, v13, v3
	v_add_f32_e32 v54, v54, v1
	ds_read_b128 v[0:3], v53 offset:3072
	s_waitcnt lgkmcnt(0)
	v_mul_f32_e32 v1, v35, v1
	v_fmac_f32_e32 v1, v34, v0
	v_fmac_f32_e32 v1, v32, v2
	v_fmac_f32_e32 v1, v33, v3
	v_add_f32_e32 v54, v54, v1
	ds_read_b128 v[0:3], v53 offset:4096
	s_waitcnt lgkmcnt(0)
	v_mul_f32_e32 v1, v39, v1
	v_fmac_f32_e32 v1, v38, v0
	v_fmac_f32_e32 v1, v36, v2
	v_fmac_f32_e32 v1, v37, v3
	v_add_f32_e32 v54, v54, v1
	ds_read_b128 v[0:3], v53 offset:5120
	s_waitcnt lgkmcnt(0)
	v_mul_f32_e32 v1, v43, v1
	v_fmac_f32_e32 v1, v42, v0
	v_fmac_f32_e32 v1, v40, v2
	v_fmac_f32_e32 v1, v41, v3
	v_add_f32_e32 v54, v54, v1
	ds_read_b128 v[0:3], v53 offset:6144
	s_waitcnt lgkmcnt(0)
	v_mul_f32_e32 v1, v47, v1
	v_fmac_f32_e32 v1, v46, v0
	v_fmac_f32_e32 v1, v44, v2
	v_fmac_f32_e32 v1, v45, v3
	v_add_f32_e32 v54, v54, v1
	ds_read_b128 v[0:3], v53 offset:7168
	s_waitcnt lgkmcnt(0)
	v_mul_f32_e32 v1, v51, v1
	v_fmac_f32_e32 v1, v50, v0
	v_fmac_f32_e32 v1, v48, v2
	v_fmac_f32_e32 v1, v49, v3
	v_add_f32_e32 v0, v54, v1
	s_nop 1
	v_add_f32_dpp v0, v0, v0 quad_perm:[1,0,3,2] row_mask:0xf bank_mask:0xf bound_ctrl:1
	s_nop 1
	v_add_f32_dpp v0, v0, v0 quad_perm:[2,3,0,1] row_mask:0xf bank_mask:0xf bound_ctrl:1
	s_nop 1
	v_add_f32_dpp v0, v0, v0 row_half_mirror row_mask:0xf bank_mask:0xf bound_ctrl:1
	s_nop 1
	v_add_f32_dpp v0, v0, v0 row_mirror row_mask:0xf bank_mask:0xf bound_ctrl:1
	s_nop 0
	v_readlane_b32 s93, v0, 0
	v_readlane_b32 s94, v0, 16
	v_readlane_b32 s91, v0, 32
	v_readlane_b32 s92, v0, 48
	v_add_u32_e32 v0, 0x1c000, v52
	s_nop 0
	v_add_u32_e32 v53, 0, v0
	ds_read_b128 v[0:3], v53
	s_waitcnt lgkmcnt(0)
	v_mul_f32_e32 v1, v11, v1
	v_fmac_f32_e32 v1, v10, v0
	v_fmac_f32_e32 v1, v6, v2
	v_fmac_f32_e32 v1, v7, v3
	v_add_f32_e32 v54, 0, v1
	ds_read_b128 v[0:3], v53 offset:1024
	s_waitcnt lgkmcnt(0)
	v_mul_f32_e32 v1, v9, v1
	v_fmac_f32_e32 v1, v8, v0
	v_fmac_f32_e32 v1, v4, v2
	v_fmac_f32_e32 v1, v5, v3
	v_add_f32_e32 v54, v54, v1
	ds_read_b128 v[0:3], v53 offset:2048
	s_waitcnt lgkmcnt(0)
	v_mul_f32_e32 v1, v15, v1
	v_fmac_f32_e32 v1, v14, v0
	v_fmac_f32_e32 v1, v12, v2
	v_fmac_f32_e32 v1, v13, v3
	v_add_f32_e32 v54, v54, v1
	ds_read_b128 v[0:3], v53 offset:3072
	s_waitcnt lgkmcnt(0)
	v_mul_f32_e32 v1, v35, v1
	v_fmac_f32_e32 v1, v34, v0
	v_fmac_f32_e32 v1, v32, v2
	v_fmac_f32_e32 v1, v33, v3
	v_add_f32_e32 v54, v54, v1
	ds_read_b128 v[0:3], v53 offset:4096
	s_waitcnt lgkmcnt(0)
	v_mul_f32_e32 v1, v39, v1
	v_fmac_f32_e32 v1, v38, v0
	v_fmac_f32_e32 v1, v36, v2
	v_fmac_f32_e32 v1, v37, v3
	v_add_f32_e32 v54, v54, v1
	ds_read_b128 v[0:3], v53 offset:5120
	s_waitcnt lgkmcnt(0)
	v_mul_f32_e32 v1, v43, v1
	v_fmac_f32_e32 v1, v42, v0
	v_fmac_f32_e32 v1, v40, v2
	v_fmac_f32_e32 v1, v41, v3
	v_add_f32_e32 v54, v54, v1
	ds_read_b128 v[0:3], v53 offset:6144
	s_waitcnt lgkmcnt(0)
	v_mul_f32_e32 v1, v47, v1
	v_fmac_f32_e32 v1, v46, v0
	v_fmac_f32_e32 v1, v44, v2
	v_fmac_f32_e32 v1, v45, v3
	v_add_f32_e32 v54, v54, v1
	ds_read_b128 v[0:3], v53 offset:7168
	s_waitcnt lgkmcnt(0)
	v_mul_f32_e32 v1, v51, v1
	v_fmac_f32_e32 v1, v50, v0
	v_fmac_f32_e32 v1, v48, v2
	v_fmac_f32_e32 v1, v49, v3
	v_add_f32_e32 v0, v54, v1
	s_nop 1
	v_add_f32_dpp v0, v0, v0 quad_perm:[1,0,3,2] row_mask:0xf bank_mask:0xf bound_ctrl:1
	s_nop 1
	v_add_f32_dpp v0, v0, v0 quad_perm:[2,3,0,1] row_mask:0xf bank_mask:0xf bound_ctrl:1
	s_nop 1
	v_add_f32_dpp v0, v0, v0 row_half_mirror row_mask:0xf bank_mask:0xf bound_ctrl:1
	s_nop 1
	v_add_f32_dpp v0, v0, v0 row_mirror row_mask:0xf bank_mask:0xf bound_ctrl:1
	s_nop 0
	v_readlane_b32 s95, v0, 0
	v_readlane_b32 s97, v0, 16
	v_readlane_b32 s96, v0, 32
	v_readlane_b32 s4, v0, 48
	v_add_u32_e32 v0, 0x1e000, v52
	s_nop 0
	v_add_u32_e32 v52, 0, v0
	ds_read_b128 v[0:3], v52
	s_waitcnt lgkmcnt(0)
	v_mul_f32_e32 v1, v11, v1
	v_fmac_f32_e32 v1, v10, v0
	v_fmac_f32_e32 v1, v6, v2
	v_fmac_f32_e32 v1, v7, v3
	v_add_f32_e32 v6, 0, v1
	ds_read_b128 v[0:3], v52 offset:1024
	s_waitcnt lgkmcnt(0)
	v_mul_f32_e32 v1, v9, v1
	v_fmac_f32_e32 v1, v8, v0
	v_fmac_f32_e32 v1, v4, v2
	v_fmac_f32_e32 v1, v5, v3
	v_add_f32_e32 v4, v6, v1
	ds_read_b128 v[0:3], v52 offset:2048
	s_waitcnt lgkmcnt(0)
	v_mul_f32_e32 v1, v15, v1
	v_fmac_f32_e32 v1, v14, v0
	v_fmac_f32_e32 v1, v12, v2
	v_fmac_f32_e32 v1, v13, v3
	v_add_f32_e32 v4, v4, v1
	ds_read_b128 v[0:3], v52 offset:3072
	s_waitcnt lgkmcnt(0)
	v_mul_f32_e32 v1, v35, v1
	v_fmac_f32_e32 v1, v34, v0
	v_fmac_f32_e32 v1, v32, v2
	v_fmac_f32_e32 v1, v33, v3
	v_add_f32_e32 v4, v4, v1
	ds_read_b128 v[0:3], v52 offset:4096
	s_waitcnt lgkmcnt(0)
	v_mul_f32_e32 v1, v39, v1
	v_fmac_f32_e32 v1, v38, v0
	v_fmac_f32_e32 v1, v36, v2
	v_fmac_f32_e32 v1, v37, v3
	v_add_f32_e32 v4, v4, v1
	ds_read_b128 v[0:3], v52 offset:5120
	s_waitcnt lgkmcnt(0)
	v_mul_f32_e32 v1, v43, v1
	v_fmac_f32_e32 v1, v42, v0
	v_fmac_f32_e32 v1, v40, v2
	v_fmac_f32_e32 v1, v41, v3
	v_add_f32_e32 v4, v4, v1
	ds_read_b128 v[0:3], v52 offset:6144
	s_waitcnt lgkmcnt(0)
	v_mul_f32_e32 v1, v47, v1
	v_fmac_f32_e32 v1, v46, v0
	v_fmac_f32_e32 v1, v44, v2
	v_fmac_f32_e32 v1, v45, v3
	v_add_f32_e32 v4, v4, v1
	ds_read_b128 v[0:3], v52 offset:7168
	s_waitcnt lgkmcnt(0)
	v_mul_f32_e32 v1, v51, v1
	v_fmac_f32_e32 v1, v50, v0
	v_fmac_f32_e32 v1, v48, v2
	v_fmac_f32_e32 v1, v49, v3
	v_add_f32_e32 v0, v4, v1
	s_nop 1
	v_add_f32_dpp v0, v0, v0 quad_perm:[1,0,3,2] row_mask:0xf bank_mask:0xf bound_ctrl:1
	s_nop 1
	v_add_f32_dpp v0, v0, v0 quad_perm:[2,3,0,1] row_mask:0xf bank_mask:0xf bound_ctrl:1
	s_nop 1
	v_add_f32_dpp v0, v0, v0 row_half_mirror row_mask:0xf bank_mask:0xf bound_ctrl:1
	s_nop 1
	v_add_f32_dpp v0, v0, v0 row_mirror row_mask:0xf bank_mask:0xf bound_ctrl:1
	s_nop 0
	v_readlane_b32 s5, v0, 0
	v_readlane_b32 s40, v0, 16
	v_readlane_b32 s33, v0, 32
	v_readlane_b32 s16, v0, 48
	s_and_saveexec_b64 s[36:37], vcc
	s_cbranch_execz .LBB0_5004
	v_mov_b32_e32 v0, s25
	v_mov_b32_e32 v1, s31
	v_pk_add_f32 v[0:1], s[8:9], v[0:1]
	s_nop 0
	v_add_f32_e32 v33, v0, v1
	v_mov_b32_e32 v0, s10
	v_mov_b32_e32 v1, s11
	v_pk_add_f32 v[0:1], s[6:7], v[0:1]
	v_mul_f32_e32 v34, 0xbfb8aa3b, v33
	v_add_f32_e32 v0, v0, v1
	v_mul_f32_e32 v1, 0xbfb8aa3b, v0
	v_fma_f32 v2, v0, s23, -v1
	v_rndne_f32_e32 v3, v1
	v_fmac_f32_e32 v2, 0xb2a5705f, v0
	v_sub_f32_e32 v1, v1, v3
	v_add_f32_e32 v1, v1, v2
	v_exp_f32_e32 v1, v1
	v_cvt_i32_f32_e32 v2, v3
	v_cmp_nlt_f32_e32 vcc, s50, v0
	v_fma_f32 v35, v33, s23, -v34
	v_rndne_f32_e32 v36, v34
	v_ldexp_f32 v1, v1, v2
	v_cndmask_b32_e32 v1, 0, v1, vcc
	v_cmp_ngt_f32_e32 vcc, s51, v0
	v_fmac_f32_e32 v35, 0xb2a5705f, v33
	v_sub_f32_e32 v34, v34, v36
	v_cndmask_b32_e32 v0, v84, v1, vcc
	v_add_f32_e32 v0, 1.0, v0
	v_div_scale_f32 v1, s[6:7], v0, v0, 1.0
	v_rcp_f32_e32 v2, v1
	v_add_f32_e32 v34, v34, v35
	v_exp_f32_e32 v34, v34
	v_cvt_i32_f32_e32 v35, v36
	v_fma_f32 v3, -v1, v2, 1.0
	v_fmac_f32_e32 v2, v3, v2
	v_div_scale_f32 v3, vcc, 1.0, v0, 1.0
	v_mul_f32_e32 v4, v3, v2
	v_fma_f32 v5, -v1, v4, v3
	v_fmac_f32_e32 v4, v5, v2
	v_fma_f32 v1, -v1, v4, v3
	v_div_fmas_f32 v1, v1, v2, v4
	v_div_fixup_f32 v32, v1, v0, 1.0
	global_load_dwordx4 v[0:3], v83, s[18:19] offset:48
	global_load_dwordx4 v[4:7], v83, s[18:19] offset:32
	global_load_dwordx4 v[8:11], v83, s[18:19] offset:16
	global_load_dwordx4 v[12:15], v83, s[18:19]
	v_ldexp_f32 v34, v34, v35
	v_cmp_nlt_f32_e32 vcc, s50, v33
	s_waitcnt vmcnt(0)
	v_add_f32_e32 v12, v32, v12
	v_cndmask_b32_e32 v34, 0, v34, vcc
	v_cmp_ngt_f32_e32 vcc, s51, v33
	v_cmp_lt_f32_e64 s[8:9], s52, v12
	s_nop 0
	v_cndmask_b32_e32 v33, v84, v34, vcc
	v_add_f32_e32 v33, 1.0, v33
	v_div_scale_f32 v34, s[6:7], v33, v33, 1.0
	v_rcp_f32_e32 v35, v34
	s_nop 0
	v_fma_f32 v36, -v34, v35, 1.0
	v_fmac_f32_e32 v35, v36, v35
	v_div_scale_f32 v36, vcc, 1.0, v33, 1.0
	v_mul_f32_e32 v37, v36, v35
	v_fma_f32 v38, -v34, v37, v36
	v_fmac_f32_e32 v37, v38, v35
	v_fma_f32 v34, -v34, v37, v36
	v_div_fmas_f32 v34, v34, v35, v37
	v_div_fixup_f32 v33, v34, v33, 1.0
	v_add_f32_e32 v34, v33, v13
	v_max_f32_e32 v35, 0xf149f2ca, v12
	v_cmp_gt_f32_e32 vcc, v34, v35
	v_cmp_ngt_f32_e64 s[6:7], v34, v35
	v_mov_b32_e32 v37, v34
	v_mov_b32_e32 v12, v35
	s_cbranch_vccnz .LBB0_5014
	v_cmp_nlt_f32_e32 vcc, s52, v34
	v_mov_b32_e32 v12, 0xf149f2ca
	s_cbranch_vccnz .LBB0_5013
	v_mov_b32_e32 v12, v34

.Lpf_skip_1:
	v_lshlrev_b32_e32 v90, 16, v88
	v_and_b32_e32 v91, 0xffff0000, v88
	v_sub_f32_e32 v90, v86, v90
	v_sub_f32_e32 v91, v87, v91
	v_cvt_pk_bf16_f32 v89, v84, v85
	v_cvt_pk_bf16_f32 v90, v90, v91
	v_lshlrev_b32_e32 v128, 4, v128
	v_lshlrev_b32_e32 v91, 16, v89
	v_sub_f32_e32 v91, v84, v91
	v_and_b32_e32 v129, 0xffff0000, v89
	v_add3_u32 v128, s46, v128, v228
	v_sub_f32_e32 v129, v85, v129
	v_cvt_pk_bf16_f32 v91, v91, v129
	ds_write_b64 v128, v[88:89]
	v_add_u32_e32 v88, 0x10000, v128
	ds_write_b64 v88, v[90:91]
	s_nop 0
	v_cvt_pk_fp8_f32 v90, v154, v155
	s_nop 0
	v_cvt_pk_fp8_f32 v91, v174, v175
	v_lshl_add_u64 v[88:89], s[6:7], 0, v[78:79]
	v_cvt_pk_fp8_f32 v90, v152, v153 op_sel:[0,0,1]
	s_nop 0
	v_cvt_pk_fp8_f32 v91, v170, v171 op_sel:[0,0,1]
	v_cvt_pk_fp8_f32 v128, v186, v187
	global_store_dword v[88:89], v90, off
	v_lshl_add_u64 v[88:89], s[6:7], 0, v[76:77]
	s_nop 0
	global_store_dword v[88:89], v91, off
	v_cvt_pk_fp8_f32 v90, v158, v159
	s_nop 0
	v_cvt_pk_fp8_f32 v91, v178, v179
	v_cvt_pk_fp8_f32 v128, v184, v185 op_sel:[0,0,1]
	v_cvt_pk_fp8_f32 v90, v156, v157 op_sel:[0,0,1]
	v_lshl_add_u64 v[88:89], s[6:7], 0, v[74:75]
	v_cvt_pk_fp8_f32 v91, v176, v177 op_sel:[0,0,1]
	global_store_dword v[88:89], v128, off
	v_lshl_add_u64 v[88:89], s[6:7], 0, v[72:73]
	s_nop 0
	global_store_dword v[88:89], v90, off
	v_lshl_add_u64 v[88:89], s[6:7], 0, v[70:71]
	v_cvt_pk_fp8_f32 v128, v134, v135
	global_store_dword v[88:89], v91, off
	s_nop 0
	v_cvt_pk_fp8_f32 v88, v144, v145
	s_nop 0
	v_cvt_pk_fp8_f32 v89, v80, v81
	v_cvt_pk_fp8_f32 v128, v130, v131 op_sel:[0,0,1]
	v_cvt_pk_fp8_f32 v88, v242, v243 op_sel:[0,0,1]
	v_lshl_add_u64 v[80:81], s[6:7], 0, v[68:69]
	v_cvt_pk_fp8_f32 v89, v82, v83 op_sel:[0,0,1]
	global_store_dword v[80:81], v128, off
	v_lshl_add_u64 v[80:81], s[6:7], 0, v[66:67]
	global_store_dword v[80:81], v88, off
	v_lshl_add_u64 v[80:81], s[6:7], 0, v[64:65]
	global_store_dword v[80:81], v89, off
	s_nop 0
	s_nop 0
	v_cvt_pk_fp8_f32 v80, v146, v147
	v_cvt_pk_fp8_f32 v81, v164, v165
	s_add_i32 s6, s1, s18
	s_ashr_i32 s7, s6, 31
	s_lshl_b64 s[6:7], s[6:7], 11
	v_cvt_pk_fp8_f32 v80, v142, v143 op_sel:[0,0,1]
	v_cvt_pk_fp8_f32 v81, v162, v163 op_sel:[0,0,1]
	s_add_u32 s6, s41, s6
	s_addc_u32 s7, s42, s7
	v_lshl_add_u64 v[78:79], s[6:7], 0, v[78:79]
	v_lshl_add_u64 v[76:77], s[6:7], 0, v[76:77]
	s_nop 0
	global_store_dword v[78:79], v80, off
	global_store_dword v[76:77], v81, off
	s_nop 0
	s_nop 0
	v_cvt_pk_fp8_f32 v82, v182, v183
	v_cvt_pk_fp8_f32 v76, v150, v151
	v_cvt_pk_fp8_f32 v77, v172, v173
	v_lshl_add_u64 v[74:75], s[6:7], 0, v[74:75]
	v_cvt_pk_fp8_f32 v82, v180, v181 op_sel:[0,0,1]
	v_cvt_pk_fp8_f32 v76, v148, v149 op_sel:[0,0,1]
	v_cvt_pk_fp8_f32 v77, v168, v169 op_sel:[0,0,1]
	v_lshl_add_u64 v[72:73], s[6:7], 0, v[72:73]
	v_lshl_add_u64 v[70:71], s[6:7], 0, v[70:71]
	global_store_dword v[74:75], v82, off
	s_nop 0
	global_store_dword v[72:73], v76, off
	global_store_dword v[70:71], v77, off
	s_nop 0
	s_nop 0
	v_cvt_pk_fp8_f32 v74, v94, v95
	v_cvt_pk_fp8_f32 v70, v138, v139
	v_cvt_pk_fp8_f32 v71, v86, v87
	v_lshl_add_u64 v[68:69], s[6:7], 0, v[68:69]
	v_cvt_pk_fp8_f32 v74, v92, v93 op_sel:[0,0,1]
	v_cvt_pk_fp8_f32 v70, v136, v137 op_sel:[0,0,1]
	v_cvt_pk_fp8_f32 v71, v84, v85 op_sel:[0,0,1]
	v_lshl_add_u64 v[66:67], s[6:7], 0, v[66:67]
	v_lshl_add_u64 v[64:65], s[6:7], 0, v[64:65]
	global_store_dword v[68:69], v74, off
	global_store_dword v[66:67], v70, off
	global_store_dword v[64:65], v71, off
	s_waitcnt lgkmcnt(0)
	s_barrier
	ds_read_b128 v[64:67], v190
	ds_read_b128 v[68:71], v191
	s_waitcnt lgkmcnt(1)
	v_mfma_f32_16x16x32_bf16 v[72:75], v[0:3], v[64:67], 0
	v_mov_b32_e32 v128, v167
	v_mfma_f32_16x16x32_bf16 v[64:67], v[4:7], v[64:67], v[72:75]
	s_waitcnt lgkmcnt(0)
	v_mfma_f32_16x16x32_bf16 v[64:67], v[0:3], v[68:71], v[64:67]
	ds_read_b128 v[68:71], v192
	s_nop 2
	ds_read_b128 v[72:75], v193
	s_waitcnt lgkmcnt(1)
	v_mfma_f32_16x16x32_bf16 v[64:67], v[8:11], v[68:71], v[64:67]
	v_mfma_f32_16x16x32_bf16 v[64:67], v[12:15], v[68:71], v[64:67]
	s_waitcnt lgkmcnt(0)
	v_mfma_f32_16x16x32_bf16 v[64:67], v[8:11], v[72:75], v[64:67]
	ds_read_b128 v[68:71], v194
	ds_read_b128 v[72:75], v195
	s_waitcnt lgkmcnt(1)
	v_mfma_f32_16x16x32_bf16 v[64:67], v[16:19], v[68:71], v[64:67]
	v_mfma_f32_16x16x32_bf16 v[64:67], v[20:23], v[68:71], v[64:67]
	s_waitcnt lgkmcnt(0)
	v_mfma_f32_16x16x32_bf16 v[64:67], v[16:19], v[72:75], v[64:67]
	ds_read_b128 v[68:71], v196
	ds_read_b128 v[72:75], v197
	s_waitcnt lgkmcnt(1)
	v_mfma_f32_16x16x32_bf16 v[64:67], v[24:27], v[68:71], v[64:67]
	v_mfma_f32_16x16x32_bf16 v[64:67], v[28:31], v[68:71], v[64:67]
	s_waitcnt lgkmcnt(0)
	v_mfma_f32_16x16x32_bf16 v[64:67], v[24:27], v[72:75], v[64:67]
	ds_read_b128 v[68:71], v198
	ds_read_b128 v[72:75], v199
	s_waitcnt lgkmcnt(1)
	v_mfma_f32_16x16x32_bf16 v[64:67], v[32:35], v[68:71], v[64:67]
	v_mfma_f32_16x16x32_bf16 v[64:67], v[36:39], v[68:71], v[64:67]
	s_waitcnt lgkmcnt(0)
	v_mfma_f32_16x16x32_bf16 v[64:67], v[32:35], v[72:75], v[64:67]
	ds_read_b128 v[68:71], v200
	ds_read_b128 v[72:75], v201
	s_waitcnt lgkmcnt(1)
	v_mfma_f32_16x16x32_bf16 v[64:67], v[40:43], v[68:71], v[64:67]
	v_mfma_f32_16x16x32_bf16 v[64:67], v[44:47], v[68:71], v[64:67]
	s_waitcnt lgkmcnt(0)
	v_mfma_f32_16x16x32_bf16 v[64:67], v[40:43], v[72:75], v[64:67]
	ds_read_b128 v[68:71], v202
	ds_read_b128 v[72:75], v203
	s_waitcnt lgkmcnt(1)
	v_mfma_f32_16x16x32_bf16 v[64:67], v[48:51], v[68:71], v[64:67]
	v_mfma_f32_16x16x32_bf16 v[64:67], v[52:55], v[68:71], v[64:67]
	s_waitcnt lgkmcnt(0)
	v_mfma_f32_16x16x32_bf16 v[64:67], v[48:51], v[72:75], v[64:67]
	ds_read_b128 v[68:71], v204
	ds_read_b128 v[72:75], v205
	s_waitcnt lgkmcnt(1)
	v_mfma_f32_16x16x32_bf16 v[64:67], v[56:59], v[68:71], v[64:67]
	v_mfma_f32_16x16x32_bf16 v[64:67], v[60:63], v[68:71], v[64:67]
	s_waitcnt lgkmcnt(0)
	v_mfma_f32_16x16x32_bf16 v[64:67], v[56:59], v[72:75], v[64:67]
	s_nop 7
	ds_write_b128 v208, v[64:67]
	s_waitcnt lgkmcnt(0)
	s_barrier
	s_nop 0
	v_cmp_gt_i32_e32 vcc, s48, v128
	s_and_saveexec_b64 s[6:7], vcc
	s_cbranch_execz .LBB0_5172
	v_lshl_add_u32 v72, v128, 2, 0
	v_add_u32_e32 v70, 0x22000, v72
	ds_read2st64_b32 v[64:65], v70 offset1:4
	ds_read2st64_b32 v[66:67], v70 offset0:8 offset1:12
	ds_read2st64_b32 v[68:69], v70 offset0:16 offset1:20
	ds_read2st64_b32 v[70:71], v70 offset0:24 offset1:28
	s_waitcnt lgkmcnt(3)
	v_add_f32_e32 v64, 0, v64
	v_add_f32_e32 v64, v64, v65
	s_waitcnt lgkmcnt(2)
	v_add_f32_e32 v64, v64, v66
	v_add_f32_e32 v64, v64, v67
	s_waitcnt lgkmcnt(1)
	v_add_f32_e32 v64, v64, v68
	v_add_f32_e32 v64, v64, v69
	s_waitcnt lgkmcnt(0)
	v_add_f32_e32 v64, v64, v70
	v_add_f32_e32 v64, v64, v71
	v_add_u32_e32 v65, 0x21000, v72
	ds_write_b32 v65, v64
	v_mul_f32_e32 v142, 0xbfb8aa3b, v64
	v_fma_f32 v143, v64, s50, -v142
	v_rndne_f32_e32 v144, v142
	v_fmac_f32_e32 v143, 0xb2a5705f, v64
	v_sub_f32_e32 v142, v142, v144
	v_add_f32_e32 v142, v142, v143
	v_cvt_i32_f32_e32 v145, v144
	v_exp_f32_e32 v146, v142
	v_cmp_nlt_f32_e32 vcc, s51, v64
	v_ldexp_f32 v145, v146, v145
	s_nop 0
	v_cndmask_b32_e32 v145, 0, v145, vcc
	v_cmp_ngt_f32_e32 vcc, s52, v64
	s_nop 1
	v_cndmask_b32_e32 v145, v211, v145, vcc
	v_add_f32_e32 v145, 1.0, v145
	v_div_scale_f32 v146, s[98:99], v145, v145, 1.0
	v_rcp_f32_e32 v147, v146
	v_div_scale_f32 v148, vcc, 1.0, v145, 1.0
	v_fma_f32 v149, -v146, v147, 1.0
	v_fmac_f32_e32 v147, v149, v147
	v_mul_f32_e32 v149, v148, v147
	v_fma_f32 v150, -v146, v149, v148
	v_fmac_f32_e32 v149, v150, v147
	v_fma_f32 v146, -v146, v149, v148
	v_div_fmas_f32 v146, v146, v147, v149
	v_div_fixup_f32 v146, v146, v145, 1.0
	ds_write_b32 v65, v146 offset:1024

.LBB0_5513:
	s_waitcnt vmcnt(31)
	v_mov_b32_e32 v128, v0
	s_waitcnt vmcnt(30)
	v_mov_b32_e32 v129, v4
	v_pk_mul_f32 v[128:129], v[128:129], s[40:41] op_sel_hi:[1,0]
	s_nop 0
	v_cvt_pk_fp8_f32 v130, v128, v129
	s_waitcnt vmcnt(29)
	v_mov_b32_e32 v128, v8
	s_waitcnt vmcnt(28)
	v_mov_b32_e32 v129, v12
	v_pk_mul_f32 v[128:129], v[128:129], s[40:41] op_sel_hi:[1,0]
	s_nop 0
	v_cvt_pk_fp8_f32 v130, v128, v129 op_sel:[0,0,1]
	v_mov_b32_e32 v128, v1
	v_mov_b32_e32 v129, v5
	v_pk_mul_f32 v[128:129], v[128:129], s[40:41] op_sel_hi:[1,0]
	s_nop 0
	v_cvt_pk_fp8_f32 v131, v128, v129
	v_mov_b32_e32 v128, v9
	v_mov_b32_e32 v129, v13
	v_pk_mul_f32 v[128:129], v[128:129], s[40:41] op_sel_hi:[1,0]
	s_nop 0
	v_cvt_pk_fp8_f32 v131, v128, v129 op_sel:[0,0,1]
	v_mov_b32_e32 v128, v2
	v_mov_b32_e32 v129, v6
	v_pk_mul_f32 v[128:129], v[128:129], s[40:41] op_sel_hi:[1,0]
	v_mov_b32_e32 v139, v135
	v_cvt_pk_fp8_f32 v134, v128, v129
	v_mov_b32_e32 v128, v10
	v_mov_b32_e32 v129, v14
	v_pk_mul_f32 v[128:129], v[128:129], s[40:41] op_sel_hi:[1,0]
	v_mov_b32_e32 v146, v135
	v_cvt_pk_fp8_f32 v134, v128, v129 op_sel:[0,0,1]
	v_mov_b32_e32 v128, v3
	v_mov_b32_e32 v129, v7
	v_pk_mul_f32 v[128:129], v[128:129], s[40:41] op_sel_hi:[1,0]
	v_add_u32_e32 v145, 0x4000, v143
	v_cvt_pk_fp8_f32 v138, v128, v129
	v_mov_b32_e32 v128, v11
	v_mov_b32_e32 v129, v15
	v_pk_mul_f32 v[128:129], v[128:129], s[40:41] op_sel_hi:[1,0]
	v_add_u32_e32 v144, 0x8400, v143
	v_cvt_pk_fp8_f32 v138, v128, v129 op_sel:[0,0,1]
	s_waitcnt vmcnt(27)
	v_mov_b32_e32 v128, v16
	s_waitcnt vmcnt(26)
	v_mov_b32_e32 v129, v20
	ds_write2_b32 v143, v130, v131 offset1:33
	ds_write2_b32 v143, v134, v138 offset0:66 offset1:99
	v_pk_mul_f32 v[128:129], v[128:129], s[40:41] op_sel_hi:[1,0]
	s_nop 0
	v_cvt_pk_fp8_f32 v130, v128, v129
	s_waitcnt vmcnt(25)
	v_mov_b32_e32 v128, v24
	s_waitcnt vmcnt(24)
	v_mov_b32_e32 v129, v28
	v_pk_mul_f32 v[128:129], v[128:129], s[40:41] op_sel_hi:[1,0]
	s_nop 0
	v_cvt_pk_fp8_f32 v130, v128, v129 op_sel:[0,0,1]
	v_mov_b32_e32 v128, v17
	v_mov_b32_e32 v129, v21
	v_pk_mul_f32 v[128:129], v[128:129], s[40:41] op_sel_hi:[1,0]
	s_nop 0
	v_cvt_pk_fp8_f32 v131, v128, v129
	v_mov_b32_e32 v128, v25
	v_mov_b32_e32 v129, v29
	v_pk_mul_f32 v[128:129], v[128:129], s[40:41] op_sel_hi:[1,0]
	s_nop 0
	v_cvt_pk_fp8_f32 v131, v128, v129 op_sel:[0,0,1]
	v_mov_b32_e32 v128, v18
	v_mov_b32_e32 v129, v22
	v_pk_mul_f32 v[128:129], v[128:129], s[40:41] op_sel_hi:[1,0]
	v_mov_b32_e32 v147, v135
	v_cvt_pk_fp8_f32 v134, v128, v129
	v_mov_b32_e32 v128, v26
	v_mov_b32_e32 v129, v30
	v_pk_mul_f32 v[128:129], v[128:129], s[40:41] op_sel_hi:[1,0]
	s_cmp_lt_i32 s73, 2
	v_cvt_pk_fp8_f32 v134, v128, v129 op_sel:[0,0,1]
	v_mov_b32_e32 v128, v19
	v_mov_b32_e32 v129, v23
	v_pk_mul_f32 v[128:129], v[128:129], s[40:41] op_sel_hi:[1,0]
	s_nop 0
	v_cvt_pk_fp8_f32 v138, v128, v129
	v_mov_b32_e32 v128, v27
	v_mov_b32_e32 v129, v31
	v_pk_mul_f32 v[128:129], v[128:129], s[40:41] op_sel_hi:[1,0]
	s_nop 0
	v_cvt_pk_fp8_f32 v138, v128, v129 op_sel:[0,0,1]
	s_waitcnt vmcnt(23)
	v_mov_b32_e32 v128, v48
	s_waitcnt vmcnt(22)
	v_mov_b32_e32 v129, v52
	v_pk_mul_f32 v[128:129], v[128:129], s[40:41] op_sel_hi:[1,0]
	ds_write2_b32 v145, v130, v131 offset0:128 offset1:161
	ds_write2_b32 v145, v134, v138 offset0:194 offset1:227
	v_cvt_pk_fp8_f32 v139, v128, v129
	s_waitcnt vmcnt(21)
	v_mov_b32_e32 v128, v56
	s_waitcnt vmcnt(20)
	v_mov_b32_e32 v129, v60
	v_pk_mul_f32 v[128:129], v[128:129], s[40:41] op_sel_hi:[1,0]
	s_nop 0
	v_cvt_pk_fp8_f32 v139, v128, v129 op_sel:[0,0,1]
	v_mov_b32_e32 v128, v49
	v_mov_b32_e32 v129, v53
	v_pk_mul_f32 v[128:129], v[128:129], s[40:41] op_sel_hi:[1,0]
	s_nop 0
	v_cvt_pk_fp8_f32 v146, v128, v129
	v_mov_b32_e32 v128, v57
	v_mov_b32_e32 v129, v61
	v_pk_mul_f32 v[128:129], v[128:129], s[40:41] op_sel_hi:[1,0]
	s_nop 0
	v_cvt_pk_fp8_f32 v146, v128, v129 op_sel:[0,0,1]
	v_mov_b32_e32 v128, v50
	v_mov_b32_e32 v129, v54
	v_pk_mul_f32 v[128:129], v[128:129], s[40:41] op_sel_hi:[1,0]
	s_nop 0
	v_cvt_pk_fp8_f32 v130, v128, v129
	v_mov_b32_e32 v128, v58
	v_mov_b32_e32 v129, v62
	v_pk_mul_f32 v[128:129], v[128:129], s[40:41] op_sel_hi:[1,0]
	ds_write2_b32 v144, v139, v146 offset1:33
	v_cvt_pk_fp8_f32 v130, v128, v129 op_sel:[0,0,1]
	v_mov_b32_e32 v128, v51
	v_mov_b32_e32 v129, v55
	v_pk_mul_f32 v[128:129], v[128:129], s[40:41] op_sel_hi:[1,0]
	s_nop 0
	v_cvt_pk_fp8_f32 v131, v128, v129
	v_mov_b32_e32 v128, v59
	v_mov_b32_e32 v129, v63
	v_pk_mul_f32 v[128:129], v[128:129], s[40:41] op_sel_hi:[1,0]
	v_add_u32_e32 v146, 0xc400, v143
	v_cvt_pk_fp8_f32 v131, v128, v129 op_sel:[0,0,1]
	s_waitcnt vmcnt(19)
	v_mov_b32_e32 v128, v96
	s_waitcnt vmcnt(18)
	v_mov_b32_e32 v129, v100
	v_pk_mul_f32 v[128:129], v[128:129], s[40:41] op_sel_hi:[1,0]
	ds_write2_b32 v144, v130, v131 offset0:66 offset1:99
	v_cvt_pk_fp8_f32 v134, v128, v129
	s_waitcnt vmcnt(17)
	v_mov_b32_e32 v128, v104
	s_waitcnt vmcnt(16)
	v_mov_b32_e32 v129, v108
	v_pk_mul_f32 v[128:129], v[128:129], s[40:41] op_sel_hi:[1,0]
	s_nop 0
	v_cvt_pk_fp8_f32 v134, v128, v129 op_sel:[0,0,1]
	v_mov_b32_e32 v128, v97
	v_mov_b32_e32 v129, v101
	v_pk_mul_f32 v[128:129], v[128:129], s[40:41] op_sel_hi:[1,0]
	s_nop 0
	v_cvt_pk_fp8_f32 v138, v128, v129
	v_mov_b32_e32 v128, v105
	v_mov_b32_e32 v129, v109
	v_pk_mul_f32 v[128:129], v[128:129], s[40:41] op_sel_hi:[1,0]
	s_nop 0
	v_cvt_pk_fp8_f32 v138, v128, v129 op_sel:[0,0,1]
	v_mov_b32_e32 v128, v98
	v_mov_b32_e32 v129, v102
	v_pk_mul_f32 v[128:129], v[128:129], s[40:41] op_sel_hi:[1,0]
	s_nop 0
	v_cvt_pk_fp8_f32 v139, v128, v129
	v_mov_b32_e32 v128, v106
	v_mov_b32_e32 v129, v110
	v_pk_mul_f32 v[128:129], v[128:129], s[40:41] op_sel_hi:[1,0]
	s_nop 0
	v_cvt_pk_fp8_f32 v139, v128, v129 op_sel:[0,0,1]
	v_mov_b32_e32 v128, v99
	v_mov_b32_e32 v129, v103
	v_pk_mul_f32 v[128:129], v[128:129], s[40:41] op_sel_hi:[1,0]
	s_nop 0
	v_cvt_pk_fp8_f32 v147, v128, v129
	v_mov_b32_e32 v128, v107
	v_mov_b32_e32 v129, v111
	v_pk_mul_f32 v[128:129], v[128:129], s[40:41] op_sel_hi:[1,0]
	s_nop 0
	v_cvt_pk_fp8_f32 v147, v128, v129 op_sel:[0,0,1]
	ds_write2_b32 v146, v134, v138 offset0:128 offset1:161
	ds_write2_b32 v146, v139, v147 offset0:194 offset1:227
	s_waitcnt lgkmcnt(0)
	s_barrier
	ds_read2_b32 v[128:129], v142 offset1:1
	ds_read2_b32 v[130:131], v142 offset0:2 offset1:3
	v_lshl_add_u32 v134, s72, 6, v140
	s_cbranch_scc1 .LBB0_5519
	s_cmp_gt_i32 s73, 2
	s_cbranch_scc0 .LBB0_5520
	s_cmp_eq_u32 s73, 3
	s_mov_b64 s[68:69], -1
	s_cbranch_scc0 .LBB0_5517
	v_lshlrev_b32_e32 v138, 1, v134
	v_and_b32_e32 v139, 0x7f, v134
	s_movk_i32 s19, 0xff00
	v_and_or_b32 v138, v138, s19, v139
	s_mov_b64 s[68:69], 0

.Lcvw_c6:
	v_mov_b32_e32 v128, v36
	v_mov_b32_e32 v129, v32
	v_pk_mul_f32 v[128:129], v[128:129], s[40:41] op_sel_hi:[1,0]
	s_nop 0
	v_cvt_pk_fp8_f32 v130, v128, v129
	v_mov_b32_e32 v128, v44
	v_mov_b32_e32 v129, v40
	v_pk_mul_f32 v[128:129], v[128:129], s[40:41] op_sel_hi:[1,0]
	s_nop 0
	v_cvt_pk_fp8_f32 v130, v128, v129 op_sel:[0,0,1]
	v_mov_b32_e32 v128, v37
	v_mov_b32_e32 v129, v33
	v_pk_mul_f32 v[128:129], v[128:129], s[40:41] op_sel_hi:[1,0]
	s_nop 0
	v_cvt_pk_fp8_f32 v131, v128, v129
	v_mov_b32_e32 v128, v45
	v_mov_b32_e32 v129, v41
	v_pk_mul_f32 v[128:129], v[128:129], s[40:41] op_sel_hi:[1,0]
	s_nop 0
	v_cvt_pk_fp8_f32 v131, v128, v129 op_sel:[0,0,1]
	v_mov_b32_e32 v128, v38
	v_mov_b32_e32 v129, v34
	v_pk_mul_f32 v[128:129], v[128:129], s[40:41] op_sel_hi:[1,0]
	s_nop 0
	v_cvt_pk_fp8_f32 v134, v128, v129
	v_mov_b32_e32 v128, v46
	v_mov_b32_e32 v129, v42
	v_pk_mul_f32 v[128:129], v[128:129], s[40:41] op_sel_hi:[1,0]
	s_nop 0
	v_cvt_pk_fp8_f32 v134, v128, v129 op_sel:[0,0,1]
	v_mov_b32_e32 v128, v39
	v_mov_b32_e32 v129, v35
	v_pk_mul_f32 v[128:129], v[128:129], s[40:41] op_sel_hi:[1,0]
	s_nop 0
	v_cvt_pk_fp8_f32 v138, v128, v129
	v_mov_b32_e32 v128, v47
	v_mov_b32_e32 v129, v43
	v_pk_mul_f32 v[128:129], v[128:129], s[40:41] op_sel_hi:[1,0]
	s_nop 0
	v_cvt_pk_fp8_f32 v138, v128, v129 op_sel:[0,0,1]
	v_mov_b32_e32 v128, v68
	v_mov_b32_e32 v129, v64
	v_pk_mul_f32 v[128:129], v[128:129], s[40:41] op_sel_hi:[1,0]
	s_cmp_lt_i32 s37, 2
	v_cvt_pk_fp8_f32 v139, v128, v129
	v_mov_b32_e32 v128, v76
	v_mov_b32_e32 v129, v72
	v_pk_mul_f32 v[128:129], v[128:129], s[40:41] op_sel_hi:[1,0]
	s_nop 0
	v_cvt_pk_fp8_f32 v139, v128, v129 op_sel:[0,0,1]
	v_mov_b32_e32 v128, v69
	v_mov_b32_e32 v129, v65
	v_pk_mul_f32 v[128:129], v[128:129], s[40:41] op_sel_hi:[1,0]
	s_nop 0
	v_cvt_pk_fp8_f32 v153, v128, v129
	v_mov_b32_e32 v128, v77
	v_mov_b32_e32 v129, v73
	v_pk_mul_f32 v[128:129], v[128:129], s[40:41] op_sel_hi:[1,0]
	s_nop 0
	v_cvt_pk_fp8_f32 v153, v128, v129 op_sel:[0,0,1]
	v_mov_b32_e32 v128, v70
	v_mov_b32_e32 v129, v66
	v_pk_mul_f32 v[128:129], v[128:129], s[40:41] op_sel_hi:[1,0]
	s_nop 0
	v_cvt_pk_fp8_f32 v154, v128, v129
	v_mov_b32_e32 v128, v78
	v_mov_b32_e32 v129, v74
	v_pk_mul_f32 v[128:129], v[128:129], s[40:41] op_sel_hi:[1,0]
	s_nop 0
	v_cvt_pk_fp8_f32 v154, v128, v129 op_sel:[0,0,1]
	v_mov_b32_e32 v128, v71
	v_mov_b32_e32 v129, v67
	v_pk_mul_f32 v[128:129], v[128:129], s[40:41] op_sel_hi:[1,0]
	s_nop 0
	v_cvt_pk_fp8_f32 v155, v128, v129
	v_mov_b32_e32 v128, v79
	v_mov_b32_e32 v129, v75
	v_pk_mul_f32 v[128:129], v[128:129], s[40:41] op_sel_hi:[1,0]
	s_nop 0
	v_cvt_pk_fp8_f32 v155, v128, v129 op_sel:[0,0,1]
	v_mov_b32_e32 v128, v84
	v_mov_b32_e32 v129, v80
	ds_write2_b32 v143, v130, v131 offset1:33
	ds_write2_b32 v143, v134, v138 offset0:66 offset1:99
	ds_write2_b32 v145, v139, v153 offset0:128 offset1:161
	ds_write2_b32 v145, v154, v155 offset0:194 offset1:227
	v_pk_mul_f32 v[128:129], v[128:129], s[40:41] op_sel_hi:[1,0]
	s_nop 0
	v_cvt_pk_fp8_f32 v130, v128, v129
	v_mov_b32_e32 v128, v92
	v_mov_b32_e32 v129, v88
	v_pk_mul_f32 v[128:129], v[128:129], s[40:41] op_sel_hi:[1,0]
	s_nop 0
	v_cvt_pk_fp8_f32 v130, v128, v129 op_sel:[0,0,1]
	v_mov_b32_e32 v128, v85
	v_mov_b32_e32 v129, v81
	v_pk_mul_f32 v[128:129], v[128:129], s[40:41] op_sel_hi:[1,0]
	s_nop 0
	v_cvt_pk_fp8_f32 v131, v128, v129
	v_mov_b32_e32 v128, v93
	v_mov_b32_e32 v129, v89
	v_pk_mul_f32 v[128:129], v[128:129], s[40:41] op_sel_hi:[1,0]
	s_nop 0
	v_cvt_pk_fp8_f32 v131, v128, v129 op_sel:[0,0,1]
	v_mov_b32_e32 v128, v86
	v_mov_b32_e32 v129, v82
	v_pk_mul_f32 v[128:129], v[128:129], s[40:41] op_sel_hi:[1,0]
	s_nop 0
	v_cvt_pk_fp8_f32 v134, v128, v129
	v_mov_b32_e32 v128, v94
	v_mov_b32_e32 v129, v90
	v_pk_mul_f32 v[128:129], v[128:129], s[40:41] op_sel_hi:[1,0]
	s_nop 0
	v_cvt_pk_fp8_f32 v134, v128, v129 op_sel:[0,0,1]
	v_mov_b32_e32 v128, v87
	v_mov_b32_e32 v129, v83
	v_pk_mul_f32 v[128:129], v[128:129], s[40:41] op_sel_hi:[1,0]
	s_nop 0
	v_cvt_pk_fp8_f32 v138, v128, v129
	v_mov_b32_e32 v128, v95
	v_mov_b32_e32 v129, v91
	v_pk_mul_f32 v[128:129], v[128:129], s[40:41] op_sel_hi:[1,0]
	s_nop 0
	v_cvt_pk_fp8_f32 v138, v128, v129 op_sel:[0,0,1]
	v_mov_b32_e32 v128, v116
	v_mov_b32_e32 v129, v112
	v_pk_mul_f32 v[128:129], v[128:129], s[40:41] op_sel_hi:[1,0]
	s_nop 0
	v_cvt_pk_fp8_f32 v139, v128, v129
	v_mov_b32_e32 v128, v124
	v_mov_b32_e32 v129, v120
	v_pk_mul_f32 v[128:129], v[128:129], s[40:41] op_sel_hi:[1,0]
	s_nop 0
	v_cvt_pk_fp8_f32 v139, v128, v129 op_sel:[0,0,1]
	v_mov_b32_e32 v128, v117
	v_mov_b32_e32 v129, v113
	v_pk_mul_f32 v[128:129], v[128:129], s[40:41] op_sel_hi:[1,0]
	s_nop 0
	v_cvt_pk_fp8_f32 v145, v128, v129
	v_mov_b32_e32 v128, v125
	v_mov_b32_e32 v129, v121
	v_pk_mul_f32 v[128:129], v[128:129], s[40:41] op_sel_hi:[1,0]
	s_nop 0
	v_cvt_pk_fp8_f32 v145, v128, v129 op_sel:[0,0,1]
	v_mov_b32_e32 v128, v118
	v_mov_b32_e32 v129, v114
	v_pk_mul_f32 v[128:129], v[128:129], s[40:41] op_sel_hi:[1,0]
	s_nop 0
	v_cvt_pk_fp8_f32 v153, v128, v129
	v_mov_b32_e32 v128, v126
	v_mov_b32_e32 v129, v122
	v_pk_mul_f32 v[128:129], v[128:129], s[40:41] op_sel_hi:[1,0]
	s_nop 0
	v_cvt_pk_fp8_f32 v153, v128, v129 op_sel:[0,0,1]
	v_mov_b32_e32 v128, v119
	v_mov_b32_e32 v129, v115
	v_pk_mul_f32 v[128:129], v[128:129], s[40:41] op_sel_hi:[1,0]
	s_nop 0
	v_cvt_pk_fp8_f32 v154, v128, v129
	v_mov_b32_e32 v128, v127
	v_mov_b32_e32 v129, v123
	v_pk_mul_f32 v[128:129], v[128:129], s[40:41] op_sel_hi:[1,0]
	s_nop 0
	v_cvt_pk_fp8_f32 v154, v128, v129 op_sel:[0,0,1]
	ds_write2_b32 v144, v130, v131 offset1:33
	ds_write2_b32 v144, v134, v138 offset0:66 offset1:99
	ds_write2_b32 v146, v139, v145 offset0:128 offset1:161
	ds_write2_b32 v146, v153, v154 offset0:194 offset1:227
	s_waitcnt lgkmcnt(0)
	s_barrier
	ds_read2_b32 v[128:129], v142 offset1:1
	ds_read2_b32 v[130:131], v142 offset0:2 offset1:3
	v_lshl_add_u32 v134, s35, 6, v140
	s_cbranch_scc1 .LBB0_5662
	s_cmp_gt_i32 s37, 2
	s_cbranch_scc0 .LBB0_5663
	s_cmp_eq_u32 s37, 3
	s_mov_b64 s[68:69], -1
	s_cbranch_scc0 .LBB0_5660
	v_lshlrev_b32_e32 v138, 1, v134
	v_and_b32_e32 v139, 0x7f, v134
	s_movk_i32 s13, 0xff00
	v_and_or_b32 v138, v138, s13, v139
	s_mov_b64 s[68:69], 0

.Lpeel_exit_9:
	v_pk_mul_f32 v[140:141], v[124:125], s[6:7] op_sel_hi:[1,0]
	v_pk_mul_f32 v[120:121], v[120:121], s[6:7] op_sel_hi:[1,0]
	v_mov_b32_e32 v125, v129
	v_cvt_pk_fp8_f32 v125, v120, v121
	v_pk_mul_f32 v[120:121], v[126:127], s[6:7] op_sel_hi:[1,0]
	v_pk_mul_f32 v[116:117], v[116:117], s[6:7] op_sel_hi:[1,0]
	s_nop 0
	v_cvt_pk_fp8_f32 v126, v116, v117
	v_pk_mul_f32 v[112:113], v[112:113], s[6:7] op_sel_hi:[1,0]
	s_nop 0
	v_cvt_pk_fp8_f32 v127, v112, v113
	v_pk_mul_f32 v[112:113], v[118:119], s[6:7] op_sel_hi:[1,0]
	v_pk_mul_f32 v[104:105], v[104:105], s[6:7] op_sel_hi:[1,0]
	v_cvt_pk_fp8_f32 v126, v112, v113 op_sel:[0,0,1]
	v_pk_mul_f32 v[112:113], v[114:115], s[6:7] op_sel_hi:[1,0]
	v_pk_mul_f32 v[100:101], v[100:101], s[6:7] op_sel_hi:[1,0]
	v_cvt_pk_fp8_f32 v127, v112, v113 op_sel:[0,0,1]
	v_pk_mul_f32 v[112:113], v[108:109], s[6:7] op_sel_hi:[1,0]
	v_mov_b32_e32 v109, v129
	v_cvt_pk_fp8_f32 v109, v104, v105
	v_pk_mul_f32 v[104:105], v[110:111], s[6:7] op_sel_hi:[1,0]
	v_mov_b32_e32 v110, v129
	v_cvt_pk_fp8_f32 v110, v100, v101
	v_pk_mul_f32 v[100:101], v[92:93], s[6:7] op_sel_hi:[1,0]
	v_pk_mul_f32 v[88:89], v[88:89], s[6:7] op_sel_hi:[1,0]
	v_mov_b32_e32 v93, v129
	v_cvt_pk_fp8_f32 v93, v88, v89
	v_pk_mul_f32 v[88:89], v[94:95], s[6:7] op_sel_hi:[1,0]
	v_pk_mul_f32 v[84:85], v[84:85], s[6:7] op_sel_hi:[1,0]
	s_nop 0
	v_cvt_pk_fp8_f32 v94, v84, v85
	v_pk_mul_f32 v[80:81], v[80:81], s[6:7] op_sel_hi:[1,0]
	s_nop 0
	v_cvt_pk_fp8_f32 v95, v80, v81
	v_pk_mul_f32 v[80:81], v[86:87], s[6:7] op_sel_hi:[1,0]
	v_pk_mul_f32 v[72:73], v[72:73], s[6:7] op_sel_hi:[1,0]
	v_cvt_pk_fp8_f32 v94, v80, v81 op_sel:[0,0,1]
	v_pk_mul_f32 v[80:81], v[82:83], s[6:7] op_sel_hi:[1,0]
	v_pk_mul_f32 v[68:69], v[68:69], s[6:7] op_sel_hi:[1,0]
	v_cvt_pk_fp8_f32 v95, v80, v81 op_sel:[0,0,1]
	v_pk_mul_f32 v[80:81], v[76:77], s[6:7] op_sel_hi:[1,0]
	v_mov_b32_e32 v77, v129
	v_cvt_pk_fp8_f32 v77, v72, v73
	v_pk_mul_f32 v[72:73], v[78:79], s[6:7] op_sel_hi:[1,0]
	s_nop 0
	v_cvt_pk_fp8_f32 v78, v68, v69
	v_pk_mul_f32 v[64:65], v[64:65], s[6:7] op_sel_hi:[1,0]
	s_nop 0
	v_cvt_pk_fp8_f32 v79, v64, v65
	v_pk_mul_f32 v[64:65], v[70:71], s[6:7] op_sel_hi:[1,0]
	v_pk_mul_f32 v[56:57], v[56:57], s[6:7] op_sel_hi:[1,0]
	v_cvt_pk_fp8_f32 v78, v64, v65 op_sel:[0,0,1]
	v_pk_mul_f32 v[64:65], v[66:67], s[6:7] op_sel_hi:[1,0]
	v_pk_mul_f32 v[52:53], v[52:53], s[6:7] op_sel_hi:[1,0]
	v_cvt_pk_fp8_f32 v79, v64, v65 op_sel:[0,0,1]
	v_pk_mul_f32 v[64:65], v[60:61], s[6:7] op_sel_hi:[1,0]
	v_mov_b32_e32 v61, v129
	v_cvt_pk_fp8_f32 v61, v56, v57
	v_pk_mul_f32 v[56:57], v[62:63], s[6:7] op_sel_hi:[1,0]
	s_nop 0
	v_cvt_pk_fp8_f32 v62, v52, v53
	v_pk_mul_f32 v[48:49], v[48:49], s[6:7] op_sel_hi:[1,0]
	s_nop 0
	v_cvt_pk_fp8_f32 v63, v48, v49
	s_lshl_b32 s14, s49, 8
	v_pk_mul_f32 v[48:49], v[54:55], s[6:7] op_sel_hi:[1,0]
	s_add_i32 s14, s14, s33
	v_cvt_pk_fp8_f32 v62, v48, v49 op_sel:[0,0,1]
	v_pk_mul_f32 v[48:49], v[50:51], s[6:7] op_sel_hi:[1,0]
	s_lshl_b32 s16, s50, 8
	s_ashr_i32 s15, s14, 31
	v_cvt_pk_fp8_f32 v63, v48, v49 op_sel:[0,0,1]
	v_pk_mul_f32 v[48:49], v[44:45], s[6:7] op_sel_hi:[1,0]
	v_pk_mul_f32 v[40:41], v[40:41], s[6:7] op_sel_hi:[1,0]
	v_mov_b32_e32 v45, v129
	s_ashr_i32 s17, s16, 31
	s_lshl_b64 s[18:19], s[14:15], 11
	v_cvt_pk_fp8_f32 v45, v40, v41
	v_pk_mul_f32 v[40:41], v[46:47], s[6:7] op_sel_hi:[1,0]
	v_pk_mul_f32 v[36:37], v[36:37], s[6:7] op_sel_hi:[1,0]
	v_mov_b32_e32 v46, v129
	s_add_u32 s15, s30, s18
	v_cvt_pk_fp8_f32 v46, v36, v37
	v_pk_mul_f32 v[36:37], v[28:29], s[6:7] op_sel_hi:[1,0]
	v_pk_mul_f32 v[24:25], v[24:25], s[6:7] op_sel_hi:[1,0]
	v_mov_b32_e32 v29, v129
	s_addc_u32 s18, s31, s19
	v_cvt_pk_fp8_f32 v29, v24, v25
	v_pk_mul_f32 v[24:25], v[30:31], s[6:7] op_sel_hi:[1,0]
	v_pk_mul_f32 v[20:21], v[20:21], s[6:7] op_sel_hi:[1,0]
	s_nop 0
	s_add_u32 s15, s15, s16
	v_cvt_pk_fp8_f32 v30, v20, v21
	v_pk_mul_f32 v[16:17], v[16:17], s[6:7] op_sel_hi:[1,0]
	s_nop 0
	s_addc_u32 s19, s18, s17
	v_cvt_pk_fp8_f32 v31, v16, v17
	s_add_u32 s18, s15, s34
	s_addc_u32 s19, s19, 0
	s_addk_i32 s14, 0x80
	v_pk_mul_f32 v[16:17], v[22:23], s[6:7] op_sel_hi:[1,0]
	s_ashr_i32 s15, s14, 31
	v_cvt_pk_fp8_f32 v30, v16, v17 op_sel:[0,0,1]
	v_pk_mul_f32 v[16:17], v[18:19], s[6:7] op_sel_hi:[1,0]
	s_nop 0
	s_nop 0
	v_pk_mul_f32 v[96:97], v[96:97], s[6:7] op_sel_hi:[1,0]
	s_nop 0
	s_nop 0
	s_lshl_b64 s[14:15], s[14:15], 11
	s_nop 0
	s_nop 0
	s_nop 0
	v_cvt_pk_fp8_f32 v31, v16, v17 op_sel:[0,0,1]
	v_pk_mul_f32 v[16:17], v[12:13], s[6:7] op_sel_hi:[1,0]
	v_pk_mul_f32 v[8:9], v[8:9], s[6:7] op_sel_hi:[1,0]
	s_nop 0
	v_mbcnt_lo_u32_b32 v128, -1, 0
	v_mbcnt_hi_u32_b32 v128, -1, v128
	v_cvt_pk_fp8_f32 v124, v140, v141
	v_ashrrev_i32_e32 v130, 1, v128
	v_cvt_pk_fp8_f32 v108, v112, v113
	v_cvt_pk_fp8_f32 v111, v96, v97
	v_cvt_pk_fp8_f32 v92, v100, v101
	s_nop 0
	v_cvt_pk_fp8_f32 v60, v64, v65
	v_cvt_pk_fp8_f32 v44, v48, v49
	v_pk_mul_f32 v[32:33], v[32:33], s[6:7] op_sel_hi:[1,0]
	s_nop 0
	s_add_u32 s14, s30, s14
	v_cvt_pk_fp8_f32 v28, v36, v37
	s_nop 0
	v_cvt_pk_fp8_f32 v13, v8, v9
	v_pk_mul_f32 v[8:9], v[14:15], s[6:7] op_sel_hi:[1,0]
	v_pk_mul_f32 v[4:5], v[4:5], s[6:7] op_sel_hi:[1,0]
	s_nop 0
	v_bfi_b32 v130, -16, v130, v128
	v_cvt_pk_fp8_f32 v76, v80, v81
	v_cvt_pk_fp8_f32 v47, v32, v33
	s_addc_u32 s15, s31, s15
	v_cvt_pk_fp8_f32 v12, v16, v17
	v_cvt_pk_fp8_f32 v14, v4, v5
	v_pk_mul_f32 v[0:1], v[0:1], s[6:7] op_sel_hi:[1,0]
	s_nop 0
	v_ashrrev_i32_e32 v131, 31, v130
	v_pk_mul_f32 v[96:97], v[102:103], s[6:7] op_sel_hi:[1,0]
	s_add_u32 s14, s14, s16
	v_cvt_pk_fp8_f32 v15, v0, v1
	v_lshlrev_b64 v[130:131], 11, v[130:131]
	v_cvt_pk_fp8_f32 v110, v96, v97 op_sel:[0,0,1]
	v_pk_mul_f32 v[96:97], v[98:99], s[6:7] op_sel_hi:[1,0]
	v_pk_mul_f32 v[32:33], v[38:39], s[6:7] op_sel_hi:[1,0]
	s_addc_u32 s15, s15, s17
	v_and_b32_e32 v128, 16, v128
	v_cvt_pk_fp8_f32 v124, v120, v121 op_sel:[0,0,1]
	v_pk_mul_f32 v[120:121], v[122:123], s[6:7] op_sel_hi:[1,0]
	v_cvt_pk_fp8_f32 v108, v104, v105 op_sel:[0,0,1]
	v_pk_mul_f32 v[104:105], v[106:107], s[6:7] op_sel_hi:[1,0]
	v_cvt_pk_fp8_f32 v111, v96, v97 op_sel:[0,0,1]
	v_lshl_add_u64 v[96:97], s[18:19], 0, v[130:131]
	v_cvt_pk_fp8_f32 v92, v88, v89 op_sel:[0,0,1]
	v_pk_mul_f32 v[88:89], v[90:91], s[6:7] op_sel_hi:[1,0]
	v_cvt_pk_fp8_f32 v60, v56, v57 op_sel:[0,0,1]
	v_pk_mul_f32 v[56:57], v[58:59], s[6:7] op_sel_hi:[1,0]
	v_cvt_pk_fp8_f32 v44, v40, v41 op_sel:[0,0,1]
	v_pk_mul_f32 v[40:41], v[42:43], s[6:7] op_sel_hi:[1,0]
	v_cvt_pk_fp8_f32 v46, v32, v33 op_sel:[0,0,1]
	v_pk_mul_f32 v[32:33], v[34:35], s[6:7] op_sel_hi:[1,0]
	s_add_u32 s14, s14, s34
	v_cvt_pk_fp8_f32 v28, v24, v25 op_sel:[0,0,1]
	v_pk_mul_f32 v[24:25], v[26:27], s[6:7] op_sel_hi:[1,0]
	v_pk_mul_f32 v[0:1], v[6:7], s[6:7] op_sel_hi:[1,0]
	v_cvt_pk_fp8_f32 v125, v120, v121 op_sel:[0,0,1]
	v_cvt_pk_fp8_f32 v109, v104, v105 op_sel:[0,0,1]
	v_lshl_add_u64 v[96:97], v[96:97], 0, v[128:129]
	v_cvt_pk_fp8_f32 v93, v88, v89 op_sel:[0,0,1]
	v_cvt_pk_fp8_f32 v76, v72, v73 op_sel:[0,0,1]
	v_pk_mul_f32 v[72:73], v[74:75], s[6:7] op_sel_hi:[1,0]
	v_cvt_pk_fp8_f32 v61, v56, v57 op_sel:[0,0,1]
	v_cvt_pk_fp8_f32 v45, v40, v41 op_sel:[0,0,1]
	v_cvt_pk_fp8_f32 v47, v32, v33 op_sel:[0,0,1]
	s_addc_u32 s15, s15, 0
	v_cvt_pk_fp8_f32 v29, v24, v25 op_sel:[0,0,1]
	v_cvt_pk_fp8_f32 v12, v8, v9 op_sel:[0,0,1]
	v_pk_mul_f32 v[8:9], v[10:11], s[6:7] op_sel_hi:[1,0]
	v_cvt_pk_fp8_f32 v14, v0, v1 op_sel:[0,0,1]
	v_pk_mul_f32 v[0:1], v[2:3], s[6:7] op_sel_hi:[1,0]
	v_add_co_u32_e32 v98, vcc, s29, v96
	v_cvt_pk_fp8_f32 v77, v72, v73 op_sel:[0,0,1]
	v_lshl_add_u64 v[32:33], s[14:15], 0, v[130:131]
	v_cvt_pk_fp8_f32 v13, v8, v9 op_sel:[0,0,1]
	v_cvt_pk_fp8_f32 v15, v0, v1 op_sel:[0,0,1]
	v_addc_co_u32_e32 v99, vcc, 0, v97, vcc
	v_lshl_add_u64 v[32:33], v[32:33], 0, v[128:129]
	v_add_co_u32_e32 v34, vcc, s29, v32
	v_permlane32_swap_b32_e32 v124, v126
	v_permlane32_swap_b32_e32 v125, v127
	v_permlane32_swap_b32_e32 v108, v110
	v_permlane32_swap_b32_e32 v109, v111
	v_permlane32_swap_b32_e32 v92, v94
	v_permlane32_swap_b32_e32 v93, v95
	v_permlane32_swap_b32_e32 v60, v62
	v_permlane32_swap_b32_e32 v61, v63
	v_permlane32_swap_b32_e32 v44, v46
	v_permlane32_swap_b32_e32 v45, v47
	v_addc_co_u32_e32 v35, vcc, 0, v33, vcc
	v_permlane32_swap_b32_e32 v28, v30
	v_permlane32_swap_b32_e32 v29, v31
	v_permlane16_swap_b32_e32 v124, v125
	v_permlane16_swap_b32_e32 v126, v127
	v_permlane16_swap_b32_e32 v108, v109
	v_permlane16_swap_b32_e32 v110, v111
	v_permlane16_swap_b32_e32 v92, v93
	v_permlane16_swap_b32_e32 v94, v95
	v_permlane32_swap_b32_e32 v76, v78
	v_permlane32_swap_b32_e32 v77, v79
	v_permlane16_swap_b32_e32 v60, v61
	v_permlane16_swap_b32_e32 v62, v63
	v_permlane16_swap_b32_e32 v44, v45
	v_permlane16_swap_b32_e32 v46, v47
	v_permlane16_swap_b32_e32 v28, v29
	v_permlane16_swap_b32_e32 v30, v31
	v_permlane32_swap_b32_e32 v12, v14
	v_permlane32_swap_b32_e32 v13, v15
	s_and_b64 vcc, exec, s[8:9]
	s_mov_b32 s50, s48
	s_mov_b32 s49, s47
	s_mov_b64 s[16:17], s[10:11]
	s_mov_b64 s[14:15], s[12:13]
	global_store_dwordx4 v[96:97], v[124:127], off
	global_store_dwordx4 v[98:99], v[108:111], off
	v_permlane16_swap_b32_e32 v76, v77
	v_permlane16_swap_b32_e32 v78, v79
	global_store_dwordx4 v[96:97], v[92:95], off offset:128
	global_store_dwordx4 v[98:99], v[76:79], off offset:128
	global_store_dwordx4 v[32:33], v[60:63], off
	global_store_dwordx4 v[34:35], v[44:47], off
	v_permlane16_swap_b32_e32 v12, v13
	v_permlane16_swap_b32_e32 v14, v15
	global_store_dwordx4 v[32:33], v[28:31], off offset:128
	global_store_dwordx4 v[34:35], v[12:15], off offset:128
	s_cbranch_vccz .LBB0_5808
	s_waitcnt vmcnt(0)
	v_readlane_b32 s0, v252, 2
	s_cmpk_gt_u32 s0, 0xff
	s_cbranch_scc1 .LBB0_5817
	s_barrier
